# layer-0 w_down regions dealt so that concurrent workgroups read whole contiguous source rows (on top of the layer-1 w_down deferral)
# speedup vs baseline: 1.0051x; 1.0051x over previous
; #define LAS __attribute__((address_space(3)))
; #define LDS_WAIT() asm volatile("s_waitcnt lgkmcnt(0)" ::: "memory")
;     const int pr = item >> 1, kb = 2 * (pr / nblk) + (item & 1), nb = pr % nblk, k0 = 64 * kb, n0 = 32 * nb;
;     const int nr = n0 + (lane & 31); const int sc = MAP == 1 ? src_col_in(nr) : nr;
;     float v[32];
; #pragma unroll
;     for (int i = 0; i < 32; ++i) v[i] = sc >= 0 ? W[(size_t)(k0 + 2 * i + (lane >> 5)) * Nsrc + sc] : 0.f;
; #pragma unroll
;     for (int i = 0; i < 32; ++i) { const int k = k0 + 2 * i + (lane >> 5); float x = v[i] * wscale; if (KS) x *= (k < ksplit ? ksA[k] : ksB[k - ksplit]); scr[(2 * i + (lane >> 5)) * 33 + (lane & 31)] = x; }
;     LDS_WAIT(); asm volatile("" ::: "memory");
;     const int c = lane & 7;
; #pragma unroll
;     for (int j = 0; j < 4; ++j) { const int n = (lane >> 3) + 8 * j; const LAS float* s = scr + (8 * c) * 33 + n;
; __global__ void __launch_bounds__(NWAVES * 64, 2) hybrid_fwd(Args args) {
;     ...
;         LAS float* scr = (LAS float*)(F.lds + RING_OFF + wave * 16384);
;         constexpr int I_IN = (DM / 64) * (NPROJ / 32), I_O = (DM / 64) * (DM / 32), I_UP = (DM / 64) * (FF / 32), I_DN = (FF / 64) * (DM / 32);
;         constexpr int I_L = I_IN + I_O + I_UP + I_DN;
;         for (int rep = 0; rep < REP_PRO; ++rep)
;         for (int it = gw; it < DEPTH * I_L; it += NGW) {
;             const int l = it / I_L; int r = it % I_L;
;             if (r < I_IN) { if (l >= PROJ_F8_FROM) p0_transpose_item_f8<true, 1>(args.in[2] + (size_t)l * DM * NSRC, DM, NSRC, NPROJ / 32, (unsigned char*)(ws + WS_WIN + l * SZ_WIN), WUP8_SCALE, args.in[1] + l * DM, args.in[1] + l * DM, DM, scr, r, lane);
.LBB0_11:
	s_or_b64 exec, exec, s[0:1]
	v_mov_b32_e32 v1, v0
	v_readlane_b32 s1, v253, 2
	v_readfirstlane_b32 s0, v1
	s_ashr_i32 s0, s0, 6
	s_lshl_b32 s1, s1, 3
	s_add_i32 s80, s0, s1
	s_lshl_b32 s0, s0, 14
	v_lshlrev_b32_e32 v2, 3, v1
	v_writelane_b32 v253, s1, 46
	s_add_i32 s1, s0, 0
	v_and_b32_e32 v18, 31, v1
	v_bfe_u32 v20, v1, 3, 3
	v_and_b32_e32 v8, 56, v2
	s_lshl_b32 s96, s83, 3
	s_lshl_b32 s76, s83, 9
	v_bfe_u32 v6, v1, 5, 1
	v_lshl_add_u32 v25, v18, 2, s1
	s_movk_i32 s0, 0x84
	v_mul_u32_u24_e32 v2, 0x84, v8
	v_lshlrev_b32_e32 v3, 2, v20
	s_cmp_gt_i32 s80, 0x2f3ff
	v_mad_u32_u24 v19, v6, s0, v25
	v_mov_b32_e32 v11, 0
	v_add3_u32 v21, s1, v2, v3
	v_or_b32_e32 v22, 8, v20
	v_or_b32_e32 v23, 16, v20
	v_or_b32_e32 v24, 24, v20
	s_cbranch_scc1 .Lco3_hop_192
	v_and_b32_e32 v249, 63, v0
	v_lshrrev_b32_e32 v250, 6, v0
	v_readlane_b32 s15, v253, 2
	s_lshr_b32 s22, s15, 3
	s_and_b32 s23, s15, 7
	v_lshrrev_b32_e32 v246, 5, v249
	v_lshl_add_u32 v247, v250, 4, v246
	v_and_b32_e32 v248, 31, v249
	v_xor_b32_e32 v248, v248, v250
	v_lshlrev_b32_e32 v248, 4, v248
	v_lshl_add_u32 v209, v247, 9, v248
	v_add_u32_e32 v210, 0x10000, v209
	v_lshlrev_b32_e32 v96, 2, v247
	v_and_b32_e32 v248, 31, v249
	v_lshlrev_b32_e32 v248, 4, v248
	s_mov_b32 s20, 0x10000
	v_mad_u32_u24 v74, v247, s20, v248
	s_mov_b32 s20, 0x4000
	v_mad_u32_u24 v75, v247, s20, v248
	s_mov_b32 s20, 0xb140
	v_mad_u32_u24 v76, v247, s20, v248
	v_and_b32_e32 v246, 7, v249
	v_lshrrev_b32_e32 v247, 5, v249
	v_lshl_add_u32 v247, v250, 2, v247
	v_xor_b32_e32 v247, v247, v246
	v_lshlrev_b32_e32 v247, 4, v247
	v_lshl_add_u32 v247, v246, 13, v247
	v_bfe_u32 v248, v249, 3, 2
	v_lshl_add_u32 v211, v248, 2, v247
	v_add_u32_e32 v212, 0x10000, v211
	v_and_b32_e32 v246, 7, v249
	v_lshrrev_b32_e32 v247, 5, v249
	v_lshl_add_u32 v247, v250, 2, v247
	v_add_u32_e32 v247, 2, v247
	v_xor_b32_e32 v247, v247, v246
	v_lshlrev_b32_e32 v247, 4, v247
	v_lshl_add_u32 v247, v246, 13, v247
	v_bfe_u32 v248, v249, 3, 2
	v_lshl_add_u32 v213, v248, 2, v247
	v_add_u32_e32 v214, 0x10000, v213
	v_and_b32_e32 v246, 15, v249
	v_lshrrev_b32_e32 v247, 1, v246
	v_lshlrev_b32_e32 v248, 2, v250
	v_xor_b32_e32 v248, v248, v247
	v_lshlrev_b32_e32 v248, 4, v248
	v_lshl_add_u32 v248, v246, 12, v248
	v_lshrrev_b32_e32 v247, 4, v249
	v_lshl_add_u32 v112, v247, 2, v248
	v_add_u32_e32 v113, 0x10000, v112
	v_and_b32_e32 v246, 15, v249
	v_lshrrev_b32_e32 v247, 1, v246
	v_lshlrev_b32_e32 v248, 2, v250
	v_add_u32_e32 v248, 1, v248
	v_xor_b32_e32 v248, v248, v247
	v_lshlrev_b32_e32 v248, 4, v248
	v_lshl_add_u32 v248, v246, 12, v248
	v_lshrrev_b32_e32 v247, 4, v249
	v_lshl_add_u32 v114, v247, 2, v248
	v_add_u32_e32 v115, 0x10000, v114
	v_and_b32_e32 v246, 15, v249
	v_lshrrev_b32_e32 v247, 1, v246
	v_lshlrev_b32_e32 v248, 2, v250
	v_add_u32_e32 v248, 2, v248
	v_xor_b32_e32 v248, v248, v247
	v_lshlrev_b32_e32 v248, 4, v248
	v_lshl_add_u32 v248, v246, 12, v248
	v_lshrrev_b32_e32 v247, 4, v249
	v_lshl_add_u32 v116, v247, 2, v248
	v_add_u32_e32 v117, 0x10000, v116
	v_and_b32_e32 v246, 15, v249
	v_lshrrev_b32_e32 v247, 1, v246
	v_lshlrev_b32_e32 v248, 2, v250
	v_add_u32_e32 v248, 3, v248
	v_xor_b32_e32 v248, v248, v247
	v_lshlrev_b32_e32 v248, 4, v248
	v_lshl_add_u32 v248, v246, 12, v248
	v_lshrrev_b32_e32 v247, 4, v249
	v_lshl_add_u32 v118, v247, 2, v248
	v_add_u32_e32 v119, 0x10000, v118
	v_lshrrev_b32_e32 v246, 3, v249
	v_lshl_add_u32 v246, v250, 4, v246
	v_and_b32_e32 v247, 7, v249
	v_lshlrev_b32_e32 v247, 4, v247
	v_lshl_add_u32 v77, v246, 12, v247
	v_lshl_add_u32 v79, v246, 14, v247
	v_and_b32_e32 v248, 63, v246
	v_lshlrev_b32_e32 v248, 1, v248
	v_lshrrev_b32_e32 v246, 6, v246
	v_or_b32_e32 v248, v248, v246
	v_lshl_add_u32 v81, v248, 12, v247
	v_lshrrev_b32_e32 v246, 3, v249
	v_lshl_add_u32 v246, v250, 4, v246
	v_add_u32_e32 v246, 8, v246
	v_and_b32_e32 v247, 7, v249
	v_lshlrev_b32_e32 v247, 4, v247
	v_lshl_add_u32 v78, v246, 12, v247
	v_lshl_add_u32 v80, v246, 14, v247
	v_and_b32_e32 v248, 63, v246
	v_lshlrev_b32_e32 v248, 1, v248
	v_lshrrev_b32_e32 v246, 6, v246
	v_or_b32_e32 v248, v248, v246
	v_lshl_add_u32 v82, v248, 12, v247
	v_lshrrev_b32_e32 v246, 4, v249
	v_lshl_add_u32 v246, v250, 4, v246
	v_and_b32_e32 v247, 15, v249
	v_lshlrev_b32_e32 v247, 4, v247
	v_lshl_add_u32 v83, v246, 13, v247
	v_and_b32_e32 v248, 63, v246
	v_lshlrev_b32_e32 v248, 1, v248
	v_lshrrev_b32_e32 v246, 6, v246
	v_or_b32_e32 v248, v248, v246
	v_lshl_add_u32 v87, v248, 13, v247
	v_lshrrev_b32_e32 v246, 4, v249
	v_lshl_add_u32 v246, v250, 4, v246
	v_add_u32_e32 v246, 4, v246
	v_and_b32_e32 v247, 15, v249
	v_lshlrev_b32_e32 v247, 4, v247
	v_lshl_add_u32 v84, v246, 13, v247
	v_and_b32_e32 v248, 63, v246
	v_lshlrev_b32_e32 v248, 1, v248
	v_lshrrev_b32_e32 v246, 6, v246
	v_or_b32_e32 v248, v248, v246
	v_lshl_add_u32 v88, v248, 13, v247
	v_lshrrev_b32_e32 v246, 4, v249
	v_lshl_add_u32 v246, v250, 4, v246
	v_add_u32_e32 v246, 8, v246
	v_and_b32_e32 v247, 15, v249
	v_lshlrev_b32_e32 v247, 4, v247
	v_lshl_add_u32 v85, v246, 13, v247
	v_and_b32_e32 v248, 63, v246
	v_lshlrev_b32_e32 v248, 1, v248
	v_lshrrev_b32_e32 v246, 6, v246
	v_or_b32_e32 v248, v248, v246
	v_lshl_add_u32 v89, v248, 13, v247
	v_lshrrev_b32_e32 v246, 4, v249
	v_lshl_add_u32 v246, v250, 4, v246
	v_add_u32_e32 v246, 12, v246
	v_and_b32_e32 v247, 15, v249
	v_lshlrev_b32_e32 v247, 4, v247
	v_lshl_add_u32 v86, v246, 13, v247
	v_and_b32_e32 v248, 63, v246
	v_lshlrev_b32_e32 v248, 1, v248
	v_lshrrev_b32_e32 v246, 6, v246
	v_or_b32_e32 v248, v248, v246
	v_lshl_add_u32 v90, v248, 13, v247
	v_mov_b32_e32 v95, 0x43e00000
	s_mov_b32 s62, 0xc3e00000
	s_mov_b32 s63, 0x7fff
	s_mov_b32 s64, 0x07060302
	v_readlane_b32 s10, v253, 5
;     ...
;     for (int i = 0; i < 32; ++i) v[i] = sc >= 0 ? W[(size_t)(k0 + 2 * i + (lane >> 5)) * Nsrc + sc] : 0.f;
; #pragma unroll
;     for (int i = 0; i < 32; ++i) { const int k = k0 + 2 * i + (lane >> 5); float x = v[i] * wscale; if (KS) x *= (k < ksplit ? ksA[k] : ksB[k - ksplit]); scr[(2 * i + (lane >> 5)) * 33 + (lane & 31)] = x; }
; __global__ void __launch_bounds__(NWAVES * 64, 2) hybrid_fwd(Args args) {
;     ...
;         for (int rep = 0; rep < REP_PRO; ++rep)
;         for (int it = gw; it < DEPTH * I_L; it += NGW) {
;             const int l = it / I_L; int r = it % I_L;
;             if (r < I_IN) { if (l >= PROJ_F8_FROM) p0_transpose_item_f8<true, 1>(args.in[2] + (size_t)l * DM * NSRC, DM, NSRC, NPROJ / 32, (unsigned char*)(ws + WS_WIN + l * SZ_WIN), WUP8_SCALE, args.in[1] + l * DM, args.in[1] + l * DM, DM, scr, r, lane);
;                 else p0_transpose_item<1, true>(args.in[2] + (size_t)l * DM * NSRC, DM, NSRC, NPROJ / 32, (bf16*)(ws + WS_WIN + l * SZ_WIN), args.in[1] + l * DM, args.in[1] + l * DM, DM, scr, r, lane); continue; } r -= I_IN;
;             if (r < I_O) { if (l >= WO_F8_FROM) p0_transpose_item_f8<true>(args.in[13] + (size_t)l * DM * DM, DM, DM, DM / 32, (unsigned char*)(ws + WS_WO + l * SZ_WO), 64.f, args.in[6] + l * 2048, args.in[12] + l * 2048, 2048, scr, r, lane);
;                 else p0_transpose_item<0, true>(args.in[13] + (size_t)l * DM * DM, DM, DM, DM / 32, (bf16*)(ws + WS_WO + l * SZ_WO), args.in[6] + l * 2048, args.in[12] + l * 2048, 2048, scr, r, lane); continue; } r -= I_O;
;             if (r < I_UP) { p0_transpose_item_f8<true>(args.in[15] + (size_t)l * DM * FF, DM, FF, FF / 32, (unsigned char*)(ws + WS_WUP + l * SZ_WUP), WUP8_SCALE, args.in[14] + l * DM, args.in[14] + l * DM, DM, scr, r, lane); continue; } r -= I_UP;
;             p0_transpose_item_f8<false>(args.in[16] + (size_t)l * FF * DM, FF, DM, DM / 32, (unsigned char*)(ws + WS_WDN + l * SZ_WDN), 128.f, args.in[16], args.in[16], 0, scr, r, lane);
	v_readlane_b32 s11, v253, 6
	s_lshl_b32 s20, s22, 9
	s_add_u32 s10, s10, s20
	s_addc_u32 s11, s11, 0
	global_load_dword v42, v96, s[10:11] offset:0
	global_load_dword v43, v96, s[10:11] offset:8
	global_load_dword v44, v96, s[10:11] offset:16
	global_load_dword v45, v96, s[10:11] offset:24
	global_load_dword v46, v96, s[10:11] offset:32
	global_load_dword v47, v96, s[10:11] offset:40
	global_load_dword v48, v96, s[10:11] offset:48
	global_load_dword v49, v96, s[10:11] offset:56
	v_readlane_b32 s10, v253, 5
	v_readlane_b32 s11, v253, 6
	s_lshl_b32 s20, s22, 9
	s_add_i32 s20, s20, 0x4000
	s_add_u32 s10, s10, s20
	s_addc_u32 s11, s11, 0
	global_load_dword v50, v96, s[10:11] offset:0
	global_load_dword v51, v96, s[10:11] offset:8
	global_load_dword v52, v96, s[10:11] offset:16
	global_load_dword v53, v96, s[10:11] offset:24
	global_load_dword v54, v96, s[10:11] offset:32
	global_load_dword v55, v96, s[10:11] offset:40
	global_load_dword v56, v96, s[10:11] offset:48
	global_load_dword v57, v96, s[10:11] offset:56
	v_readlane_b32 s10, v253, 15
	v_readlane_b32 s11, v253, 16
	v_readlane_b32 s20, v253, 27
	v_readlane_b32 s21, v253, 28
	s_sub_i32 s26, s22, 16
	s_cmp_lt_u32 s22, 16
	s_cselect_b32 s10, s10, s20
	s_cselect_b32 s11, s11, s21
	s_cselect_b32 s26, s22, s26
	s_lshl_b32 s20, s26, 9
	s_add_u32 s10, s10, s20
	s_addc_u32 s11, s11, 0
	global_load_dword v58, v96, s[10:11] offset:0
	global_load_dword v59, v96, s[10:11] offset:8
	global_load_dword v60, v96, s[10:11] offset:16
	global_load_dword v61, v96, s[10:11] offset:24
	global_load_dword v62, v96, s[10:11] offset:32
	global_load_dword v63, v96, s[10:11] offset:40
	global_load_dword v64, v96, s[10:11] offset:48
	global_load_dword v65, v96, s[10:11] offset:56
	v_readlane_b32 s10, v253, 15
	v_readlane_b32 s11, v253, 16
	v_readlane_b32 s20, v253, 27
	v_readlane_b32 s21, v253, 28
	s_sub_i32 s26, s22, 16
	s_cmp_lt_u32 s22, 16
	s_cselect_b32 s10, s10, s20
	s_cselect_b32 s11, s11, s21
	s_cselect_b32 s26, s22, s26
	s_lshl_b32 s20, s26, 9
	s_add_i32 s20, s20, 0x2000
	s_add_u32 s10, s10, s20
	s_addc_u32 s11, s11, 0
	global_load_dword v66, v96, s[10:11] offset:0
	global_load_dword v67, v96, s[10:11] offset:8
	global_load_dword v68, v96, s[10:11] offset:16
	global_load_dword v69, v96, s[10:11] offset:24
	global_load_dword v70, v96, s[10:11] offset:32
	global_load_dword v71, v96, s[10:11] offset:40
	global_load_dword v72, v96, s[10:11] offset:48
	global_load_dword v73, v96, s[10:11] offset:56
	v_readlane_b32 s10, v253, 31
	v_readlane_b32 s11, v253, 32
	s_lshl_b32 s20, s22, 9
	s_add_u32 s10, s10, s20
	s_addc_u32 s11, s11, 0
	global_load_dword v26, v96, s[10:11] offset:0
	global_load_dword v27, v96, s[10:11] offset:8
	global_load_dword v28, v96, s[10:11] offset:16
	global_load_dword v29, v96, s[10:11] offset:24
	global_load_dword v30, v96, s[10:11] offset:32
	global_load_dword v31, v96, s[10:11] offset:40
	global_load_dword v32, v96, s[10:11] offset:48
	global_load_dword v33, v96, s[10:11] offset:56
	v_readlane_b32 s10, v253, 31
	v_readlane_b32 s11, v253, 32
	s_lshl_b32 s20, s22, 9
	s_add_i32 s20, s20, 0x4000
	s_add_u32 s10, s10, s20
	s_addc_u32 s11, s11, 0
	global_load_dword v34, v96, s[10:11] offset:0
	global_load_dword v35, v96, s[10:11] offset:8
	global_load_dword v36, v96, s[10:11] offset:16
	global_load_dword v37, v96, s[10:11] offset:24
	global_load_dword v38, v96, s[10:11] offset:32
	global_load_dword v39, v96, s[10:11] offset:40
	global_load_dword v40, v96, s[10:11] offset:48
	global_load_dword v41, v96, s[10:11] offset:56
	s_waitcnt vmcnt(0)
	v_mul_f32_e32 v50, 0x42800000, v50
	v_mul_f32_e32 v51, 0x42800000, v51
	v_mul_f32_e32 v52, 0x42800000, v52
	v_mul_f32_e32 v53, 0x42800000, v53
	v_mul_f32_e32 v54, 0x42800000, v54
	v_mul_f32_e32 v55, 0x42800000, v55
	v_mul_f32_e32 v56, 0x42800000, v56
	v_mul_f32_e32 v57, 0x42800000, v57
	v_mul_f32_e32 v66, 0x42800000, v66
	v_mul_f32_e32 v67, 0x42800000, v67
	v_mul_f32_e32 v68, 0x42800000, v68
	v_mul_f32_e32 v69, 0x42800000, v69
	v_mul_f32_e32 v70, 0x42800000, v70
	v_mul_f32_e32 v71, 0x42800000, v71
	v_mul_f32_e32 v72, 0x42800000, v72
	v_mul_f32_e32 v73, 0x42800000, v73
	v_mul_f32_e32 v26, 0x42800000, v26
	v_mul_f32_e32 v27, 0x42800000, v27
	v_mul_f32_e32 v28, 0x42800000, v28
	v_mul_f32_e32 v29, 0x42800000, v29
	v_mul_f32_e32 v30, 0x42800000, v30
	v_mul_f32_e32 v31, 0x42800000, v31
	v_mul_f32_e32 v32, 0x42800000, v32
	v_mul_f32_e32 v33, 0x42800000, v33
	v_mul_f32_e32 v34, 0x42800000, v34
	v_mul_f32_e32 v35, 0x42800000, v35
	v_mul_f32_e32 v36, 0x42800000, v36
	v_mul_f32_e32 v37, 0x42800000, v37
	v_mul_f32_e32 v38, 0x42800000, v38
	v_mul_f32_e32 v39, 0x42800000, v39
	v_mul_f32_e32 v40, 0x42800000, v40
	v_mul_f32_e32 v41, 0x42800000, v41
	v_readlane_b32 s30, v253, 33
	v_readlane_b32 s31, v253, 34
	v_readlane_b32 s32, v253, 41
	v_readlane_b32 s33, v253, 42
	s_mul_i32 s20, s22, 0x800000
	s_lshl_b32 s21, s23, 9
	s_add_u32 s20, s20, s21
	s_add_u32 s30, s30, s20
	s_addc_u32 s31, s31, 0
	s_add_u32 s32, s32, 0xf600000
	s_addc_u32 s33, s33, 0
	s_lshl_b32 s20, s22, 7
	s_mul_i32 s21, s23, 0x80000
	s_add_u32 s20, s20, s21
	s_add_u32 s32, s32, s20
	s_addc_u32 s33, s33, 0
	v_readlane_b32 s34, v253, 33
	v_readlane_b32 s35, v253, 34
	v_readlane_b32 s36, v253, 41
	v_readlane_b32 s37, v253, 42
	s_add_u32 s34, s34, 0x10000000
	s_addc_u32 s35, s35, 0
	s_mul_i32 s20, s22, 0x800000
	s_lshl_b32 s21, s23, 9
	s_add_u32 s20, s20, s21
	s_add_u32 s34, s34, s20
	s_addc_u32 s35, s35, 0
	s_add_u32 s36, s36, 0x17600000
	s_addc_u32 s37, s37, 0
	s_lshl_b32 s20, s22, 7
	s_mul_i32 s21, s23, 0x80000
	s_add_u32 s20, s20, s21
	s_add_u32 s36, s36, s20
	s_addc_u32 s37, s37, 0
	v_readlane_b32 s38, v253, 35
;     ...
; #pragma unroll
;     for (int i = 0; i < 32; ++i) v[i] = sc >= 0 ? W[(size_t)(k0 + 2 * i + (lane >> 5)) * Nsrc + sc] : 0.f;
; #pragma unroll
;     for (int i = 0; i < 32; ++i) { const int k = k0 + 2 * i + (lane >> 5); float x = v[i] * wscale; if (KS) x *= (k < ksplit ? ksA[k] : ksB[k - ksplit]); scr[(2 * i + (lane >> 5)) * 33 + (lane & 31)] = x; }
; __global__ void __launch_bounds__(NWAVES * 64, 2) hybrid_fwd(Args args) {
;     ...
;         for (int it = gw; it < DEPTH * I_L; it += NGW) {
;             const int l = it / I_L; int r = it % I_L;
;             if (r < I_IN) { if (l >= PROJ_F8_FROM) p0_transpose_item_f8<true, 1>(args.in[2] + (size_t)l * DM * NSRC, DM, NSRC, NPROJ / 32, (unsigned char*)(ws + WS_WIN + l * SZ_WIN), WUP8_SCALE, args.in[1] + l * DM, args.in[1] + l * DM, DM, scr, r, lane);
;                 else p0_transpose_item<1, true>(args.in[2] + (size_t)l * DM * NSRC, DM, NSRC, NPROJ / 32, (bf16*)(ws + WS_WIN + l * SZ_WIN), args.in[1] + l * DM, args.in[1] + l * DM, DM, scr, r, lane); continue; } r -= I_IN;
;             if (r < I_O) { if (l >= WO_F8_FROM) p0_transpose_item_f8<true>(args.in[13] + (size_t)l * DM * DM, DM, DM, DM / 32, (unsigned char*)(ws + WS_WO + l * SZ_WO), 64.f, args.in[6] + l * 2048, args.in[12] + l * 2048, 2048, scr, r, lane);
;                 else p0_transpose_item<0, true>(args.in[13] + (size_t)l * DM * DM, DM, DM, DM / 32, (bf16*)(ws + WS_WO + l * SZ_WO), args.in[6] + l * 2048, args.in[12] + l * 2048, 2048, scr, r, lane); continue; } r -= I_O;
;             if (r < I_UP) { p0_transpose_item_f8<true>(args.in[15] + (size_t)l * DM * FF, DM, FF, FF / 32, (unsigned char*)(ws + WS_WUP + l * SZ_WUP), WUP8_SCALE, args.in[14] + l * DM, args.in[14] + l * DM, DM, scr, r, lane); continue; } r -= I_UP;
;             p0_transpose_item_f8<false>(args.in[16] + (size_t)l * FF * DM, FF, DM, DM / 32, (unsigned char*)(ws + WS_WDN + l * SZ_WDN), 128.f, args.in[16], args.in[16], 0, scr, r, lane);
	v_readlane_b32 s39, v253, 36
	v_readlane_b32 s40, v253, 41
	v_readlane_b32 s41, v253, 42
	s_lshr_b32 s26, s15, 5
	s_and_b32 s27, s15, 31
	s_mul_i32 s20, s26, 0x200000
	s_lshl_b32 s21, s27, 9
	s_add_u32 s20, s20, s21
	s_add_u32 s38, s38, s20
	s_addc_u32 s39, s39, 0
	s_add_u32 s40, s40, 0x1f600000
	s_addc_u32 s41, s41, 0
	s_lshl_b32 s20, s26, 7
	s_mul_i32 s21, s27, 0x200000
	s_add_u32 s20, s20, s21
	s_add_u32 s40, s40, s20
	s_addc_u32 s41, s41, 0
	v_readlane_b32 s42, v253, 35
	v_readlane_b32 s43, v253, 36
	v_readlane_b32 s44, v253, 41
	v_readlane_b32 s45, v253, 42
	s_add_u32 s42, s42, 0x10000000
	s_addc_u32 s43, s43, 0
	s_lshr_b32 s26, s15, 5
	s_and_b32 s27, s15, 31
	s_mul_i32 s20, s26, 0x200000
	s_lshl_b32 s21, s27, 9
	s_add_u32 s20, s20, s21
	s_add_u32 s42, s42, s20
	s_addc_u32 s43, s43, 0
	s_add_u32 s44, s44, 0x27600000
	s_addc_u32 s45, s45, 0
	s_lshl_b32 s20, s26, 7
	s_mul_i32 s21, s27, 0x200000
	s_add_u32 s20, s20, s21
	s_add_u32 s44, s44, s20
	s_addc_u32 s45, s45, 0
	v_readlane_b32 s46, v253, 7
	v_readlane_b32 s47, v253, 8
	v_readlane_b32 s48, v253, 41
	v_readlane_b32 s49, v253, 42
	s_mul_i32 s20, s22, 0x58a000
	s_add_u32 s46, s46, s20
	s_addc_u32 s47, s47, 0
	s_add_u32 s48, s48, 0x200000
	s_addc_u32 s49, s49, 0
	s_lshl_b32 s20, s22, 8
	s_add_u32 s48, s48, s20
	s_addc_u32 s49, s49, 0
	v_readlane_b32 s50, v253, 7
	v_readlane_b32 s51, v253, 8
	v_readlane_b32 s52, v253, 41
	v_readlane_b32 s53, v253, 42
	s_add_u32 s50, s50, 0xb140000
	s_addc_u32 s51, s51, 0
	s_mul_i32 s20, s22, 0x58a000
	s_add_u32 s50, s50, s20
	s_addc_u32 s51, s51, 0
	s_add_u32 s52, s52, 0x5c00000
	s_addc_u32 s53, s53, 0
	s_lshl_b32 s20, s22, 7
	s_add_u32 s52, s52, s20
	s_addc_u32 s53, s53, 0
	v_readlane_b32 s54, v253, 29
	v_readlane_b32 s55, v253, 30
	v_readlane_b32 s56, v253, 41
	v_readlane_b32 s57, v253, 42
	s_mul_i32 s20, s22, 0x200000
	s_lshl_b32 s21, s23, 9
	s_add_u32 s20, s20, s21
	s_add_u32 s54, s54, s20
	s_addc_u32 s55, s55, 0
	s_add_u32 s56, s56, 0xb600000
	s_addc_u32 s57, s57, 0
	s_lshl_b32 s20, s22, 8
	s_mul_i32 s21, s23, 0x100000
	s_add_u32 s20, s20, s21
	s_add_u32 s56, s56, s20
	s_addc_u32 s57, s57, 0
	v_readlane_b32 s58, v253, 29
	v_readlane_b32 s59, v253, 30
	v_readlane_b32 s60, v253, 41
	v_readlane_b32 s61, v253, 42
	s_add_u32 s58, s58, 0x4000000
	s_addc_u32 s59, s59, 0
	s_mul_i32 s20, s22, 0x200000
	s_lshl_b32 s21, s23, 9
	s_add_u32 s20, s20, s21
	s_add_u32 s58, s58, s20
	s_addc_u32 s59, s59, 0
	s_add_u32 s60, s60, 0xd600000
	s_addc_u32 s61, s61, 0
	s_lshl_b32 s20, s22, 7
	s_mul_i32 s21, s23, 0x80000
	s_add_u32 s20, s20, s21
	s_add_u32 s60, s60, s20
	s_addc_u32 s61, s61, 0
	s_mov_b64 s[8:9], s[30:31]
	global_load_dwordx4 v[144:147], v74, s[8:9]
	s_add_u32 s8, s8, 0x20000
	s_addc_u32 s9, s9, 0
	global_load_dwordx4 v[148:151], v74, s[8:9]
	s_add_u32 s8, s8, 0x20000
	s_addc_u32 s9, s9, 0
	global_load_dwordx4 v[152:155], v74, s[8:9]
	s_add_u32 s8, s8, 0x20000
	s_addc_u32 s9, s9, 0
	global_load_dwordx4 v[156:159], v74, s[8:9]
	s_add_u32 s8, s8, 0x20000
	s_addc_u32 s9, s9, 0
	global_load_dwordx4 v[160:163], v74, s[8:9]
	s_add_u32 s8, s8, 0x20000
	s_addc_u32 s9, s9, 0
	global_load_dwordx4 v[164:167], v74, s[8:9]
	s_add_u32 s8, s8, 0x20000
	s_addc_u32 s9, s9, 0
	global_load_dwordx4 v[168:171], v74, s[8:9]
	s_add_u32 s8, s8, 0x20000
	s_addc_u32 s9, s9, 0
	global_load_dwordx4 v[172:175], v74, s[8:9]
	s_add_u32 s8, s30, 0x1000
	s_addc_u32 s9, s31, 0
	global_load_dwordx4 v[176:179], v74, s[8:9]
	s_add_u32 s8, s8, 0x20000
	s_addc_u32 s9, s9, 0
	global_load_dwordx4 v[180:183], v74, s[8:9]
	s_add_u32 s8, s8, 0x20000
	s_addc_u32 s9, s9, 0
	global_load_dwordx4 v[184:187], v74, s[8:9]
	s_add_u32 s8, s8, 0x20000
	s_addc_u32 s9, s9, 0
	global_load_dwordx4 v[188:191], v74, s[8:9]
	s_add_u32 s8, s8, 0x20000
	s_addc_u32 s9, s9, 0
	global_load_dwordx4 v[192:195], v74, s[8:9]
	s_add_u32 s8, s8, 0x20000
	s_addc_u32 s9, s9, 0
	global_load_dwordx4 v[196:199], v74, s[8:9]
	s_add_u32 s8, s8, 0x20000
	s_addc_u32 s9, s9, 0
	global_load_dwordx4 v[200:203], v74, s[8:9]
	s_add_u32 s8, s8, 0x20000
	s_addc_u32 s9, s9, 0
	global_load_dwordx4 v[204:207], v74, s[8:9]
	s_waitcnt vmcnt(8)
	v_mul_f32_e32 v144, v26, v144
	v_mul_f32_e32 v145, v26, v145
	v_mul_f32_e32 v146, v26, v146
	v_mul_f32_e32 v147, v26, v147
	ds_write_b128 v209, v[144:147]
	v_mul_f32_e32 v148, v27, v148
	v_mul_f32_e32 v149, v27, v149
	v_mul_f32_e32 v150, v27, v150
	v_mul_f32_e32 v151, v27, v151
	ds_write_b128 v209, v[148:151] offset:1024
	v_mul_f32_e32 v152, v28, v152
	v_mul_f32_e32 v153, v28, v153
	v_mul_f32_e32 v154, v28, v154
	v_mul_f32_e32 v155, v28, v155
	ds_write_b128 v209, v[152:155] offset:2048
	v_mul_f32_e32 v156, v29, v156
	v_mul_f32_e32 v157, v29, v157
	v_mul_f32_e32 v158, v29, v158
	v_mul_f32_e32 v159, v29, v159
	ds_write_b128 v209, v[156:159] offset:3072
	v_mul_f32_e32 v160, v30, v160
	v_mul_f32_e32 v161, v30, v161
	v_mul_f32_e32 v162, v30, v162
	v_mul_f32_e32 v163, v30, v163
	ds_write_b128 v209, v[160:163] offset:4096
	v_mul_f32_e32 v164, v31, v164
	v_mul_f32_e32 v165, v31, v165
	v_mul_f32_e32 v166, v31, v166
	v_mul_f32_e32 v167, v31, v167
	ds_write_b128 v209, v[164:167] offset:5120
	v_mul_f32_e32 v168, v32, v168
	v_mul_f32_e32 v169, v32, v169
	v_mul_f32_e32 v170, v32, v170
	v_mul_f32_e32 v171, v32, v171
	ds_write_b128 v209, v[168:171] offset:6144
	v_mul_f32_e32 v172, v33, v172
	v_mul_f32_e32 v173, v33, v173
	v_mul_f32_e32 v174, v33, v174
	v_mul_f32_e32 v175, v33, v175
	ds_write_b128 v209, v[172:175] offset:7168
	s_waitcnt lgkmcnt(0)
	s_barrier
; #define GAS __attribute__((address_space(1)))
; #define LAS __attribute__((address_space(3)))
; #define LDS_WAIT() asm volatile("s_waitcnt lgkmcnt(0)" ::: "memory")
;     ...
; #pragma unroll
;     for (int i = 0; i < 32; ++i) v[i] = sc >= 0 ? W[(size_t)(k0 + 2 * i + (lane >> 5)) * Nsrc + sc] : 0.f;
; #pragma unroll
;     for (int i = 0; i < 32; ++i) { const int k = k0 + 2 * i + (lane >> 5); float x = v[i] * wscale; if (KS) x *= (k < ksplit ? ksA[k] : ksB[k - ksplit]); scr[(2 * i + (lane >> 5)) * 33 + (lane & 31)] = x; }
;     LDS_WAIT(); asm volatile("" ::: "memory");
;     const int c = lane & 7;
; #pragma unroll
;     for (int j = 0; j < 4; ++j) { const int n = (lane >> 3) + 8 * j; const LAS float* s = scr + (8 * c) * 33 + n;
;         const unsigned long long o = (unsigned long long)pg8::pk4_fp8(s[0 * 33], s[1 * 33], s[2 * 33], s[3 * 33]) | ((unsigned long long)pg8::pk4_fp8(s[4 * 33], s[5 * 33], s[6 * 33], s[7 * 33]) << 32);
;         *(GAS unsigned long long*)(WT + (size_t)(n0 + n) * K + k0 + 8 * c) = o; }
;     LDS_WAIT(); asm volatile("" ::: "memory");
	s_add_u32 s8, s30, 0x2000
	s_addc_u32 s9, s31, 0
	global_load_dwordx4 v[144:147], v74, s[8:9]
	s_add_u32 s8, s8, 0x20000
	s_addc_u32 s9, s9, 0
	global_load_dwordx4 v[148:151], v74, s[8:9]
	s_add_u32 s8, s8, 0x20000
	s_addc_u32 s9, s9, 0
	global_load_dwordx4 v[152:155], v74, s[8:9]
	s_add_u32 s8, s8, 0x20000
	s_addc_u32 s9, s9, 0
	global_load_dwordx4 v[156:159], v74, s[8:9]
	s_add_u32 s8, s8, 0x20000
	s_addc_u32 s9, s9, 0
	global_load_dwordx4 v[160:163], v74, s[8:9]
	s_add_u32 s8, s8, 0x20000
	s_addc_u32 s9, s9, 0
	global_load_dwordx4 v[164:167], v74, s[8:9]
	s_add_u32 s8, s8, 0x20000
	s_addc_u32 s9, s9, 0
	global_load_dwordx4 v[168:171], v74, s[8:9]
	s_add_u32 s8, s8, 0x20000
	s_addc_u32 s9, s9, 0
	global_load_dwordx4 v[172:175], v74, s[8:9]
	s_mov_b64 s[6:7], s[32:33]
	ds_read_b32 v226, v211
	ds_read_b32 v227, v211 offset:512
	ds_read_b32 v228, v211 offset:1024
	ds_read_b32 v229, v211 offset:1536
	ds_read_b32 v230, v211 offset:2048
	ds_read_b32 v231, v211 offset:2560
	ds_read_b32 v232, v211 offset:3072
	ds_read_b32 v233, v211 offset:3584
	ds_read_b32 v234, v211 offset:4096
	ds_read_b32 v235, v211 offset:4608
	ds_read_b32 v236, v211 offset:5120
	ds_read_b32 v237, v211 offset:5632
	ds_read_b32 v238, v211 offset:6144
	ds_read_b32 v239, v211 offset:6656
	ds_read_b32 v240, v211 offset:7168
	ds_read_b32 v241, v211 offset:7680
	s_waitcnt lgkmcnt(0)
	v_max_f32_e32 v226, v226, v226
	v_max_f32_e32 v227, v227, v227
	v_max_f32_e32 v228, v228, v228
	v_max_f32_e32 v229, v229, v229
	v_max_f32_e32 v230, v230, v230
	v_max_f32_e32 v231, v231, v231
	v_max_f32_e32 v232, v232, v232
	v_max_f32_e32 v233, v233, v233
	v_max_f32_e32 v234, v234, v234
	v_max_f32_e32 v235, v235, v235
	v_max_f32_e32 v236, v236, v236
	v_max_f32_e32 v237, v237, v237
	v_max_f32_e32 v238, v238, v238
	v_max_f32_e32 v239, v239, v239
	v_max_f32_e32 v240, v240, v240
	v_max_f32_e32 v241, v241, v241
	v_med3_f32 v226, v226, s62, v95
	v_med3_f32 v227, v227, s62, v95
	v_med3_f32 v228, v228, s62, v95
	v_med3_f32 v229, v229, s62, v95
	v_med3_f32 v230, v230, s62, v95
	v_med3_f32 v231, v231, s62, v95
	v_med3_f32 v232, v232, s62, v95
	v_med3_f32 v233, v233, s62, v95
	v_med3_f32 v234, v234, s62, v95
	v_med3_f32 v235, v235, s62, v95
	v_med3_f32 v236, v236, s62, v95
	v_med3_f32 v237, v237, s62, v95
	v_med3_f32 v238, v238, s62, v95
	v_med3_f32 v239, v239, s62, v95
	v_med3_f32 v240, v240, s62, v95
	v_med3_f32 v241, v241, s62, v95
	v_mov_b32_e32 v242, 0
	v_mov_b32_e32 v243, 0
	v_mov_b32_e32 v244, 0
	v_mov_b32_e32 v245, 0
	v_cvt_pk_fp8_f32 v242, v226, v227
	v_cvt_pk_fp8_f32 v243, v230, v231
	v_cvt_pk_fp8_f32 v244, v234, v235
	v_cvt_pk_fp8_f32 v245, v238, v239
	v_cvt_pk_fp8_f32 v242, v228, v229 op_sel:[0,0,1]
	v_cvt_pk_fp8_f32 v243, v232, v233 op_sel:[0,0,1]
	v_cvt_pk_fp8_f32 v244, v236, v237 op_sel:[0,0,1]
	v_cvt_pk_fp8_f32 v245, v240, v241 op_sel:[0,0,1]
	s_nop 0
	global_store_dwordx4 v77, v[242:245], s[6:7]
	ds_read_b32 v226, v213
	ds_read_b32 v227, v213 offset:512
	ds_read_b32 v228, v213 offset:1024
	ds_read_b32 v229, v213 offset:1536
	ds_read_b32 v230, v213 offset:2048
	ds_read_b32 v231, v213 offset:2560
	ds_read_b32 v232, v213 offset:3072
	ds_read_b32 v233, v213 offset:3584
	ds_read_b32 v234, v213 offset:4096
	ds_read_b32 v235, v213 offset:4608
	ds_read_b32 v236, v213 offset:5120
	ds_read_b32 v237, v213 offset:5632
	ds_read_b32 v238, v213 offset:6144
	ds_read_b32 v239, v213 offset:6656
	ds_read_b32 v240, v213 offset:7168
	ds_read_b32 v241, v213 offset:7680
	s_waitcnt lgkmcnt(0)
	v_max_f32_e32 v226, v226, v226
	v_max_f32_e32 v227, v227, v227
	v_max_f32_e32 v228, v228, v228
	v_max_f32_e32 v229, v229, v229
	v_max_f32_e32 v230, v230, v230
	v_max_f32_e32 v231, v231, v231
	v_max_f32_e32 v232, v232, v232
	v_max_f32_e32 v233, v233, v233
	v_max_f32_e32 v234, v234, v234
	v_max_f32_e32 v235, v235, v235
	v_max_f32_e32 v236, v236, v236
	v_max_f32_e32 v237, v237, v237
	v_max_f32_e32 v238, v238, v238
	v_max_f32_e32 v239, v239, v239
	v_max_f32_e32 v240, v240, v240
	v_max_f32_e32 v241, v241, v241
	v_med3_f32 v226, v226, s62, v95
	v_med3_f32 v227, v227, s62, v95
	v_med3_f32 v228, v228, s62, v95
	v_med3_f32 v229, v229, s62, v95
	v_med3_f32 v230, v230, s62, v95
	v_med3_f32 v231, v231, s62, v95
	v_med3_f32 v232, v232, s62, v95
	v_med3_f32 v233, v233, s62, v95
	v_med3_f32 v234, v234, s62, v95
	v_med3_f32 v235, v235, s62, v95
	v_med3_f32 v236, v236, s62, v95
	v_med3_f32 v237, v237, s62, v95
	v_med3_f32 v238, v238, s62, v95
	v_med3_f32 v239, v239, s62, v95
	v_med3_f32 v240, v240, s62, v95
	v_med3_f32 v241, v241, s62, v95
	v_mov_b32_e32 v242, 0
	v_mov_b32_e32 v243, 0
	v_mov_b32_e32 v244, 0
	v_mov_b32_e32 v245, 0
	v_cvt_pk_fp8_f32 v242, v226, v227
	v_cvt_pk_fp8_f32 v243, v230, v231
	v_cvt_pk_fp8_f32 v244, v234, v235
	v_cvt_pk_fp8_f32 v245, v238, v239
	v_cvt_pk_fp8_f32 v242, v228, v229 op_sel:[0,0,1]
	v_cvt_pk_fp8_f32 v243, v232, v233 op_sel:[0,0,1]
	v_cvt_pk_fp8_f32 v244, v236, v237 op_sel:[0,0,1]
	v_cvt_pk_fp8_f32 v245, v240, v241 op_sel:[0,0,1]
	s_nop 0
	global_store_dwordx4 v78, v[242:245], s[6:7]
	s_waitcnt vmcnt(10)
	v_mul_f32_e32 v176, v26, v176
	v_mul_f32_e32 v177, v26, v177
	v_mul_f32_e32 v178, v26, v178
	v_mul_f32_e32 v179, v26, v179
	ds_write_b128 v210, v[176:179]
	v_mul_f32_e32 v180, v27, v180
	v_mul_f32_e32 v181, v27, v181
	v_mul_f32_e32 v182, v27, v182
	v_mul_f32_e32 v183, v27, v183
	ds_write_b128 v210, v[180:183] offset:1024
	v_mul_f32_e32 v184, v28, v184
	v_mul_f32_e32 v185, v28, v185
	v_mul_f32_e32 v186, v28, v186
	v_mul_f32_e32 v187, v28, v187
	ds_write_b128 v210, v[184:187] offset:2048
	v_mul_f32_e32 v188, v29, v188
	v_mul_f32_e32 v189, v29, v189
	v_mul_f32_e32 v190, v29, v190
	v_mul_f32_e32 v191, v29, v191
	ds_write_b128 v210, v[188:191] offset:3072
	v_mul_f32_e32 v192, v30, v192
	v_mul_f32_e32 v193, v30, v193
	v_mul_f32_e32 v194, v30, v194
	v_mul_f32_e32 v195, v30, v195
	ds_write_b128 v210, v[192:195] offset:4096
	v_mul_f32_e32 v196, v31, v196
	v_mul_f32_e32 v197, v31, v197
	v_mul_f32_e32 v198, v31, v198
	v_mul_f32_e32 v199, v31, v199
	ds_write_b128 v210, v[196:199] offset:5120
	v_mul_f32_e32 v200, v32, v200
	v_mul_f32_e32 v201, v32, v201
	v_mul_f32_e32 v202, v32, v202
	v_mul_f32_e32 v203, v32, v203
	ds_write_b128 v210, v[200:203] offset:6144
	v_mul_f32_e32 v204, v33, v204
	v_mul_f32_e32 v205, v33, v205
	v_mul_f32_e32 v206, v33, v206
	v_mul_f32_e32 v207, v33, v207
	ds_write_b128 v210, v[204:207] offset:7168
	s_waitcnt lgkmcnt(0)
	s_barrier
; #define GAS __attribute__((address_space(1)))
; #define LAS __attribute__((address_space(3)))
; #define LDS_WAIT() asm volatile("s_waitcnt lgkmcnt(0)" ::: "memory")
;     ...
; #pragma unroll
;     for (int i = 0; i < 32; ++i) v[i] = sc >= 0 ? W[(size_t)(k0 + 2 * i + (lane >> 5)) * Nsrc + sc] : 0.f;
; #pragma unroll
;     for (int i = 0; i < 32; ++i) { const int k = k0 + 2 * i + (lane >> 5); float x = v[i] * wscale; if (KS) x *= (k < ksplit ? ksA[k] : ksB[k - ksplit]); scr[(2 * i + (lane >> 5)) * 33 + (lane & 31)] = x; }
;     LDS_WAIT(); asm volatile("" ::: "memory");
;     const int c = lane & 7;
; #pragma unroll
;     for (int j = 0; j < 4; ++j) { const int n = (lane >> 3) + 8 * j; const LAS float* s = scr + (8 * c) * 33 + n;
;         const unsigned long long o = (unsigned long long)pg8::pk4_fp8(s[0 * 33], s[1 * 33], s[2 * 33], s[3 * 33]) | ((unsigned long long)pg8::pk4_fp8(s[4 * 33], s[5 * 33], s[6 * 33], s[7 * 33]) << 32);
;         *(GAS unsigned long long*)(WT + (size_t)(n0 + n) * K + k0 + 8 * c) = o; }
;     LDS_WAIT(); asm volatile("" ::: "memory");
	s_add_u32 s8, s30, 0x3000
	s_addc_u32 s9, s31, 0
	global_load_dwordx4 v[176:179], v74, s[8:9]
	s_add_u32 s8, s8, 0x20000
	s_addc_u32 s9, s9, 0
	global_load_dwordx4 v[180:183], v74, s[8:9]
	s_add_u32 s8, s8, 0x20000
	s_addc_u32 s9, s9, 0
	global_load_dwordx4 v[184:187], v74, s[8:9]
	s_add_u32 s8, s8, 0x20000
	s_addc_u32 s9, s9, 0
	global_load_dwordx4 v[188:191], v74, s[8:9]
	s_add_u32 s8, s8, 0x20000
	s_addc_u32 s9, s9, 0
	global_load_dwordx4 v[192:195], v74, s[8:9]
	s_add_u32 s8, s8, 0x20000
	s_addc_u32 s9, s9, 0
	global_load_dwordx4 v[196:199], v74, s[8:9]
	s_add_u32 s8, s8, 0x20000
	s_addc_u32 s9, s9, 0
	global_load_dwordx4 v[200:203], v74, s[8:9]
	s_add_u32 s8, s8, 0x20000
	s_addc_u32 s9, s9, 0
	global_load_dwordx4 v[204:207], v74, s[8:9]
	s_add_u32 s6, s32, 0x400000
	s_addc_u32 s7, s33, 0
	ds_read_b32 v226, v212
	ds_read_b32 v227, v212 offset:512
	ds_read_b32 v228, v212 offset:1024
	ds_read_b32 v229, v212 offset:1536
	ds_read_b32 v230, v212 offset:2048
	ds_read_b32 v231, v212 offset:2560
	ds_read_b32 v232, v212 offset:3072
	ds_read_b32 v233, v212 offset:3584
	ds_read_b32 v234, v212 offset:4096
	ds_read_b32 v235, v212 offset:4608
	ds_read_b32 v236, v212 offset:5120
	ds_read_b32 v237, v212 offset:5632
	ds_read_b32 v238, v212 offset:6144
	ds_read_b32 v239, v212 offset:6656
	ds_read_b32 v240, v212 offset:7168
	ds_read_b32 v241, v212 offset:7680
	s_waitcnt lgkmcnt(0)
	v_max_f32_e32 v226, v226, v226
	v_max_f32_e32 v227, v227, v227
	v_max_f32_e32 v228, v228, v228
	v_max_f32_e32 v229, v229, v229
	v_max_f32_e32 v230, v230, v230
	v_max_f32_e32 v231, v231, v231
	v_max_f32_e32 v232, v232, v232
	v_max_f32_e32 v233, v233, v233
	v_max_f32_e32 v234, v234, v234
	v_max_f32_e32 v235, v235, v235
	v_max_f32_e32 v236, v236, v236
	v_max_f32_e32 v237, v237, v237
	v_max_f32_e32 v238, v238, v238
	v_max_f32_e32 v239, v239, v239
	v_max_f32_e32 v240, v240, v240
	v_max_f32_e32 v241, v241, v241
	v_med3_f32 v226, v226, s62, v95
	v_med3_f32 v227, v227, s62, v95
	v_med3_f32 v228, v228, s62, v95
	v_med3_f32 v229, v229, s62, v95
	v_med3_f32 v230, v230, s62, v95
	v_med3_f32 v231, v231, s62, v95
	v_med3_f32 v232, v232, s62, v95
	v_med3_f32 v233, v233, s62, v95
	v_med3_f32 v234, v234, s62, v95
	v_med3_f32 v235, v235, s62, v95
	v_med3_f32 v236, v236, s62, v95
	v_med3_f32 v237, v237, s62, v95
	v_med3_f32 v238, v238, s62, v95
	v_med3_f32 v239, v239, s62, v95
	v_med3_f32 v240, v240, s62, v95
	v_med3_f32 v241, v241, s62, v95
	v_mov_b32_e32 v242, 0
	v_mov_b32_e32 v243, 0
	v_mov_b32_e32 v244, 0
	v_mov_b32_e32 v245, 0
	v_cvt_pk_fp8_f32 v242, v226, v227
	v_cvt_pk_fp8_f32 v243, v230, v231
	v_cvt_pk_fp8_f32 v244, v234, v235
	v_cvt_pk_fp8_f32 v245, v238, v239
	v_cvt_pk_fp8_f32 v242, v228, v229 op_sel:[0,0,1]
	v_cvt_pk_fp8_f32 v243, v232, v233 op_sel:[0,0,1]
	v_cvt_pk_fp8_f32 v244, v236, v237 op_sel:[0,0,1]
	v_cvt_pk_fp8_f32 v245, v240, v241 op_sel:[0,0,1]
	s_nop 0
	global_store_dwordx4 v77, v[242:245], s[6:7]
	ds_read_b32 v226, v214
	ds_read_b32 v227, v214 offset:512
	ds_read_b32 v228, v214 offset:1024
	ds_read_b32 v229, v214 offset:1536
	ds_read_b32 v230, v214 offset:2048
	ds_read_b32 v231, v214 offset:2560
	ds_read_b32 v232, v214 offset:3072
	ds_read_b32 v233, v214 offset:3584
	ds_read_b32 v234, v214 offset:4096
	ds_read_b32 v235, v214 offset:4608
	ds_read_b32 v236, v214 offset:5120
	ds_read_b32 v237, v214 offset:5632
	ds_read_b32 v238, v214 offset:6144
	ds_read_b32 v239, v214 offset:6656
	ds_read_b32 v240, v214 offset:7168
	ds_read_b32 v241, v214 offset:7680
	s_waitcnt lgkmcnt(0)
	v_max_f32_e32 v226, v226, v226
	v_max_f32_e32 v227, v227, v227
	v_max_f32_e32 v228, v228, v228
	v_max_f32_e32 v229, v229, v229
	v_max_f32_e32 v230, v230, v230
	v_max_f32_e32 v231, v231, v231
	v_max_f32_e32 v232, v232, v232
	v_max_f32_e32 v233, v233, v233
	v_max_f32_e32 v234, v234, v234
	v_max_f32_e32 v235, v235, v235
	v_max_f32_e32 v236, v236, v236
	v_max_f32_e32 v237, v237, v237
	v_max_f32_e32 v238, v238, v238
	v_max_f32_e32 v239, v239, v239
	v_max_f32_e32 v240, v240, v240
	v_max_f32_e32 v241, v241, v241
	v_med3_f32 v226, v226, s62, v95
	v_med3_f32 v227, v227, s62, v95
	v_med3_f32 v228, v228, s62, v95
	v_med3_f32 v229, v229, s62, v95
	v_med3_f32 v230, v230, s62, v95
	v_med3_f32 v231, v231, s62, v95
	v_med3_f32 v232, v232, s62, v95
	v_med3_f32 v233, v233, s62, v95
	v_med3_f32 v234, v234, s62, v95
	v_med3_f32 v235, v235, s62, v95
	v_med3_f32 v236, v236, s62, v95
	v_med3_f32 v237, v237, s62, v95
	v_med3_f32 v238, v238, s62, v95
	v_med3_f32 v239, v239, s62, v95
	v_med3_f32 v240, v240, s62, v95
	v_med3_f32 v241, v241, s62, v95
	v_mov_b32_e32 v242, 0
	v_mov_b32_e32 v243, 0
	v_mov_b32_e32 v244, 0
	v_mov_b32_e32 v245, 0
	v_cvt_pk_fp8_f32 v242, v226, v227
	v_cvt_pk_fp8_f32 v243, v230, v231
	v_cvt_pk_fp8_f32 v244, v234, v235
	v_cvt_pk_fp8_f32 v245, v238, v239
	v_cvt_pk_fp8_f32 v242, v228, v229 op_sel:[0,0,1]
	v_cvt_pk_fp8_f32 v243, v232, v233 op_sel:[0,0,1]
	v_cvt_pk_fp8_f32 v244, v236, v237 op_sel:[0,0,1]
	v_cvt_pk_fp8_f32 v245, v240, v241 op_sel:[0,0,1]
	s_nop 0
	global_store_dwordx4 v78, v[242:245], s[6:7]
	s_waitcnt vmcnt(12)
	v_mul_f32_e32 v144, v26, v144
	v_mul_f32_e32 v145, v26, v145
	v_mul_f32_e32 v146, v26, v146
	v_mul_f32_e32 v147, v26, v147
	ds_write_b128 v209, v[144:147]
	v_mul_f32_e32 v148, v27, v148
	v_mul_f32_e32 v149, v27, v149
	v_mul_f32_e32 v150, v27, v150
	v_mul_f32_e32 v151, v27, v151
	ds_write_b128 v209, v[148:151] offset:1024
	v_mul_f32_e32 v152, v28, v152
	v_mul_f32_e32 v153, v28, v153
	v_mul_f32_e32 v154, v28, v154
	v_mul_f32_e32 v155, v28, v155
	ds_write_b128 v209, v[152:155] offset:2048
	v_mul_f32_e32 v156, v29, v156
	v_mul_f32_e32 v157, v29, v157
	v_mul_f32_e32 v158, v29, v158
	v_mul_f32_e32 v159, v29, v159
	ds_write_b128 v209, v[156:159] offset:3072
	v_mul_f32_e32 v160, v30, v160
	v_mul_f32_e32 v161, v30, v161
	v_mul_f32_e32 v162, v30, v162
	v_mul_f32_e32 v163, v30, v163
	ds_write_b128 v209, v[160:163] offset:4096
	v_mul_f32_e32 v164, v31, v164
	v_mul_f32_e32 v165, v31, v165
	v_mul_f32_e32 v166, v31, v166
	v_mul_f32_e32 v167, v31, v167
	ds_write_b128 v209, v[164:167] offset:5120
	v_mul_f32_e32 v168, v32, v168
	v_mul_f32_e32 v169, v32, v169
	v_mul_f32_e32 v170, v32, v170
	v_mul_f32_e32 v171, v32, v171
	ds_write_b128 v209, v[168:171] offset:6144
	v_mul_f32_e32 v172, v33, v172
	v_mul_f32_e32 v173, v33, v173
	v_mul_f32_e32 v174, v33, v174
	v_mul_f32_e32 v175, v33, v175
	ds_write_b128 v209, v[172:175] offset:7168
	s_waitcnt lgkmcnt(0)
	s_barrier
; #define GAS __attribute__((address_space(1)))
; #define LAS __attribute__((address_space(3)))
; #define LDS_WAIT() asm volatile("s_waitcnt lgkmcnt(0)" ::: "memory")
;     ...
; #pragma unroll
;     for (int i = 0; i < 32; ++i) v[i] = sc >= 0 ? W[(size_t)(k0 + 2 * i + (lane >> 5)) * Nsrc + sc] : 0.f;
; #pragma unroll
;     for (int i = 0; i < 32; ++i) { const int k = k0 + 2 * i + (lane >> 5); float x = v[i] * wscale; if (KS) x *= (k < ksplit ? ksA[k] : ksB[k - ksplit]); scr[(2 * i + (lane >> 5)) * 33 + (lane & 31)] = x; }
;     LDS_WAIT(); asm volatile("" ::: "memory");
;     const int c = lane & 7;
; #pragma unroll
;     for (int j = 0; j < 4; ++j) { const int n = (lane >> 3) + 8 * j; const LAS float* s = scr + (8 * c) * 33 + n;
;         const unsigned long long o = (unsigned long long)pg8::pk4_fp8(s[0 * 33], s[1 * 33], s[2 * 33], s[3 * 33]) | ((unsigned long long)pg8::pk4_fp8(s[4 * 33], s[5 * 33], s[6 * 33], s[7 * 33]) << 32);
;         *(GAS unsigned long long*)(WT + (size_t)(n0 + n) * K + k0 + 8 * c) = o; }
;     LDS_WAIT(); asm volatile("" ::: "memory");
	s_add_u32 s8, s30, 0x4000
	s_addc_u32 s9, s31, 0
	global_load_dwordx4 v[144:147], v74, s[8:9]
	s_add_u32 s8, s8, 0x20000
	s_addc_u32 s9, s9, 0
	global_load_dwordx4 v[148:151], v74, s[8:9]
	s_add_u32 s8, s8, 0x20000
	s_addc_u32 s9, s9, 0
	global_load_dwordx4 v[152:155], v74, s[8:9]
	s_add_u32 s8, s8, 0x20000
	s_addc_u32 s9, s9, 0
	global_load_dwordx4 v[156:159], v74, s[8:9]
	s_add_u32 s8, s8, 0x20000
	s_addc_u32 s9, s9, 0
	global_load_dwordx4 v[160:163], v74, s[8:9]
	s_add_u32 s8, s8, 0x20000
	s_addc_u32 s9, s9, 0
	global_load_dwordx4 v[164:167], v74, s[8:9]
	s_add_u32 s8, s8, 0x20000
	s_addc_u32 s9, s9, 0
	global_load_dwordx4 v[168:171], v74, s[8:9]
	s_add_u32 s8, s8, 0x20000
	s_addc_u32 s9, s9, 0
	global_load_dwordx4 v[172:175], v74, s[8:9]
	s_add_u32 s6, s32, 0x800000
	s_addc_u32 s7, s33, 0
	ds_read_b32 v226, v211
	ds_read_b32 v227, v211 offset:512
	ds_read_b32 v228, v211 offset:1024
	ds_read_b32 v229, v211 offset:1536
	ds_read_b32 v230, v211 offset:2048
	ds_read_b32 v231, v211 offset:2560
	ds_read_b32 v232, v211 offset:3072
	ds_read_b32 v233, v211 offset:3584
	ds_read_b32 v234, v211 offset:4096
	ds_read_b32 v235, v211 offset:4608
	ds_read_b32 v236, v211 offset:5120
	ds_read_b32 v237, v211 offset:5632
	ds_read_b32 v238, v211 offset:6144
	ds_read_b32 v239, v211 offset:6656
	ds_read_b32 v240, v211 offset:7168
	ds_read_b32 v241, v211 offset:7680
	s_waitcnt lgkmcnt(0)
	v_max_f32_e32 v226, v226, v226
	v_max_f32_e32 v227, v227, v227
	v_max_f32_e32 v228, v228, v228
	v_max_f32_e32 v229, v229, v229
	v_max_f32_e32 v230, v230, v230
	v_max_f32_e32 v231, v231, v231
	v_max_f32_e32 v232, v232, v232
	v_max_f32_e32 v233, v233, v233
	v_max_f32_e32 v234, v234, v234
	v_max_f32_e32 v235, v235, v235
	v_max_f32_e32 v236, v236, v236
	v_max_f32_e32 v237, v237, v237
	v_max_f32_e32 v238, v238, v238
	v_max_f32_e32 v239, v239, v239
	v_max_f32_e32 v240, v240, v240
	v_max_f32_e32 v241, v241, v241
	v_med3_f32 v226, v226, s62, v95
	v_med3_f32 v227, v227, s62, v95
	v_med3_f32 v228, v228, s62, v95
	v_med3_f32 v229, v229, s62, v95
	v_med3_f32 v230, v230, s62, v95
	v_med3_f32 v231, v231, s62, v95
	v_med3_f32 v232, v232, s62, v95
	v_med3_f32 v233, v233, s62, v95
	v_med3_f32 v234, v234, s62, v95
	v_med3_f32 v235, v235, s62, v95
	v_med3_f32 v236, v236, s62, v95
	v_med3_f32 v237, v237, s62, v95
	v_med3_f32 v238, v238, s62, v95
	v_med3_f32 v239, v239, s62, v95
	v_med3_f32 v240, v240, s62, v95
	v_med3_f32 v241, v241, s62, v95
	v_mov_b32_e32 v242, 0
	v_mov_b32_e32 v243, 0
	v_mov_b32_e32 v244, 0
	v_mov_b32_e32 v245, 0
	v_cvt_pk_fp8_f32 v242, v226, v227
	v_cvt_pk_fp8_f32 v243, v230, v231
	v_cvt_pk_fp8_f32 v244, v234, v235
	v_cvt_pk_fp8_f32 v245, v238, v239
	v_cvt_pk_fp8_f32 v242, v228, v229 op_sel:[0,0,1]
	v_cvt_pk_fp8_f32 v243, v232, v233 op_sel:[0,0,1]
	v_cvt_pk_fp8_f32 v244, v236, v237 op_sel:[0,0,1]
	v_cvt_pk_fp8_f32 v245, v240, v241 op_sel:[0,0,1]
	s_nop 0
	global_store_dwordx4 v77, v[242:245], s[6:7]
	ds_read_b32 v226, v213
	ds_read_b32 v227, v213 offset:512
	ds_read_b32 v228, v213 offset:1024
	ds_read_b32 v229, v213 offset:1536
	ds_read_b32 v230, v213 offset:2048
	ds_read_b32 v231, v213 offset:2560
	ds_read_b32 v232, v213 offset:3072
	ds_read_b32 v233, v213 offset:3584
	ds_read_b32 v234, v213 offset:4096
	ds_read_b32 v235, v213 offset:4608
	ds_read_b32 v236, v213 offset:5120
	ds_read_b32 v237, v213 offset:5632
	ds_read_b32 v238, v213 offset:6144
	ds_read_b32 v239, v213 offset:6656
	ds_read_b32 v240, v213 offset:7168
	ds_read_b32 v241, v213 offset:7680
	s_waitcnt lgkmcnt(0)
	v_max_f32_e32 v226, v226, v226
	v_max_f32_e32 v227, v227, v227
	v_max_f32_e32 v228, v228, v228
	v_max_f32_e32 v229, v229, v229
	v_max_f32_e32 v230, v230, v230
	v_max_f32_e32 v231, v231, v231
	v_max_f32_e32 v232, v232, v232
	v_max_f32_e32 v233, v233, v233
	v_max_f32_e32 v234, v234, v234
	v_max_f32_e32 v235, v235, v235
	v_max_f32_e32 v236, v236, v236
	v_max_f32_e32 v237, v237, v237
	v_max_f32_e32 v238, v238, v238
	v_max_f32_e32 v239, v239, v239
	v_max_f32_e32 v240, v240, v240
	v_max_f32_e32 v241, v241, v241
	v_med3_f32 v226, v226, s62, v95
	v_med3_f32 v227, v227, s62, v95
	v_med3_f32 v228, v228, s62, v95
	v_med3_f32 v229, v229, s62, v95
	v_med3_f32 v230, v230, s62, v95
	v_med3_f32 v231, v231, s62, v95
	v_med3_f32 v232, v232, s62, v95
	v_med3_f32 v233, v233, s62, v95
	v_med3_f32 v234, v234, s62, v95
	v_med3_f32 v235, v235, s62, v95
	v_med3_f32 v236, v236, s62, v95
	v_med3_f32 v237, v237, s62, v95
	v_med3_f32 v238, v238, s62, v95
	v_med3_f32 v239, v239, s62, v95
	v_med3_f32 v240, v240, s62, v95
	v_med3_f32 v241, v241, s62, v95
	v_mov_b32_e32 v242, 0
	v_mov_b32_e32 v243, 0
	v_mov_b32_e32 v244, 0
	v_mov_b32_e32 v245, 0
	v_cvt_pk_fp8_f32 v242, v226, v227
	v_cvt_pk_fp8_f32 v243, v230, v231
	v_cvt_pk_fp8_f32 v244, v234, v235
	v_cvt_pk_fp8_f32 v245, v238, v239
	v_cvt_pk_fp8_f32 v242, v228, v229 op_sel:[0,0,1]
	v_cvt_pk_fp8_f32 v243, v232, v233 op_sel:[0,0,1]
	v_cvt_pk_fp8_f32 v244, v236, v237 op_sel:[0,0,1]
	v_cvt_pk_fp8_f32 v245, v240, v241 op_sel:[0,0,1]
	s_nop 0
	global_store_dwordx4 v78, v[242:245], s[6:7]
	s_waitcnt vmcnt(12)
	v_mul_f32_e32 v176, v26, v176
	v_mul_f32_e32 v177, v26, v177
	v_mul_f32_e32 v178, v26, v178
	v_mul_f32_e32 v179, v26, v179
	ds_write_b128 v210, v[176:179]
	v_mul_f32_e32 v180, v27, v180
	v_mul_f32_e32 v181, v27, v181
	v_mul_f32_e32 v182, v27, v182
	v_mul_f32_e32 v183, v27, v183
	ds_write_b128 v210, v[180:183] offset:1024
	v_mul_f32_e32 v184, v28, v184
	v_mul_f32_e32 v185, v28, v185
	v_mul_f32_e32 v186, v28, v186
	v_mul_f32_e32 v187, v28, v187
	ds_write_b128 v210, v[184:187] offset:2048
	v_mul_f32_e32 v188, v29, v188
	v_mul_f32_e32 v189, v29, v189
	v_mul_f32_e32 v190, v29, v190
	v_mul_f32_e32 v191, v29, v191
	ds_write_b128 v210, v[188:191] offset:3072
	v_mul_f32_e32 v192, v30, v192
	v_mul_f32_e32 v193, v30, v193
	v_mul_f32_e32 v194, v30, v194
	v_mul_f32_e32 v195, v30, v195
	ds_write_b128 v210, v[192:195] offset:4096
	v_mul_f32_e32 v196, v31, v196
	v_mul_f32_e32 v197, v31, v197
	v_mul_f32_e32 v198, v31, v198
	v_mul_f32_e32 v199, v31, v199
	ds_write_b128 v210, v[196:199] offset:5120
	v_mul_f32_e32 v200, v32, v200
	v_mul_f32_e32 v201, v32, v201
	v_mul_f32_e32 v202, v32, v202
	v_mul_f32_e32 v203, v32, v203
	ds_write_b128 v210, v[200:203] offset:6144
	v_mul_f32_e32 v204, v33, v204
	v_mul_f32_e32 v205, v33, v205
	v_mul_f32_e32 v206, v33, v206
	v_mul_f32_e32 v207, v33, v207
	ds_write_b128 v210, v[204:207] offset:7168
	s_waitcnt lgkmcnt(0)
	s_barrier
; #define GAS __attribute__((address_space(1)))
; #define LAS __attribute__((address_space(3)))
; #define LDS_WAIT() asm volatile("s_waitcnt lgkmcnt(0)" ::: "memory")
;     ...
; #pragma unroll
;     for (int i = 0; i < 32; ++i) v[i] = sc >= 0 ? W[(size_t)(k0 + 2 * i + (lane >> 5)) * Nsrc + sc] : 0.f;
; #pragma unroll
;     for (int i = 0; i < 32; ++i) { const int k = k0 + 2 * i + (lane >> 5); float x = v[i] * wscale; if (KS) x *= (k < ksplit ? ksA[k] : ksB[k - ksplit]); scr[(2 * i + (lane >> 5)) * 33 + (lane & 31)] = x; }
;     LDS_WAIT(); asm volatile("" ::: "memory");
;     const int c = lane & 7;
; #pragma unroll
;     for (int j = 0; j < 4; ++j) { const int n = (lane >> 3) + 8 * j; const LAS float* s = scr + (8 * c) * 33 + n;
;         const unsigned long long o = (unsigned long long)pg8::pk4_fp8(s[0 * 33], s[1 * 33], s[2 * 33], s[3 * 33]) | ((unsigned long long)pg8::pk4_fp8(s[4 * 33], s[5 * 33], s[6 * 33], s[7 * 33]) << 32);
;         *(GAS unsigned long long*)(WT + (size_t)(n0 + n) * K + k0 + 8 * c) = o; }
;     LDS_WAIT(); asm volatile("" ::: "memory");
	s_add_u32 s8, s30, 0x5000
	s_addc_u32 s9, s31, 0
	global_load_dwordx4 v[176:179], v74, s[8:9]
	s_add_u32 s8, s8, 0x20000
	s_addc_u32 s9, s9, 0
	global_load_dwordx4 v[180:183], v74, s[8:9]
	s_add_u32 s8, s8, 0x20000
	s_addc_u32 s9, s9, 0
	global_load_dwordx4 v[184:187], v74, s[8:9]
	s_add_u32 s8, s8, 0x20000
	s_addc_u32 s9, s9, 0
	global_load_dwordx4 v[188:191], v74, s[8:9]
	s_add_u32 s8, s8, 0x20000
	s_addc_u32 s9, s9, 0
	global_load_dwordx4 v[192:195], v74, s[8:9]
	s_add_u32 s8, s8, 0x20000
	s_addc_u32 s9, s9, 0
	global_load_dwordx4 v[196:199], v74, s[8:9]
	s_add_u32 s8, s8, 0x20000
	s_addc_u32 s9, s9, 0
	global_load_dwordx4 v[200:203], v74, s[8:9]
	s_add_u32 s8, s8, 0x20000
	s_addc_u32 s9, s9, 0
	global_load_dwordx4 v[204:207], v74, s[8:9]
	s_add_u32 s6, s32, 0xc00000
	s_addc_u32 s7, s33, 0
	ds_read_b32 v226, v212
	ds_read_b32 v227, v212 offset:512
	ds_read_b32 v228, v212 offset:1024
	ds_read_b32 v229, v212 offset:1536
	ds_read_b32 v230, v212 offset:2048
	ds_read_b32 v231, v212 offset:2560
	ds_read_b32 v232, v212 offset:3072
	ds_read_b32 v233, v212 offset:3584
	ds_read_b32 v234, v212 offset:4096
	ds_read_b32 v235, v212 offset:4608
	ds_read_b32 v236, v212 offset:5120
	ds_read_b32 v237, v212 offset:5632
	ds_read_b32 v238, v212 offset:6144
	ds_read_b32 v239, v212 offset:6656
	ds_read_b32 v240, v212 offset:7168
	ds_read_b32 v241, v212 offset:7680
	s_waitcnt lgkmcnt(0)
	v_max_f32_e32 v226, v226, v226
	v_max_f32_e32 v227, v227, v227
	v_max_f32_e32 v228, v228, v228
	v_max_f32_e32 v229, v229, v229
	v_max_f32_e32 v230, v230, v230
	v_max_f32_e32 v231, v231, v231
	v_max_f32_e32 v232, v232, v232
	v_max_f32_e32 v233, v233, v233
	v_max_f32_e32 v234, v234, v234
	v_max_f32_e32 v235, v235, v235
	v_max_f32_e32 v236, v236, v236
	v_max_f32_e32 v237, v237, v237
	v_max_f32_e32 v238, v238, v238
	v_max_f32_e32 v239, v239, v239
	v_max_f32_e32 v240, v240, v240
	v_max_f32_e32 v241, v241, v241
	v_med3_f32 v226, v226, s62, v95
	v_med3_f32 v227, v227, s62, v95
	v_med3_f32 v228, v228, s62, v95
	v_med3_f32 v229, v229, s62, v95
	v_med3_f32 v230, v230, s62, v95
	v_med3_f32 v231, v231, s62, v95
	v_med3_f32 v232, v232, s62, v95
	v_med3_f32 v233, v233, s62, v95
	v_med3_f32 v234, v234, s62, v95
	v_med3_f32 v235, v235, s62, v95
	v_med3_f32 v236, v236, s62, v95
	v_med3_f32 v237, v237, s62, v95
	v_med3_f32 v238, v238, s62, v95
	v_med3_f32 v239, v239, s62, v95
	v_med3_f32 v240, v240, s62, v95
	v_med3_f32 v241, v241, s62, v95
	v_mov_b32_e32 v242, 0
	v_mov_b32_e32 v243, 0
	v_mov_b32_e32 v244, 0
	v_mov_b32_e32 v245, 0
	v_cvt_pk_fp8_f32 v242, v226, v227
	v_cvt_pk_fp8_f32 v243, v230, v231
	v_cvt_pk_fp8_f32 v244, v234, v235
	v_cvt_pk_fp8_f32 v245, v238, v239
	v_cvt_pk_fp8_f32 v242, v228, v229 op_sel:[0,0,1]
	v_cvt_pk_fp8_f32 v243, v232, v233 op_sel:[0,0,1]
	v_cvt_pk_fp8_f32 v244, v236, v237 op_sel:[0,0,1]
	v_cvt_pk_fp8_f32 v245, v240, v241 op_sel:[0,0,1]
	s_nop 0
	global_store_dwordx4 v77, v[242:245], s[6:7]
	ds_read_b32 v226, v214
	ds_read_b32 v227, v214 offset:512
	ds_read_b32 v228, v214 offset:1024
	ds_read_b32 v229, v214 offset:1536
	ds_read_b32 v230, v214 offset:2048
	ds_read_b32 v231, v214 offset:2560
	ds_read_b32 v232, v214 offset:3072
	ds_read_b32 v233, v214 offset:3584
	ds_read_b32 v234, v214 offset:4096
	ds_read_b32 v235, v214 offset:4608
	ds_read_b32 v236, v214 offset:5120
	ds_read_b32 v237, v214 offset:5632
	ds_read_b32 v238, v214 offset:6144
	ds_read_b32 v239, v214 offset:6656
	ds_read_b32 v240, v214 offset:7168
	ds_read_b32 v241, v214 offset:7680
	s_waitcnt lgkmcnt(0)
	v_max_f32_e32 v226, v226, v226
	v_max_f32_e32 v227, v227, v227
	v_max_f32_e32 v228, v228, v228
	v_max_f32_e32 v229, v229, v229
	v_max_f32_e32 v230, v230, v230
	v_max_f32_e32 v231, v231, v231
	v_max_f32_e32 v232, v232, v232
	v_max_f32_e32 v233, v233, v233
	v_max_f32_e32 v234, v234, v234
	v_max_f32_e32 v235, v235, v235
	v_max_f32_e32 v236, v236, v236
	v_max_f32_e32 v237, v237, v237
	v_max_f32_e32 v238, v238, v238
	v_max_f32_e32 v239, v239, v239
	v_max_f32_e32 v240, v240, v240
	v_max_f32_e32 v241, v241, v241
	v_med3_f32 v226, v226, s62, v95
	v_med3_f32 v227, v227, s62, v95
	v_med3_f32 v228, v228, s62, v95
	v_med3_f32 v229, v229, s62, v95
	v_med3_f32 v230, v230, s62, v95
	v_med3_f32 v231, v231, s62, v95
	v_med3_f32 v232, v232, s62, v95
	v_med3_f32 v233, v233, s62, v95
	v_med3_f32 v234, v234, s62, v95
	v_med3_f32 v235, v235, s62, v95
	v_med3_f32 v236, v236, s62, v95
	v_med3_f32 v237, v237, s62, v95
	v_med3_f32 v238, v238, s62, v95
	v_med3_f32 v239, v239, s62, v95
	v_med3_f32 v240, v240, s62, v95
	v_med3_f32 v241, v241, s62, v95
	v_mov_b32_e32 v242, 0
	v_mov_b32_e32 v243, 0
	v_mov_b32_e32 v244, 0
	v_mov_b32_e32 v245, 0
	v_cvt_pk_fp8_f32 v242, v226, v227
	v_cvt_pk_fp8_f32 v243, v230, v231
	v_cvt_pk_fp8_f32 v244, v234, v235
	v_cvt_pk_fp8_f32 v245, v238, v239
	v_cvt_pk_fp8_f32 v242, v228, v229 op_sel:[0,0,1]
	v_cvt_pk_fp8_f32 v243, v232, v233 op_sel:[0,0,1]
	v_cvt_pk_fp8_f32 v244, v236, v237 op_sel:[0,0,1]
	v_cvt_pk_fp8_f32 v245, v240, v241 op_sel:[0,0,1]
	s_nop 0
	global_store_dwordx4 v78, v[242:245], s[6:7]
	s_waitcnt vmcnt(12)
	v_mul_f32_e32 v144, v26, v144
	v_mul_f32_e32 v145, v26, v145
	v_mul_f32_e32 v146, v26, v146
	v_mul_f32_e32 v147, v26, v147
	ds_write_b128 v209, v[144:147]
	v_mul_f32_e32 v148, v27, v148
	v_mul_f32_e32 v149, v27, v149
	v_mul_f32_e32 v150, v27, v150
	v_mul_f32_e32 v151, v27, v151
	ds_write_b128 v209, v[148:151] offset:1024
	v_mul_f32_e32 v152, v28, v152
	v_mul_f32_e32 v153, v28, v153
	v_mul_f32_e32 v154, v28, v154
	v_mul_f32_e32 v155, v28, v155
	ds_write_b128 v209, v[152:155] offset:2048
	v_mul_f32_e32 v156, v29, v156
	v_mul_f32_e32 v157, v29, v157
	v_mul_f32_e32 v158, v29, v158
	v_mul_f32_e32 v159, v29, v159
	ds_write_b128 v209, v[156:159] offset:3072
	v_mul_f32_e32 v160, v30, v160
	v_mul_f32_e32 v161, v30, v161
	v_mul_f32_e32 v162, v30, v162
	v_mul_f32_e32 v163, v30, v163
	ds_write_b128 v209, v[160:163] offset:4096
	v_mul_f32_e32 v164, v31, v164
	v_mul_f32_e32 v165, v31, v165
	v_mul_f32_e32 v166, v31, v166
	v_mul_f32_e32 v167, v31, v167
	ds_write_b128 v209, v[164:167] offset:5120
	v_mul_f32_e32 v168, v32, v168
	v_mul_f32_e32 v169, v32, v169
	v_mul_f32_e32 v170, v32, v170
	v_mul_f32_e32 v171, v32, v171
	ds_write_b128 v209, v[168:171] offset:6144
	v_mul_f32_e32 v172, v33, v172
	v_mul_f32_e32 v173, v33, v173
	v_mul_f32_e32 v174, v33, v174
	v_mul_f32_e32 v175, v33, v175
	ds_write_b128 v209, v[172:175] offset:7168
	s_waitcnt lgkmcnt(0)
	s_barrier
; #define GAS __attribute__((address_space(1)))
; #define LAS __attribute__((address_space(3)))
; #define LDS_WAIT() asm volatile("s_waitcnt lgkmcnt(0)" ::: "memory")
;     ...
; #pragma unroll
;     for (int i = 0; i < 32; ++i) v[i] = sc >= 0 ? W[(size_t)(k0 + 2 * i + (lane >> 5)) * Nsrc + sc] : 0.f;
; #pragma unroll
;     for (int i = 0; i < 32; ++i) { const int k = k0 + 2 * i + (lane >> 5); float x = v[i] * wscale; if (KS) x *= (k < ksplit ? ksA[k] : ksB[k - ksplit]); scr[(2 * i + (lane >> 5)) * 33 + (lane & 31)] = x; }
;     LDS_WAIT(); asm volatile("" ::: "memory");
;     const int c = lane & 7;
; #pragma unroll
;     for (int j = 0; j < 4; ++j) { const int n = (lane >> 3) + 8 * j; const LAS float* s = scr + (8 * c) * 33 + n;
;         const unsigned long long o = (unsigned long long)pg8::pk4_fp8(s[0 * 33], s[1 * 33], s[2 * 33], s[3 * 33]) | ((unsigned long long)pg8::pk4_fp8(s[4 * 33], s[5 * 33], s[6 * 33], s[7 * 33]) << 32);
;         *(GAS unsigned long long*)(WT + (size_t)(n0 + n) * K + k0 + 8 * c) = o; }
;     LDS_WAIT(); asm volatile("" ::: "memory");
	s_add_u32 s8, s30, 0x6000
	s_addc_u32 s9, s31, 0
	global_load_dwordx4 v[144:147], v74, s[8:9]
	s_add_u32 s8, s8, 0x20000
	s_addc_u32 s9, s9, 0
	global_load_dwordx4 v[148:151], v74, s[8:9]
	s_add_u32 s8, s8, 0x20000
	s_addc_u32 s9, s9, 0
	global_load_dwordx4 v[152:155], v74, s[8:9]
	s_add_u32 s8, s8, 0x20000
	s_addc_u32 s9, s9, 0
	global_load_dwordx4 v[156:159], v74, s[8:9]
	s_add_u32 s8, s8, 0x20000
	s_addc_u32 s9, s9, 0
	global_load_dwordx4 v[160:163], v74, s[8:9]
	s_add_u32 s8, s8, 0x20000
	s_addc_u32 s9, s9, 0
	global_load_dwordx4 v[164:167], v74, s[8:9]
	s_add_u32 s8, s8, 0x20000
	s_addc_u32 s9, s9, 0
	global_load_dwordx4 v[168:171], v74, s[8:9]
	s_add_u32 s8, s8, 0x20000
	s_addc_u32 s9, s9, 0
	global_load_dwordx4 v[172:175], v74, s[8:9]
	s_add_u32 s6, s32, 0x1000000
	s_addc_u32 s7, s33, 0
	ds_read_b32 v226, v211
	ds_read_b32 v227, v211 offset:512
	ds_read_b32 v228, v211 offset:1024
	ds_read_b32 v229, v211 offset:1536
	ds_read_b32 v230, v211 offset:2048
	ds_read_b32 v231, v211 offset:2560
	ds_read_b32 v232, v211 offset:3072
	ds_read_b32 v233, v211 offset:3584
	ds_read_b32 v234, v211 offset:4096
	ds_read_b32 v235, v211 offset:4608
	ds_read_b32 v236, v211 offset:5120
	ds_read_b32 v237, v211 offset:5632
	ds_read_b32 v238, v211 offset:6144
	ds_read_b32 v239, v211 offset:6656
	ds_read_b32 v240, v211 offset:7168
	ds_read_b32 v241, v211 offset:7680
	s_waitcnt lgkmcnt(0)
	v_max_f32_e32 v226, v226, v226
	v_max_f32_e32 v227, v227, v227
	v_max_f32_e32 v228, v228, v228
	v_max_f32_e32 v229, v229, v229
	v_max_f32_e32 v230, v230, v230
	v_max_f32_e32 v231, v231, v231
	v_max_f32_e32 v232, v232, v232
	v_max_f32_e32 v233, v233, v233
	v_max_f32_e32 v234, v234, v234
	v_max_f32_e32 v235, v235, v235
	v_max_f32_e32 v236, v236, v236
	v_max_f32_e32 v237, v237, v237
	v_max_f32_e32 v238, v238, v238
	v_max_f32_e32 v239, v239, v239
	v_max_f32_e32 v240, v240, v240
	v_max_f32_e32 v241, v241, v241
	v_med3_f32 v226, v226, s62, v95
	v_med3_f32 v227, v227, s62, v95
	v_med3_f32 v228, v228, s62, v95
	v_med3_f32 v229, v229, s62, v95
	v_med3_f32 v230, v230, s62, v95
	v_med3_f32 v231, v231, s62, v95
	v_med3_f32 v232, v232, s62, v95
	v_med3_f32 v233, v233, s62, v95
	v_med3_f32 v234, v234, s62, v95
	v_med3_f32 v235, v235, s62, v95
	v_med3_f32 v236, v236, s62, v95
	v_med3_f32 v237, v237, s62, v95
	v_med3_f32 v238, v238, s62, v95
	v_med3_f32 v239, v239, s62, v95
	v_med3_f32 v240, v240, s62, v95
	v_med3_f32 v241, v241, s62, v95
	v_mov_b32_e32 v242, 0
	v_mov_b32_e32 v243, 0
	v_mov_b32_e32 v244, 0
	v_mov_b32_e32 v245, 0
	v_cvt_pk_fp8_f32 v242, v226, v227
	v_cvt_pk_fp8_f32 v243, v230, v231
	v_cvt_pk_fp8_f32 v244, v234, v235
	v_cvt_pk_fp8_f32 v245, v238, v239
	v_cvt_pk_fp8_f32 v242, v228, v229 op_sel:[0,0,1]
	v_cvt_pk_fp8_f32 v243, v232, v233 op_sel:[0,0,1]
	v_cvt_pk_fp8_f32 v244, v236, v237 op_sel:[0,0,1]
	v_cvt_pk_fp8_f32 v245, v240, v241 op_sel:[0,0,1]
	s_nop 0
	global_store_dwordx4 v77, v[242:245], s[6:7]
	ds_read_b32 v226, v213
	ds_read_b32 v227, v213 offset:512
	ds_read_b32 v228, v213 offset:1024
	ds_read_b32 v229, v213 offset:1536
	ds_read_b32 v230, v213 offset:2048
	ds_read_b32 v231, v213 offset:2560
	ds_read_b32 v232, v213 offset:3072
	ds_read_b32 v233, v213 offset:3584
	ds_read_b32 v234, v213 offset:4096
	ds_read_b32 v235, v213 offset:4608
	ds_read_b32 v236, v213 offset:5120
	ds_read_b32 v237, v213 offset:5632
	ds_read_b32 v238, v213 offset:6144
	ds_read_b32 v239, v213 offset:6656
	ds_read_b32 v240, v213 offset:7168
	ds_read_b32 v241, v213 offset:7680
	s_waitcnt lgkmcnt(0)
	v_max_f32_e32 v226, v226, v226
	v_max_f32_e32 v227, v227, v227
	v_max_f32_e32 v228, v228, v228
	v_max_f32_e32 v229, v229, v229
	v_max_f32_e32 v230, v230, v230
	v_max_f32_e32 v231, v231, v231
	v_max_f32_e32 v232, v232, v232
	v_max_f32_e32 v233, v233, v233
	v_max_f32_e32 v234, v234, v234
	v_max_f32_e32 v235, v235, v235
	v_max_f32_e32 v236, v236, v236
	v_max_f32_e32 v237, v237, v237
	v_max_f32_e32 v238, v238, v238
	v_max_f32_e32 v239, v239, v239
	v_max_f32_e32 v240, v240, v240
	v_max_f32_e32 v241, v241, v241
	v_med3_f32 v226, v226, s62, v95
	v_med3_f32 v227, v227, s62, v95
	v_med3_f32 v228, v228, s62, v95
	v_med3_f32 v229, v229, s62, v95
	v_med3_f32 v230, v230, s62, v95
	v_med3_f32 v231, v231, s62, v95
	v_med3_f32 v232, v232, s62, v95
	v_med3_f32 v233, v233, s62, v95
	v_med3_f32 v234, v234, s62, v95
	v_med3_f32 v235, v235, s62, v95
	v_med3_f32 v236, v236, s62, v95
	v_med3_f32 v237, v237, s62, v95
	v_med3_f32 v238, v238, s62, v95
	v_med3_f32 v239, v239, s62, v95
	v_med3_f32 v240, v240, s62, v95
	v_med3_f32 v241, v241, s62, v95
	v_mov_b32_e32 v242, 0
	v_mov_b32_e32 v243, 0
	v_mov_b32_e32 v244, 0
	v_mov_b32_e32 v245, 0
	v_cvt_pk_fp8_f32 v242, v226, v227
	v_cvt_pk_fp8_f32 v243, v230, v231
	v_cvt_pk_fp8_f32 v244, v234, v235
	v_cvt_pk_fp8_f32 v245, v238, v239
	v_cvt_pk_fp8_f32 v242, v228, v229 op_sel:[0,0,1]
	v_cvt_pk_fp8_f32 v243, v232, v233 op_sel:[0,0,1]
	v_cvt_pk_fp8_f32 v244, v236, v237 op_sel:[0,0,1]
	v_cvt_pk_fp8_f32 v245, v240, v241 op_sel:[0,0,1]
	s_nop 0
	global_store_dwordx4 v78, v[242:245], s[6:7]
	s_waitcnt vmcnt(12)
	v_mul_f32_e32 v176, v26, v176
	v_mul_f32_e32 v177, v26, v177
	v_mul_f32_e32 v178, v26, v178
	v_mul_f32_e32 v179, v26, v179
	ds_write_b128 v210, v[176:179]
	v_mul_f32_e32 v180, v27, v180
	v_mul_f32_e32 v181, v27, v181
	v_mul_f32_e32 v182, v27, v182
	v_mul_f32_e32 v183, v27, v183
	ds_write_b128 v210, v[180:183] offset:1024
	v_mul_f32_e32 v184, v28, v184
	v_mul_f32_e32 v185, v28, v185
	v_mul_f32_e32 v186, v28, v186
	v_mul_f32_e32 v187, v28, v187
	ds_write_b128 v210, v[184:187] offset:2048
	v_mul_f32_e32 v188, v29, v188
	v_mul_f32_e32 v189, v29, v189
	v_mul_f32_e32 v190, v29, v190
	v_mul_f32_e32 v191, v29, v191
	ds_write_b128 v210, v[188:191] offset:3072
	v_mul_f32_e32 v192, v30, v192
	v_mul_f32_e32 v193, v30, v193
	v_mul_f32_e32 v194, v30, v194
	v_mul_f32_e32 v195, v30, v195
	ds_write_b128 v210, v[192:195] offset:4096
	v_mul_f32_e32 v196, v31, v196
	v_mul_f32_e32 v197, v31, v197
	v_mul_f32_e32 v198, v31, v198
	v_mul_f32_e32 v199, v31, v199
	ds_write_b128 v210, v[196:199] offset:5120
	v_mul_f32_e32 v200, v32, v200
	v_mul_f32_e32 v201, v32, v201
	v_mul_f32_e32 v202, v32, v202
	v_mul_f32_e32 v203, v32, v203
	ds_write_b128 v210, v[200:203] offset:6144
	v_mul_f32_e32 v204, v33, v204
	v_mul_f32_e32 v205, v33, v205
	v_mul_f32_e32 v206, v33, v206
	v_mul_f32_e32 v207, v33, v207
	ds_write_b128 v210, v[204:207] offset:7168
	s_waitcnt lgkmcnt(0)
	s_barrier
; #define GAS __attribute__((address_space(1)))
; #define LAS __attribute__((address_space(3)))
; #define LDS_WAIT() asm volatile("s_waitcnt lgkmcnt(0)" ::: "memory")
;     ...
; #pragma unroll
;     for (int i = 0; i < 32; ++i) v[i] = sc >= 0 ? W[(size_t)(k0 + 2 * i + (lane >> 5)) * Nsrc + sc] : 0.f;
; #pragma unroll
;     for (int i = 0; i < 32; ++i) { const int k = k0 + 2 * i + (lane >> 5); float x = v[i] * wscale; if (KS) x *= (k < ksplit ? ksA[k] : ksB[k - ksplit]); scr[(2 * i + (lane >> 5)) * 33 + (lane & 31)] = x; }
;     LDS_WAIT(); asm volatile("" ::: "memory");
;     const int c = lane & 7;
; #pragma unroll
;     for (int j = 0; j < 4; ++j) { const int n = (lane >> 3) + 8 * j; const LAS float* s = scr + (8 * c) * 33 + n;
;         const unsigned long long o = (unsigned long long)pg8::pk4_fp8(s[0 * 33], s[1 * 33], s[2 * 33], s[3 * 33]) | ((unsigned long long)pg8::pk4_fp8(s[4 * 33], s[5 * 33], s[6 * 33], s[7 * 33]) << 32);
;         *(GAS unsigned long long*)(WT + (size_t)(n0 + n) * K + k0 + 8 * c) = o; }
;     LDS_WAIT(); asm volatile("" ::: "memory");
	s_add_u32 s8, s30, 0x7000
	s_addc_u32 s9, s31, 0
	global_load_dwordx4 v[176:179], v74, s[8:9]
	s_add_u32 s8, s8, 0x20000
	s_addc_u32 s9, s9, 0
	global_load_dwordx4 v[180:183], v74, s[8:9]
	s_add_u32 s8, s8, 0x20000
	s_addc_u32 s9, s9, 0
	global_load_dwordx4 v[184:187], v74, s[8:9]
	s_add_u32 s8, s8, 0x20000
	s_addc_u32 s9, s9, 0
	global_load_dwordx4 v[188:191], v74, s[8:9]
	s_add_u32 s8, s8, 0x20000
	s_addc_u32 s9, s9, 0
	global_load_dwordx4 v[192:195], v74, s[8:9]
	s_add_u32 s8, s8, 0x20000
	s_addc_u32 s9, s9, 0
	global_load_dwordx4 v[196:199], v74, s[8:9]
	s_add_u32 s8, s8, 0x20000
	s_addc_u32 s9, s9, 0
	global_load_dwordx4 v[200:203], v74, s[8:9]
	s_add_u32 s8, s8, 0x20000
	s_addc_u32 s9, s9, 0
	global_load_dwordx4 v[204:207], v74, s[8:9]
	s_add_u32 s6, s32, 0x1400000
	s_addc_u32 s7, s33, 0
	ds_read_b32 v226, v212
	ds_read_b32 v227, v212 offset:512
	ds_read_b32 v228, v212 offset:1024
	ds_read_b32 v229, v212 offset:1536
	ds_read_b32 v230, v212 offset:2048
	ds_read_b32 v231, v212 offset:2560
	ds_read_b32 v232, v212 offset:3072
	ds_read_b32 v233, v212 offset:3584
	ds_read_b32 v234, v212 offset:4096
	ds_read_b32 v235, v212 offset:4608
	ds_read_b32 v236, v212 offset:5120
	ds_read_b32 v237, v212 offset:5632
	ds_read_b32 v238, v212 offset:6144
	ds_read_b32 v239, v212 offset:6656
	ds_read_b32 v240, v212 offset:7168
	ds_read_b32 v241, v212 offset:7680
	s_waitcnt lgkmcnt(0)
	v_max_f32_e32 v226, v226, v226
	v_max_f32_e32 v227, v227, v227
	v_max_f32_e32 v228, v228, v228
	v_max_f32_e32 v229, v229, v229
	v_max_f32_e32 v230, v230, v230
	v_max_f32_e32 v231, v231, v231
	v_max_f32_e32 v232, v232, v232
	v_max_f32_e32 v233, v233, v233
	v_max_f32_e32 v234, v234, v234
	v_max_f32_e32 v235, v235, v235
	v_max_f32_e32 v236, v236, v236
	v_max_f32_e32 v237, v237, v237
	v_max_f32_e32 v238, v238, v238
	v_max_f32_e32 v239, v239, v239
	v_max_f32_e32 v240, v240, v240
	v_max_f32_e32 v241, v241, v241
	v_med3_f32 v226, v226, s62, v95
	v_med3_f32 v227, v227, s62, v95
	v_med3_f32 v228, v228, s62, v95
	v_med3_f32 v229, v229, s62, v95
	v_med3_f32 v230, v230, s62, v95
	v_med3_f32 v231, v231, s62, v95
	v_med3_f32 v232, v232, s62, v95
	v_med3_f32 v233, v233, s62, v95
	v_med3_f32 v234, v234, s62, v95
	v_med3_f32 v235, v235, s62, v95
	v_med3_f32 v236, v236, s62, v95
	v_med3_f32 v237, v237, s62, v95
	v_med3_f32 v238, v238, s62, v95
	v_med3_f32 v239, v239, s62, v95
	v_med3_f32 v240, v240, s62, v95
	v_med3_f32 v241, v241, s62, v95
	v_mov_b32_e32 v242, 0
	v_mov_b32_e32 v243, 0
	v_mov_b32_e32 v244, 0
	v_mov_b32_e32 v245, 0
	v_cvt_pk_fp8_f32 v242, v226, v227
	v_cvt_pk_fp8_f32 v243, v230, v231
	v_cvt_pk_fp8_f32 v244, v234, v235
	v_cvt_pk_fp8_f32 v245, v238, v239
	v_cvt_pk_fp8_f32 v242, v228, v229 op_sel:[0,0,1]
	v_cvt_pk_fp8_f32 v243, v232, v233 op_sel:[0,0,1]
	v_cvt_pk_fp8_f32 v244, v236, v237 op_sel:[0,0,1]
	v_cvt_pk_fp8_f32 v245, v240, v241 op_sel:[0,0,1]
	s_nop 0
	global_store_dwordx4 v77, v[242:245], s[6:7]
	ds_read_b32 v226, v214
	ds_read_b32 v227, v214 offset:512
	ds_read_b32 v228, v214 offset:1024
	ds_read_b32 v229, v214 offset:1536
	ds_read_b32 v230, v214 offset:2048
	ds_read_b32 v231, v214 offset:2560
	ds_read_b32 v232, v214 offset:3072
	ds_read_b32 v233, v214 offset:3584
	ds_read_b32 v234, v214 offset:4096
	ds_read_b32 v235, v214 offset:4608
	ds_read_b32 v236, v214 offset:5120
	ds_read_b32 v237, v214 offset:5632
	ds_read_b32 v238, v214 offset:6144
	ds_read_b32 v239, v214 offset:6656
	ds_read_b32 v240, v214 offset:7168
	ds_read_b32 v241, v214 offset:7680
	s_waitcnt lgkmcnt(0)
	v_max_f32_e32 v226, v226, v226
	v_max_f32_e32 v227, v227, v227
	v_max_f32_e32 v228, v228, v228
	v_max_f32_e32 v229, v229, v229
	v_max_f32_e32 v230, v230, v230
	v_max_f32_e32 v231, v231, v231
	v_max_f32_e32 v232, v232, v232
	v_max_f32_e32 v233, v233, v233
	v_max_f32_e32 v234, v234, v234
	v_max_f32_e32 v235, v235, v235
	v_max_f32_e32 v236, v236, v236
	v_max_f32_e32 v237, v237, v237
	v_max_f32_e32 v238, v238, v238
	v_max_f32_e32 v239, v239, v239
	v_max_f32_e32 v240, v240, v240
	v_max_f32_e32 v241, v241, v241
	v_med3_f32 v226, v226, s62, v95
	v_med3_f32 v227, v227, s62, v95
	v_med3_f32 v228, v228, s62, v95
	v_med3_f32 v229, v229, s62, v95
	v_med3_f32 v230, v230, s62, v95
	v_med3_f32 v231, v231, s62, v95
	v_med3_f32 v232, v232, s62, v95
	v_med3_f32 v233, v233, s62, v95
	v_med3_f32 v234, v234, s62, v95
	v_med3_f32 v235, v235, s62, v95
	v_med3_f32 v236, v236, s62, v95
	v_med3_f32 v237, v237, s62, v95
	v_med3_f32 v238, v238, s62, v95
	v_med3_f32 v239, v239, s62, v95
	v_med3_f32 v240, v240, s62, v95
	v_med3_f32 v241, v241, s62, v95
	v_mov_b32_e32 v242, 0
	v_mov_b32_e32 v243, 0
	v_mov_b32_e32 v244, 0
	v_mov_b32_e32 v245, 0
	v_cvt_pk_fp8_f32 v242, v226, v227
	v_cvt_pk_fp8_f32 v243, v230, v231
	v_cvt_pk_fp8_f32 v244, v234, v235
	v_cvt_pk_fp8_f32 v245, v238, v239
	v_cvt_pk_fp8_f32 v242, v228, v229 op_sel:[0,0,1]
	v_cvt_pk_fp8_f32 v243, v232, v233 op_sel:[0,0,1]
	v_cvt_pk_fp8_f32 v244, v236, v237 op_sel:[0,0,1]
	v_cvt_pk_fp8_f32 v245, v240, v241 op_sel:[0,0,1]
	s_nop 0
	global_store_dwordx4 v78, v[242:245], s[6:7]
	s_waitcnt vmcnt(12)
	v_mul_f32_e32 v144, v26, v144
	v_mul_f32_e32 v145, v26, v145
	v_mul_f32_e32 v146, v26, v146
	v_mul_f32_e32 v147, v26, v147
	ds_write_b128 v209, v[144:147]
	v_mul_f32_e32 v148, v27, v148
	v_mul_f32_e32 v149, v27, v149
	v_mul_f32_e32 v150, v27, v150
	v_mul_f32_e32 v151, v27, v151
	ds_write_b128 v209, v[148:151] offset:1024
	v_mul_f32_e32 v152, v28, v152
	v_mul_f32_e32 v153, v28, v153
	v_mul_f32_e32 v154, v28, v154
	v_mul_f32_e32 v155, v28, v155
	ds_write_b128 v209, v[152:155] offset:2048
	v_mul_f32_e32 v156, v29, v156
	v_mul_f32_e32 v157, v29, v157
	v_mul_f32_e32 v158, v29, v158
	v_mul_f32_e32 v159, v29, v159
	ds_write_b128 v209, v[156:159] offset:3072
	v_mul_f32_e32 v160, v30, v160
	v_mul_f32_e32 v161, v30, v161
	v_mul_f32_e32 v162, v30, v162
	v_mul_f32_e32 v163, v30, v163
	ds_write_b128 v209, v[160:163] offset:4096
	v_mul_f32_e32 v164, v31, v164
	v_mul_f32_e32 v165, v31, v165
	v_mul_f32_e32 v166, v31, v166
	v_mul_f32_e32 v167, v31, v167
	ds_write_b128 v209, v[164:167] offset:5120
	v_mul_f32_e32 v168, v32, v168
	v_mul_f32_e32 v169, v32, v169
	v_mul_f32_e32 v170, v32, v170
	v_mul_f32_e32 v171, v32, v171
	ds_write_b128 v209, v[168:171] offset:6144
	v_mul_f32_e32 v172, v33, v172
	v_mul_f32_e32 v173, v33, v173
	v_mul_f32_e32 v174, v33, v174
	v_mul_f32_e32 v175, v33, v175
	ds_write_b128 v209, v[172:175] offset:7168
	s_waitcnt lgkmcnt(0)
	s_barrier
; #define GAS __attribute__((address_space(1)))
; #define LAS __attribute__((address_space(3)))
; #define LDS_WAIT() asm volatile("s_waitcnt lgkmcnt(0)" ::: "memory")
;     ...
; #pragma unroll
;     for (int i = 0; i < 32; ++i) v[i] = sc >= 0 ? W[(size_t)(k0 + 2 * i + (lane >> 5)) * Nsrc + sc] : 0.f;
; #pragma unroll
;     for (int i = 0; i < 32; ++i) { const int k = k0 + 2 * i + (lane >> 5); float x = v[i] * wscale; if (KS) x *= (k < ksplit ? ksA[k] : ksB[k - ksplit]); scr[(2 * i + (lane >> 5)) * 33 + (lane & 31)] = x; }
;     LDS_WAIT(); asm volatile("" ::: "memory");
;     const int c = lane & 7;
; #pragma unroll
;     for (int j = 0; j < 4; ++j) { const int n = (lane >> 3) + 8 * j; const LAS float* s = scr + (8 * c) * 33 + n;
;         const unsigned long long o = (unsigned long long)pg8::pk4_fp8(s[0 * 33], s[1 * 33], s[2 * 33], s[3 * 33]) | ((unsigned long long)pg8::pk4_fp8(s[4 * 33], s[5 * 33], s[6 * 33], s[7 * 33]) << 32);
;         *(GAS unsigned long long*)(WT + (size_t)(n0 + n) * K + k0 + 8 * c) = o; }
;     LDS_WAIT(); asm volatile("" ::: "memory");
	s_add_u32 s8, s30, 0x8000
	s_addc_u32 s9, s31, 0
	global_load_dwordx4 v[144:147], v74, s[8:9]
	s_add_u32 s8, s8, 0x20000
	s_addc_u32 s9, s9, 0
	global_load_dwordx4 v[148:151], v74, s[8:9]
	s_add_u32 s8, s8, 0x20000
	s_addc_u32 s9, s9, 0
	global_load_dwordx4 v[152:155], v74, s[8:9]
	s_add_u32 s8, s8, 0x20000
	s_addc_u32 s9, s9, 0
	global_load_dwordx4 v[156:159], v74, s[8:9]
	s_add_u32 s8, s8, 0x20000
	s_addc_u32 s9, s9, 0
	global_load_dwordx4 v[160:163], v74, s[8:9]
	s_add_u32 s8, s8, 0x20000
	s_addc_u32 s9, s9, 0
	global_load_dwordx4 v[164:167], v74, s[8:9]
	s_add_u32 s8, s8, 0x20000
	s_addc_u32 s9, s9, 0
	global_load_dwordx4 v[168:171], v74, s[8:9]
	s_add_u32 s8, s8, 0x20000
	s_addc_u32 s9, s9, 0
	global_load_dwordx4 v[172:175], v74, s[8:9]
	s_add_u32 s6, s32, 0x1800000
	s_addc_u32 s7, s33, 0
	ds_read_b32 v226, v211
	ds_read_b32 v227, v211 offset:512
	ds_read_b32 v228, v211 offset:1024
	ds_read_b32 v229, v211 offset:1536
	ds_read_b32 v230, v211 offset:2048
	ds_read_b32 v231, v211 offset:2560
	ds_read_b32 v232, v211 offset:3072
	ds_read_b32 v233, v211 offset:3584
	ds_read_b32 v234, v211 offset:4096
	ds_read_b32 v235, v211 offset:4608
	ds_read_b32 v236, v211 offset:5120
	ds_read_b32 v237, v211 offset:5632
	ds_read_b32 v238, v211 offset:6144
	ds_read_b32 v239, v211 offset:6656
	ds_read_b32 v240, v211 offset:7168
	ds_read_b32 v241, v211 offset:7680
	s_waitcnt lgkmcnt(0)
	v_max_f32_e32 v226, v226, v226
	v_max_f32_e32 v227, v227, v227
	v_max_f32_e32 v228, v228, v228
	v_max_f32_e32 v229, v229, v229
	v_max_f32_e32 v230, v230, v230
	v_max_f32_e32 v231, v231, v231
	v_max_f32_e32 v232, v232, v232
	v_max_f32_e32 v233, v233, v233
	v_max_f32_e32 v234, v234, v234
	v_max_f32_e32 v235, v235, v235
	v_max_f32_e32 v236, v236, v236
	v_max_f32_e32 v237, v237, v237
	v_max_f32_e32 v238, v238, v238
	v_max_f32_e32 v239, v239, v239
	v_max_f32_e32 v240, v240, v240
	v_max_f32_e32 v241, v241, v241
	v_med3_f32 v226, v226, s62, v95
	v_med3_f32 v227, v227, s62, v95
	v_med3_f32 v228, v228, s62, v95
	v_med3_f32 v229, v229, s62, v95
	v_med3_f32 v230, v230, s62, v95
	v_med3_f32 v231, v231, s62, v95
	v_med3_f32 v232, v232, s62, v95
	v_med3_f32 v233, v233, s62, v95
	v_med3_f32 v234, v234, s62, v95
	v_med3_f32 v235, v235, s62, v95
	v_med3_f32 v236, v236, s62, v95
	v_med3_f32 v237, v237, s62, v95
	v_med3_f32 v238, v238, s62, v95
	v_med3_f32 v239, v239, s62, v95
	v_med3_f32 v240, v240, s62, v95
	v_med3_f32 v241, v241, s62, v95
	v_mov_b32_e32 v242, 0
	v_mov_b32_e32 v243, 0
	v_mov_b32_e32 v244, 0
	v_mov_b32_e32 v245, 0
	v_cvt_pk_fp8_f32 v242, v226, v227
	v_cvt_pk_fp8_f32 v243, v230, v231
	v_cvt_pk_fp8_f32 v244, v234, v235
	v_cvt_pk_fp8_f32 v245, v238, v239
	v_cvt_pk_fp8_f32 v242, v228, v229 op_sel:[0,0,1]
	v_cvt_pk_fp8_f32 v243, v232, v233 op_sel:[0,0,1]
	v_cvt_pk_fp8_f32 v244, v236, v237 op_sel:[0,0,1]
	v_cvt_pk_fp8_f32 v245, v240, v241 op_sel:[0,0,1]
	s_nop 0
	global_store_dwordx4 v77, v[242:245], s[6:7]
	ds_read_b32 v226, v213
	ds_read_b32 v227, v213 offset:512
	ds_read_b32 v228, v213 offset:1024
	ds_read_b32 v229, v213 offset:1536
	ds_read_b32 v230, v213 offset:2048
	ds_read_b32 v231, v213 offset:2560
	ds_read_b32 v232, v213 offset:3072
	ds_read_b32 v233, v213 offset:3584
	ds_read_b32 v234, v213 offset:4096
	ds_read_b32 v235, v213 offset:4608
	ds_read_b32 v236, v213 offset:5120
	ds_read_b32 v237, v213 offset:5632
	ds_read_b32 v238, v213 offset:6144
	ds_read_b32 v239, v213 offset:6656
	ds_read_b32 v240, v213 offset:7168
	ds_read_b32 v241, v213 offset:7680
	s_waitcnt lgkmcnt(0)
	v_max_f32_e32 v226, v226, v226
	v_max_f32_e32 v227, v227, v227
	v_max_f32_e32 v228, v228, v228
	v_max_f32_e32 v229, v229, v229
	v_max_f32_e32 v230, v230, v230
	v_max_f32_e32 v231, v231, v231
	v_max_f32_e32 v232, v232, v232
	v_max_f32_e32 v233, v233, v233
	v_max_f32_e32 v234, v234, v234
	v_max_f32_e32 v235, v235, v235
	v_max_f32_e32 v236, v236, v236
	v_max_f32_e32 v237, v237, v237
	v_max_f32_e32 v238, v238, v238
	v_max_f32_e32 v239, v239, v239
	v_max_f32_e32 v240, v240, v240
	v_max_f32_e32 v241, v241, v241
	v_med3_f32 v226, v226, s62, v95
	v_med3_f32 v227, v227, s62, v95
	v_med3_f32 v228, v228, s62, v95
	v_med3_f32 v229, v229, s62, v95
	v_med3_f32 v230, v230, s62, v95
	v_med3_f32 v231, v231, s62, v95
	v_med3_f32 v232, v232, s62, v95
	v_med3_f32 v233, v233, s62, v95
	v_med3_f32 v234, v234, s62, v95
	v_med3_f32 v235, v235, s62, v95
	v_med3_f32 v236, v236, s62, v95
	v_med3_f32 v237, v237, s62, v95
	v_med3_f32 v238, v238, s62, v95
	v_med3_f32 v239, v239, s62, v95
	v_med3_f32 v240, v240, s62, v95
	v_med3_f32 v241, v241, s62, v95
	v_mov_b32_e32 v242, 0
	v_mov_b32_e32 v243, 0
	v_mov_b32_e32 v244, 0
	v_mov_b32_e32 v245, 0
	v_cvt_pk_fp8_f32 v242, v226, v227
	v_cvt_pk_fp8_f32 v243, v230, v231
	v_cvt_pk_fp8_f32 v244, v234, v235
	v_cvt_pk_fp8_f32 v245, v238, v239
	v_cvt_pk_fp8_f32 v242, v228, v229 op_sel:[0,0,1]
	v_cvt_pk_fp8_f32 v243, v232, v233 op_sel:[0,0,1]
	v_cvt_pk_fp8_f32 v244, v236, v237 op_sel:[0,0,1]
	v_cvt_pk_fp8_f32 v245, v240, v241 op_sel:[0,0,1]
	s_nop 0
	global_store_dwordx4 v78, v[242:245], s[6:7]
	s_waitcnt vmcnt(12)
	v_mul_f32_e32 v176, v26, v176
	v_mul_f32_e32 v177, v26, v177
	v_mul_f32_e32 v178, v26, v178
	v_mul_f32_e32 v179, v26, v179
	ds_write_b128 v210, v[176:179]
	v_mul_f32_e32 v180, v27, v180
	v_mul_f32_e32 v181, v27, v181
	v_mul_f32_e32 v182, v27, v182
	v_mul_f32_e32 v183, v27, v183
	ds_write_b128 v210, v[180:183] offset:1024
	v_mul_f32_e32 v184, v28, v184
	v_mul_f32_e32 v185, v28, v185
	v_mul_f32_e32 v186, v28, v186
	v_mul_f32_e32 v187, v28, v187
	ds_write_b128 v210, v[184:187] offset:2048
	v_mul_f32_e32 v188, v29, v188
	v_mul_f32_e32 v189, v29, v189
	v_mul_f32_e32 v190, v29, v190
	v_mul_f32_e32 v191, v29, v191
	ds_write_b128 v210, v[188:191] offset:3072
	v_mul_f32_e32 v192, v30, v192
	v_mul_f32_e32 v193, v30, v193
	v_mul_f32_e32 v194, v30, v194
	v_mul_f32_e32 v195, v30, v195
	ds_write_b128 v210, v[192:195] offset:4096
	v_mul_f32_e32 v196, v31, v196
	v_mul_f32_e32 v197, v31, v197
	v_mul_f32_e32 v198, v31, v198
	v_mul_f32_e32 v199, v31, v199
	ds_write_b128 v210, v[196:199] offset:5120
	v_mul_f32_e32 v200, v32, v200
	v_mul_f32_e32 v201, v32, v201
	v_mul_f32_e32 v202, v32, v202
	v_mul_f32_e32 v203, v32, v203
	ds_write_b128 v210, v[200:203] offset:6144
	v_mul_f32_e32 v204, v33, v204
	v_mul_f32_e32 v205, v33, v205
	v_mul_f32_e32 v206, v33, v206
	v_mul_f32_e32 v207, v33, v207
	ds_write_b128 v210, v[204:207] offset:7168
	s_waitcnt lgkmcnt(0)
	s_barrier
; #define GAS __attribute__((address_space(1)))
; #define LAS __attribute__((address_space(3)))
; #define LDS_WAIT() asm volatile("s_waitcnt lgkmcnt(0)" ::: "memory")
;     ...
; #pragma unroll
;     for (int i = 0; i < 32; ++i) v[i] = sc >= 0 ? W[(size_t)(k0 + 2 * i + (lane >> 5)) * Nsrc + sc] : 0.f;
; #pragma unroll
;     for (int i = 0; i < 32; ++i) { const int k = k0 + 2 * i + (lane >> 5); float x = v[i] * wscale; if (KS) x *= (k < ksplit ? ksA[k] : ksB[k - ksplit]); scr[(2 * i + (lane >> 5)) * 33 + (lane & 31)] = x; }
;     LDS_WAIT(); asm volatile("" ::: "memory");
;     const int c = lane & 7;
; #pragma unroll
;     for (int j = 0; j < 4; ++j) { const int n = (lane >> 3) + 8 * j; const LAS float* s = scr + (8 * c) * 33 + n;
;         const unsigned long long o = (unsigned long long)pg8::pk4_fp8(s[0 * 33], s[1 * 33], s[2 * 33], s[3 * 33]) | ((unsigned long long)pg8::pk4_fp8(s[4 * 33], s[5 * 33], s[6 * 33], s[7 * 33]) << 32);
;         *(GAS unsigned long long*)(WT + (size_t)(n0 + n) * K + k0 + 8 * c) = o; }
;     LDS_WAIT(); asm volatile("" ::: "memory");
	s_add_u32 s8, s30, 0x9000
	s_addc_u32 s9, s31, 0
	global_load_dwordx4 v[176:179], v74, s[8:9]
	s_add_u32 s8, s8, 0x20000
	s_addc_u32 s9, s9, 0
	global_load_dwordx4 v[180:183], v74, s[8:9]
	s_add_u32 s8, s8, 0x20000
	s_addc_u32 s9, s9, 0
	global_load_dwordx4 v[184:187], v74, s[8:9]
	s_add_u32 s8, s8, 0x20000
	s_addc_u32 s9, s9, 0
	global_load_dwordx4 v[188:191], v74, s[8:9]
	s_add_u32 s8, s8, 0x20000
	s_addc_u32 s9, s9, 0
	global_load_dwordx4 v[192:195], v74, s[8:9]
	s_add_u32 s8, s8, 0x20000
	s_addc_u32 s9, s9, 0
	global_load_dwordx4 v[196:199], v74, s[8:9]
	s_add_u32 s8, s8, 0x20000
	s_addc_u32 s9, s9, 0
	global_load_dwordx4 v[200:203], v74, s[8:9]
	s_add_u32 s8, s8, 0x20000
	s_addc_u32 s9, s9, 0
	global_load_dwordx4 v[204:207], v74, s[8:9]
	s_add_u32 s6, s32, 0x1c00000
	s_addc_u32 s7, s33, 0
	ds_read_b32 v226, v212
	ds_read_b32 v227, v212 offset:512
	ds_read_b32 v228, v212 offset:1024
	ds_read_b32 v229, v212 offset:1536
	ds_read_b32 v230, v212 offset:2048
	ds_read_b32 v231, v212 offset:2560
	ds_read_b32 v232, v212 offset:3072
	ds_read_b32 v233, v212 offset:3584
	ds_read_b32 v234, v212 offset:4096
	ds_read_b32 v235, v212 offset:4608
	ds_read_b32 v236, v212 offset:5120
	ds_read_b32 v237, v212 offset:5632
	ds_read_b32 v238, v212 offset:6144
	ds_read_b32 v239, v212 offset:6656
	ds_read_b32 v240, v212 offset:7168
	ds_read_b32 v241, v212 offset:7680
	s_waitcnt lgkmcnt(0)
	v_max_f32_e32 v226, v226, v226
	v_max_f32_e32 v227, v227, v227
	v_max_f32_e32 v228, v228, v228
	v_max_f32_e32 v229, v229, v229
	v_max_f32_e32 v230, v230, v230
	v_max_f32_e32 v231, v231, v231
	v_max_f32_e32 v232, v232, v232
	v_max_f32_e32 v233, v233, v233
	v_max_f32_e32 v234, v234, v234
	v_max_f32_e32 v235, v235, v235
	v_max_f32_e32 v236, v236, v236
	v_max_f32_e32 v237, v237, v237
	v_max_f32_e32 v238, v238, v238
	v_max_f32_e32 v239, v239, v239
	v_max_f32_e32 v240, v240, v240
	v_max_f32_e32 v241, v241, v241
	v_med3_f32 v226, v226, s62, v95
	v_med3_f32 v227, v227, s62, v95
	v_med3_f32 v228, v228, s62, v95
	v_med3_f32 v229, v229, s62, v95
	v_med3_f32 v230, v230, s62, v95
	v_med3_f32 v231, v231, s62, v95
	v_med3_f32 v232, v232, s62, v95
	v_med3_f32 v233, v233, s62, v95
	v_med3_f32 v234, v234, s62, v95
	v_med3_f32 v235, v235, s62, v95
	v_med3_f32 v236, v236, s62, v95
	v_med3_f32 v237, v237, s62, v95
	v_med3_f32 v238, v238, s62, v95
	v_med3_f32 v239, v239, s62, v95
	v_med3_f32 v240, v240, s62, v95
	v_med3_f32 v241, v241, s62, v95
	v_mov_b32_e32 v242, 0
	v_mov_b32_e32 v243, 0
	v_mov_b32_e32 v244, 0
	v_mov_b32_e32 v245, 0
	v_cvt_pk_fp8_f32 v242, v226, v227
	v_cvt_pk_fp8_f32 v243, v230, v231
	v_cvt_pk_fp8_f32 v244, v234, v235
	v_cvt_pk_fp8_f32 v245, v238, v239
	v_cvt_pk_fp8_f32 v242, v228, v229 op_sel:[0,0,1]
	v_cvt_pk_fp8_f32 v243, v232, v233 op_sel:[0,0,1]
	v_cvt_pk_fp8_f32 v244, v236, v237 op_sel:[0,0,1]
	v_cvt_pk_fp8_f32 v245, v240, v241 op_sel:[0,0,1]
	s_nop 0
	global_store_dwordx4 v77, v[242:245], s[6:7]
	ds_read_b32 v226, v214
	ds_read_b32 v227, v214 offset:512
	ds_read_b32 v228, v214 offset:1024
	ds_read_b32 v229, v214 offset:1536
	ds_read_b32 v230, v214 offset:2048
	ds_read_b32 v231, v214 offset:2560
	ds_read_b32 v232, v214 offset:3072
	ds_read_b32 v233, v214 offset:3584
	ds_read_b32 v234, v214 offset:4096
	ds_read_b32 v235, v214 offset:4608
	ds_read_b32 v236, v214 offset:5120
	ds_read_b32 v237, v214 offset:5632
	ds_read_b32 v238, v214 offset:6144
	ds_read_b32 v239, v214 offset:6656
	ds_read_b32 v240, v214 offset:7168
	ds_read_b32 v241, v214 offset:7680
	s_waitcnt lgkmcnt(0)
	v_max_f32_e32 v226, v226, v226
	v_max_f32_e32 v227, v227, v227
	v_max_f32_e32 v228, v228, v228
	v_max_f32_e32 v229, v229, v229
	v_max_f32_e32 v230, v230, v230
	v_max_f32_e32 v231, v231, v231
	v_max_f32_e32 v232, v232, v232
	v_max_f32_e32 v233, v233, v233
	v_max_f32_e32 v234, v234, v234
	v_max_f32_e32 v235, v235, v235
	v_max_f32_e32 v236, v236, v236
	v_max_f32_e32 v237, v237, v237
	v_max_f32_e32 v238, v238, v238
	v_max_f32_e32 v239, v239, v239
	v_max_f32_e32 v240, v240, v240
	v_max_f32_e32 v241, v241, v241
	v_med3_f32 v226, v226, s62, v95
	v_med3_f32 v227, v227, s62, v95
	v_med3_f32 v228, v228, s62, v95
	v_med3_f32 v229, v229, s62, v95
	v_med3_f32 v230, v230, s62, v95
	v_med3_f32 v231, v231, s62, v95
	v_med3_f32 v232, v232, s62, v95
	v_med3_f32 v233, v233, s62, v95
	v_med3_f32 v234, v234, s62, v95
	v_med3_f32 v235, v235, s62, v95
	v_med3_f32 v236, v236, s62, v95
	v_med3_f32 v237, v237, s62, v95
	v_med3_f32 v238, v238, s62, v95
	v_med3_f32 v239, v239, s62, v95
	v_med3_f32 v240, v240, s62, v95
	v_med3_f32 v241, v241, s62, v95
	v_mov_b32_e32 v242, 0
	v_mov_b32_e32 v243, 0
	v_mov_b32_e32 v244, 0
	v_mov_b32_e32 v245, 0
	v_cvt_pk_fp8_f32 v242, v226, v227
	v_cvt_pk_fp8_f32 v243, v230, v231
	v_cvt_pk_fp8_f32 v244, v234, v235
	v_cvt_pk_fp8_f32 v245, v238, v239
	v_cvt_pk_fp8_f32 v242, v228, v229 op_sel:[0,0,1]
	v_cvt_pk_fp8_f32 v243, v232, v233 op_sel:[0,0,1]
	v_cvt_pk_fp8_f32 v244, v236, v237 op_sel:[0,0,1]
	v_cvt_pk_fp8_f32 v245, v240, v241 op_sel:[0,0,1]
	s_nop 0
	global_store_dwordx4 v78, v[242:245], s[6:7]
	s_waitcnt vmcnt(12)
	v_mul_f32_e32 v144, v26, v144
	v_mul_f32_e32 v145, v26, v145
	v_mul_f32_e32 v146, v26, v146
	v_mul_f32_e32 v147, v26, v147
	ds_write_b128 v209, v[144:147]
	v_mul_f32_e32 v148, v27, v148
	v_mul_f32_e32 v149, v27, v149
	v_mul_f32_e32 v150, v27, v150
	v_mul_f32_e32 v151, v27, v151
	ds_write_b128 v209, v[148:151] offset:1024
	v_mul_f32_e32 v152, v28, v152
	v_mul_f32_e32 v153, v28, v153
	v_mul_f32_e32 v154, v28, v154
	v_mul_f32_e32 v155, v28, v155
	ds_write_b128 v209, v[152:155] offset:2048
	v_mul_f32_e32 v156, v29, v156
	v_mul_f32_e32 v157, v29, v157
	v_mul_f32_e32 v158, v29, v158
	v_mul_f32_e32 v159, v29, v159
	ds_write_b128 v209, v[156:159] offset:3072
	v_mul_f32_e32 v160, v30, v160
	v_mul_f32_e32 v161, v30, v161
	v_mul_f32_e32 v162, v30, v162
	v_mul_f32_e32 v163, v30, v163
	ds_write_b128 v209, v[160:163] offset:4096
	v_mul_f32_e32 v164, v31, v164
	v_mul_f32_e32 v165, v31, v165
	v_mul_f32_e32 v166, v31, v166
	v_mul_f32_e32 v167, v31, v167
	ds_write_b128 v209, v[164:167] offset:5120
	v_mul_f32_e32 v168, v32, v168
	v_mul_f32_e32 v169, v32, v169
	v_mul_f32_e32 v170, v32, v170
	v_mul_f32_e32 v171, v32, v171
	ds_write_b128 v209, v[168:171] offset:6144
	v_mul_f32_e32 v172, v33, v172
	v_mul_f32_e32 v173, v33, v173
	v_mul_f32_e32 v174, v33, v174
	v_mul_f32_e32 v175, v33, v175
	ds_write_b128 v209, v[172:175] offset:7168
	s_waitcnt lgkmcnt(0)
	s_barrier
; #define GAS __attribute__((address_space(1)))
; #define LAS __attribute__((address_space(3)))
; #define LDS_WAIT() asm volatile("s_waitcnt lgkmcnt(0)" ::: "memory")
; __device__ __forceinline__ unsigned pk4_fp8(float a, float b, float c, float d) {
;     a = fminf(fmaxf(a, -448.f), 448.f); b = fminf(fmaxf(b, -448.f), 448.f); c = fminf(fmaxf(c, -448.f), 448.f); d = fminf(fmaxf(d, -448.f), 448.f);
;     int w = __builtin_amdgcn_cvt_pk_fp8_f32(a, b, 0, false); w = __builtin_amdgcn_cvt_pk_fp8_f32(c, d, w, true); return (unsigned)w; }
;     const int pr = item >> 1, kb = 2 * (pr / nblk) + (item & 1), nb = pr % nblk, k0 = 64 * kb, n0 = 32 * nb;
;     const int nr = n0 + (lane & 31); const int sc = MAP == 1 ? src_col_in(nr) : nr;
;     float v[32];
; #pragma unroll
;     for (int i = 0; i < 32; ++i) v[i] = sc >= 0 ? W[(size_t)(k0 + 2 * i + (lane >> 5)) * Nsrc + sc] : 0.f;
; #pragma unroll
;     for (int i = 0; i < 32; ++i) { const int k = k0 + 2 * i + (lane >> 5); float x = v[i] * wscale; if (KS) x *= (k < ksplit ? ksA[k] : ksB[k - ksplit]); scr[(2 * i + (lane >> 5)) * 33 + (lane & 31)] = x; }
;     LDS_WAIT(); asm volatile("" ::: "memory");
;     const int c = lane & 7;
; #pragma unroll
;     for (int j = 0; j < 4; ++j) { const int n = (lane >> 3) + 8 * j; const LAS float* s = scr + (8 * c) * 33 + n;
;         const unsigned long long o = (unsigned long long)pg8::pk4_fp8(s[0 * 33], s[1 * 33], s[2 * 33], s[3 * 33]) | ((unsigned long long)pg8::pk4_fp8(s[4 * 33], s[5 * 33], s[6 * 33], s[7 * 33]) << 32);
;         *(GAS unsigned long long*)(WT + (size_t)(n0 + n) * K + k0 + 8 * c) = o; }
;     LDS_WAIT(); asm volatile("" ::: "memory");
; }
	s_add_u32 s8, s30, 0xa000
	s_addc_u32 s9, s31, 0
	global_load_dwordx4 v[144:147], v74, s[8:9]
	s_add_u32 s8, s8, 0x20000
	s_addc_u32 s9, s9, 0
	global_load_dwordx4 v[148:151], v74, s[8:9]
	s_add_u32 s8, s8, 0x20000
	s_addc_u32 s9, s9, 0
	global_load_dwordx4 v[152:155], v74, s[8:9]
	s_add_u32 s8, s8, 0x20000
	s_addc_u32 s9, s9, 0
	global_load_dwordx4 v[156:159], v74, s[8:9]
	s_add_u32 s8, s8, 0x20000
	s_addc_u32 s9, s9, 0
	global_load_dwordx4 v[160:163], v74, s[8:9]
	s_add_u32 s8, s8, 0x20000
	s_addc_u32 s9, s9, 0
	global_load_dwordx4 v[164:167], v74, s[8:9]
	s_add_u32 s8, s8, 0x20000
	s_addc_u32 s9, s9, 0
	global_load_dwordx4 v[168:171], v74, s[8:9]
	s_add_u32 s8, s8, 0x20000
	s_addc_u32 s9, s9, 0
	global_load_dwordx4 v[172:175], v74, s[8:9]
	s_add_u32 s6, s32, 0x2000000
	s_addc_u32 s7, s33, 0
	ds_read_b32 v226, v211
	ds_read_b32 v227, v211 offset:512
	ds_read_b32 v228, v211 offset:1024
	ds_read_b32 v229, v211 offset:1536
	ds_read_b32 v230, v211 offset:2048
	ds_read_b32 v231, v211 offset:2560
	ds_read_b32 v232, v211 offset:3072
	ds_read_b32 v233, v211 offset:3584
	ds_read_b32 v234, v211 offset:4096
	ds_read_b32 v235, v211 offset:4608
	ds_read_b32 v236, v211 offset:5120
	ds_read_b32 v237, v211 offset:5632
	ds_read_b32 v238, v211 offset:6144
	ds_read_b32 v239, v211 offset:6656
	ds_read_b32 v240, v211 offset:7168
	ds_read_b32 v241, v211 offset:7680
	s_waitcnt lgkmcnt(0)
	v_max_f32_e32 v226, v226, v226
	v_max_f32_e32 v227, v227, v227
	v_max_f32_e32 v228, v228, v228
	v_max_f32_e32 v229, v229, v229
	v_max_f32_e32 v230, v230, v230
	v_max_f32_e32 v231, v231, v231
	v_max_f32_e32 v232, v232, v232
	v_max_f32_e32 v233, v233, v233
	v_max_f32_e32 v234, v234, v234
	v_max_f32_e32 v235, v235, v235
	v_max_f32_e32 v236, v236, v236
	v_max_f32_e32 v237, v237, v237
	v_max_f32_e32 v238, v238, v238
	v_max_f32_e32 v239, v239, v239
	v_max_f32_e32 v240, v240, v240
	v_max_f32_e32 v241, v241, v241
	v_med3_f32 v226, v226, s62, v95
	v_med3_f32 v227, v227, s62, v95
	v_med3_f32 v228, v228, s62, v95
	v_med3_f32 v229, v229, s62, v95
	v_med3_f32 v230, v230, s62, v95
	v_med3_f32 v231, v231, s62, v95
	v_med3_f32 v232, v232, s62, v95
	v_med3_f32 v233, v233, s62, v95
	v_med3_f32 v234, v234, s62, v95
	v_med3_f32 v235, v235, s62, v95
	v_med3_f32 v236, v236, s62, v95
	v_med3_f32 v237, v237, s62, v95
	v_med3_f32 v238, v238, s62, v95
	v_med3_f32 v239, v239, s62, v95
	v_med3_f32 v240, v240, s62, v95
	v_med3_f32 v241, v241, s62, v95
	v_mov_b32_e32 v242, 0
	v_mov_b32_e32 v243, 0
	v_mov_b32_e32 v244, 0
	v_mov_b32_e32 v245, 0
	v_cvt_pk_fp8_f32 v242, v226, v227
	v_cvt_pk_fp8_f32 v243, v230, v231
	v_cvt_pk_fp8_f32 v244, v234, v235
	v_cvt_pk_fp8_f32 v245, v238, v239
	v_cvt_pk_fp8_f32 v242, v228, v229 op_sel:[0,0,1]
	v_cvt_pk_fp8_f32 v243, v232, v233 op_sel:[0,0,1]
	v_cvt_pk_fp8_f32 v244, v236, v237 op_sel:[0,0,1]
	v_cvt_pk_fp8_f32 v245, v240, v241 op_sel:[0,0,1]
	s_nop 0
	global_store_dwordx4 v77, v[242:245], s[6:7]
	ds_read_b32 v226, v213
	ds_read_b32 v227, v213 offset:512
	ds_read_b32 v228, v213 offset:1024
	ds_read_b32 v229, v213 offset:1536
	ds_read_b32 v230, v213 offset:2048
	ds_read_b32 v231, v213 offset:2560
	ds_read_b32 v232, v213 offset:3072
	ds_read_b32 v233, v213 offset:3584
	ds_read_b32 v234, v213 offset:4096
	ds_read_b32 v235, v213 offset:4608
	ds_read_b32 v236, v213 offset:5120
	ds_read_b32 v237, v213 offset:5632
	ds_read_b32 v238, v213 offset:6144
	ds_read_b32 v239, v213 offset:6656
	ds_read_b32 v240, v213 offset:7168
	ds_read_b32 v241, v213 offset:7680
	s_waitcnt lgkmcnt(0)
	v_max_f32_e32 v226, v226, v226
	v_max_f32_e32 v227, v227, v227
	v_max_f32_e32 v228, v228, v228
	v_max_f32_e32 v229, v229, v229
	v_max_f32_e32 v230, v230, v230
	v_max_f32_e32 v231, v231, v231
	v_max_f32_e32 v232, v232, v232
	v_max_f32_e32 v233, v233, v233
	v_max_f32_e32 v234, v234, v234
	v_max_f32_e32 v235, v235, v235
	v_max_f32_e32 v236, v236, v236
	v_max_f32_e32 v237, v237, v237
	v_max_f32_e32 v238, v238, v238
	v_max_f32_e32 v239, v239, v239
	v_max_f32_e32 v240, v240, v240
	v_max_f32_e32 v241, v241, v241
	v_med3_f32 v226, v226, s62, v95
	v_med3_f32 v227, v227, s62, v95
	v_med3_f32 v228, v228, s62, v95
	v_med3_f32 v229, v229, s62, v95
	v_med3_f32 v230, v230, s62, v95
	v_med3_f32 v231, v231, s62, v95
	v_med3_f32 v232, v232, s62, v95
	v_med3_f32 v233, v233, s62, v95
	v_med3_f32 v234, v234, s62, v95
	v_med3_f32 v235, v235, s62, v95
	v_med3_f32 v236, v236, s62, v95
	v_med3_f32 v237, v237, s62, v95
	v_med3_f32 v238, v238, s62, v95
	v_med3_f32 v239, v239, s62, v95
	v_med3_f32 v240, v240, s62, v95
	v_med3_f32 v241, v241, s62, v95
	v_mov_b32_e32 v242, 0
	v_mov_b32_e32 v243, 0
	v_mov_b32_e32 v244, 0
	v_mov_b32_e32 v245, 0
	v_cvt_pk_fp8_f32 v242, v226, v227
	v_cvt_pk_fp8_f32 v243, v230, v231
	v_cvt_pk_fp8_f32 v244, v234, v235
	v_cvt_pk_fp8_f32 v245, v238, v239
	v_cvt_pk_fp8_f32 v242, v228, v229 op_sel:[0,0,1]
	v_cvt_pk_fp8_f32 v243, v232, v233 op_sel:[0,0,1]
	v_cvt_pk_fp8_f32 v244, v236, v237 op_sel:[0,0,1]
	v_cvt_pk_fp8_f32 v245, v240, v241 op_sel:[0,0,1]
	s_nop 0
	global_store_dwordx4 v78, v[242:245], s[6:7]
	s_waitcnt vmcnt(12)
	v_mul_f32_e32 v176, v26, v176
	v_mul_f32_e32 v177, v26, v177
	v_mul_f32_e32 v178, v26, v178
	v_mul_f32_e32 v179, v26, v179
	ds_write_b128 v210, v[176:179]
	v_mul_f32_e32 v180, v27, v180
	v_mul_f32_e32 v181, v27, v181
	v_mul_f32_e32 v182, v27, v182
	v_mul_f32_e32 v183, v27, v183
	ds_write_b128 v210, v[180:183] offset:1024
	v_mul_f32_e32 v184, v28, v184
	v_mul_f32_e32 v185, v28, v185
	v_mul_f32_e32 v186, v28, v186
	v_mul_f32_e32 v187, v28, v187
	ds_write_b128 v210, v[184:187] offset:2048
	v_mul_f32_e32 v188, v29, v188
	v_mul_f32_e32 v189, v29, v189
	v_mul_f32_e32 v190, v29, v190
	v_mul_f32_e32 v191, v29, v191
	ds_write_b128 v210, v[188:191] offset:3072
	v_mul_f32_e32 v192, v30, v192
	v_mul_f32_e32 v193, v30, v193
	v_mul_f32_e32 v194, v30, v194
	v_mul_f32_e32 v195, v30, v195
	ds_write_b128 v210, v[192:195] offset:4096
	v_mul_f32_e32 v196, v31, v196
	v_mul_f32_e32 v197, v31, v197
	v_mul_f32_e32 v198, v31, v198
	v_mul_f32_e32 v199, v31, v199
	ds_write_b128 v210, v[196:199] offset:5120
	v_mul_f32_e32 v200, v32, v200
	v_mul_f32_e32 v201, v32, v201
	v_mul_f32_e32 v202, v32, v202
	v_mul_f32_e32 v203, v32, v203
	ds_write_b128 v210, v[200:203] offset:6144
	v_mul_f32_e32 v204, v33, v204
	v_mul_f32_e32 v205, v33, v205
	v_mul_f32_e32 v206, v33, v206
	v_mul_f32_e32 v207, v33, v207
	ds_write_b128 v210, v[204:207] offset:7168
	s_waitcnt lgkmcnt(0)
	s_barrier
; #define GAS __attribute__((address_space(1)))
; #define LAS __attribute__((address_space(3)))
; #define LDS_WAIT() asm volatile("s_waitcnt lgkmcnt(0)" ::: "memory")
; __device__ __forceinline__ unsigned pk4_fp8(float a, float b, float c, float d) {
;     a = fminf(fmaxf(a, -448.f), 448.f); b = fminf(fmaxf(b, -448.f), 448.f); c = fminf(fmaxf(c, -448.f), 448.f); d = fminf(fmaxf(d, -448.f), 448.f);
;     int w = __builtin_amdgcn_cvt_pk_fp8_f32(a, b, 0, false); w = __builtin_amdgcn_cvt_pk_fp8_f32(c, d, w, true); return (unsigned)w; }
;     const int pr = item >> 1, kb = 2 * (pr / nblk) + (item & 1), nb = pr % nblk, k0 = 64 * kb, n0 = 32 * nb;
;     const int nr = n0 + (lane & 31); const int sc = MAP == 1 ? src_col_in(nr) : nr;
;     float v[32];
; #pragma unroll
;     for (int i = 0; i < 32; ++i) v[i] = sc >= 0 ? W[(size_t)(k0 + 2 * i + (lane >> 5)) * Nsrc + sc] : 0.f;
; #pragma unroll
;     for (int i = 0; i < 32; ++i) { const int k = k0 + 2 * i + (lane >> 5); float x = v[i] * wscale; if (KS) x *= (k < ksplit ? ksA[k] : ksB[k - ksplit]); scr[(2 * i + (lane >> 5)) * 33 + (lane & 31)] = x; }
;     LDS_WAIT(); asm volatile("" ::: "memory");
;     const int c = lane & 7;
; #pragma unroll
;     for (int j = 0; j < 4; ++j) { const int n = (lane >> 3) + 8 * j; const LAS float* s = scr + (8 * c) * 33 + n;
;         const unsigned long long o = (unsigned long long)pg8::pk4_fp8(s[0 * 33], s[1 * 33], s[2 * 33], s[3 * 33]) | ((unsigned long long)pg8::pk4_fp8(s[4 * 33], s[5 * 33], s[6 * 33], s[7 * 33]) << 32);
;         *(GAS unsigned long long*)(WT + (size_t)(n0 + n) * K + k0 + 8 * c) = o; }
;     LDS_WAIT(); asm volatile("" ::: "memory");
; }
	s_add_u32 s8, s30, 0xb000
	s_addc_u32 s9, s31, 0
	global_load_dwordx4 v[176:179], v74, s[8:9]
	s_add_u32 s8, s8, 0x20000
	s_addc_u32 s9, s9, 0
	global_load_dwordx4 v[180:183], v74, s[8:9]
	s_add_u32 s8, s8, 0x20000
	s_addc_u32 s9, s9, 0
	global_load_dwordx4 v[184:187], v74, s[8:9]
	s_add_u32 s8, s8, 0x20000
	s_addc_u32 s9, s9, 0
	global_load_dwordx4 v[188:191], v74, s[8:9]
	s_add_u32 s8, s8, 0x20000
	s_addc_u32 s9, s9, 0
	global_load_dwordx4 v[192:195], v74, s[8:9]
	s_add_u32 s8, s8, 0x20000
	s_addc_u32 s9, s9, 0
	global_load_dwordx4 v[196:199], v74, s[8:9]
	s_add_u32 s8, s8, 0x20000
	s_addc_u32 s9, s9, 0
	global_load_dwordx4 v[200:203], v74, s[8:9]
	s_add_u32 s8, s8, 0x20000
	s_addc_u32 s9, s9, 0
	global_load_dwordx4 v[204:207], v74, s[8:9]
	s_add_u32 s6, s32, 0x2400000
	s_addc_u32 s7, s33, 0
	ds_read_b32 v226, v212
	ds_read_b32 v227, v212 offset:512
	ds_read_b32 v228, v212 offset:1024
	ds_read_b32 v229, v212 offset:1536
	ds_read_b32 v230, v212 offset:2048
	ds_read_b32 v231, v212 offset:2560
	ds_read_b32 v232, v212 offset:3072
	ds_read_b32 v233, v212 offset:3584
	ds_read_b32 v234, v212 offset:4096
	ds_read_b32 v235, v212 offset:4608
	ds_read_b32 v236, v212 offset:5120
	ds_read_b32 v237, v212 offset:5632
	ds_read_b32 v238, v212 offset:6144
	ds_read_b32 v239, v212 offset:6656
	ds_read_b32 v240, v212 offset:7168
	ds_read_b32 v241, v212 offset:7680
	s_waitcnt lgkmcnt(0)
	v_max_f32_e32 v226, v226, v226
	v_max_f32_e32 v227, v227, v227
	v_max_f32_e32 v228, v228, v228
	v_max_f32_e32 v229, v229, v229
	v_max_f32_e32 v230, v230, v230
	v_max_f32_e32 v231, v231, v231
	v_max_f32_e32 v232, v232, v232
	v_max_f32_e32 v233, v233, v233
	v_max_f32_e32 v234, v234, v234
	v_max_f32_e32 v235, v235, v235
	v_max_f32_e32 v236, v236, v236
	v_max_f32_e32 v237, v237, v237
	v_max_f32_e32 v238, v238, v238
	v_max_f32_e32 v239, v239, v239
	v_max_f32_e32 v240, v240, v240
	v_max_f32_e32 v241, v241, v241
	v_med3_f32 v226, v226, s62, v95
	v_med3_f32 v227, v227, s62, v95
	v_med3_f32 v228, v228, s62, v95
	v_med3_f32 v229, v229, s62, v95
	v_med3_f32 v230, v230, s62, v95
	v_med3_f32 v231, v231, s62, v95
	v_med3_f32 v232, v232, s62, v95
	v_med3_f32 v233, v233, s62, v95
	v_med3_f32 v234, v234, s62, v95
	v_med3_f32 v235, v235, s62, v95
	v_med3_f32 v236, v236, s62, v95
	v_med3_f32 v237, v237, s62, v95
	v_med3_f32 v238, v238, s62, v95
	v_med3_f32 v239, v239, s62, v95
	v_med3_f32 v240, v240, s62, v95
	v_med3_f32 v241, v241, s62, v95
	v_mov_b32_e32 v242, 0
	v_mov_b32_e32 v243, 0
	v_mov_b32_e32 v244, 0
	v_mov_b32_e32 v245, 0
	v_cvt_pk_fp8_f32 v242, v226, v227
	v_cvt_pk_fp8_f32 v243, v230, v231
	v_cvt_pk_fp8_f32 v244, v234, v235
	v_cvt_pk_fp8_f32 v245, v238, v239
	v_cvt_pk_fp8_f32 v242, v228, v229 op_sel:[0,0,1]
	v_cvt_pk_fp8_f32 v243, v232, v233 op_sel:[0,0,1]
	v_cvt_pk_fp8_f32 v244, v236, v237 op_sel:[0,0,1]
	v_cvt_pk_fp8_f32 v245, v240, v241 op_sel:[0,0,1]
	s_nop 0
	global_store_dwordx4 v77, v[242:245], s[6:7]
	ds_read_b32 v226, v214
	ds_read_b32 v227, v214 offset:512
	ds_read_b32 v228, v214 offset:1024
	ds_read_b32 v229, v214 offset:1536
	ds_read_b32 v230, v214 offset:2048
	ds_read_b32 v231, v214 offset:2560
	ds_read_b32 v232, v214 offset:3072
	ds_read_b32 v233, v214 offset:3584
	ds_read_b32 v234, v214 offset:4096
	ds_read_b32 v235, v214 offset:4608
	ds_read_b32 v236, v214 offset:5120
	ds_read_b32 v237, v214 offset:5632
	ds_read_b32 v238, v214 offset:6144
	ds_read_b32 v239, v214 offset:6656
	ds_read_b32 v240, v214 offset:7168
	ds_read_b32 v241, v214 offset:7680
	s_waitcnt lgkmcnt(0)
	v_max_f32_e32 v226, v226, v226
	v_max_f32_e32 v227, v227, v227
	v_max_f32_e32 v228, v228, v228
	v_max_f32_e32 v229, v229, v229
	v_max_f32_e32 v230, v230, v230
	v_max_f32_e32 v231, v231, v231
	v_max_f32_e32 v232, v232, v232
	v_max_f32_e32 v233, v233, v233
	v_max_f32_e32 v234, v234, v234
	v_max_f32_e32 v235, v235, v235
	v_max_f32_e32 v236, v236, v236
	v_max_f32_e32 v237, v237, v237
	v_max_f32_e32 v238, v238, v238
	v_max_f32_e32 v239, v239, v239
	v_max_f32_e32 v240, v240, v240
	v_max_f32_e32 v241, v241, v241
	v_med3_f32 v226, v226, s62, v95
	v_med3_f32 v227, v227, s62, v95
	v_med3_f32 v228, v228, s62, v95
	v_med3_f32 v229, v229, s62, v95
	v_med3_f32 v230, v230, s62, v95
	v_med3_f32 v231, v231, s62, v95
	v_med3_f32 v232, v232, s62, v95
	v_med3_f32 v233, v233, s62, v95
	v_med3_f32 v234, v234, s62, v95
	v_med3_f32 v235, v235, s62, v95
	v_med3_f32 v236, v236, s62, v95
	v_med3_f32 v237, v237, s62, v95
	v_med3_f32 v238, v238, s62, v95
	v_med3_f32 v239, v239, s62, v95
	v_med3_f32 v240, v240, s62, v95
	v_med3_f32 v241, v241, s62, v95
	v_mov_b32_e32 v242, 0
	v_mov_b32_e32 v243, 0
	v_mov_b32_e32 v244, 0
	v_mov_b32_e32 v245, 0
	v_cvt_pk_fp8_f32 v242, v226, v227
	v_cvt_pk_fp8_f32 v243, v230, v231
	v_cvt_pk_fp8_f32 v244, v234, v235
	v_cvt_pk_fp8_f32 v245, v238, v239
	v_cvt_pk_fp8_f32 v242, v228, v229 op_sel:[0,0,1]
	v_cvt_pk_fp8_f32 v243, v232, v233 op_sel:[0,0,1]
	v_cvt_pk_fp8_f32 v244, v236, v237 op_sel:[0,0,1]
	v_cvt_pk_fp8_f32 v245, v240, v241 op_sel:[0,0,1]
	s_nop 0
	global_store_dwordx4 v78, v[242:245], s[6:7]
	s_waitcnt vmcnt(12)
	v_mul_f32_e32 v144, v26, v144
	v_mul_f32_e32 v145, v26, v145
	v_mul_f32_e32 v146, v26, v146
	v_mul_f32_e32 v147, v26, v147
	ds_write_b128 v209, v[144:147]
	v_mul_f32_e32 v148, v27, v148
	v_mul_f32_e32 v149, v27, v149
	v_mul_f32_e32 v150, v27, v150
	v_mul_f32_e32 v151, v27, v151
	ds_write_b128 v209, v[148:151] offset:1024
	v_mul_f32_e32 v152, v28, v152
	v_mul_f32_e32 v153, v28, v153
	v_mul_f32_e32 v154, v28, v154
	v_mul_f32_e32 v155, v28, v155
	ds_write_b128 v209, v[152:155] offset:2048
	v_mul_f32_e32 v156, v29, v156
	v_mul_f32_e32 v157, v29, v157
	v_mul_f32_e32 v158, v29, v158
	v_mul_f32_e32 v159, v29, v159
	ds_write_b128 v209, v[156:159] offset:3072
	v_mul_f32_e32 v160, v30, v160
	v_mul_f32_e32 v161, v30, v161
	v_mul_f32_e32 v162, v30, v162
	v_mul_f32_e32 v163, v30, v163
	ds_write_b128 v209, v[160:163] offset:4096
	v_mul_f32_e32 v164, v31, v164
	v_mul_f32_e32 v165, v31, v165
	v_mul_f32_e32 v166, v31, v166
	v_mul_f32_e32 v167, v31, v167
	ds_write_b128 v209, v[164:167] offset:5120
	v_mul_f32_e32 v168, v32, v168
	v_mul_f32_e32 v169, v32, v169
	v_mul_f32_e32 v170, v32, v170
	v_mul_f32_e32 v171, v32, v171
	ds_write_b128 v209, v[168:171] offset:6144
	v_mul_f32_e32 v172, v33, v172
	v_mul_f32_e32 v173, v33, v173
	v_mul_f32_e32 v174, v33, v174
	v_mul_f32_e32 v175, v33, v175
	ds_write_b128 v209, v[172:175] offset:7168
	s_waitcnt lgkmcnt(0)
	s_barrier
; #define GAS __attribute__((address_space(1)))
; #define LAS __attribute__((address_space(3)))
; #define LDS_WAIT() asm volatile("s_waitcnt lgkmcnt(0)" ::: "memory")
; __device__ __forceinline__ unsigned pk4_fp8(float a, float b, float c, float d) {
;     a = fminf(fmaxf(a, -448.f), 448.f); b = fminf(fmaxf(b, -448.f), 448.f); c = fminf(fmaxf(c, -448.f), 448.f); d = fminf(fmaxf(d, -448.f), 448.f);
;     int w = __builtin_amdgcn_cvt_pk_fp8_f32(a, b, 0, false); w = __builtin_amdgcn_cvt_pk_fp8_f32(c, d, w, true); return (unsigned)w; }
;     const int pr = item >> 1, kb = 2 * (pr / nblk) + (item & 1), nb = pr % nblk, k0 = 64 * kb, n0 = 32 * nb;
;     const int nr = n0 + (lane & 31); const int sc = MAP == 1 ? src_col_in(nr) : nr;
;     float v[32];
; #pragma unroll
;     for (int i = 0; i < 32; ++i) v[i] = sc >= 0 ? W[(size_t)(k0 + 2 * i + (lane >> 5)) * Nsrc + sc] : 0.f;
; #pragma unroll
;     for (int i = 0; i < 32; ++i) { const int k = k0 + 2 * i + (lane >> 5); float x = v[i] * wscale; if (KS) x *= (k < ksplit ? ksA[k] : ksB[k - ksplit]); scr[(2 * i + (lane >> 5)) * 33 + (lane & 31)] = x; }
;     LDS_WAIT(); asm volatile("" ::: "memory");
;     const int c = lane & 7;
; #pragma unroll
;     for (int j = 0; j < 4; ++j) { const int n = (lane >> 3) + 8 * j; const LAS float* s = scr + (8 * c) * 33 + n;
;         const unsigned long long o = (unsigned long long)pg8::pk4_fp8(s[0 * 33], s[1 * 33], s[2 * 33], s[3 * 33]) | ((unsigned long long)pg8::pk4_fp8(s[4 * 33], s[5 * 33], s[6 * 33], s[7 * 33]) << 32);
;         *(GAS unsigned long long*)(WT + (size_t)(n0 + n) * K + k0 + 8 * c) = o; }
;     LDS_WAIT(); asm volatile("" ::: "memory");
; }
	s_add_u32 s8, s30, 0xc000
	s_addc_u32 s9, s31, 0
	global_load_dwordx4 v[144:147], v74, s[8:9]
	s_add_u32 s8, s8, 0x20000
	s_addc_u32 s9, s9, 0
	global_load_dwordx4 v[148:151], v74, s[8:9]
	s_add_u32 s8, s8, 0x20000
	s_addc_u32 s9, s9, 0
	global_load_dwordx4 v[152:155], v74, s[8:9]
	s_add_u32 s8, s8, 0x20000
	s_addc_u32 s9, s9, 0
	global_load_dwordx4 v[156:159], v74, s[8:9]
	s_add_u32 s8, s8, 0x20000
	s_addc_u32 s9, s9, 0
	global_load_dwordx4 v[160:163], v74, s[8:9]
	s_add_u32 s8, s8, 0x20000
	s_addc_u32 s9, s9, 0
	global_load_dwordx4 v[164:167], v74, s[8:9]
	s_add_u32 s8, s8, 0x20000
	s_addc_u32 s9, s9, 0
	global_load_dwordx4 v[168:171], v74, s[8:9]
	s_add_u32 s8, s8, 0x20000
	s_addc_u32 s9, s9, 0
	global_load_dwordx4 v[172:175], v74, s[8:9]
	s_add_u32 s6, s32, 0x2800000
	s_addc_u32 s7, s33, 0
	ds_read_b32 v226, v211
	ds_read_b32 v227, v211 offset:512
	ds_read_b32 v228, v211 offset:1024
	ds_read_b32 v229, v211 offset:1536
	ds_read_b32 v230, v211 offset:2048
	ds_read_b32 v231, v211 offset:2560
	ds_read_b32 v232, v211 offset:3072
	ds_read_b32 v233, v211 offset:3584
	ds_read_b32 v234, v211 offset:4096
	ds_read_b32 v235, v211 offset:4608
	ds_read_b32 v236, v211 offset:5120
	ds_read_b32 v237, v211 offset:5632
	ds_read_b32 v238, v211 offset:6144
	ds_read_b32 v239, v211 offset:6656
	ds_read_b32 v240, v211 offset:7168
	ds_read_b32 v241, v211 offset:7680
	s_waitcnt lgkmcnt(0)
	v_max_f32_e32 v226, v226, v226
	v_max_f32_e32 v227, v227, v227
	v_max_f32_e32 v228, v228, v228
	v_max_f32_e32 v229, v229, v229
	v_max_f32_e32 v230, v230, v230
	v_max_f32_e32 v231, v231, v231
	v_max_f32_e32 v232, v232, v232
	v_max_f32_e32 v233, v233, v233
	v_max_f32_e32 v234, v234, v234
	v_max_f32_e32 v235, v235, v235
	v_max_f32_e32 v236, v236, v236
	v_max_f32_e32 v237, v237, v237
	v_max_f32_e32 v238, v238, v238
	v_max_f32_e32 v239, v239, v239
	v_max_f32_e32 v240, v240, v240
	v_max_f32_e32 v241, v241, v241
	v_med3_f32 v226, v226, s62, v95
	v_med3_f32 v227, v227, s62, v95
	v_med3_f32 v228, v228, s62, v95
	v_med3_f32 v229, v229, s62, v95
	v_med3_f32 v230, v230, s62, v95
	v_med3_f32 v231, v231, s62, v95
	v_med3_f32 v232, v232, s62, v95
	v_med3_f32 v233, v233, s62, v95
	v_med3_f32 v234, v234, s62, v95
	v_med3_f32 v235, v235, s62, v95
	v_med3_f32 v236, v236, s62, v95
	v_med3_f32 v237, v237, s62, v95
	v_med3_f32 v238, v238, s62, v95
	v_med3_f32 v239, v239, s62, v95
	v_med3_f32 v240, v240, s62, v95
	v_med3_f32 v241, v241, s62, v95
	v_mov_b32_e32 v242, 0
	v_mov_b32_e32 v243, 0
	v_mov_b32_e32 v244, 0
	v_mov_b32_e32 v245, 0
	v_cvt_pk_fp8_f32 v242, v226, v227
	v_cvt_pk_fp8_f32 v243, v230, v231
	v_cvt_pk_fp8_f32 v244, v234, v235
	v_cvt_pk_fp8_f32 v245, v238, v239
	v_cvt_pk_fp8_f32 v242, v228, v229 op_sel:[0,0,1]
	v_cvt_pk_fp8_f32 v243, v232, v233 op_sel:[0,0,1]
	v_cvt_pk_fp8_f32 v244, v236, v237 op_sel:[0,0,1]
	v_cvt_pk_fp8_f32 v245, v240, v241 op_sel:[0,0,1]
	s_nop 0
	global_store_dwordx4 v77, v[242:245], s[6:7]
	ds_read_b32 v226, v213
	ds_read_b32 v227, v213 offset:512
	ds_read_b32 v228, v213 offset:1024
	ds_read_b32 v229, v213 offset:1536
	ds_read_b32 v230, v213 offset:2048
	ds_read_b32 v231, v213 offset:2560
	ds_read_b32 v232, v213 offset:3072
	ds_read_b32 v233, v213 offset:3584
	ds_read_b32 v234, v213 offset:4096
	ds_read_b32 v235, v213 offset:4608
	ds_read_b32 v236, v213 offset:5120
	ds_read_b32 v237, v213 offset:5632
	ds_read_b32 v238, v213 offset:6144
	ds_read_b32 v239, v213 offset:6656
	ds_read_b32 v240, v213 offset:7168
	ds_read_b32 v241, v213 offset:7680
	s_waitcnt lgkmcnt(0)
	v_max_f32_e32 v226, v226, v226
	v_max_f32_e32 v227, v227, v227
	v_max_f32_e32 v228, v228, v228
	v_max_f32_e32 v229, v229, v229
	v_max_f32_e32 v230, v230, v230
	v_max_f32_e32 v231, v231, v231
	v_max_f32_e32 v232, v232, v232
	v_max_f32_e32 v233, v233, v233
	v_max_f32_e32 v234, v234, v234
	v_max_f32_e32 v235, v235, v235
	v_max_f32_e32 v236, v236, v236
	v_max_f32_e32 v237, v237, v237
	v_max_f32_e32 v238, v238, v238
	v_max_f32_e32 v239, v239, v239
	v_max_f32_e32 v240, v240, v240
	v_max_f32_e32 v241, v241, v241
	v_med3_f32 v226, v226, s62, v95
	v_med3_f32 v227, v227, s62, v95
	v_med3_f32 v228, v228, s62, v95
	v_med3_f32 v229, v229, s62, v95
	v_med3_f32 v230, v230, s62, v95
	v_med3_f32 v231, v231, s62, v95
	v_med3_f32 v232, v232, s62, v95
	v_med3_f32 v233, v233, s62, v95
	v_med3_f32 v234, v234, s62, v95
	v_med3_f32 v235, v235, s62, v95
	v_med3_f32 v236, v236, s62, v95
	v_med3_f32 v237, v237, s62, v95
	v_med3_f32 v238, v238, s62, v95
	v_med3_f32 v239, v239, s62, v95
	v_med3_f32 v240, v240, s62, v95
	v_med3_f32 v241, v241, s62, v95
	v_mov_b32_e32 v242, 0
	v_mov_b32_e32 v243, 0
	v_mov_b32_e32 v244, 0
	v_mov_b32_e32 v245, 0
	v_cvt_pk_fp8_f32 v242, v226, v227
	v_cvt_pk_fp8_f32 v243, v230, v231
	v_cvt_pk_fp8_f32 v244, v234, v235
	v_cvt_pk_fp8_f32 v245, v238, v239
	v_cvt_pk_fp8_f32 v242, v228, v229 op_sel:[0,0,1]
	v_cvt_pk_fp8_f32 v243, v232, v233 op_sel:[0,0,1]
	v_cvt_pk_fp8_f32 v244, v236, v237 op_sel:[0,0,1]
	v_cvt_pk_fp8_f32 v245, v240, v241 op_sel:[0,0,1]
	s_nop 0
	global_store_dwordx4 v78, v[242:245], s[6:7]
	s_waitcnt vmcnt(12)
	v_mul_f32_e32 v176, v26, v176
	v_mul_f32_e32 v177, v26, v177
	v_mul_f32_e32 v178, v26, v178
	v_mul_f32_e32 v179, v26, v179
	ds_write_b128 v210, v[176:179]
	v_mul_f32_e32 v180, v27, v180
	v_mul_f32_e32 v181, v27, v181
	v_mul_f32_e32 v182, v27, v182
	v_mul_f32_e32 v183, v27, v183
	ds_write_b128 v210, v[180:183] offset:1024
	v_mul_f32_e32 v184, v28, v184
	v_mul_f32_e32 v185, v28, v185
	v_mul_f32_e32 v186, v28, v186
	v_mul_f32_e32 v187, v28, v187
	ds_write_b128 v210, v[184:187] offset:2048
	v_mul_f32_e32 v188, v29, v188
	v_mul_f32_e32 v189, v29, v189
	v_mul_f32_e32 v190, v29, v190
	v_mul_f32_e32 v191, v29, v191
	ds_write_b128 v210, v[188:191] offset:3072
	v_mul_f32_e32 v192, v30, v192
	v_mul_f32_e32 v193, v30, v193
	v_mul_f32_e32 v194, v30, v194
	v_mul_f32_e32 v195, v30, v195
	ds_write_b128 v210, v[192:195] offset:4096
	v_mul_f32_e32 v196, v31, v196
	v_mul_f32_e32 v197, v31, v197
	v_mul_f32_e32 v198, v31, v198
	v_mul_f32_e32 v199, v31, v199
	ds_write_b128 v210, v[196:199] offset:5120
	v_mul_f32_e32 v200, v32, v200
	v_mul_f32_e32 v201, v32, v201
	v_mul_f32_e32 v202, v32, v202
	v_mul_f32_e32 v203, v32, v203
	ds_write_b128 v210, v[200:203] offset:6144
	v_mul_f32_e32 v204, v33, v204
	v_mul_f32_e32 v205, v33, v205
	v_mul_f32_e32 v206, v33, v206
	v_mul_f32_e32 v207, v33, v207
	ds_write_b128 v210, v[204:207] offset:7168
	s_waitcnt lgkmcnt(0)
	s_barrier
; #define GAS __attribute__((address_space(1)))
; #define LAS __attribute__((address_space(3)))
; #define LDS_WAIT() asm volatile("s_waitcnt lgkmcnt(0)" ::: "memory")
; __device__ __forceinline__ unsigned pk4_fp8(float a, float b, float c, float d) {
;     a = fminf(fmaxf(a, -448.f), 448.f); b = fminf(fmaxf(b, -448.f), 448.f); c = fminf(fmaxf(c, -448.f), 448.f); d = fminf(fmaxf(d, -448.f), 448.f);
;     int w = __builtin_amdgcn_cvt_pk_fp8_f32(a, b, 0, false); w = __builtin_amdgcn_cvt_pk_fp8_f32(c, d, w, true); return (unsigned)w; }
;     const int pr = item >> 1, kb = 2 * (pr / nblk) + (item & 1), nb = pr % nblk, k0 = 64 * kb, n0 = 32 * nb;
;     const int nr = n0 + (lane & 31); const int sc = MAP == 1 ? src_col_in(nr) : nr;
;     float v[32];
; #pragma unroll
;     for (int i = 0; i < 32; ++i) v[i] = sc >= 0 ? W[(size_t)(k0 + 2 * i + (lane >> 5)) * Nsrc + sc] : 0.f;
; #pragma unroll
;     for (int i = 0; i < 32; ++i) { const int k = k0 + 2 * i + (lane >> 5); float x = v[i] * wscale; if (KS) x *= (k < ksplit ? ksA[k] : ksB[k - ksplit]); scr[(2 * i + (lane >> 5)) * 33 + (lane & 31)] = x; }
;     LDS_WAIT(); asm volatile("" ::: "memory");
;     const int c = lane & 7;
; #pragma unroll
;     for (int j = 0; j < 4; ++j) { const int n = (lane >> 3) + 8 * j; const LAS float* s = scr + (8 * c) * 33 + n;
;         const unsigned long long o = (unsigned long long)pg8::pk4_fp8(s[0 * 33], s[1 * 33], s[2 * 33], s[3 * 33]) | ((unsigned long long)pg8::pk4_fp8(s[4 * 33], s[5 * 33], s[6 * 33], s[7 * 33]) << 32);
;         *(GAS unsigned long long*)(WT + (size_t)(n0 + n) * K + k0 + 8 * c) = o; }
;     LDS_WAIT(); asm volatile("" ::: "memory");
; }
	s_add_u32 s8, s30, 0xd000
	s_addc_u32 s9, s31, 0
	global_load_dwordx4 v[176:179], v74, s[8:9]
	s_add_u32 s8, s8, 0x20000
	s_addc_u32 s9, s9, 0
	global_load_dwordx4 v[180:183], v74, s[8:9]
	s_add_u32 s8, s8, 0x20000
	s_addc_u32 s9, s9, 0
	global_load_dwordx4 v[184:187], v74, s[8:9]
	s_add_u32 s8, s8, 0x20000
	s_addc_u32 s9, s9, 0
	global_load_dwordx4 v[188:191], v74, s[8:9]
	s_add_u32 s8, s8, 0x20000
	s_addc_u32 s9, s9, 0
	global_load_dwordx4 v[192:195], v74, s[8:9]
	s_add_u32 s8, s8, 0x20000
	s_addc_u32 s9, s9, 0
	global_load_dwordx4 v[196:199], v74, s[8:9]
	s_add_u32 s8, s8, 0x20000
	s_addc_u32 s9, s9, 0
	global_load_dwordx4 v[200:203], v74, s[8:9]
	s_add_u32 s8, s8, 0x20000
	s_addc_u32 s9, s9, 0
	global_load_dwordx4 v[204:207], v74, s[8:9]
	s_add_u32 s6, s32, 0x2c00000
	s_addc_u32 s7, s33, 0
	ds_read_b32 v226, v212
	ds_read_b32 v227, v212 offset:512
	ds_read_b32 v228, v212 offset:1024
	ds_read_b32 v229, v212 offset:1536
	ds_read_b32 v230, v212 offset:2048
	ds_read_b32 v231, v212 offset:2560
	ds_read_b32 v232, v212 offset:3072
	ds_read_b32 v233, v212 offset:3584
	ds_read_b32 v234, v212 offset:4096
	ds_read_b32 v235, v212 offset:4608
	ds_read_b32 v236, v212 offset:5120
	ds_read_b32 v237, v212 offset:5632
	ds_read_b32 v238, v212 offset:6144
	ds_read_b32 v239, v212 offset:6656
	ds_read_b32 v240, v212 offset:7168
	ds_read_b32 v241, v212 offset:7680
	s_waitcnt lgkmcnt(0)
	v_max_f32_e32 v226, v226, v226
	v_max_f32_e32 v227, v227, v227
	v_max_f32_e32 v228, v228, v228
	v_max_f32_e32 v229, v229, v229
	v_max_f32_e32 v230, v230, v230
	v_max_f32_e32 v231, v231, v231
	v_max_f32_e32 v232, v232, v232
	v_max_f32_e32 v233, v233, v233
	v_max_f32_e32 v234, v234, v234
	v_max_f32_e32 v235, v235, v235
	v_max_f32_e32 v236, v236, v236
	v_max_f32_e32 v237, v237, v237
	v_max_f32_e32 v238, v238, v238
	v_max_f32_e32 v239, v239, v239
	v_max_f32_e32 v240, v240, v240
	v_max_f32_e32 v241, v241, v241
	v_med3_f32 v226, v226, s62, v95
	v_med3_f32 v227, v227, s62, v95
	v_med3_f32 v228, v228, s62, v95
	v_med3_f32 v229, v229, s62, v95
	v_med3_f32 v230, v230, s62, v95
	v_med3_f32 v231, v231, s62, v95
	v_med3_f32 v232, v232, s62, v95
	v_med3_f32 v233, v233, s62, v95
	v_med3_f32 v234, v234, s62, v95
	v_med3_f32 v235, v235, s62, v95
	v_med3_f32 v236, v236, s62, v95
	v_med3_f32 v237, v237, s62, v95
	v_med3_f32 v238, v238, s62, v95
	v_med3_f32 v239, v239, s62, v95
	v_med3_f32 v240, v240, s62, v95
	v_med3_f32 v241, v241, s62, v95
	v_mov_b32_e32 v242, 0
	v_mov_b32_e32 v243, 0
	v_mov_b32_e32 v244, 0
	v_mov_b32_e32 v245, 0
	v_cvt_pk_fp8_f32 v242, v226, v227
	v_cvt_pk_fp8_f32 v243, v230, v231
	v_cvt_pk_fp8_f32 v244, v234, v235
	v_cvt_pk_fp8_f32 v245, v238, v239
	v_cvt_pk_fp8_f32 v242, v228, v229 op_sel:[0,0,1]
	v_cvt_pk_fp8_f32 v243, v232, v233 op_sel:[0,0,1]
	v_cvt_pk_fp8_f32 v244, v236, v237 op_sel:[0,0,1]
	v_cvt_pk_fp8_f32 v245, v240, v241 op_sel:[0,0,1]
	s_nop 0
	global_store_dwordx4 v77, v[242:245], s[6:7]
	ds_read_b32 v226, v214
	ds_read_b32 v227, v214 offset:512
	ds_read_b32 v228, v214 offset:1024
	ds_read_b32 v229, v214 offset:1536
	ds_read_b32 v230, v214 offset:2048
	ds_read_b32 v231, v214 offset:2560
	ds_read_b32 v232, v214 offset:3072
	ds_read_b32 v233, v214 offset:3584
	ds_read_b32 v234, v214 offset:4096
	ds_read_b32 v235, v214 offset:4608
	ds_read_b32 v236, v214 offset:5120
	ds_read_b32 v237, v214 offset:5632
	ds_read_b32 v238, v214 offset:6144
	ds_read_b32 v239, v214 offset:6656
	ds_read_b32 v240, v214 offset:7168
	ds_read_b32 v241, v214 offset:7680
	s_waitcnt lgkmcnt(0)
	v_max_f32_e32 v226, v226, v226
	v_max_f32_e32 v227, v227, v227
	v_max_f32_e32 v228, v228, v228
	v_max_f32_e32 v229, v229, v229
	v_max_f32_e32 v230, v230, v230
	v_max_f32_e32 v231, v231, v231
	v_max_f32_e32 v232, v232, v232
	v_max_f32_e32 v233, v233, v233
	v_max_f32_e32 v234, v234, v234
	v_max_f32_e32 v235, v235, v235
	v_max_f32_e32 v236, v236, v236
	v_max_f32_e32 v237, v237, v237
	v_max_f32_e32 v238, v238, v238
	v_max_f32_e32 v239, v239, v239
	v_max_f32_e32 v240, v240, v240
	v_max_f32_e32 v241, v241, v241
	v_med3_f32 v226, v226, s62, v95
	v_med3_f32 v227, v227, s62, v95
	v_med3_f32 v228, v228, s62, v95
	v_med3_f32 v229, v229, s62, v95
	v_med3_f32 v230, v230, s62, v95
	v_med3_f32 v231, v231, s62, v95
	v_med3_f32 v232, v232, s62, v95
	v_med3_f32 v233, v233, s62, v95
	v_med3_f32 v234, v234, s62, v95
	v_med3_f32 v235, v235, s62, v95
	v_med3_f32 v236, v236, s62, v95
	v_med3_f32 v237, v237, s62, v95
	v_med3_f32 v238, v238, s62, v95
	v_med3_f32 v239, v239, s62, v95
	v_med3_f32 v240, v240, s62, v95
	v_med3_f32 v241, v241, s62, v95
	v_mov_b32_e32 v242, 0
	v_mov_b32_e32 v243, 0
	v_mov_b32_e32 v244, 0
	v_mov_b32_e32 v245, 0
	v_cvt_pk_fp8_f32 v242, v226, v227
	v_cvt_pk_fp8_f32 v243, v230, v231
	v_cvt_pk_fp8_f32 v244, v234, v235
	v_cvt_pk_fp8_f32 v245, v238, v239
	v_cvt_pk_fp8_f32 v242, v228, v229 op_sel:[0,0,1]
	v_cvt_pk_fp8_f32 v243, v232, v233 op_sel:[0,0,1]
	v_cvt_pk_fp8_f32 v244, v236, v237 op_sel:[0,0,1]
	v_cvt_pk_fp8_f32 v245, v240, v241 op_sel:[0,0,1]
	s_nop 0
	global_store_dwordx4 v78, v[242:245], s[6:7]
	s_waitcnt vmcnt(12)
	v_mul_f32_e32 v144, v26, v144
	v_mul_f32_e32 v145, v26, v145
	v_mul_f32_e32 v146, v26, v146
	v_mul_f32_e32 v147, v26, v147
	ds_write_b128 v209, v[144:147]
	v_mul_f32_e32 v148, v27, v148
	v_mul_f32_e32 v149, v27, v149
	v_mul_f32_e32 v150, v27, v150
	v_mul_f32_e32 v151, v27, v151
	ds_write_b128 v209, v[148:151] offset:1024
	v_mul_f32_e32 v152, v28, v152
	v_mul_f32_e32 v153, v28, v153
	v_mul_f32_e32 v154, v28, v154
	v_mul_f32_e32 v155, v28, v155
	ds_write_b128 v209, v[152:155] offset:2048
	v_mul_f32_e32 v156, v29, v156
	v_mul_f32_e32 v157, v29, v157
	v_mul_f32_e32 v158, v29, v158
	v_mul_f32_e32 v159, v29, v159
	ds_write_b128 v209, v[156:159] offset:3072
	v_mul_f32_e32 v160, v30, v160
	v_mul_f32_e32 v161, v30, v161
	v_mul_f32_e32 v162, v30, v162
	v_mul_f32_e32 v163, v30, v163
	ds_write_b128 v209, v[160:163] offset:4096
	v_mul_f32_e32 v164, v31, v164
	v_mul_f32_e32 v165, v31, v165
	v_mul_f32_e32 v166, v31, v166
	v_mul_f32_e32 v167, v31, v167
	ds_write_b128 v209, v[164:167] offset:5120
	v_mul_f32_e32 v168, v32, v168
	v_mul_f32_e32 v169, v32, v169
	v_mul_f32_e32 v170, v32, v170
	v_mul_f32_e32 v171, v32, v171
	ds_write_b128 v209, v[168:171] offset:6144
	v_mul_f32_e32 v172, v33, v172
	v_mul_f32_e32 v173, v33, v173
	v_mul_f32_e32 v174, v33, v174
	v_mul_f32_e32 v175, v33, v175
	ds_write_b128 v209, v[172:175] offset:7168
	s_waitcnt lgkmcnt(0)
	s_barrier
; #define GAS __attribute__((address_space(1)))
; #define LAS __attribute__((address_space(3)))
; #define LDS_WAIT() asm volatile("s_waitcnt lgkmcnt(0)" ::: "memory")
; __device__ __forceinline__ unsigned pk4_fp8(float a, float b, float c, float d) {
;     a = fminf(fmaxf(a, -448.f), 448.f); b = fminf(fmaxf(b, -448.f), 448.f); c = fminf(fmaxf(c, -448.f), 448.f); d = fminf(fmaxf(d, -448.f), 448.f);
;     int w = __builtin_amdgcn_cvt_pk_fp8_f32(a, b, 0, false); w = __builtin_amdgcn_cvt_pk_fp8_f32(c, d, w, true); return (unsigned)w; }
;     const int pr = item >> 1, kb = 2 * (pr / nblk) + (item & 1), nb = pr % nblk, k0 = 64 * kb, n0 = 32 * nb;
;     const int nr = n0 + (lane & 31); const int sc = MAP == 1 ? src_col_in(nr) : nr;
;     float v[32];
; #pragma unroll
;     for (int i = 0; i < 32; ++i) v[i] = sc >= 0 ? W[(size_t)(k0 + 2 * i + (lane >> 5)) * Nsrc + sc] : 0.f;
; #pragma unroll
;     for (int i = 0; i < 32; ++i) { const int k = k0 + 2 * i + (lane >> 5); float x = v[i] * wscale; if (KS) x *= (k < ksplit ? ksA[k] : ksB[k - ksplit]); scr[(2 * i + (lane >> 5)) * 33 + (lane & 31)] = x; }
;     LDS_WAIT(); asm volatile("" ::: "memory");
;     const int c = lane & 7;
; #pragma unroll
;     for (int j = 0; j < 4; ++j) { const int n = (lane >> 3) + 8 * j; const LAS float* s = scr + (8 * c) * 33 + n;
;         const unsigned long long o = (unsigned long long)pg8::pk4_fp8(s[0 * 33], s[1 * 33], s[2 * 33], s[3 * 33]) | ((unsigned long long)pg8::pk4_fp8(s[4 * 33], s[5 * 33], s[6 * 33], s[7 * 33]) << 32);
;         *(GAS unsigned long long*)(WT + (size_t)(n0 + n) * K + k0 + 8 * c) = o; }
;     LDS_WAIT(); asm volatile("" ::: "memory");
; }
	s_add_u32 s8, s30, 0xe000
	s_addc_u32 s9, s31, 0
	global_load_dwordx4 v[144:147], v74, s[8:9]
	s_add_u32 s8, s8, 0x20000
	s_addc_u32 s9, s9, 0
	global_load_dwordx4 v[148:151], v74, s[8:9]
	s_add_u32 s8, s8, 0x20000
	s_addc_u32 s9, s9, 0
	global_load_dwordx4 v[152:155], v74, s[8:9]
	s_add_u32 s8, s8, 0x20000
	s_addc_u32 s9, s9, 0
	global_load_dwordx4 v[156:159], v74, s[8:9]
	s_add_u32 s8, s8, 0x20000
	s_addc_u32 s9, s9, 0
	global_load_dwordx4 v[160:163], v74, s[8:9]
	s_add_u32 s8, s8, 0x20000
	s_addc_u32 s9, s9, 0
	global_load_dwordx4 v[164:167], v74, s[8:9]
	s_add_u32 s8, s8, 0x20000
	s_addc_u32 s9, s9, 0
	global_load_dwordx4 v[168:171], v74, s[8:9]
	s_add_u32 s8, s8, 0x20000
	s_addc_u32 s9, s9, 0
	global_load_dwordx4 v[172:175], v74, s[8:9]
	s_add_u32 s6, s32, 0x3000000
	s_addc_u32 s7, s33, 0
	ds_read_b32 v226, v211
	ds_read_b32 v227, v211 offset:512
	ds_read_b32 v228, v211 offset:1024
	ds_read_b32 v229, v211 offset:1536
	ds_read_b32 v230, v211 offset:2048
	ds_read_b32 v231, v211 offset:2560
	ds_read_b32 v232, v211 offset:3072
	ds_read_b32 v233, v211 offset:3584
	ds_read_b32 v234, v211 offset:4096
	ds_read_b32 v235, v211 offset:4608
	ds_read_b32 v236, v211 offset:5120
	ds_read_b32 v237, v211 offset:5632
	ds_read_b32 v238, v211 offset:6144
	ds_read_b32 v239, v211 offset:6656
	ds_read_b32 v240, v211 offset:7168
	ds_read_b32 v241, v211 offset:7680
	s_waitcnt lgkmcnt(0)
	v_max_f32_e32 v226, v226, v226
	v_max_f32_e32 v227, v227, v227
	v_max_f32_e32 v228, v228, v228
	v_max_f32_e32 v229, v229, v229
	v_max_f32_e32 v230, v230, v230
	v_max_f32_e32 v231, v231, v231
	v_max_f32_e32 v232, v232, v232
	v_max_f32_e32 v233, v233, v233
	v_max_f32_e32 v234, v234, v234
	v_max_f32_e32 v235, v235, v235
	v_max_f32_e32 v236, v236, v236
	v_max_f32_e32 v237, v237, v237
	v_max_f32_e32 v238, v238, v238
	v_max_f32_e32 v239, v239, v239
	v_max_f32_e32 v240, v240, v240
	v_max_f32_e32 v241, v241, v241
	v_med3_f32 v226, v226, s62, v95
	v_med3_f32 v227, v227, s62, v95
	v_med3_f32 v228, v228, s62, v95
	v_med3_f32 v229, v229, s62, v95
	v_med3_f32 v230, v230, s62, v95
	v_med3_f32 v231, v231, s62, v95
	v_med3_f32 v232, v232, s62, v95
	v_med3_f32 v233, v233, s62, v95
	v_med3_f32 v234, v234, s62, v95
	v_med3_f32 v235, v235, s62, v95
	v_med3_f32 v236, v236, s62, v95
	v_med3_f32 v237, v237, s62, v95
	v_med3_f32 v238, v238, s62, v95
	v_med3_f32 v239, v239, s62, v95
	v_med3_f32 v240, v240, s62, v95
	v_med3_f32 v241, v241, s62, v95
	v_mov_b32_e32 v242, 0
	v_mov_b32_e32 v243, 0
	v_mov_b32_e32 v244, 0
	v_mov_b32_e32 v245, 0
	v_cvt_pk_fp8_f32 v242, v226, v227
	v_cvt_pk_fp8_f32 v243, v230, v231
	v_cvt_pk_fp8_f32 v244, v234, v235
	v_cvt_pk_fp8_f32 v245, v238, v239
	v_cvt_pk_fp8_f32 v242, v228, v229 op_sel:[0,0,1]
	v_cvt_pk_fp8_f32 v243, v232, v233 op_sel:[0,0,1]
	v_cvt_pk_fp8_f32 v244, v236, v237 op_sel:[0,0,1]
	v_cvt_pk_fp8_f32 v245, v240, v241 op_sel:[0,0,1]
	s_nop 0
	global_store_dwordx4 v77, v[242:245], s[6:7]
	ds_read_b32 v226, v213
	ds_read_b32 v227, v213 offset:512
	ds_read_b32 v228, v213 offset:1024
	ds_read_b32 v229, v213 offset:1536
	ds_read_b32 v230, v213 offset:2048
	ds_read_b32 v231, v213 offset:2560
	ds_read_b32 v232, v213 offset:3072
	ds_read_b32 v233, v213 offset:3584
	ds_read_b32 v234, v213 offset:4096
	ds_read_b32 v235, v213 offset:4608
	ds_read_b32 v236, v213 offset:5120
	ds_read_b32 v237, v213 offset:5632
	ds_read_b32 v238, v213 offset:6144
	ds_read_b32 v239, v213 offset:6656
	ds_read_b32 v240, v213 offset:7168
	ds_read_b32 v241, v213 offset:7680
	s_waitcnt lgkmcnt(0)
	v_max_f32_e32 v226, v226, v226
	v_max_f32_e32 v227, v227, v227
	v_max_f32_e32 v228, v228, v228
	v_max_f32_e32 v229, v229, v229
	v_max_f32_e32 v230, v230, v230
	v_max_f32_e32 v231, v231, v231
	v_max_f32_e32 v232, v232, v232
	v_max_f32_e32 v233, v233, v233
	v_max_f32_e32 v234, v234, v234
	v_max_f32_e32 v235, v235, v235
	v_max_f32_e32 v236, v236, v236
	v_max_f32_e32 v237, v237, v237
	v_max_f32_e32 v238, v238, v238
	v_max_f32_e32 v239, v239, v239
	v_max_f32_e32 v240, v240, v240
	v_max_f32_e32 v241, v241, v241
	v_med3_f32 v226, v226, s62, v95
	v_med3_f32 v227, v227, s62, v95
	v_med3_f32 v228, v228, s62, v95
	v_med3_f32 v229, v229, s62, v95
	v_med3_f32 v230, v230, s62, v95
	v_med3_f32 v231, v231, s62, v95
	v_med3_f32 v232, v232, s62, v95
	v_med3_f32 v233, v233, s62, v95
	v_med3_f32 v234, v234, s62, v95
	v_med3_f32 v235, v235, s62, v95
	v_med3_f32 v236, v236, s62, v95
	v_med3_f32 v237, v237, s62, v95
	v_med3_f32 v238, v238, s62, v95
	v_med3_f32 v239, v239, s62, v95
	v_med3_f32 v240, v240, s62, v95
	v_med3_f32 v241, v241, s62, v95
	v_mov_b32_e32 v242, 0
	v_mov_b32_e32 v243, 0
	v_mov_b32_e32 v244, 0
	v_mov_b32_e32 v245, 0
	v_cvt_pk_fp8_f32 v242, v226, v227
	v_cvt_pk_fp8_f32 v243, v230, v231
	v_cvt_pk_fp8_f32 v244, v234, v235
	v_cvt_pk_fp8_f32 v245, v238, v239
	v_cvt_pk_fp8_f32 v242, v228, v229 op_sel:[0,0,1]
	v_cvt_pk_fp8_f32 v243, v232, v233 op_sel:[0,0,1]
	v_cvt_pk_fp8_f32 v244, v236, v237 op_sel:[0,0,1]
	v_cvt_pk_fp8_f32 v245, v240, v241 op_sel:[0,0,1]
	s_nop 0
	global_store_dwordx4 v78, v[242:245], s[6:7]
	s_waitcnt vmcnt(12)
	v_mul_f32_e32 v176, v26, v176
	v_mul_f32_e32 v177, v26, v177
	v_mul_f32_e32 v178, v26, v178
	v_mul_f32_e32 v179, v26, v179
	ds_write_b128 v210, v[176:179]
	v_mul_f32_e32 v180, v27, v180
	v_mul_f32_e32 v181, v27, v181
	v_mul_f32_e32 v182, v27, v182
	v_mul_f32_e32 v183, v27, v183
	ds_write_b128 v210, v[180:183] offset:1024
	v_mul_f32_e32 v184, v28, v184
	v_mul_f32_e32 v185, v28, v185
	v_mul_f32_e32 v186, v28, v186
	v_mul_f32_e32 v187, v28, v187
	ds_write_b128 v210, v[184:187] offset:2048
	v_mul_f32_e32 v188, v29, v188
	v_mul_f32_e32 v189, v29, v189
	v_mul_f32_e32 v190, v29, v190
	v_mul_f32_e32 v191, v29, v191
	ds_write_b128 v210, v[188:191] offset:3072
	v_mul_f32_e32 v192, v30, v192
	v_mul_f32_e32 v193, v30, v193
	v_mul_f32_e32 v194, v30, v194
	v_mul_f32_e32 v195, v30, v195
	ds_write_b128 v210, v[192:195] offset:4096
	v_mul_f32_e32 v196, v31, v196
	v_mul_f32_e32 v197, v31, v197
	v_mul_f32_e32 v198, v31, v198
	v_mul_f32_e32 v199, v31, v199
	ds_write_b128 v210, v[196:199] offset:5120
	v_mul_f32_e32 v200, v32, v200
	v_mul_f32_e32 v201, v32, v201
	v_mul_f32_e32 v202, v32, v202
	v_mul_f32_e32 v203, v32, v203
	ds_write_b128 v210, v[200:203] offset:6144
	v_mul_f32_e32 v204, v33, v204
	v_mul_f32_e32 v205, v33, v205
	v_mul_f32_e32 v206, v33, v206
	v_mul_f32_e32 v207, v33, v207
	ds_write_b128 v210, v[204:207] offset:7168
	s_waitcnt lgkmcnt(0)
	s_barrier
; #define GAS __attribute__((address_space(1)))
; #define LAS __attribute__((address_space(3)))
; #define LDS_WAIT() asm volatile("s_waitcnt lgkmcnt(0)" ::: "memory")
; __device__ __forceinline__ unsigned pk4_fp8(float a, float b, float c, float d) {
;     a = fminf(fmaxf(a, -448.f), 448.f); b = fminf(fmaxf(b, -448.f), 448.f); c = fminf(fmaxf(c, -448.f), 448.f); d = fminf(fmaxf(d, -448.f), 448.f);
;     int w = __builtin_amdgcn_cvt_pk_fp8_f32(a, b, 0, false); w = __builtin_amdgcn_cvt_pk_fp8_f32(c, d, w, true); return (unsigned)w; }
;     const int pr = item >> 1, kb = 2 * (pr / nblk) + (item & 1), nb = pr % nblk, k0 = 64 * kb, n0 = 32 * nb;
;     const int nr = n0 + (lane & 31); const int sc = MAP == 1 ? src_col_in(nr) : nr;
;     float v[32];
; #pragma unroll
;     for (int i = 0; i < 32; ++i) v[i] = sc >= 0 ? W[(size_t)(k0 + 2 * i + (lane >> 5)) * Nsrc + sc] : 0.f;
; #pragma unroll
;     for (int i = 0; i < 32; ++i) { const int k = k0 + 2 * i + (lane >> 5); float x = v[i] * wscale; if (KS) x *= (k < ksplit ? ksA[k] : ksB[k - ksplit]); scr[(2 * i + (lane >> 5)) * 33 + (lane & 31)] = x; }
;     LDS_WAIT(); asm volatile("" ::: "memory");
;     const int c = lane & 7;
; #pragma unroll
;     for (int j = 0; j < 4; ++j) { const int n = (lane >> 3) + 8 * j; const LAS float* s = scr + (8 * c) * 33 + n;
;         const unsigned long long o = (unsigned long long)pg8::pk4_fp8(s[0 * 33], s[1 * 33], s[2 * 33], s[3 * 33]) | ((unsigned long long)pg8::pk4_fp8(s[4 * 33], s[5 * 33], s[6 * 33], s[7 * 33]) << 32);
;         *(GAS unsigned long long*)(WT + (size_t)(n0 + n) * K + k0 + 8 * c) = o; }
;     LDS_WAIT(); asm volatile("" ::: "memory");
; }
	s_add_u32 s8, s30, 0xf000
	s_addc_u32 s9, s31, 0
	global_load_dwordx4 v[176:179], v74, s[8:9]
	s_add_u32 s8, s8, 0x20000
	s_addc_u32 s9, s9, 0
	global_load_dwordx4 v[180:183], v74, s[8:9]
	s_add_u32 s8, s8, 0x20000
	s_addc_u32 s9, s9, 0
	global_load_dwordx4 v[184:187], v74, s[8:9]
	s_add_u32 s8, s8, 0x20000
	s_addc_u32 s9, s9, 0
	global_load_dwordx4 v[188:191], v74, s[8:9]
	s_add_u32 s8, s8, 0x20000
	s_addc_u32 s9, s9, 0
	global_load_dwordx4 v[192:195], v74, s[8:9]
	s_add_u32 s8, s8, 0x20000
	s_addc_u32 s9, s9, 0
	global_load_dwordx4 v[196:199], v74, s[8:9]
	s_add_u32 s8, s8, 0x20000
	s_addc_u32 s9, s9, 0
	global_load_dwordx4 v[200:203], v74, s[8:9]
	s_add_u32 s8, s8, 0x20000
	s_addc_u32 s9, s9, 0
	global_load_dwordx4 v[204:207], v74, s[8:9]
	s_add_u32 s6, s32, 0x3400000
	s_addc_u32 s7, s33, 0
	ds_read_b32 v226, v212
	ds_read_b32 v227, v212 offset:512
	ds_read_b32 v228, v212 offset:1024
	ds_read_b32 v229, v212 offset:1536
	ds_read_b32 v230, v212 offset:2048
	ds_read_b32 v231, v212 offset:2560
	ds_read_b32 v232, v212 offset:3072
	ds_read_b32 v233, v212 offset:3584
	ds_read_b32 v234, v212 offset:4096
	ds_read_b32 v235, v212 offset:4608
	ds_read_b32 v236, v212 offset:5120
	ds_read_b32 v237, v212 offset:5632
	ds_read_b32 v238, v212 offset:6144
	ds_read_b32 v239, v212 offset:6656
	ds_read_b32 v240, v212 offset:7168
	ds_read_b32 v241, v212 offset:7680
	s_waitcnt lgkmcnt(0)
	v_max_f32_e32 v226, v226, v226
	v_max_f32_e32 v227, v227, v227
	v_max_f32_e32 v228, v228, v228
	v_max_f32_e32 v229, v229, v229
	v_max_f32_e32 v230, v230, v230
	v_max_f32_e32 v231, v231, v231
	v_max_f32_e32 v232, v232, v232
	v_max_f32_e32 v233, v233, v233
	v_max_f32_e32 v234, v234, v234
	v_max_f32_e32 v235, v235, v235
	v_max_f32_e32 v236, v236, v236
	v_max_f32_e32 v237, v237, v237
	v_max_f32_e32 v238, v238, v238
	v_max_f32_e32 v239, v239, v239
	v_max_f32_e32 v240, v240, v240
	v_max_f32_e32 v241, v241, v241
	v_med3_f32 v226, v226, s62, v95
	v_med3_f32 v227, v227, s62, v95
	v_med3_f32 v228, v228, s62, v95
	v_med3_f32 v229, v229, s62, v95
	v_med3_f32 v230, v230, s62, v95
	v_med3_f32 v231, v231, s62, v95
	v_med3_f32 v232, v232, s62, v95
	v_med3_f32 v233, v233, s62, v95
	v_med3_f32 v234, v234, s62, v95
	v_med3_f32 v235, v235, s62, v95
	v_med3_f32 v236, v236, s62, v95
	v_med3_f32 v237, v237, s62, v95
	v_med3_f32 v238, v238, s62, v95
	v_med3_f32 v239, v239, s62, v95
	v_med3_f32 v240, v240, s62, v95
	v_med3_f32 v241, v241, s62, v95
	v_mov_b32_e32 v242, 0
	v_mov_b32_e32 v243, 0
	v_mov_b32_e32 v244, 0
	v_mov_b32_e32 v245, 0
	v_cvt_pk_fp8_f32 v242, v226, v227
	v_cvt_pk_fp8_f32 v243, v230, v231
	v_cvt_pk_fp8_f32 v244, v234, v235
	v_cvt_pk_fp8_f32 v245, v238, v239
	v_cvt_pk_fp8_f32 v242, v228, v229 op_sel:[0,0,1]
	v_cvt_pk_fp8_f32 v243, v232, v233 op_sel:[0,0,1]
	v_cvt_pk_fp8_f32 v244, v236, v237 op_sel:[0,0,1]
	v_cvt_pk_fp8_f32 v245, v240, v241 op_sel:[0,0,1]
	s_nop 0
	global_store_dwordx4 v77, v[242:245], s[6:7]
	ds_read_b32 v226, v214
	ds_read_b32 v227, v214 offset:512
	ds_read_b32 v228, v214 offset:1024
	ds_read_b32 v229, v214 offset:1536
	ds_read_b32 v230, v214 offset:2048
	ds_read_b32 v231, v214 offset:2560
	ds_read_b32 v232, v214 offset:3072
	ds_read_b32 v233, v214 offset:3584
	ds_read_b32 v234, v214 offset:4096
	ds_read_b32 v235, v214 offset:4608
	ds_read_b32 v236, v214 offset:5120
	ds_read_b32 v237, v214 offset:5632
	ds_read_b32 v238, v214 offset:6144
	ds_read_b32 v239, v214 offset:6656
	ds_read_b32 v240, v214 offset:7168
	ds_read_b32 v241, v214 offset:7680
	s_waitcnt lgkmcnt(0)
	v_max_f32_e32 v226, v226, v226
	v_max_f32_e32 v227, v227, v227
	v_max_f32_e32 v228, v228, v228
	v_max_f32_e32 v229, v229, v229
	v_max_f32_e32 v230, v230, v230
	v_max_f32_e32 v231, v231, v231
	v_max_f32_e32 v232, v232, v232
	v_max_f32_e32 v233, v233, v233
	v_max_f32_e32 v234, v234, v234
	v_max_f32_e32 v235, v235, v235
	v_max_f32_e32 v236, v236, v236
	v_max_f32_e32 v237, v237, v237
	v_max_f32_e32 v238, v238, v238
	v_max_f32_e32 v239, v239, v239
	v_max_f32_e32 v240, v240, v240
	v_max_f32_e32 v241, v241, v241
	v_med3_f32 v226, v226, s62, v95
	v_med3_f32 v227, v227, s62, v95
	v_med3_f32 v228, v228, s62, v95
	v_med3_f32 v229, v229, s62, v95
	v_med3_f32 v230, v230, s62, v95
	v_med3_f32 v231, v231, s62, v95
	v_med3_f32 v232, v232, s62, v95
	v_med3_f32 v233, v233, s62, v95
	v_med3_f32 v234, v234, s62, v95
	v_med3_f32 v235, v235, s62, v95
	v_med3_f32 v236, v236, s62, v95
	v_med3_f32 v237, v237, s62, v95
	v_med3_f32 v238, v238, s62, v95
	v_med3_f32 v239, v239, s62, v95
	v_med3_f32 v240, v240, s62, v95
	v_med3_f32 v241, v241, s62, v95
	v_mov_b32_e32 v242, 0
	v_mov_b32_e32 v243, 0
	v_mov_b32_e32 v244, 0
	v_mov_b32_e32 v245, 0
	v_cvt_pk_fp8_f32 v242, v226, v227
	v_cvt_pk_fp8_f32 v243, v230, v231
	v_cvt_pk_fp8_f32 v244, v234, v235
	v_cvt_pk_fp8_f32 v245, v238, v239
	v_cvt_pk_fp8_f32 v242, v228, v229 op_sel:[0,0,1]
	v_cvt_pk_fp8_f32 v243, v232, v233 op_sel:[0,0,1]
	v_cvt_pk_fp8_f32 v244, v236, v237 op_sel:[0,0,1]
	v_cvt_pk_fp8_f32 v245, v240, v241 op_sel:[0,0,1]
	s_nop 0
	global_store_dwordx4 v78, v[242:245], s[6:7]
	s_waitcnt vmcnt(12)
	v_mul_f32_e32 v144, v26, v144
	v_mul_f32_e32 v145, v26, v145
	v_mul_f32_e32 v146, v26, v146
	v_mul_f32_e32 v147, v26, v147
	ds_write_b128 v209, v[144:147]
	v_mul_f32_e32 v148, v27, v148
	v_mul_f32_e32 v149, v27, v149
	v_mul_f32_e32 v150, v27, v150
	v_mul_f32_e32 v151, v27, v151
	ds_write_b128 v209, v[148:151] offset:1024
	v_mul_f32_e32 v152, v28, v152
	v_mul_f32_e32 v153, v28, v153
	v_mul_f32_e32 v154, v28, v154
	v_mul_f32_e32 v155, v28, v155
	ds_write_b128 v209, v[152:155] offset:2048
	v_mul_f32_e32 v156, v29, v156
	v_mul_f32_e32 v157, v29, v157
	v_mul_f32_e32 v158, v29, v158
	v_mul_f32_e32 v159, v29, v159
	ds_write_b128 v209, v[156:159] offset:3072
	v_mul_f32_e32 v160, v30, v160
	v_mul_f32_e32 v161, v30, v161
	v_mul_f32_e32 v162, v30, v162
	v_mul_f32_e32 v163, v30, v163
	ds_write_b128 v209, v[160:163] offset:4096
	v_mul_f32_e32 v164, v31, v164
	v_mul_f32_e32 v165, v31, v165
	v_mul_f32_e32 v166, v31, v166
	v_mul_f32_e32 v167, v31, v167
	ds_write_b128 v209, v[164:167] offset:5120
	v_mul_f32_e32 v168, v32, v168
	v_mul_f32_e32 v169, v32, v169
	v_mul_f32_e32 v170, v32, v170
	v_mul_f32_e32 v171, v32, v171
	ds_write_b128 v209, v[168:171] offset:6144
	v_mul_f32_e32 v172, v33, v172
	v_mul_f32_e32 v173, v33, v173
	v_mul_f32_e32 v174, v33, v174
	v_mul_f32_e32 v175, v33, v175
	ds_write_b128 v209, v[172:175] offset:7168
	s_waitcnt lgkmcnt(0)
	s_barrier
; #define GAS __attribute__((address_space(1)))
; #define LAS __attribute__((address_space(3)))
; #define LDS_WAIT() asm volatile("s_waitcnt lgkmcnt(0)" ::: "memory")
; __device__ __forceinline__ unsigned pk4_fp8(float a, float b, float c, float d) {
;     a = fminf(fmaxf(a, -448.f), 448.f); b = fminf(fmaxf(b, -448.f), 448.f); c = fminf(fmaxf(c, -448.f), 448.f); d = fminf(fmaxf(d, -448.f), 448.f);
;     int w = __builtin_amdgcn_cvt_pk_fp8_f32(a, b, 0, false); w = __builtin_amdgcn_cvt_pk_fp8_f32(c, d, w, true); return (unsigned)w; }
;     const int pr = item >> 1, kb = 2 * (pr / nblk) + (item & 1), nb = pr % nblk, k0 = 64 * kb, n0 = 32 * nb;
;     const int nr = n0 + (lane & 31); const int sc = MAP == 1 ? src_col_in(nr) : nr;
;     float v[32];
; #pragma unroll
;     for (int i = 0; i < 32; ++i) v[i] = sc >= 0 ? W[(size_t)(k0 + 2 * i + (lane >> 5)) * Nsrc + sc] : 0.f;
; #pragma unroll
;     for (int i = 0; i < 32; ++i) { const int k = k0 + 2 * i + (lane >> 5); float x = v[i] * wscale; if (KS) x *= (k < ksplit ? ksA[k] : ksB[k - ksplit]); scr[(2 * i + (lane >> 5)) * 33 + (lane & 31)] = x; }
;     LDS_WAIT(); asm volatile("" ::: "memory");
;     const int c = lane & 7;
; #pragma unroll
;     for (int j = 0; j < 4; ++j) { const int n = (lane >> 3) + 8 * j; const LAS float* s = scr + (8 * c) * 33 + n;
;         const unsigned long long o = (unsigned long long)pg8::pk4_fp8(s[0 * 33], s[1 * 33], s[2 * 33], s[3 * 33]) | ((unsigned long long)pg8::pk4_fp8(s[4 * 33], s[5 * 33], s[6 * 33], s[7 * 33]) << 32);
;         *(GAS unsigned long long*)(WT + (size_t)(n0 + n) * K + k0 + 8 * c) = o; }
;     LDS_WAIT(); asm volatile("" ::: "memory");
; }
	s_mov_b64 s[8:9], s[34:35]
	global_load_dwordx4 v[144:147], v74, s[8:9]
	s_add_u32 s8, s8, 0x20000
	s_addc_u32 s9, s9, 0
	global_load_dwordx4 v[148:151], v74, s[8:9]
	s_add_u32 s8, s8, 0x20000
	s_addc_u32 s9, s9, 0
	global_load_dwordx4 v[152:155], v74, s[8:9]
	s_add_u32 s8, s8, 0x20000
	s_addc_u32 s9, s9, 0
	global_load_dwordx4 v[156:159], v74, s[8:9]
	s_add_u32 s8, s8, 0x20000
	s_addc_u32 s9, s9, 0
	global_load_dwordx4 v[160:163], v74, s[8:9]
	s_add_u32 s8, s8, 0x20000
	s_addc_u32 s9, s9, 0
	global_load_dwordx4 v[164:167], v74, s[8:9]
	s_add_u32 s8, s8, 0x20000
	s_addc_u32 s9, s9, 0
	global_load_dwordx4 v[168:171], v74, s[8:9]
	s_add_u32 s8, s8, 0x20000
	s_addc_u32 s9, s9, 0
	global_load_dwordx4 v[172:175], v74, s[8:9]
	s_add_u32 s6, s32, 0x3800000
	s_addc_u32 s7, s33, 0
	ds_read_b32 v226, v211
	ds_read_b32 v227, v211 offset:512
	ds_read_b32 v228, v211 offset:1024
	ds_read_b32 v229, v211 offset:1536
	ds_read_b32 v230, v211 offset:2048
	ds_read_b32 v231, v211 offset:2560
	ds_read_b32 v232, v211 offset:3072
	ds_read_b32 v233, v211 offset:3584
	ds_read_b32 v234, v211 offset:4096
	ds_read_b32 v235, v211 offset:4608
	ds_read_b32 v236, v211 offset:5120
	ds_read_b32 v237, v211 offset:5632
	ds_read_b32 v238, v211 offset:6144
	ds_read_b32 v239, v211 offset:6656
	ds_read_b32 v240, v211 offset:7168
	ds_read_b32 v241, v211 offset:7680
	s_waitcnt lgkmcnt(0)
	v_max_f32_e32 v226, v226, v226
	v_max_f32_e32 v227, v227, v227
	v_max_f32_e32 v228, v228, v228
	v_max_f32_e32 v229, v229, v229
	v_max_f32_e32 v230, v230, v230
	v_max_f32_e32 v231, v231, v231
	v_max_f32_e32 v232, v232, v232
	v_max_f32_e32 v233, v233, v233
	v_max_f32_e32 v234, v234, v234
	v_max_f32_e32 v235, v235, v235
	v_max_f32_e32 v236, v236, v236
	v_max_f32_e32 v237, v237, v237
	v_max_f32_e32 v238, v238, v238
	v_max_f32_e32 v239, v239, v239
	v_max_f32_e32 v240, v240, v240
	v_max_f32_e32 v241, v241, v241
	v_med3_f32 v226, v226, s62, v95
	v_med3_f32 v227, v227, s62, v95
	v_med3_f32 v228, v228, s62, v95
	v_med3_f32 v229, v229, s62, v95
	v_med3_f32 v230, v230, s62, v95
	v_med3_f32 v231, v231, s62, v95
	v_med3_f32 v232, v232, s62, v95
	v_med3_f32 v233, v233, s62, v95
	v_med3_f32 v234, v234, s62, v95
	v_med3_f32 v235, v235, s62, v95
	v_med3_f32 v236, v236, s62, v95
	v_med3_f32 v237, v237, s62, v95
	v_med3_f32 v238, v238, s62, v95
	v_med3_f32 v239, v239, s62, v95
	v_med3_f32 v240, v240, s62, v95
	v_med3_f32 v241, v241, s62, v95
	v_mov_b32_e32 v242, 0
	v_mov_b32_e32 v243, 0
	v_mov_b32_e32 v244, 0
	v_mov_b32_e32 v245, 0
	v_cvt_pk_fp8_f32 v242, v226, v227
	v_cvt_pk_fp8_f32 v243, v230, v231
	v_cvt_pk_fp8_f32 v244, v234, v235
	v_cvt_pk_fp8_f32 v245, v238, v239
	v_cvt_pk_fp8_f32 v242, v228, v229 op_sel:[0,0,1]
	v_cvt_pk_fp8_f32 v243, v232, v233 op_sel:[0,0,1]
	v_cvt_pk_fp8_f32 v244, v236, v237 op_sel:[0,0,1]
	v_cvt_pk_fp8_f32 v245, v240, v241 op_sel:[0,0,1]
	s_nop 0
	global_store_dwordx4 v77, v[242:245], s[6:7]
	ds_read_b32 v226, v213
	ds_read_b32 v227, v213 offset:512
	ds_read_b32 v228, v213 offset:1024
	ds_read_b32 v229, v213 offset:1536
	ds_read_b32 v230, v213 offset:2048
	ds_read_b32 v231, v213 offset:2560
	ds_read_b32 v232, v213 offset:3072
	ds_read_b32 v233, v213 offset:3584
	ds_read_b32 v234, v213 offset:4096
	ds_read_b32 v235, v213 offset:4608
	ds_read_b32 v236, v213 offset:5120
	ds_read_b32 v237, v213 offset:5632
	ds_read_b32 v238, v213 offset:6144
	ds_read_b32 v239, v213 offset:6656
	ds_read_b32 v240, v213 offset:7168
	ds_read_b32 v241, v213 offset:7680
	s_waitcnt lgkmcnt(0)
	v_max_f32_e32 v226, v226, v226
	v_max_f32_e32 v227, v227, v227
	v_max_f32_e32 v228, v228, v228
	v_max_f32_e32 v229, v229, v229
	v_max_f32_e32 v230, v230, v230
	v_max_f32_e32 v231, v231, v231
	v_max_f32_e32 v232, v232, v232
	v_max_f32_e32 v233, v233, v233
	v_max_f32_e32 v234, v234, v234
	v_max_f32_e32 v235, v235, v235
	v_max_f32_e32 v236, v236, v236
	v_max_f32_e32 v237, v237, v237
	v_max_f32_e32 v238, v238, v238
	v_max_f32_e32 v239, v239, v239
	v_max_f32_e32 v240, v240, v240
	v_max_f32_e32 v241, v241, v241
	v_med3_f32 v226, v226, s62, v95
	v_med3_f32 v227, v227, s62, v95
	v_med3_f32 v228, v228, s62, v95
	v_med3_f32 v229, v229, s62, v95
	v_med3_f32 v230, v230, s62, v95
	v_med3_f32 v231, v231, s62, v95
	v_med3_f32 v232, v232, s62, v95
	v_med3_f32 v233, v233, s62, v95
	v_med3_f32 v234, v234, s62, v95
	v_med3_f32 v235, v235, s62, v95
	v_med3_f32 v236, v236, s62, v95
	v_med3_f32 v237, v237, s62, v95
	v_med3_f32 v238, v238, s62, v95
	v_med3_f32 v239, v239, s62, v95
	v_med3_f32 v240, v240, s62, v95
	v_med3_f32 v241, v241, s62, v95
	v_mov_b32_e32 v242, 0
	v_mov_b32_e32 v243, 0
	v_mov_b32_e32 v244, 0
	v_mov_b32_e32 v245, 0
	v_cvt_pk_fp8_f32 v242, v226, v227
	v_cvt_pk_fp8_f32 v243, v230, v231
	v_cvt_pk_fp8_f32 v244, v234, v235
	v_cvt_pk_fp8_f32 v245, v238, v239
	v_cvt_pk_fp8_f32 v242, v228, v229 op_sel:[0,0,1]
	v_cvt_pk_fp8_f32 v243, v232, v233 op_sel:[0,0,1]
	v_cvt_pk_fp8_f32 v244, v236, v237 op_sel:[0,0,1]
	v_cvt_pk_fp8_f32 v245, v240, v241 op_sel:[0,0,1]
	s_nop 0
	global_store_dwordx4 v78, v[242:245], s[6:7]
	s_waitcnt vmcnt(12)
	v_mul_f32_e32 v176, v26, v176
	v_mul_f32_e32 v177, v26, v177
	v_mul_f32_e32 v178, v26, v178
	v_mul_f32_e32 v179, v26, v179
	ds_write_b128 v210, v[176:179]
	v_mul_f32_e32 v180, v27, v180
	v_mul_f32_e32 v181, v27, v181
	v_mul_f32_e32 v182, v27, v182
	v_mul_f32_e32 v183, v27, v183
	ds_write_b128 v210, v[180:183] offset:1024
	v_mul_f32_e32 v184, v28, v184
	v_mul_f32_e32 v185, v28, v185
	v_mul_f32_e32 v186, v28, v186
	v_mul_f32_e32 v187, v28, v187
	ds_write_b128 v210, v[184:187] offset:2048
	v_mul_f32_e32 v188, v29, v188
	v_mul_f32_e32 v189, v29, v189
	v_mul_f32_e32 v190, v29, v190
	v_mul_f32_e32 v191, v29, v191
	ds_write_b128 v210, v[188:191] offset:3072
	v_mul_f32_e32 v192, v30, v192
	v_mul_f32_e32 v193, v30, v193
	v_mul_f32_e32 v194, v30, v194
	v_mul_f32_e32 v195, v30, v195
	ds_write_b128 v210, v[192:195] offset:4096
	v_mul_f32_e32 v196, v31, v196
	v_mul_f32_e32 v197, v31, v197
	v_mul_f32_e32 v198, v31, v198
	v_mul_f32_e32 v199, v31, v199
	ds_write_b128 v210, v[196:199] offset:5120
	v_mul_f32_e32 v200, v32, v200
	v_mul_f32_e32 v201, v32, v201
	v_mul_f32_e32 v202, v32, v202
	v_mul_f32_e32 v203, v32, v203
	ds_write_b128 v210, v[200:203] offset:6144
	v_mul_f32_e32 v204, v33, v204
	v_mul_f32_e32 v205, v33, v205
	v_mul_f32_e32 v206, v33, v206
	v_mul_f32_e32 v207, v33, v207
	ds_write_b128 v210, v[204:207] offset:7168
	s_waitcnt lgkmcnt(0)
	s_barrier
; #define GAS __attribute__((address_space(1)))
; #define LAS __attribute__((address_space(3)))
; #define LDS_WAIT() asm volatile("s_waitcnt lgkmcnt(0)" ::: "memory")
; __device__ __forceinline__ unsigned pk4_fp8(float a, float b, float c, float d) {
;     a = fminf(fmaxf(a, -448.f), 448.f); b = fminf(fmaxf(b, -448.f), 448.f); c = fminf(fmaxf(c, -448.f), 448.f); d = fminf(fmaxf(d, -448.f), 448.f);
;     int w = __builtin_amdgcn_cvt_pk_fp8_f32(a, b, 0, false); w = __builtin_amdgcn_cvt_pk_fp8_f32(c, d, w, true); return (unsigned)w; }
;     const int pr = item >> 1, kb = 2 * (pr / nblk) + (item & 1), nb = pr % nblk, k0 = 64 * kb, n0 = 32 * nb;
;     const int nr = n0 + (lane & 31); const int sc = MAP == 1 ? src_col_in(nr) : nr;
;     float v[32];
; #pragma unroll
;     for (int i = 0; i < 32; ++i) v[i] = sc >= 0 ? W[(size_t)(k0 + 2 * i + (lane >> 5)) * Nsrc + sc] : 0.f;
; #pragma unroll
;     for (int i = 0; i < 32; ++i) { const int k = k0 + 2 * i + (lane >> 5); float x = v[i] * wscale; if (KS) x *= (k < ksplit ? ksA[k] : ksB[k - ksplit]); scr[(2 * i + (lane >> 5)) * 33 + (lane & 31)] = x; }
;     LDS_WAIT(); asm volatile("" ::: "memory");
;     const int c = lane & 7;
; #pragma unroll
;     for (int j = 0; j < 4; ++j) { const int n = (lane >> 3) + 8 * j; const LAS float* s = scr + (8 * c) * 33 + n;
;         const unsigned long long o = (unsigned long long)pg8::pk4_fp8(s[0 * 33], s[1 * 33], s[2 * 33], s[3 * 33]) | ((unsigned long long)pg8::pk4_fp8(s[4 * 33], s[5 * 33], s[6 * 33], s[7 * 33]) << 32);
;         *(GAS unsigned long long*)(WT + (size_t)(n0 + n) * K + k0 + 8 * c) = o; }
;     LDS_WAIT(); asm volatile("" ::: "memory");
; }
	s_add_u32 s8, s34, 0x1000
	s_addc_u32 s9, s35, 0
	global_load_dwordx4 v[176:179], v74, s[8:9]
	s_add_u32 s8, s8, 0x20000
	s_addc_u32 s9, s9, 0
	global_load_dwordx4 v[180:183], v74, s[8:9]
	s_add_u32 s8, s8, 0x20000
	s_addc_u32 s9, s9, 0
	global_load_dwordx4 v[184:187], v74, s[8:9]
	s_add_u32 s8, s8, 0x20000
	s_addc_u32 s9, s9, 0
	global_load_dwordx4 v[188:191], v74, s[8:9]
	s_add_u32 s8, s8, 0x20000
	s_addc_u32 s9, s9, 0
	global_load_dwordx4 v[192:195], v74, s[8:9]
	s_add_u32 s8, s8, 0x20000
	s_addc_u32 s9, s9, 0
	global_load_dwordx4 v[196:199], v74, s[8:9]
	s_add_u32 s8, s8, 0x20000
	s_addc_u32 s9, s9, 0
	global_load_dwordx4 v[200:203], v74, s[8:9]
	s_add_u32 s8, s8, 0x20000
	s_addc_u32 s9, s9, 0
	global_load_dwordx4 v[204:207], v74, s[8:9]
	s_add_u32 s6, s32, 0x3c00000
	s_addc_u32 s7, s33, 0
	ds_read_b32 v226, v212
	ds_read_b32 v227, v212 offset:512
	ds_read_b32 v228, v212 offset:1024
	ds_read_b32 v229, v212 offset:1536
	ds_read_b32 v230, v212 offset:2048
	ds_read_b32 v231, v212 offset:2560
	ds_read_b32 v232, v212 offset:3072
	ds_read_b32 v233, v212 offset:3584
	ds_read_b32 v234, v212 offset:4096
	ds_read_b32 v235, v212 offset:4608
	ds_read_b32 v236, v212 offset:5120
	ds_read_b32 v237, v212 offset:5632
	ds_read_b32 v238, v212 offset:6144
	ds_read_b32 v239, v212 offset:6656
	ds_read_b32 v240, v212 offset:7168
	ds_read_b32 v241, v212 offset:7680
	s_waitcnt lgkmcnt(0)
	v_max_f32_e32 v226, v226, v226
	v_max_f32_e32 v227, v227, v227
	v_max_f32_e32 v228, v228, v228
	v_max_f32_e32 v229, v229, v229
	v_max_f32_e32 v230, v230, v230
	v_max_f32_e32 v231, v231, v231
	v_max_f32_e32 v232, v232, v232
	v_max_f32_e32 v233, v233, v233
	v_max_f32_e32 v234, v234, v234
	v_max_f32_e32 v235, v235, v235
	v_max_f32_e32 v236, v236, v236
	v_max_f32_e32 v237, v237, v237
	v_max_f32_e32 v238, v238, v238
	v_max_f32_e32 v239, v239, v239
	v_max_f32_e32 v240, v240, v240
	v_max_f32_e32 v241, v241, v241
	v_med3_f32 v226, v226, s62, v95
	v_med3_f32 v227, v227, s62, v95
	v_med3_f32 v228, v228, s62, v95
	v_med3_f32 v229, v229, s62, v95
	v_med3_f32 v230, v230, s62, v95
	v_med3_f32 v231, v231, s62, v95
	v_med3_f32 v232, v232, s62, v95
	v_med3_f32 v233, v233, s62, v95
	v_med3_f32 v234, v234, s62, v95
	v_med3_f32 v235, v235, s62, v95
	v_med3_f32 v236, v236, s62, v95
	v_med3_f32 v237, v237, s62, v95
	v_med3_f32 v238, v238, s62, v95
	v_med3_f32 v239, v239, s62, v95
	v_med3_f32 v240, v240, s62, v95
	v_med3_f32 v241, v241, s62, v95
	v_mov_b32_e32 v242, 0
	v_mov_b32_e32 v243, 0
	v_mov_b32_e32 v244, 0
	v_mov_b32_e32 v245, 0
	v_cvt_pk_fp8_f32 v242, v226, v227
	v_cvt_pk_fp8_f32 v243, v230, v231
	v_cvt_pk_fp8_f32 v244, v234, v235
	v_cvt_pk_fp8_f32 v245, v238, v239
	v_cvt_pk_fp8_f32 v242, v228, v229 op_sel:[0,0,1]
	v_cvt_pk_fp8_f32 v243, v232, v233 op_sel:[0,0,1]
	v_cvt_pk_fp8_f32 v244, v236, v237 op_sel:[0,0,1]
	v_cvt_pk_fp8_f32 v245, v240, v241 op_sel:[0,0,1]
	s_nop 0
	global_store_dwordx4 v77, v[242:245], s[6:7]
	ds_read_b32 v226, v214
	ds_read_b32 v227, v214 offset:512
	ds_read_b32 v228, v214 offset:1024
	ds_read_b32 v229, v214 offset:1536
	ds_read_b32 v230, v214 offset:2048
	ds_read_b32 v231, v214 offset:2560
	ds_read_b32 v232, v214 offset:3072
	ds_read_b32 v233, v214 offset:3584
	ds_read_b32 v234, v214 offset:4096
	ds_read_b32 v235, v214 offset:4608
	ds_read_b32 v236, v214 offset:5120
	ds_read_b32 v237, v214 offset:5632
	ds_read_b32 v238, v214 offset:6144
	ds_read_b32 v239, v214 offset:6656
	ds_read_b32 v240, v214 offset:7168
	ds_read_b32 v241, v214 offset:7680
	s_waitcnt lgkmcnt(0)
	v_max_f32_e32 v226, v226, v226
	v_max_f32_e32 v227, v227, v227
	v_max_f32_e32 v228, v228, v228
	v_max_f32_e32 v229, v229, v229
	v_max_f32_e32 v230, v230, v230
	v_max_f32_e32 v231, v231, v231
	v_max_f32_e32 v232, v232, v232
	v_max_f32_e32 v233, v233, v233
	v_max_f32_e32 v234, v234, v234
	v_max_f32_e32 v235, v235, v235
	v_max_f32_e32 v236, v236, v236
	v_max_f32_e32 v237, v237, v237
	v_max_f32_e32 v238, v238, v238
	v_max_f32_e32 v239, v239, v239
	v_max_f32_e32 v240, v240, v240
	v_max_f32_e32 v241, v241, v241
	v_med3_f32 v226, v226, s62, v95
	v_med3_f32 v227, v227, s62, v95
	v_med3_f32 v228, v228, s62, v95
	v_med3_f32 v229, v229, s62, v95
	v_med3_f32 v230, v230, s62, v95
	v_med3_f32 v231, v231, s62, v95
	v_med3_f32 v232, v232, s62, v95
	v_med3_f32 v233, v233, s62, v95
	v_med3_f32 v234, v234, s62, v95
	v_med3_f32 v235, v235, s62, v95
	v_med3_f32 v236, v236, s62, v95
	v_med3_f32 v237, v237, s62, v95
	v_med3_f32 v238, v238, s62, v95
	v_med3_f32 v239, v239, s62, v95
	v_med3_f32 v240, v240, s62, v95
	v_med3_f32 v241, v241, s62, v95
	v_mov_b32_e32 v242, 0
	v_mov_b32_e32 v243, 0
	v_mov_b32_e32 v244, 0
	v_mov_b32_e32 v245, 0
	v_cvt_pk_fp8_f32 v242, v226, v227
	v_cvt_pk_fp8_f32 v243, v230, v231
	v_cvt_pk_fp8_f32 v244, v234, v235
	v_cvt_pk_fp8_f32 v245, v238, v239
	v_cvt_pk_fp8_f32 v242, v228, v229 op_sel:[0,0,1]
	v_cvt_pk_fp8_f32 v243, v232, v233 op_sel:[0,0,1]
	v_cvt_pk_fp8_f32 v244, v236, v237 op_sel:[0,0,1]
	v_cvt_pk_fp8_f32 v245, v240, v241 op_sel:[0,0,1]
	s_nop 0
	global_store_dwordx4 v78, v[242:245], s[6:7]
	s_waitcnt vmcnt(12)
	v_mul_f32_e32 v144, v34, v144
	v_mul_f32_e32 v145, v34, v145
	v_mul_f32_e32 v146, v34, v146
	v_mul_f32_e32 v147, v34, v147
	ds_write_b128 v209, v[144:147]
	v_mul_f32_e32 v148, v35, v148
	v_mul_f32_e32 v149, v35, v149
	v_mul_f32_e32 v150, v35, v150
	v_mul_f32_e32 v151, v35, v151
	ds_write_b128 v209, v[148:151] offset:1024
	v_mul_f32_e32 v152, v36, v152
	v_mul_f32_e32 v153, v36, v153
	v_mul_f32_e32 v154, v36, v154
	v_mul_f32_e32 v155, v36, v155
	ds_write_b128 v209, v[152:155] offset:2048
	v_mul_f32_e32 v156, v37, v156
	v_mul_f32_e32 v157, v37, v157
	v_mul_f32_e32 v158, v37, v158
	v_mul_f32_e32 v159, v37, v159
	ds_write_b128 v209, v[156:159] offset:3072
	v_mul_f32_e32 v160, v38, v160
	v_mul_f32_e32 v161, v38, v161
	v_mul_f32_e32 v162, v38, v162
	v_mul_f32_e32 v163, v38, v163
	ds_write_b128 v209, v[160:163] offset:4096
	v_mul_f32_e32 v164, v39, v164
	v_mul_f32_e32 v165, v39, v165
	v_mul_f32_e32 v166, v39, v166
	v_mul_f32_e32 v167, v39, v167
	ds_write_b128 v209, v[164:167] offset:5120
	v_mul_f32_e32 v168, v40, v168
	v_mul_f32_e32 v169, v40, v169
	v_mul_f32_e32 v170, v40, v170
	v_mul_f32_e32 v171, v40, v171
	ds_write_b128 v209, v[168:171] offset:6144
	v_mul_f32_e32 v172, v41, v172
	v_mul_f32_e32 v173, v41, v173
	v_mul_f32_e32 v174, v41, v174
	v_mul_f32_e32 v175, v41, v175
	ds_write_b128 v209, v[172:175] offset:7168
	s_waitcnt lgkmcnt(0)
	s_barrier
; #define GAS __attribute__((address_space(1)))
; #define LAS __attribute__((address_space(3)))
; #define LDS_WAIT() asm volatile("s_waitcnt lgkmcnt(0)" ::: "memory")
; __device__ __forceinline__ unsigned pk4_fp8(float a, float b, float c, float d) {
;     a = fminf(fmaxf(a, -448.f), 448.f); b = fminf(fmaxf(b, -448.f), 448.f); c = fminf(fmaxf(c, -448.f), 448.f); d = fminf(fmaxf(d, -448.f), 448.f);
;     int w = __builtin_amdgcn_cvt_pk_fp8_f32(a, b, 0, false); w = __builtin_amdgcn_cvt_pk_fp8_f32(c, d, w, true); return (unsigned)w; }
;     const int pr = item >> 1, kb = 2 * (pr / nblk) + (item & 1), nb = pr % nblk, k0 = 64 * kb, n0 = 32 * nb;
;     const int nr = n0 + (lane & 31); const int sc = MAP == 1 ? src_col_in(nr) : nr;
;     float v[32];
; #pragma unroll
;     for (int i = 0; i < 32; ++i) v[i] = sc >= 0 ? W[(size_t)(k0 + 2 * i + (lane >> 5)) * Nsrc + sc] : 0.f;
; #pragma unroll
;     for (int i = 0; i < 32; ++i) { const int k = k0 + 2 * i + (lane >> 5); float x = v[i] * wscale; if (KS) x *= (k < ksplit ? ksA[k] : ksB[k - ksplit]); scr[(2 * i + (lane >> 5)) * 33 + (lane & 31)] = x; }
;     LDS_WAIT(); asm volatile("" ::: "memory");
;     const int c = lane & 7;
; #pragma unroll
;     for (int j = 0; j < 4; ++j) { const int n = (lane >> 3) + 8 * j; const LAS float* s = scr + (8 * c) * 33 + n;
;         const unsigned long long o = (unsigned long long)pg8::pk4_fp8(s[0 * 33], s[1 * 33], s[2 * 33], s[3 * 33]) | ((unsigned long long)pg8::pk4_fp8(s[4 * 33], s[5 * 33], s[6 * 33], s[7 * 33]) << 32);
;         *(GAS unsigned long long*)(WT + (size_t)(n0 + n) * K + k0 + 8 * c) = o; }
;     LDS_WAIT(); asm volatile("" ::: "memory");
; }
	s_add_u32 s8, s34, 0x2000
	s_addc_u32 s9, s35, 0
	global_load_dwordx4 v[144:147], v74, s[8:9]
	s_add_u32 s8, s8, 0x20000
	s_addc_u32 s9, s9, 0
	global_load_dwordx4 v[148:151], v74, s[8:9]
	s_add_u32 s8, s8, 0x20000
	s_addc_u32 s9, s9, 0
	global_load_dwordx4 v[152:155], v74, s[8:9]
	s_add_u32 s8, s8, 0x20000
	s_addc_u32 s9, s9, 0
	global_load_dwordx4 v[156:159], v74, s[8:9]
	s_add_u32 s8, s8, 0x20000
	s_addc_u32 s9, s9, 0
	global_load_dwordx4 v[160:163], v74, s[8:9]
	s_add_u32 s8, s8, 0x20000
	s_addc_u32 s9, s9, 0
	global_load_dwordx4 v[164:167], v74, s[8:9]
	s_add_u32 s8, s8, 0x20000
	s_addc_u32 s9, s9, 0
	global_load_dwordx4 v[168:171], v74, s[8:9]
	s_add_u32 s8, s8, 0x20000
	s_addc_u32 s9, s9, 0
	global_load_dwordx4 v[172:175], v74, s[8:9]
	s_mov_b64 s[6:7], s[36:37]
	ds_read_b32 v226, v211
	ds_read_b32 v227, v211 offset:512
	ds_read_b32 v228, v211 offset:1024
	ds_read_b32 v229, v211 offset:1536
	ds_read_b32 v230, v211 offset:2048
	ds_read_b32 v231, v211 offset:2560
	ds_read_b32 v232, v211 offset:3072
	ds_read_b32 v233, v211 offset:3584
	ds_read_b32 v234, v211 offset:4096
	ds_read_b32 v235, v211 offset:4608
	ds_read_b32 v236, v211 offset:5120
	ds_read_b32 v237, v211 offset:5632
	ds_read_b32 v238, v211 offset:6144
	ds_read_b32 v239, v211 offset:6656
	ds_read_b32 v240, v211 offset:7168
	ds_read_b32 v241, v211 offset:7680
	s_waitcnt lgkmcnt(0)
	v_max_f32_e32 v226, v226, v226
	v_max_f32_e32 v227, v227, v227
	v_max_f32_e32 v228, v228, v228
	v_max_f32_e32 v229, v229, v229
	v_max_f32_e32 v230, v230, v230
	v_max_f32_e32 v231, v231, v231
	v_max_f32_e32 v232, v232, v232
	v_max_f32_e32 v233, v233, v233
	v_max_f32_e32 v234, v234, v234
	v_max_f32_e32 v235, v235, v235
	v_max_f32_e32 v236, v236, v236
	v_max_f32_e32 v237, v237, v237
	v_max_f32_e32 v238, v238, v238
	v_max_f32_e32 v239, v239, v239
	v_max_f32_e32 v240, v240, v240
	v_max_f32_e32 v241, v241, v241
	v_med3_f32 v226, v226, s62, v95
	v_med3_f32 v227, v227, s62, v95
	v_med3_f32 v228, v228, s62, v95
	v_med3_f32 v229, v229, s62, v95
	v_med3_f32 v230, v230, s62, v95
	v_med3_f32 v231, v231, s62, v95
	v_med3_f32 v232, v232, s62, v95
	v_med3_f32 v233, v233, s62, v95
	v_med3_f32 v234, v234, s62, v95
	v_med3_f32 v235, v235, s62, v95
	v_med3_f32 v236, v236, s62, v95
	v_med3_f32 v237, v237, s62, v95
	v_med3_f32 v238, v238, s62, v95
	v_med3_f32 v239, v239, s62, v95
	v_med3_f32 v240, v240, s62, v95
	v_med3_f32 v241, v241, s62, v95
	v_mov_b32_e32 v242, 0
	v_mov_b32_e32 v243, 0
	v_mov_b32_e32 v244, 0
	v_mov_b32_e32 v245, 0
	v_cvt_pk_fp8_f32 v242, v226, v227
	v_cvt_pk_fp8_f32 v243, v230, v231
	v_cvt_pk_fp8_f32 v244, v234, v235
	v_cvt_pk_fp8_f32 v245, v238, v239
	v_cvt_pk_fp8_f32 v242, v228, v229 op_sel:[0,0,1]
	v_cvt_pk_fp8_f32 v243, v232, v233 op_sel:[0,0,1]
	v_cvt_pk_fp8_f32 v244, v236, v237 op_sel:[0,0,1]
	v_cvt_pk_fp8_f32 v245, v240, v241 op_sel:[0,0,1]
	s_nop 0
	global_store_dwordx4 v77, v[242:245], s[6:7]
	ds_read_b32 v226, v213
	ds_read_b32 v227, v213 offset:512
	ds_read_b32 v228, v213 offset:1024
	ds_read_b32 v229, v213 offset:1536
	ds_read_b32 v230, v213 offset:2048
	ds_read_b32 v231, v213 offset:2560
	ds_read_b32 v232, v213 offset:3072
	ds_read_b32 v233, v213 offset:3584
	ds_read_b32 v234, v213 offset:4096
	ds_read_b32 v235, v213 offset:4608
	ds_read_b32 v236, v213 offset:5120
	ds_read_b32 v237, v213 offset:5632
	ds_read_b32 v238, v213 offset:6144
	ds_read_b32 v239, v213 offset:6656
	ds_read_b32 v240, v213 offset:7168
	ds_read_b32 v241, v213 offset:7680
	s_waitcnt lgkmcnt(0)
	v_max_f32_e32 v226, v226, v226
	v_max_f32_e32 v227, v227, v227
	v_max_f32_e32 v228, v228, v228
	v_max_f32_e32 v229, v229, v229
	v_max_f32_e32 v230, v230, v230
	v_max_f32_e32 v231, v231, v231
	v_max_f32_e32 v232, v232, v232
	v_max_f32_e32 v233, v233, v233
	v_max_f32_e32 v234, v234, v234
	v_max_f32_e32 v235, v235, v235
	v_max_f32_e32 v236, v236, v236
	v_max_f32_e32 v237, v237, v237
	v_max_f32_e32 v238, v238, v238
	v_max_f32_e32 v239, v239, v239
	v_max_f32_e32 v240, v240, v240
	v_max_f32_e32 v241, v241, v241
	v_med3_f32 v226, v226, s62, v95
	v_med3_f32 v227, v227, s62, v95
	v_med3_f32 v228, v228, s62, v95
	v_med3_f32 v229, v229, s62, v95
	v_med3_f32 v230, v230, s62, v95
	v_med3_f32 v231, v231, s62, v95
	v_med3_f32 v232, v232, s62, v95
	v_med3_f32 v233, v233, s62, v95
	v_med3_f32 v234, v234, s62, v95
	v_med3_f32 v235, v235, s62, v95
	v_med3_f32 v236, v236, s62, v95
	v_med3_f32 v237, v237, s62, v95
	v_med3_f32 v238, v238, s62, v95
	v_med3_f32 v239, v239, s62, v95
	v_med3_f32 v240, v240, s62, v95
	v_med3_f32 v241, v241, s62, v95
	v_mov_b32_e32 v242, 0
	v_mov_b32_e32 v243, 0
	v_mov_b32_e32 v244, 0
	v_mov_b32_e32 v245, 0
	v_cvt_pk_fp8_f32 v242, v226, v227
	v_cvt_pk_fp8_f32 v243, v230, v231
	v_cvt_pk_fp8_f32 v244, v234, v235
	v_cvt_pk_fp8_f32 v245, v238, v239
	v_cvt_pk_fp8_f32 v242, v228, v229 op_sel:[0,0,1]
	v_cvt_pk_fp8_f32 v243, v232, v233 op_sel:[0,0,1]
	v_cvt_pk_fp8_f32 v244, v236, v237 op_sel:[0,0,1]
	v_cvt_pk_fp8_f32 v245, v240, v241 op_sel:[0,0,1]
	s_nop 0
	global_store_dwordx4 v78, v[242:245], s[6:7]
	s_waitcnt vmcnt(12)
	v_mul_f32_e32 v176, v34, v176
	v_mul_f32_e32 v177, v34, v177
	v_mul_f32_e32 v178, v34, v178
	v_mul_f32_e32 v179, v34, v179
	ds_write_b128 v210, v[176:179]
	v_mul_f32_e32 v180, v35, v180
	v_mul_f32_e32 v181, v35, v181
	v_mul_f32_e32 v182, v35, v182
	v_mul_f32_e32 v183, v35, v183
	ds_write_b128 v210, v[180:183] offset:1024
	v_mul_f32_e32 v184, v36, v184
	v_mul_f32_e32 v185, v36, v185
	v_mul_f32_e32 v186, v36, v186
	v_mul_f32_e32 v187, v36, v187
	ds_write_b128 v210, v[184:187] offset:2048
	v_mul_f32_e32 v188, v37, v188
	v_mul_f32_e32 v189, v37, v189
	v_mul_f32_e32 v190, v37, v190
	v_mul_f32_e32 v191, v37, v191
	ds_write_b128 v210, v[188:191] offset:3072
	v_mul_f32_e32 v192, v38, v192
	v_mul_f32_e32 v193, v38, v193
	v_mul_f32_e32 v194, v38, v194
	v_mul_f32_e32 v195, v38, v195
	ds_write_b128 v210, v[192:195] offset:4096
	v_mul_f32_e32 v196, v39, v196
	v_mul_f32_e32 v197, v39, v197
	v_mul_f32_e32 v198, v39, v198
	v_mul_f32_e32 v199, v39, v199
	ds_write_b128 v210, v[196:199] offset:5120
	v_mul_f32_e32 v200, v40, v200
	v_mul_f32_e32 v201, v40, v201
	v_mul_f32_e32 v202, v40, v202
	v_mul_f32_e32 v203, v40, v203
	ds_write_b128 v210, v[200:203] offset:6144
	v_mul_f32_e32 v204, v41, v204
	v_mul_f32_e32 v205, v41, v205
	v_mul_f32_e32 v206, v41, v206
	v_mul_f32_e32 v207, v41, v207
	ds_write_b128 v210, v[204:207] offset:7168
	s_waitcnt lgkmcnt(0)
	s_barrier
; #define GAS __attribute__((address_space(1)))
; #define LAS __attribute__((address_space(3)))
; #define LDS_WAIT() asm volatile("s_waitcnt lgkmcnt(0)" ::: "memory")
; __device__ __forceinline__ unsigned pk4_fp8(float a, float b, float c, float d) {
;     a = fminf(fmaxf(a, -448.f), 448.f); b = fminf(fmaxf(b, -448.f), 448.f); c = fminf(fmaxf(c, -448.f), 448.f); d = fminf(fmaxf(d, -448.f), 448.f);
;     int w = __builtin_amdgcn_cvt_pk_fp8_f32(a, b, 0, false); w = __builtin_amdgcn_cvt_pk_fp8_f32(c, d, w, true); return (unsigned)w; }
;     const int pr = item >> 1, kb = 2 * (pr / nblk) + (item & 1), nb = pr % nblk, k0 = 64 * kb, n0 = 32 * nb;
;     const int nr = n0 + (lane & 31); const int sc = MAP == 1 ? src_col_in(nr) : nr;
;     float v[32];
; #pragma unroll
;     for (int i = 0; i < 32; ++i) v[i] = sc >= 0 ? W[(size_t)(k0 + 2 * i + (lane >> 5)) * Nsrc + sc] : 0.f;
; #pragma unroll
;     for (int i = 0; i < 32; ++i) { const int k = k0 + 2 * i + (lane >> 5); float x = v[i] * wscale; if (KS) x *= (k < ksplit ? ksA[k] : ksB[k - ksplit]); scr[(2 * i + (lane >> 5)) * 33 + (lane & 31)] = x; }
;     LDS_WAIT(); asm volatile("" ::: "memory");
;     const int c = lane & 7;
; #pragma unroll
;     for (int j = 0; j < 4; ++j) { const int n = (lane >> 3) + 8 * j; const LAS float* s = scr + (8 * c) * 33 + n;
;         const unsigned long long o = (unsigned long long)pg8::pk4_fp8(s[0 * 33], s[1 * 33], s[2 * 33], s[3 * 33]) | ((unsigned long long)pg8::pk4_fp8(s[4 * 33], s[5 * 33], s[6 * 33], s[7 * 33]) << 32);
;         *(GAS unsigned long long*)(WT + (size_t)(n0 + n) * K + k0 + 8 * c) = o; }
;     LDS_WAIT(); asm volatile("" ::: "memory");
; }
	s_add_u32 s8, s34, 0x3000
	s_addc_u32 s9, s35, 0
	global_load_dwordx4 v[176:179], v74, s[8:9]
	s_add_u32 s8, s8, 0x20000
	s_addc_u32 s9, s9, 0
	global_load_dwordx4 v[180:183], v74, s[8:9]
	s_add_u32 s8, s8, 0x20000
	s_addc_u32 s9, s9, 0
	global_load_dwordx4 v[184:187], v74, s[8:9]
	s_add_u32 s8, s8, 0x20000
	s_addc_u32 s9, s9, 0
	global_load_dwordx4 v[188:191], v74, s[8:9]
	s_add_u32 s8, s8, 0x20000
	s_addc_u32 s9, s9, 0
	global_load_dwordx4 v[192:195], v74, s[8:9]
	s_add_u32 s8, s8, 0x20000
	s_addc_u32 s9, s9, 0
	global_load_dwordx4 v[196:199], v74, s[8:9]
	s_add_u32 s8, s8, 0x20000
	s_addc_u32 s9, s9, 0
	global_load_dwordx4 v[200:203], v74, s[8:9]
	s_add_u32 s8, s8, 0x20000
	s_addc_u32 s9, s9, 0
	global_load_dwordx4 v[204:207], v74, s[8:9]
	s_add_u32 s6, s36, 0x400000
	s_addc_u32 s7, s37, 0
	ds_read_b32 v226, v212
	ds_read_b32 v227, v212 offset:512
	ds_read_b32 v228, v212 offset:1024
	ds_read_b32 v229, v212 offset:1536
	ds_read_b32 v230, v212 offset:2048
	ds_read_b32 v231, v212 offset:2560
	ds_read_b32 v232, v212 offset:3072
	ds_read_b32 v233, v212 offset:3584
	ds_read_b32 v234, v212 offset:4096
	ds_read_b32 v235, v212 offset:4608
	ds_read_b32 v236, v212 offset:5120
	ds_read_b32 v237, v212 offset:5632
	ds_read_b32 v238, v212 offset:6144
	ds_read_b32 v239, v212 offset:6656
	ds_read_b32 v240, v212 offset:7168
	ds_read_b32 v241, v212 offset:7680
	s_waitcnt lgkmcnt(0)
	v_max_f32_e32 v226, v226, v226
	v_max_f32_e32 v227, v227, v227
	v_max_f32_e32 v228, v228, v228
	v_max_f32_e32 v229, v229, v229
	v_max_f32_e32 v230, v230, v230
	v_max_f32_e32 v231, v231, v231
	v_max_f32_e32 v232, v232, v232
	v_max_f32_e32 v233, v233, v233
	v_max_f32_e32 v234, v234, v234
	v_max_f32_e32 v235, v235, v235
	v_max_f32_e32 v236, v236, v236
	v_max_f32_e32 v237, v237, v237
	v_max_f32_e32 v238, v238, v238
	v_max_f32_e32 v239, v239, v239
	v_max_f32_e32 v240, v240, v240
	v_max_f32_e32 v241, v241, v241
	v_med3_f32 v226, v226, s62, v95
	v_med3_f32 v227, v227, s62, v95
	v_med3_f32 v228, v228, s62, v95
	v_med3_f32 v229, v229, s62, v95
	v_med3_f32 v230, v230, s62, v95
	v_med3_f32 v231, v231, s62, v95
	v_med3_f32 v232, v232, s62, v95
	v_med3_f32 v233, v233, s62, v95
	v_med3_f32 v234, v234, s62, v95
	v_med3_f32 v235, v235, s62, v95
	v_med3_f32 v236, v236, s62, v95
	v_med3_f32 v237, v237, s62, v95
	v_med3_f32 v238, v238, s62, v95
	v_med3_f32 v239, v239, s62, v95
	v_med3_f32 v240, v240, s62, v95
	v_med3_f32 v241, v241, s62, v95
	v_mov_b32_e32 v242, 0
	v_mov_b32_e32 v243, 0
	v_mov_b32_e32 v244, 0
	v_mov_b32_e32 v245, 0
	v_cvt_pk_fp8_f32 v242, v226, v227
	v_cvt_pk_fp8_f32 v243, v230, v231
	v_cvt_pk_fp8_f32 v244, v234, v235
	v_cvt_pk_fp8_f32 v245, v238, v239
	v_cvt_pk_fp8_f32 v242, v228, v229 op_sel:[0,0,1]
	v_cvt_pk_fp8_f32 v243, v232, v233 op_sel:[0,0,1]
	v_cvt_pk_fp8_f32 v244, v236, v237 op_sel:[0,0,1]
	v_cvt_pk_fp8_f32 v245, v240, v241 op_sel:[0,0,1]
	s_nop 0
	global_store_dwordx4 v77, v[242:245], s[6:7]
	ds_read_b32 v226, v214
	ds_read_b32 v227, v214 offset:512
	ds_read_b32 v228, v214 offset:1024
	ds_read_b32 v229, v214 offset:1536
	ds_read_b32 v230, v214 offset:2048
	ds_read_b32 v231, v214 offset:2560
	ds_read_b32 v232, v214 offset:3072
	ds_read_b32 v233, v214 offset:3584
	ds_read_b32 v234, v214 offset:4096
	ds_read_b32 v235, v214 offset:4608
	ds_read_b32 v236, v214 offset:5120
	ds_read_b32 v237, v214 offset:5632
	ds_read_b32 v238, v214 offset:6144
	ds_read_b32 v239, v214 offset:6656
	ds_read_b32 v240, v214 offset:7168
	ds_read_b32 v241, v214 offset:7680
	s_waitcnt lgkmcnt(0)
	v_max_f32_e32 v226, v226, v226
	v_max_f32_e32 v227, v227, v227
	v_max_f32_e32 v228, v228, v228
	v_max_f32_e32 v229, v229, v229
	v_max_f32_e32 v230, v230, v230
	v_max_f32_e32 v231, v231, v231
	v_max_f32_e32 v232, v232, v232
	v_max_f32_e32 v233, v233, v233
	v_max_f32_e32 v234, v234, v234
	v_max_f32_e32 v235, v235, v235
	v_max_f32_e32 v236, v236, v236
	v_max_f32_e32 v237, v237, v237
	v_max_f32_e32 v238, v238, v238
	v_max_f32_e32 v239, v239, v239
	v_max_f32_e32 v240, v240, v240
	v_max_f32_e32 v241, v241, v241
	v_med3_f32 v226, v226, s62, v95
	v_med3_f32 v227, v227, s62, v95
	v_med3_f32 v228, v228, s62, v95
	v_med3_f32 v229, v229, s62, v95
	v_med3_f32 v230, v230, s62, v95
	v_med3_f32 v231, v231, s62, v95
	v_med3_f32 v232, v232, s62, v95
	v_med3_f32 v233, v233, s62, v95
	v_med3_f32 v234, v234, s62, v95
	v_med3_f32 v235, v235, s62, v95
	v_med3_f32 v236, v236, s62, v95
	v_med3_f32 v237, v237, s62, v95
	v_med3_f32 v238, v238, s62, v95
	v_med3_f32 v239, v239, s62, v95
	v_med3_f32 v240, v240, s62, v95
	v_med3_f32 v241, v241, s62, v95
	v_mov_b32_e32 v242, 0
	v_mov_b32_e32 v243, 0
	v_mov_b32_e32 v244, 0
	v_mov_b32_e32 v245, 0
	v_cvt_pk_fp8_f32 v242, v226, v227
	v_cvt_pk_fp8_f32 v243, v230, v231
	v_cvt_pk_fp8_f32 v244, v234, v235
	v_cvt_pk_fp8_f32 v245, v238, v239
	v_cvt_pk_fp8_f32 v242, v228, v229 op_sel:[0,0,1]
	v_cvt_pk_fp8_f32 v243, v232, v233 op_sel:[0,0,1]
	v_cvt_pk_fp8_f32 v244, v236, v237 op_sel:[0,0,1]
	v_cvt_pk_fp8_f32 v245, v240, v241 op_sel:[0,0,1]
	s_nop 0
	global_store_dwordx4 v78, v[242:245], s[6:7]
	s_waitcnt vmcnt(12)
	v_mul_f32_e32 v144, v34, v144
	v_mul_f32_e32 v145, v34, v145
	v_mul_f32_e32 v146, v34, v146
	v_mul_f32_e32 v147, v34, v147
	ds_write_b128 v209, v[144:147]
	v_mul_f32_e32 v148, v35, v148
	v_mul_f32_e32 v149, v35, v149
	v_mul_f32_e32 v150, v35, v150
	v_mul_f32_e32 v151, v35, v151
	ds_write_b128 v209, v[148:151] offset:1024
	v_mul_f32_e32 v152, v36, v152
	v_mul_f32_e32 v153, v36, v153
	v_mul_f32_e32 v154, v36, v154
	v_mul_f32_e32 v155, v36, v155
	ds_write_b128 v209, v[152:155] offset:2048
	v_mul_f32_e32 v156, v37, v156
	v_mul_f32_e32 v157, v37, v157
	v_mul_f32_e32 v158, v37, v158
	v_mul_f32_e32 v159, v37, v159
	ds_write_b128 v209, v[156:159] offset:3072
	v_mul_f32_e32 v160, v38, v160
	v_mul_f32_e32 v161, v38, v161
	v_mul_f32_e32 v162, v38, v162
	v_mul_f32_e32 v163, v38, v163
	ds_write_b128 v209, v[160:163] offset:4096
	v_mul_f32_e32 v164, v39, v164
	v_mul_f32_e32 v165, v39, v165
	v_mul_f32_e32 v166, v39, v166
	v_mul_f32_e32 v167, v39, v167
	ds_write_b128 v209, v[164:167] offset:5120
	v_mul_f32_e32 v168, v40, v168
	v_mul_f32_e32 v169, v40, v169
	v_mul_f32_e32 v170, v40, v170
	v_mul_f32_e32 v171, v40, v171
	ds_write_b128 v209, v[168:171] offset:6144
	v_mul_f32_e32 v172, v41, v172
	v_mul_f32_e32 v173, v41, v173
	v_mul_f32_e32 v174, v41, v174
	v_mul_f32_e32 v175, v41, v175
	ds_write_b128 v209, v[172:175] offset:7168
	s_waitcnt lgkmcnt(0)
	s_barrier
; #define GAS __attribute__((address_space(1)))
; #define LAS __attribute__((address_space(3)))
; #define LDS_WAIT() asm volatile("s_waitcnt lgkmcnt(0)" ::: "memory")
; __device__ __forceinline__ unsigned pk4_fp8(float a, float b, float c, float d) {
;     a = fminf(fmaxf(a, -448.f), 448.f); b = fminf(fmaxf(b, -448.f), 448.f); c = fminf(fmaxf(c, -448.f), 448.f); d = fminf(fmaxf(d, -448.f), 448.f);
;     int w = __builtin_amdgcn_cvt_pk_fp8_f32(a, b, 0, false); w = __builtin_amdgcn_cvt_pk_fp8_f32(c, d, w, true); return (unsigned)w; }
;     const int pr = item >> 1, kb = 2 * (pr / nblk) + (item & 1), nb = pr % nblk, k0 = 64 * kb, n0 = 32 * nb;
;     const int nr = n0 + (lane & 31); const int sc = MAP == 1 ? src_col_in(nr) : nr;
;     float v[32];
; #pragma unroll
;     for (int i = 0; i < 32; ++i) v[i] = sc >= 0 ? W[(size_t)(k0 + 2 * i + (lane >> 5)) * Nsrc + sc] : 0.f;
; #pragma unroll
;     for (int i = 0; i < 32; ++i) { const int k = k0 + 2 * i + (lane >> 5); float x = v[i] * wscale; if (KS) x *= (k < ksplit ? ksA[k] : ksB[k - ksplit]); scr[(2 * i + (lane >> 5)) * 33 + (lane & 31)] = x; }
;     LDS_WAIT(); asm volatile("" ::: "memory");
;     const int c = lane & 7;
; #pragma unroll
;     for (int j = 0; j < 4; ++j) { const int n = (lane >> 3) + 8 * j; const LAS float* s = scr + (8 * c) * 33 + n;
;         const unsigned long long o = (unsigned long long)pg8::pk4_fp8(s[0 * 33], s[1 * 33], s[2 * 33], s[3 * 33]) | ((unsigned long long)pg8::pk4_fp8(s[4 * 33], s[5 * 33], s[6 * 33], s[7 * 33]) << 32);
;         *(GAS unsigned long long*)(WT + (size_t)(n0 + n) * K + k0 + 8 * c) = o; }
;     LDS_WAIT(); asm volatile("" ::: "memory");
; }
	s_add_u32 s8, s34, 0x4000
	s_addc_u32 s9, s35, 0
	global_load_dwordx4 v[144:147], v74, s[8:9]
	s_add_u32 s8, s8, 0x20000
	s_addc_u32 s9, s9, 0
	global_load_dwordx4 v[148:151], v74, s[8:9]
	s_add_u32 s8, s8, 0x20000
	s_addc_u32 s9, s9, 0
	global_load_dwordx4 v[152:155], v74, s[8:9]
	s_add_u32 s8, s8, 0x20000
	s_addc_u32 s9, s9, 0
	global_load_dwordx4 v[156:159], v74, s[8:9]
	s_add_u32 s8, s8, 0x20000
	s_addc_u32 s9, s9, 0
	global_load_dwordx4 v[160:163], v74, s[8:9]
	s_add_u32 s8, s8, 0x20000
	s_addc_u32 s9, s9, 0
	global_load_dwordx4 v[164:167], v74, s[8:9]
	s_add_u32 s8, s8, 0x20000
	s_addc_u32 s9, s9, 0
	global_load_dwordx4 v[168:171], v74, s[8:9]
	s_add_u32 s8, s8, 0x20000
	s_addc_u32 s9, s9, 0
	global_load_dwordx4 v[172:175], v74, s[8:9]
	s_add_u32 s6, s36, 0x800000
	s_addc_u32 s7, s37, 0
	ds_read_b32 v226, v211
	ds_read_b32 v227, v211 offset:512
	ds_read_b32 v228, v211 offset:1024
	ds_read_b32 v229, v211 offset:1536
	ds_read_b32 v230, v211 offset:2048
	ds_read_b32 v231, v211 offset:2560
	ds_read_b32 v232, v211 offset:3072
	ds_read_b32 v233, v211 offset:3584
	ds_read_b32 v234, v211 offset:4096
	ds_read_b32 v235, v211 offset:4608
	ds_read_b32 v236, v211 offset:5120
	ds_read_b32 v237, v211 offset:5632
	ds_read_b32 v238, v211 offset:6144
	ds_read_b32 v239, v211 offset:6656
	ds_read_b32 v240, v211 offset:7168
	ds_read_b32 v241, v211 offset:7680
	s_waitcnt lgkmcnt(0)
	v_max_f32_e32 v226, v226, v226
	v_max_f32_e32 v227, v227, v227
	v_max_f32_e32 v228, v228, v228
	v_max_f32_e32 v229, v229, v229
	v_max_f32_e32 v230, v230, v230
	v_max_f32_e32 v231, v231, v231
	v_max_f32_e32 v232, v232, v232
	v_max_f32_e32 v233, v233, v233
	v_max_f32_e32 v234, v234, v234
	v_max_f32_e32 v235, v235, v235
	v_max_f32_e32 v236, v236, v236
	v_max_f32_e32 v237, v237, v237
	v_max_f32_e32 v238, v238, v238
	v_max_f32_e32 v239, v239, v239
	v_max_f32_e32 v240, v240, v240
	v_max_f32_e32 v241, v241, v241
	v_med3_f32 v226, v226, s62, v95
	v_med3_f32 v227, v227, s62, v95
	v_med3_f32 v228, v228, s62, v95
	v_med3_f32 v229, v229, s62, v95
	v_med3_f32 v230, v230, s62, v95
	v_med3_f32 v231, v231, s62, v95
	v_med3_f32 v232, v232, s62, v95
	v_med3_f32 v233, v233, s62, v95
	v_med3_f32 v234, v234, s62, v95
	v_med3_f32 v235, v235, s62, v95
	v_med3_f32 v236, v236, s62, v95
	v_med3_f32 v237, v237, s62, v95
	v_med3_f32 v238, v238, s62, v95
	v_med3_f32 v239, v239, s62, v95
	v_med3_f32 v240, v240, s62, v95
	v_med3_f32 v241, v241, s62, v95
	v_mov_b32_e32 v242, 0
	v_mov_b32_e32 v243, 0
	v_mov_b32_e32 v244, 0
	v_mov_b32_e32 v245, 0
	v_cvt_pk_fp8_f32 v242, v226, v227
	v_cvt_pk_fp8_f32 v243, v230, v231
	v_cvt_pk_fp8_f32 v244, v234, v235
	v_cvt_pk_fp8_f32 v245, v238, v239
	v_cvt_pk_fp8_f32 v242, v228, v229 op_sel:[0,0,1]
	v_cvt_pk_fp8_f32 v243, v232, v233 op_sel:[0,0,1]
	v_cvt_pk_fp8_f32 v244, v236, v237 op_sel:[0,0,1]
	v_cvt_pk_fp8_f32 v245, v240, v241 op_sel:[0,0,1]
	s_nop 0
	global_store_dwordx4 v77, v[242:245], s[6:7]
	ds_read_b32 v226, v213
	ds_read_b32 v227, v213 offset:512
	ds_read_b32 v228, v213 offset:1024
	ds_read_b32 v229, v213 offset:1536
	ds_read_b32 v230, v213 offset:2048
	ds_read_b32 v231, v213 offset:2560
	ds_read_b32 v232, v213 offset:3072
	ds_read_b32 v233, v213 offset:3584
	ds_read_b32 v234, v213 offset:4096
	ds_read_b32 v235, v213 offset:4608
	ds_read_b32 v236, v213 offset:5120
	ds_read_b32 v237, v213 offset:5632
	ds_read_b32 v238, v213 offset:6144
	ds_read_b32 v239, v213 offset:6656
	ds_read_b32 v240, v213 offset:7168
	ds_read_b32 v241, v213 offset:7680
	s_waitcnt lgkmcnt(0)
	v_max_f32_e32 v226, v226, v226
	v_max_f32_e32 v227, v227, v227
	v_max_f32_e32 v228, v228, v228
	v_max_f32_e32 v229, v229, v229
	v_max_f32_e32 v230, v230, v230
	v_max_f32_e32 v231, v231, v231
	v_max_f32_e32 v232, v232, v232
	v_max_f32_e32 v233, v233, v233
	v_max_f32_e32 v234, v234, v234
	v_max_f32_e32 v235, v235, v235
	v_max_f32_e32 v236, v236, v236
	v_max_f32_e32 v237, v237, v237
	v_max_f32_e32 v238, v238, v238
	v_max_f32_e32 v239, v239, v239
	v_max_f32_e32 v240, v240, v240
	v_max_f32_e32 v241, v241, v241
	v_med3_f32 v226, v226, s62, v95
	v_med3_f32 v227, v227, s62, v95
	v_med3_f32 v228, v228, s62, v95
	v_med3_f32 v229, v229, s62, v95
	v_med3_f32 v230, v230, s62, v95
	v_med3_f32 v231, v231, s62, v95
	v_med3_f32 v232, v232, s62, v95
	v_med3_f32 v233, v233, s62, v95
	v_med3_f32 v234, v234, s62, v95
	v_med3_f32 v235, v235, s62, v95
	v_med3_f32 v236, v236, s62, v95
	v_med3_f32 v237, v237, s62, v95
	v_med3_f32 v238, v238, s62, v95
	v_med3_f32 v239, v239, s62, v95
	v_med3_f32 v240, v240, s62, v95
	v_med3_f32 v241, v241, s62, v95
	v_mov_b32_e32 v242, 0
	v_mov_b32_e32 v243, 0
	v_mov_b32_e32 v244, 0
	v_mov_b32_e32 v245, 0
	v_cvt_pk_fp8_f32 v242, v226, v227
	v_cvt_pk_fp8_f32 v243, v230, v231
	v_cvt_pk_fp8_f32 v244, v234, v235
	v_cvt_pk_fp8_f32 v245, v238, v239
	v_cvt_pk_fp8_f32 v242, v228, v229 op_sel:[0,0,1]
	v_cvt_pk_fp8_f32 v243, v232, v233 op_sel:[0,0,1]
	v_cvt_pk_fp8_f32 v244, v236, v237 op_sel:[0,0,1]
	v_cvt_pk_fp8_f32 v245, v240, v241 op_sel:[0,0,1]
	s_nop 0
	global_store_dwordx4 v78, v[242:245], s[6:7]
	s_waitcnt vmcnt(12)
	v_mul_f32_e32 v176, v34, v176
	v_mul_f32_e32 v177, v34, v177
	v_mul_f32_e32 v178, v34, v178
	v_mul_f32_e32 v179, v34, v179
	ds_write_b128 v210, v[176:179]
	v_mul_f32_e32 v180, v35, v180
	v_mul_f32_e32 v181, v35, v181
	v_mul_f32_e32 v182, v35, v182
	v_mul_f32_e32 v183, v35, v183
	ds_write_b128 v210, v[180:183] offset:1024
	v_mul_f32_e32 v184, v36, v184
	v_mul_f32_e32 v185, v36, v185
	v_mul_f32_e32 v186, v36, v186
	v_mul_f32_e32 v187, v36, v187
	ds_write_b128 v210, v[184:187] offset:2048
	v_mul_f32_e32 v188, v37, v188
	v_mul_f32_e32 v189, v37, v189
	v_mul_f32_e32 v190, v37, v190
	v_mul_f32_e32 v191, v37, v191
	ds_write_b128 v210, v[188:191] offset:3072
	v_mul_f32_e32 v192, v38, v192
	v_mul_f32_e32 v193, v38, v193
	v_mul_f32_e32 v194, v38, v194
	v_mul_f32_e32 v195, v38, v195
	ds_write_b128 v210, v[192:195] offset:4096
	v_mul_f32_e32 v196, v39, v196
	v_mul_f32_e32 v197, v39, v197
	v_mul_f32_e32 v198, v39, v198
	v_mul_f32_e32 v199, v39, v199
	ds_write_b128 v210, v[196:199] offset:5120
	v_mul_f32_e32 v200, v40, v200
	v_mul_f32_e32 v201, v40, v201
	v_mul_f32_e32 v202, v40, v202
	v_mul_f32_e32 v203, v40, v203
	ds_write_b128 v210, v[200:203] offset:6144
	v_mul_f32_e32 v204, v41, v204
	v_mul_f32_e32 v205, v41, v205
	v_mul_f32_e32 v206, v41, v206
	v_mul_f32_e32 v207, v41, v207
	ds_write_b128 v210, v[204:207] offset:7168
	s_waitcnt lgkmcnt(0)
	s_barrier
; #define GAS __attribute__((address_space(1)))
; #define LAS __attribute__((address_space(3)))
; #define LDS_WAIT() asm volatile("s_waitcnt lgkmcnt(0)" ::: "memory")
; __device__ __forceinline__ unsigned pk4_fp8(float a, float b, float c, float d) {
;     a = fminf(fmaxf(a, -448.f), 448.f); b = fminf(fmaxf(b, -448.f), 448.f); c = fminf(fmaxf(c, -448.f), 448.f); d = fminf(fmaxf(d, -448.f), 448.f);
;     int w = __builtin_amdgcn_cvt_pk_fp8_f32(a, b, 0, false); w = __builtin_amdgcn_cvt_pk_fp8_f32(c, d, w, true); return (unsigned)w; }
;     const int pr = item >> 1, kb = 2 * (pr / nblk) + (item & 1), nb = pr % nblk, k0 = 64 * kb, n0 = 32 * nb;
;     const int nr = n0 + (lane & 31); const int sc = MAP == 1 ? src_col_in(nr) : nr;
;     float v[32];
; #pragma unroll
;     for (int i = 0; i < 32; ++i) v[i] = sc >= 0 ? W[(size_t)(k0 + 2 * i + (lane >> 5)) * Nsrc + sc] : 0.f;
; #pragma unroll
;     for (int i = 0; i < 32; ++i) { const int k = k0 + 2 * i + (lane >> 5); float x = v[i] * wscale; if (KS) x *= (k < ksplit ? ksA[k] : ksB[k - ksplit]); scr[(2 * i + (lane >> 5)) * 33 + (lane & 31)] = x; }
;     LDS_WAIT(); asm volatile("" ::: "memory");
;     const int c = lane & 7;
; #pragma unroll
;     for (int j = 0; j < 4; ++j) { const int n = (lane >> 3) + 8 * j; const LAS float* s = scr + (8 * c) * 33 + n;
;         const unsigned long long o = (unsigned long long)pg8::pk4_fp8(s[0 * 33], s[1 * 33], s[2 * 33], s[3 * 33]) | ((unsigned long long)pg8::pk4_fp8(s[4 * 33], s[5 * 33], s[6 * 33], s[7 * 33]) << 32);
;         *(GAS unsigned long long*)(WT + (size_t)(n0 + n) * K + k0 + 8 * c) = o; }
;     LDS_WAIT(); asm volatile("" ::: "memory");
; }
	s_add_u32 s8, s34, 0x5000
	s_addc_u32 s9, s35, 0
	global_load_dwordx4 v[176:179], v74, s[8:9]
	s_add_u32 s8, s8, 0x20000
	s_addc_u32 s9, s9, 0
	global_load_dwordx4 v[180:183], v74, s[8:9]
	s_add_u32 s8, s8, 0x20000
	s_addc_u32 s9, s9, 0
	global_load_dwordx4 v[184:187], v74, s[8:9]
	s_add_u32 s8, s8, 0x20000
	s_addc_u32 s9, s9, 0
	global_load_dwordx4 v[188:191], v74, s[8:9]
	s_add_u32 s8, s8, 0x20000
	s_addc_u32 s9, s9, 0
	global_load_dwordx4 v[192:195], v74, s[8:9]
	s_add_u32 s8, s8, 0x20000
	s_addc_u32 s9, s9, 0
	global_load_dwordx4 v[196:199], v74, s[8:9]
	s_add_u32 s8, s8, 0x20000
	s_addc_u32 s9, s9, 0
	global_load_dwordx4 v[200:203], v74, s[8:9]
	s_add_u32 s8, s8, 0x20000
	s_addc_u32 s9, s9, 0
	global_load_dwordx4 v[204:207], v74, s[8:9]
	s_add_u32 s6, s36, 0xc00000
	s_addc_u32 s7, s37, 0
	ds_read_b32 v226, v212
	ds_read_b32 v227, v212 offset:512
	ds_read_b32 v228, v212 offset:1024
	ds_read_b32 v229, v212 offset:1536
	ds_read_b32 v230, v212 offset:2048
	ds_read_b32 v231, v212 offset:2560
	ds_read_b32 v232, v212 offset:3072
	ds_read_b32 v233, v212 offset:3584
	ds_read_b32 v234, v212 offset:4096
	ds_read_b32 v235, v212 offset:4608
	ds_read_b32 v236, v212 offset:5120
	ds_read_b32 v237, v212 offset:5632
	ds_read_b32 v238, v212 offset:6144
	ds_read_b32 v239, v212 offset:6656
	ds_read_b32 v240, v212 offset:7168
	ds_read_b32 v241, v212 offset:7680
	s_waitcnt lgkmcnt(0)
	v_max_f32_e32 v226, v226, v226
	v_max_f32_e32 v227, v227, v227
	v_max_f32_e32 v228, v228, v228
	v_max_f32_e32 v229, v229, v229
	v_max_f32_e32 v230, v230, v230
	v_max_f32_e32 v231, v231, v231
	v_max_f32_e32 v232, v232, v232
	v_max_f32_e32 v233, v233, v233
	v_max_f32_e32 v234, v234, v234
	v_max_f32_e32 v235, v235, v235
	v_max_f32_e32 v236, v236, v236
	v_max_f32_e32 v237, v237, v237
	v_max_f32_e32 v238, v238, v238
	v_max_f32_e32 v239, v239, v239
	v_max_f32_e32 v240, v240, v240
	v_max_f32_e32 v241, v241, v241
	v_med3_f32 v226, v226, s62, v95
	v_med3_f32 v227, v227, s62, v95
	v_med3_f32 v228, v228, s62, v95
	v_med3_f32 v229, v229, s62, v95
	v_med3_f32 v230, v230, s62, v95
	v_med3_f32 v231, v231, s62, v95
	v_med3_f32 v232, v232, s62, v95
	v_med3_f32 v233, v233, s62, v95
	v_med3_f32 v234, v234, s62, v95
	v_med3_f32 v235, v235, s62, v95
	v_med3_f32 v236, v236, s62, v95
	v_med3_f32 v237, v237, s62, v95
	v_med3_f32 v238, v238, s62, v95
	v_med3_f32 v239, v239, s62, v95
	v_med3_f32 v240, v240, s62, v95
	v_med3_f32 v241, v241, s62, v95
	v_mov_b32_e32 v242, 0
	v_mov_b32_e32 v243, 0
	v_mov_b32_e32 v244, 0
	v_mov_b32_e32 v245, 0
	v_cvt_pk_fp8_f32 v242, v226, v227
	v_cvt_pk_fp8_f32 v243, v230, v231
	v_cvt_pk_fp8_f32 v244, v234, v235
	v_cvt_pk_fp8_f32 v245, v238, v239
	v_cvt_pk_fp8_f32 v242, v228, v229 op_sel:[0,0,1]
	v_cvt_pk_fp8_f32 v243, v232, v233 op_sel:[0,0,1]
	v_cvt_pk_fp8_f32 v244, v236, v237 op_sel:[0,0,1]
	v_cvt_pk_fp8_f32 v245, v240, v241 op_sel:[0,0,1]
	s_nop 0
	global_store_dwordx4 v77, v[242:245], s[6:7]
	ds_read_b32 v226, v214
	ds_read_b32 v227, v214 offset:512
	ds_read_b32 v228, v214 offset:1024
	ds_read_b32 v229, v214 offset:1536
	ds_read_b32 v230, v214 offset:2048
	ds_read_b32 v231, v214 offset:2560
	ds_read_b32 v232, v214 offset:3072
	ds_read_b32 v233, v214 offset:3584
	ds_read_b32 v234, v214 offset:4096
	ds_read_b32 v235, v214 offset:4608
	ds_read_b32 v236, v214 offset:5120
	ds_read_b32 v237, v214 offset:5632
	ds_read_b32 v238, v214 offset:6144
	ds_read_b32 v239, v214 offset:6656
	ds_read_b32 v240, v214 offset:7168
	ds_read_b32 v241, v214 offset:7680
	s_waitcnt lgkmcnt(0)
	v_max_f32_e32 v226, v226, v226
	v_max_f32_e32 v227, v227, v227
	v_max_f32_e32 v228, v228, v228
	v_max_f32_e32 v229, v229, v229
	v_max_f32_e32 v230, v230, v230
	v_max_f32_e32 v231, v231, v231
	v_max_f32_e32 v232, v232, v232
	v_max_f32_e32 v233, v233, v233
	v_max_f32_e32 v234, v234, v234
	v_max_f32_e32 v235, v235, v235
	v_max_f32_e32 v236, v236, v236
	v_max_f32_e32 v237, v237, v237
	v_max_f32_e32 v238, v238, v238
	v_max_f32_e32 v239, v239, v239
	v_max_f32_e32 v240, v240, v240
	v_max_f32_e32 v241, v241, v241
	v_med3_f32 v226, v226, s62, v95
	v_med3_f32 v227, v227, s62, v95
	v_med3_f32 v228, v228, s62, v95
	v_med3_f32 v229, v229, s62, v95
	v_med3_f32 v230, v230, s62, v95
	v_med3_f32 v231, v231, s62, v95
	v_med3_f32 v232, v232, s62, v95
	v_med3_f32 v233, v233, s62, v95
	v_med3_f32 v234, v234, s62, v95
	v_med3_f32 v235, v235, s62, v95
	v_med3_f32 v236, v236, s62, v95
	v_med3_f32 v237, v237, s62, v95
	v_med3_f32 v238, v238, s62, v95
	v_med3_f32 v239, v239, s62, v95
	v_med3_f32 v240, v240, s62, v95
	v_med3_f32 v241, v241, s62, v95
	v_mov_b32_e32 v242, 0
	v_mov_b32_e32 v243, 0
	v_mov_b32_e32 v244, 0
	v_mov_b32_e32 v245, 0
	v_cvt_pk_fp8_f32 v242, v226, v227
	v_cvt_pk_fp8_f32 v243, v230, v231
	v_cvt_pk_fp8_f32 v244, v234, v235
	v_cvt_pk_fp8_f32 v245, v238, v239
	v_cvt_pk_fp8_f32 v242, v228, v229 op_sel:[0,0,1]
	v_cvt_pk_fp8_f32 v243, v232, v233 op_sel:[0,0,1]
	v_cvt_pk_fp8_f32 v244, v236, v237 op_sel:[0,0,1]
	v_cvt_pk_fp8_f32 v245, v240, v241 op_sel:[0,0,1]
	s_nop 0
	global_store_dwordx4 v78, v[242:245], s[6:7]
	s_waitcnt vmcnt(12)
	v_mul_f32_e32 v144, v34, v144
	v_mul_f32_e32 v145, v34, v145
	v_mul_f32_e32 v146, v34, v146
	v_mul_f32_e32 v147, v34, v147
	ds_write_b128 v209, v[144:147]
	v_mul_f32_e32 v148, v35, v148
	v_mul_f32_e32 v149, v35, v149
	v_mul_f32_e32 v150, v35, v150
	v_mul_f32_e32 v151, v35, v151
	ds_write_b128 v209, v[148:151] offset:1024
	v_mul_f32_e32 v152, v36, v152
	v_mul_f32_e32 v153, v36, v153
	v_mul_f32_e32 v154, v36, v154
	v_mul_f32_e32 v155, v36, v155
	ds_write_b128 v209, v[152:155] offset:2048
	v_mul_f32_e32 v156, v37, v156
	v_mul_f32_e32 v157, v37, v157
	v_mul_f32_e32 v158, v37, v158
	v_mul_f32_e32 v159, v37, v159
	ds_write_b128 v209, v[156:159] offset:3072
	v_mul_f32_e32 v160, v38, v160
	v_mul_f32_e32 v161, v38, v161
	v_mul_f32_e32 v162, v38, v162
	v_mul_f32_e32 v163, v38, v163
	ds_write_b128 v209, v[160:163] offset:4096
	v_mul_f32_e32 v164, v39, v164
	v_mul_f32_e32 v165, v39, v165
	v_mul_f32_e32 v166, v39, v166
	v_mul_f32_e32 v167, v39, v167
	ds_write_b128 v209, v[164:167] offset:5120
	v_mul_f32_e32 v168, v40, v168
	v_mul_f32_e32 v169, v40, v169
	v_mul_f32_e32 v170, v40, v170
	v_mul_f32_e32 v171, v40, v171
	ds_write_b128 v209, v[168:171] offset:6144
	v_mul_f32_e32 v172, v41, v172
	v_mul_f32_e32 v173, v41, v173
	v_mul_f32_e32 v174, v41, v174
	v_mul_f32_e32 v175, v41, v175
	ds_write_b128 v209, v[172:175] offset:7168
	s_waitcnt lgkmcnt(0)
	s_barrier
; #define GAS __attribute__((address_space(1)))
; #define LAS __attribute__((address_space(3)))
; #define LDS_WAIT() asm volatile("s_waitcnt lgkmcnt(0)" ::: "memory")
; __device__ __forceinline__ unsigned pk4_fp8(float a, float b, float c, float d) {
;     a = fminf(fmaxf(a, -448.f), 448.f); b = fminf(fmaxf(b, -448.f), 448.f); c = fminf(fmaxf(c, -448.f), 448.f); d = fminf(fmaxf(d, -448.f), 448.f);
;     int w = __builtin_amdgcn_cvt_pk_fp8_f32(a, b, 0, false); w = __builtin_amdgcn_cvt_pk_fp8_f32(c, d, w, true); return (unsigned)w; }
;     const int pr = item >> 1, kb = 2 * (pr / nblk) + (item & 1), nb = pr % nblk, k0 = 64 * kb, n0 = 32 * nb;
;     const int nr = n0 + (lane & 31); const int sc = MAP == 1 ? src_col_in(nr) : nr;
;     float v[32];
; #pragma unroll
;     for (int i = 0; i < 32; ++i) v[i] = sc >= 0 ? W[(size_t)(k0 + 2 * i + (lane >> 5)) * Nsrc + sc] : 0.f;
; #pragma unroll
;     for (int i = 0; i < 32; ++i) { const int k = k0 + 2 * i + (lane >> 5); float x = v[i] * wscale; if (KS) x *= (k < ksplit ? ksA[k] : ksB[k - ksplit]); scr[(2 * i + (lane >> 5)) * 33 + (lane & 31)] = x; }
;     LDS_WAIT(); asm volatile("" ::: "memory");
;     const int c = lane & 7;
; #pragma unroll
;     for (int j = 0; j < 4; ++j) { const int n = (lane >> 3) + 8 * j; const LAS float* s = scr + (8 * c) * 33 + n;
;         const unsigned long long o = (unsigned long long)pg8::pk4_fp8(s[0 * 33], s[1 * 33], s[2 * 33], s[3 * 33]) | ((unsigned long long)pg8::pk4_fp8(s[4 * 33], s[5 * 33], s[6 * 33], s[7 * 33]) << 32);
;         *(GAS unsigned long long*)(WT + (size_t)(n0 + n) * K + k0 + 8 * c) = o; }
;     LDS_WAIT(); asm volatile("" ::: "memory");
; }
	s_add_u32 s8, s34, 0x6000
	s_addc_u32 s9, s35, 0
	global_load_dwordx4 v[144:147], v74, s[8:9]
	s_add_u32 s8, s8, 0x20000
	s_addc_u32 s9, s9, 0
	global_load_dwordx4 v[148:151], v74, s[8:9]
	s_add_u32 s8, s8, 0x20000
	s_addc_u32 s9, s9, 0
	global_load_dwordx4 v[152:155], v74, s[8:9]
	s_add_u32 s8, s8, 0x20000
	s_addc_u32 s9, s9, 0
	global_load_dwordx4 v[156:159], v74, s[8:9]
	s_add_u32 s8, s8, 0x20000
	s_addc_u32 s9, s9, 0
	global_load_dwordx4 v[160:163], v74, s[8:9]
	s_add_u32 s8, s8, 0x20000
	s_addc_u32 s9, s9, 0
	global_load_dwordx4 v[164:167], v74, s[8:9]
	s_add_u32 s8, s8, 0x20000
	s_addc_u32 s9, s9, 0
	global_load_dwordx4 v[168:171], v74, s[8:9]
	s_add_u32 s8, s8, 0x20000
	s_addc_u32 s9, s9, 0
	global_load_dwordx4 v[172:175], v74, s[8:9]
	s_add_u32 s6, s36, 0x1000000
	s_addc_u32 s7, s37, 0
	ds_read_b32 v226, v211
	ds_read_b32 v227, v211 offset:512
	ds_read_b32 v228, v211 offset:1024
	ds_read_b32 v229, v211 offset:1536
	ds_read_b32 v230, v211 offset:2048
	ds_read_b32 v231, v211 offset:2560
	ds_read_b32 v232, v211 offset:3072
	ds_read_b32 v233, v211 offset:3584
	ds_read_b32 v234, v211 offset:4096
	ds_read_b32 v235, v211 offset:4608
	ds_read_b32 v236, v211 offset:5120
	ds_read_b32 v237, v211 offset:5632
	ds_read_b32 v238, v211 offset:6144
	ds_read_b32 v239, v211 offset:6656
	ds_read_b32 v240, v211 offset:7168
	ds_read_b32 v241, v211 offset:7680
	s_waitcnt lgkmcnt(0)
	v_max_f32_e32 v226, v226, v226
	v_max_f32_e32 v227, v227, v227
	v_max_f32_e32 v228, v228, v228
	v_max_f32_e32 v229, v229, v229
	v_max_f32_e32 v230, v230, v230
	v_max_f32_e32 v231, v231, v231
	v_max_f32_e32 v232, v232, v232
	v_max_f32_e32 v233, v233, v233
	v_max_f32_e32 v234, v234, v234
	v_max_f32_e32 v235, v235, v235
	v_max_f32_e32 v236, v236, v236
	v_max_f32_e32 v237, v237, v237
	v_max_f32_e32 v238, v238, v238
	v_max_f32_e32 v239, v239, v239
	v_max_f32_e32 v240, v240, v240
	v_max_f32_e32 v241, v241, v241
	v_med3_f32 v226, v226, s62, v95
	v_med3_f32 v227, v227, s62, v95
	v_med3_f32 v228, v228, s62, v95
	v_med3_f32 v229, v229, s62, v95
	v_med3_f32 v230, v230, s62, v95
	v_med3_f32 v231, v231, s62, v95
	v_med3_f32 v232, v232, s62, v95
	v_med3_f32 v233, v233, s62, v95
	v_med3_f32 v234, v234, s62, v95
	v_med3_f32 v235, v235, s62, v95
	v_med3_f32 v236, v236, s62, v95
	v_med3_f32 v237, v237, s62, v95
	v_med3_f32 v238, v238, s62, v95
	v_med3_f32 v239, v239, s62, v95
	v_med3_f32 v240, v240, s62, v95
	v_med3_f32 v241, v241, s62, v95
	v_mov_b32_e32 v242, 0
	v_mov_b32_e32 v243, 0
	v_mov_b32_e32 v244, 0
	v_mov_b32_e32 v245, 0
	v_cvt_pk_fp8_f32 v242, v226, v227
	v_cvt_pk_fp8_f32 v243, v230, v231
	v_cvt_pk_fp8_f32 v244, v234, v235
	v_cvt_pk_fp8_f32 v245, v238, v239
	v_cvt_pk_fp8_f32 v242, v228, v229 op_sel:[0,0,1]
	v_cvt_pk_fp8_f32 v243, v232, v233 op_sel:[0,0,1]
	v_cvt_pk_fp8_f32 v244, v236, v237 op_sel:[0,0,1]
	v_cvt_pk_fp8_f32 v245, v240, v241 op_sel:[0,0,1]
	s_nop 0
	global_store_dwordx4 v77, v[242:245], s[6:7]
	ds_read_b32 v226, v213
	ds_read_b32 v227, v213 offset:512
	ds_read_b32 v228, v213 offset:1024
	ds_read_b32 v229, v213 offset:1536
	ds_read_b32 v230, v213 offset:2048
	ds_read_b32 v231, v213 offset:2560
	ds_read_b32 v232, v213 offset:3072
	ds_read_b32 v233, v213 offset:3584
	ds_read_b32 v234, v213 offset:4096
	ds_read_b32 v235, v213 offset:4608
	ds_read_b32 v236, v213 offset:5120
	ds_read_b32 v237, v213 offset:5632
	ds_read_b32 v238, v213 offset:6144
	ds_read_b32 v239, v213 offset:6656
	ds_read_b32 v240, v213 offset:7168
	ds_read_b32 v241, v213 offset:7680
	s_waitcnt lgkmcnt(0)
	v_max_f32_e32 v226, v226, v226
	v_max_f32_e32 v227, v227, v227
	v_max_f32_e32 v228, v228, v228
	v_max_f32_e32 v229, v229, v229
	v_max_f32_e32 v230, v230, v230
	v_max_f32_e32 v231, v231, v231
	v_max_f32_e32 v232, v232, v232
	v_max_f32_e32 v233, v233, v233
	v_max_f32_e32 v234, v234, v234
	v_max_f32_e32 v235, v235, v235
	v_max_f32_e32 v236, v236, v236
	v_max_f32_e32 v237, v237, v237
	v_max_f32_e32 v238, v238, v238
	v_max_f32_e32 v239, v239, v239
	v_max_f32_e32 v240, v240, v240
	v_max_f32_e32 v241, v241, v241
	v_med3_f32 v226, v226, s62, v95
	v_med3_f32 v227, v227, s62, v95
	v_med3_f32 v228, v228, s62, v95
	v_med3_f32 v229, v229, s62, v95
	v_med3_f32 v230, v230, s62, v95
	v_med3_f32 v231, v231, s62, v95
	v_med3_f32 v232, v232, s62, v95
	v_med3_f32 v233, v233, s62, v95
	v_med3_f32 v234, v234, s62, v95
	v_med3_f32 v235, v235, s62, v95
	v_med3_f32 v236, v236, s62, v95
	v_med3_f32 v237, v237, s62, v95
	v_med3_f32 v238, v238, s62, v95
	v_med3_f32 v239, v239, s62, v95
	v_med3_f32 v240, v240, s62, v95
	v_med3_f32 v241, v241, s62, v95
	v_mov_b32_e32 v242, 0
	v_mov_b32_e32 v243, 0
	v_mov_b32_e32 v244, 0
	v_mov_b32_e32 v245, 0
	v_cvt_pk_fp8_f32 v242, v226, v227
	v_cvt_pk_fp8_f32 v243, v230, v231
	v_cvt_pk_fp8_f32 v244, v234, v235
	v_cvt_pk_fp8_f32 v245, v238, v239
	v_cvt_pk_fp8_f32 v242, v228, v229 op_sel:[0,0,1]
	v_cvt_pk_fp8_f32 v243, v232, v233 op_sel:[0,0,1]
	v_cvt_pk_fp8_f32 v244, v236, v237 op_sel:[0,0,1]
	v_cvt_pk_fp8_f32 v245, v240, v241 op_sel:[0,0,1]
	s_nop 0
	global_store_dwordx4 v78, v[242:245], s[6:7]
	s_waitcnt vmcnt(12)
	v_mul_f32_e32 v176, v34, v176
	v_mul_f32_e32 v177, v34, v177
	v_mul_f32_e32 v178, v34, v178
	v_mul_f32_e32 v179, v34, v179
	ds_write_b128 v210, v[176:179]
	v_mul_f32_e32 v180, v35, v180
	v_mul_f32_e32 v181, v35, v181
	v_mul_f32_e32 v182, v35, v182
	v_mul_f32_e32 v183, v35, v183
	ds_write_b128 v210, v[180:183] offset:1024
	v_mul_f32_e32 v184, v36, v184
	v_mul_f32_e32 v185, v36, v185
	v_mul_f32_e32 v186, v36, v186
	v_mul_f32_e32 v187, v36, v187
	ds_write_b128 v210, v[184:187] offset:2048
	v_mul_f32_e32 v188, v37, v188
	v_mul_f32_e32 v189, v37, v189
	v_mul_f32_e32 v190, v37, v190
	v_mul_f32_e32 v191, v37, v191
	ds_write_b128 v210, v[188:191] offset:3072
	v_mul_f32_e32 v192, v38, v192
	v_mul_f32_e32 v193, v38, v193
	v_mul_f32_e32 v194, v38, v194
	v_mul_f32_e32 v195, v38, v195
	ds_write_b128 v210, v[192:195] offset:4096
	v_mul_f32_e32 v196, v39, v196
	v_mul_f32_e32 v197, v39, v197
	v_mul_f32_e32 v198, v39, v198
	v_mul_f32_e32 v199, v39, v199
	ds_write_b128 v210, v[196:199] offset:5120
	v_mul_f32_e32 v200, v40, v200
	v_mul_f32_e32 v201, v40, v201
	v_mul_f32_e32 v202, v40, v202
	v_mul_f32_e32 v203, v40, v203
	ds_write_b128 v210, v[200:203] offset:6144
	v_mul_f32_e32 v204, v41, v204
	v_mul_f32_e32 v205, v41, v205
	v_mul_f32_e32 v206, v41, v206
	v_mul_f32_e32 v207, v41, v207
	ds_write_b128 v210, v[204:207] offset:7168
	s_waitcnt lgkmcnt(0)
	s_barrier
; #define GAS __attribute__((address_space(1)))
; #define LAS __attribute__((address_space(3)))
; #define LDS_WAIT() asm volatile("s_waitcnt lgkmcnt(0)" ::: "memory")
; __device__ __forceinline__ unsigned pk4_fp8(float a, float b, float c, float d) {
;     a = fminf(fmaxf(a, -448.f), 448.f); b = fminf(fmaxf(b, -448.f), 448.f); c = fminf(fmaxf(c, -448.f), 448.f); d = fminf(fmaxf(d, -448.f), 448.f);
;     int w = __builtin_amdgcn_cvt_pk_fp8_f32(a, b, 0, false); w = __builtin_amdgcn_cvt_pk_fp8_f32(c, d, w, true); return (unsigned)w; }
;     const int pr = item >> 1, kb = 2 * (pr / nblk) + (item & 1), nb = pr % nblk, k0 = 64 * kb, n0 = 32 * nb;
;     const int nr = n0 + (lane & 31); const int sc = MAP == 1 ? src_col_in(nr) : nr;
;     float v[32];
; #pragma unroll
;     for (int i = 0; i < 32; ++i) v[i] = sc >= 0 ? W[(size_t)(k0 + 2 * i + (lane >> 5)) * Nsrc + sc] : 0.f;
; #pragma unroll
;     for (int i = 0; i < 32; ++i) { const int k = k0 + 2 * i + (lane >> 5); float x = v[i] * wscale; if (KS) x *= (k < ksplit ? ksA[k] : ksB[k - ksplit]); scr[(2 * i + (lane >> 5)) * 33 + (lane & 31)] = x; }
;     LDS_WAIT(); asm volatile("" ::: "memory");
;     const int c = lane & 7;
; #pragma unroll
;     for (int j = 0; j < 4; ++j) { const int n = (lane >> 3) + 8 * j; const LAS float* s = scr + (8 * c) * 33 + n;
;         const unsigned long long o = (unsigned long long)pg8::pk4_fp8(s[0 * 33], s[1 * 33], s[2 * 33], s[3 * 33]) | ((unsigned long long)pg8::pk4_fp8(s[4 * 33], s[5 * 33], s[6 * 33], s[7 * 33]) << 32);
;         *(GAS unsigned long long*)(WT + (size_t)(n0 + n) * K + k0 + 8 * c) = o; }
;     LDS_WAIT(); asm volatile("" ::: "memory");
; }
	s_add_u32 s8, s34, 0x7000
	s_addc_u32 s9, s35, 0
	global_load_dwordx4 v[176:179], v74, s[8:9]
	s_add_u32 s8, s8, 0x20000
	s_addc_u32 s9, s9, 0
	global_load_dwordx4 v[180:183], v74, s[8:9]
	s_add_u32 s8, s8, 0x20000
	s_addc_u32 s9, s9, 0
	global_load_dwordx4 v[184:187], v74, s[8:9]
	s_add_u32 s8, s8, 0x20000
	s_addc_u32 s9, s9, 0
	global_load_dwordx4 v[188:191], v74, s[8:9]
	s_add_u32 s8, s8, 0x20000
	s_addc_u32 s9, s9, 0
	global_load_dwordx4 v[192:195], v74, s[8:9]
	s_add_u32 s8, s8, 0x20000
	s_addc_u32 s9, s9, 0
	global_load_dwordx4 v[196:199], v74, s[8:9]
	s_add_u32 s8, s8, 0x20000
	s_addc_u32 s9, s9, 0
	global_load_dwordx4 v[200:203], v74, s[8:9]
	s_add_u32 s8, s8, 0x20000
	s_addc_u32 s9, s9, 0
	global_load_dwordx4 v[204:207], v74, s[8:9]
	s_add_u32 s6, s36, 0x1400000
	s_addc_u32 s7, s37, 0
	ds_read_b32 v226, v212
	ds_read_b32 v227, v212 offset:512
	ds_read_b32 v228, v212 offset:1024
	ds_read_b32 v229, v212 offset:1536
	ds_read_b32 v230, v212 offset:2048
	ds_read_b32 v231, v212 offset:2560
	ds_read_b32 v232, v212 offset:3072
	ds_read_b32 v233, v212 offset:3584
	ds_read_b32 v234, v212 offset:4096
	ds_read_b32 v235, v212 offset:4608
	ds_read_b32 v236, v212 offset:5120
	ds_read_b32 v237, v212 offset:5632
	ds_read_b32 v238, v212 offset:6144
	ds_read_b32 v239, v212 offset:6656
	ds_read_b32 v240, v212 offset:7168
	ds_read_b32 v241, v212 offset:7680
	s_waitcnt lgkmcnt(0)
	v_max_f32_e32 v226, v226, v226
	v_max_f32_e32 v227, v227, v227
	v_max_f32_e32 v228, v228, v228
	v_max_f32_e32 v229, v229, v229
	v_max_f32_e32 v230, v230, v230
	v_max_f32_e32 v231, v231, v231
	v_max_f32_e32 v232, v232, v232
	v_max_f32_e32 v233, v233, v233
	v_max_f32_e32 v234, v234, v234
	v_max_f32_e32 v235, v235, v235
	v_max_f32_e32 v236, v236, v236
	v_max_f32_e32 v237, v237, v237
	v_max_f32_e32 v238, v238, v238
	v_max_f32_e32 v239, v239, v239
	v_max_f32_e32 v240, v240, v240
	v_max_f32_e32 v241, v241, v241
	v_med3_f32 v226, v226, s62, v95
	v_med3_f32 v227, v227, s62, v95
	v_med3_f32 v228, v228, s62, v95
	v_med3_f32 v229, v229, s62, v95
	v_med3_f32 v230, v230, s62, v95
	v_med3_f32 v231, v231, s62, v95
	v_med3_f32 v232, v232, s62, v95
	v_med3_f32 v233, v233, s62, v95
	v_med3_f32 v234, v234, s62, v95
	v_med3_f32 v235, v235, s62, v95
	v_med3_f32 v236, v236, s62, v95
	v_med3_f32 v237, v237, s62, v95
	v_med3_f32 v238, v238, s62, v95
	v_med3_f32 v239, v239, s62, v95
	v_med3_f32 v240, v240, s62, v95
	v_med3_f32 v241, v241, s62, v95
	v_mov_b32_e32 v242, 0
	v_mov_b32_e32 v243, 0
	v_mov_b32_e32 v244, 0
	v_mov_b32_e32 v245, 0
	v_cvt_pk_fp8_f32 v242, v226, v227
	v_cvt_pk_fp8_f32 v243, v230, v231
	v_cvt_pk_fp8_f32 v244, v234, v235
	v_cvt_pk_fp8_f32 v245, v238, v239
	v_cvt_pk_fp8_f32 v242, v228, v229 op_sel:[0,0,1]
	v_cvt_pk_fp8_f32 v243, v232, v233 op_sel:[0,0,1]
	v_cvt_pk_fp8_f32 v244, v236, v237 op_sel:[0,0,1]
	v_cvt_pk_fp8_f32 v245, v240, v241 op_sel:[0,0,1]
	s_nop 0
	global_store_dwordx4 v77, v[242:245], s[6:7]
	ds_read_b32 v226, v214
	ds_read_b32 v227, v214 offset:512
	ds_read_b32 v228, v214 offset:1024
	ds_read_b32 v229, v214 offset:1536
	ds_read_b32 v230, v214 offset:2048
	ds_read_b32 v231, v214 offset:2560
	ds_read_b32 v232, v214 offset:3072
	ds_read_b32 v233, v214 offset:3584
	ds_read_b32 v234, v214 offset:4096
	ds_read_b32 v235, v214 offset:4608
	ds_read_b32 v236, v214 offset:5120
	ds_read_b32 v237, v214 offset:5632
	ds_read_b32 v238, v214 offset:6144
	ds_read_b32 v239, v214 offset:6656
	ds_read_b32 v240, v214 offset:7168
	ds_read_b32 v241, v214 offset:7680
	s_waitcnt lgkmcnt(0)
	v_max_f32_e32 v226, v226, v226
	v_max_f32_e32 v227, v227, v227
	v_max_f32_e32 v228, v228, v228
	v_max_f32_e32 v229, v229, v229
	v_max_f32_e32 v230, v230, v230
	v_max_f32_e32 v231, v231, v231
	v_max_f32_e32 v232, v232, v232
	v_max_f32_e32 v233, v233, v233
	v_max_f32_e32 v234, v234, v234
	v_max_f32_e32 v235, v235, v235
	v_max_f32_e32 v236, v236, v236
	v_max_f32_e32 v237, v237, v237
	v_max_f32_e32 v238, v238, v238
	v_max_f32_e32 v239, v239, v239
	v_max_f32_e32 v240, v240, v240
	v_max_f32_e32 v241, v241, v241
	v_med3_f32 v226, v226, s62, v95
	v_med3_f32 v227, v227, s62, v95
	v_med3_f32 v228, v228, s62, v95
	v_med3_f32 v229, v229, s62, v95
	v_med3_f32 v230, v230, s62, v95
	v_med3_f32 v231, v231, s62, v95
	v_med3_f32 v232, v232, s62, v95
	v_med3_f32 v233, v233, s62, v95
	v_med3_f32 v234, v234, s62, v95
	v_med3_f32 v235, v235, s62, v95
	v_med3_f32 v236, v236, s62, v95
	v_med3_f32 v237, v237, s62, v95
	v_med3_f32 v238, v238, s62, v95
	v_med3_f32 v239, v239, s62, v95
	v_med3_f32 v240, v240, s62, v95
	v_med3_f32 v241, v241, s62, v95
	v_mov_b32_e32 v242, 0
	v_mov_b32_e32 v243, 0
	v_mov_b32_e32 v244, 0
	v_mov_b32_e32 v245, 0
	v_cvt_pk_fp8_f32 v242, v226, v227
	v_cvt_pk_fp8_f32 v243, v230, v231
	v_cvt_pk_fp8_f32 v244, v234, v235
	v_cvt_pk_fp8_f32 v245, v238, v239
	v_cvt_pk_fp8_f32 v242, v228, v229 op_sel:[0,0,1]
	v_cvt_pk_fp8_f32 v243, v232, v233 op_sel:[0,0,1]
	v_cvt_pk_fp8_f32 v244, v236, v237 op_sel:[0,0,1]
	v_cvt_pk_fp8_f32 v245, v240, v241 op_sel:[0,0,1]
	s_nop 0
	global_store_dwordx4 v78, v[242:245], s[6:7]
	s_waitcnt vmcnt(12)
	v_mul_f32_e32 v144, v34, v144
	v_mul_f32_e32 v145, v34, v145
	v_mul_f32_e32 v146, v34, v146
	v_mul_f32_e32 v147, v34, v147
	ds_write_b128 v209, v[144:147]
	v_mul_f32_e32 v148, v35, v148
	v_mul_f32_e32 v149, v35, v149
	v_mul_f32_e32 v150, v35, v150
	v_mul_f32_e32 v151, v35, v151
	ds_write_b128 v209, v[148:151] offset:1024
	v_mul_f32_e32 v152, v36, v152
	v_mul_f32_e32 v153, v36, v153
	v_mul_f32_e32 v154, v36, v154
	v_mul_f32_e32 v155, v36, v155
	ds_write_b128 v209, v[152:155] offset:2048
	v_mul_f32_e32 v156, v37, v156
	v_mul_f32_e32 v157, v37, v157
	v_mul_f32_e32 v158, v37, v158
	v_mul_f32_e32 v159, v37, v159
	ds_write_b128 v209, v[156:159] offset:3072
	v_mul_f32_e32 v160, v38, v160
	v_mul_f32_e32 v161, v38, v161
	v_mul_f32_e32 v162, v38, v162
	v_mul_f32_e32 v163, v38, v163
	ds_write_b128 v209, v[160:163] offset:4096
	v_mul_f32_e32 v164, v39, v164
	v_mul_f32_e32 v165, v39, v165
	v_mul_f32_e32 v166, v39, v166
	v_mul_f32_e32 v167, v39, v167
	ds_write_b128 v209, v[164:167] offset:5120
	v_mul_f32_e32 v168, v40, v168
	v_mul_f32_e32 v169, v40, v169
	v_mul_f32_e32 v170, v40, v170
	v_mul_f32_e32 v171, v40, v171
	ds_write_b128 v209, v[168:171] offset:6144
	v_mul_f32_e32 v172, v41, v172
	v_mul_f32_e32 v173, v41, v173
	v_mul_f32_e32 v174, v41, v174
	v_mul_f32_e32 v175, v41, v175
	ds_write_b128 v209, v[172:175] offset:7168
	s_waitcnt lgkmcnt(0)
	s_barrier
; #define GAS __attribute__((address_space(1)))
; #define LAS __attribute__((address_space(3)))
; #define LDS_WAIT() asm volatile("s_waitcnt lgkmcnt(0)" ::: "memory")
; __device__ __forceinline__ unsigned pk4_fp8(float a, float b, float c, float d) {
;     a = fminf(fmaxf(a, -448.f), 448.f); b = fminf(fmaxf(b, -448.f), 448.f); c = fminf(fmaxf(c, -448.f), 448.f); d = fminf(fmaxf(d, -448.f), 448.f);
;     int w = __builtin_amdgcn_cvt_pk_fp8_f32(a, b, 0, false); w = __builtin_amdgcn_cvt_pk_fp8_f32(c, d, w, true); return (unsigned)w; }
;     const int pr = item >> 1, kb = 2 * (pr / nblk) + (item & 1), nb = pr % nblk, k0 = 64 * kb, n0 = 32 * nb;
;     const int nr = n0 + (lane & 31); const int sc = MAP == 1 ? src_col_in(nr) : nr;
;     float v[32];
; #pragma unroll
;     for (int i = 0; i < 32; ++i) v[i] = sc >= 0 ? W[(size_t)(k0 + 2 * i + (lane >> 5)) * Nsrc + sc] : 0.f;
; #pragma unroll
;     for (int i = 0; i < 32; ++i) { const int k = k0 + 2 * i + (lane >> 5); float x = v[i] * wscale; if (KS) x *= (k < ksplit ? ksA[k] : ksB[k - ksplit]); scr[(2 * i + (lane >> 5)) * 33 + (lane & 31)] = x; }
;     LDS_WAIT(); asm volatile("" ::: "memory");
;     const int c = lane & 7;
; #pragma unroll
;     for (int j = 0; j < 4; ++j) { const int n = (lane >> 3) + 8 * j; const LAS float* s = scr + (8 * c) * 33 + n;
;         const unsigned long long o = (unsigned long long)pg8::pk4_fp8(s[0 * 33], s[1 * 33], s[2 * 33], s[3 * 33]) | ((unsigned long long)pg8::pk4_fp8(s[4 * 33], s[5 * 33], s[6 * 33], s[7 * 33]) << 32);
;         *(GAS unsigned long long*)(WT + (size_t)(n0 + n) * K + k0 + 8 * c) = o; }
;     LDS_WAIT(); asm volatile("" ::: "memory");
; }
	s_add_u32 s8, s34, 0x8000
	s_addc_u32 s9, s35, 0
	global_load_dwordx4 v[144:147], v74, s[8:9]
	s_add_u32 s8, s8, 0x20000
	s_addc_u32 s9, s9, 0
	global_load_dwordx4 v[148:151], v74, s[8:9]
	s_add_u32 s8, s8, 0x20000
	s_addc_u32 s9, s9, 0
	global_load_dwordx4 v[152:155], v74, s[8:9]
	s_add_u32 s8, s8, 0x20000
	s_addc_u32 s9, s9, 0
	global_load_dwordx4 v[156:159], v74, s[8:9]
	s_add_u32 s8, s8, 0x20000
	s_addc_u32 s9, s9, 0
	global_load_dwordx4 v[160:163], v74, s[8:9]
	s_add_u32 s8, s8, 0x20000
	s_addc_u32 s9, s9, 0
	global_load_dwordx4 v[164:167], v74, s[8:9]
	s_add_u32 s8, s8, 0x20000
	s_addc_u32 s9, s9, 0
	global_load_dwordx4 v[168:171], v74, s[8:9]
	s_add_u32 s8, s8, 0x20000
	s_addc_u32 s9, s9, 0
	global_load_dwordx4 v[172:175], v74, s[8:9]
	s_add_u32 s6, s36, 0x1800000
	s_addc_u32 s7, s37, 0
	ds_read_b32 v226, v211
	ds_read_b32 v227, v211 offset:512
	ds_read_b32 v228, v211 offset:1024
	ds_read_b32 v229, v211 offset:1536
	ds_read_b32 v230, v211 offset:2048
	ds_read_b32 v231, v211 offset:2560
	ds_read_b32 v232, v211 offset:3072
	ds_read_b32 v233, v211 offset:3584
	ds_read_b32 v234, v211 offset:4096
	ds_read_b32 v235, v211 offset:4608
	ds_read_b32 v236, v211 offset:5120
	ds_read_b32 v237, v211 offset:5632
	ds_read_b32 v238, v211 offset:6144
	ds_read_b32 v239, v211 offset:6656
	ds_read_b32 v240, v211 offset:7168
	ds_read_b32 v241, v211 offset:7680
	s_waitcnt lgkmcnt(0)
	v_max_f32_e32 v226, v226, v226
	v_max_f32_e32 v227, v227, v227
	v_max_f32_e32 v228, v228, v228
	v_max_f32_e32 v229, v229, v229
	v_max_f32_e32 v230, v230, v230
	v_max_f32_e32 v231, v231, v231
	v_max_f32_e32 v232, v232, v232
	v_max_f32_e32 v233, v233, v233
	v_max_f32_e32 v234, v234, v234
	v_max_f32_e32 v235, v235, v235
	v_max_f32_e32 v236, v236, v236
	v_max_f32_e32 v237, v237, v237
	v_max_f32_e32 v238, v238, v238
	v_max_f32_e32 v239, v239, v239
	v_max_f32_e32 v240, v240, v240
	v_max_f32_e32 v241, v241, v241
	v_med3_f32 v226, v226, s62, v95
	v_med3_f32 v227, v227, s62, v95
	v_med3_f32 v228, v228, s62, v95
	v_med3_f32 v229, v229, s62, v95
	v_med3_f32 v230, v230, s62, v95
	v_med3_f32 v231, v231, s62, v95
	v_med3_f32 v232, v232, s62, v95
	v_med3_f32 v233, v233, s62, v95
	v_med3_f32 v234, v234, s62, v95
	v_med3_f32 v235, v235, s62, v95
	v_med3_f32 v236, v236, s62, v95
	v_med3_f32 v237, v237, s62, v95
	v_med3_f32 v238, v238, s62, v95
	v_med3_f32 v239, v239, s62, v95
	v_med3_f32 v240, v240, s62, v95
	v_med3_f32 v241, v241, s62, v95
	v_mov_b32_e32 v242, 0
	v_mov_b32_e32 v243, 0
	v_mov_b32_e32 v244, 0
	v_mov_b32_e32 v245, 0
	v_cvt_pk_fp8_f32 v242, v226, v227
	v_cvt_pk_fp8_f32 v243, v230, v231
	v_cvt_pk_fp8_f32 v244, v234, v235
	v_cvt_pk_fp8_f32 v245, v238, v239
	v_cvt_pk_fp8_f32 v242, v228, v229 op_sel:[0,0,1]
	v_cvt_pk_fp8_f32 v243, v232, v233 op_sel:[0,0,1]
	v_cvt_pk_fp8_f32 v244, v236, v237 op_sel:[0,0,1]
	v_cvt_pk_fp8_f32 v245, v240, v241 op_sel:[0,0,1]
	s_nop 0
	global_store_dwordx4 v77, v[242:245], s[6:7]
	ds_read_b32 v226, v213
	ds_read_b32 v227, v213 offset:512
	ds_read_b32 v228, v213 offset:1024
	ds_read_b32 v229, v213 offset:1536
	ds_read_b32 v230, v213 offset:2048
	ds_read_b32 v231, v213 offset:2560
	ds_read_b32 v232, v213 offset:3072
	ds_read_b32 v233, v213 offset:3584
	ds_read_b32 v234, v213 offset:4096
	ds_read_b32 v235, v213 offset:4608
	ds_read_b32 v236, v213 offset:5120
	ds_read_b32 v237, v213 offset:5632
	ds_read_b32 v238, v213 offset:6144
	ds_read_b32 v239, v213 offset:6656
	ds_read_b32 v240, v213 offset:7168
	ds_read_b32 v241, v213 offset:7680
	s_waitcnt lgkmcnt(0)
	v_max_f32_e32 v226, v226, v226
	v_max_f32_e32 v227, v227, v227
	v_max_f32_e32 v228, v228, v228
	v_max_f32_e32 v229, v229, v229
	v_max_f32_e32 v230, v230, v230
	v_max_f32_e32 v231, v231, v231
	v_max_f32_e32 v232, v232, v232
	v_max_f32_e32 v233, v233, v233
	v_max_f32_e32 v234, v234, v234
	v_max_f32_e32 v235, v235, v235
	v_max_f32_e32 v236, v236, v236
	v_max_f32_e32 v237, v237, v237
	v_max_f32_e32 v238, v238, v238
	v_max_f32_e32 v239, v239, v239
	v_max_f32_e32 v240, v240, v240
	v_max_f32_e32 v241, v241, v241
	v_med3_f32 v226, v226, s62, v95
	v_med3_f32 v227, v227, s62, v95
	v_med3_f32 v228, v228, s62, v95
	v_med3_f32 v229, v229, s62, v95
	v_med3_f32 v230, v230, s62, v95
	v_med3_f32 v231, v231, s62, v95
	v_med3_f32 v232, v232, s62, v95
	v_med3_f32 v233, v233, s62, v95
	v_med3_f32 v234, v234, s62, v95
	v_med3_f32 v235, v235, s62, v95
	v_med3_f32 v236, v236, s62, v95
	v_med3_f32 v237, v237, s62, v95
	v_med3_f32 v238, v238, s62, v95
	v_med3_f32 v239, v239, s62, v95
	v_med3_f32 v240, v240, s62, v95
	v_med3_f32 v241, v241, s62, v95
	v_mov_b32_e32 v242, 0
	v_mov_b32_e32 v243, 0
	v_mov_b32_e32 v244, 0
	v_mov_b32_e32 v245, 0
	v_cvt_pk_fp8_f32 v242, v226, v227
	v_cvt_pk_fp8_f32 v243, v230, v231
	v_cvt_pk_fp8_f32 v244, v234, v235
	v_cvt_pk_fp8_f32 v245, v238, v239
	v_cvt_pk_fp8_f32 v242, v228, v229 op_sel:[0,0,1]
	v_cvt_pk_fp8_f32 v243, v232, v233 op_sel:[0,0,1]
	v_cvt_pk_fp8_f32 v244, v236, v237 op_sel:[0,0,1]
	v_cvt_pk_fp8_f32 v245, v240, v241 op_sel:[0,0,1]
	s_nop 0
	global_store_dwordx4 v78, v[242:245], s[6:7]
	s_waitcnt vmcnt(12)
	v_mul_f32_e32 v176, v34, v176
	v_mul_f32_e32 v177, v34, v177
	v_mul_f32_e32 v178, v34, v178
	v_mul_f32_e32 v179, v34, v179
	ds_write_b128 v210, v[176:179]
	v_mul_f32_e32 v180, v35, v180
	v_mul_f32_e32 v181, v35, v181
	v_mul_f32_e32 v182, v35, v182
	v_mul_f32_e32 v183, v35, v183
	ds_write_b128 v210, v[180:183] offset:1024
	v_mul_f32_e32 v184, v36, v184
	v_mul_f32_e32 v185, v36, v185
	v_mul_f32_e32 v186, v36, v186
	v_mul_f32_e32 v187, v36, v187
	ds_write_b128 v210, v[184:187] offset:2048
	v_mul_f32_e32 v188, v37, v188
	v_mul_f32_e32 v189, v37, v189
	v_mul_f32_e32 v190, v37, v190
	v_mul_f32_e32 v191, v37, v191
	ds_write_b128 v210, v[188:191] offset:3072
	v_mul_f32_e32 v192, v38, v192
	v_mul_f32_e32 v193, v38, v193
	v_mul_f32_e32 v194, v38, v194
	v_mul_f32_e32 v195, v38, v195
	ds_write_b128 v210, v[192:195] offset:4096
	v_mul_f32_e32 v196, v39, v196
	v_mul_f32_e32 v197, v39, v197
	v_mul_f32_e32 v198, v39, v198
	v_mul_f32_e32 v199, v39, v199
	ds_write_b128 v210, v[196:199] offset:5120
	v_mul_f32_e32 v200, v40, v200
	v_mul_f32_e32 v201, v40, v201
	v_mul_f32_e32 v202, v40, v202
	v_mul_f32_e32 v203, v40, v203
	ds_write_b128 v210, v[200:203] offset:6144
	v_mul_f32_e32 v204, v41, v204
	v_mul_f32_e32 v205, v41, v205
	v_mul_f32_e32 v206, v41, v206
	v_mul_f32_e32 v207, v41, v207
	ds_write_b128 v210, v[204:207] offset:7168
	s_waitcnt lgkmcnt(0)
	s_barrier
; #define GAS __attribute__((address_space(1)))
; #define LAS __attribute__((address_space(3)))
; #define LDS_WAIT() asm volatile("s_waitcnt lgkmcnt(0)" ::: "memory")
; __device__ __forceinline__ unsigned pk4_fp8(float a, float b, float c, float d) {
;     a = fminf(fmaxf(a, -448.f), 448.f); b = fminf(fmaxf(b, -448.f), 448.f); c = fminf(fmaxf(c, -448.f), 448.f); d = fminf(fmaxf(d, -448.f), 448.f);
;     int w = __builtin_amdgcn_cvt_pk_fp8_f32(a, b, 0, false); w = __builtin_amdgcn_cvt_pk_fp8_f32(c, d, w, true); return (unsigned)w; }
;     const int pr = item >> 1, kb = 2 * (pr / nblk) + (item & 1), nb = pr % nblk, k0 = 64 * kb, n0 = 32 * nb;
;     const int nr = n0 + (lane & 31); const int sc = MAP == 1 ? src_col_in(nr) : nr;
;     float v[32];
; #pragma unroll
;     for (int i = 0; i < 32; ++i) v[i] = sc >= 0 ? W[(size_t)(k0 + 2 * i + (lane >> 5)) * Nsrc + sc] : 0.f;
; #pragma unroll
;     for (int i = 0; i < 32; ++i) { const int k = k0 + 2 * i + (lane >> 5); float x = v[i] * wscale; if (KS) x *= (k < ksplit ? ksA[k] : ksB[k - ksplit]); scr[(2 * i + (lane >> 5)) * 33 + (lane & 31)] = x; }
;     LDS_WAIT(); asm volatile("" ::: "memory");
;     const int c = lane & 7;
; #pragma unroll
;     for (int j = 0; j < 4; ++j) { const int n = (lane >> 3) + 8 * j; const LAS float* s = scr + (8 * c) * 33 + n;
;         const unsigned long long o = (unsigned long long)pg8::pk4_fp8(s[0 * 33], s[1 * 33], s[2 * 33], s[3 * 33]) | ((unsigned long long)pg8::pk4_fp8(s[4 * 33], s[5 * 33], s[6 * 33], s[7 * 33]) << 32);
;         *(GAS unsigned long long*)(WT + (size_t)(n0 + n) * K + k0 + 8 * c) = o; }
;     LDS_WAIT(); asm volatile("" ::: "memory");
; }
	s_add_u32 s8, s34, 0x9000
	s_addc_u32 s9, s35, 0
	global_load_dwordx4 v[176:179], v74, s[8:9]
	s_add_u32 s8, s8, 0x20000
	s_addc_u32 s9, s9, 0
	global_load_dwordx4 v[180:183], v74, s[8:9]
	s_add_u32 s8, s8, 0x20000
	s_addc_u32 s9, s9, 0
	global_load_dwordx4 v[184:187], v74, s[8:9]
	s_add_u32 s8, s8, 0x20000
	s_addc_u32 s9, s9, 0
	global_load_dwordx4 v[188:191], v74, s[8:9]
	s_add_u32 s8, s8, 0x20000
	s_addc_u32 s9, s9, 0
	global_load_dwordx4 v[192:195], v74, s[8:9]
	s_add_u32 s8, s8, 0x20000
	s_addc_u32 s9, s9, 0
	global_load_dwordx4 v[196:199], v74, s[8:9]
	s_add_u32 s8, s8, 0x20000
	s_addc_u32 s9, s9, 0
	global_load_dwordx4 v[200:203], v74, s[8:9]
	s_add_u32 s8, s8, 0x20000
	s_addc_u32 s9, s9, 0
	global_load_dwordx4 v[204:207], v74, s[8:9]
	s_add_u32 s6, s36, 0x1c00000
	s_addc_u32 s7, s37, 0
	ds_read_b32 v226, v212
	ds_read_b32 v227, v212 offset:512
	ds_read_b32 v228, v212 offset:1024
	ds_read_b32 v229, v212 offset:1536
	ds_read_b32 v230, v212 offset:2048
	ds_read_b32 v231, v212 offset:2560
	ds_read_b32 v232, v212 offset:3072
	ds_read_b32 v233, v212 offset:3584
	ds_read_b32 v234, v212 offset:4096
	ds_read_b32 v235, v212 offset:4608
	ds_read_b32 v236, v212 offset:5120
	ds_read_b32 v237, v212 offset:5632
	ds_read_b32 v238, v212 offset:6144
	ds_read_b32 v239, v212 offset:6656
	ds_read_b32 v240, v212 offset:7168
	ds_read_b32 v241, v212 offset:7680
	s_waitcnt lgkmcnt(0)
	v_max_f32_e32 v226, v226, v226
	v_max_f32_e32 v227, v227, v227
	v_max_f32_e32 v228, v228, v228
	v_max_f32_e32 v229, v229, v229
	v_max_f32_e32 v230, v230, v230
	v_max_f32_e32 v231, v231, v231
	v_max_f32_e32 v232, v232, v232
	v_max_f32_e32 v233, v233, v233
	v_max_f32_e32 v234, v234, v234
	v_max_f32_e32 v235, v235, v235
	v_max_f32_e32 v236, v236, v236
	v_max_f32_e32 v237, v237, v237
	v_max_f32_e32 v238, v238, v238
	v_max_f32_e32 v239, v239, v239
	v_max_f32_e32 v240, v240, v240
	v_max_f32_e32 v241, v241, v241
	v_med3_f32 v226, v226, s62, v95
	v_med3_f32 v227, v227, s62, v95
	v_med3_f32 v228, v228, s62, v95
	v_med3_f32 v229, v229, s62, v95
	v_med3_f32 v230, v230, s62, v95
	v_med3_f32 v231, v231, s62, v95
	v_med3_f32 v232, v232, s62, v95
	v_med3_f32 v233, v233, s62, v95
	v_med3_f32 v234, v234, s62, v95
	v_med3_f32 v235, v235, s62, v95
	v_med3_f32 v236, v236, s62, v95
	v_med3_f32 v237, v237, s62, v95
	v_med3_f32 v238, v238, s62, v95
	v_med3_f32 v239, v239, s62, v95
	v_med3_f32 v240, v240, s62, v95
	v_med3_f32 v241, v241, s62, v95
	v_mov_b32_e32 v242, 0
	v_mov_b32_e32 v243, 0
	v_mov_b32_e32 v244, 0
	v_mov_b32_e32 v245, 0
	v_cvt_pk_fp8_f32 v242, v226, v227
	v_cvt_pk_fp8_f32 v243, v230, v231
	v_cvt_pk_fp8_f32 v244, v234, v235
	v_cvt_pk_fp8_f32 v245, v238, v239
	v_cvt_pk_fp8_f32 v242, v228, v229 op_sel:[0,0,1]
	v_cvt_pk_fp8_f32 v243, v232, v233 op_sel:[0,0,1]
	v_cvt_pk_fp8_f32 v244, v236, v237 op_sel:[0,0,1]
	v_cvt_pk_fp8_f32 v245, v240, v241 op_sel:[0,0,1]
	s_nop 0
	global_store_dwordx4 v77, v[242:245], s[6:7]
	ds_read_b32 v226, v214
	ds_read_b32 v227, v214 offset:512
	ds_read_b32 v228, v214 offset:1024
	ds_read_b32 v229, v214 offset:1536
	ds_read_b32 v230, v214 offset:2048
	ds_read_b32 v231, v214 offset:2560
	ds_read_b32 v232, v214 offset:3072
	ds_read_b32 v233, v214 offset:3584
	ds_read_b32 v234, v214 offset:4096
	ds_read_b32 v235, v214 offset:4608
	ds_read_b32 v236, v214 offset:5120
	ds_read_b32 v237, v214 offset:5632
	ds_read_b32 v238, v214 offset:6144
	ds_read_b32 v239, v214 offset:6656
	ds_read_b32 v240, v214 offset:7168
	ds_read_b32 v241, v214 offset:7680
	s_waitcnt lgkmcnt(0)
	v_max_f32_e32 v226, v226, v226
	v_max_f32_e32 v227, v227, v227
	v_max_f32_e32 v228, v228, v228
	v_max_f32_e32 v229, v229, v229
	v_max_f32_e32 v230, v230, v230
	v_max_f32_e32 v231, v231, v231
	v_max_f32_e32 v232, v232, v232
	v_max_f32_e32 v233, v233, v233
	v_max_f32_e32 v234, v234, v234
	v_max_f32_e32 v235, v235, v235
	v_max_f32_e32 v236, v236, v236
	v_max_f32_e32 v237, v237, v237
	v_max_f32_e32 v238, v238, v238
	v_max_f32_e32 v239, v239, v239
	v_max_f32_e32 v240, v240, v240
	v_max_f32_e32 v241, v241, v241
	v_med3_f32 v226, v226, s62, v95
	v_med3_f32 v227, v227, s62, v95
	v_med3_f32 v228, v228, s62, v95
	v_med3_f32 v229, v229, s62, v95
	v_med3_f32 v230, v230, s62, v95
	v_med3_f32 v231, v231, s62, v95
	v_med3_f32 v232, v232, s62, v95
	v_med3_f32 v233, v233, s62, v95
	v_med3_f32 v234, v234, s62, v95
	v_med3_f32 v235, v235, s62, v95
	v_med3_f32 v236, v236, s62, v95
	v_med3_f32 v237, v237, s62, v95
	v_med3_f32 v238, v238, s62, v95
	v_med3_f32 v239, v239, s62, v95
	v_med3_f32 v240, v240, s62, v95
	v_med3_f32 v241, v241, s62, v95
	v_mov_b32_e32 v242, 0
	v_mov_b32_e32 v243, 0
	v_mov_b32_e32 v244, 0
	v_mov_b32_e32 v245, 0
	v_cvt_pk_fp8_f32 v242, v226, v227
	v_cvt_pk_fp8_f32 v243, v230, v231
	v_cvt_pk_fp8_f32 v244, v234, v235
	v_cvt_pk_fp8_f32 v245, v238, v239
	v_cvt_pk_fp8_f32 v242, v228, v229 op_sel:[0,0,1]
	v_cvt_pk_fp8_f32 v243, v232, v233 op_sel:[0,0,1]
	v_cvt_pk_fp8_f32 v244, v236, v237 op_sel:[0,0,1]
	v_cvt_pk_fp8_f32 v245, v240, v241 op_sel:[0,0,1]
	s_nop 0
	global_store_dwordx4 v78, v[242:245], s[6:7]
	s_waitcnt vmcnt(12)
	v_mul_f32_e32 v144, v34, v144
	v_mul_f32_e32 v145, v34, v145
	v_mul_f32_e32 v146, v34, v146
	v_mul_f32_e32 v147, v34, v147
	ds_write_b128 v209, v[144:147]
	v_mul_f32_e32 v148, v35, v148
	v_mul_f32_e32 v149, v35, v149
	v_mul_f32_e32 v150, v35, v150
	v_mul_f32_e32 v151, v35, v151
	ds_write_b128 v209, v[148:151] offset:1024
	v_mul_f32_e32 v152, v36, v152
	v_mul_f32_e32 v153, v36, v153
	v_mul_f32_e32 v154, v36, v154
	v_mul_f32_e32 v155, v36, v155
	ds_write_b128 v209, v[152:155] offset:2048
	v_mul_f32_e32 v156, v37, v156
	v_mul_f32_e32 v157, v37, v157
	v_mul_f32_e32 v158, v37, v158
	v_mul_f32_e32 v159, v37, v159
	ds_write_b128 v209, v[156:159] offset:3072
	v_mul_f32_e32 v160, v38, v160
	v_mul_f32_e32 v161, v38, v161
	v_mul_f32_e32 v162, v38, v162
	v_mul_f32_e32 v163, v38, v163
	ds_write_b128 v209, v[160:163] offset:4096
	v_mul_f32_e32 v164, v39, v164
	v_mul_f32_e32 v165, v39, v165
	v_mul_f32_e32 v166, v39, v166
	v_mul_f32_e32 v167, v39, v167
	ds_write_b128 v209, v[164:167] offset:5120
	v_mul_f32_e32 v168, v40, v168
	v_mul_f32_e32 v169, v40, v169
	v_mul_f32_e32 v170, v40, v170
	v_mul_f32_e32 v171, v40, v171
	ds_write_b128 v209, v[168:171] offset:6144
	v_mul_f32_e32 v172, v41, v172
	v_mul_f32_e32 v173, v41, v173
	v_mul_f32_e32 v174, v41, v174
	v_mul_f32_e32 v175, v41, v175
	ds_write_b128 v209, v[172:175] offset:7168
	s_waitcnt lgkmcnt(0)
	s_barrier
; #define GAS __attribute__((address_space(1)))
; #define LAS __attribute__((address_space(3)))
; #define LDS_WAIT() asm volatile("s_waitcnt lgkmcnt(0)" ::: "memory")
; __device__ __forceinline__ unsigned pk4_fp8(float a, float b, float c, float d) {
;     a = fminf(fmaxf(a, -448.f), 448.f); b = fminf(fmaxf(b, -448.f), 448.f); c = fminf(fmaxf(c, -448.f), 448.f); d = fminf(fmaxf(d, -448.f), 448.f);
;     int w = __builtin_amdgcn_cvt_pk_fp8_f32(a, b, 0, false); w = __builtin_amdgcn_cvt_pk_fp8_f32(c, d, w, true); return (unsigned)w; }
;     const int pr = item >> 1, kb = 2 * (pr / nblk) + (item & 1), nb = pr % nblk, k0 = 64 * kb, n0 = 32 * nb;
;     const int nr = n0 + (lane & 31); const int sc = MAP == 1 ? src_col_in(nr) : nr;
;     float v[32];
; #pragma unroll
;     for (int i = 0; i < 32; ++i) v[i] = sc >= 0 ? W[(size_t)(k0 + 2 * i + (lane >> 5)) * Nsrc + sc] : 0.f;
; #pragma unroll
;     for (int i = 0; i < 32; ++i) { const int k = k0 + 2 * i + (lane >> 5); float x = v[i] * wscale; if (KS) x *= (k < ksplit ? ksA[k] : ksB[k - ksplit]); scr[(2 * i + (lane >> 5)) * 33 + (lane & 31)] = x; }
;     LDS_WAIT(); asm volatile("" ::: "memory");
;     const int c = lane & 7;
; #pragma unroll
;     for (int j = 0; j < 4; ++j) { const int n = (lane >> 3) + 8 * j; const LAS float* s = scr + (8 * c) * 33 + n;
;         const unsigned long long o = (unsigned long long)pg8::pk4_fp8(s[0 * 33], s[1 * 33], s[2 * 33], s[3 * 33]) | ((unsigned long long)pg8::pk4_fp8(s[4 * 33], s[5 * 33], s[6 * 33], s[7 * 33]) << 32);
;         *(GAS unsigned long long*)(WT + (size_t)(n0 + n) * K + k0 + 8 * c) = o; }
;     LDS_WAIT(); asm volatile("" ::: "memory");
; }
	s_add_u32 s8, s34, 0xa000
	s_addc_u32 s9, s35, 0
	global_load_dwordx4 v[144:147], v74, s[8:9]
	s_add_u32 s8, s8, 0x20000
	s_addc_u32 s9, s9, 0
	global_load_dwordx4 v[148:151], v74, s[8:9]
	s_add_u32 s8, s8, 0x20000
	s_addc_u32 s9, s9, 0
	global_load_dwordx4 v[152:155], v74, s[8:9]
	s_add_u32 s8, s8, 0x20000
	s_addc_u32 s9, s9, 0
	global_load_dwordx4 v[156:159], v74, s[8:9]
	s_add_u32 s8, s8, 0x20000
	s_addc_u32 s9, s9, 0
	global_load_dwordx4 v[160:163], v74, s[8:9]
	s_add_u32 s8, s8, 0x20000
	s_addc_u32 s9, s9, 0
	global_load_dwordx4 v[164:167], v74, s[8:9]
	s_add_u32 s8, s8, 0x20000
	s_addc_u32 s9, s9, 0
	global_load_dwordx4 v[168:171], v74, s[8:9]
	s_add_u32 s8, s8, 0x20000
	s_addc_u32 s9, s9, 0
	global_load_dwordx4 v[172:175], v74, s[8:9]
	s_add_u32 s6, s36, 0x2000000
	s_addc_u32 s7, s37, 0
	ds_read_b32 v226, v211
	ds_read_b32 v227, v211 offset:512
	ds_read_b32 v228, v211 offset:1024
	ds_read_b32 v229, v211 offset:1536
	ds_read_b32 v230, v211 offset:2048
	ds_read_b32 v231, v211 offset:2560
	ds_read_b32 v232, v211 offset:3072
	ds_read_b32 v233, v211 offset:3584
	ds_read_b32 v234, v211 offset:4096
	ds_read_b32 v235, v211 offset:4608
	ds_read_b32 v236, v211 offset:5120
	ds_read_b32 v237, v211 offset:5632
	ds_read_b32 v238, v211 offset:6144
	ds_read_b32 v239, v211 offset:6656
	ds_read_b32 v240, v211 offset:7168
	ds_read_b32 v241, v211 offset:7680
	s_waitcnt lgkmcnt(0)
	v_max_f32_e32 v226, v226, v226
	v_max_f32_e32 v227, v227, v227
	v_max_f32_e32 v228, v228, v228
	v_max_f32_e32 v229, v229, v229
	v_max_f32_e32 v230, v230, v230
	v_max_f32_e32 v231, v231, v231
	v_max_f32_e32 v232, v232, v232
	v_max_f32_e32 v233, v233, v233
	v_max_f32_e32 v234, v234, v234
	v_max_f32_e32 v235, v235, v235
	v_max_f32_e32 v236, v236, v236
	v_max_f32_e32 v237, v237, v237
	v_max_f32_e32 v238, v238, v238
	v_max_f32_e32 v239, v239, v239
	v_max_f32_e32 v240, v240, v240
	v_max_f32_e32 v241, v241, v241
	v_med3_f32 v226, v226, s62, v95
	v_med3_f32 v227, v227, s62, v95
	v_med3_f32 v228, v228, s62, v95
	v_med3_f32 v229, v229, s62, v95
	v_med3_f32 v230, v230, s62, v95
	v_med3_f32 v231, v231, s62, v95
	v_med3_f32 v232, v232, s62, v95
	v_med3_f32 v233, v233, s62, v95
	v_med3_f32 v234, v234, s62, v95
	v_med3_f32 v235, v235, s62, v95
	v_med3_f32 v236, v236, s62, v95
	v_med3_f32 v237, v237, s62, v95
	v_med3_f32 v238, v238, s62, v95
	v_med3_f32 v239, v239, s62, v95
	v_med3_f32 v240, v240, s62, v95
	v_med3_f32 v241, v241, s62, v95
	v_mov_b32_e32 v242, 0
	v_mov_b32_e32 v243, 0
	v_mov_b32_e32 v244, 0
	v_mov_b32_e32 v245, 0
	v_cvt_pk_fp8_f32 v242, v226, v227
	v_cvt_pk_fp8_f32 v243, v230, v231
	v_cvt_pk_fp8_f32 v244, v234, v235
	v_cvt_pk_fp8_f32 v245, v238, v239
	v_cvt_pk_fp8_f32 v242, v228, v229 op_sel:[0,0,1]
	v_cvt_pk_fp8_f32 v243, v232, v233 op_sel:[0,0,1]
	v_cvt_pk_fp8_f32 v244, v236, v237 op_sel:[0,0,1]
	v_cvt_pk_fp8_f32 v245, v240, v241 op_sel:[0,0,1]
	s_nop 0
	global_store_dwordx4 v77, v[242:245], s[6:7]
	ds_read_b32 v226, v213
	ds_read_b32 v227, v213 offset:512
	ds_read_b32 v228, v213 offset:1024
	ds_read_b32 v229, v213 offset:1536
	ds_read_b32 v230, v213 offset:2048
	ds_read_b32 v231, v213 offset:2560
	ds_read_b32 v232, v213 offset:3072
	ds_read_b32 v233, v213 offset:3584
	ds_read_b32 v234, v213 offset:4096
	ds_read_b32 v235, v213 offset:4608
	ds_read_b32 v236, v213 offset:5120
	ds_read_b32 v237, v213 offset:5632
	ds_read_b32 v238, v213 offset:6144
	ds_read_b32 v239, v213 offset:6656
	ds_read_b32 v240, v213 offset:7168
	ds_read_b32 v241, v213 offset:7680
	s_waitcnt lgkmcnt(0)
	v_max_f32_e32 v226, v226, v226
	v_max_f32_e32 v227, v227, v227
	v_max_f32_e32 v228, v228, v228
	v_max_f32_e32 v229, v229, v229
	v_max_f32_e32 v230, v230, v230
	v_max_f32_e32 v231, v231, v231
	v_max_f32_e32 v232, v232, v232
	v_max_f32_e32 v233, v233, v233
	v_max_f32_e32 v234, v234, v234
	v_max_f32_e32 v235, v235, v235
	v_max_f32_e32 v236, v236, v236
	v_max_f32_e32 v237, v237, v237
	v_max_f32_e32 v238, v238, v238
	v_max_f32_e32 v239, v239, v239
	v_max_f32_e32 v240, v240, v240
	v_max_f32_e32 v241, v241, v241
	v_med3_f32 v226, v226, s62, v95
	v_med3_f32 v227, v227, s62, v95
	v_med3_f32 v228, v228, s62, v95
	v_med3_f32 v229, v229, s62, v95
	v_med3_f32 v230, v230, s62, v95
	v_med3_f32 v231, v231, s62, v95
	v_med3_f32 v232, v232, s62, v95
	v_med3_f32 v233, v233, s62, v95
	v_med3_f32 v234, v234, s62, v95
	v_med3_f32 v235, v235, s62, v95
	v_med3_f32 v236, v236, s62, v95
	v_med3_f32 v237, v237, s62, v95
	v_med3_f32 v238, v238, s62, v95
	v_med3_f32 v239, v239, s62, v95
	v_med3_f32 v240, v240, s62, v95
	v_med3_f32 v241, v241, s62, v95
	v_mov_b32_e32 v242, 0
	v_mov_b32_e32 v243, 0
	v_mov_b32_e32 v244, 0
	v_mov_b32_e32 v245, 0
	v_cvt_pk_fp8_f32 v242, v226, v227
	v_cvt_pk_fp8_f32 v243, v230, v231
	v_cvt_pk_fp8_f32 v244, v234, v235
	v_cvt_pk_fp8_f32 v245, v238, v239
	v_cvt_pk_fp8_f32 v242, v228, v229 op_sel:[0,0,1]
	v_cvt_pk_fp8_f32 v243, v232, v233 op_sel:[0,0,1]
	v_cvt_pk_fp8_f32 v244, v236, v237 op_sel:[0,0,1]
	v_cvt_pk_fp8_f32 v245, v240, v241 op_sel:[0,0,1]
	s_nop 0
	global_store_dwordx4 v78, v[242:245], s[6:7]
	s_waitcnt vmcnt(12)
	v_mul_f32_e32 v176, v34, v176
	v_mul_f32_e32 v177, v34, v177
	v_mul_f32_e32 v178, v34, v178
	v_mul_f32_e32 v179, v34, v179
	ds_write_b128 v210, v[176:179]
	v_mul_f32_e32 v180, v35, v180
	v_mul_f32_e32 v181, v35, v181
	v_mul_f32_e32 v182, v35, v182
	v_mul_f32_e32 v183, v35, v183
	ds_write_b128 v210, v[180:183] offset:1024
	v_mul_f32_e32 v184, v36, v184
	v_mul_f32_e32 v185, v36, v185
	v_mul_f32_e32 v186, v36, v186
	v_mul_f32_e32 v187, v36, v187
	ds_write_b128 v210, v[184:187] offset:2048
	v_mul_f32_e32 v188, v37, v188
	v_mul_f32_e32 v189, v37, v189
	v_mul_f32_e32 v190, v37, v190
	v_mul_f32_e32 v191, v37, v191
	ds_write_b128 v210, v[188:191] offset:3072
	v_mul_f32_e32 v192, v38, v192
	v_mul_f32_e32 v193, v38, v193
	v_mul_f32_e32 v194, v38, v194
	v_mul_f32_e32 v195, v38, v195
	ds_write_b128 v210, v[192:195] offset:4096
	v_mul_f32_e32 v196, v39, v196
	v_mul_f32_e32 v197, v39, v197
	v_mul_f32_e32 v198, v39, v198
	v_mul_f32_e32 v199, v39, v199
	ds_write_b128 v210, v[196:199] offset:5120
	v_mul_f32_e32 v200, v40, v200
	v_mul_f32_e32 v201, v40, v201
	v_mul_f32_e32 v202, v40, v202
	v_mul_f32_e32 v203, v40, v203
	ds_write_b128 v210, v[200:203] offset:6144
	v_mul_f32_e32 v204, v41, v204
	v_mul_f32_e32 v205, v41, v205
	v_mul_f32_e32 v206, v41, v206
	v_mul_f32_e32 v207, v41, v207
	ds_write_b128 v210, v[204:207] offset:7168
	s_waitcnt lgkmcnt(0)
	s_barrier
; #define GAS __attribute__((address_space(1)))
; #define LAS __attribute__((address_space(3)))
; #define LDS_WAIT() asm volatile("s_waitcnt lgkmcnt(0)" ::: "memory")
; __device__ __forceinline__ unsigned pk4_fp8(float a, float b, float c, float d) {
;     a = fminf(fmaxf(a, -448.f), 448.f); b = fminf(fmaxf(b, -448.f), 448.f); c = fminf(fmaxf(c, -448.f), 448.f); d = fminf(fmaxf(d, -448.f), 448.f);
;     int w = __builtin_amdgcn_cvt_pk_fp8_f32(a, b, 0, false); w = __builtin_amdgcn_cvt_pk_fp8_f32(c, d, w, true); return (unsigned)w; }
;     const int pr = item >> 1, kb = 2 * (pr / nblk) + (item & 1), nb = pr % nblk, k0 = 64 * kb, n0 = 32 * nb;
;     const int nr = n0 + (lane & 31); const int sc = MAP == 1 ? src_col_in(nr) : nr;
;     float v[32];
; #pragma unroll
;     for (int i = 0; i < 32; ++i) v[i] = sc >= 0 ? W[(size_t)(k0 + 2 * i + (lane >> 5)) * Nsrc + sc] : 0.f;
; #pragma unroll
;     for (int i = 0; i < 32; ++i) { const int k = k0 + 2 * i + (lane >> 5); float x = v[i] * wscale; if (KS) x *= (k < ksplit ? ksA[k] : ksB[k - ksplit]); scr[(2 * i + (lane >> 5)) * 33 + (lane & 31)] = x; }
;     LDS_WAIT(); asm volatile("" ::: "memory");
;     const int c = lane & 7;
; #pragma unroll
;     for (int j = 0; j < 4; ++j) { const int n = (lane >> 3) + 8 * j; const LAS float* s = scr + (8 * c) * 33 + n;
;         const unsigned long long o = (unsigned long long)pg8::pk4_fp8(s[0 * 33], s[1 * 33], s[2 * 33], s[3 * 33]) | ((unsigned long long)pg8::pk4_fp8(s[4 * 33], s[5 * 33], s[6 * 33], s[7 * 33]) << 32);
;         *(GAS unsigned long long*)(WT + (size_t)(n0 + n) * K + k0 + 8 * c) = o; }
;     LDS_WAIT(); asm volatile("" ::: "memory");
; }
	s_add_u32 s8, s34, 0xb000
	s_addc_u32 s9, s35, 0
	global_load_dwordx4 v[176:179], v74, s[8:9]
	s_add_u32 s8, s8, 0x20000
	s_addc_u32 s9, s9, 0
	global_load_dwordx4 v[180:183], v74, s[8:9]
	s_add_u32 s8, s8, 0x20000
	s_addc_u32 s9, s9, 0
	global_load_dwordx4 v[184:187], v74, s[8:9]
	s_add_u32 s8, s8, 0x20000
	s_addc_u32 s9, s9, 0
	global_load_dwordx4 v[188:191], v74, s[8:9]
	s_add_u32 s8, s8, 0x20000
	s_addc_u32 s9, s9, 0
	global_load_dwordx4 v[192:195], v74, s[8:9]
	s_add_u32 s8, s8, 0x20000
	s_addc_u32 s9, s9, 0
	global_load_dwordx4 v[196:199], v74, s[8:9]
	s_add_u32 s8, s8, 0x20000
	s_addc_u32 s9, s9, 0
	global_load_dwordx4 v[200:203], v74, s[8:9]
	s_add_u32 s8, s8, 0x20000
	s_addc_u32 s9, s9, 0
	global_load_dwordx4 v[204:207], v74, s[8:9]
	s_add_u32 s6, s36, 0x2400000
	s_addc_u32 s7, s37, 0
	ds_read_b32 v226, v212
	ds_read_b32 v227, v212 offset:512
	ds_read_b32 v228, v212 offset:1024
	ds_read_b32 v229, v212 offset:1536
	ds_read_b32 v230, v212 offset:2048
	ds_read_b32 v231, v212 offset:2560
	ds_read_b32 v232, v212 offset:3072
	ds_read_b32 v233, v212 offset:3584
	ds_read_b32 v234, v212 offset:4096
	ds_read_b32 v235, v212 offset:4608
	ds_read_b32 v236, v212 offset:5120
	ds_read_b32 v237, v212 offset:5632
	ds_read_b32 v238, v212 offset:6144
	ds_read_b32 v239, v212 offset:6656
	ds_read_b32 v240, v212 offset:7168
	ds_read_b32 v241, v212 offset:7680
	s_waitcnt lgkmcnt(0)
	v_max_f32_e32 v226, v226, v226
	v_max_f32_e32 v227, v227, v227
	v_max_f32_e32 v228, v228, v228
	v_max_f32_e32 v229, v229, v229
	v_max_f32_e32 v230, v230, v230
	v_max_f32_e32 v231, v231, v231
	v_max_f32_e32 v232, v232, v232
	v_max_f32_e32 v233, v233, v233
	v_max_f32_e32 v234, v234, v234
	v_max_f32_e32 v235, v235, v235
	v_max_f32_e32 v236, v236, v236
	v_max_f32_e32 v237, v237, v237
	v_max_f32_e32 v238, v238, v238
	v_max_f32_e32 v239, v239, v239
	v_max_f32_e32 v240, v240, v240
	v_max_f32_e32 v241, v241, v241
	v_med3_f32 v226, v226, s62, v95
	v_med3_f32 v227, v227, s62, v95
	v_med3_f32 v228, v228, s62, v95
	v_med3_f32 v229, v229, s62, v95
	v_med3_f32 v230, v230, s62, v95
	v_med3_f32 v231, v231, s62, v95
	v_med3_f32 v232, v232, s62, v95
	v_med3_f32 v233, v233, s62, v95
	v_med3_f32 v234, v234, s62, v95
	v_med3_f32 v235, v235, s62, v95
	v_med3_f32 v236, v236, s62, v95
	v_med3_f32 v237, v237, s62, v95
	v_med3_f32 v238, v238, s62, v95
	v_med3_f32 v239, v239, s62, v95
	v_med3_f32 v240, v240, s62, v95
	v_med3_f32 v241, v241, s62, v95
	v_mov_b32_e32 v242, 0
	v_mov_b32_e32 v243, 0
	v_mov_b32_e32 v244, 0
	v_mov_b32_e32 v245, 0
	v_cvt_pk_fp8_f32 v242, v226, v227
	v_cvt_pk_fp8_f32 v243, v230, v231
	v_cvt_pk_fp8_f32 v244, v234, v235
	v_cvt_pk_fp8_f32 v245, v238, v239
	v_cvt_pk_fp8_f32 v242, v228, v229 op_sel:[0,0,1]
	v_cvt_pk_fp8_f32 v243, v232, v233 op_sel:[0,0,1]
	v_cvt_pk_fp8_f32 v244, v236, v237 op_sel:[0,0,1]
	v_cvt_pk_fp8_f32 v245, v240, v241 op_sel:[0,0,1]
	s_nop 0
	global_store_dwordx4 v77, v[242:245], s[6:7]
	ds_read_b32 v226, v214
	ds_read_b32 v227, v214 offset:512
	ds_read_b32 v228, v214 offset:1024
	ds_read_b32 v229, v214 offset:1536
	ds_read_b32 v230, v214 offset:2048
	ds_read_b32 v231, v214 offset:2560
	ds_read_b32 v232, v214 offset:3072
	ds_read_b32 v233, v214 offset:3584
	ds_read_b32 v234, v214 offset:4096
	ds_read_b32 v235, v214 offset:4608
	ds_read_b32 v236, v214 offset:5120
	ds_read_b32 v237, v214 offset:5632
	ds_read_b32 v238, v214 offset:6144
	ds_read_b32 v239, v214 offset:6656
	ds_read_b32 v240, v214 offset:7168
	ds_read_b32 v241, v214 offset:7680
	s_waitcnt lgkmcnt(0)
	v_max_f32_e32 v226, v226, v226
	v_max_f32_e32 v227, v227, v227
	v_max_f32_e32 v228, v228, v228
	v_max_f32_e32 v229, v229, v229
	v_max_f32_e32 v230, v230, v230
	v_max_f32_e32 v231, v231, v231
	v_max_f32_e32 v232, v232, v232
	v_max_f32_e32 v233, v233, v233
	v_max_f32_e32 v234, v234, v234
	v_max_f32_e32 v235, v235, v235
	v_max_f32_e32 v236, v236, v236
	v_max_f32_e32 v237, v237, v237
	v_max_f32_e32 v238, v238, v238
	v_max_f32_e32 v239, v239, v239
	v_max_f32_e32 v240, v240, v240
	v_max_f32_e32 v241, v241, v241
	v_med3_f32 v226, v226, s62, v95
	v_med3_f32 v227, v227, s62, v95
	v_med3_f32 v228, v228, s62, v95
	v_med3_f32 v229, v229, s62, v95
	v_med3_f32 v230, v230, s62, v95
	v_med3_f32 v231, v231, s62, v95
	v_med3_f32 v232, v232, s62, v95
	v_med3_f32 v233, v233, s62, v95
	v_med3_f32 v234, v234, s62, v95
	v_med3_f32 v235, v235, s62, v95
	v_med3_f32 v236, v236, s62, v95
	v_med3_f32 v237, v237, s62, v95
	v_med3_f32 v238, v238, s62, v95
	v_med3_f32 v239, v239, s62, v95
	v_med3_f32 v240, v240, s62, v95
	v_med3_f32 v241, v241, s62, v95
	v_mov_b32_e32 v242, 0
	v_mov_b32_e32 v243, 0
	v_mov_b32_e32 v244, 0
	v_mov_b32_e32 v245, 0
	v_cvt_pk_fp8_f32 v242, v226, v227
	v_cvt_pk_fp8_f32 v243, v230, v231
	v_cvt_pk_fp8_f32 v244, v234, v235
	v_cvt_pk_fp8_f32 v245, v238, v239
	v_cvt_pk_fp8_f32 v242, v228, v229 op_sel:[0,0,1]
	v_cvt_pk_fp8_f32 v243, v232, v233 op_sel:[0,0,1]
	v_cvt_pk_fp8_f32 v244, v236, v237 op_sel:[0,0,1]
	v_cvt_pk_fp8_f32 v245, v240, v241 op_sel:[0,0,1]
	s_nop 0
	global_store_dwordx4 v78, v[242:245], s[6:7]
	s_waitcnt vmcnt(12)
	v_mul_f32_e32 v144, v34, v144
	v_mul_f32_e32 v145, v34, v145
	v_mul_f32_e32 v146, v34, v146
	v_mul_f32_e32 v147, v34, v147
	ds_write_b128 v209, v[144:147]
	v_mul_f32_e32 v148, v35, v148
	v_mul_f32_e32 v149, v35, v149
	v_mul_f32_e32 v150, v35, v150
	v_mul_f32_e32 v151, v35, v151
	ds_write_b128 v209, v[148:151] offset:1024
	v_mul_f32_e32 v152, v36, v152
	v_mul_f32_e32 v153, v36, v153
	v_mul_f32_e32 v154, v36, v154
	v_mul_f32_e32 v155, v36, v155
	ds_write_b128 v209, v[152:155] offset:2048
	v_mul_f32_e32 v156, v37, v156
	v_mul_f32_e32 v157, v37, v157
	v_mul_f32_e32 v158, v37, v158
	v_mul_f32_e32 v159, v37, v159
	ds_write_b128 v209, v[156:159] offset:3072
	v_mul_f32_e32 v160, v38, v160
	v_mul_f32_e32 v161, v38, v161
	v_mul_f32_e32 v162, v38, v162
	v_mul_f32_e32 v163, v38, v163
	ds_write_b128 v209, v[160:163] offset:4096
	v_mul_f32_e32 v164, v39, v164
	v_mul_f32_e32 v165, v39, v165
	v_mul_f32_e32 v166, v39, v166
	v_mul_f32_e32 v167, v39, v167
	ds_write_b128 v209, v[164:167] offset:5120
	v_mul_f32_e32 v168, v40, v168
	v_mul_f32_e32 v169, v40, v169
	v_mul_f32_e32 v170, v40, v170
	v_mul_f32_e32 v171, v40, v171
	ds_write_b128 v209, v[168:171] offset:6144
	v_mul_f32_e32 v172, v41, v172
	v_mul_f32_e32 v173, v41, v173
	v_mul_f32_e32 v174, v41, v174
	v_mul_f32_e32 v175, v41, v175
	ds_write_b128 v209, v[172:175] offset:7168
	s_waitcnt lgkmcnt(0)
	s_barrier
; #define GAS __attribute__((address_space(1)))
; #define LAS __attribute__((address_space(3)))
; #define LDS_WAIT() asm volatile("s_waitcnt lgkmcnt(0)" ::: "memory")
; __device__ __forceinline__ unsigned pk4_fp8(float a, float b, float c, float d) {
;     a = fminf(fmaxf(a, -448.f), 448.f); b = fminf(fmaxf(b, -448.f), 448.f); c = fminf(fmaxf(c, -448.f), 448.f); d = fminf(fmaxf(d, -448.f), 448.f);
;     int w = __builtin_amdgcn_cvt_pk_fp8_f32(a, b, 0, false); w = __builtin_amdgcn_cvt_pk_fp8_f32(c, d, w, true); return (unsigned)w; }
;     const int pr = item >> 1, kb = 2 * (pr / nblk) + (item & 1), nb = pr % nblk, k0 = 64 * kb, n0 = 32 * nb;
;     const int nr = n0 + (lane & 31); const int sc = MAP == 1 ? src_col_in(nr) : nr;
;     float v[32];
; #pragma unroll
;     for (int i = 0; i < 32; ++i) v[i] = sc >= 0 ? W[(size_t)(k0 + 2 * i + (lane >> 5)) * Nsrc + sc] : 0.f;
; #pragma unroll
;     for (int i = 0; i < 32; ++i) { const int k = k0 + 2 * i + (lane >> 5); float x = v[i] * wscale; if (KS) x *= (k < ksplit ? ksA[k] : ksB[k - ksplit]); scr[(2 * i + (lane >> 5)) * 33 + (lane & 31)] = x; }
;     LDS_WAIT(); asm volatile("" ::: "memory");
;     const int c = lane & 7;
; #pragma unroll
;     for (int j = 0; j < 4; ++j) { const int n = (lane >> 3) + 8 * j; const LAS float* s = scr + (8 * c) * 33 + n;
;         const unsigned long long o = (unsigned long long)pg8::pk4_fp8(s[0 * 33], s[1 * 33], s[2 * 33], s[3 * 33]) | ((unsigned long long)pg8::pk4_fp8(s[4 * 33], s[5 * 33], s[6 * 33], s[7 * 33]) << 32);
;         *(GAS unsigned long long*)(WT + (size_t)(n0 + n) * K + k0 + 8 * c) = o; }
;     LDS_WAIT(); asm volatile("" ::: "memory");
; }
	s_add_u32 s8, s34, 0xc000
	s_addc_u32 s9, s35, 0
	global_load_dwordx4 v[144:147], v74, s[8:9]
	s_add_u32 s8, s8, 0x20000
	s_addc_u32 s9, s9, 0
	global_load_dwordx4 v[148:151], v74, s[8:9]
	s_add_u32 s8, s8, 0x20000
	s_addc_u32 s9, s9, 0
	global_load_dwordx4 v[152:155], v74, s[8:9]
	s_add_u32 s8, s8, 0x20000
	s_addc_u32 s9, s9, 0
	global_load_dwordx4 v[156:159], v74, s[8:9]
	s_add_u32 s8, s8, 0x20000
	s_addc_u32 s9, s9, 0
	global_load_dwordx4 v[160:163], v74, s[8:9]
	s_add_u32 s8, s8, 0x20000
	s_addc_u32 s9, s9, 0
	global_load_dwordx4 v[164:167], v74, s[8:9]
	s_add_u32 s8, s8, 0x20000
	s_addc_u32 s9, s9, 0
	global_load_dwordx4 v[168:171], v74, s[8:9]
	s_add_u32 s8, s8, 0x20000
	s_addc_u32 s9, s9, 0
	global_load_dwordx4 v[172:175], v74, s[8:9]
	s_add_u32 s6, s36, 0x2800000
	s_addc_u32 s7, s37, 0
	ds_read_b32 v226, v211
	ds_read_b32 v227, v211 offset:512
	ds_read_b32 v228, v211 offset:1024
	ds_read_b32 v229, v211 offset:1536
	ds_read_b32 v230, v211 offset:2048
	ds_read_b32 v231, v211 offset:2560
	ds_read_b32 v232, v211 offset:3072
	ds_read_b32 v233, v211 offset:3584
	ds_read_b32 v234, v211 offset:4096
	ds_read_b32 v235, v211 offset:4608
	ds_read_b32 v236, v211 offset:5120
	ds_read_b32 v237, v211 offset:5632
	ds_read_b32 v238, v211 offset:6144
	ds_read_b32 v239, v211 offset:6656
	ds_read_b32 v240, v211 offset:7168
	ds_read_b32 v241, v211 offset:7680
	s_waitcnt lgkmcnt(0)
	v_max_f32_e32 v226, v226, v226
	v_max_f32_e32 v227, v227, v227
	v_max_f32_e32 v228, v228, v228
	v_max_f32_e32 v229, v229, v229
	v_max_f32_e32 v230, v230, v230
	v_max_f32_e32 v231, v231, v231
	v_max_f32_e32 v232, v232, v232
	v_max_f32_e32 v233, v233, v233
	v_max_f32_e32 v234, v234, v234
	v_max_f32_e32 v235, v235, v235
	v_max_f32_e32 v236, v236, v236
	v_max_f32_e32 v237, v237, v237
	v_max_f32_e32 v238, v238, v238
	v_max_f32_e32 v239, v239, v239
	v_max_f32_e32 v240, v240, v240
	v_max_f32_e32 v241, v241, v241
	v_med3_f32 v226, v226, s62, v95
	v_med3_f32 v227, v227, s62, v95
	v_med3_f32 v228, v228, s62, v95
	v_med3_f32 v229, v229, s62, v95
	v_med3_f32 v230, v230, s62, v95
	v_med3_f32 v231, v231, s62, v95
	v_med3_f32 v232, v232, s62, v95
	v_med3_f32 v233, v233, s62, v95
	v_med3_f32 v234, v234, s62, v95
	v_med3_f32 v235, v235, s62, v95
	v_med3_f32 v236, v236, s62, v95
	v_med3_f32 v237, v237, s62, v95
	v_med3_f32 v238, v238, s62, v95
	v_med3_f32 v239, v239, s62, v95
	v_med3_f32 v240, v240, s62, v95
	v_med3_f32 v241, v241, s62, v95
	v_mov_b32_e32 v242, 0
	v_mov_b32_e32 v243, 0
	v_mov_b32_e32 v244, 0
	v_mov_b32_e32 v245, 0
	v_cvt_pk_fp8_f32 v242, v226, v227
	v_cvt_pk_fp8_f32 v243, v230, v231
	v_cvt_pk_fp8_f32 v244, v234, v235
	v_cvt_pk_fp8_f32 v245, v238, v239
	v_cvt_pk_fp8_f32 v242, v228, v229 op_sel:[0,0,1]
	v_cvt_pk_fp8_f32 v243, v232, v233 op_sel:[0,0,1]
	v_cvt_pk_fp8_f32 v244, v236, v237 op_sel:[0,0,1]
	v_cvt_pk_fp8_f32 v245, v240, v241 op_sel:[0,0,1]
	s_nop 0
	global_store_dwordx4 v77, v[242:245], s[6:7]
	ds_read_b32 v226, v213
	ds_read_b32 v227, v213 offset:512
	ds_read_b32 v228, v213 offset:1024
	ds_read_b32 v229, v213 offset:1536
	ds_read_b32 v230, v213 offset:2048
	ds_read_b32 v231, v213 offset:2560
	ds_read_b32 v232, v213 offset:3072
	ds_read_b32 v233, v213 offset:3584
	ds_read_b32 v234, v213 offset:4096
	ds_read_b32 v235, v213 offset:4608
	ds_read_b32 v236, v213 offset:5120
	ds_read_b32 v237, v213 offset:5632
	ds_read_b32 v238, v213 offset:6144
	ds_read_b32 v239, v213 offset:6656
	ds_read_b32 v240, v213 offset:7168
	ds_read_b32 v241, v213 offset:7680
	s_waitcnt lgkmcnt(0)
	v_max_f32_e32 v226, v226, v226
	v_max_f32_e32 v227, v227, v227
	v_max_f32_e32 v228, v228, v228
	v_max_f32_e32 v229, v229, v229
	v_max_f32_e32 v230, v230, v230
	v_max_f32_e32 v231, v231, v231
	v_max_f32_e32 v232, v232, v232
	v_max_f32_e32 v233, v233, v233
	v_max_f32_e32 v234, v234, v234
	v_max_f32_e32 v235, v235, v235
	v_max_f32_e32 v236, v236, v236
	v_max_f32_e32 v237, v237, v237
	v_max_f32_e32 v238, v238, v238
	v_max_f32_e32 v239, v239, v239
	v_max_f32_e32 v240, v240, v240
	v_max_f32_e32 v241, v241, v241
	v_med3_f32 v226, v226, s62, v95
	v_med3_f32 v227, v227, s62, v95
	v_med3_f32 v228, v228, s62, v95
	v_med3_f32 v229, v229, s62, v95
	v_med3_f32 v230, v230, s62, v95
	v_med3_f32 v231, v231, s62, v95
	v_med3_f32 v232, v232, s62, v95
	v_med3_f32 v233, v233, s62, v95
	v_med3_f32 v234, v234, s62, v95
	v_med3_f32 v235, v235, s62, v95
	v_med3_f32 v236, v236, s62, v95
	v_med3_f32 v237, v237, s62, v95
	v_med3_f32 v238, v238, s62, v95
	v_med3_f32 v239, v239, s62, v95
	v_med3_f32 v240, v240, s62, v95
	v_med3_f32 v241, v241, s62, v95
	v_mov_b32_e32 v242, 0
	v_mov_b32_e32 v243, 0
	v_mov_b32_e32 v244, 0
	v_mov_b32_e32 v245, 0
	v_cvt_pk_fp8_f32 v242, v226, v227
	v_cvt_pk_fp8_f32 v243, v230, v231
	v_cvt_pk_fp8_f32 v244, v234, v235
	v_cvt_pk_fp8_f32 v245, v238, v239
	v_cvt_pk_fp8_f32 v242, v228, v229 op_sel:[0,0,1]
	v_cvt_pk_fp8_f32 v243, v232, v233 op_sel:[0,0,1]
	v_cvt_pk_fp8_f32 v244, v236, v237 op_sel:[0,0,1]
	v_cvt_pk_fp8_f32 v245, v240, v241 op_sel:[0,0,1]
	s_nop 0
	global_store_dwordx4 v78, v[242:245], s[6:7]
	s_waitcnt vmcnt(12)
	v_mul_f32_e32 v176, v34, v176
	v_mul_f32_e32 v177, v34, v177
	v_mul_f32_e32 v178, v34, v178
	v_mul_f32_e32 v179, v34, v179
	ds_write_b128 v210, v[176:179]
	v_mul_f32_e32 v180, v35, v180
	v_mul_f32_e32 v181, v35, v181
	v_mul_f32_e32 v182, v35, v182
	v_mul_f32_e32 v183, v35, v183
	ds_write_b128 v210, v[180:183] offset:1024
	v_mul_f32_e32 v184, v36, v184
	v_mul_f32_e32 v185, v36, v185
	v_mul_f32_e32 v186, v36, v186
	v_mul_f32_e32 v187, v36, v187
	ds_write_b128 v210, v[184:187] offset:2048
	v_mul_f32_e32 v188, v37, v188
	v_mul_f32_e32 v189, v37, v189
	v_mul_f32_e32 v190, v37, v190
	v_mul_f32_e32 v191, v37, v191
	ds_write_b128 v210, v[188:191] offset:3072
	v_mul_f32_e32 v192, v38, v192
	v_mul_f32_e32 v193, v38, v193
	v_mul_f32_e32 v194, v38, v194
	v_mul_f32_e32 v195, v38, v195
	ds_write_b128 v210, v[192:195] offset:4096
	v_mul_f32_e32 v196, v39, v196
	v_mul_f32_e32 v197, v39, v197
	v_mul_f32_e32 v198, v39, v198
	v_mul_f32_e32 v199, v39, v199
	ds_write_b128 v210, v[196:199] offset:5120
	v_mul_f32_e32 v200, v40, v200
	v_mul_f32_e32 v201, v40, v201
	v_mul_f32_e32 v202, v40, v202
	v_mul_f32_e32 v203, v40, v203
	ds_write_b128 v210, v[200:203] offset:6144
	v_mul_f32_e32 v204, v41, v204
	v_mul_f32_e32 v205, v41, v205
	v_mul_f32_e32 v206, v41, v206
	v_mul_f32_e32 v207, v41, v207
	ds_write_b128 v210, v[204:207] offset:7168
	s_waitcnt lgkmcnt(0)
	s_barrier
; #define GAS __attribute__((address_space(1)))
; #define LAS __attribute__((address_space(3)))
; #define LDS_WAIT() asm volatile("s_waitcnt lgkmcnt(0)" ::: "memory")
;     const int pr = item >> 1, kb = 2 * (pr / nblk) + (item & 1), nb = pr % nblk, k0 = 64 * kb, n0 = 32 * nb;
;     const int nr = n0 + (lane & 31); const int sc = MAP == 1 ? src_col_in(nr) : nr;
;     float v[32];
; #pragma unroll
;     for (int i = 0; i < 32; ++i) v[i] = sc >= 0 ? W[(size_t)(k0 + 2 * i + (lane >> 5)) * Nsrc + sc] : 0.f;
; #pragma unroll
;     for (int i = 0; i < 32; ++i) { const int k = k0 + 2 * i + (lane >> 5); float x = v[i] * wscale; if (KS) x *= (k < ksplit ? ksA[k] : ksB[k - ksplit]); scr[(2 * i + (lane >> 5)) * 33 + (lane & 31)] = x; }
;     LDS_WAIT(); asm volatile("" ::: "memory");
;     const int c = lane & 7;
; #pragma unroll
;     for (int j = 0; j < 4; ++j) { const int n = (lane >> 3) + 8 * j; const LAS float* s = scr + (8 * c) * 33 + n;
;         const unsigned long long o = (unsigned long long)pg8::pk4_fp8(s[0 * 33], s[1 * 33], s[2 * 33], s[3 * 33]) | ((unsigned long long)pg8::pk4_fp8(s[4 * 33], s[5 * 33], s[6 * 33], s[7 * 33]) << 32);
;         *(GAS unsigned long long*)(WT + (size_t)(n0 + n) * K + k0 + 8 * c) = o; }
;     LDS_WAIT(); asm volatile("" ::: "memory");
	s_add_u32 s8, s34, 0xd000
	s_addc_u32 s9, s35, 0
	global_load_dwordx4 v[176:179], v74, s[8:9]
	s_add_u32 s8, s8, 0x20000
	s_addc_u32 s9, s9, 0
	global_load_dwordx4 v[180:183], v74, s[8:9]
	s_add_u32 s8, s8, 0x20000
	s_addc_u32 s9, s9, 0
	global_load_dwordx4 v[184:187], v74, s[8:9]
	s_add_u32 s8, s8, 0x20000
	s_addc_u32 s9, s9, 0
	global_load_dwordx4 v[188:191], v74, s[8:9]
	s_add_u32 s8, s8, 0x20000
	s_addc_u32 s9, s9, 0
	global_load_dwordx4 v[192:195], v74, s[8:9]
	s_add_u32 s8, s8, 0x20000
	s_addc_u32 s9, s9, 0
	global_load_dwordx4 v[196:199], v74, s[8:9]
	s_add_u32 s8, s8, 0x20000
	s_addc_u32 s9, s9, 0
	global_load_dwordx4 v[200:203], v74, s[8:9]
	s_add_u32 s8, s8, 0x20000
	s_addc_u32 s9, s9, 0
	global_load_dwordx4 v[204:207], v74, s[8:9]
	s_add_u32 s6, s36, 0x2c00000
	s_addc_u32 s7, s37, 0
	ds_read_b32 v226, v212
	ds_read_b32 v227, v212 offset:512
	ds_read_b32 v228, v212 offset:1024
	ds_read_b32 v229, v212 offset:1536
	ds_read_b32 v230, v212 offset:2048
	ds_read_b32 v231, v212 offset:2560
	ds_read_b32 v232, v212 offset:3072
	ds_read_b32 v233, v212 offset:3584
	ds_read_b32 v234, v212 offset:4096
	ds_read_b32 v235, v212 offset:4608
	ds_read_b32 v236, v212 offset:5120
	ds_read_b32 v237, v212 offset:5632
	ds_read_b32 v238, v212 offset:6144
	ds_read_b32 v239, v212 offset:6656
	ds_read_b32 v240, v212 offset:7168
	ds_read_b32 v241, v212 offset:7680
	s_waitcnt lgkmcnt(0)
	v_max_f32_e32 v226, v226, v226
	v_max_f32_e32 v227, v227, v227
	v_max_f32_e32 v228, v228, v228
	v_max_f32_e32 v229, v229, v229
	v_max_f32_e32 v230, v230, v230
	v_max_f32_e32 v231, v231, v231
	v_max_f32_e32 v232, v232, v232
	v_max_f32_e32 v233, v233, v233
	v_max_f32_e32 v234, v234, v234
	v_max_f32_e32 v235, v235, v235
	v_max_f32_e32 v236, v236, v236
	v_max_f32_e32 v237, v237, v237
	v_max_f32_e32 v238, v238, v238
	v_max_f32_e32 v239, v239, v239
	v_max_f32_e32 v240, v240, v240
	v_max_f32_e32 v241, v241, v241
	v_med3_f32 v226, v226, s62, v95
	v_med3_f32 v227, v227, s62, v95
	v_med3_f32 v228, v228, s62, v95
	v_med3_f32 v229, v229, s62, v95
	v_med3_f32 v230, v230, s62, v95
	v_med3_f32 v231, v231, s62, v95
	v_med3_f32 v232, v232, s62, v95
	v_med3_f32 v233, v233, s62, v95
	v_med3_f32 v234, v234, s62, v95
	v_med3_f32 v235, v235, s62, v95
	v_med3_f32 v236, v236, s62, v95
	v_med3_f32 v237, v237, s62, v95
	v_med3_f32 v238, v238, s62, v95
	v_med3_f32 v239, v239, s62, v95
	v_med3_f32 v240, v240, s62, v95
	v_med3_f32 v241, v241, s62, v95
	v_mov_b32_e32 v242, 0
	v_mov_b32_e32 v243, 0
	v_mov_b32_e32 v244, 0
	v_mov_b32_e32 v245, 0
	v_cvt_pk_fp8_f32 v242, v226, v227
	v_cvt_pk_fp8_f32 v243, v230, v231
	v_cvt_pk_fp8_f32 v244, v234, v235
	v_cvt_pk_fp8_f32 v245, v238, v239
	v_cvt_pk_fp8_f32 v242, v228, v229 op_sel:[0,0,1]
	v_cvt_pk_fp8_f32 v243, v232, v233 op_sel:[0,0,1]
	v_cvt_pk_fp8_f32 v244, v236, v237 op_sel:[0,0,1]
	v_cvt_pk_fp8_f32 v245, v240, v241 op_sel:[0,0,1]
	s_nop 0
	global_store_dwordx4 v77, v[242:245], s[6:7]
	ds_read_b32 v226, v214
	ds_read_b32 v227, v214 offset:512
	ds_read_b32 v228, v214 offset:1024
	ds_read_b32 v229, v214 offset:1536
	ds_read_b32 v230, v214 offset:2048
	ds_read_b32 v231, v214 offset:2560
	ds_read_b32 v232, v214 offset:3072
	ds_read_b32 v233, v214 offset:3584
	ds_read_b32 v234, v214 offset:4096
	ds_read_b32 v235, v214 offset:4608
	ds_read_b32 v236, v214 offset:5120
	ds_read_b32 v237, v214 offset:5632
	ds_read_b32 v238, v214 offset:6144
	ds_read_b32 v239, v214 offset:6656
	ds_read_b32 v240, v214 offset:7168
	ds_read_b32 v241, v214 offset:7680
	s_waitcnt lgkmcnt(0)
	v_max_f32_e32 v226, v226, v226
	v_max_f32_e32 v227, v227, v227
	v_max_f32_e32 v228, v228, v228
	v_max_f32_e32 v229, v229, v229
	v_max_f32_e32 v230, v230, v230
	v_max_f32_e32 v231, v231, v231
	v_max_f32_e32 v232, v232, v232
	v_max_f32_e32 v233, v233, v233
	v_max_f32_e32 v234, v234, v234
	v_max_f32_e32 v235, v235, v235
	v_max_f32_e32 v236, v236, v236
	v_max_f32_e32 v237, v237, v237
	v_max_f32_e32 v238, v238, v238
	v_max_f32_e32 v239, v239, v239
	v_max_f32_e32 v240, v240, v240
	v_max_f32_e32 v241, v241, v241
	v_med3_f32 v226, v226, s62, v95
	v_med3_f32 v227, v227, s62, v95
	v_med3_f32 v228, v228, s62, v95
	v_med3_f32 v229, v229, s62, v95
	v_med3_f32 v230, v230, s62, v95
	v_med3_f32 v231, v231, s62, v95
	v_med3_f32 v232, v232, s62, v95
	v_med3_f32 v233, v233, s62, v95
	v_med3_f32 v234, v234, s62, v95
	v_med3_f32 v235, v235, s62, v95
	v_med3_f32 v236, v236, s62, v95
	v_med3_f32 v237, v237, s62, v95
	v_med3_f32 v238, v238, s62, v95
	v_med3_f32 v239, v239, s62, v95
	v_med3_f32 v240, v240, s62, v95
	v_med3_f32 v241, v241, s62, v95
	v_mov_b32_e32 v242, 0
	v_mov_b32_e32 v243, 0
	v_mov_b32_e32 v244, 0
	v_mov_b32_e32 v245, 0
	v_cvt_pk_fp8_f32 v242, v226, v227
	v_cvt_pk_fp8_f32 v243, v230, v231
	v_cvt_pk_fp8_f32 v244, v234, v235
	v_cvt_pk_fp8_f32 v245, v238, v239
	v_cvt_pk_fp8_f32 v242, v228, v229 op_sel:[0,0,1]
	v_cvt_pk_fp8_f32 v243, v232, v233 op_sel:[0,0,1]
	v_cvt_pk_fp8_f32 v244, v236, v237 op_sel:[0,0,1]
	v_cvt_pk_fp8_f32 v245, v240, v241 op_sel:[0,0,1]
	s_nop 0
	global_store_dwordx4 v78, v[242:245], s[6:7]
	s_waitcnt vmcnt(12)
	v_mul_f32_e32 v144, v34, v144
	v_mul_f32_e32 v145, v34, v145
	v_mul_f32_e32 v146, v34, v146
	v_mul_f32_e32 v147, v34, v147
	ds_write_b128 v209, v[144:147]
	v_mul_f32_e32 v148, v35, v148
	v_mul_f32_e32 v149, v35, v149
	v_mul_f32_e32 v150, v35, v150
	v_mul_f32_e32 v151, v35, v151
	ds_write_b128 v209, v[148:151] offset:1024
	v_mul_f32_e32 v152, v36, v152
	v_mul_f32_e32 v153, v36, v153
	v_mul_f32_e32 v154, v36, v154
	v_mul_f32_e32 v155, v36, v155
	ds_write_b128 v209, v[152:155] offset:2048
	v_mul_f32_e32 v156, v37, v156
	v_mul_f32_e32 v157, v37, v157
	v_mul_f32_e32 v158, v37, v158
	v_mul_f32_e32 v159, v37, v159
	ds_write_b128 v209, v[156:159] offset:3072
	v_mul_f32_e32 v160, v38, v160
	v_mul_f32_e32 v161, v38, v161
	v_mul_f32_e32 v162, v38, v162
	v_mul_f32_e32 v163, v38, v163
	ds_write_b128 v209, v[160:163] offset:4096
	v_mul_f32_e32 v164, v39, v164
	v_mul_f32_e32 v165, v39, v165
	v_mul_f32_e32 v166, v39, v166
	v_mul_f32_e32 v167, v39, v167
	ds_write_b128 v209, v[164:167] offset:5120
	v_mul_f32_e32 v168, v40, v168
	v_mul_f32_e32 v169, v40, v169
	v_mul_f32_e32 v170, v40, v170
	v_mul_f32_e32 v171, v40, v171
	ds_write_b128 v209, v[168:171] offset:6144
	v_mul_f32_e32 v172, v41, v172
	v_mul_f32_e32 v173, v41, v173
	v_mul_f32_e32 v174, v41, v174
	v_mul_f32_e32 v175, v41, v175
	ds_write_b128 v209, v[172:175] offset:7168
	s_waitcnt lgkmcnt(0)
	s_barrier
; #define GAS __attribute__((address_space(1)))
; #define LAS __attribute__((address_space(3)))
; #define LDS_WAIT() asm volatile("s_waitcnt lgkmcnt(0)" ::: "memory")
;     const int pr = item >> 1, kb = 2 * (pr / nblk) + (item & 1), nb = pr % nblk, k0 = 64 * kb, n0 = 32 * nb;
;     const int nr = n0 + (lane & 31); const int sc = MAP == 1 ? src_col_in(nr) : nr;
;     float v[32];
; #pragma unroll
;     for (int i = 0; i < 32; ++i) v[i] = sc >= 0 ? W[(size_t)(k0 + 2 * i + (lane >> 5)) * Nsrc + sc] : 0.f;
; #pragma unroll
;     for (int i = 0; i < 32; ++i) { const int k = k0 + 2 * i + (lane >> 5); float x = v[i] * wscale; if (KS) x *= (k < ksplit ? ksA[k] : ksB[k - ksplit]); scr[(2 * i + (lane >> 5)) * 33 + (lane & 31)] = x; }
;     LDS_WAIT(); asm volatile("" ::: "memory");
;     const int c = lane & 7;
; #pragma unroll
;     for (int j = 0; j < 4; ++j) { const int n = (lane >> 3) + 8 * j; const LAS float* s = scr + (8 * c) * 33 + n;
;         const unsigned long long o = (unsigned long long)pg8::pk4_fp8(s[0 * 33], s[1 * 33], s[2 * 33], s[3 * 33]) | ((unsigned long long)pg8::pk4_fp8(s[4 * 33], s[5 * 33], s[6 * 33], s[7 * 33]) << 32);
;         *(GAS unsigned long long*)(WT + (size_t)(n0 + n) * K + k0 + 8 * c) = o; }
;     LDS_WAIT(); asm volatile("" ::: "memory");
	s_add_u32 s8, s34, 0xe000
	s_addc_u32 s9, s35, 0
	global_load_dwordx4 v[144:147], v74, s[8:9]
	s_add_u32 s8, s8, 0x20000
	s_addc_u32 s9, s9, 0
	global_load_dwordx4 v[148:151], v74, s[8:9]
	s_add_u32 s8, s8, 0x20000
	s_addc_u32 s9, s9, 0
	global_load_dwordx4 v[152:155], v74, s[8:9]
	s_add_u32 s8, s8, 0x20000
	s_addc_u32 s9, s9, 0
	global_load_dwordx4 v[156:159], v74, s[8:9]
	s_add_u32 s8, s8, 0x20000
	s_addc_u32 s9, s9, 0
	global_load_dwordx4 v[160:163], v74, s[8:9]
	s_add_u32 s8, s8, 0x20000
	s_addc_u32 s9, s9, 0
	global_load_dwordx4 v[164:167], v74, s[8:9]
	s_add_u32 s8, s8, 0x20000
	s_addc_u32 s9, s9, 0
	global_load_dwordx4 v[168:171], v74, s[8:9]
	s_add_u32 s8, s8, 0x20000
	s_addc_u32 s9, s9, 0
	global_load_dwordx4 v[172:175], v74, s[8:9]
	s_add_u32 s6, s36, 0x3000000
	s_addc_u32 s7, s37, 0
	ds_read_b32 v226, v211
	ds_read_b32 v227, v211 offset:512
	ds_read_b32 v228, v211 offset:1024
	ds_read_b32 v229, v211 offset:1536
	ds_read_b32 v230, v211 offset:2048
	ds_read_b32 v231, v211 offset:2560
	ds_read_b32 v232, v211 offset:3072
	ds_read_b32 v233, v211 offset:3584
	ds_read_b32 v234, v211 offset:4096
	ds_read_b32 v235, v211 offset:4608
	ds_read_b32 v236, v211 offset:5120
	ds_read_b32 v237, v211 offset:5632
	ds_read_b32 v238, v211 offset:6144
	ds_read_b32 v239, v211 offset:6656
	ds_read_b32 v240, v211 offset:7168
	ds_read_b32 v241, v211 offset:7680
	s_waitcnt lgkmcnt(0)
	v_max_f32_e32 v226, v226, v226
	v_max_f32_e32 v227, v227, v227
	v_max_f32_e32 v228, v228, v228
	v_max_f32_e32 v229, v229, v229
	v_max_f32_e32 v230, v230, v230
	v_max_f32_e32 v231, v231, v231
	v_max_f32_e32 v232, v232, v232
	v_max_f32_e32 v233, v233, v233
	v_max_f32_e32 v234, v234, v234
	v_max_f32_e32 v235, v235, v235
	v_max_f32_e32 v236, v236, v236
	v_max_f32_e32 v237, v237, v237
	v_max_f32_e32 v238, v238, v238
	v_max_f32_e32 v239, v239, v239
	v_max_f32_e32 v240, v240, v240
	v_max_f32_e32 v241, v241, v241
	v_med3_f32 v226, v226, s62, v95
	v_med3_f32 v227, v227, s62, v95
	v_med3_f32 v228, v228, s62, v95
	v_med3_f32 v229, v229, s62, v95
	v_med3_f32 v230, v230, s62, v95
	v_med3_f32 v231, v231, s62, v95
	v_med3_f32 v232, v232, s62, v95
	v_med3_f32 v233, v233, s62, v95
	v_med3_f32 v234, v234, s62, v95
	v_med3_f32 v235, v235, s62, v95
	v_med3_f32 v236, v236, s62, v95
	v_med3_f32 v237, v237, s62, v95
	v_med3_f32 v238, v238, s62, v95
	v_med3_f32 v239, v239, s62, v95
	v_med3_f32 v240, v240, s62, v95
	v_med3_f32 v241, v241, s62, v95
	v_mov_b32_e32 v242, 0
	v_mov_b32_e32 v243, 0
	v_mov_b32_e32 v244, 0
	v_mov_b32_e32 v245, 0
	v_cvt_pk_fp8_f32 v242, v226, v227
	v_cvt_pk_fp8_f32 v243, v230, v231
	v_cvt_pk_fp8_f32 v244, v234, v235
	v_cvt_pk_fp8_f32 v245, v238, v239
	v_cvt_pk_fp8_f32 v242, v228, v229 op_sel:[0,0,1]
	v_cvt_pk_fp8_f32 v243, v232, v233 op_sel:[0,0,1]
	v_cvt_pk_fp8_f32 v244, v236, v237 op_sel:[0,0,1]
	v_cvt_pk_fp8_f32 v245, v240, v241 op_sel:[0,0,1]
	s_nop 0
	global_store_dwordx4 v77, v[242:245], s[6:7]
	ds_read_b32 v226, v213
	ds_read_b32 v227, v213 offset:512
	ds_read_b32 v228, v213 offset:1024
	ds_read_b32 v229, v213 offset:1536
	ds_read_b32 v230, v213 offset:2048
	ds_read_b32 v231, v213 offset:2560
	ds_read_b32 v232, v213 offset:3072
	ds_read_b32 v233, v213 offset:3584
	ds_read_b32 v234, v213 offset:4096
	ds_read_b32 v235, v213 offset:4608
	ds_read_b32 v236, v213 offset:5120
	ds_read_b32 v237, v213 offset:5632
	ds_read_b32 v238, v213 offset:6144
	ds_read_b32 v239, v213 offset:6656
	ds_read_b32 v240, v213 offset:7168
	ds_read_b32 v241, v213 offset:7680
	s_waitcnt lgkmcnt(0)
	v_max_f32_e32 v226, v226, v226
	v_max_f32_e32 v227, v227, v227
	v_max_f32_e32 v228, v228, v228
	v_max_f32_e32 v229, v229, v229
	v_max_f32_e32 v230, v230, v230
	v_max_f32_e32 v231, v231, v231
	v_max_f32_e32 v232, v232, v232
	v_max_f32_e32 v233, v233, v233
	v_max_f32_e32 v234, v234, v234
	v_max_f32_e32 v235, v235, v235
	v_max_f32_e32 v236, v236, v236
	v_max_f32_e32 v237, v237, v237
	v_max_f32_e32 v238, v238, v238
	v_max_f32_e32 v239, v239, v239
	v_max_f32_e32 v240, v240, v240
	v_max_f32_e32 v241, v241, v241
	v_med3_f32 v226, v226, s62, v95
	v_med3_f32 v227, v227, s62, v95
	v_med3_f32 v228, v228, s62, v95
	v_med3_f32 v229, v229, s62, v95
	v_med3_f32 v230, v230, s62, v95
	v_med3_f32 v231, v231, s62, v95
	v_med3_f32 v232, v232, s62, v95
	v_med3_f32 v233, v233, s62, v95
	v_med3_f32 v234, v234, s62, v95
	v_med3_f32 v235, v235, s62, v95
	v_med3_f32 v236, v236, s62, v95
	v_med3_f32 v237, v237, s62, v95
	v_med3_f32 v238, v238, s62, v95
	v_med3_f32 v239, v239, s62, v95
	v_med3_f32 v240, v240, s62, v95
	v_med3_f32 v241, v241, s62, v95
	v_mov_b32_e32 v242, 0
	v_mov_b32_e32 v243, 0
	v_mov_b32_e32 v244, 0
	v_mov_b32_e32 v245, 0
	v_cvt_pk_fp8_f32 v242, v226, v227
	v_cvt_pk_fp8_f32 v243, v230, v231
	v_cvt_pk_fp8_f32 v244, v234, v235
	v_cvt_pk_fp8_f32 v245, v238, v239
	v_cvt_pk_fp8_f32 v242, v228, v229 op_sel:[0,0,1]
	v_cvt_pk_fp8_f32 v243, v232, v233 op_sel:[0,0,1]
	v_cvt_pk_fp8_f32 v244, v236, v237 op_sel:[0,0,1]
	v_cvt_pk_fp8_f32 v245, v240, v241 op_sel:[0,0,1]
	s_nop 0
	global_store_dwordx4 v78, v[242:245], s[6:7]
	s_waitcnt vmcnt(12)
	v_mul_f32_e32 v176, v34, v176
	v_mul_f32_e32 v177, v34, v177
	v_mul_f32_e32 v178, v34, v178
	v_mul_f32_e32 v179, v34, v179
	ds_write_b128 v210, v[176:179]
	v_mul_f32_e32 v180, v35, v180
	v_mul_f32_e32 v181, v35, v181
	v_mul_f32_e32 v182, v35, v182
	v_mul_f32_e32 v183, v35, v183
	ds_write_b128 v210, v[180:183] offset:1024
	v_mul_f32_e32 v184, v36, v184
	v_mul_f32_e32 v185, v36, v185
	v_mul_f32_e32 v186, v36, v186
	v_mul_f32_e32 v187, v36, v187
	ds_write_b128 v210, v[184:187] offset:2048
	v_mul_f32_e32 v188, v37, v188
	v_mul_f32_e32 v189, v37, v189
	v_mul_f32_e32 v190, v37, v190
	v_mul_f32_e32 v191, v37, v191
	ds_write_b128 v210, v[188:191] offset:3072
	v_mul_f32_e32 v192, v38, v192
	v_mul_f32_e32 v193, v38, v193
	v_mul_f32_e32 v194, v38, v194
	v_mul_f32_e32 v195, v38, v195
	ds_write_b128 v210, v[192:195] offset:4096
	v_mul_f32_e32 v196, v39, v196
	v_mul_f32_e32 v197, v39, v197
	v_mul_f32_e32 v198, v39, v198
	v_mul_f32_e32 v199, v39, v199
	ds_write_b128 v210, v[196:199] offset:5120
	v_mul_f32_e32 v200, v40, v200
	v_mul_f32_e32 v201, v40, v201
	v_mul_f32_e32 v202, v40, v202
	v_mul_f32_e32 v203, v40, v203
	ds_write_b128 v210, v[200:203] offset:6144
	v_mul_f32_e32 v204, v41, v204
	v_mul_f32_e32 v205, v41, v205
	v_mul_f32_e32 v206, v41, v206
	v_mul_f32_e32 v207, v41, v207
	ds_write_b128 v210, v[204:207] offset:7168
	s_waitcnt lgkmcnt(0)
	s_barrier
; #define GAS __attribute__((address_space(1)))
; #define LAS __attribute__((address_space(3)))
; #define LDS_WAIT() asm volatile("s_waitcnt lgkmcnt(0)" ::: "memory")
;     const int pr = item >> 1, kb = 2 * (pr / nblk) + (item & 1), nb = pr % nblk, k0 = 64 * kb, n0 = 32 * nb;
;     const int nr = n0 + (lane & 31); const int sc = MAP == 1 ? src_col_in(nr) : nr;
;     float v[32];
; #pragma unroll
;     for (int i = 0; i < 32; ++i) v[i] = sc >= 0 ? W[(size_t)(k0 + 2 * i + (lane >> 5)) * Nsrc + sc] : 0.f;
; #pragma unroll
;     for (int i = 0; i < 32; ++i) { const int k = k0 + 2 * i + (lane >> 5); float x = v[i] * wscale; if (KS) x *= (k < ksplit ? ksA[k] : ksB[k - ksplit]); scr[(2 * i + (lane >> 5)) * 33 + (lane & 31)] = x; }
;     LDS_WAIT(); asm volatile("" ::: "memory");
;     const int c = lane & 7;
; #pragma unroll
;     for (int j = 0; j < 4; ++j) { const int n = (lane >> 3) + 8 * j; const LAS float* s = scr + (8 * c) * 33 + n;
;         const unsigned long long o = (unsigned long long)pg8::pk4_fp8(s[0 * 33], s[1 * 33], s[2 * 33], s[3 * 33]) | ((unsigned long long)pg8::pk4_fp8(s[4 * 33], s[5 * 33], s[6 * 33], s[7 * 33]) << 32);
;         *(GAS unsigned long long*)(WT + (size_t)(n0 + n) * K + k0 + 8 * c) = o; }
;     LDS_WAIT(); asm volatile("" ::: "memory");
	s_add_u32 s8, s34, 0xf000
	s_addc_u32 s9, s35, 0
	global_load_dwordx4 v[176:179], v74, s[8:9]
	s_add_u32 s8, s8, 0x20000
	s_addc_u32 s9, s9, 0
	global_load_dwordx4 v[180:183], v74, s[8:9]
	s_add_u32 s8, s8, 0x20000
	s_addc_u32 s9, s9, 0
	global_load_dwordx4 v[184:187], v74, s[8:9]
	s_add_u32 s8, s8, 0x20000
	s_addc_u32 s9, s9, 0
	global_load_dwordx4 v[188:191], v74, s[8:9]
	s_add_u32 s8, s8, 0x20000
	s_addc_u32 s9, s9, 0
	global_load_dwordx4 v[192:195], v74, s[8:9]
	s_add_u32 s8, s8, 0x20000
	s_addc_u32 s9, s9, 0
	global_load_dwordx4 v[196:199], v74, s[8:9]
	s_add_u32 s8, s8, 0x20000
	s_addc_u32 s9, s9, 0
	global_load_dwordx4 v[200:203], v74, s[8:9]
	s_add_u32 s8, s8, 0x20000
	s_addc_u32 s9, s9, 0
	global_load_dwordx4 v[204:207], v74, s[8:9]
	s_add_u32 s6, s36, 0x3400000
	s_addc_u32 s7, s37, 0
	ds_read_b32 v226, v212
	ds_read_b32 v227, v212 offset:512
	ds_read_b32 v228, v212 offset:1024
	ds_read_b32 v229, v212 offset:1536
	ds_read_b32 v230, v212 offset:2048
	ds_read_b32 v231, v212 offset:2560
	ds_read_b32 v232, v212 offset:3072
	ds_read_b32 v233, v212 offset:3584
	ds_read_b32 v234, v212 offset:4096
	ds_read_b32 v235, v212 offset:4608
	ds_read_b32 v236, v212 offset:5120
	ds_read_b32 v237, v212 offset:5632
	ds_read_b32 v238, v212 offset:6144
	ds_read_b32 v239, v212 offset:6656
	ds_read_b32 v240, v212 offset:7168
	ds_read_b32 v241, v212 offset:7680
	s_waitcnt lgkmcnt(0)
	v_max_f32_e32 v226, v226, v226
	v_max_f32_e32 v227, v227, v227
	v_max_f32_e32 v228, v228, v228
	v_max_f32_e32 v229, v229, v229
	v_max_f32_e32 v230, v230, v230
	v_max_f32_e32 v231, v231, v231
	v_max_f32_e32 v232, v232, v232
	v_max_f32_e32 v233, v233, v233
	v_max_f32_e32 v234, v234, v234
	v_max_f32_e32 v235, v235, v235
	v_max_f32_e32 v236, v236, v236
	v_max_f32_e32 v237, v237, v237
	v_max_f32_e32 v238, v238, v238
	v_max_f32_e32 v239, v239, v239
	v_max_f32_e32 v240, v240, v240
	v_max_f32_e32 v241, v241, v241
	v_med3_f32 v226, v226, s62, v95
	v_med3_f32 v227, v227, s62, v95
	v_med3_f32 v228, v228, s62, v95
	v_med3_f32 v229, v229, s62, v95
	v_med3_f32 v230, v230, s62, v95
	v_med3_f32 v231, v231, s62, v95
	v_med3_f32 v232, v232, s62, v95
	v_med3_f32 v233, v233, s62, v95
	v_med3_f32 v234, v234, s62, v95
	v_med3_f32 v235, v235, s62, v95
	v_med3_f32 v236, v236, s62, v95
	v_med3_f32 v237, v237, s62, v95
	v_med3_f32 v238, v238, s62, v95
	v_med3_f32 v239, v239, s62, v95
	v_med3_f32 v240, v240, s62, v95
	v_med3_f32 v241, v241, s62, v95
	v_mov_b32_e32 v242, 0
	v_mov_b32_e32 v243, 0
	v_mov_b32_e32 v244, 0
	v_mov_b32_e32 v245, 0
	v_cvt_pk_fp8_f32 v242, v226, v227
	v_cvt_pk_fp8_f32 v243, v230, v231
	v_cvt_pk_fp8_f32 v244, v234, v235
	v_cvt_pk_fp8_f32 v245, v238, v239
	v_cvt_pk_fp8_f32 v242, v228, v229 op_sel:[0,0,1]
	v_cvt_pk_fp8_f32 v243, v232, v233 op_sel:[0,0,1]
	v_cvt_pk_fp8_f32 v244, v236, v237 op_sel:[0,0,1]
	v_cvt_pk_fp8_f32 v245, v240, v241 op_sel:[0,0,1]
	s_nop 0
	global_store_dwordx4 v77, v[242:245], s[6:7]
	ds_read_b32 v226, v214
	ds_read_b32 v227, v214 offset:512
	ds_read_b32 v228, v214 offset:1024
	ds_read_b32 v229, v214 offset:1536
	ds_read_b32 v230, v214 offset:2048
	ds_read_b32 v231, v214 offset:2560
	ds_read_b32 v232, v214 offset:3072
	ds_read_b32 v233, v214 offset:3584
	ds_read_b32 v234, v214 offset:4096
	ds_read_b32 v235, v214 offset:4608
	ds_read_b32 v236, v214 offset:5120
	ds_read_b32 v237, v214 offset:5632
	ds_read_b32 v238, v214 offset:6144
	ds_read_b32 v239, v214 offset:6656
	ds_read_b32 v240, v214 offset:7168
	ds_read_b32 v241, v214 offset:7680
	s_waitcnt lgkmcnt(0)
	v_max_f32_e32 v226, v226, v226
	v_max_f32_e32 v227, v227, v227
	v_max_f32_e32 v228, v228, v228
	v_max_f32_e32 v229, v229, v229
	v_max_f32_e32 v230, v230, v230
	v_max_f32_e32 v231, v231, v231
	v_max_f32_e32 v232, v232, v232
	v_max_f32_e32 v233, v233, v233
	v_max_f32_e32 v234, v234, v234
	v_max_f32_e32 v235, v235, v235
	v_max_f32_e32 v236, v236, v236
	v_max_f32_e32 v237, v237, v237
	v_max_f32_e32 v238, v238, v238
	v_max_f32_e32 v239, v239, v239
	v_max_f32_e32 v240, v240, v240
	v_max_f32_e32 v241, v241, v241
	v_med3_f32 v226, v226, s62, v95
	v_med3_f32 v227, v227, s62, v95
	v_med3_f32 v228, v228, s62, v95
	v_med3_f32 v229, v229, s62, v95
	v_med3_f32 v230, v230, s62, v95
	v_med3_f32 v231, v231, s62, v95
	v_med3_f32 v232, v232, s62, v95
	v_med3_f32 v233, v233, s62, v95
	v_med3_f32 v234, v234, s62, v95
	v_med3_f32 v235, v235, s62, v95
	v_med3_f32 v236, v236, s62, v95
	v_med3_f32 v237, v237, s62, v95
	v_med3_f32 v238, v238, s62, v95
	v_med3_f32 v239, v239, s62, v95
	v_med3_f32 v240, v240, s62, v95
	v_med3_f32 v241, v241, s62, v95
	v_mov_b32_e32 v242, 0
	v_mov_b32_e32 v243, 0
	v_mov_b32_e32 v244, 0
	v_mov_b32_e32 v245, 0
	v_cvt_pk_fp8_f32 v242, v226, v227
	v_cvt_pk_fp8_f32 v243, v230, v231
	v_cvt_pk_fp8_f32 v244, v234, v235
	v_cvt_pk_fp8_f32 v245, v238, v239
	v_cvt_pk_fp8_f32 v242, v228, v229 op_sel:[0,0,1]
	v_cvt_pk_fp8_f32 v243, v232, v233 op_sel:[0,0,1]
	v_cvt_pk_fp8_f32 v244, v236, v237 op_sel:[0,0,1]
	v_cvt_pk_fp8_f32 v245, v240, v241 op_sel:[0,0,1]
	s_nop 0
	global_store_dwordx4 v78, v[242:245], s[6:7]
	s_waitcnt vmcnt(12)
	v_mul_f32_e32 v144, v34, v144
	v_mul_f32_e32 v145, v34, v145
	v_mul_f32_e32 v146, v34, v146
	v_mul_f32_e32 v147, v34, v147
	ds_write_b128 v209, v[144:147]
	v_mul_f32_e32 v148, v35, v148
	v_mul_f32_e32 v149, v35, v149
	v_mul_f32_e32 v150, v35, v150
	v_mul_f32_e32 v151, v35, v151
	ds_write_b128 v209, v[148:151] offset:1024
	v_mul_f32_e32 v152, v36, v152
	v_mul_f32_e32 v153, v36, v153
	v_mul_f32_e32 v154, v36, v154
	v_mul_f32_e32 v155, v36, v155
	ds_write_b128 v209, v[152:155] offset:2048
	v_mul_f32_e32 v156, v37, v156
	v_mul_f32_e32 v157, v37, v157
	v_mul_f32_e32 v158, v37, v158
	v_mul_f32_e32 v159, v37, v159
	ds_write_b128 v209, v[156:159] offset:3072
	v_mul_f32_e32 v160, v38, v160
	v_mul_f32_e32 v161, v38, v161
	v_mul_f32_e32 v162, v38, v162
	v_mul_f32_e32 v163, v38, v163
	ds_write_b128 v209, v[160:163] offset:4096
	v_mul_f32_e32 v164, v39, v164
	v_mul_f32_e32 v165, v39, v165
	v_mul_f32_e32 v166, v39, v166
	v_mul_f32_e32 v167, v39, v167
	ds_write_b128 v209, v[164:167] offset:5120
	v_mul_f32_e32 v168, v40, v168
	v_mul_f32_e32 v169, v40, v169
	v_mul_f32_e32 v170, v40, v170
	v_mul_f32_e32 v171, v40, v171
	ds_write_b128 v209, v[168:171] offset:6144
	v_mul_f32_e32 v172, v41, v172
	v_mul_f32_e32 v173, v41, v173
	v_mul_f32_e32 v174, v41, v174
	v_mul_f32_e32 v175, v41, v175
	ds_write_b128 v209, v[172:175] offset:7168
	s_waitcnt lgkmcnt(0)
	s_barrier
; #define GAS __attribute__((address_space(1)))
; #define LAS __attribute__((address_space(3)))
; #define LDS_WAIT() asm volatile("s_waitcnt lgkmcnt(0)" ::: "memory")
;     const int pr = item >> 1, kb = 2 * (pr / nblk) + (item & 1), nb = pr % nblk, k0 = 64 * kb, n0 = 32 * nb;
;     const int nr = n0 + (lane & 31); const int sc = MAP == 1 ? src_col_in(nr) : nr;
;     float v[32];
; #pragma unroll
;     for (int i = 0; i < 32; ++i) v[i] = sc >= 0 ? W[(size_t)(k0 + 2 * i + (lane >> 5)) * Nsrc + sc] : 0.f;
; #pragma unroll
;     for (int i = 0; i < 32; ++i) { const int k = k0 + 2 * i + (lane >> 5); float x = v[i] * wscale; if (KS) x *= (k < ksplit ? ksA[k] : ksB[k - ksplit]); scr[(2 * i + (lane >> 5)) * 33 + (lane & 31)] = x; }
;     LDS_WAIT(); asm volatile("" ::: "memory");
;     const int c = lane & 7;
; #pragma unroll
;     for (int j = 0; j < 4; ++j) { const int n = (lane >> 3) + 8 * j; const LAS float* s = scr + (8 * c) * 33 + n;
;         const unsigned long long o = (unsigned long long)pg8::pk4_fp8(s[0 * 33], s[1 * 33], s[2 * 33], s[3 * 33]) | ((unsigned long long)pg8::pk4_fp8(s[4 * 33], s[5 * 33], s[6 * 33], s[7 * 33]) << 32);
;         *(GAS unsigned long long*)(WT + (size_t)(n0 + n) * K + k0 + 8 * c) = o; }
;     LDS_WAIT(); asm volatile("" ::: "memory");
	s_mov_b64 s[8:9], s[38:39]
	global_load_dwordx4 v[144:147], v75, s[8:9]
	s_add_u32 s8, s8, 0x8000
	s_addc_u32 s9, s9, 0
	global_load_dwordx4 v[148:151], v75, s[8:9]
	s_add_u32 s8, s8, 0x8000
	s_addc_u32 s9, s9, 0
	global_load_dwordx4 v[152:155], v75, s[8:9]
	s_add_u32 s8, s8, 0x8000
	s_addc_u32 s9, s9, 0
	global_load_dwordx4 v[156:159], v75, s[8:9]
	s_add_u32 s8, s8, 0x8000
	s_addc_u32 s9, s9, 0
	global_load_dwordx4 v[160:163], v75, s[8:9]
	s_add_u32 s8, s8, 0x8000
	s_addc_u32 s9, s9, 0
	global_load_dwordx4 v[164:167], v75, s[8:9]
	s_add_u32 s8, s8, 0x8000
	s_addc_u32 s9, s9, 0
	global_load_dwordx4 v[168:171], v75, s[8:9]
	s_add_u32 s8, s8, 0x8000
	s_addc_u32 s9, s9, 0
	global_load_dwordx4 v[172:175], v75, s[8:9]
	s_add_u32 s6, s36, 0x3800000
	s_addc_u32 s7, s37, 0
	ds_read_b32 v226, v211
	ds_read_b32 v227, v211 offset:512
	ds_read_b32 v228, v211 offset:1024
	ds_read_b32 v229, v211 offset:1536
	ds_read_b32 v230, v211 offset:2048
	ds_read_b32 v231, v211 offset:2560
	ds_read_b32 v232, v211 offset:3072
	ds_read_b32 v233, v211 offset:3584
	ds_read_b32 v234, v211 offset:4096
	ds_read_b32 v235, v211 offset:4608
	ds_read_b32 v236, v211 offset:5120
	ds_read_b32 v237, v211 offset:5632
	ds_read_b32 v238, v211 offset:6144
	ds_read_b32 v239, v211 offset:6656
	ds_read_b32 v240, v211 offset:7168
	ds_read_b32 v241, v211 offset:7680
	s_waitcnt lgkmcnt(0)
	v_max_f32_e32 v226, v226, v226
	v_max_f32_e32 v227, v227, v227
	v_max_f32_e32 v228, v228, v228
	v_max_f32_e32 v229, v229, v229
	v_max_f32_e32 v230, v230, v230
	v_max_f32_e32 v231, v231, v231
	v_max_f32_e32 v232, v232, v232
	v_max_f32_e32 v233, v233, v233
	v_max_f32_e32 v234, v234, v234
	v_max_f32_e32 v235, v235, v235
	v_max_f32_e32 v236, v236, v236
	v_max_f32_e32 v237, v237, v237
	v_max_f32_e32 v238, v238, v238
	v_max_f32_e32 v239, v239, v239
	v_max_f32_e32 v240, v240, v240
	v_max_f32_e32 v241, v241, v241
	v_med3_f32 v226, v226, s62, v95
	v_med3_f32 v227, v227, s62, v95
	v_med3_f32 v228, v228, s62, v95
	v_med3_f32 v229, v229, s62, v95
	v_med3_f32 v230, v230, s62, v95
	v_med3_f32 v231, v231, s62, v95
	v_med3_f32 v232, v232, s62, v95
	v_med3_f32 v233, v233, s62, v95
	v_med3_f32 v234, v234, s62, v95
	v_med3_f32 v235, v235, s62, v95
	v_med3_f32 v236, v236, s62, v95
	v_med3_f32 v237, v237, s62, v95
	v_med3_f32 v238, v238, s62, v95
	v_med3_f32 v239, v239, s62, v95
	v_med3_f32 v240, v240, s62, v95
	v_med3_f32 v241, v241, s62, v95
	v_mov_b32_e32 v242, 0
	v_mov_b32_e32 v243, 0
	v_mov_b32_e32 v244, 0
	v_mov_b32_e32 v245, 0
	v_cvt_pk_fp8_f32 v242, v226, v227
	v_cvt_pk_fp8_f32 v243, v230, v231
	v_cvt_pk_fp8_f32 v244, v234, v235
	v_cvt_pk_fp8_f32 v245, v238, v239
	v_cvt_pk_fp8_f32 v242, v228, v229 op_sel:[0,0,1]
	v_cvt_pk_fp8_f32 v243, v232, v233 op_sel:[0,0,1]
	v_cvt_pk_fp8_f32 v244, v236, v237 op_sel:[0,0,1]
	v_cvt_pk_fp8_f32 v245, v240, v241 op_sel:[0,0,1]
	s_nop 0
	global_store_dwordx4 v77, v[242:245], s[6:7]
	ds_read_b32 v226, v213
	ds_read_b32 v227, v213 offset:512
	ds_read_b32 v228, v213 offset:1024
	ds_read_b32 v229, v213 offset:1536
	ds_read_b32 v230, v213 offset:2048
	ds_read_b32 v231, v213 offset:2560
	ds_read_b32 v232, v213 offset:3072
	ds_read_b32 v233, v213 offset:3584
	ds_read_b32 v234, v213 offset:4096
	ds_read_b32 v235, v213 offset:4608
	ds_read_b32 v236, v213 offset:5120
	ds_read_b32 v237, v213 offset:5632
	ds_read_b32 v238, v213 offset:6144
	ds_read_b32 v239, v213 offset:6656
	ds_read_b32 v240, v213 offset:7168
	ds_read_b32 v241, v213 offset:7680
	s_waitcnt lgkmcnt(0)
	v_max_f32_e32 v226, v226, v226
	v_max_f32_e32 v227, v227, v227
	v_max_f32_e32 v228, v228, v228
	v_max_f32_e32 v229, v229, v229
	v_max_f32_e32 v230, v230, v230
	v_max_f32_e32 v231, v231, v231
	v_max_f32_e32 v232, v232, v232
	v_max_f32_e32 v233, v233, v233
	v_max_f32_e32 v234, v234, v234
	v_max_f32_e32 v235, v235, v235
	v_max_f32_e32 v236, v236, v236
	v_max_f32_e32 v237, v237, v237
	v_max_f32_e32 v238, v238, v238
	v_max_f32_e32 v239, v239, v239
	v_max_f32_e32 v240, v240, v240
	v_max_f32_e32 v241, v241, v241
	v_med3_f32 v226, v226, s62, v95
	v_med3_f32 v227, v227, s62, v95
	v_med3_f32 v228, v228, s62, v95
	v_med3_f32 v229, v229, s62, v95
	v_med3_f32 v230, v230, s62, v95
	v_med3_f32 v231, v231, s62, v95
	v_med3_f32 v232, v232, s62, v95
	v_med3_f32 v233, v233, s62, v95
	v_med3_f32 v234, v234, s62, v95
	v_med3_f32 v235, v235, s62, v95
	v_med3_f32 v236, v236, s62, v95
	v_med3_f32 v237, v237, s62, v95
	v_med3_f32 v238, v238, s62, v95
	v_med3_f32 v239, v239, s62, v95
	v_med3_f32 v240, v240, s62, v95
	v_med3_f32 v241, v241, s62, v95
	v_mov_b32_e32 v242, 0
	v_mov_b32_e32 v243, 0
	v_mov_b32_e32 v244, 0
	v_mov_b32_e32 v245, 0
	v_cvt_pk_fp8_f32 v242, v226, v227
	v_cvt_pk_fp8_f32 v243, v230, v231
	v_cvt_pk_fp8_f32 v244, v234, v235
	v_cvt_pk_fp8_f32 v245, v238, v239
	v_cvt_pk_fp8_f32 v242, v228, v229 op_sel:[0,0,1]
	v_cvt_pk_fp8_f32 v243, v232, v233 op_sel:[0,0,1]
	v_cvt_pk_fp8_f32 v244, v236, v237 op_sel:[0,0,1]
	v_cvt_pk_fp8_f32 v245, v240, v241 op_sel:[0,0,1]
	s_nop 0
	global_store_dwordx4 v78, v[242:245], s[6:7]
	s_waitcnt vmcnt(12)
	v_mul_f32_e32 v176, v34, v176
	v_mul_f32_e32 v177, v34, v177
	v_mul_f32_e32 v178, v34, v178
	v_mul_f32_e32 v179, v34, v179
	ds_write_b128 v210, v[176:179]
	v_mul_f32_e32 v180, v35, v180
	v_mul_f32_e32 v181, v35, v181
	v_mul_f32_e32 v182, v35, v182
	v_mul_f32_e32 v183, v35, v183
	ds_write_b128 v210, v[180:183] offset:1024
	v_mul_f32_e32 v184, v36, v184
	v_mul_f32_e32 v185, v36, v185
	v_mul_f32_e32 v186, v36, v186
	v_mul_f32_e32 v187, v36, v187
	ds_write_b128 v210, v[184:187] offset:2048
	v_mul_f32_e32 v188, v37, v188
	v_mul_f32_e32 v189, v37, v189
	v_mul_f32_e32 v190, v37, v190
	v_mul_f32_e32 v191, v37, v191
	ds_write_b128 v210, v[188:191] offset:3072
	v_mul_f32_e32 v192, v38, v192
	v_mul_f32_e32 v193, v38, v193
	v_mul_f32_e32 v194, v38, v194
	v_mul_f32_e32 v195, v38, v195
	ds_write_b128 v210, v[192:195] offset:4096
	v_mul_f32_e32 v196, v39, v196
	v_mul_f32_e32 v197, v39, v197
	v_mul_f32_e32 v198, v39, v198
	v_mul_f32_e32 v199, v39, v199
	ds_write_b128 v210, v[196:199] offset:5120
	v_mul_f32_e32 v200, v40, v200
	v_mul_f32_e32 v201, v40, v201
	v_mul_f32_e32 v202, v40, v202
	v_mul_f32_e32 v203, v40, v203
	ds_write_b128 v210, v[200:203] offset:6144
	v_mul_f32_e32 v204, v41, v204
	v_mul_f32_e32 v205, v41, v205
	v_mul_f32_e32 v206, v41, v206
	v_mul_f32_e32 v207, v41, v207
	ds_write_b128 v210, v[204:207] offset:7168
	s_waitcnt lgkmcnt(0)
	s_barrier
; #define GAS __attribute__((address_space(1)))
; #define LAS __attribute__((address_space(3)))
; #define LDS_WAIT() asm volatile("s_waitcnt lgkmcnt(0)" ::: "memory")
;     const int pr = item >> 1, kb = 2 * (pr / nblk) + (item & 1), nb = pr % nblk, k0 = 64 * kb, n0 = 32 * nb;
;     const int nr = n0 + (lane & 31); const int sc = MAP == 1 ? src_col_in(nr) : nr;
;     float v[32];
; #pragma unroll
;     for (int i = 0; i < 32; ++i) v[i] = sc >= 0 ? W[(size_t)(k0 + 2 * i + (lane >> 5)) * Nsrc + sc] : 0.f;
; #pragma unroll
;     for (int i = 0; i < 32; ++i) { const int k = k0 + 2 * i + (lane >> 5); float x = v[i] * wscale; if (KS) x *= (k < ksplit ? ksA[k] : ksB[k - ksplit]); scr[(2 * i + (lane >> 5)) * 33 + (lane & 31)] = x; }
;     LDS_WAIT(); asm volatile("" ::: "memory");
;     const int c = lane & 7;
; #pragma unroll
;     for (int j = 0; j < 4; ++j) { const int n = (lane >> 3) + 8 * j; const LAS float* s = scr + (8 * c) * 33 + n;
;         const unsigned long long o = (unsigned long long)pg8::pk4_fp8(s[0 * 33], s[1 * 33], s[2 * 33], s[3 * 33]) | ((unsigned long long)pg8::pk4_fp8(s[4 * 33], s[5 * 33], s[6 * 33], s[7 * 33]) << 32);
;         *(GAS unsigned long long*)(WT + (size_t)(n0 + n) * K + k0 + 8 * c) = o; }
;     LDS_WAIT(); asm volatile("" ::: "memory");
	s_add_u32 s8, s38, 0x1000000
	s_addc_u32 s9, s39, 0
	global_load_dwordx4 v[176:179], v75, s[8:9]
	s_add_u32 s8, s8, 0x8000
	s_addc_u32 s9, s9, 0
	global_load_dwordx4 v[180:183], v75, s[8:9]
	s_add_u32 s8, s8, 0x8000
	s_addc_u32 s9, s9, 0
	global_load_dwordx4 v[184:187], v75, s[8:9]
	s_add_u32 s8, s8, 0x8000
	s_addc_u32 s9, s9, 0
	global_load_dwordx4 v[188:191], v75, s[8:9]
	s_add_u32 s8, s8, 0x8000
	s_addc_u32 s9, s9, 0
	global_load_dwordx4 v[192:195], v75, s[8:9]
	s_add_u32 s8, s8, 0x8000
	s_addc_u32 s9, s9, 0
	global_load_dwordx4 v[196:199], v75, s[8:9]
	s_add_u32 s8, s8, 0x8000
	s_addc_u32 s9, s9, 0
	global_load_dwordx4 v[200:203], v75, s[8:9]
	s_add_u32 s8, s8, 0x8000
	s_addc_u32 s9, s9, 0
	global_load_dwordx4 v[204:207], v75, s[8:9]
	s_add_u32 s6, s36, 0x3c00000
	s_addc_u32 s7, s37, 0
	ds_read_b32 v226, v212
	ds_read_b32 v227, v212 offset:512
	ds_read_b32 v228, v212 offset:1024
	ds_read_b32 v229, v212 offset:1536
	ds_read_b32 v230, v212 offset:2048
	ds_read_b32 v231, v212 offset:2560
	ds_read_b32 v232, v212 offset:3072
	ds_read_b32 v233, v212 offset:3584
	ds_read_b32 v234, v212 offset:4096
	ds_read_b32 v235, v212 offset:4608
	ds_read_b32 v236, v212 offset:5120
	ds_read_b32 v237, v212 offset:5632
	ds_read_b32 v238, v212 offset:6144
	ds_read_b32 v239, v212 offset:6656
	ds_read_b32 v240, v212 offset:7168
	ds_read_b32 v241, v212 offset:7680
	s_waitcnt lgkmcnt(0)
	v_max_f32_e32 v226, v226, v226
	v_max_f32_e32 v227, v227, v227
	v_max_f32_e32 v228, v228, v228
	v_max_f32_e32 v229, v229, v229
	v_max_f32_e32 v230, v230, v230
	v_max_f32_e32 v231, v231, v231
	v_max_f32_e32 v232, v232, v232
	v_max_f32_e32 v233, v233, v233
	v_max_f32_e32 v234, v234, v234
	v_max_f32_e32 v235, v235, v235
	v_max_f32_e32 v236, v236, v236
	v_max_f32_e32 v237, v237, v237
	v_max_f32_e32 v238, v238, v238
	v_max_f32_e32 v239, v239, v239
	v_max_f32_e32 v240, v240, v240
	v_max_f32_e32 v241, v241, v241
	v_med3_f32 v226, v226, s62, v95
	v_med3_f32 v227, v227, s62, v95
	v_med3_f32 v228, v228, s62, v95
	v_med3_f32 v229, v229, s62, v95
	v_med3_f32 v230, v230, s62, v95
	v_med3_f32 v231, v231, s62, v95
	v_med3_f32 v232, v232, s62, v95
	v_med3_f32 v233, v233, s62, v95
	v_med3_f32 v234, v234, s62, v95
	v_med3_f32 v235, v235, s62, v95
	v_med3_f32 v236, v236, s62, v95
	v_med3_f32 v237, v237, s62, v95
	v_med3_f32 v238, v238, s62, v95
	v_med3_f32 v239, v239, s62, v95
	v_med3_f32 v240, v240, s62, v95
	v_med3_f32 v241, v241, s62, v95
	v_mov_b32_e32 v242, 0
	v_mov_b32_e32 v243, 0
	v_mov_b32_e32 v244, 0
	v_mov_b32_e32 v245, 0
	v_cvt_pk_fp8_f32 v242, v226, v227
	v_cvt_pk_fp8_f32 v243, v230, v231
	v_cvt_pk_fp8_f32 v244, v234, v235
	v_cvt_pk_fp8_f32 v245, v238, v239
	v_cvt_pk_fp8_f32 v242, v228, v229 op_sel:[0,0,1]
	v_cvt_pk_fp8_f32 v243, v232, v233 op_sel:[0,0,1]
	v_cvt_pk_fp8_f32 v244, v236, v237 op_sel:[0,0,1]
	v_cvt_pk_fp8_f32 v245, v240, v241 op_sel:[0,0,1]
	s_nop 0
	global_store_dwordx4 v77, v[242:245], s[6:7]
	ds_read_b32 v226, v214
	ds_read_b32 v227, v214 offset:512
	ds_read_b32 v228, v214 offset:1024
	ds_read_b32 v229, v214 offset:1536
	ds_read_b32 v230, v214 offset:2048
	ds_read_b32 v231, v214 offset:2560
	ds_read_b32 v232, v214 offset:3072
	ds_read_b32 v233, v214 offset:3584
	ds_read_b32 v234, v214 offset:4096
	ds_read_b32 v235, v214 offset:4608
	ds_read_b32 v236, v214 offset:5120
	ds_read_b32 v237, v214 offset:5632
	ds_read_b32 v238, v214 offset:6144
	ds_read_b32 v239, v214 offset:6656
	ds_read_b32 v240, v214 offset:7168
	ds_read_b32 v241, v214 offset:7680
	s_waitcnt lgkmcnt(0)
	v_max_f32_e32 v226, v226, v226
	v_max_f32_e32 v227, v227, v227
	v_max_f32_e32 v228, v228, v228
	v_max_f32_e32 v229, v229, v229
	v_max_f32_e32 v230, v230, v230
	v_max_f32_e32 v231, v231, v231
	v_max_f32_e32 v232, v232, v232
	v_max_f32_e32 v233, v233, v233
	v_max_f32_e32 v234, v234, v234
	v_max_f32_e32 v235, v235, v235
	v_max_f32_e32 v236, v236, v236
	v_max_f32_e32 v237, v237, v237
	v_max_f32_e32 v238, v238, v238
	v_max_f32_e32 v239, v239, v239
	v_max_f32_e32 v240, v240, v240
	v_max_f32_e32 v241, v241, v241
	v_med3_f32 v226, v226, s62, v95
	v_med3_f32 v227, v227, s62, v95
	v_med3_f32 v228, v228, s62, v95
	v_med3_f32 v229, v229, s62, v95
	v_med3_f32 v230, v230, s62, v95
	v_med3_f32 v231, v231, s62, v95
	v_med3_f32 v232, v232, s62, v95
	v_med3_f32 v233, v233, s62, v95
	v_med3_f32 v234, v234, s62, v95
	v_med3_f32 v235, v235, s62, v95
	v_med3_f32 v236, v236, s62, v95
	v_med3_f32 v237, v237, s62, v95
	v_med3_f32 v238, v238, s62, v95
	v_med3_f32 v239, v239, s62, v95
	v_med3_f32 v240, v240, s62, v95
	v_med3_f32 v241, v241, s62, v95
	v_mov_b32_e32 v242, 0
	v_mov_b32_e32 v243, 0
	v_mov_b32_e32 v244, 0
	v_mov_b32_e32 v245, 0
	v_cvt_pk_fp8_f32 v242, v226, v227
	v_cvt_pk_fp8_f32 v243, v230, v231
	v_cvt_pk_fp8_f32 v244, v234, v235
	v_cvt_pk_fp8_f32 v245, v238, v239
	v_cvt_pk_fp8_f32 v242, v228, v229 op_sel:[0,0,1]
	v_cvt_pk_fp8_f32 v243, v232, v233 op_sel:[0,0,1]
	v_cvt_pk_fp8_f32 v244, v236, v237 op_sel:[0,0,1]
	v_cvt_pk_fp8_f32 v245, v240, v241 op_sel:[0,0,1]
	s_nop 0
	global_store_dwordx4 v78, v[242:245], s[6:7]
	s_waitcnt vmcnt(12)
	v_mul_f32_e32 v144, 0x43000000, v144
	v_mul_f32_e32 v145, 0x43000000, v145
	v_mul_f32_e32 v146, 0x43000000, v146
	v_mul_f32_e32 v147, 0x43000000, v147
	ds_write_b128 v209, v[144:147]
	v_mul_f32_e32 v148, 0x43000000, v148
	v_mul_f32_e32 v149, 0x43000000, v149
	v_mul_f32_e32 v150, 0x43000000, v150
	v_mul_f32_e32 v151, 0x43000000, v151
	ds_write_b128 v209, v[148:151] offset:1024
	v_mul_f32_e32 v152, 0x43000000, v152
	v_mul_f32_e32 v153, 0x43000000, v153
	v_mul_f32_e32 v154, 0x43000000, v154
	v_mul_f32_e32 v155, 0x43000000, v155
	ds_write_b128 v209, v[152:155] offset:2048
	v_mul_f32_e32 v156, 0x43000000, v156
	v_mul_f32_e32 v157, 0x43000000, v157
	v_mul_f32_e32 v158, 0x43000000, v158
	v_mul_f32_e32 v159, 0x43000000, v159
	ds_write_b128 v209, v[156:159] offset:3072
	v_mul_f32_e32 v160, 0x43000000, v160
	v_mul_f32_e32 v161, 0x43000000, v161
	v_mul_f32_e32 v162, 0x43000000, v162
	v_mul_f32_e32 v163, 0x43000000, v163
	ds_write_b128 v209, v[160:163] offset:4096
	v_mul_f32_e32 v164, 0x43000000, v164
	v_mul_f32_e32 v165, 0x43000000, v165
	v_mul_f32_e32 v166, 0x43000000, v166
	v_mul_f32_e32 v167, 0x43000000, v167
	ds_write_b128 v209, v[164:167] offset:5120
	v_mul_f32_e32 v168, 0x43000000, v168
	v_mul_f32_e32 v169, 0x43000000, v169
	v_mul_f32_e32 v170, 0x43000000, v170
	v_mul_f32_e32 v171, 0x43000000, v171
	ds_write_b128 v209, v[168:171] offset:6144
	v_mul_f32_e32 v172, 0x43000000, v172
	v_mul_f32_e32 v173, 0x43000000, v173
	v_mul_f32_e32 v174, 0x43000000, v174
	v_mul_f32_e32 v175, 0x43000000, v175
	ds_write_b128 v209, v[172:175] offset:7168
	s_waitcnt lgkmcnt(0)
	s_barrier
; #define GAS __attribute__((address_space(1)))
; #define LAS __attribute__((address_space(3)))
; #define LDS_WAIT() asm volatile("s_waitcnt lgkmcnt(0)" ::: "memory")
;     const int pr = item >> 1, kb = 2 * (pr / nblk) + (item & 1), nb = pr % nblk, k0 = 64 * kb, n0 = 32 * nb;
;     const int nr = n0 + (lane & 31); const int sc = MAP == 1 ? src_col_in(nr) : nr;
;     float v[32];
; #pragma unroll
;     for (int i = 0; i < 32; ++i) v[i] = sc >= 0 ? W[(size_t)(k0 + 2 * i + (lane >> 5)) * Nsrc + sc] : 0.f;
; #pragma unroll
;     for (int i = 0; i < 32; ++i) { const int k = k0 + 2 * i + (lane >> 5); float x = v[i] * wscale; if (KS) x *= (k < ksplit ? ksA[k] : ksB[k - ksplit]); scr[(2 * i + (lane >> 5)) * 33 + (lane & 31)] = x; }
;     LDS_WAIT(); asm volatile("" ::: "memory");
;     const int c = lane & 7;
; #pragma unroll
;     for (int j = 0; j < 4; ++j) { const int n = (lane >> 3) + 8 * j; const LAS float* s = scr + (8 * c) * 33 + n;
;         const unsigned long long o = (unsigned long long)pg8::pk4_fp8(s[0 * 33], s[1 * 33], s[2 * 33], s[3 * 33]) | ((unsigned long long)pg8::pk4_fp8(s[4 * 33], s[5 * 33], s[6 * 33], s[7 * 33]) << 32);
;         *(GAS unsigned long long*)(WT + (size_t)(n0 + n) * K + k0 + 8 * c) = o; }
;     LDS_WAIT(); asm volatile("" ::: "memory");
	s_add_u32 s8, s38, 0x2000000
	s_addc_u32 s9, s39, 0
	global_load_dwordx4 v[144:147], v75, s[8:9]
	s_add_u32 s8, s8, 0x8000
	s_addc_u32 s9, s9, 0
	global_load_dwordx4 v[148:151], v75, s[8:9]
	s_add_u32 s8, s8, 0x8000
	s_addc_u32 s9, s9, 0
	global_load_dwordx4 v[152:155], v75, s[8:9]
	s_add_u32 s8, s8, 0x8000
	s_addc_u32 s9, s9, 0
	global_load_dwordx4 v[156:159], v75, s[8:9]
	s_add_u32 s8, s8, 0x8000
	s_addc_u32 s9, s9, 0
	global_load_dwordx4 v[160:163], v75, s[8:9]
	s_add_u32 s8, s8, 0x8000
	s_addc_u32 s9, s9, 0
	global_load_dwordx4 v[164:167], v75, s[8:9]
	s_add_u32 s8, s8, 0x8000
	s_addc_u32 s9, s9, 0
	global_load_dwordx4 v[168:171], v75, s[8:9]
	s_add_u32 s8, s8, 0x8000
	s_addc_u32 s9, s9, 0
	global_load_dwordx4 v[172:175], v75, s[8:9]
	s_mov_b64 s[6:7], s[40:41]
	ds_read_b32 v226, v211
	ds_read_b32 v227, v211 offset:512
	ds_read_b32 v228, v211 offset:1024
	ds_read_b32 v229, v211 offset:1536
	ds_read_b32 v230, v211 offset:2048
	ds_read_b32 v231, v211 offset:2560
	ds_read_b32 v232, v211 offset:3072
	ds_read_b32 v233, v211 offset:3584
	ds_read_b32 v234, v211 offset:4096
	ds_read_b32 v235, v211 offset:4608
	ds_read_b32 v236, v211 offset:5120
	ds_read_b32 v237, v211 offset:5632
	ds_read_b32 v238, v211 offset:6144
	ds_read_b32 v239, v211 offset:6656
	ds_read_b32 v240, v211 offset:7168
	ds_read_b32 v241, v211 offset:7680
	s_waitcnt lgkmcnt(0)
	v_max_f32_e32 v226, v226, v226
	v_max_f32_e32 v227, v227, v227
	v_max_f32_e32 v228, v228, v228
	v_max_f32_e32 v229, v229, v229
	v_max_f32_e32 v230, v230, v230
	v_max_f32_e32 v231, v231, v231
	v_max_f32_e32 v232, v232, v232
	v_max_f32_e32 v233, v233, v233
	v_max_f32_e32 v234, v234, v234
	v_max_f32_e32 v235, v235, v235
	v_max_f32_e32 v236, v236, v236
	v_max_f32_e32 v237, v237, v237
	v_max_f32_e32 v238, v238, v238
	v_max_f32_e32 v239, v239, v239
	v_max_f32_e32 v240, v240, v240
	v_max_f32_e32 v241, v241, v241
	v_med3_f32 v226, v226, s62, v95
	v_med3_f32 v227, v227, s62, v95
	v_med3_f32 v228, v228, s62, v95
	v_med3_f32 v229, v229, s62, v95
	v_med3_f32 v230, v230, s62, v95
	v_med3_f32 v231, v231, s62, v95
	v_med3_f32 v232, v232, s62, v95
	v_med3_f32 v233, v233, s62, v95
	v_med3_f32 v234, v234, s62, v95
	v_med3_f32 v235, v235, s62, v95
	v_med3_f32 v236, v236, s62, v95
	v_med3_f32 v237, v237, s62, v95
	v_med3_f32 v238, v238, s62, v95
	v_med3_f32 v239, v239, s62, v95
	v_med3_f32 v240, v240, s62, v95
	v_med3_f32 v241, v241, s62, v95
	v_mov_b32_e32 v242, 0
	v_mov_b32_e32 v243, 0
	v_mov_b32_e32 v244, 0
	v_mov_b32_e32 v245, 0
	v_cvt_pk_fp8_f32 v242, v226, v227
	v_cvt_pk_fp8_f32 v243, v230, v231
	v_cvt_pk_fp8_f32 v244, v234, v235
	v_cvt_pk_fp8_f32 v245, v238, v239
	v_cvt_pk_fp8_f32 v242, v228, v229 op_sel:[0,0,1]
	v_cvt_pk_fp8_f32 v243, v232, v233 op_sel:[0,0,1]
	v_cvt_pk_fp8_f32 v244, v236, v237 op_sel:[0,0,1]
	v_cvt_pk_fp8_f32 v245, v240, v241 op_sel:[0,0,1]
	s_nop 0
	global_store_dwordx4 v79, v[242:245], s[6:7]
	ds_read_b32 v226, v213
	ds_read_b32 v227, v213 offset:512
	ds_read_b32 v228, v213 offset:1024
	ds_read_b32 v229, v213 offset:1536
	ds_read_b32 v230, v213 offset:2048
	ds_read_b32 v231, v213 offset:2560
	ds_read_b32 v232, v213 offset:3072
	ds_read_b32 v233, v213 offset:3584
	ds_read_b32 v234, v213 offset:4096
	ds_read_b32 v235, v213 offset:4608
	ds_read_b32 v236, v213 offset:5120
	ds_read_b32 v237, v213 offset:5632
	ds_read_b32 v238, v213 offset:6144
	ds_read_b32 v239, v213 offset:6656
	ds_read_b32 v240, v213 offset:7168
	ds_read_b32 v241, v213 offset:7680
	s_waitcnt lgkmcnt(0)
	v_max_f32_e32 v226, v226, v226
	v_max_f32_e32 v227, v227, v227
	v_max_f32_e32 v228, v228, v228
	v_max_f32_e32 v229, v229, v229
	v_max_f32_e32 v230, v230, v230
	v_max_f32_e32 v231, v231, v231
	v_max_f32_e32 v232, v232, v232
	v_max_f32_e32 v233, v233, v233
	v_max_f32_e32 v234, v234, v234
	v_max_f32_e32 v235, v235, v235
	v_max_f32_e32 v236, v236, v236
	v_max_f32_e32 v237, v237, v237
	v_max_f32_e32 v238, v238, v238
	v_max_f32_e32 v239, v239, v239
	v_max_f32_e32 v240, v240, v240
	v_max_f32_e32 v241, v241, v241
	v_med3_f32 v226, v226, s62, v95
	v_med3_f32 v227, v227, s62, v95
	v_med3_f32 v228, v228, s62, v95
	v_med3_f32 v229, v229, s62, v95
	v_med3_f32 v230, v230, s62, v95
	v_med3_f32 v231, v231, s62, v95
	v_med3_f32 v232, v232, s62, v95
	v_med3_f32 v233, v233, s62, v95
	v_med3_f32 v234, v234, s62, v95
	v_med3_f32 v235, v235, s62, v95
	v_med3_f32 v236, v236, s62, v95
	v_med3_f32 v237, v237, s62, v95
	v_med3_f32 v238, v238, s62, v95
	v_med3_f32 v239, v239, s62, v95
	v_med3_f32 v240, v240, s62, v95
	v_med3_f32 v241, v241, s62, v95
	v_mov_b32_e32 v242, 0
	v_mov_b32_e32 v243, 0
	v_mov_b32_e32 v244, 0
	v_mov_b32_e32 v245, 0
	v_cvt_pk_fp8_f32 v242, v226, v227
	v_cvt_pk_fp8_f32 v243, v230, v231
	v_cvt_pk_fp8_f32 v244, v234, v235
	v_cvt_pk_fp8_f32 v245, v238, v239
	v_cvt_pk_fp8_f32 v242, v228, v229 op_sel:[0,0,1]
	v_cvt_pk_fp8_f32 v243, v232, v233 op_sel:[0,0,1]
	v_cvt_pk_fp8_f32 v244, v236, v237 op_sel:[0,0,1]
	v_cvt_pk_fp8_f32 v245, v240, v241 op_sel:[0,0,1]
	s_nop 0
	global_store_dwordx4 v80, v[242:245], s[6:7]
	s_waitcnt vmcnt(12)
	v_mul_f32_e32 v176, 0x43000000, v176
	v_mul_f32_e32 v177, 0x43000000, v177
	v_mul_f32_e32 v178, 0x43000000, v178
	v_mul_f32_e32 v179, 0x43000000, v179
	ds_write_b128 v210, v[176:179]
	v_mul_f32_e32 v180, 0x43000000, v180
	v_mul_f32_e32 v181, 0x43000000, v181
	v_mul_f32_e32 v182, 0x43000000, v182
	v_mul_f32_e32 v183, 0x43000000, v183
	ds_write_b128 v210, v[180:183] offset:1024
	v_mul_f32_e32 v184, 0x43000000, v184
	v_mul_f32_e32 v185, 0x43000000, v185
	v_mul_f32_e32 v186, 0x43000000, v186
	v_mul_f32_e32 v187, 0x43000000, v187
	ds_write_b128 v210, v[184:187] offset:2048
	v_mul_f32_e32 v188, 0x43000000, v188
	v_mul_f32_e32 v189, 0x43000000, v189
	v_mul_f32_e32 v190, 0x43000000, v190
	v_mul_f32_e32 v191, 0x43000000, v191
	ds_write_b128 v210, v[188:191] offset:3072
	v_mul_f32_e32 v192, 0x43000000, v192
	v_mul_f32_e32 v193, 0x43000000, v193
	v_mul_f32_e32 v194, 0x43000000, v194
	v_mul_f32_e32 v195, 0x43000000, v195
	ds_write_b128 v210, v[192:195] offset:4096
	v_mul_f32_e32 v196, 0x43000000, v196
	v_mul_f32_e32 v197, 0x43000000, v197
	v_mul_f32_e32 v198, 0x43000000, v198
	v_mul_f32_e32 v199, 0x43000000, v199
	ds_write_b128 v210, v[196:199] offset:5120
	v_mul_f32_e32 v200, 0x43000000, v200
	v_mul_f32_e32 v201, 0x43000000, v201
	v_mul_f32_e32 v202, 0x43000000, v202
	v_mul_f32_e32 v203, 0x43000000, v203
	ds_write_b128 v210, v[200:203] offset:6144
	v_mul_f32_e32 v204, 0x43000000, v204
	v_mul_f32_e32 v205, 0x43000000, v205
	v_mul_f32_e32 v206, 0x43000000, v206
	v_mul_f32_e32 v207, 0x43000000, v207
	ds_write_b128 v210, v[204:207] offset:7168
	s_waitcnt lgkmcnt(0)
	s_barrier
; #define GAS __attribute__((address_space(1)))
; #define LAS __attribute__((address_space(3)))
; #define LDS_WAIT() asm volatile("s_waitcnt lgkmcnt(0)" ::: "memory")
;     const int pr = item >> 1, kb = 2 * (pr / nblk) + (item & 1), nb = pr % nblk, k0 = 64 * kb, n0 = 32 * nb;
;     const int nr = n0 + (lane & 31); const int sc = MAP == 1 ? src_col_in(nr) : nr;
;     float v[32];
; #pragma unroll
;     for (int i = 0; i < 32; ++i) v[i] = sc >= 0 ? W[(size_t)(k0 + 2 * i + (lane >> 5)) * Nsrc + sc] : 0.f;
; #pragma unroll
;     for (int i = 0; i < 32; ++i) { const int k = k0 + 2 * i + (lane >> 5); float x = v[i] * wscale; if (KS) x *= (k < ksplit ? ksA[k] : ksB[k - ksplit]); scr[(2 * i + (lane >> 5)) * 33 + (lane & 31)] = x; }
;     LDS_WAIT(); asm volatile("" ::: "memory");
;     const int c = lane & 7;
; #pragma unroll
;     for (int j = 0; j < 4; ++j) { const int n = (lane >> 3) + 8 * j; const LAS float* s = scr + (8 * c) * 33 + n;
;         const unsigned long long o = (unsigned long long)pg8::pk4_fp8(s[0 * 33], s[1 * 33], s[2 * 33], s[3 * 33]) | ((unsigned long long)pg8::pk4_fp8(s[4 * 33], s[5 * 33], s[6 * 33], s[7 * 33]) << 32);
;         *(GAS unsigned long long*)(WT + (size_t)(n0 + n) * K + k0 + 8 * c) = o; }
;     LDS_WAIT(); asm volatile("" ::: "memory");
	s_add_u32 s8, s38, 0x3000000
	s_addc_u32 s9, s39, 0
	global_load_dwordx4 v[176:179], v75, s[8:9]
	s_add_u32 s8, s8, 0x8000
	s_addc_u32 s9, s9, 0
	global_load_dwordx4 v[180:183], v75, s[8:9]
	s_add_u32 s8, s8, 0x8000
	s_addc_u32 s9, s9, 0
	global_load_dwordx4 v[184:187], v75, s[8:9]
	s_add_u32 s8, s8, 0x8000
	s_addc_u32 s9, s9, 0
	global_load_dwordx4 v[188:191], v75, s[8:9]
	s_add_u32 s8, s8, 0x8000
	s_addc_u32 s9, s9, 0
	global_load_dwordx4 v[192:195], v75, s[8:9]
	s_add_u32 s8, s8, 0x8000
	s_addc_u32 s9, s9, 0
	global_load_dwordx4 v[196:199], v75, s[8:9]
	s_add_u32 s8, s8, 0x8000
	s_addc_u32 s9, s9, 0
	global_load_dwordx4 v[200:203], v75, s[8:9]
	s_add_u32 s8, s8, 0x8000
	s_addc_u32 s9, s9, 0
	global_load_dwordx4 v[204:207], v75, s[8:9]
	s_add_u32 s6, s40, 0x400
	s_addc_u32 s7, s41, 0
	ds_read_b32 v226, v212
	ds_read_b32 v227, v212 offset:512
	ds_read_b32 v228, v212 offset:1024
	ds_read_b32 v229, v212 offset:1536
	ds_read_b32 v230, v212 offset:2048
	ds_read_b32 v231, v212 offset:2560
	ds_read_b32 v232, v212 offset:3072
	ds_read_b32 v233, v212 offset:3584
	ds_read_b32 v234, v212 offset:4096
	ds_read_b32 v235, v212 offset:4608
	ds_read_b32 v236, v212 offset:5120
	ds_read_b32 v237, v212 offset:5632
	ds_read_b32 v238, v212 offset:6144
	ds_read_b32 v239, v212 offset:6656
	ds_read_b32 v240, v212 offset:7168
	ds_read_b32 v241, v212 offset:7680
	s_waitcnt lgkmcnt(0)
	v_max_f32_e32 v226, v226, v226
	v_max_f32_e32 v227, v227, v227
	v_max_f32_e32 v228, v228, v228
	v_max_f32_e32 v229, v229, v229
	v_max_f32_e32 v230, v230, v230
	v_max_f32_e32 v231, v231, v231
	v_max_f32_e32 v232, v232, v232
	v_max_f32_e32 v233, v233, v233
	v_max_f32_e32 v234, v234, v234
	v_max_f32_e32 v235, v235, v235
	v_max_f32_e32 v236, v236, v236
	v_max_f32_e32 v237, v237, v237
	v_max_f32_e32 v238, v238, v238
	v_max_f32_e32 v239, v239, v239
	v_max_f32_e32 v240, v240, v240
	v_max_f32_e32 v241, v241, v241
	v_med3_f32 v226, v226, s62, v95
	v_med3_f32 v227, v227, s62, v95
	v_med3_f32 v228, v228, s62, v95
	v_med3_f32 v229, v229, s62, v95
	v_med3_f32 v230, v230, s62, v95
	v_med3_f32 v231, v231, s62, v95
	v_med3_f32 v232, v232, s62, v95
	v_med3_f32 v233, v233, s62, v95
	v_med3_f32 v234, v234, s62, v95
	v_med3_f32 v235, v235, s62, v95
	v_med3_f32 v236, v236, s62, v95
	v_med3_f32 v237, v237, s62, v95
	v_med3_f32 v238, v238, s62, v95
	v_med3_f32 v239, v239, s62, v95
	v_med3_f32 v240, v240, s62, v95
	v_med3_f32 v241, v241, s62, v95
	v_mov_b32_e32 v242, 0
	v_mov_b32_e32 v243, 0
	v_mov_b32_e32 v244, 0
	v_mov_b32_e32 v245, 0
	v_cvt_pk_fp8_f32 v242, v226, v227
	v_cvt_pk_fp8_f32 v243, v230, v231
	v_cvt_pk_fp8_f32 v244, v234, v235
	v_cvt_pk_fp8_f32 v245, v238, v239
	v_cvt_pk_fp8_f32 v242, v228, v229 op_sel:[0,0,1]
	v_cvt_pk_fp8_f32 v243, v232, v233 op_sel:[0,0,1]
	v_cvt_pk_fp8_f32 v244, v236, v237 op_sel:[0,0,1]
	v_cvt_pk_fp8_f32 v245, v240, v241 op_sel:[0,0,1]
	s_nop 0
	global_store_dwordx4 v79, v[242:245], s[6:7]
	ds_read_b32 v226, v214
	ds_read_b32 v227, v214 offset:512
	ds_read_b32 v228, v214 offset:1024
	ds_read_b32 v229, v214 offset:1536
	ds_read_b32 v230, v214 offset:2048
	ds_read_b32 v231, v214 offset:2560
	ds_read_b32 v232, v214 offset:3072
	ds_read_b32 v233, v214 offset:3584
	ds_read_b32 v234, v214 offset:4096
	ds_read_b32 v235, v214 offset:4608
	ds_read_b32 v236, v214 offset:5120
	ds_read_b32 v237, v214 offset:5632
	ds_read_b32 v238, v214 offset:6144
	ds_read_b32 v239, v214 offset:6656
	ds_read_b32 v240, v214 offset:7168
	ds_read_b32 v241, v214 offset:7680
	s_waitcnt lgkmcnt(0)
	v_max_f32_e32 v226, v226, v226
	v_max_f32_e32 v227, v227, v227
	v_max_f32_e32 v228, v228, v228
	v_max_f32_e32 v229, v229, v229
	v_max_f32_e32 v230, v230, v230
	v_max_f32_e32 v231, v231, v231
	v_max_f32_e32 v232, v232, v232
	v_max_f32_e32 v233, v233, v233
	v_max_f32_e32 v234, v234, v234
	v_max_f32_e32 v235, v235, v235
	v_max_f32_e32 v236, v236, v236
	v_max_f32_e32 v237, v237, v237
	v_max_f32_e32 v238, v238, v238
	v_max_f32_e32 v239, v239, v239
	v_max_f32_e32 v240, v240, v240
	v_max_f32_e32 v241, v241, v241
	v_med3_f32 v226, v226, s62, v95
	v_med3_f32 v227, v227, s62, v95
	v_med3_f32 v228, v228, s62, v95
	v_med3_f32 v229, v229, s62, v95
	v_med3_f32 v230, v230, s62, v95
	v_med3_f32 v231, v231, s62, v95
	v_med3_f32 v232, v232, s62, v95
	v_med3_f32 v233, v233, s62, v95
	v_med3_f32 v234, v234, s62, v95
	v_med3_f32 v235, v235, s62, v95
	v_med3_f32 v236, v236, s62, v95
	v_med3_f32 v237, v237, s62, v95
	v_med3_f32 v238, v238, s62, v95
	v_med3_f32 v239, v239, s62, v95
	v_med3_f32 v240, v240, s62, v95
	v_med3_f32 v241, v241, s62, v95
	v_mov_b32_e32 v242, 0
	v_mov_b32_e32 v243, 0
	v_mov_b32_e32 v244, 0
	v_mov_b32_e32 v245, 0
	v_cvt_pk_fp8_f32 v242, v226, v227
	v_cvt_pk_fp8_f32 v243, v230, v231
	v_cvt_pk_fp8_f32 v244, v234, v235
	v_cvt_pk_fp8_f32 v245, v238, v239
	v_cvt_pk_fp8_f32 v242, v228, v229 op_sel:[0,0,1]
	v_cvt_pk_fp8_f32 v243, v232, v233 op_sel:[0,0,1]
	v_cvt_pk_fp8_f32 v244, v236, v237 op_sel:[0,0,1]
	v_cvt_pk_fp8_f32 v245, v240, v241 op_sel:[0,0,1]
	s_nop 0
	global_store_dwordx4 v80, v[242:245], s[6:7]
	s_waitcnt vmcnt(12)
	v_mul_f32_e32 v144, 0x43000000, v144
	v_mul_f32_e32 v145, 0x43000000, v145
	v_mul_f32_e32 v146, 0x43000000, v146
	v_mul_f32_e32 v147, 0x43000000, v147
	ds_write_b128 v209, v[144:147]
	v_mul_f32_e32 v148, 0x43000000, v148
	v_mul_f32_e32 v149, 0x43000000, v149
	v_mul_f32_e32 v150, 0x43000000, v150
	v_mul_f32_e32 v151, 0x43000000, v151
	ds_write_b128 v209, v[148:151] offset:1024
	v_mul_f32_e32 v152, 0x43000000, v152
	v_mul_f32_e32 v153, 0x43000000, v153
	v_mul_f32_e32 v154, 0x43000000, v154
	v_mul_f32_e32 v155, 0x43000000, v155
	ds_write_b128 v209, v[152:155] offset:2048
	v_mul_f32_e32 v156, 0x43000000, v156
	v_mul_f32_e32 v157, 0x43000000, v157
	v_mul_f32_e32 v158, 0x43000000, v158
	v_mul_f32_e32 v159, 0x43000000, v159
	ds_write_b128 v209, v[156:159] offset:3072
	v_mul_f32_e32 v160, 0x43000000, v160
	v_mul_f32_e32 v161, 0x43000000, v161
	v_mul_f32_e32 v162, 0x43000000, v162
	v_mul_f32_e32 v163, 0x43000000, v163
	ds_write_b128 v209, v[160:163] offset:4096
	v_mul_f32_e32 v164, 0x43000000, v164
	v_mul_f32_e32 v165, 0x43000000, v165
	v_mul_f32_e32 v166, 0x43000000, v166
	v_mul_f32_e32 v167, 0x43000000, v167
	ds_write_b128 v209, v[164:167] offset:5120
	v_mul_f32_e32 v168, 0x43000000, v168
	v_mul_f32_e32 v169, 0x43000000, v169
	v_mul_f32_e32 v170, 0x43000000, v170
	v_mul_f32_e32 v171, 0x43000000, v171
	ds_write_b128 v209, v[168:171] offset:6144
	v_mul_f32_e32 v172, 0x43000000, v172
	v_mul_f32_e32 v173, 0x43000000, v173
	v_mul_f32_e32 v174, 0x43000000, v174
	v_mul_f32_e32 v175, 0x43000000, v175
	ds_write_b128 v209, v[172:175] offset:7168
	s_waitcnt lgkmcnt(0)
	s_barrier
; #define GAS __attribute__((address_space(1)))
; #define LAS __attribute__((address_space(3)))
; #define LDS_WAIT() asm volatile("s_waitcnt lgkmcnt(0)" ::: "memory")
;     const int pr = item >> 1, kb = 2 * (pr / nblk) + (item & 1), nb = pr % nblk, k0 = 64 * kb, n0 = 32 * nb;
;     const int nr = n0 + (lane & 31); const int sc = MAP == 1 ? src_col_in(nr) : nr;
;     float v[32];
; #pragma unroll
;     for (int i = 0; i < 32; ++i) v[i] = sc >= 0 ? W[(size_t)(k0 + 2 * i + (lane >> 5)) * Nsrc + sc] : 0.f;
; #pragma unroll
;     for (int i = 0; i < 32; ++i) { const int k = k0 + 2 * i + (lane >> 5); float x = v[i] * wscale; if (KS) x *= (k < ksplit ? ksA[k] : ksB[k - ksplit]); scr[(2 * i + (lane >> 5)) * 33 + (lane & 31)] = x; }
;     LDS_WAIT(); asm volatile("" ::: "memory");
;     const int c = lane & 7;
; #pragma unroll
;     for (int j = 0; j < 4; ++j) { const int n = (lane >> 3) + 8 * j; const LAS float* s = scr + (8 * c) * 33 + n;
;         const unsigned long long o = (unsigned long long)pg8::pk4_fp8(s[0 * 33], s[1 * 33], s[2 * 33], s[3 * 33]) | ((unsigned long long)pg8::pk4_fp8(s[4 * 33], s[5 * 33], s[6 * 33], s[7 * 33]) << 32);
;         *(GAS unsigned long long*)(WT + (size_t)(n0 + n) * K + k0 + 8 * c) = o; }
;     LDS_WAIT(); asm volatile("" ::: "memory");
	s_add_u32 s8, s38, 0x4000000
	s_addc_u32 s9, s39, 0
	global_load_dwordx4 v[144:147], v75, s[8:9]
	s_add_u32 s8, s8, 0x8000
	s_addc_u32 s9, s9, 0
	global_load_dwordx4 v[148:151], v75, s[8:9]
	s_add_u32 s8, s8, 0x8000
	s_addc_u32 s9, s9, 0
	global_load_dwordx4 v[152:155], v75, s[8:9]
	s_add_u32 s8, s8, 0x8000
	s_addc_u32 s9, s9, 0
	global_load_dwordx4 v[156:159], v75, s[8:9]
	s_add_u32 s8, s8, 0x8000
	s_addc_u32 s9, s9, 0
	global_load_dwordx4 v[160:163], v75, s[8:9]
	s_add_u32 s8, s8, 0x8000
	s_addc_u32 s9, s9, 0
	global_load_dwordx4 v[164:167], v75, s[8:9]
	s_add_u32 s8, s8, 0x8000
	s_addc_u32 s9, s9, 0
	global_load_dwordx4 v[168:171], v75, s[8:9]
	s_add_u32 s8, s8, 0x8000
	s_addc_u32 s9, s9, 0
	global_load_dwordx4 v[172:175], v75, s[8:9]
	s_add_u32 s6, s40, 0x800
	s_addc_u32 s7, s41, 0
	ds_read_b32 v226, v211
	ds_read_b32 v227, v211 offset:512
	ds_read_b32 v228, v211 offset:1024
	ds_read_b32 v229, v211 offset:1536
	ds_read_b32 v230, v211 offset:2048
	ds_read_b32 v231, v211 offset:2560
	ds_read_b32 v232, v211 offset:3072
	ds_read_b32 v233, v211 offset:3584
	ds_read_b32 v234, v211 offset:4096
	ds_read_b32 v235, v211 offset:4608
	ds_read_b32 v236, v211 offset:5120
	ds_read_b32 v237, v211 offset:5632
	ds_read_b32 v238, v211 offset:6144
	ds_read_b32 v239, v211 offset:6656
	ds_read_b32 v240, v211 offset:7168
	ds_read_b32 v241, v211 offset:7680
	s_waitcnt lgkmcnt(0)
	v_max_f32_e32 v226, v226, v226
	v_max_f32_e32 v227, v227, v227
	v_max_f32_e32 v228, v228, v228
	v_max_f32_e32 v229, v229, v229
	v_max_f32_e32 v230, v230, v230
	v_max_f32_e32 v231, v231, v231
	v_max_f32_e32 v232, v232, v232
	v_max_f32_e32 v233, v233, v233
	v_max_f32_e32 v234, v234, v234
	v_max_f32_e32 v235, v235, v235
	v_max_f32_e32 v236, v236, v236
	v_max_f32_e32 v237, v237, v237
	v_max_f32_e32 v238, v238, v238
	v_max_f32_e32 v239, v239, v239
	v_max_f32_e32 v240, v240, v240
	v_max_f32_e32 v241, v241, v241
	v_med3_f32 v226, v226, s62, v95
	v_med3_f32 v227, v227, s62, v95
	v_med3_f32 v228, v228, s62, v95
	v_med3_f32 v229, v229, s62, v95
	v_med3_f32 v230, v230, s62, v95
	v_med3_f32 v231, v231, s62, v95
	v_med3_f32 v232, v232, s62, v95
	v_med3_f32 v233, v233, s62, v95
	v_med3_f32 v234, v234, s62, v95
	v_med3_f32 v235, v235, s62, v95
	v_med3_f32 v236, v236, s62, v95
	v_med3_f32 v237, v237, s62, v95
	v_med3_f32 v238, v238, s62, v95
	v_med3_f32 v239, v239, s62, v95
	v_med3_f32 v240, v240, s62, v95
	v_med3_f32 v241, v241, s62, v95
	v_mov_b32_e32 v242, 0
	v_mov_b32_e32 v243, 0
	v_mov_b32_e32 v244, 0
	v_mov_b32_e32 v245, 0
	v_cvt_pk_fp8_f32 v242, v226, v227
	v_cvt_pk_fp8_f32 v243, v230, v231
	v_cvt_pk_fp8_f32 v244, v234, v235
	v_cvt_pk_fp8_f32 v245, v238, v239
	v_cvt_pk_fp8_f32 v242, v228, v229 op_sel:[0,0,1]
	v_cvt_pk_fp8_f32 v243, v232, v233 op_sel:[0,0,1]
	v_cvt_pk_fp8_f32 v244, v236, v237 op_sel:[0,0,1]
	v_cvt_pk_fp8_f32 v245, v240, v241 op_sel:[0,0,1]
	s_nop 0
	global_store_dwordx4 v79, v[242:245], s[6:7]
	ds_read_b32 v226, v213
	ds_read_b32 v227, v213 offset:512
	ds_read_b32 v228, v213 offset:1024
	ds_read_b32 v229, v213 offset:1536
	ds_read_b32 v230, v213 offset:2048
	ds_read_b32 v231, v213 offset:2560
	ds_read_b32 v232, v213 offset:3072
	ds_read_b32 v233, v213 offset:3584
	ds_read_b32 v234, v213 offset:4096
	ds_read_b32 v235, v213 offset:4608
	ds_read_b32 v236, v213 offset:5120
	ds_read_b32 v237, v213 offset:5632
	ds_read_b32 v238, v213 offset:6144
	ds_read_b32 v239, v213 offset:6656
	ds_read_b32 v240, v213 offset:7168
	ds_read_b32 v241, v213 offset:7680
	s_waitcnt lgkmcnt(0)
	v_max_f32_e32 v226, v226, v226
	v_max_f32_e32 v227, v227, v227
	v_max_f32_e32 v228, v228, v228
	v_max_f32_e32 v229, v229, v229
	v_max_f32_e32 v230, v230, v230
	v_max_f32_e32 v231, v231, v231
	v_max_f32_e32 v232, v232, v232
	v_max_f32_e32 v233, v233, v233
	v_max_f32_e32 v234, v234, v234
	v_max_f32_e32 v235, v235, v235
	v_max_f32_e32 v236, v236, v236
	v_max_f32_e32 v237, v237, v237
	v_max_f32_e32 v238, v238, v238
	v_max_f32_e32 v239, v239, v239
	v_max_f32_e32 v240, v240, v240
	v_max_f32_e32 v241, v241, v241
	v_med3_f32 v226, v226, s62, v95
	v_med3_f32 v227, v227, s62, v95
	v_med3_f32 v228, v228, s62, v95
	v_med3_f32 v229, v229, s62, v95
	v_med3_f32 v230, v230, s62, v95
	v_med3_f32 v231, v231, s62, v95
	v_med3_f32 v232, v232, s62, v95
	v_med3_f32 v233, v233, s62, v95
	v_med3_f32 v234, v234, s62, v95
	v_med3_f32 v235, v235, s62, v95
	v_med3_f32 v236, v236, s62, v95
	v_med3_f32 v237, v237, s62, v95
	v_med3_f32 v238, v238, s62, v95
	v_med3_f32 v239, v239, s62, v95
	v_med3_f32 v240, v240, s62, v95
	v_med3_f32 v241, v241, s62, v95
	v_mov_b32_e32 v242, 0
	v_mov_b32_e32 v243, 0
	v_mov_b32_e32 v244, 0
	v_mov_b32_e32 v245, 0
	v_cvt_pk_fp8_f32 v242, v226, v227
	v_cvt_pk_fp8_f32 v243, v230, v231
	v_cvt_pk_fp8_f32 v244, v234, v235
	v_cvt_pk_fp8_f32 v245, v238, v239
	v_cvt_pk_fp8_f32 v242, v228, v229 op_sel:[0,0,1]
	v_cvt_pk_fp8_f32 v243, v232, v233 op_sel:[0,0,1]
	v_cvt_pk_fp8_f32 v244, v236, v237 op_sel:[0,0,1]
	v_cvt_pk_fp8_f32 v245, v240, v241 op_sel:[0,0,1]
	s_nop 0
	global_store_dwordx4 v80, v[242:245], s[6:7]
	s_waitcnt vmcnt(12)
	v_mul_f32_e32 v176, 0x43000000, v176
	v_mul_f32_e32 v177, 0x43000000, v177
	v_mul_f32_e32 v178, 0x43000000, v178
	v_mul_f32_e32 v179, 0x43000000, v179
	ds_write_b128 v210, v[176:179]
	v_mul_f32_e32 v180, 0x43000000, v180
	v_mul_f32_e32 v181, 0x43000000, v181
	v_mul_f32_e32 v182, 0x43000000, v182
	v_mul_f32_e32 v183, 0x43000000, v183
	ds_write_b128 v210, v[180:183] offset:1024
	v_mul_f32_e32 v184, 0x43000000, v184
	v_mul_f32_e32 v185, 0x43000000, v185
	v_mul_f32_e32 v186, 0x43000000, v186
	v_mul_f32_e32 v187, 0x43000000, v187
	ds_write_b128 v210, v[184:187] offset:2048
	v_mul_f32_e32 v188, 0x43000000, v188
	v_mul_f32_e32 v189, 0x43000000, v189
	v_mul_f32_e32 v190, 0x43000000, v190
	v_mul_f32_e32 v191, 0x43000000, v191
	ds_write_b128 v210, v[188:191] offset:3072
	v_mul_f32_e32 v192, 0x43000000, v192
	v_mul_f32_e32 v193, 0x43000000, v193
	v_mul_f32_e32 v194, 0x43000000, v194
	v_mul_f32_e32 v195, 0x43000000, v195
	ds_write_b128 v210, v[192:195] offset:4096
	v_mul_f32_e32 v196, 0x43000000, v196
	v_mul_f32_e32 v197, 0x43000000, v197
	v_mul_f32_e32 v198, 0x43000000, v198
	v_mul_f32_e32 v199, 0x43000000, v199
	ds_write_b128 v210, v[196:199] offset:5120
	v_mul_f32_e32 v200, 0x43000000, v200
	v_mul_f32_e32 v201, 0x43000000, v201
	v_mul_f32_e32 v202, 0x43000000, v202
	v_mul_f32_e32 v203, 0x43000000, v203
	ds_write_b128 v210, v[200:203] offset:6144
	v_mul_f32_e32 v204, 0x43000000, v204
	v_mul_f32_e32 v205, 0x43000000, v205
	v_mul_f32_e32 v206, 0x43000000, v206
	v_mul_f32_e32 v207, 0x43000000, v207
	ds_write_b128 v210, v[204:207] offset:7168
	s_waitcnt lgkmcnt(0)
	s_barrier
; #define GAS __attribute__((address_space(1)))
; #define LAS __attribute__((address_space(3)))
; #define LDS_WAIT() asm volatile("s_waitcnt lgkmcnt(0)" ::: "memory")
;     const int pr = item >> 1, kb = 2 * (pr / nblk) + (item & 1), nb = pr % nblk, k0 = 64 * kb, n0 = 32 * nb;
;     const int nr = n0 + (lane & 31); const int sc = MAP == 1 ? src_col_in(nr) : nr;
;     float v[32];
; #pragma unroll
;     for (int i = 0; i < 32; ++i) v[i] = sc >= 0 ? W[(size_t)(k0 + 2 * i + (lane >> 5)) * Nsrc + sc] : 0.f;
; #pragma unroll
;     for (int i = 0; i < 32; ++i) { const int k = k0 + 2 * i + (lane >> 5); float x = v[i] * wscale; if (KS) x *= (k < ksplit ? ksA[k] : ksB[k - ksplit]); scr[(2 * i + (lane >> 5)) * 33 + (lane & 31)] = x; }
;     LDS_WAIT(); asm volatile("" ::: "memory");
;     const int c = lane & 7;
; #pragma unroll
;     for (int j = 0; j < 4; ++j) { const int n = (lane >> 3) + 8 * j; const LAS float* s = scr + (8 * c) * 33 + n;
;         const unsigned long long o = (unsigned long long)pg8::pk4_fp8(s[0 * 33], s[1 * 33], s[2 * 33], s[3 * 33]) | ((unsigned long long)pg8::pk4_fp8(s[4 * 33], s[5 * 33], s[6 * 33], s[7 * 33]) << 32);
;         *(GAS unsigned long long*)(WT + (size_t)(n0 + n) * K + k0 + 8 * c) = o; }
;     LDS_WAIT(); asm volatile("" ::: "memory");
	s_add_u32 s8, s38, 0x5000000
	s_addc_u32 s9, s39, 0
	global_load_dwordx4 v[176:179], v75, s[8:9]
	s_add_u32 s8, s8, 0x8000
	s_addc_u32 s9, s9, 0
	global_load_dwordx4 v[180:183], v75, s[8:9]
	s_add_u32 s8, s8, 0x8000
	s_addc_u32 s9, s9, 0
	global_load_dwordx4 v[184:187], v75, s[8:9]
	s_add_u32 s8, s8, 0x8000
	s_addc_u32 s9, s9, 0
	global_load_dwordx4 v[188:191], v75, s[8:9]
	s_add_u32 s8, s8, 0x8000
	s_addc_u32 s9, s9, 0
	global_load_dwordx4 v[192:195], v75, s[8:9]
	s_add_u32 s8, s8, 0x8000
	s_addc_u32 s9, s9, 0
	global_load_dwordx4 v[196:199], v75, s[8:9]
	s_add_u32 s8, s8, 0x8000
	s_addc_u32 s9, s9, 0
	global_load_dwordx4 v[200:203], v75, s[8:9]
	s_add_u32 s8, s8, 0x8000
	s_addc_u32 s9, s9, 0
	global_load_dwordx4 v[204:207], v75, s[8:9]
	s_add_u32 s6, s40, 0xc00
	s_addc_u32 s7, s41, 0
	ds_read_b32 v226, v212
	ds_read_b32 v227, v212 offset:512
	ds_read_b32 v228, v212 offset:1024
	ds_read_b32 v229, v212 offset:1536
	ds_read_b32 v230, v212 offset:2048
	ds_read_b32 v231, v212 offset:2560
	ds_read_b32 v232, v212 offset:3072
	ds_read_b32 v233, v212 offset:3584
	ds_read_b32 v234, v212 offset:4096
	ds_read_b32 v235, v212 offset:4608
	ds_read_b32 v236, v212 offset:5120
	ds_read_b32 v237, v212 offset:5632
	ds_read_b32 v238, v212 offset:6144
	ds_read_b32 v239, v212 offset:6656
	ds_read_b32 v240, v212 offset:7168
	ds_read_b32 v241, v212 offset:7680
	s_waitcnt lgkmcnt(0)
	v_max_f32_e32 v226, v226, v226
	v_max_f32_e32 v227, v227, v227
	v_max_f32_e32 v228, v228, v228
	v_max_f32_e32 v229, v229, v229
	v_max_f32_e32 v230, v230, v230
	v_max_f32_e32 v231, v231, v231
	v_max_f32_e32 v232, v232, v232
	v_max_f32_e32 v233, v233, v233
	v_max_f32_e32 v234, v234, v234
	v_max_f32_e32 v235, v235, v235
	v_max_f32_e32 v236, v236, v236
	v_max_f32_e32 v237, v237, v237
	v_max_f32_e32 v238, v238, v238
	v_max_f32_e32 v239, v239, v239
	v_max_f32_e32 v240, v240, v240
	v_max_f32_e32 v241, v241, v241
	v_med3_f32 v226, v226, s62, v95
	v_med3_f32 v227, v227, s62, v95
	v_med3_f32 v228, v228, s62, v95
	v_med3_f32 v229, v229, s62, v95
	v_med3_f32 v230, v230, s62, v95
	v_med3_f32 v231, v231, s62, v95
	v_med3_f32 v232, v232, s62, v95
	v_med3_f32 v233, v233, s62, v95
	v_med3_f32 v234, v234, s62, v95
	v_med3_f32 v235, v235, s62, v95
	v_med3_f32 v236, v236, s62, v95
	v_med3_f32 v237, v237, s62, v95
	v_med3_f32 v238, v238, s62, v95
	v_med3_f32 v239, v239, s62, v95
	v_med3_f32 v240, v240, s62, v95
	v_med3_f32 v241, v241, s62, v95
	v_mov_b32_e32 v242, 0
	v_mov_b32_e32 v243, 0
	v_mov_b32_e32 v244, 0
	v_mov_b32_e32 v245, 0
	v_cvt_pk_fp8_f32 v242, v226, v227
	v_cvt_pk_fp8_f32 v243, v230, v231
	v_cvt_pk_fp8_f32 v244, v234, v235
	v_cvt_pk_fp8_f32 v245, v238, v239
	v_cvt_pk_fp8_f32 v242, v228, v229 op_sel:[0,0,1]
	v_cvt_pk_fp8_f32 v243, v232, v233 op_sel:[0,0,1]
	v_cvt_pk_fp8_f32 v244, v236, v237 op_sel:[0,0,1]
	v_cvt_pk_fp8_f32 v245, v240, v241 op_sel:[0,0,1]
	s_nop 0
	global_store_dwordx4 v79, v[242:245], s[6:7]
	ds_read_b32 v226, v214
	ds_read_b32 v227, v214 offset:512
	ds_read_b32 v228, v214 offset:1024
	ds_read_b32 v229, v214 offset:1536
	ds_read_b32 v230, v214 offset:2048
	ds_read_b32 v231, v214 offset:2560
	ds_read_b32 v232, v214 offset:3072
	ds_read_b32 v233, v214 offset:3584
	ds_read_b32 v234, v214 offset:4096
	ds_read_b32 v235, v214 offset:4608
	ds_read_b32 v236, v214 offset:5120
	ds_read_b32 v237, v214 offset:5632
	ds_read_b32 v238, v214 offset:6144
	ds_read_b32 v239, v214 offset:6656
	ds_read_b32 v240, v214 offset:7168
	ds_read_b32 v241, v214 offset:7680
	s_waitcnt lgkmcnt(0)
	v_max_f32_e32 v226, v226, v226
	v_max_f32_e32 v227, v227, v227
	v_max_f32_e32 v228, v228, v228
	v_max_f32_e32 v229, v229, v229
	v_max_f32_e32 v230, v230, v230
	v_max_f32_e32 v231, v231, v231
	v_max_f32_e32 v232, v232, v232
	v_max_f32_e32 v233, v233, v233
	v_max_f32_e32 v234, v234, v234
	v_max_f32_e32 v235, v235, v235
	v_max_f32_e32 v236, v236, v236
	v_max_f32_e32 v237, v237, v237
	v_max_f32_e32 v238, v238, v238
	v_max_f32_e32 v239, v239, v239
	v_max_f32_e32 v240, v240, v240
	v_max_f32_e32 v241, v241, v241
	v_med3_f32 v226, v226, s62, v95
	v_med3_f32 v227, v227, s62, v95
	v_med3_f32 v228, v228, s62, v95
	v_med3_f32 v229, v229, s62, v95
	v_med3_f32 v230, v230, s62, v95
	v_med3_f32 v231, v231, s62, v95
	v_med3_f32 v232, v232, s62, v95
	v_med3_f32 v233, v233, s62, v95
	v_med3_f32 v234, v234, s62, v95
	v_med3_f32 v235, v235, s62, v95
	v_med3_f32 v236, v236, s62, v95
	v_med3_f32 v237, v237, s62, v95
	v_med3_f32 v238, v238, s62, v95
	v_med3_f32 v239, v239, s62, v95
	v_med3_f32 v240, v240, s62, v95
	v_med3_f32 v241, v241, s62, v95
	v_mov_b32_e32 v242, 0
	v_mov_b32_e32 v243, 0
	v_mov_b32_e32 v244, 0
	v_mov_b32_e32 v245, 0
	v_cvt_pk_fp8_f32 v242, v226, v227
	v_cvt_pk_fp8_f32 v243, v230, v231
	v_cvt_pk_fp8_f32 v244, v234, v235
	v_cvt_pk_fp8_f32 v245, v238, v239
	v_cvt_pk_fp8_f32 v242, v228, v229 op_sel:[0,0,1]
	v_cvt_pk_fp8_f32 v243, v232, v233 op_sel:[0,0,1]
	v_cvt_pk_fp8_f32 v244, v236, v237 op_sel:[0,0,1]
	v_cvt_pk_fp8_f32 v245, v240, v241 op_sel:[0,0,1]
	s_nop 0
	global_store_dwordx4 v80, v[242:245], s[6:7]
	s_waitcnt vmcnt(12)
	v_mul_f32_e32 v144, 0x43000000, v144
	v_mul_f32_e32 v145, 0x43000000, v145
	v_mul_f32_e32 v146, 0x43000000, v146
	v_mul_f32_e32 v147, 0x43000000, v147
	ds_write_b128 v209, v[144:147]
	v_mul_f32_e32 v148, 0x43000000, v148
	v_mul_f32_e32 v149, 0x43000000, v149
	v_mul_f32_e32 v150, 0x43000000, v150
	v_mul_f32_e32 v151, 0x43000000, v151
	ds_write_b128 v209, v[148:151] offset:1024
	v_mul_f32_e32 v152, 0x43000000, v152
	v_mul_f32_e32 v153, 0x43000000, v153
	v_mul_f32_e32 v154, 0x43000000, v154
	v_mul_f32_e32 v155, 0x43000000, v155
	ds_write_b128 v209, v[152:155] offset:2048
	v_mul_f32_e32 v156, 0x43000000, v156
	v_mul_f32_e32 v157, 0x43000000, v157
	v_mul_f32_e32 v158, 0x43000000, v158
	v_mul_f32_e32 v159, 0x43000000, v159
	ds_write_b128 v209, v[156:159] offset:3072
	v_mul_f32_e32 v160, 0x43000000, v160
	v_mul_f32_e32 v161, 0x43000000, v161
	v_mul_f32_e32 v162, 0x43000000, v162
	v_mul_f32_e32 v163, 0x43000000, v163
	ds_write_b128 v209, v[160:163] offset:4096
	v_mul_f32_e32 v164, 0x43000000, v164
	v_mul_f32_e32 v165, 0x43000000, v165
	v_mul_f32_e32 v166, 0x43000000, v166
	v_mul_f32_e32 v167, 0x43000000, v167
	ds_write_b128 v209, v[164:167] offset:5120
	v_mul_f32_e32 v168, 0x43000000, v168
	v_mul_f32_e32 v169, 0x43000000, v169
	v_mul_f32_e32 v170, 0x43000000, v170
	v_mul_f32_e32 v171, 0x43000000, v171
	ds_write_b128 v209, v[168:171] offset:6144
	v_mul_f32_e32 v172, 0x43000000, v172
	v_mul_f32_e32 v173, 0x43000000, v173
	v_mul_f32_e32 v174, 0x43000000, v174
	v_mul_f32_e32 v175, 0x43000000, v175
	ds_write_b128 v209, v[172:175] offset:7168
	s_waitcnt lgkmcnt(0)
	s_barrier
; #define GAS __attribute__((address_space(1)))
; #define LAS __attribute__((address_space(3)))
; #define LDS_WAIT() asm volatile("s_waitcnt lgkmcnt(0)" ::: "memory")
;     const int pr = item >> 1, kb = 2 * (pr / nblk) + (item & 1), nb = pr % nblk, k0 = 64 * kb, n0 = 32 * nb;
;     const int nr = n0 + (lane & 31); const int sc = MAP == 1 ? src_col_in(nr) : nr;
;     float v[32];
; #pragma unroll
;     for (int i = 0; i < 32; ++i) v[i] = sc >= 0 ? W[(size_t)(k0 + 2 * i + (lane >> 5)) * Nsrc + sc] : 0.f;
; #pragma unroll
;     for (int i = 0; i < 32; ++i) { const int k = k0 + 2 * i + (lane >> 5); float x = v[i] * wscale; if (KS) x *= (k < ksplit ? ksA[k] : ksB[k - ksplit]); scr[(2 * i + (lane >> 5)) * 33 + (lane & 31)] = x; }
;     LDS_WAIT(); asm volatile("" ::: "memory");
;     const int c = lane & 7;
; #pragma unroll
;     for (int j = 0; j < 4; ++j) { const int n = (lane >> 3) + 8 * j; const LAS float* s = scr + (8 * c) * 33 + n;
;         const unsigned long long o = (unsigned long long)pg8::pk4_fp8(s[0 * 33], s[1 * 33], s[2 * 33], s[3 * 33]) | ((unsigned long long)pg8::pk4_fp8(s[4 * 33], s[5 * 33], s[6 * 33], s[7 * 33]) << 32);
;         *(GAS unsigned long long*)(WT + (size_t)(n0 + n) * K + k0 + 8 * c) = o; }
;     LDS_WAIT(); asm volatile("" ::: "memory");
	s_add_u32 s8, s38, 0x6000000
	s_addc_u32 s9, s39, 0
	global_load_dwordx4 v[144:147], v75, s[8:9]
	s_add_u32 s8, s8, 0x8000
	s_addc_u32 s9, s9, 0
	global_load_dwordx4 v[148:151], v75, s[8:9]
	s_add_u32 s8, s8, 0x8000
	s_addc_u32 s9, s9, 0
	global_load_dwordx4 v[152:155], v75, s[8:9]
	s_add_u32 s8, s8, 0x8000
	s_addc_u32 s9, s9, 0
	global_load_dwordx4 v[156:159], v75, s[8:9]
	s_add_u32 s8, s8, 0x8000
	s_addc_u32 s9, s9, 0
	global_load_dwordx4 v[160:163], v75, s[8:9]
	s_add_u32 s8, s8, 0x8000
	s_addc_u32 s9, s9, 0
	global_load_dwordx4 v[164:167], v75, s[8:9]
	s_add_u32 s8, s8, 0x8000
	s_addc_u32 s9, s9, 0
	global_load_dwordx4 v[168:171], v75, s[8:9]
	s_add_u32 s8, s8, 0x8000
	s_addc_u32 s9, s9, 0
	global_load_dwordx4 v[172:175], v75, s[8:9]
	s_add_u32 s6, s40, 0x1000
	s_addc_u32 s7, s41, 0
	ds_read_b32 v226, v211
	ds_read_b32 v227, v211 offset:512
	ds_read_b32 v228, v211 offset:1024
	ds_read_b32 v229, v211 offset:1536
	ds_read_b32 v230, v211 offset:2048
	ds_read_b32 v231, v211 offset:2560
	ds_read_b32 v232, v211 offset:3072
	ds_read_b32 v233, v211 offset:3584
	ds_read_b32 v234, v211 offset:4096
	ds_read_b32 v235, v211 offset:4608
	ds_read_b32 v236, v211 offset:5120
	ds_read_b32 v237, v211 offset:5632
	ds_read_b32 v238, v211 offset:6144
	ds_read_b32 v239, v211 offset:6656
	ds_read_b32 v240, v211 offset:7168
	ds_read_b32 v241, v211 offset:7680
	s_waitcnt lgkmcnt(0)
	v_max_f32_e32 v226, v226, v226
	v_max_f32_e32 v227, v227, v227
	v_max_f32_e32 v228, v228, v228
	v_max_f32_e32 v229, v229, v229
	v_max_f32_e32 v230, v230, v230
	v_max_f32_e32 v231, v231, v231
	v_max_f32_e32 v232, v232, v232
	v_max_f32_e32 v233, v233, v233
	v_max_f32_e32 v234, v234, v234
	v_max_f32_e32 v235, v235, v235
	v_max_f32_e32 v236, v236, v236
	v_max_f32_e32 v237, v237, v237
	v_max_f32_e32 v238, v238, v238
	v_max_f32_e32 v239, v239, v239
	v_max_f32_e32 v240, v240, v240
	v_max_f32_e32 v241, v241, v241
	v_med3_f32 v226, v226, s62, v95
	v_med3_f32 v227, v227, s62, v95
	v_med3_f32 v228, v228, s62, v95
	v_med3_f32 v229, v229, s62, v95
	v_med3_f32 v230, v230, s62, v95
	v_med3_f32 v231, v231, s62, v95
	v_med3_f32 v232, v232, s62, v95
	v_med3_f32 v233, v233, s62, v95
	v_med3_f32 v234, v234, s62, v95
	v_med3_f32 v235, v235, s62, v95
	v_med3_f32 v236, v236, s62, v95
	v_med3_f32 v237, v237, s62, v95
	v_med3_f32 v238, v238, s62, v95
	v_med3_f32 v239, v239, s62, v95
	v_med3_f32 v240, v240, s62, v95
	v_med3_f32 v241, v241, s62, v95
	v_mov_b32_e32 v242, 0
	v_mov_b32_e32 v243, 0
	v_mov_b32_e32 v244, 0
	v_mov_b32_e32 v245, 0
	v_cvt_pk_fp8_f32 v242, v226, v227
	v_cvt_pk_fp8_f32 v243, v230, v231
	v_cvt_pk_fp8_f32 v244, v234, v235
	v_cvt_pk_fp8_f32 v245, v238, v239
	v_cvt_pk_fp8_f32 v242, v228, v229 op_sel:[0,0,1]
	v_cvt_pk_fp8_f32 v243, v232, v233 op_sel:[0,0,1]
	v_cvt_pk_fp8_f32 v244, v236, v237 op_sel:[0,0,1]
	v_cvt_pk_fp8_f32 v245, v240, v241 op_sel:[0,0,1]
	s_nop 0
	global_store_dwordx4 v79, v[242:245], s[6:7]
	ds_read_b32 v226, v213
	ds_read_b32 v227, v213 offset:512
	ds_read_b32 v228, v213 offset:1024
	ds_read_b32 v229, v213 offset:1536
	ds_read_b32 v230, v213 offset:2048
	ds_read_b32 v231, v213 offset:2560
	ds_read_b32 v232, v213 offset:3072
	ds_read_b32 v233, v213 offset:3584
	ds_read_b32 v234, v213 offset:4096
	ds_read_b32 v235, v213 offset:4608
	ds_read_b32 v236, v213 offset:5120
	ds_read_b32 v237, v213 offset:5632
	ds_read_b32 v238, v213 offset:6144
	ds_read_b32 v239, v213 offset:6656
	ds_read_b32 v240, v213 offset:7168
	ds_read_b32 v241, v213 offset:7680
	s_waitcnt lgkmcnt(0)
	v_max_f32_e32 v226, v226, v226
	v_max_f32_e32 v227, v227, v227
	v_max_f32_e32 v228, v228, v228
	v_max_f32_e32 v229, v229, v229
	v_max_f32_e32 v230, v230, v230
	v_max_f32_e32 v231, v231, v231
	v_max_f32_e32 v232, v232, v232
	v_max_f32_e32 v233, v233, v233
	v_max_f32_e32 v234, v234, v234
	v_max_f32_e32 v235, v235, v235
	v_max_f32_e32 v236, v236, v236
	v_max_f32_e32 v237, v237, v237
	v_max_f32_e32 v238, v238, v238
	v_max_f32_e32 v239, v239, v239
	v_max_f32_e32 v240, v240, v240
	v_max_f32_e32 v241, v241, v241
	v_med3_f32 v226, v226, s62, v95
	v_med3_f32 v227, v227, s62, v95
	v_med3_f32 v228, v228, s62, v95
	v_med3_f32 v229, v229, s62, v95
	v_med3_f32 v230, v230, s62, v95
	v_med3_f32 v231, v231, s62, v95
	v_med3_f32 v232, v232, s62, v95
	v_med3_f32 v233, v233, s62, v95
	v_med3_f32 v234, v234, s62, v95
	v_med3_f32 v235, v235, s62, v95
	v_med3_f32 v236, v236, s62, v95
	v_med3_f32 v237, v237, s62, v95
	v_med3_f32 v238, v238, s62, v95
	v_med3_f32 v239, v239, s62, v95
	v_med3_f32 v240, v240, s62, v95
	v_med3_f32 v241, v241, s62, v95
	v_mov_b32_e32 v242, 0
	v_mov_b32_e32 v243, 0
	v_mov_b32_e32 v244, 0
	v_mov_b32_e32 v245, 0
	v_cvt_pk_fp8_f32 v242, v226, v227
	v_cvt_pk_fp8_f32 v243, v230, v231
	v_cvt_pk_fp8_f32 v244, v234, v235
	v_cvt_pk_fp8_f32 v245, v238, v239
	v_cvt_pk_fp8_f32 v242, v228, v229 op_sel:[0,0,1]
	v_cvt_pk_fp8_f32 v243, v232, v233 op_sel:[0,0,1]
	v_cvt_pk_fp8_f32 v244, v236, v237 op_sel:[0,0,1]
	v_cvt_pk_fp8_f32 v245, v240, v241 op_sel:[0,0,1]
	s_nop 0
	global_store_dwordx4 v80, v[242:245], s[6:7]
	s_waitcnt vmcnt(12)
	v_mul_f32_e32 v176, 0x43000000, v176
	v_mul_f32_e32 v177, 0x43000000, v177
	v_mul_f32_e32 v178, 0x43000000, v178
	v_mul_f32_e32 v179, 0x43000000, v179
	ds_write_b128 v210, v[176:179]
	v_mul_f32_e32 v180, 0x43000000, v180
	v_mul_f32_e32 v181, 0x43000000, v181
	v_mul_f32_e32 v182, 0x43000000, v182
	v_mul_f32_e32 v183, 0x43000000, v183
	ds_write_b128 v210, v[180:183] offset:1024
	v_mul_f32_e32 v184, 0x43000000, v184
	v_mul_f32_e32 v185, 0x43000000, v185
	v_mul_f32_e32 v186, 0x43000000, v186
	v_mul_f32_e32 v187, 0x43000000, v187
	ds_write_b128 v210, v[184:187] offset:2048
	v_mul_f32_e32 v188, 0x43000000, v188
	v_mul_f32_e32 v189, 0x43000000, v189
	v_mul_f32_e32 v190, 0x43000000, v190
	v_mul_f32_e32 v191, 0x43000000, v191
	ds_write_b128 v210, v[188:191] offset:3072
	v_mul_f32_e32 v192, 0x43000000, v192
	v_mul_f32_e32 v193, 0x43000000, v193
	v_mul_f32_e32 v194, 0x43000000, v194
	v_mul_f32_e32 v195, 0x43000000, v195
	ds_write_b128 v210, v[192:195] offset:4096
	v_mul_f32_e32 v196, 0x43000000, v196
	v_mul_f32_e32 v197, 0x43000000, v197
	v_mul_f32_e32 v198, 0x43000000, v198
	v_mul_f32_e32 v199, 0x43000000, v199
	ds_write_b128 v210, v[196:199] offset:5120
	v_mul_f32_e32 v200, 0x43000000, v200
	v_mul_f32_e32 v201, 0x43000000, v201
	v_mul_f32_e32 v202, 0x43000000, v202
	v_mul_f32_e32 v203, 0x43000000, v203
	ds_write_b128 v210, v[200:203] offset:6144
	v_mul_f32_e32 v204, 0x43000000, v204
	v_mul_f32_e32 v205, 0x43000000, v205
	v_mul_f32_e32 v206, 0x43000000, v206
	v_mul_f32_e32 v207, 0x43000000, v207
	ds_write_b128 v210, v[204:207] offset:7168
	s_waitcnt lgkmcnt(0)
	s_barrier
; #define GAS __attribute__((address_space(1)))
; #define LAS __attribute__((address_space(3)))
; #define LDS_WAIT() asm volatile("s_waitcnt lgkmcnt(0)" ::: "memory")
;     const int pr = item >> 1, kb = 2 * (pr / nblk) + (item & 1), nb = pr % nblk, k0 = 64 * kb, n0 = 32 * nb;
;     const int nr = n0 + (lane & 31); const int sc = MAP == 1 ? src_col_in(nr) : nr;
;     float v[32];
; #pragma unroll
;     for (int i = 0; i < 32; ++i) v[i] = sc >= 0 ? W[(size_t)(k0 + 2 * i + (lane >> 5)) * Nsrc + sc] : 0.f;
; #pragma unroll
;     for (int i = 0; i < 32; ++i) { const int k = k0 + 2 * i + (lane >> 5); float x = v[i] * wscale; if (KS) x *= (k < ksplit ? ksA[k] : ksB[k - ksplit]); scr[(2 * i + (lane >> 5)) * 33 + (lane & 31)] = x; }
;     LDS_WAIT(); asm volatile("" ::: "memory");
;     const int c = lane & 7;
; #pragma unroll
;     for (int j = 0; j < 4; ++j) { const int n = (lane >> 3) + 8 * j; const LAS float* s = scr + (8 * c) * 33 + n;
;         const unsigned long long o = (unsigned long long)pg8::pk4_fp8(s[0 * 33], s[1 * 33], s[2 * 33], s[3 * 33]) | ((unsigned long long)pg8::pk4_fp8(s[4 * 33], s[5 * 33], s[6 * 33], s[7 * 33]) << 32);
;         *(GAS unsigned long long*)(WT + (size_t)(n0 + n) * K + k0 + 8 * c) = o; }
;     LDS_WAIT(); asm volatile("" ::: "memory");
	s_add_u32 s8, s38, 0x7000000
	s_addc_u32 s9, s39, 0
	global_load_dwordx4 v[176:179], v75, s[8:9]
	s_add_u32 s8, s8, 0x8000
	s_addc_u32 s9, s9, 0
	global_load_dwordx4 v[180:183], v75, s[8:9]
	s_add_u32 s8, s8, 0x8000
	s_addc_u32 s9, s9, 0
	global_load_dwordx4 v[184:187], v75, s[8:9]
	s_add_u32 s8, s8, 0x8000
	s_addc_u32 s9, s9, 0
	global_load_dwordx4 v[188:191], v75, s[8:9]
	s_add_u32 s8, s8, 0x8000
	s_addc_u32 s9, s9, 0
	global_load_dwordx4 v[192:195], v75, s[8:9]
	s_add_u32 s8, s8, 0x8000
	s_addc_u32 s9, s9, 0
	global_load_dwordx4 v[196:199], v75, s[8:9]
	s_add_u32 s8, s8, 0x8000
	s_addc_u32 s9, s9, 0
	global_load_dwordx4 v[200:203], v75, s[8:9]
	s_add_u32 s8, s8, 0x8000
	s_addc_u32 s9, s9, 0
	global_load_dwordx4 v[204:207], v75, s[8:9]
	s_add_u32 s6, s40, 0x1400
	s_addc_u32 s7, s41, 0
	ds_read_b32 v226, v212
	ds_read_b32 v227, v212 offset:512
	ds_read_b32 v228, v212 offset:1024
	ds_read_b32 v229, v212 offset:1536
	ds_read_b32 v230, v212 offset:2048
	ds_read_b32 v231, v212 offset:2560
	ds_read_b32 v232, v212 offset:3072
	ds_read_b32 v233, v212 offset:3584
	ds_read_b32 v234, v212 offset:4096
	ds_read_b32 v235, v212 offset:4608
	ds_read_b32 v236, v212 offset:5120
	ds_read_b32 v237, v212 offset:5632
	ds_read_b32 v238, v212 offset:6144
	ds_read_b32 v239, v212 offset:6656
	ds_read_b32 v240, v212 offset:7168
	ds_read_b32 v241, v212 offset:7680
	s_waitcnt lgkmcnt(0)
	v_max_f32_e32 v226, v226, v226
	v_max_f32_e32 v227, v227, v227
	v_max_f32_e32 v228, v228, v228
	v_max_f32_e32 v229, v229, v229
	v_max_f32_e32 v230, v230, v230
	v_max_f32_e32 v231, v231, v231
	v_max_f32_e32 v232, v232, v232
	v_max_f32_e32 v233, v233, v233
	v_max_f32_e32 v234, v234, v234
	v_max_f32_e32 v235, v235, v235
	v_max_f32_e32 v236, v236, v236
	v_max_f32_e32 v237, v237, v237
	v_max_f32_e32 v238, v238, v238
	v_max_f32_e32 v239, v239, v239
	v_max_f32_e32 v240, v240, v240
	v_max_f32_e32 v241, v241, v241
	v_med3_f32 v226, v226, s62, v95
	v_med3_f32 v227, v227, s62, v95
	v_med3_f32 v228, v228, s62, v95
	v_med3_f32 v229, v229, s62, v95
	v_med3_f32 v230, v230, s62, v95
	v_med3_f32 v231, v231, s62, v95
	v_med3_f32 v232, v232, s62, v95
	v_med3_f32 v233, v233, s62, v95
	v_med3_f32 v234, v234, s62, v95
	v_med3_f32 v235, v235, s62, v95
	v_med3_f32 v236, v236, s62, v95
	v_med3_f32 v237, v237, s62, v95
	v_med3_f32 v238, v238, s62, v95
	v_med3_f32 v239, v239, s62, v95
	v_med3_f32 v240, v240, s62, v95
	v_med3_f32 v241, v241, s62, v95
	v_mov_b32_e32 v242, 0
	v_mov_b32_e32 v243, 0
	v_mov_b32_e32 v244, 0
	v_mov_b32_e32 v245, 0
	v_cvt_pk_fp8_f32 v242, v226, v227
	v_cvt_pk_fp8_f32 v243, v230, v231
	v_cvt_pk_fp8_f32 v244, v234, v235
	v_cvt_pk_fp8_f32 v245, v238, v239
	v_cvt_pk_fp8_f32 v242, v228, v229 op_sel:[0,0,1]
	v_cvt_pk_fp8_f32 v243, v232, v233 op_sel:[0,0,1]
	v_cvt_pk_fp8_f32 v244, v236, v237 op_sel:[0,0,1]
	v_cvt_pk_fp8_f32 v245, v240, v241 op_sel:[0,0,1]
	s_nop 0
	global_store_dwordx4 v79, v[242:245], s[6:7]
	ds_read_b32 v226, v214
	ds_read_b32 v227, v214 offset:512
	ds_read_b32 v228, v214 offset:1024
	ds_read_b32 v229, v214 offset:1536
	ds_read_b32 v230, v214 offset:2048
	ds_read_b32 v231, v214 offset:2560
	ds_read_b32 v232, v214 offset:3072
	ds_read_b32 v233, v214 offset:3584
	ds_read_b32 v234, v214 offset:4096
	ds_read_b32 v235, v214 offset:4608
	ds_read_b32 v236, v214 offset:5120
	ds_read_b32 v237, v214 offset:5632
	ds_read_b32 v238, v214 offset:6144
	ds_read_b32 v239, v214 offset:6656
	ds_read_b32 v240, v214 offset:7168
	ds_read_b32 v241, v214 offset:7680
	s_waitcnt lgkmcnt(0)
	v_max_f32_e32 v226, v226, v226
	v_max_f32_e32 v227, v227, v227
	v_max_f32_e32 v228, v228, v228
	v_max_f32_e32 v229, v229, v229
	v_max_f32_e32 v230, v230, v230
	v_max_f32_e32 v231, v231, v231
	v_max_f32_e32 v232, v232, v232
	v_max_f32_e32 v233, v233, v233
	v_max_f32_e32 v234, v234, v234
	v_max_f32_e32 v235, v235, v235
	v_max_f32_e32 v236, v236, v236
	v_max_f32_e32 v237, v237, v237
	v_max_f32_e32 v238, v238, v238
	v_max_f32_e32 v239, v239, v239
	v_max_f32_e32 v240, v240, v240
	v_max_f32_e32 v241, v241, v241
	v_med3_f32 v226, v226, s62, v95
	v_med3_f32 v227, v227, s62, v95
	v_med3_f32 v228, v228, s62, v95
	v_med3_f32 v229, v229, s62, v95
	v_med3_f32 v230, v230, s62, v95
	v_med3_f32 v231, v231, s62, v95
	v_med3_f32 v232, v232, s62, v95
	v_med3_f32 v233, v233, s62, v95
	v_med3_f32 v234, v234, s62, v95
	v_med3_f32 v235, v235, s62, v95
	v_med3_f32 v236, v236, s62, v95
	v_med3_f32 v237, v237, s62, v95
	v_med3_f32 v238, v238, s62, v95
	v_med3_f32 v239, v239, s62, v95
	v_med3_f32 v240, v240, s62, v95
	v_med3_f32 v241, v241, s62, v95
	v_mov_b32_e32 v242, 0
	v_mov_b32_e32 v243, 0
	v_mov_b32_e32 v244, 0
	v_mov_b32_e32 v245, 0
	v_cvt_pk_fp8_f32 v242, v226, v227
	v_cvt_pk_fp8_f32 v243, v230, v231
	v_cvt_pk_fp8_f32 v244, v234, v235
	v_cvt_pk_fp8_f32 v245, v238, v239
	v_cvt_pk_fp8_f32 v242, v228, v229 op_sel:[0,0,1]
	v_cvt_pk_fp8_f32 v243, v232, v233 op_sel:[0,0,1]
	v_cvt_pk_fp8_f32 v244, v236, v237 op_sel:[0,0,1]
	v_cvt_pk_fp8_f32 v245, v240, v241 op_sel:[0,0,1]
	s_nop 0
	global_store_dwordx4 v80, v[242:245], s[6:7]
	s_waitcnt vmcnt(12)
	v_mul_f32_e32 v144, 0x43000000, v144
	v_mul_f32_e32 v145, 0x43000000, v145
	v_mul_f32_e32 v146, 0x43000000, v146
	v_mul_f32_e32 v147, 0x43000000, v147
	ds_write_b128 v209, v[144:147]
	v_mul_f32_e32 v148, 0x43000000, v148
	v_mul_f32_e32 v149, 0x43000000, v149
	v_mul_f32_e32 v150, 0x43000000, v150
	v_mul_f32_e32 v151, 0x43000000, v151
	ds_write_b128 v209, v[148:151] offset:1024
	v_mul_f32_e32 v152, 0x43000000, v152
	v_mul_f32_e32 v153, 0x43000000, v153
	v_mul_f32_e32 v154, 0x43000000, v154
	v_mul_f32_e32 v155, 0x43000000, v155
	ds_write_b128 v209, v[152:155] offset:2048
	v_mul_f32_e32 v156, 0x43000000, v156
	v_mul_f32_e32 v157, 0x43000000, v157
	v_mul_f32_e32 v158, 0x43000000, v158
	v_mul_f32_e32 v159, 0x43000000, v159
	ds_write_b128 v209, v[156:159] offset:3072
	v_mul_f32_e32 v160, 0x43000000, v160
	v_mul_f32_e32 v161, 0x43000000, v161
	v_mul_f32_e32 v162, 0x43000000, v162
	v_mul_f32_e32 v163, 0x43000000, v163
	ds_write_b128 v209, v[160:163] offset:4096
	v_mul_f32_e32 v164, 0x43000000, v164
	v_mul_f32_e32 v165, 0x43000000, v165
	v_mul_f32_e32 v166, 0x43000000, v166
	v_mul_f32_e32 v167, 0x43000000, v167
	ds_write_b128 v209, v[164:167] offset:5120
	v_mul_f32_e32 v168, 0x43000000, v168
	v_mul_f32_e32 v169, 0x43000000, v169
	v_mul_f32_e32 v170, 0x43000000, v170
	v_mul_f32_e32 v171, 0x43000000, v171
	ds_write_b128 v209, v[168:171] offset:6144
	v_mul_f32_e32 v172, 0x43000000, v172
	v_mul_f32_e32 v173, 0x43000000, v173
	v_mul_f32_e32 v174, 0x43000000, v174
	v_mul_f32_e32 v175, 0x43000000, v175
	ds_write_b128 v209, v[172:175] offset:7168
	s_waitcnt lgkmcnt(0)
	s_barrier
; #define GAS __attribute__((address_space(1)))
; #define LAS __attribute__((address_space(3)))
; #define LDS_WAIT() asm volatile("s_waitcnt lgkmcnt(0)" ::: "memory")
;     const int pr = item >> 1, kb = 2 * (pr / nblk) + (item & 1), nb = pr % nblk, k0 = 64 * kb, n0 = 32 * nb;
;     const int nr = n0 + (lane & 31); const int sc = MAP == 1 ? src_col_in(nr) : nr;
;     float v[32];
; #pragma unroll
;     for (int i = 0; i < 32; ++i) v[i] = sc >= 0 ? W[(size_t)(k0 + 2 * i + (lane >> 5)) * Nsrc + sc] : 0.f;
; #pragma unroll
;     for (int i = 0; i < 32; ++i) { const int k = k0 + 2 * i + (lane >> 5); float x = v[i] * wscale; if (KS) x *= (k < ksplit ? ksA[k] : ksB[k - ksplit]); scr[(2 * i + (lane >> 5)) * 33 + (lane & 31)] = x; }
;     LDS_WAIT(); asm volatile("" ::: "memory");
;     const int c = lane & 7;
; #pragma unroll
;     for (int j = 0; j < 4; ++j) { const int n = (lane >> 3) + 8 * j; const LAS float* s = scr + (8 * c) * 33 + n;
;         const unsigned long long o = (unsigned long long)pg8::pk4_fp8(s[0 * 33], s[1 * 33], s[2 * 33], s[3 * 33]) | ((unsigned long long)pg8::pk4_fp8(s[4 * 33], s[5 * 33], s[6 * 33], s[7 * 33]) << 32);
;         *(GAS unsigned long long*)(WT + (size_t)(n0 + n) * K + k0 + 8 * c) = o; }
;     LDS_WAIT(); asm volatile("" ::: "memory");
	s_add_u32 s8, s38, 0x8000000
	s_addc_u32 s9, s39, 0
	global_load_dwordx4 v[144:147], v75, s[8:9]
	s_add_u32 s8, s8, 0x8000
	s_addc_u32 s9, s9, 0
	global_load_dwordx4 v[148:151], v75, s[8:9]
	s_add_u32 s8, s8, 0x8000
	s_addc_u32 s9, s9, 0
	global_load_dwordx4 v[152:155], v75, s[8:9]
	s_add_u32 s8, s8, 0x8000
	s_addc_u32 s9, s9, 0
	global_load_dwordx4 v[156:159], v75, s[8:9]
	s_add_u32 s8, s8, 0x8000
	s_addc_u32 s9, s9, 0
	global_load_dwordx4 v[160:163], v75, s[8:9]
	s_add_u32 s8, s8, 0x8000
	s_addc_u32 s9, s9, 0
	global_load_dwordx4 v[164:167], v75, s[8:9]
	s_add_u32 s8, s8, 0x8000
	s_addc_u32 s9, s9, 0
	global_load_dwordx4 v[168:171], v75, s[8:9]
	s_add_u32 s8, s8, 0x8000
	s_addc_u32 s9, s9, 0
	global_load_dwordx4 v[172:175], v75, s[8:9]
	s_add_u32 s6, s40, 0x1800
	s_addc_u32 s7, s41, 0
	ds_read_b32 v226, v211
	ds_read_b32 v227, v211 offset:512
	ds_read_b32 v228, v211 offset:1024
	ds_read_b32 v229, v211 offset:1536
	ds_read_b32 v230, v211 offset:2048
	ds_read_b32 v231, v211 offset:2560
	ds_read_b32 v232, v211 offset:3072
	ds_read_b32 v233, v211 offset:3584
	ds_read_b32 v234, v211 offset:4096
	ds_read_b32 v235, v211 offset:4608
	ds_read_b32 v236, v211 offset:5120
	ds_read_b32 v237, v211 offset:5632
	ds_read_b32 v238, v211 offset:6144
	ds_read_b32 v239, v211 offset:6656
	ds_read_b32 v240, v211 offset:7168
	ds_read_b32 v241, v211 offset:7680
	s_waitcnt lgkmcnt(0)
	v_max_f32_e32 v226, v226, v226
	v_max_f32_e32 v227, v227, v227
	v_max_f32_e32 v228, v228, v228
	v_max_f32_e32 v229, v229, v229
	v_max_f32_e32 v230, v230, v230
	v_max_f32_e32 v231, v231, v231
	v_max_f32_e32 v232, v232, v232
	v_max_f32_e32 v233, v233, v233
	v_max_f32_e32 v234, v234, v234
	v_max_f32_e32 v235, v235, v235
	v_max_f32_e32 v236, v236, v236
	v_max_f32_e32 v237, v237, v237
	v_max_f32_e32 v238, v238, v238
	v_max_f32_e32 v239, v239, v239
	v_max_f32_e32 v240, v240, v240
	v_max_f32_e32 v241, v241, v241
	v_med3_f32 v226, v226, s62, v95
	v_med3_f32 v227, v227, s62, v95
	v_med3_f32 v228, v228, s62, v95
	v_med3_f32 v229, v229, s62, v95
	v_med3_f32 v230, v230, s62, v95
	v_med3_f32 v231, v231, s62, v95
	v_med3_f32 v232, v232, s62, v95
	v_med3_f32 v233, v233, s62, v95
	v_med3_f32 v234, v234, s62, v95
	v_med3_f32 v235, v235, s62, v95
	v_med3_f32 v236, v236, s62, v95
	v_med3_f32 v237, v237, s62, v95
	v_med3_f32 v238, v238, s62, v95
	v_med3_f32 v239, v239, s62, v95
	v_med3_f32 v240, v240, s62, v95
	v_med3_f32 v241, v241, s62, v95
	v_mov_b32_e32 v242, 0
	v_mov_b32_e32 v243, 0
	v_mov_b32_e32 v244, 0
	v_mov_b32_e32 v245, 0
	v_cvt_pk_fp8_f32 v242, v226, v227
	v_cvt_pk_fp8_f32 v243, v230, v231
	v_cvt_pk_fp8_f32 v244, v234, v235
	v_cvt_pk_fp8_f32 v245, v238, v239
	v_cvt_pk_fp8_f32 v242, v228, v229 op_sel:[0,0,1]
	v_cvt_pk_fp8_f32 v243, v232, v233 op_sel:[0,0,1]
	v_cvt_pk_fp8_f32 v244, v236, v237 op_sel:[0,0,1]
	v_cvt_pk_fp8_f32 v245, v240, v241 op_sel:[0,0,1]
	s_nop 0
	global_store_dwordx4 v79, v[242:245], s[6:7]
	ds_read_b32 v226, v213
	ds_read_b32 v227, v213 offset:512
	ds_read_b32 v228, v213 offset:1024
	ds_read_b32 v229, v213 offset:1536
	ds_read_b32 v230, v213 offset:2048
	ds_read_b32 v231, v213 offset:2560
	ds_read_b32 v232, v213 offset:3072
	ds_read_b32 v233, v213 offset:3584
	ds_read_b32 v234, v213 offset:4096
	ds_read_b32 v235, v213 offset:4608
	ds_read_b32 v236, v213 offset:5120
	ds_read_b32 v237, v213 offset:5632
	ds_read_b32 v238, v213 offset:6144
	ds_read_b32 v239, v213 offset:6656
	ds_read_b32 v240, v213 offset:7168
	ds_read_b32 v241, v213 offset:7680
	s_waitcnt lgkmcnt(0)
	v_max_f32_e32 v226, v226, v226
	v_max_f32_e32 v227, v227, v227
	v_max_f32_e32 v228, v228, v228
	v_max_f32_e32 v229, v229, v229
	v_max_f32_e32 v230, v230, v230
	v_max_f32_e32 v231, v231, v231
	v_max_f32_e32 v232, v232, v232
	v_max_f32_e32 v233, v233, v233
	v_max_f32_e32 v234, v234, v234
	v_max_f32_e32 v235, v235, v235
	v_max_f32_e32 v236, v236, v236
	v_max_f32_e32 v237, v237, v237
	v_max_f32_e32 v238, v238, v238
	v_max_f32_e32 v239, v239, v239
	v_max_f32_e32 v240, v240, v240
	v_max_f32_e32 v241, v241, v241
	v_med3_f32 v226, v226, s62, v95
	v_med3_f32 v227, v227, s62, v95
	v_med3_f32 v228, v228, s62, v95
	v_med3_f32 v229, v229, s62, v95
	v_med3_f32 v230, v230, s62, v95
	v_med3_f32 v231, v231, s62, v95
	v_med3_f32 v232, v232, s62, v95
	v_med3_f32 v233, v233, s62, v95
	v_med3_f32 v234, v234, s62, v95
	v_med3_f32 v235, v235, s62, v95
	v_med3_f32 v236, v236, s62, v95
	v_med3_f32 v237, v237, s62, v95
	v_med3_f32 v238, v238, s62, v95
	v_med3_f32 v239, v239, s62, v95
	v_med3_f32 v240, v240, s62, v95
	v_med3_f32 v241, v241, s62, v95
	v_mov_b32_e32 v242, 0
	v_mov_b32_e32 v243, 0
	v_mov_b32_e32 v244, 0
	v_mov_b32_e32 v245, 0
	v_cvt_pk_fp8_f32 v242, v226, v227
	v_cvt_pk_fp8_f32 v243, v230, v231
	v_cvt_pk_fp8_f32 v244, v234, v235
	v_cvt_pk_fp8_f32 v245, v238, v239
	v_cvt_pk_fp8_f32 v242, v228, v229 op_sel:[0,0,1]
	v_cvt_pk_fp8_f32 v243, v232, v233 op_sel:[0,0,1]
	v_cvt_pk_fp8_f32 v244, v236, v237 op_sel:[0,0,1]
	v_cvt_pk_fp8_f32 v245, v240, v241 op_sel:[0,0,1]
	s_nop 0
	global_store_dwordx4 v80, v[242:245], s[6:7]
	s_branch .Lco3_hop_skip

; #define GAS __attribute__((address_space(1)))
; #define LAS __attribute__((address_space(3)))
; #define LDS_WAIT() asm volatile("s_waitcnt lgkmcnt(0)" ::: "memory")
;     const int pr = item >> 1, kb = 2 * (pr / nblk) + (item & 1), nb = pr % nblk, k0 = 64 * kb, n0 = 32 * nb;
;     const int nr = n0 + (lane & 31); const int sc = MAP == 1 ? src_col_in(nr) : nr;
;     float v[32];
; #pragma unroll
;     for (int i = 0; i < 32; ++i) v[i] = sc >= 0 ? W[(size_t)(k0 + 2 * i + (lane >> 5)) * Nsrc + sc] : 0.f;
; #pragma unroll
;     for (int i = 0; i < 32; ++i) { const int k = k0 + 2 * i + (lane >> 5); float x = v[i] * wscale; if (KS) x *= (k < ksplit ? ksA[k] : ksB[k - ksplit]); scr[(2 * i + (lane >> 5)) * 33 + (lane & 31)] = x; }
;     LDS_WAIT(); asm volatile("" ::: "memory");
;     const int c = lane & 7;
; #pragma unroll
;     for (int j = 0; j < 4; ++j) { const int n = (lane >> 3) + 8 * j; const LAS float* s = scr + (8 * c) * 33 + n;
;         const unsigned long long o = (unsigned long long)pg8::pk4_fp8(s[0 * 33], s[1 * 33], s[2 * 33], s[3 * 33]) | ((unsigned long long)pg8::pk4_fp8(s[4 * 33], s[5 * 33], s[6 * 33], s[7 * 33]) << 32);
;         *(GAS unsigned long long*)(WT + (size_t)(n0 + n) * K + k0 + 8 * c) = o; }
;     LDS_WAIT(); asm volatile("" ::: "memory");
.Lco3_hop_skip:
	s_waitcnt vmcnt(12)
	v_mul_f32_e32 v176, 0x43000000, v176
	v_mul_f32_e32 v177, 0x43000000, v177
	v_mul_f32_e32 v178, 0x43000000, v178
	v_mul_f32_e32 v179, 0x43000000, v179
	ds_write_b128 v210, v[176:179]
	v_mul_f32_e32 v180, 0x43000000, v180
	v_mul_f32_e32 v181, 0x43000000, v181
	v_mul_f32_e32 v182, 0x43000000, v182
	v_mul_f32_e32 v183, 0x43000000, v183
	ds_write_b128 v210, v[180:183] offset:1024
	v_mul_f32_e32 v184, 0x43000000, v184
	v_mul_f32_e32 v185, 0x43000000, v185
	v_mul_f32_e32 v186, 0x43000000, v186
	v_mul_f32_e32 v187, 0x43000000, v187
	ds_write_b128 v210, v[184:187] offset:2048
	v_mul_f32_e32 v188, 0x43000000, v188
	v_mul_f32_e32 v189, 0x43000000, v189
	v_mul_f32_e32 v190, 0x43000000, v190
	v_mul_f32_e32 v191, 0x43000000, v191
	ds_write_b128 v210, v[188:191] offset:3072
	v_mul_f32_e32 v192, 0x43000000, v192
	v_mul_f32_e32 v193, 0x43000000, v193
	v_mul_f32_e32 v194, 0x43000000, v194
	v_mul_f32_e32 v195, 0x43000000, v195
	ds_write_b128 v210, v[192:195] offset:4096
	v_mul_f32_e32 v196, 0x43000000, v196
	v_mul_f32_e32 v197, 0x43000000, v197
	v_mul_f32_e32 v198, 0x43000000, v198
	v_mul_f32_e32 v199, 0x43000000, v199
	ds_write_b128 v210, v[196:199] offset:5120
	v_mul_f32_e32 v200, 0x43000000, v200
	v_mul_f32_e32 v201, 0x43000000, v201
	v_mul_f32_e32 v202, 0x43000000, v202
	v_mul_f32_e32 v203, 0x43000000, v203
	ds_write_b128 v210, v[200:203] offset:6144
	v_mul_f32_e32 v204, 0x43000000, v204
	v_mul_f32_e32 v205, 0x43000000, v205
	v_mul_f32_e32 v206, 0x43000000, v206
	v_mul_f32_e32 v207, 0x43000000, v207
	ds_write_b128 v210, v[204:207] offset:7168
	s_waitcnt lgkmcnt(0)
	s_barrier
	s_add_u32 s8, s38, 0x9000000
	s_addc_u32 s9, s39, 0
	global_load_dwordx4 v[176:179], v75, s[8:9]
	s_add_u32 s8, s8, 0x8000
	s_addc_u32 s9, s9, 0
	global_load_dwordx4 v[180:183], v75, s[8:9]
	s_add_u32 s8, s8, 0x8000
	s_addc_u32 s9, s9, 0
	global_load_dwordx4 v[184:187], v75, s[8:9]
	s_add_u32 s8, s8, 0x8000
	s_addc_u32 s9, s9, 0
	global_load_dwordx4 v[188:191], v75, s[8:9]
	s_add_u32 s8, s8, 0x8000
	s_addc_u32 s9, s9, 0
	global_load_dwordx4 v[192:195], v75, s[8:9]
	s_add_u32 s8, s8, 0x8000
	s_addc_u32 s9, s9, 0
	global_load_dwordx4 v[196:199], v75, s[8:9]
	s_add_u32 s8, s8, 0x8000
	s_addc_u32 s9, s9, 0
	global_load_dwordx4 v[200:203], v75, s[8:9]
	s_add_u32 s8, s8, 0x8000
	s_addc_u32 s9, s9, 0
	global_load_dwordx4 v[204:207], v75, s[8:9]
	s_add_u32 s6, s40, 0x1c00
	s_addc_u32 s7, s41, 0
	ds_read_b32 v226, v212
	ds_read_b32 v227, v212 offset:512
	ds_read_b32 v228, v212 offset:1024
	ds_read_b32 v229, v212 offset:1536
	ds_read_b32 v230, v212 offset:2048
	ds_read_b32 v231, v212 offset:2560
	ds_read_b32 v232, v212 offset:3072
	ds_read_b32 v233, v212 offset:3584
	ds_read_b32 v234, v212 offset:4096
	ds_read_b32 v235, v212 offset:4608
	ds_read_b32 v236, v212 offset:5120
	ds_read_b32 v237, v212 offset:5632
	ds_read_b32 v238, v212 offset:6144
	ds_read_b32 v239, v212 offset:6656
	ds_read_b32 v240, v212 offset:7168
	ds_read_b32 v241, v212 offset:7680
	s_waitcnt lgkmcnt(0)
	v_max_f32_e32 v226, v226, v226
	v_max_f32_e32 v227, v227, v227
	v_max_f32_e32 v228, v228, v228
	v_max_f32_e32 v229, v229, v229
	v_max_f32_e32 v230, v230, v230
	v_max_f32_e32 v231, v231, v231
	v_max_f32_e32 v232, v232, v232
	v_max_f32_e32 v233, v233, v233
	v_max_f32_e32 v234, v234, v234
	v_max_f32_e32 v235, v235, v235
	v_max_f32_e32 v236, v236, v236
	v_max_f32_e32 v237, v237, v237
	v_max_f32_e32 v238, v238, v238
	v_max_f32_e32 v239, v239, v239
	v_max_f32_e32 v240, v240, v240
	v_max_f32_e32 v241, v241, v241
	v_med3_f32 v226, v226, s62, v95
	v_med3_f32 v227, v227, s62, v95
	v_med3_f32 v228, v228, s62, v95
	v_med3_f32 v229, v229, s62, v95
	v_med3_f32 v230, v230, s62, v95
	v_med3_f32 v231, v231, s62, v95
	v_med3_f32 v232, v232, s62, v95
	v_med3_f32 v233, v233, s62, v95
	v_med3_f32 v234, v234, s62, v95
	v_med3_f32 v235, v235, s62, v95
	v_med3_f32 v236, v236, s62, v95
	v_med3_f32 v237, v237, s62, v95
	v_med3_f32 v238, v238, s62, v95
	v_med3_f32 v239, v239, s62, v95
	v_med3_f32 v240, v240, s62, v95
	v_med3_f32 v241, v241, s62, v95
	v_mov_b32_e32 v242, 0
	v_mov_b32_e32 v243, 0
	v_mov_b32_e32 v244, 0
	v_mov_b32_e32 v245, 0
	v_cvt_pk_fp8_f32 v242, v226, v227
	v_cvt_pk_fp8_f32 v243, v230, v231
	v_cvt_pk_fp8_f32 v244, v234, v235
	v_cvt_pk_fp8_f32 v245, v238, v239
	v_cvt_pk_fp8_f32 v242, v228, v229 op_sel:[0,0,1]
	v_cvt_pk_fp8_f32 v243, v232, v233 op_sel:[0,0,1]
	v_cvt_pk_fp8_f32 v244, v236, v237 op_sel:[0,0,1]
	v_cvt_pk_fp8_f32 v245, v240, v241 op_sel:[0,0,1]
	s_nop 0
	global_store_dwordx4 v79, v[242:245], s[6:7]
	ds_read_b32 v226, v214
	ds_read_b32 v227, v214 offset:512
	ds_read_b32 v228, v214 offset:1024
	ds_read_b32 v229, v214 offset:1536
	ds_read_b32 v230, v214 offset:2048
	ds_read_b32 v231, v214 offset:2560
	ds_read_b32 v232, v214 offset:3072
	ds_read_b32 v233, v214 offset:3584
	ds_read_b32 v234, v214 offset:4096
	ds_read_b32 v235, v214 offset:4608
	ds_read_b32 v236, v214 offset:5120
	ds_read_b32 v237, v214 offset:5632
	ds_read_b32 v238, v214 offset:6144
	ds_read_b32 v239, v214 offset:6656
	ds_read_b32 v240, v214 offset:7168
	ds_read_b32 v241, v214 offset:7680
	s_waitcnt lgkmcnt(0)
; #define GAS __attribute__((address_space(1)))
; #define LAS __attribute__((address_space(3)))
; #define LDS_WAIT() asm volatile("s_waitcnt lgkmcnt(0)" ::: "memory")
;     const int pr = item >> 1, kb = 2 * (pr / nblk) + (item & 1), nb = pr % nblk, k0 = 64 * kb, n0 = 32 * nb;
;     const int nr = n0 + (lane & 31); const int sc = MAP == 1 ? src_col_in(nr) : nr;
;     float v[32];
; #pragma unroll
;     for (int i = 0; i < 32; ++i) v[i] = sc >= 0 ? W[(size_t)(k0 + 2 * i + (lane >> 5)) * Nsrc + sc] : 0.f;
; #pragma unroll
;     for (int i = 0; i < 32; ++i) { const int k = k0 + 2 * i + (lane >> 5); float x = v[i] * wscale; if (KS) x *= (k < ksplit ? ksA[k] : ksB[k - ksplit]); scr[(2 * i + (lane >> 5)) * 33 + (lane & 31)] = x; }
;     LDS_WAIT(); asm volatile("" ::: "memory");
;     const int c = lane & 7;
; #pragma unroll
;     for (int j = 0; j < 4; ++j) { const int n = (lane >> 3) + 8 * j; const LAS float* s = scr + (8 * c) * 33 + n;
;         const unsigned long long o = (unsigned long long)pg8::pk4_fp8(s[0 * 33], s[1 * 33], s[2 * 33], s[3 * 33]) | ((unsigned long long)pg8::pk4_fp8(s[4 * 33], s[5 * 33], s[6 * 33], s[7 * 33]) << 32);
;         *(GAS unsigned long long*)(WT + (size_t)(n0 + n) * K + k0 + 8 * c) = o; }
;     LDS_WAIT(); asm volatile("" ::: "memory");
	v_max_f32_e32 v226, v226, v226
	v_max_f32_e32 v227, v227, v227
	v_max_f32_e32 v228, v228, v228
	v_max_f32_e32 v229, v229, v229
	v_max_f32_e32 v230, v230, v230
	v_max_f32_e32 v231, v231, v231
	v_max_f32_e32 v232, v232, v232
	v_max_f32_e32 v233, v233, v233
	v_max_f32_e32 v234, v234, v234
	v_max_f32_e32 v235, v235, v235
	v_max_f32_e32 v236, v236, v236
	v_max_f32_e32 v237, v237, v237
	v_max_f32_e32 v238, v238, v238
	v_max_f32_e32 v239, v239, v239
	v_max_f32_e32 v240, v240, v240
	v_max_f32_e32 v241, v241, v241
	v_med3_f32 v226, v226, s62, v95
	v_med3_f32 v227, v227, s62, v95
	v_med3_f32 v228, v228, s62, v95
	v_med3_f32 v229, v229, s62, v95
	v_med3_f32 v230, v230, s62, v95
	v_med3_f32 v231, v231, s62, v95
	v_med3_f32 v232, v232, s62, v95
	v_med3_f32 v233, v233, s62, v95
	v_med3_f32 v234, v234, s62, v95
	v_med3_f32 v235, v235, s62, v95
	v_med3_f32 v236, v236, s62, v95
	v_med3_f32 v237, v237, s62, v95
	v_med3_f32 v238, v238, s62, v95
	v_med3_f32 v239, v239, s62, v95
	v_med3_f32 v240, v240, s62, v95
	v_med3_f32 v241, v241, s62, v95
	v_mov_b32_e32 v242, 0
	v_mov_b32_e32 v243, 0
	v_mov_b32_e32 v244, 0
	v_mov_b32_e32 v245, 0
	v_cvt_pk_fp8_f32 v242, v226, v227
	v_cvt_pk_fp8_f32 v243, v230, v231
	v_cvt_pk_fp8_f32 v244, v234, v235
	v_cvt_pk_fp8_f32 v245, v238, v239
	v_cvt_pk_fp8_f32 v242, v228, v229 op_sel:[0,0,1]
	v_cvt_pk_fp8_f32 v243, v232, v233 op_sel:[0,0,1]
	v_cvt_pk_fp8_f32 v244, v236, v237 op_sel:[0,0,1]
	v_cvt_pk_fp8_f32 v245, v240, v241 op_sel:[0,0,1]
	s_nop 0
	global_store_dwordx4 v80, v[242:245], s[6:7]
	s_waitcnt vmcnt(12)
	v_mul_f32_e32 v144, 0x43000000, v144
	v_mul_f32_e32 v145, 0x43000000, v145
	v_mul_f32_e32 v146, 0x43000000, v146
	v_mul_f32_e32 v147, 0x43000000, v147
	ds_write_b128 v209, v[144:147]
	v_mul_f32_e32 v148, 0x43000000, v148
	v_mul_f32_e32 v149, 0x43000000, v149
	v_mul_f32_e32 v150, 0x43000000, v150
	v_mul_f32_e32 v151, 0x43000000, v151
	ds_write_b128 v209, v[148:151] offset:1024
	v_mul_f32_e32 v152, 0x43000000, v152
	v_mul_f32_e32 v153, 0x43000000, v153
	v_mul_f32_e32 v154, 0x43000000, v154
	v_mul_f32_e32 v155, 0x43000000, v155
	ds_write_b128 v209, v[152:155] offset:2048
	v_mul_f32_e32 v156, 0x43000000, v156
	v_mul_f32_e32 v157, 0x43000000, v157
	v_mul_f32_e32 v158, 0x43000000, v158
	v_mul_f32_e32 v159, 0x43000000, v159
	ds_write_b128 v209, v[156:159] offset:3072
	v_mul_f32_e32 v160, 0x43000000, v160
	v_mul_f32_e32 v161, 0x43000000, v161
	v_mul_f32_e32 v162, 0x43000000, v162
	v_mul_f32_e32 v163, 0x43000000, v163
	ds_write_b128 v209, v[160:163] offset:4096
	v_mul_f32_e32 v164, 0x43000000, v164
	v_mul_f32_e32 v165, 0x43000000, v165
	v_mul_f32_e32 v166, 0x43000000, v166
	v_mul_f32_e32 v167, 0x43000000, v167
	ds_write_b128 v209, v[164:167] offset:5120
	v_mul_f32_e32 v168, 0x43000000, v168
	v_mul_f32_e32 v169, 0x43000000, v169
	v_mul_f32_e32 v170, 0x43000000, v170
	v_mul_f32_e32 v171, 0x43000000, v171
	ds_write_b128 v209, v[168:171] offset:6144
	v_mul_f32_e32 v172, 0x43000000, v172
	v_mul_f32_e32 v173, 0x43000000, v173
	v_mul_f32_e32 v174, 0x43000000, v174
	v_mul_f32_e32 v175, 0x43000000, v175
	ds_write_b128 v209, v[172:175] offset:7168
	s_waitcnt lgkmcnt(0)
	s_barrier
	s_add_u32 s8, s38, 0xa000000
	s_addc_u32 s9, s39, 0
	global_load_dwordx4 v[144:147], v75, s[8:9]
	s_add_u32 s8, s8, 0x8000
	s_addc_u32 s9, s9, 0
	global_load_dwordx4 v[148:151], v75, s[8:9]
	s_add_u32 s8, s8, 0x8000
	s_addc_u32 s9, s9, 0
	global_load_dwordx4 v[152:155], v75, s[8:9]
	s_add_u32 s8, s8, 0x8000
	s_addc_u32 s9, s9, 0
	global_load_dwordx4 v[156:159], v75, s[8:9]
	s_add_u32 s8, s8, 0x8000
	s_addc_u32 s9, s9, 0
	global_load_dwordx4 v[160:163], v75, s[8:9]
	s_add_u32 s8, s8, 0x8000
	s_addc_u32 s9, s9, 0
	global_load_dwordx4 v[164:167], v75, s[8:9]
	s_add_u32 s8, s8, 0x8000
	s_addc_u32 s9, s9, 0
	global_load_dwordx4 v[168:171], v75, s[8:9]
	s_add_u32 s8, s8, 0x8000
	s_addc_u32 s9, s9, 0
	global_load_dwordx4 v[172:175], v75, s[8:9]
	s_add_u32 s6, s40, 0x2000
	s_addc_u32 s7, s41, 0
	ds_read_b32 v226, v211
	ds_read_b32 v227, v211 offset:512
	ds_read_b32 v228, v211 offset:1024
	ds_read_b32 v229, v211 offset:1536
	ds_read_b32 v230, v211 offset:2048
	ds_read_b32 v231, v211 offset:2560
	ds_read_b32 v232, v211 offset:3072
	ds_read_b32 v233, v211 offset:3584
	ds_read_b32 v234, v211 offset:4096
	ds_read_b32 v235, v211 offset:4608
	ds_read_b32 v236, v211 offset:5120
	ds_read_b32 v237, v211 offset:5632
	ds_read_b32 v238, v211 offset:6144
	ds_read_b32 v239, v211 offset:6656
	ds_read_b32 v240, v211 offset:7168
	ds_read_b32 v241, v211 offset:7680
	s_waitcnt lgkmcnt(0)
	v_max_f32_e32 v226, v226, v226
	v_max_f32_e32 v227, v227, v227
	v_max_f32_e32 v228, v228, v228
	v_max_f32_e32 v229, v229, v229
	v_max_f32_e32 v230, v230, v230
	v_max_f32_e32 v231, v231, v231
	v_max_f32_e32 v232, v232, v232
	v_max_f32_e32 v233, v233, v233
	v_max_f32_e32 v234, v234, v234
	v_max_f32_e32 v235, v235, v235
	v_max_f32_e32 v236, v236, v236
	v_max_f32_e32 v237, v237, v237
	v_max_f32_e32 v238, v238, v238
	v_max_f32_e32 v239, v239, v239
	v_max_f32_e32 v240, v240, v240
	v_max_f32_e32 v241, v241, v241
	v_med3_f32 v226, v226, s62, v95
	v_med3_f32 v227, v227, s62, v95
	v_med3_f32 v228, v228, s62, v95
	v_med3_f32 v229, v229, s62, v95
	v_med3_f32 v230, v230, s62, v95
	v_med3_f32 v231, v231, s62, v95
	v_med3_f32 v232, v232, s62, v95
	v_med3_f32 v233, v233, s62, v95
	v_med3_f32 v234, v234, s62, v95
	v_med3_f32 v235, v235, s62, v95
	v_med3_f32 v236, v236, s62, v95
	v_med3_f32 v237, v237, s62, v95
	v_med3_f32 v238, v238, s62, v95
	v_med3_f32 v239, v239, s62, v95
	v_med3_f32 v240, v240, s62, v95
	v_med3_f32 v241, v241, s62, v95
	v_mov_b32_e32 v242, 0
	v_mov_b32_e32 v243, 0
	v_mov_b32_e32 v244, 0
	v_mov_b32_e32 v245, 0
	v_cvt_pk_fp8_f32 v242, v226, v227
	v_cvt_pk_fp8_f32 v243, v230, v231
	v_cvt_pk_fp8_f32 v244, v234, v235
	v_cvt_pk_fp8_f32 v245, v238, v239
	v_cvt_pk_fp8_f32 v242, v228, v229 op_sel:[0,0,1]
	v_cvt_pk_fp8_f32 v243, v232, v233 op_sel:[0,0,1]
	v_cvt_pk_fp8_f32 v244, v236, v237 op_sel:[0,0,1]
	v_cvt_pk_fp8_f32 v245, v240, v241 op_sel:[0,0,1]
	s_nop 0
	global_store_dwordx4 v79, v[242:245], s[6:7]
	ds_read_b32 v226, v213
	ds_read_b32 v227, v213 offset:512
	ds_read_b32 v228, v213 offset:1024
	ds_read_b32 v229, v213 offset:1536
	ds_read_b32 v230, v213 offset:2048
	ds_read_b32 v231, v213 offset:2560
	ds_read_b32 v232, v213 offset:3072
	ds_read_b32 v233, v213 offset:3584
	ds_read_b32 v234, v213 offset:4096
	ds_read_b32 v235, v213 offset:4608
	ds_read_b32 v236, v213 offset:5120
	ds_read_b32 v237, v213 offset:5632
	ds_read_b32 v238, v213 offset:6144
	ds_read_b32 v239, v213 offset:6656
	ds_read_b32 v240, v213 offset:7168
	ds_read_b32 v241, v213 offset:7680
	s_waitcnt lgkmcnt(0)
; #define GAS __attribute__((address_space(1)))
; #define LAS __attribute__((address_space(3)))
; #define LDS_WAIT() asm volatile("s_waitcnt lgkmcnt(0)" ::: "memory")
;     const int pr = item >> 1, kb = 2 * (pr / nblk) + (item & 1), nb = pr % nblk, k0 = 64 * kb, n0 = 32 * nb;
;     const int nr = n0 + (lane & 31); const int sc = MAP == 1 ? src_col_in(nr) : nr;
;     float v[32];
; #pragma unroll
;     for (int i = 0; i < 32; ++i) v[i] = sc >= 0 ? W[(size_t)(k0 + 2 * i + (lane >> 5)) * Nsrc + sc] : 0.f;
; #pragma unroll
;     for (int i = 0; i < 32; ++i) { const int k = k0 + 2 * i + (lane >> 5); float x = v[i] * wscale; if (KS) x *= (k < ksplit ? ksA[k] : ksB[k - ksplit]); scr[(2 * i + (lane >> 5)) * 33 + (lane & 31)] = x; }
;     LDS_WAIT(); asm volatile("" ::: "memory");
;     const int c = lane & 7;
; #pragma unroll
;     for (int j = 0; j < 4; ++j) { const int n = (lane >> 3) + 8 * j; const LAS float* s = scr + (8 * c) * 33 + n;
;         const unsigned long long o = (unsigned long long)pg8::pk4_fp8(s[0 * 33], s[1 * 33], s[2 * 33], s[3 * 33]) | ((unsigned long long)pg8::pk4_fp8(s[4 * 33], s[5 * 33], s[6 * 33], s[7 * 33]) << 32);
;         *(GAS unsigned long long*)(WT + (size_t)(n0 + n) * K + k0 + 8 * c) = o; }
;     LDS_WAIT(); asm volatile("" ::: "memory");
	v_max_f32_e32 v226, v226, v226
	v_max_f32_e32 v227, v227, v227
	v_max_f32_e32 v228, v228, v228
	v_max_f32_e32 v229, v229, v229
	v_max_f32_e32 v230, v230, v230
	v_max_f32_e32 v231, v231, v231
	v_max_f32_e32 v232, v232, v232
	v_max_f32_e32 v233, v233, v233
	v_max_f32_e32 v234, v234, v234
	v_max_f32_e32 v235, v235, v235
	v_max_f32_e32 v236, v236, v236
	v_max_f32_e32 v237, v237, v237
	v_max_f32_e32 v238, v238, v238
	v_max_f32_e32 v239, v239, v239
	v_max_f32_e32 v240, v240, v240
	v_max_f32_e32 v241, v241, v241
	v_med3_f32 v226, v226, s62, v95
	v_med3_f32 v227, v227, s62, v95
	v_med3_f32 v228, v228, s62, v95
	v_med3_f32 v229, v229, s62, v95
	v_med3_f32 v230, v230, s62, v95
	v_med3_f32 v231, v231, s62, v95
	v_med3_f32 v232, v232, s62, v95
	v_med3_f32 v233, v233, s62, v95
	v_med3_f32 v234, v234, s62, v95
	v_med3_f32 v235, v235, s62, v95
	v_med3_f32 v236, v236, s62, v95
	v_med3_f32 v237, v237, s62, v95
	v_med3_f32 v238, v238, s62, v95
	v_med3_f32 v239, v239, s62, v95
	v_med3_f32 v240, v240, s62, v95
	v_med3_f32 v241, v241, s62, v95
	v_mov_b32_e32 v242, 0
	v_mov_b32_e32 v243, 0
	v_mov_b32_e32 v244, 0
	v_mov_b32_e32 v245, 0
	v_cvt_pk_fp8_f32 v242, v226, v227
	v_cvt_pk_fp8_f32 v243, v230, v231
	v_cvt_pk_fp8_f32 v244, v234, v235
	v_cvt_pk_fp8_f32 v245, v238, v239
	v_cvt_pk_fp8_f32 v242, v228, v229 op_sel:[0,0,1]
	v_cvt_pk_fp8_f32 v243, v232, v233 op_sel:[0,0,1]
	v_cvt_pk_fp8_f32 v244, v236, v237 op_sel:[0,0,1]
	v_cvt_pk_fp8_f32 v245, v240, v241 op_sel:[0,0,1]
	s_nop 0
	global_store_dwordx4 v80, v[242:245], s[6:7]
	s_waitcnt vmcnt(12)
	v_mul_f32_e32 v176, 0x43000000, v176
	v_mul_f32_e32 v177, 0x43000000, v177
	v_mul_f32_e32 v178, 0x43000000, v178
	v_mul_f32_e32 v179, 0x43000000, v179
	ds_write_b128 v210, v[176:179]
	v_mul_f32_e32 v180, 0x43000000, v180
	v_mul_f32_e32 v181, 0x43000000, v181
	v_mul_f32_e32 v182, 0x43000000, v182
	v_mul_f32_e32 v183, 0x43000000, v183
	ds_write_b128 v210, v[180:183] offset:1024
	v_mul_f32_e32 v184, 0x43000000, v184
	v_mul_f32_e32 v185, 0x43000000, v185
	v_mul_f32_e32 v186, 0x43000000, v186
	v_mul_f32_e32 v187, 0x43000000, v187
	ds_write_b128 v210, v[184:187] offset:2048
	v_mul_f32_e32 v188, 0x43000000, v188
	v_mul_f32_e32 v189, 0x43000000, v189
	v_mul_f32_e32 v190, 0x43000000, v190
	v_mul_f32_e32 v191, 0x43000000, v191
	ds_write_b128 v210, v[188:191] offset:3072
	v_mul_f32_e32 v192, 0x43000000, v192
	v_mul_f32_e32 v193, 0x43000000, v193
	v_mul_f32_e32 v194, 0x43000000, v194
	v_mul_f32_e32 v195, 0x43000000, v195
	ds_write_b128 v210, v[192:195] offset:4096
	v_mul_f32_e32 v196, 0x43000000, v196
	v_mul_f32_e32 v197, 0x43000000, v197
	v_mul_f32_e32 v198, 0x43000000, v198
	v_mul_f32_e32 v199, 0x43000000, v199
	ds_write_b128 v210, v[196:199] offset:5120
	v_mul_f32_e32 v200, 0x43000000, v200
	v_mul_f32_e32 v201, 0x43000000, v201
	v_mul_f32_e32 v202, 0x43000000, v202
	v_mul_f32_e32 v203, 0x43000000, v203
	ds_write_b128 v210, v[200:203] offset:6144
	v_mul_f32_e32 v204, 0x43000000, v204
	v_mul_f32_e32 v205, 0x43000000, v205
	v_mul_f32_e32 v206, 0x43000000, v206
	v_mul_f32_e32 v207, 0x43000000, v207
	ds_write_b128 v210, v[204:207] offset:7168
	s_waitcnt lgkmcnt(0)
	s_barrier
	s_add_u32 s8, s38, 0xb000000
	s_addc_u32 s9, s39, 0
	global_load_dwordx4 v[176:179], v75, s[8:9]
	s_add_u32 s8, s8, 0x8000
	s_addc_u32 s9, s9, 0
	global_load_dwordx4 v[180:183], v75, s[8:9]
	s_add_u32 s8, s8, 0x8000
	s_addc_u32 s9, s9, 0
	global_load_dwordx4 v[184:187], v75, s[8:9]
	s_add_u32 s8, s8, 0x8000
	s_addc_u32 s9, s9, 0
	global_load_dwordx4 v[188:191], v75, s[8:9]
	s_add_u32 s8, s8, 0x8000
	s_addc_u32 s9, s9, 0
	global_load_dwordx4 v[192:195], v75, s[8:9]
	s_add_u32 s8, s8, 0x8000
	s_addc_u32 s9, s9, 0
	global_load_dwordx4 v[196:199], v75, s[8:9]
	s_add_u32 s8, s8, 0x8000
	s_addc_u32 s9, s9, 0
	global_load_dwordx4 v[200:203], v75, s[8:9]
	s_add_u32 s8, s8, 0x8000
	s_addc_u32 s9, s9, 0
	global_load_dwordx4 v[204:207], v75, s[8:9]
	s_add_u32 s6, s40, 0x2400
	s_addc_u32 s7, s41, 0
	ds_read_b32 v226, v212
	ds_read_b32 v227, v212 offset:512
	ds_read_b32 v228, v212 offset:1024
	ds_read_b32 v229, v212 offset:1536
	ds_read_b32 v230, v212 offset:2048
	ds_read_b32 v231, v212 offset:2560
	ds_read_b32 v232, v212 offset:3072
	ds_read_b32 v233, v212 offset:3584
	ds_read_b32 v234, v212 offset:4096
	ds_read_b32 v235, v212 offset:4608
	ds_read_b32 v236, v212 offset:5120
	ds_read_b32 v237, v212 offset:5632
	ds_read_b32 v238, v212 offset:6144
	ds_read_b32 v239, v212 offset:6656
	ds_read_b32 v240, v212 offset:7168
	ds_read_b32 v241, v212 offset:7680
	s_waitcnt lgkmcnt(0)
	v_max_f32_e32 v226, v226, v226
	v_max_f32_e32 v227, v227, v227
	v_max_f32_e32 v228, v228, v228
	v_max_f32_e32 v229, v229, v229
	v_max_f32_e32 v230, v230, v230
	v_max_f32_e32 v231, v231, v231
	v_max_f32_e32 v232, v232, v232
	v_max_f32_e32 v233, v233, v233
	v_max_f32_e32 v234, v234, v234
	v_max_f32_e32 v235, v235, v235
	v_max_f32_e32 v236, v236, v236
	v_max_f32_e32 v237, v237, v237
	v_max_f32_e32 v238, v238, v238
	v_max_f32_e32 v239, v239, v239
	v_max_f32_e32 v240, v240, v240
	v_max_f32_e32 v241, v241, v241
	v_med3_f32 v226, v226, s62, v95
	v_med3_f32 v227, v227, s62, v95
	v_med3_f32 v228, v228, s62, v95
	v_med3_f32 v229, v229, s62, v95
	v_med3_f32 v230, v230, s62, v95
	v_med3_f32 v231, v231, s62, v95
	v_med3_f32 v232, v232, s62, v95
	v_med3_f32 v233, v233, s62, v95
	v_med3_f32 v234, v234, s62, v95
	v_med3_f32 v235, v235, s62, v95
	v_med3_f32 v236, v236, s62, v95
	v_med3_f32 v237, v237, s62, v95
	v_med3_f32 v238, v238, s62, v95
	v_med3_f32 v239, v239, s62, v95
	v_med3_f32 v240, v240, s62, v95
	v_med3_f32 v241, v241, s62, v95
	v_mov_b32_e32 v242, 0
	v_mov_b32_e32 v243, 0
	v_mov_b32_e32 v244, 0
	v_mov_b32_e32 v245, 0
	v_cvt_pk_fp8_f32 v242, v226, v227
	v_cvt_pk_fp8_f32 v243, v230, v231
	v_cvt_pk_fp8_f32 v244, v234, v235
	v_cvt_pk_fp8_f32 v245, v238, v239
	v_cvt_pk_fp8_f32 v242, v228, v229 op_sel:[0,0,1]
	v_cvt_pk_fp8_f32 v243, v232, v233 op_sel:[0,0,1]
	v_cvt_pk_fp8_f32 v244, v236, v237 op_sel:[0,0,1]
	v_cvt_pk_fp8_f32 v245, v240, v241 op_sel:[0,0,1]
	s_nop 0
	global_store_dwordx4 v79, v[242:245], s[6:7]
	ds_read_b32 v226, v214
	ds_read_b32 v227, v214 offset:512
	ds_read_b32 v228, v214 offset:1024
	ds_read_b32 v229, v214 offset:1536
	ds_read_b32 v230, v214 offset:2048
	ds_read_b32 v231, v214 offset:2560
	ds_read_b32 v232, v214 offset:3072
	ds_read_b32 v233, v214 offset:3584
	ds_read_b32 v234, v214 offset:4096
	ds_read_b32 v235, v214 offset:4608
	ds_read_b32 v236, v214 offset:5120
	ds_read_b32 v237, v214 offset:5632
	ds_read_b32 v238, v214 offset:6144
	ds_read_b32 v239, v214 offset:6656
	ds_read_b32 v240, v214 offset:7168
	ds_read_b32 v241, v214 offset:7680
	s_waitcnt lgkmcnt(0)
; #define GAS __attribute__((address_space(1)))
; #define LAS __attribute__((address_space(3)))
; #define LDS_WAIT() asm volatile("s_waitcnt lgkmcnt(0)" ::: "memory")
;     const int pr = item >> 1, kb = 2 * (pr / nblk) + (item & 1), nb = pr % nblk, k0 = 64 * kb, n0 = 32 * nb;
;     const int nr = n0 + (lane & 31); const int sc = MAP == 1 ? src_col_in(nr) : nr;
;     float v[32];
; #pragma unroll
;     for (int i = 0; i < 32; ++i) v[i] = sc >= 0 ? W[(size_t)(k0 + 2 * i + (lane >> 5)) * Nsrc + sc] : 0.f;
; #pragma unroll
;     for (int i = 0; i < 32; ++i) { const int k = k0 + 2 * i + (lane >> 5); float x = v[i] * wscale; if (KS) x *= (k < ksplit ? ksA[k] : ksB[k - ksplit]); scr[(2 * i + (lane >> 5)) * 33 + (lane & 31)] = x; }
;     LDS_WAIT(); asm volatile("" ::: "memory");
;     const int c = lane & 7;
; #pragma unroll
;     for (int j = 0; j < 4; ++j) { const int n = (lane >> 3) + 8 * j; const LAS float* s = scr + (8 * c) * 33 + n;
;         const unsigned long long o = (unsigned long long)pg8::pk4_fp8(s[0 * 33], s[1 * 33], s[2 * 33], s[3 * 33]) | ((unsigned long long)pg8::pk4_fp8(s[4 * 33], s[5 * 33], s[6 * 33], s[7 * 33]) << 32);
;         *(GAS unsigned long long*)(WT + (size_t)(n0 + n) * K + k0 + 8 * c) = o; }
;     LDS_WAIT(); asm volatile("" ::: "memory");
	v_max_f32_e32 v226, v226, v226
	v_max_f32_e32 v227, v227, v227
	v_max_f32_e32 v228, v228, v228
	v_max_f32_e32 v229, v229, v229
	v_max_f32_e32 v230, v230, v230
	v_max_f32_e32 v231, v231, v231
	v_max_f32_e32 v232, v232, v232
	v_max_f32_e32 v233, v233, v233
	v_max_f32_e32 v234, v234, v234
	v_max_f32_e32 v235, v235, v235
	v_max_f32_e32 v236, v236, v236
	v_max_f32_e32 v237, v237, v237
	v_max_f32_e32 v238, v238, v238
	v_max_f32_e32 v239, v239, v239
	v_max_f32_e32 v240, v240, v240
	v_max_f32_e32 v241, v241, v241
	v_med3_f32 v226, v226, s62, v95
	v_med3_f32 v227, v227, s62, v95
	v_med3_f32 v228, v228, s62, v95
	v_med3_f32 v229, v229, s62, v95
	v_med3_f32 v230, v230, s62, v95
	v_med3_f32 v231, v231, s62, v95
	v_med3_f32 v232, v232, s62, v95
	v_med3_f32 v233, v233, s62, v95
	v_med3_f32 v234, v234, s62, v95
	v_med3_f32 v235, v235, s62, v95
	v_med3_f32 v236, v236, s62, v95
	v_med3_f32 v237, v237, s62, v95
	v_med3_f32 v238, v238, s62, v95
	v_med3_f32 v239, v239, s62, v95
	v_med3_f32 v240, v240, s62, v95
	v_med3_f32 v241, v241, s62, v95
	v_mov_b32_e32 v242, 0
	v_mov_b32_e32 v243, 0
	v_mov_b32_e32 v244, 0
	v_mov_b32_e32 v245, 0
	v_cvt_pk_fp8_f32 v242, v226, v227
	v_cvt_pk_fp8_f32 v243, v230, v231
	v_cvt_pk_fp8_f32 v244, v234, v235
	v_cvt_pk_fp8_f32 v245, v238, v239
	v_cvt_pk_fp8_f32 v242, v228, v229 op_sel:[0,0,1]
	v_cvt_pk_fp8_f32 v243, v232, v233 op_sel:[0,0,1]
	v_cvt_pk_fp8_f32 v244, v236, v237 op_sel:[0,0,1]
	v_cvt_pk_fp8_f32 v245, v240, v241 op_sel:[0,0,1]
	s_nop 0
	global_store_dwordx4 v80, v[242:245], s[6:7]
	s_waitcnt vmcnt(12)
	v_mul_f32_e32 v144, 0x43000000, v144
	v_mul_f32_e32 v145, 0x43000000, v145
	v_mul_f32_e32 v146, 0x43000000, v146
	v_mul_f32_e32 v147, 0x43000000, v147
	ds_write_b128 v209, v[144:147]
	v_mul_f32_e32 v148, 0x43000000, v148
	v_mul_f32_e32 v149, 0x43000000, v149
	v_mul_f32_e32 v150, 0x43000000, v150
	v_mul_f32_e32 v151, 0x43000000, v151
	ds_write_b128 v209, v[148:151] offset:1024
	v_mul_f32_e32 v152, 0x43000000, v152
	v_mul_f32_e32 v153, 0x43000000, v153
	v_mul_f32_e32 v154, 0x43000000, v154
	v_mul_f32_e32 v155, 0x43000000, v155
	ds_write_b128 v209, v[152:155] offset:2048
	v_mul_f32_e32 v156, 0x43000000, v156
	v_mul_f32_e32 v157, 0x43000000, v157
	v_mul_f32_e32 v158, 0x43000000, v158
	v_mul_f32_e32 v159, 0x43000000, v159
	ds_write_b128 v209, v[156:159] offset:3072
	v_mul_f32_e32 v160, 0x43000000, v160
	v_mul_f32_e32 v161, 0x43000000, v161
	v_mul_f32_e32 v162, 0x43000000, v162
	v_mul_f32_e32 v163, 0x43000000, v163
	ds_write_b128 v209, v[160:163] offset:4096
	v_mul_f32_e32 v164, 0x43000000, v164
	v_mul_f32_e32 v165, 0x43000000, v165
	v_mul_f32_e32 v166, 0x43000000, v166
	v_mul_f32_e32 v167, 0x43000000, v167
	ds_write_b128 v209, v[164:167] offset:5120
	v_mul_f32_e32 v168, 0x43000000, v168
	v_mul_f32_e32 v169, 0x43000000, v169
	v_mul_f32_e32 v170, 0x43000000, v170
	v_mul_f32_e32 v171, 0x43000000, v171
	ds_write_b128 v209, v[168:171] offset:6144
	v_mul_f32_e32 v172, 0x43000000, v172
	v_mul_f32_e32 v173, 0x43000000, v173
	v_mul_f32_e32 v174, 0x43000000, v174
	v_mul_f32_e32 v175, 0x43000000, v175
	ds_write_b128 v209, v[172:175] offset:7168
	s_waitcnt lgkmcnt(0)
	s_barrier
	s_add_u32 s8, s38, 0xc000000
	s_addc_u32 s9, s39, 0
	global_load_dwordx4 v[144:147], v75, s[8:9]
	s_add_u32 s8, s8, 0x8000
	s_addc_u32 s9, s9, 0
	global_load_dwordx4 v[148:151], v75, s[8:9]
	s_add_u32 s8, s8, 0x8000
	s_addc_u32 s9, s9, 0
	global_load_dwordx4 v[152:155], v75, s[8:9]
	s_add_u32 s8, s8, 0x8000
	s_addc_u32 s9, s9, 0
	global_load_dwordx4 v[156:159], v75, s[8:9]
	s_add_u32 s8, s8, 0x8000
	s_addc_u32 s9, s9, 0
	global_load_dwordx4 v[160:163], v75, s[8:9]
	s_add_u32 s8, s8, 0x8000
	s_addc_u32 s9, s9, 0
	global_load_dwordx4 v[164:167], v75, s[8:9]
	s_add_u32 s8, s8, 0x8000
	s_addc_u32 s9, s9, 0
	global_load_dwordx4 v[168:171], v75, s[8:9]
	s_add_u32 s8, s8, 0x8000
	s_addc_u32 s9, s9, 0
	global_load_dwordx4 v[172:175], v75, s[8:9]
	s_add_u32 s6, s40, 0x2800
	s_addc_u32 s7, s41, 0
	ds_read_b32 v226, v211
	ds_read_b32 v227, v211 offset:512
	ds_read_b32 v228, v211 offset:1024
	ds_read_b32 v229, v211 offset:1536
	ds_read_b32 v230, v211 offset:2048
	ds_read_b32 v231, v211 offset:2560
	ds_read_b32 v232, v211 offset:3072
	ds_read_b32 v233, v211 offset:3584
	ds_read_b32 v234, v211 offset:4096
	ds_read_b32 v235, v211 offset:4608
	ds_read_b32 v236, v211 offset:5120
	ds_read_b32 v237, v211 offset:5632
	ds_read_b32 v238, v211 offset:6144
	ds_read_b32 v239, v211 offset:6656
	ds_read_b32 v240, v211 offset:7168
	ds_read_b32 v241, v211 offset:7680
	s_waitcnt lgkmcnt(0)
	v_max_f32_e32 v226, v226, v226
	v_max_f32_e32 v227, v227, v227
	v_max_f32_e32 v228, v228, v228
	v_max_f32_e32 v229, v229, v229
	v_max_f32_e32 v230, v230, v230
	v_max_f32_e32 v231, v231, v231
	v_max_f32_e32 v232, v232, v232
	v_max_f32_e32 v233, v233, v233
	v_max_f32_e32 v234, v234, v234
	v_max_f32_e32 v235, v235, v235
	v_max_f32_e32 v236, v236, v236
	v_max_f32_e32 v237, v237, v237
	v_max_f32_e32 v238, v238, v238
	v_max_f32_e32 v239, v239, v239
	v_max_f32_e32 v240, v240, v240
	v_max_f32_e32 v241, v241, v241
	v_med3_f32 v226, v226, s62, v95
	v_med3_f32 v227, v227, s62, v95
	v_med3_f32 v228, v228, s62, v95
	v_med3_f32 v229, v229, s62, v95
	v_med3_f32 v230, v230, s62, v95
	v_med3_f32 v231, v231, s62, v95
	v_med3_f32 v232, v232, s62, v95
	v_med3_f32 v233, v233, s62, v95
	v_med3_f32 v234, v234, s62, v95
	v_med3_f32 v235, v235, s62, v95
	v_med3_f32 v236, v236, s62, v95
	v_med3_f32 v237, v237, s62, v95
	v_med3_f32 v238, v238, s62, v95
	v_med3_f32 v239, v239, s62, v95
	v_med3_f32 v240, v240, s62, v95
	v_med3_f32 v241, v241, s62, v95
	v_mov_b32_e32 v242, 0
	v_mov_b32_e32 v243, 0
	v_mov_b32_e32 v244, 0
	v_mov_b32_e32 v245, 0
	v_cvt_pk_fp8_f32 v242, v226, v227
	v_cvt_pk_fp8_f32 v243, v230, v231
	v_cvt_pk_fp8_f32 v244, v234, v235
	v_cvt_pk_fp8_f32 v245, v238, v239
	v_cvt_pk_fp8_f32 v242, v228, v229 op_sel:[0,0,1]
	v_cvt_pk_fp8_f32 v243, v232, v233 op_sel:[0,0,1]
	v_cvt_pk_fp8_f32 v244, v236, v237 op_sel:[0,0,1]
	v_cvt_pk_fp8_f32 v245, v240, v241 op_sel:[0,0,1]
	s_nop 0
	global_store_dwordx4 v79, v[242:245], s[6:7]
	ds_read_b32 v226, v213
	ds_read_b32 v227, v213 offset:512
	ds_read_b32 v228, v213 offset:1024
	ds_read_b32 v229, v213 offset:1536
	ds_read_b32 v230, v213 offset:2048
	ds_read_b32 v231, v213 offset:2560
	ds_read_b32 v232, v213 offset:3072
	ds_read_b32 v233, v213 offset:3584
	ds_read_b32 v234, v213 offset:4096
	ds_read_b32 v235, v213 offset:4608
	ds_read_b32 v236, v213 offset:5120
	ds_read_b32 v237, v213 offset:5632
	ds_read_b32 v238, v213 offset:6144
	ds_read_b32 v239, v213 offset:6656
	ds_read_b32 v240, v213 offset:7168
	ds_read_b32 v241, v213 offset:7680
	s_waitcnt lgkmcnt(0)
; #define GAS __attribute__((address_space(1)))
; #define LAS __attribute__((address_space(3)))
; #define LDS_WAIT() asm volatile("s_waitcnt lgkmcnt(0)" ::: "memory")
;     const int pr = item >> 1, kb = 2 * (pr / nblk) + (item & 1), nb = pr % nblk, k0 = 64 * kb, n0 = 32 * nb;
;     const int nr = n0 + (lane & 31); const int sc = MAP == 1 ? src_col_in(nr) : nr;
;     float v[32];
; #pragma unroll
;     for (int i = 0; i < 32; ++i) v[i] = sc >= 0 ? W[(size_t)(k0 + 2 * i + (lane >> 5)) * Nsrc + sc] : 0.f;
; #pragma unroll
;     for (int i = 0; i < 32; ++i) { const int k = k0 + 2 * i + (lane >> 5); float x = v[i] * wscale; if (KS) x *= (k < ksplit ? ksA[k] : ksB[k - ksplit]); scr[(2 * i + (lane >> 5)) * 33 + (lane & 31)] = x; }
;     LDS_WAIT(); asm volatile("" ::: "memory");
;     const int c = lane & 7;
; #pragma unroll
;     for (int j = 0; j < 4; ++j) { const int n = (lane >> 3) + 8 * j; const LAS float* s = scr + (8 * c) * 33 + n;
;         const unsigned long long o = (unsigned long long)pg8::pk4_fp8(s[0 * 33], s[1 * 33], s[2 * 33], s[3 * 33]) | ((unsigned long long)pg8::pk4_fp8(s[4 * 33], s[5 * 33], s[6 * 33], s[7 * 33]) << 32);
;         *(GAS unsigned long long*)(WT + (size_t)(n0 + n) * K + k0 + 8 * c) = o; }
;     LDS_WAIT(); asm volatile("" ::: "memory");
	v_max_f32_e32 v226, v226, v226
	v_max_f32_e32 v227, v227, v227
	v_max_f32_e32 v228, v228, v228
	v_max_f32_e32 v229, v229, v229
	v_max_f32_e32 v230, v230, v230
	v_max_f32_e32 v231, v231, v231
	v_max_f32_e32 v232, v232, v232
	v_max_f32_e32 v233, v233, v233
	v_max_f32_e32 v234, v234, v234
	v_max_f32_e32 v235, v235, v235
	v_max_f32_e32 v236, v236, v236
	v_max_f32_e32 v237, v237, v237
	v_max_f32_e32 v238, v238, v238
	v_max_f32_e32 v239, v239, v239
	v_max_f32_e32 v240, v240, v240
	v_max_f32_e32 v241, v241, v241
	v_med3_f32 v226, v226, s62, v95
	v_med3_f32 v227, v227, s62, v95
	v_med3_f32 v228, v228, s62, v95
	v_med3_f32 v229, v229, s62, v95
	v_med3_f32 v230, v230, s62, v95
	v_med3_f32 v231, v231, s62, v95
	v_med3_f32 v232, v232, s62, v95
	v_med3_f32 v233, v233, s62, v95
	v_med3_f32 v234, v234, s62, v95
	v_med3_f32 v235, v235, s62, v95
	v_med3_f32 v236, v236, s62, v95
	v_med3_f32 v237, v237, s62, v95
	v_med3_f32 v238, v238, s62, v95
	v_med3_f32 v239, v239, s62, v95
	v_med3_f32 v240, v240, s62, v95
	v_med3_f32 v241, v241, s62, v95
	v_mov_b32_e32 v242, 0
	v_mov_b32_e32 v243, 0
	v_mov_b32_e32 v244, 0
	v_mov_b32_e32 v245, 0
	v_cvt_pk_fp8_f32 v242, v226, v227
	v_cvt_pk_fp8_f32 v243, v230, v231
	v_cvt_pk_fp8_f32 v244, v234, v235
	v_cvt_pk_fp8_f32 v245, v238, v239
	v_cvt_pk_fp8_f32 v242, v228, v229 op_sel:[0,0,1]
	v_cvt_pk_fp8_f32 v243, v232, v233 op_sel:[0,0,1]
	v_cvt_pk_fp8_f32 v244, v236, v237 op_sel:[0,0,1]
	v_cvt_pk_fp8_f32 v245, v240, v241 op_sel:[0,0,1]
	s_nop 0
	global_store_dwordx4 v80, v[242:245], s[6:7]
	s_waitcnt vmcnt(12)
	v_mul_f32_e32 v176, 0x43000000, v176
	v_mul_f32_e32 v177, 0x43000000, v177
	v_mul_f32_e32 v178, 0x43000000, v178
	v_mul_f32_e32 v179, 0x43000000, v179
	ds_write_b128 v210, v[176:179]
	v_mul_f32_e32 v180, 0x43000000, v180
	v_mul_f32_e32 v181, 0x43000000, v181
	v_mul_f32_e32 v182, 0x43000000, v182
	v_mul_f32_e32 v183, 0x43000000, v183
	ds_write_b128 v210, v[180:183] offset:1024
	v_mul_f32_e32 v184, 0x43000000, v184
	v_mul_f32_e32 v185, 0x43000000, v185
	v_mul_f32_e32 v186, 0x43000000, v186
	v_mul_f32_e32 v187, 0x43000000, v187
	ds_write_b128 v210, v[184:187] offset:2048
	v_mul_f32_e32 v188, 0x43000000, v188
	v_mul_f32_e32 v189, 0x43000000, v189
	v_mul_f32_e32 v190, 0x43000000, v190
	v_mul_f32_e32 v191, 0x43000000, v191
	ds_write_b128 v210, v[188:191] offset:3072
	v_mul_f32_e32 v192, 0x43000000, v192
	v_mul_f32_e32 v193, 0x43000000, v193
	v_mul_f32_e32 v194, 0x43000000, v194
	v_mul_f32_e32 v195, 0x43000000, v195
	ds_write_b128 v210, v[192:195] offset:4096
	v_mul_f32_e32 v196, 0x43000000, v196
	v_mul_f32_e32 v197, 0x43000000, v197
	v_mul_f32_e32 v198, 0x43000000, v198
	v_mul_f32_e32 v199, 0x43000000, v199
	ds_write_b128 v210, v[196:199] offset:5120
	v_mul_f32_e32 v200, 0x43000000, v200
	v_mul_f32_e32 v201, 0x43000000, v201
	v_mul_f32_e32 v202, 0x43000000, v202
	v_mul_f32_e32 v203, 0x43000000, v203
	ds_write_b128 v210, v[200:203] offset:6144
	v_mul_f32_e32 v204, 0x43000000, v204
	v_mul_f32_e32 v205, 0x43000000, v205
	v_mul_f32_e32 v206, 0x43000000, v206
	v_mul_f32_e32 v207, 0x43000000, v207
	ds_write_b128 v210, v[204:207] offset:7168
	s_waitcnt lgkmcnt(0)
	s_barrier
	s_add_u32 s8, s38, 0xd000000
	s_addc_u32 s9, s39, 0
	global_load_dwordx4 v[176:179], v75, s[8:9]
	s_add_u32 s8, s8, 0x8000
	s_addc_u32 s9, s9, 0
	global_load_dwordx4 v[180:183], v75, s[8:9]
	s_add_u32 s8, s8, 0x8000
	s_addc_u32 s9, s9, 0
	global_load_dwordx4 v[184:187], v75, s[8:9]
	s_add_u32 s8, s8, 0x8000
	s_addc_u32 s9, s9, 0
	global_load_dwordx4 v[188:191], v75, s[8:9]
	s_add_u32 s8, s8, 0x8000
	s_addc_u32 s9, s9, 0
	global_load_dwordx4 v[192:195], v75, s[8:9]
	s_add_u32 s8, s8, 0x8000
	s_addc_u32 s9, s9, 0
	global_load_dwordx4 v[196:199], v75, s[8:9]
	s_add_u32 s8, s8, 0x8000
	s_addc_u32 s9, s9, 0
	global_load_dwordx4 v[200:203], v75, s[8:9]
	s_add_u32 s8, s8, 0x8000
	s_addc_u32 s9, s9, 0
	global_load_dwordx4 v[204:207], v75, s[8:9]
	s_add_u32 s6, s40, 0x2c00
	s_addc_u32 s7, s41, 0
	ds_read_b32 v226, v212
	ds_read_b32 v227, v212 offset:512
	ds_read_b32 v228, v212 offset:1024
	ds_read_b32 v229, v212 offset:1536
	ds_read_b32 v230, v212 offset:2048
	ds_read_b32 v231, v212 offset:2560
	ds_read_b32 v232, v212 offset:3072
	ds_read_b32 v233, v212 offset:3584
	ds_read_b32 v234, v212 offset:4096
	ds_read_b32 v235, v212 offset:4608
	ds_read_b32 v236, v212 offset:5120
	ds_read_b32 v237, v212 offset:5632
	ds_read_b32 v238, v212 offset:6144
	ds_read_b32 v239, v212 offset:6656
	ds_read_b32 v240, v212 offset:7168
	ds_read_b32 v241, v212 offset:7680
	s_waitcnt lgkmcnt(0)
	v_max_f32_e32 v226, v226, v226
	v_max_f32_e32 v227, v227, v227
	v_max_f32_e32 v228, v228, v228
	v_max_f32_e32 v229, v229, v229
	v_max_f32_e32 v230, v230, v230
	v_max_f32_e32 v231, v231, v231
	v_max_f32_e32 v232, v232, v232
	v_max_f32_e32 v233, v233, v233
	v_max_f32_e32 v234, v234, v234
	v_max_f32_e32 v235, v235, v235
	v_max_f32_e32 v236, v236, v236
	v_max_f32_e32 v237, v237, v237
	v_max_f32_e32 v238, v238, v238
	v_max_f32_e32 v239, v239, v239
	v_max_f32_e32 v240, v240, v240
	v_max_f32_e32 v241, v241, v241
	v_med3_f32 v226, v226, s62, v95
	v_med3_f32 v227, v227, s62, v95
	v_med3_f32 v228, v228, s62, v95
	v_med3_f32 v229, v229, s62, v95
	v_med3_f32 v230, v230, s62, v95
	v_med3_f32 v231, v231, s62, v95
	v_med3_f32 v232, v232, s62, v95
	v_med3_f32 v233, v233, s62, v95
	v_med3_f32 v234, v234, s62, v95
	v_med3_f32 v235, v235, s62, v95
	v_med3_f32 v236, v236, s62, v95
	v_med3_f32 v237, v237, s62, v95
	v_med3_f32 v238, v238, s62, v95
	v_med3_f32 v239, v239, s62, v95
	v_med3_f32 v240, v240, s62, v95
	v_med3_f32 v241, v241, s62, v95
	v_mov_b32_e32 v242, 0
	v_mov_b32_e32 v243, 0
	v_mov_b32_e32 v244, 0
	v_mov_b32_e32 v245, 0
	v_cvt_pk_fp8_f32 v242, v226, v227
	v_cvt_pk_fp8_f32 v243, v230, v231
	v_cvt_pk_fp8_f32 v244, v234, v235
	v_cvt_pk_fp8_f32 v245, v238, v239
	v_cvt_pk_fp8_f32 v242, v228, v229 op_sel:[0,0,1]
	v_cvt_pk_fp8_f32 v243, v232, v233 op_sel:[0,0,1]
	v_cvt_pk_fp8_f32 v244, v236, v237 op_sel:[0,0,1]
	v_cvt_pk_fp8_f32 v245, v240, v241 op_sel:[0,0,1]
	s_nop 0
	global_store_dwordx4 v79, v[242:245], s[6:7]
	ds_read_b32 v226, v214
	ds_read_b32 v227, v214 offset:512
	ds_read_b32 v228, v214 offset:1024
	ds_read_b32 v229, v214 offset:1536
	ds_read_b32 v230, v214 offset:2048
	ds_read_b32 v231, v214 offset:2560
	ds_read_b32 v232, v214 offset:3072
	ds_read_b32 v233, v214 offset:3584
	ds_read_b32 v234, v214 offset:4096
	ds_read_b32 v235, v214 offset:4608
	ds_read_b32 v236, v214 offset:5120
	ds_read_b32 v237, v214 offset:5632
	ds_read_b32 v238, v214 offset:6144
	ds_read_b32 v239, v214 offset:6656
	ds_read_b32 v240, v214 offset:7168
	ds_read_b32 v241, v214 offset:7680
	s_waitcnt lgkmcnt(0)
; #define GAS __attribute__((address_space(1)))
; #define LAS __attribute__((address_space(3)))
; #define LDS_WAIT() asm volatile("s_waitcnt lgkmcnt(0)" ::: "memory")
;     const int pr = item >> 1, kb = 2 * (pr / nblk) + (item & 1), nb = pr % nblk, k0 = 64 * kb, n0 = 32 * nb;
;     const int nr = n0 + (lane & 31); const int sc = MAP == 1 ? src_col_in(nr) : nr;
;     float v[32];
; #pragma unroll
;     for (int i = 0; i < 32; ++i) v[i] = sc >= 0 ? W[(size_t)(k0 + 2 * i + (lane >> 5)) * Nsrc + sc] : 0.f;
; #pragma unroll
;     for (int i = 0; i < 32; ++i) { const int k = k0 + 2 * i + (lane >> 5); float x = v[i] * wscale; if (KS) x *= (k < ksplit ? ksA[k] : ksB[k - ksplit]); scr[(2 * i + (lane >> 5)) * 33 + (lane & 31)] = x; }
;     LDS_WAIT(); asm volatile("" ::: "memory");
;     const int c = lane & 7;
; #pragma unroll
;     for (int j = 0; j < 4; ++j) { const int n = (lane >> 3) + 8 * j; const LAS float* s = scr + (8 * c) * 33 + n;
;         const unsigned long long o = (unsigned long long)pg8::pk4_fp8(s[0 * 33], s[1 * 33], s[2 * 33], s[3 * 33]) | ((unsigned long long)pg8::pk4_fp8(s[4 * 33], s[5 * 33], s[6 * 33], s[7 * 33]) << 32);
;         *(GAS unsigned long long*)(WT + (size_t)(n0 + n) * K + k0 + 8 * c) = o; }
;     LDS_WAIT(); asm volatile("" ::: "memory");
	v_max_f32_e32 v226, v226, v226
	v_max_f32_e32 v227, v227, v227
	v_max_f32_e32 v228, v228, v228
	v_max_f32_e32 v229, v229, v229
	v_max_f32_e32 v230, v230, v230
	v_max_f32_e32 v231, v231, v231
	v_max_f32_e32 v232, v232, v232
	v_max_f32_e32 v233, v233, v233
	v_max_f32_e32 v234, v234, v234
	v_max_f32_e32 v235, v235, v235
	v_max_f32_e32 v236, v236, v236
	v_max_f32_e32 v237, v237, v237
	v_max_f32_e32 v238, v238, v238
	v_max_f32_e32 v239, v239, v239
	v_max_f32_e32 v240, v240, v240
	v_max_f32_e32 v241, v241, v241
	v_med3_f32 v226, v226, s62, v95
	v_med3_f32 v227, v227, s62, v95
	v_med3_f32 v228, v228, s62, v95
	v_med3_f32 v229, v229, s62, v95
	v_med3_f32 v230, v230, s62, v95
	v_med3_f32 v231, v231, s62, v95
	v_med3_f32 v232, v232, s62, v95
	v_med3_f32 v233, v233, s62, v95
	v_med3_f32 v234, v234, s62, v95
	v_med3_f32 v235, v235, s62, v95
	v_med3_f32 v236, v236, s62, v95
	v_med3_f32 v237, v237, s62, v95
	v_med3_f32 v238, v238, s62, v95
	v_med3_f32 v239, v239, s62, v95
	v_med3_f32 v240, v240, s62, v95
	v_med3_f32 v241, v241, s62, v95
	v_mov_b32_e32 v242, 0
	v_mov_b32_e32 v243, 0
	v_mov_b32_e32 v244, 0
	v_mov_b32_e32 v245, 0
	v_cvt_pk_fp8_f32 v242, v226, v227
	v_cvt_pk_fp8_f32 v243, v230, v231
	v_cvt_pk_fp8_f32 v244, v234, v235
	v_cvt_pk_fp8_f32 v245, v238, v239
	v_cvt_pk_fp8_f32 v242, v228, v229 op_sel:[0,0,1]
	v_cvt_pk_fp8_f32 v243, v232, v233 op_sel:[0,0,1]
	v_cvt_pk_fp8_f32 v244, v236, v237 op_sel:[0,0,1]
	v_cvt_pk_fp8_f32 v245, v240, v241 op_sel:[0,0,1]
	s_nop 0
	global_store_dwordx4 v80, v[242:245], s[6:7]
	s_waitcnt vmcnt(12)
	v_mul_f32_e32 v144, 0x43000000, v144
	v_mul_f32_e32 v145, 0x43000000, v145
	v_mul_f32_e32 v146, 0x43000000, v146
	v_mul_f32_e32 v147, 0x43000000, v147
	ds_write_b128 v209, v[144:147]
	v_mul_f32_e32 v148, 0x43000000, v148
	v_mul_f32_e32 v149, 0x43000000, v149
	v_mul_f32_e32 v150, 0x43000000, v150
	v_mul_f32_e32 v151, 0x43000000, v151
	ds_write_b128 v209, v[148:151] offset:1024
	v_mul_f32_e32 v152, 0x43000000, v152
	v_mul_f32_e32 v153, 0x43000000, v153
	v_mul_f32_e32 v154, 0x43000000, v154
	v_mul_f32_e32 v155, 0x43000000, v155
	ds_write_b128 v209, v[152:155] offset:2048
	v_mul_f32_e32 v156, 0x43000000, v156
	v_mul_f32_e32 v157, 0x43000000, v157
	v_mul_f32_e32 v158, 0x43000000, v158
	v_mul_f32_e32 v159, 0x43000000, v159
	ds_write_b128 v209, v[156:159] offset:3072
	v_mul_f32_e32 v160, 0x43000000, v160
	v_mul_f32_e32 v161, 0x43000000, v161
	v_mul_f32_e32 v162, 0x43000000, v162
	v_mul_f32_e32 v163, 0x43000000, v163
	ds_write_b128 v209, v[160:163] offset:4096
	v_mul_f32_e32 v164, 0x43000000, v164
	v_mul_f32_e32 v165, 0x43000000, v165
	v_mul_f32_e32 v166, 0x43000000, v166
	v_mul_f32_e32 v167, 0x43000000, v167
	ds_write_b128 v209, v[164:167] offset:5120
	v_mul_f32_e32 v168, 0x43000000, v168
	v_mul_f32_e32 v169, 0x43000000, v169
	v_mul_f32_e32 v170, 0x43000000, v170
	v_mul_f32_e32 v171, 0x43000000, v171
	ds_write_b128 v209, v[168:171] offset:6144
	v_mul_f32_e32 v172, 0x43000000, v172
	v_mul_f32_e32 v173, 0x43000000, v173
	v_mul_f32_e32 v174, 0x43000000, v174
	v_mul_f32_e32 v175, 0x43000000, v175
	ds_write_b128 v209, v[172:175] offset:7168
	s_waitcnt lgkmcnt(0)
	s_barrier
	s_add_u32 s8, s38, 0xe000000
	s_addc_u32 s9, s39, 0
	global_load_dwordx4 v[144:147], v75, s[8:9]
	s_add_u32 s8, s8, 0x8000
	s_addc_u32 s9, s9, 0
	global_load_dwordx4 v[148:151], v75, s[8:9]
	s_add_u32 s8, s8, 0x8000
	s_addc_u32 s9, s9, 0
	global_load_dwordx4 v[152:155], v75, s[8:9]
	s_add_u32 s8, s8, 0x8000
	s_addc_u32 s9, s9, 0
	global_load_dwordx4 v[156:159], v75, s[8:9]
	s_add_u32 s8, s8, 0x8000
	s_addc_u32 s9, s9, 0
	global_load_dwordx4 v[160:163], v75, s[8:9]
	s_add_u32 s8, s8, 0x8000
	s_addc_u32 s9, s9, 0
	global_load_dwordx4 v[164:167], v75, s[8:9]
	s_add_u32 s8, s8, 0x8000
	s_addc_u32 s9, s9, 0
	global_load_dwordx4 v[168:171], v75, s[8:9]
	s_add_u32 s8, s8, 0x8000
	s_addc_u32 s9, s9, 0
	global_load_dwordx4 v[172:175], v75, s[8:9]
	s_add_u32 s6, s40, 0x3000
	s_addc_u32 s7, s41, 0
	ds_read_b32 v226, v211
	ds_read_b32 v227, v211 offset:512
	ds_read_b32 v228, v211 offset:1024
	ds_read_b32 v229, v211 offset:1536
	ds_read_b32 v230, v211 offset:2048
	ds_read_b32 v231, v211 offset:2560
	ds_read_b32 v232, v211 offset:3072
	ds_read_b32 v233, v211 offset:3584
	ds_read_b32 v234, v211 offset:4096
	ds_read_b32 v235, v211 offset:4608
	ds_read_b32 v236, v211 offset:5120
	ds_read_b32 v237, v211 offset:5632
	ds_read_b32 v238, v211 offset:6144
	ds_read_b32 v239, v211 offset:6656
	ds_read_b32 v240, v211 offset:7168
	ds_read_b32 v241, v211 offset:7680
	s_waitcnt lgkmcnt(0)
	v_max_f32_e32 v226, v226, v226
	v_max_f32_e32 v227, v227, v227
	v_max_f32_e32 v228, v228, v228
	v_max_f32_e32 v229, v229, v229
	v_max_f32_e32 v230, v230, v230
	v_max_f32_e32 v231, v231, v231
	v_max_f32_e32 v232, v232, v232
	v_max_f32_e32 v233, v233, v233
	v_max_f32_e32 v234, v234, v234
	v_max_f32_e32 v235, v235, v235
	v_max_f32_e32 v236, v236, v236
	v_max_f32_e32 v237, v237, v237
	v_max_f32_e32 v238, v238, v238
	v_max_f32_e32 v239, v239, v239
	v_max_f32_e32 v240, v240, v240
	v_max_f32_e32 v241, v241, v241
	v_med3_f32 v226, v226, s62, v95
	v_med3_f32 v227, v227, s62, v95
	v_med3_f32 v228, v228, s62, v95
	v_med3_f32 v229, v229, s62, v95
	v_med3_f32 v230, v230, s62, v95
	v_med3_f32 v231, v231, s62, v95
	v_med3_f32 v232, v232, s62, v95
	v_med3_f32 v233, v233, s62, v95
	v_med3_f32 v234, v234, s62, v95
	v_med3_f32 v235, v235, s62, v95
	v_med3_f32 v236, v236, s62, v95
	v_med3_f32 v237, v237, s62, v95
	v_med3_f32 v238, v238, s62, v95
	v_med3_f32 v239, v239, s62, v95
	v_med3_f32 v240, v240, s62, v95
	v_med3_f32 v241, v241, s62, v95
	v_mov_b32_e32 v242, 0
	v_mov_b32_e32 v243, 0
	v_mov_b32_e32 v244, 0
	v_mov_b32_e32 v245, 0
	v_cvt_pk_fp8_f32 v242, v226, v227
	v_cvt_pk_fp8_f32 v243, v230, v231
	v_cvt_pk_fp8_f32 v244, v234, v235
	v_cvt_pk_fp8_f32 v245, v238, v239
	v_cvt_pk_fp8_f32 v242, v228, v229 op_sel:[0,0,1]
	v_cvt_pk_fp8_f32 v243, v232, v233 op_sel:[0,0,1]
	v_cvt_pk_fp8_f32 v244, v236, v237 op_sel:[0,0,1]
	v_cvt_pk_fp8_f32 v245, v240, v241 op_sel:[0,0,1]
	s_nop 0
	global_store_dwordx4 v79, v[242:245], s[6:7]
	ds_read_b32 v226, v213
	ds_read_b32 v227, v213 offset:512
	ds_read_b32 v228, v213 offset:1024
	ds_read_b32 v229, v213 offset:1536
	ds_read_b32 v230, v213 offset:2048
	ds_read_b32 v231, v213 offset:2560
	ds_read_b32 v232, v213 offset:3072
	ds_read_b32 v233, v213 offset:3584
	ds_read_b32 v234, v213 offset:4096
	ds_read_b32 v235, v213 offset:4608
	ds_read_b32 v236, v213 offset:5120
	ds_read_b32 v237, v213 offset:5632
	ds_read_b32 v238, v213 offset:6144
	ds_read_b32 v239, v213 offset:6656
	ds_read_b32 v240, v213 offset:7168
	ds_read_b32 v241, v213 offset:7680
	s_waitcnt lgkmcnt(0)
; #define GAS __attribute__((address_space(1)))
; #define LAS __attribute__((address_space(3)))
; #define LDS_WAIT() asm volatile("s_waitcnt lgkmcnt(0)" ::: "memory")
;     const int pr = item >> 1, kb = 2 * (pr / nblk) + (item & 1), nb = pr % nblk, k0 = 64 * kb, n0 = 32 * nb;
;     const int nr = n0 + (lane & 31); const int sc = MAP == 1 ? src_col_in(nr) : nr;
;     float v[32];
; #pragma unroll
;     for (int i = 0; i < 32; ++i) v[i] = sc >= 0 ? W[(size_t)(k0 + 2 * i + (lane >> 5)) * Nsrc + sc] : 0.f;
; #pragma unroll
;     for (int i = 0; i < 32; ++i) { const int k = k0 + 2 * i + (lane >> 5); float x = v[i] * wscale; if (KS) x *= (k < ksplit ? ksA[k] : ksB[k - ksplit]); scr[(2 * i + (lane >> 5)) * 33 + (lane & 31)] = x; }
;     LDS_WAIT(); asm volatile("" ::: "memory");
;     const int c = lane & 7;
; #pragma unroll
;     for (int j = 0; j < 4; ++j) { const int n = (lane >> 3) + 8 * j; const LAS float* s = scr + (8 * c) * 33 + n;
;         const unsigned long long o = (unsigned long long)pg8::pk4_fp8(s[0 * 33], s[1 * 33], s[2 * 33], s[3 * 33]) | ((unsigned long long)pg8::pk4_fp8(s[4 * 33], s[5 * 33], s[6 * 33], s[7 * 33]) << 32);
;         *(GAS unsigned long long*)(WT + (size_t)(n0 + n) * K + k0 + 8 * c) = o; }
;     LDS_WAIT(); asm volatile("" ::: "memory");
	v_max_f32_e32 v226, v226, v226
	v_max_f32_e32 v227, v227, v227
	v_max_f32_e32 v228, v228, v228
	v_max_f32_e32 v229, v229, v229
	v_max_f32_e32 v230, v230, v230
	v_max_f32_e32 v231, v231, v231
	v_max_f32_e32 v232, v232, v232
	v_max_f32_e32 v233, v233, v233
	v_max_f32_e32 v234, v234, v234
	v_max_f32_e32 v235, v235, v235
	v_max_f32_e32 v236, v236, v236
	v_max_f32_e32 v237, v237, v237
	v_max_f32_e32 v238, v238, v238
	v_max_f32_e32 v239, v239, v239
	v_max_f32_e32 v240, v240, v240
	v_max_f32_e32 v241, v241, v241
	v_med3_f32 v226, v226, s62, v95
	v_med3_f32 v227, v227, s62, v95
	v_med3_f32 v228, v228, s62, v95
	v_med3_f32 v229, v229, s62, v95
	v_med3_f32 v230, v230, s62, v95
	v_med3_f32 v231, v231, s62, v95
	v_med3_f32 v232, v232, s62, v95
	v_med3_f32 v233, v233, s62, v95
	v_med3_f32 v234, v234, s62, v95
	v_med3_f32 v235, v235, s62, v95
	v_med3_f32 v236, v236, s62, v95
	v_med3_f32 v237, v237, s62, v95
	v_med3_f32 v238, v238, s62, v95
	v_med3_f32 v239, v239, s62, v95
	v_med3_f32 v240, v240, s62, v95
	v_med3_f32 v241, v241, s62, v95
	v_mov_b32_e32 v242, 0
	v_mov_b32_e32 v243, 0
	v_mov_b32_e32 v244, 0
	v_mov_b32_e32 v245, 0
	v_cvt_pk_fp8_f32 v242, v226, v227
	v_cvt_pk_fp8_f32 v243, v230, v231
	v_cvt_pk_fp8_f32 v244, v234, v235
	v_cvt_pk_fp8_f32 v245, v238, v239
	v_cvt_pk_fp8_f32 v242, v228, v229 op_sel:[0,0,1]
	v_cvt_pk_fp8_f32 v243, v232, v233 op_sel:[0,0,1]
	v_cvt_pk_fp8_f32 v244, v236, v237 op_sel:[0,0,1]
	v_cvt_pk_fp8_f32 v245, v240, v241 op_sel:[0,0,1]
	s_nop 0
	global_store_dwordx4 v80, v[242:245], s[6:7]
	s_waitcnt vmcnt(12)
	v_mul_f32_e32 v176, 0x43000000, v176
	v_mul_f32_e32 v177, 0x43000000, v177
	v_mul_f32_e32 v178, 0x43000000, v178
	v_mul_f32_e32 v179, 0x43000000, v179
	ds_write_b128 v210, v[176:179]
	v_mul_f32_e32 v180, 0x43000000, v180
	v_mul_f32_e32 v181, 0x43000000, v181
	v_mul_f32_e32 v182, 0x43000000, v182
	v_mul_f32_e32 v183, 0x43000000, v183
	ds_write_b128 v210, v[180:183] offset:1024
	v_mul_f32_e32 v184, 0x43000000, v184
	v_mul_f32_e32 v185, 0x43000000, v185
	v_mul_f32_e32 v186, 0x43000000, v186
	v_mul_f32_e32 v187, 0x43000000, v187
	ds_write_b128 v210, v[184:187] offset:2048
	v_mul_f32_e32 v188, 0x43000000, v188
	v_mul_f32_e32 v189, 0x43000000, v189
	v_mul_f32_e32 v190, 0x43000000, v190
	v_mul_f32_e32 v191, 0x43000000, v191
	ds_write_b128 v210, v[188:191] offset:3072
	v_mul_f32_e32 v192, 0x43000000, v192
	v_mul_f32_e32 v193, 0x43000000, v193
	v_mul_f32_e32 v194, 0x43000000, v194
	v_mul_f32_e32 v195, 0x43000000, v195
	ds_write_b128 v210, v[192:195] offset:4096
	v_mul_f32_e32 v196, 0x43000000, v196
	v_mul_f32_e32 v197, 0x43000000, v197
	v_mul_f32_e32 v198, 0x43000000, v198
	v_mul_f32_e32 v199, 0x43000000, v199
	ds_write_b128 v210, v[196:199] offset:5120
	v_mul_f32_e32 v200, 0x43000000, v200
	v_mul_f32_e32 v201, 0x43000000, v201
	v_mul_f32_e32 v202, 0x43000000, v202
	v_mul_f32_e32 v203, 0x43000000, v203
	ds_write_b128 v210, v[200:203] offset:6144
	v_mul_f32_e32 v204, 0x43000000, v204
	v_mul_f32_e32 v205, 0x43000000, v205
	v_mul_f32_e32 v206, 0x43000000, v206
	v_mul_f32_e32 v207, 0x43000000, v207
	ds_write_b128 v210, v[204:207] offset:7168
	s_waitcnt lgkmcnt(0)
	s_barrier
	s_add_u32 s8, s38, 0xf000000
	s_addc_u32 s9, s39, 0
	global_load_dwordx4 v[176:179], v75, s[8:9]
	s_add_u32 s8, s8, 0x8000
	s_addc_u32 s9, s9, 0
	global_load_dwordx4 v[180:183], v75, s[8:9]
	s_add_u32 s8, s8, 0x8000
	s_addc_u32 s9, s9, 0
	global_load_dwordx4 v[184:187], v75, s[8:9]
	s_add_u32 s8, s8, 0x8000
	s_addc_u32 s9, s9, 0
	global_load_dwordx4 v[188:191], v75, s[8:9]
	s_add_u32 s8, s8, 0x8000
	s_addc_u32 s9, s9, 0
	global_load_dwordx4 v[192:195], v75, s[8:9]
	s_add_u32 s8, s8, 0x8000
	s_addc_u32 s9, s9, 0
	global_load_dwordx4 v[196:199], v75, s[8:9]
	s_add_u32 s8, s8, 0x8000
	s_addc_u32 s9, s9, 0
	global_load_dwordx4 v[200:203], v75, s[8:9]
	s_add_u32 s8, s8, 0x8000
	s_addc_u32 s9, s9, 0
	global_load_dwordx4 v[204:207], v75, s[8:9]
	s_add_u32 s6, s40, 0x3400
	s_addc_u32 s7, s41, 0
	ds_read_b32 v226, v212
	ds_read_b32 v227, v212 offset:512
	ds_read_b32 v228, v212 offset:1024
	ds_read_b32 v229, v212 offset:1536
	ds_read_b32 v230, v212 offset:2048
	ds_read_b32 v231, v212 offset:2560
	ds_read_b32 v232, v212 offset:3072
	ds_read_b32 v233, v212 offset:3584
	ds_read_b32 v234, v212 offset:4096
	ds_read_b32 v235, v212 offset:4608
	ds_read_b32 v236, v212 offset:5120
	ds_read_b32 v237, v212 offset:5632
	ds_read_b32 v238, v212 offset:6144
	ds_read_b32 v239, v212 offset:6656
	ds_read_b32 v240, v212 offset:7168
	ds_read_b32 v241, v212 offset:7680
	s_waitcnt lgkmcnt(0)
	v_max_f32_e32 v226, v226, v226
	v_max_f32_e32 v227, v227, v227
	v_max_f32_e32 v228, v228, v228
	v_max_f32_e32 v229, v229, v229
	v_max_f32_e32 v230, v230, v230
	v_max_f32_e32 v231, v231, v231
	v_max_f32_e32 v232, v232, v232
	v_max_f32_e32 v233, v233, v233
	v_max_f32_e32 v234, v234, v234
	v_max_f32_e32 v235, v235, v235
	v_max_f32_e32 v236, v236, v236
	v_max_f32_e32 v237, v237, v237
	v_max_f32_e32 v238, v238, v238
	v_max_f32_e32 v239, v239, v239
	v_max_f32_e32 v240, v240, v240
	v_max_f32_e32 v241, v241, v241
	v_med3_f32 v226, v226, s62, v95
	v_med3_f32 v227, v227, s62, v95
	v_med3_f32 v228, v228, s62, v95
	v_med3_f32 v229, v229, s62, v95
	v_med3_f32 v230, v230, s62, v95
	v_med3_f32 v231, v231, s62, v95
	v_med3_f32 v232, v232, s62, v95
	v_med3_f32 v233, v233, s62, v95
	v_med3_f32 v234, v234, s62, v95
	v_med3_f32 v235, v235, s62, v95
	v_med3_f32 v236, v236, s62, v95
	v_med3_f32 v237, v237, s62, v95
	v_med3_f32 v238, v238, s62, v95
	v_med3_f32 v239, v239, s62, v95
	v_med3_f32 v240, v240, s62, v95
	v_med3_f32 v241, v241, s62, v95
	v_mov_b32_e32 v242, 0
	v_mov_b32_e32 v243, 0
	v_mov_b32_e32 v244, 0
	v_mov_b32_e32 v245, 0
	v_cvt_pk_fp8_f32 v242, v226, v227
	v_cvt_pk_fp8_f32 v243, v230, v231
	v_cvt_pk_fp8_f32 v244, v234, v235
	v_cvt_pk_fp8_f32 v245, v238, v239
	v_cvt_pk_fp8_f32 v242, v228, v229 op_sel:[0,0,1]
	v_cvt_pk_fp8_f32 v243, v232, v233 op_sel:[0,0,1]
	v_cvt_pk_fp8_f32 v244, v236, v237 op_sel:[0,0,1]
	v_cvt_pk_fp8_f32 v245, v240, v241 op_sel:[0,0,1]
	s_nop 0
	global_store_dwordx4 v79, v[242:245], s[6:7]
	ds_read_b32 v226, v214
	ds_read_b32 v227, v214 offset:512
	ds_read_b32 v228, v214 offset:1024
	ds_read_b32 v229, v214 offset:1536
	ds_read_b32 v230, v214 offset:2048
	ds_read_b32 v231, v214 offset:2560
	ds_read_b32 v232, v214 offset:3072
	ds_read_b32 v233, v214 offset:3584
	ds_read_b32 v234, v214 offset:4096
	ds_read_b32 v235, v214 offset:4608
	ds_read_b32 v236, v214 offset:5120
	ds_read_b32 v237, v214 offset:5632
	ds_read_b32 v238, v214 offset:6144
	ds_read_b32 v239, v214 offset:6656
	ds_read_b32 v240, v214 offset:7168
	ds_read_b32 v241, v214 offset:7680
	s_waitcnt lgkmcnt(0)
; #define GAS __attribute__((address_space(1)))
; #define LAS __attribute__((address_space(3)))
; #define LDS_WAIT() asm volatile("s_waitcnt lgkmcnt(0)" ::: "memory")
; __device__ __forceinline__ int src_col_in(int c) {
;     if (c < 5120) { const int blk = c >> 7, p = c & 127; const bool rope = blk < 16 || ((((blk - 16) >> 2) & 1) == 0); const int d = rope ? (p >> 1) + 64 * (p & 1) : p; return blk * 128 + d; }
;     if (c < OFF_Z) return c + 2096;
;     if (c < OFF_G) return c - 4048;
;     if (c < OFF_DT) return 5120 + (c - OFF_G);
;     const int pr = item >> 1, kb = 2 * (pr / nblk) + (item & 1), nb = pr % nblk, k0 = 64 * kb, n0 = 32 * nb;
;     const int nr = n0 + (lane & 31); const int sc = MAP == 1 ? src_col_in(nr) : nr;
;     float v[32];
; #pragma unroll
;     for (int i = 0; i < 32; ++i) v[i] = sc >= 0 ? W[(size_t)(k0 + 2 * i + (lane >> 5)) * Nsrc + sc] : 0.f;
; #pragma unroll
;     for (int i = 0; i < 32; ++i) { const int k = k0 + 2 * i + (lane >> 5); float x = v[i] * wscale; if (KS) x *= (k < ksplit ? ksA[k] : ksB[k - ksplit]); scr[(2 * i + (lane >> 5)) * 33 + (lane & 31)] = x; }
;     LDS_WAIT(); asm volatile("" ::: "memory");
;     const int c = lane & 7;
; #pragma unroll
;     for (int j = 0; j < 4; ++j) { const int n = (lane >> 3) + 8 * j; const LAS float* s = scr + (8 * c) * 33 + n;
;         const unsigned long long o = (unsigned long long)pg8::pk4_fp8(s[0 * 33], s[1 * 33], s[2 * 33], s[3 * 33]) | ((unsigned long long)pg8::pk4_fp8(s[4 * 33], s[5 * 33], s[6 * 33], s[7 * 33]) << 32);
;         *(GAS unsigned long long*)(WT + (size_t)(n0 + n) * K + k0 + 8 * c) = o; }
;     LDS_WAIT(); asm volatile("" ::: "memory");
	v_max_f32_e32 v226, v226, v226
	v_max_f32_e32 v227, v227, v227
	v_max_f32_e32 v228, v228, v228
	v_max_f32_e32 v229, v229, v229
	v_max_f32_e32 v230, v230, v230
	v_max_f32_e32 v231, v231, v231
	v_max_f32_e32 v232, v232, v232
	v_max_f32_e32 v233, v233, v233
	v_max_f32_e32 v234, v234, v234
	v_max_f32_e32 v235, v235, v235
	v_max_f32_e32 v236, v236, v236
	v_max_f32_e32 v237, v237, v237
	v_max_f32_e32 v238, v238, v238
	v_max_f32_e32 v239, v239, v239
	v_max_f32_e32 v240, v240, v240
	v_max_f32_e32 v241, v241, v241
	v_med3_f32 v226, v226, s62, v95
	v_med3_f32 v227, v227, s62, v95
	v_med3_f32 v228, v228, s62, v95
	v_med3_f32 v229, v229, s62, v95
	v_med3_f32 v230, v230, s62, v95
	v_med3_f32 v231, v231, s62, v95
	v_med3_f32 v232, v232, s62, v95
	v_med3_f32 v233, v233, s62, v95
	v_med3_f32 v234, v234, s62, v95
	v_med3_f32 v235, v235, s62, v95
	v_med3_f32 v236, v236, s62, v95
	v_med3_f32 v237, v237, s62, v95
	v_med3_f32 v238, v238, s62, v95
	v_med3_f32 v239, v239, s62, v95
	v_med3_f32 v240, v240, s62, v95
	v_med3_f32 v241, v241, s62, v95
	v_mov_b32_e32 v242, 0
	v_mov_b32_e32 v243, 0
	v_mov_b32_e32 v244, 0
	v_mov_b32_e32 v245, 0
	v_cvt_pk_fp8_f32 v242, v226, v227
	v_cvt_pk_fp8_f32 v243, v230, v231
	v_cvt_pk_fp8_f32 v244, v234, v235
	v_cvt_pk_fp8_f32 v245, v238, v239
	v_cvt_pk_fp8_f32 v242, v228, v229 op_sel:[0,0,1]
	v_cvt_pk_fp8_f32 v243, v232, v233 op_sel:[0,0,1]
	v_cvt_pk_fp8_f32 v244, v236, v237 op_sel:[0,0,1]
	v_cvt_pk_fp8_f32 v245, v240, v241 op_sel:[0,0,1]
	s_nop 0
	global_store_dwordx4 v80, v[242:245], s[6:7]
	s_waitcnt vmcnt(12)
	v_mul_f32_e32 v144, 0x43000000, v144
	v_mul_f32_e32 v145, 0x43000000, v145
	v_mul_f32_e32 v146, 0x43000000, v146
	v_mul_f32_e32 v147, 0x43000000, v147
	ds_write_b128 v209, v[144:147]
	v_mul_f32_e32 v148, 0x43000000, v148
	v_mul_f32_e32 v149, 0x43000000, v149
	v_mul_f32_e32 v150, 0x43000000, v150
	v_mul_f32_e32 v151, 0x43000000, v151
	ds_write_b128 v209, v[148:151] offset:1024
	v_mul_f32_e32 v152, 0x43000000, v152
	v_mul_f32_e32 v153, 0x43000000, v153
	v_mul_f32_e32 v154, 0x43000000, v154
	v_mul_f32_e32 v155, 0x43000000, v155
	ds_write_b128 v209, v[152:155] offset:2048
	v_mul_f32_e32 v156, 0x43000000, v156
	v_mul_f32_e32 v157, 0x43000000, v157
	v_mul_f32_e32 v158, 0x43000000, v158
	v_mul_f32_e32 v159, 0x43000000, v159
	ds_write_b128 v209, v[156:159] offset:3072
	v_mul_f32_e32 v160, 0x43000000, v160
	v_mul_f32_e32 v161, 0x43000000, v161
	v_mul_f32_e32 v162, 0x43000000, v162
	v_mul_f32_e32 v163, 0x43000000, v163
	ds_write_b128 v209, v[160:163] offset:4096
	v_mul_f32_e32 v164, 0x43000000, v164
	v_mul_f32_e32 v165, 0x43000000, v165
	v_mul_f32_e32 v166, 0x43000000, v166
	v_mul_f32_e32 v167, 0x43000000, v167
	ds_write_b128 v209, v[164:167] offset:5120
	v_mul_f32_e32 v168, 0x43000000, v168
	v_mul_f32_e32 v169, 0x43000000, v169
	v_mul_f32_e32 v170, 0x43000000, v170
	v_mul_f32_e32 v171, 0x43000000, v171
	ds_write_b128 v209, v[168:171] offset:6144
	v_mul_f32_e32 v172, 0x43000000, v172
	v_mul_f32_e32 v173, 0x43000000, v173
	v_mul_f32_e32 v174, 0x43000000, v174
	v_mul_f32_e32 v175, 0x43000000, v175
	ds_write_b128 v209, v[172:175] offset:7168
	s_waitcnt lgkmcnt(0)
	s_barrier
	s_add_i32 s24, s23, 0
	s_lshl_b32 s20, s24, 7
	s_cmp_lt_u32 s24, 40
	s_cselect_b32 s21, 0, 0x830
	s_cmp_lt_u32 s24, 72
	s_cselect_b32 s21, s21, 0xfffff030
	s_add_i32 s20, s20, s21
	s_lshl_b32 s20, s20, 2
	s_add_u32 s8, s46, s20
	s_addc_u32 s9, s47, 0
	global_load_dwordx4 v[144:147], v76, s[8:9]
	s_add_u32 s8, s8, 0x16280
	s_addc_u32 s9, s9, 0
	global_load_dwordx4 v[148:151], v76, s[8:9]
	s_add_u32 s8, s8, 0x16280
	s_addc_u32 s9, s9, 0
	global_load_dwordx4 v[152:155], v76, s[8:9]
	s_add_u32 s8, s8, 0x16280
	s_addc_u32 s9, s9, 0
	global_load_dwordx4 v[156:159], v76, s[8:9]
	s_add_u32 s8, s8, 0x16280
	s_addc_u32 s9, s9, 0
	global_load_dwordx4 v[160:163], v76, s[8:9]
	s_add_u32 s8, s8, 0x16280
	s_addc_u32 s9, s9, 0
	global_load_dwordx4 v[164:167], v76, s[8:9]
	s_add_u32 s8, s8, 0x16280
	s_addc_u32 s9, s9, 0
	global_load_dwordx4 v[168:171], v76, s[8:9]
	s_add_u32 s8, s8, 0x16280
	s_addc_u32 s9, s9, 0
	global_load_dwordx4 v[172:175], v76, s[8:9]
	s_add_u32 s6, s40, 0x3800
	s_addc_u32 s7, s41, 0
	ds_read_b32 v226, v211
	ds_read_b32 v227, v211 offset:512
	ds_read_b32 v228, v211 offset:1024
	ds_read_b32 v229, v211 offset:1536
	ds_read_b32 v230, v211 offset:2048
	ds_read_b32 v231, v211 offset:2560
	ds_read_b32 v232, v211 offset:3072
	ds_read_b32 v233, v211 offset:3584
	ds_read_b32 v234, v211 offset:4096
	ds_read_b32 v235, v211 offset:4608
	ds_read_b32 v236, v211 offset:5120
	ds_read_b32 v237, v211 offset:5632
	ds_read_b32 v238, v211 offset:6144
	ds_read_b32 v239, v211 offset:6656
	ds_read_b32 v240, v211 offset:7168
	ds_read_b32 v241, v211 offset:7680
	s_waitcnt lgkmcnt(0)
; #define GAS __attribute__((address_space(1)))
; #define LAS __attribute__((address_space(3)))
; #define LDS_WAIT() asm volatile("s_waitcnt lgkmcnt(0)" ::: "memory")
;     const int pr = item >> 1, kb = 2 * (pr / nblk) + (item & 1), nb = pr % nblk, k0 = 64 * kb, n0 = 32 * nb;
;     const int nr = n0 + (lane & 31); const int sc = MAP == 1 ? src_col_in(nr) : nr;
;     float v[32];
; #pragma unroll
;     for (int i = 0; i < 32; ++i) v[i] = sc >= 0 ? W[(size_t)(k0 + 2 * i + (lane >> 5)) * Nsrc + sc] : 0.f;
; #pragma unroll
;     for (int i = 0; i < 32; ++i) { const int k = k0 + 2 * i + (lane >> 5); float x = v[i] * wscale; if (KS) x *= (k < ksplit ? ksA[k] : ksB[k - ksplit]); scr[(2 * i + (lane >> 5)) * 33 + (lane & 31)] = x; }
;     LDS_WAIT(); asm volatile("" ::: "memory");
;     const int c = lane & 7;
; #pragma unroll
;     for (int j = 0; j < 4; ++j) { const int n = (lane >> 3) + 8 * j; const LAS float* s = scr + (8 * c) * 33 + n;
;         const unsigned long long o = (unsigned long long)pg8::pk4_fp8(s[0 * 33], s[1 * 33], s[2 * 33], s[3 * 33]) | ((unsigned long long)pg8::pk4_fp8(s[4 * 33], s[5 * 33], s[6 * 33], s[7 * 33]) << 32);
;         *(GAS unsigned long long*)(WT + (size_t)(n0 + n) * K + k0 + 8 * c) = o; }
;     LDS_WAIT(); asm volatile("" ::: "memory");
	v_max_f32_e32 v226, v226, v226
	v_max_f32_e32 v227, v227, v227
	v_max_f32_e32 v228, v228, v228
	v_max_f32_e32 v229, v229, v229
	v_max_f32_e32 v230, v230, v230
	v_max_f32_e32 v231, v231, v231
	v_max_f32_e32 v232, v232, v232
	v_max_f32_e32 v233, v233, v233
	v_max_f32_e32 v234, v234, v234
	v_max_f32_e32 v235, v235, v235
	v_max_f32_e32 v236, v236, v236
	v_max_f32_e32 v237, v237, v237
	v_max_f32_e32 v238, v238, v238
	v_max_f32_e32 v239, v239, v239
	v_max_f32_e32 v240, v240, v240
	v_max_f32_e32 v241, v241, v241
	v_med3_f32 v226, v226, s62, v95
	v_med3_f32 v227, v227, s62, v95
	v_med3_f32 v228, v228, s62, v95
	v_med3_f32 v229, v229, s62, v95
	v_med3_f32 v230, v230, s62, v95
	v_med3_f32 v231, v231, s62, v95
	v_med3_f32 v232, v232, s62, v95
	v_med3_f32 v233, v233, s62, v95
	v_med3_f32 v234, v234, s62, v95
	v_med3_f32 v235, v235, s62, v95
	v_med3_f32 v236, v236, s62, v95
	v_med3_f32 v237, v237, s62, v95
	v_med3_f32 v238, v238, s62, v95
	v_med3_f32 v239, v239, s62, v95
	v_med3_f32 v240, v240, s62, v95
	v_med3_f32 v241, v241, s62, v95
	v_mov_b32_e32 v242, 0
	v_mov_b32_e32 v243, 0
	v_mov_b32_e32 v244, 0
	v_mov_b32_e32 v245, 0
	v_cvt_pk_fp8_f32 v242, v226, v227
	v_cvt_pk_fp8_f32 v243, v230, v231
	v_cvt_pk_fp8_f32 v244, v234, v235
	v_cvt_pk_fp8_f32 v245, v238, v239
	v_cvt_pk_fp8_f32 v242, v228, v229 op_sel:[0,0,1]
	v_cvt_pk_fp8_f32 v243, v232, v233 op_sel:[0,0,1]
	v_cvt_pk_fp8_f32 v244, v236, v237 op_sel:[0,0,1]
	v_cvt_pk_fp8_f32 v245, v240, v241 op_sel:[0,0,1]
	s_nop 0
	global_store_dwordx4 v79, v[242:245], s[6:7]
	ds_read_b32 v226, v213
	ds_read_b32 v227, v213 offset:512
	ds_read_b32 v228, v213 offset:1024
	ds_read_b32 v229, v213 offset:1536
	ds_read_b32 v230, v213 offset:2048
	ds_read_b32 v231, v213 offset:2560
	ds_read_b32 v232, v213 offset:3072
	ds_read_b32 v233, v213 offset:3584
	ds_read_b32 v234, v213 offset:4096
	ds_read_b32 v235, v213 offset:4608
	ds_read_b32 v236, v213 offset:5120
	ds_read_b32 v237, v213 offset:5632
	ds_read_b32 v238, v213 offset:6144
	ds_read_b32 v239, v213 offset:6656
	ds_read_b32 v240, v213 offset:7168
	ds_read_b32 v241, v213 offset:7680
	s_waitcnt lgkmcnt(0)
	v_max_f32_e32 v226, v226, v226
	v_max_f32_e32 v227, v227, v227
	v_max_f32_e32 v228, v228, v228
	v_max_f32_e32 v229, v229, v229
	v_max_f32_e32 v230, v230, v230
	v_max_f32_e32 v231, v231, v231
	v_max_f32_e32 v232, v232, v232
	v_max_f32_e32 v233, v233, v233
	v_max_f32_e32 v234, v234, v234
	v_max_f32_e32 v235, v235, v235
	v_max_f32_e32 v236, v236, v236
	v_max_f32_e32 v237, v237, v237
	v_max_f32_e32 v238, v238, v238
	v_max_f32_e32 v239, v239, v239
	v_max_f32_e32 v240, v240, v240
	v_max_f32_e32 v241, v241, v241
	v_med3_f32 v226, v226, s62, v95
	v_med3_f32 v227, v227, s62, v95
	v_med3_f32 v228, v228, s62, v95
	v_med3_f32 v229, v229, s62, v95
	v_med3_f32 v230, v230, s62, v95
	v_med3_f32 v231, v231, s62, v95
	v_med3_f32 v232, v232, s62, v95
	v_med3_f32 v233, v233, s62, v95
	v_med3_f32 v234, v234, s62, v95
	v_med3_f32 v235, v235, s62, v95
	v_med3_f32 v236, v236, s62, v95
	v_med3_f32 v237, v237, s62, v95
	v_med3_f32 v238, v238, s62, v95
	v_med3_f32 v239, v239, s62, v95
	v_med3_f32 v240, v240, s62, v95
	v_med3_f32 v241, v241, s62, v95
	v_mov_b32_e32 v242, 0
	v_mov_b32_e32 v243, 0
	v_mov_b32_e32 v244, 0
	v_mov_b32_e32 v245, 0
	v_cvt_pk_fp8_f32 v242, v226, v227
	v_cvt_pk_fp8_f32 v243, v230, v231
	v_cvt_pk_fp8_f32 v244, v234, v235
	v_cvt_pk_fp8_f32 v245, v238, v239
	v_cvt_pk_fp8_f32 v242, v228, v229 op_sel:[0,0,1]
	v_cvt_pk_fp8_f32 v243, v232, v233 op_sel:[0,0,1]
	v_cvt_pk_fp8_f32 v244, v236, v237 op_sel:[0,0,1]
	v_cvt_pk_fp8_f32 v245, v240, v241 op_sel:[0,0,1]
	s_nop 0
	global_store_dwordx4 v80, v[242:245], s[6:7]
	s_waitcnt vmcnt(12)
	v_mul_f32_e32 v176, 0x43000000, v176
	v_mul_f32_e32 v177, 0x43000000, v177
	v_mul_f32_e32 v178, 0x43000000, v178
	v_mul_f32_e32 v179, 0x43000000, v179
	ds_write_b128 v210, v[176:179]
	v_mul_f32_e32 v180, 0x43000000, v180
	v_mul_f32_e32 v181, 0x43000000, v181
	v_mul_f32_e32 v182, 0x43000000, v182
	v_mul_f32_e32 v183, 0x43000000, v183
	ds_write_b128 v210, v[180:183] offset:1024
	v_mul_f32_e32 v184, 0x43000000, v184
	v_mul_f32_e32 v185, 0x43000000, v185
	v_mul_f32_e32 v186, 0x43000000, v186
	v_mul_f32_e32 v187, 0x43000000, v187
	ds_write_b128 v210, v[184:187] offset:2048
	v_mul_f32_e32 v188, 0x43000000, v188
	v_mul_f32_e32 v189, 0x43000000, v189
	v_mul_f32_e32 v190, 0x43000000, v190
	v_mul_f32_e32 v191, 0x43000000, v191
	ds_write_b128 v210, v[188:191] offset:3072
	v_mul_f32_e32 v192, 0x43000000, v192
	v_mul_f32_e32 v193, 0x43000000, v193
	v_mul_f32_e32 v194, 0x43000000, v194
	v_mul_f32_e32 v195, 0x43000000, v195
	ds_write_b128 v210, v[192:195] offset:4096
	v_mul_f32_e32 v196, 0x43000000, v196
	v_mul_f32_e32 v197, 0x43000000, v197
	v_mul_f32_e32 v198, 0x43000000, v198
	v_mul_f32_e32 v199, 0x43000000, v199
	ds_write_b128 v210, v[196:199] offset:5120
	v_mul_f32_e32 v200, 0x43000000, v200
	v_mul_f32_e32 v201, 0x43000000, v201
	v_mul_f32_e32 v202, 0x43000000, v202
	v_mul_f32_e32 v203, 0x43000000, v203
	ds_write_b128 v210, v[200:203] offset:6144
	v_mul_f32_e32 v204, 0x43000000, v204
	v_mul_f32_e32 v205, 0x43000000, v205
	v_mul_f32_e32 v206, 0x43000000, v206
	v_mul_f32_e32 v207, 0x43000000, v207
	ds_write_b128 v210, v[204:207] offset:7168
	s_waitcnt lgkmcnt(0)
	s_barrier
; #define GAS __attribute__((address_space(1)))
; #define LAS __attribute__((address_space(3)))
; #define LDS_WAIT() asm volatile("s_waitcnt lgkmcnt(0)" ::: "memory")
; __device__ __forceinline__ int nat_dim(int p) { return (p >> 1) + 64 * (p & 1); }
; template <int MAP, bool KS, bool KPERM = false>
; __device__ __forceinline__ void p0_transpose_item(const float* W, int K, int Nsrc, int nblk, bf16* WT, const float* ksA, const float* ksB, int ksplit, LAS float* scr, int item, int lane) {
;     const int kb = item / nblk, nb = item % nblk, k0 = 64 * kb, n0 = 32 * nb;
;     const int nr = n0 + (lane & 31); const int sc = MAP == 1 ? src_col_in(nr) : (MAP == 2 ? nat_dim(nr) : nr);
;     float v[32];
; #pragma unroll
;     for (int i = 0; i < 32; ++i) { const int k = k0 + 2 * i + (lane >> 5); const int ksrc = KPERM ? ((k & ~127) + nat_dim(k & 127)) : k;
;         v[i] = sc >= 0 ? W[(size_t)ksrc * Nsrc + sc] : 0.f; }
; #pragma unroll
;     for (int i = 0; i < 32; ++i) { const int kk = 2 * i + (lane >> 5); const int k = k0 + kk;
;         if (KS) v[i] *= (k < ksplit ? ksA[k] : ksB[k - ksplit]);
;         scr[kk * 33 + (lane & 31)] = v[i]; }
;     const int pr = item >> 1, kb = 2 * (pr / nblk) + (item & 1), nb = pr % nblk, k0 = 64 * kb, n0 = 32 * nb;
;     const int nr = n0 + (lane & 31); const int sc = MAP == 1 ? src_col_in(nr) : nr;
;     float v[32];
; #pragma unroll
;     for (int i = 0; i < 32; ++i) v[i] = sc >= 0 ? W[(size_t)(k0 + 2 * i + (lane >> 5)) * Nsrc + sc] : 0.f;
; #pragma unroll
;     for (int i = 0; i < 32; ++i) { const int k = k0 + 2 * i + (lane >> 5); float x = v[i] * wscale; if (KS) x *= (k < ksplit ? ksA[k] : ksB[k - ksplit]); scr[(2 * i + (lane >> 5)) * 33 + (lane & 31)] = x; }
;     LDS_WAIT(); asm volatile("" ::: "memory");
;     const int c = lane & 7;
; #pragma unroll
;     for (int j = 0; j < 4; ++j) { const int n = (lane >> 3) + 8 * j; const LAS float* s = scr + (8 * c) * 33 + n;
;         const unsigned long long o = (unsigned long long)pg8::pk4_fp8(s[0 * 33], s[1 * 33], s[2 * 33], s[3 * 33]) | ((unsigned long long)pg8::pk4_fp8(s[4 * 33], s[5 * 33], s[6 * 33], s[7 * 33]) << 32);
;         *(GAS unsigned long long*)(WT + (size_t)(n0 + n) * K + k0 + 8 * c) = o; }
;     LDS_WAIT(); asm volatile("" ::: "memory");
	s_add_i32 s24, s23, 8
	s_lshl_b32 s20, s24, 7
	s_cmp_lt_u32 s24, 40
	s_cselect_b32 s21, 0, 0x830
	s_cmp_lt_u32 s24, 72
	s_cselect_b32 s21, s21, 0xfffff030
	s_add_i32 s20, s20, s21
	s_lshl_b32 s20, s20, 2
	s_add_u32 s8, s46, s20
	s_addc_u32 s9, s47, 0
	global_load_dwordx4 v[176:179], v76, s[8:9]
	s_add_u32 s8, s8, 0x16280
	s_addc_u32 s9, s9, 0
	global_load_dwordx4 v[180:183], v76, s[8:9]
	s_add_u32 s8, s8, 0x16280
	s_addc_u32 s9, s9, 0
	global_load_dwordx4 v[184:187], v76, s[8:9]
	s_add_u32 s8, s8, 0x16280
	s_addc_u32 s9, s9, 0
	global_load_dwordx4 v[188:191], v76, s[8:9]
	s_add_u32 s8, s8, 0x16280
	s_addc_u32 s9, s9, 0
	global_load_dwordx4 v[192:195], v76, s[8:9]
	s_add_u32 s8, s8, 0x16280
	s_addc_u32 s9, s9, 0
	global_load_dwordx4 v[196:199], v76, s[8:9]
	s_add_u32 s8, s8, 0x16280
	s_addc_u32 s9, s9, 0
	global_load_dwordx4 v[200:203], v76, s[8:9]
	s_add_u32 s8, s8, 0x16280
	s_addc_u32 s9, s9, 0
	global_load_dwordx4 v[204:207], v76, s[8:9]
	s_add_u32 s6, s40, 0x3c00
	s_addc_u32 s7, s41, 0
	ds_read_b32 v226, v212
	ds_read_b32 v227, v212 offset:512
	ds_read_b32 v228, v212 offset:1024
	ds_read_b32 v229, v212 offset:1536
	ds_read_b32 v230, v212 offset:2048
	ds_read_b32 v231, v212 offset:2560
	ds_read_b32 v232, v212 offset:3072
	ds_read_b32 v233, v212 offset:3584
	ds_read_b32 v234, v212 offset:4096
	ds_read_b32 v235, v212 offset:4608
	ds_read_b32 v236, v212 offset:5120
	ds_read_b32 v237, v212 offset:5632
	ds_read_b32 v238, v212 offset:6144
	ds_read_b32 v239, v212 offset:6656
	ds_read_b32 v240, v212 offset:7168
	ds_read_b32 v241, v212 offset:7680
	s_waitcnt lgkmcnt(0)
	v_max_f32_e32 v226, v226, v226
	v_max_f32_e32 v227, v227, v227
	v_max_f32_e32 v228, v228, v228
	v_max_f32_e32 v229, v229, v229
	v_max_f32_e32 v230, v230, v230
	v_max_f32_e32 v231, v231, v231
	v_max_f32_e32 v232, v232, v232
	v_max_f32_e32 v233, v233, v233
	v_max_f32_e32 v234, v234, v234
	v_max_f32_e32 v235, v235, v235
	v_max_f32_e32 v236, v236, v236
	v_max_f32_e32 v237, v237, v237
	v_max_f32_e32 v238, v238, v238
	v_max_f32_e32 v239, v239, v239
	v_max_f32_e32 v240, v240, v240
	v_max_f32_e32 v241, v241, v241
	v_med3_f32 v226, v226, s62, v95
	v_med3_f32 v227, v227, s62, v95
	v_med3_f32 v228, v228, s62, v95
	v_med3_f32 v229, v229, s62, v95
	v_med3_f32 v230, v230, s62, v95
	v_med3_f32 v231, v231, s62, v95
	v_med3_f32 v232, v232, s62, v95
	v_med3_f32 v233, v233, s62, v95
	v_med3_f32 v234, v234, s62, v95
	v_med3_f32 v235, v235, s62, v95
	v_med3_f32 v236, v236, s62, v95
	v_med3_f32 v237, v237, s62, v95
	v_med3_f32 v238, v238, s62, v95
	v_med3_f32 v239, v239, s62, v95
	v_med3_f32 v240, v240, s62, v95
	v_med3_f32 v241, v241, s62, v95
	v_mov_b32_e32 v242, 0
	v_mov_b32_e32 v243, 0
	v_mov_b32_e32 v244, 0
	v_mov_b32_e32 v245, 0
	v_cvt_pk_fp8_f32 v242, v226, v227
	v_cvt_pk_fp8_f32 v243, v230, v231
	v_cvt_pk_fp8_f32 v244, v234, v235
	v_cvt_pk_fp8_f32 v245, v238, v239
	v_cvt_pk_fp8_f32 v242, v228, v229 op_sel:[0,0,1]
	v_cvt_pk_fp8_f32 v243, v232, v233 op_sel:[0,0,1]
	v_cvt_pk_fp8_f32 v244, v236, v237 op_sel:[0,0,1]
	v_cvt_pk_fp8_f32 v245, v240, v241 op_sel:[0,0,1]
	s_nop 0
	global_store_dwordx4 v79, v[242:245], s[6:7]
	ds_read_b32 v226, v214
	ds_read_b32 v227, v214 offset:512
	ds_read_b32 v228, v214 offset:1024
	ds_read_b32 v229, v214 offset:1536
	ds_read_b32 v230, v214 offset:2048
	ds_read_b32 v231, v214 offset:2560
	ds_read_b32 v232, v214 offset:3072
	ds_read_b32 v233, v214 offset:3584
	ds_read_b32 v234, v214 offset:4096
	ds_read_b32 v235, v214 offset:4608
	ds_read_b32 v236, v214 offset:5120
	ds_read_b32 v237, v214 offset:5632
	ds_read_b32 v238, v214 offset:6144
	ds_read_b32 v239, v214 offset:6656
	ds_read_b32 v240, v214 offset:7168
	ds_read_b32 v241, v214 offset:7680
	s_waitcnt lgkmcnt(0)
	v_max_f32_e32 v226, v226, v226
	v_max_f32_e32 v227, v227, v227
	v_max_f32_e32 v228, v228, v228
	v_max_f32_e32 v229, v229, v229
	v_max_f32_e32 v230, v230, v230
	v_max_f32_e32 v231, v231, v231
	v_max_f32_e32 v232, v232, v232
	v_max_f32_e32 v233, v233, v233
	v_max_f32_e32 v234, v234, v234
	v_max_f32_e32 v235, v235, v235
	v_max_f32_e32 v236, v236, v236
	v_max_f32_e32 v237, v237, v237
	v_max_f32_e32 v238, v238, v238
	v_max_f32_e32 v239, v239, v239
	v_max_f32_e32 v240, v240, v240
	v_max_f32_e32 v241, v241, v241
	v_med3_f32 v226, v226, s62, v95
	v_med3_f32 v227, v227, s62, v95
	v_med3_f32 v228, v228, s62, v95
	v_med3_f32 v229, v229, s62, v95
	v_med3_f32 v230, v230, s62, v95
	v_med3_f32 v231, v231, s62, v95
	v_med3_f32 v232, v232, s62, v95
	v_med3_f32 v233, v233, s62, v95
	v_med3_f32 v234, v234, s62, v95
	v_med3_f32 v235, v235, s62, v95
	v_med3_f32 v236, v236, s62, v95
	v_med3_f32 v237, v237, s62, v95
	v_med3_f32 v238, v238, s62, v95
	v_med3_f32 v239, v239, s62, v95
	v_med3_f32 v240, v240, s62, v95
	v_med3_f32 v241, v241, s62, v95
	v_mov_b32_e32 v242, 0
	v_mov_b32_e32 v243, 0
	v_mov_b32_e32 v244, 0
	v_mov_b32_e32 v245, 0
	v_cvt_pk_fp8_f32 v242, v226, v227
	v_cvt_pk_fp8_f32 v243, v230, v231
	v_cvt_pk_fp8_f32 v244, v234, v235
	v_cvt_pk_fp8_f32 v245, v238, v239
	v_cvt_pk_fp8_f32 v242, v228, v229 op_sel:[0,0,1]
	v_cvt_pk_fp8_f32 v243, v232, v233 op_sel:[0,0,1]
	v_cvt_pk_fp8_f32 v244, v236, v237 op_sel:[0,0,1]
	v_cvt_pk_fp8_f32 v245, v240, v241 op_sel:[0,0,1]
	s_nop 0
	global_store_dwordx4 v80, v[242:245], s[6:7]
	s_waitcnt vmcnt(12)
	v_mul_f32_e32 v144, v42, v144
	v_mul_f32_e32 v145, v42, v145
	v_mul_f32_e32 v146, v42, v146
	v_mul_f32_e32 v147, v42, v147
	ds_write_b128 v209, v[144:147]
	v_mul_f32_e32 v148, v43, v148
	v_mul_f32_e32 v149, v43, v149
	v_mul_f32_e32 v150, v43, v150
	v_mul_f32_e32 v151, v43, v151
	ds_write_b128 v209, v[148:151] offset:1024
	v_mul_f32_e32 v152, v44, v152
	v_mul_f32_e32 v153, v44, v153
	v_mul_f32_e32 v154, v44, v154
	v_mul_f32_e32 v155, v44, v155
	ds_write_b128 v209, v[152:155] offset:2048
	v_mul_f32_e32 v156, v45, v156
	v_mul_f32_e32 v157, v45, v157
	v_mul_f32_e32 v158, v45, v158
	v_mul_f32_e32 v159, v45, v159
	ds_write_b128 v209, v[156:159] offset:3072
	v_mul_f32_e32 v160, v46, v160
	v_mul_f32_e32 v161, v46, v161
	v_mul_f32_e32 v162, v46, v162
	v_mul_f32_e32 v163, v46, v163
	ds_write_b128 v209, v[160:163] offset:4096
	v_mul_f32_e32 v164, v47, v164
	v_mul_f32_e32 v165, v47, v165
	v_mul_f32_e32 v166, v47, v166
	v_mul_f32_e32 v167, v47, v167
	ds_write_b128 v209, v[164:167] offset:5120
	v_mul_f32_e32 v168, v48, v168
	v_mul_f32_e32 v169, v48, v169
	v_mul_f32_e32 v170, v48, v170
	v_mul_f32_e32 v171, v48, v171
	ds_write_b128 v209, v[168:171] offset:6144
	v_mul_f32_e32 v172, v49, v172
	v_mul_f32_e32 v173, v49, v173
	v_mul_f32_e32 v174, v49, v174
	v_mul_f32_e32 v175, v49, v175
	ds_write_b128 v209, v[172:175] offset:7168
	s_waitcnt lgkmcnt(0)
	s_barrier
; #define GAS __attribute__((address_space(1)))
; #define LAS __attribute__((address_space(3)))
; #define LDS_WAIT() asm volatile("s_waitcnt lgkmcnt(0)" ::: "memory")
; __device__ __forceinline__ unsigned pk2(float lo, float hi) { return f2bf(lo) | (f2bf(hi) << 16); }
; __device__ __forceinline__ int nat_dim(int p) { return (p >> 1) + 64 * (p & 1); }
; __device__ __forceinline__ int src_col_in(int c) {
;     if (c < 5120) { const int blk = c >> 7, p = c & 127; const bool rope = blk < 16 || ((((blk - 16) >> 2) & 1) == 0); const int d = rope ? (p >> 1) + 64 * (p & 1) : p; return blk * 128 + d; }
;     if (c < OFF_Z) return c + 2096;
; template <int MAP, bool KS, bool KPERM = false>
; __device__ __forceinline__ void p0_transpose_item(const float* W, int K, int Nsrc, int nblk, bf16* WT, const float* ksA, const float* ksB, int ksplit, LAS float* scr, int item, int lane) {
;     const int kb = item / nblk, nb = item % nblk, k0 = 64 * kb, n0 = 32 * nb;
;     const int nr = n0 + (lane & 31); const int sc = MAP == 1 ? src_col_in(nr) : (MAP == 2 ? nat_dim(nr) : nr);
;     float v[32];
; #pragma unroll
;     for (int i = 0; i < 32; ++i) { const int k = k0 + 2 * i + (lane >> 5); const int ksrc = KPERM ? ((k & ~127) + nat_dim(k & 127)) : k;
;         v[i] = sc >= 0 ? W[(size_t)ksrc * Nsrc + sc] : 0.f; }
; #pragma unroll
;     for (int i = 0; i < 32; ++i) { const int kk = 2 * i + (lane >> 5); const int k = k0 + kk;
;         if (KS) v[i] *= (k < ksplit ? ksA[k] : ksB[k - ksplit]);
;         scr[kk * 33 + (lane & 31)] = v[i]; }
;     LDS_WAIT(); asm volatile("" ::: "memory");
;     const int c = lane & 7;
; #pragma unroll
;     for (int j = 0; j < 4; ++j) { const int n = (lane >> 3) + 8 * j; const LAS float* s = scr + (8 * c) * 33 + n;
;         v4u o; o.x = pk2(s[0 * 33], s[1 * 33]); o.y = pk2(s[2 * 33], s[3 * 33]); o.z = pk2(s[4 * 33], s[5 * 33]); o.w = pk2(s[6 * 33], s[7 * 33]);
;         *(GAS v4u*)(WT + (size_t)(n0 + n) * K + k0 + 8 * c) = o; }
;     LDS_WAIT(); asm volatile("" ::: "memory");
	s_add_i32 s24, s23, 16
	s_lshl_b32 s20, s24, 7
	s_cmp_lt_u32 s24, 40
	s_cselect_b32 s21, 0, 0x830
	s_cmp_lt_u32 s24, 72
	s_cselect_b32 s21, s21, 0xfffff030
	s_add_i32 s20, s20, s21
	s_lshl_b32 s20, s20, 2
	s_add_u32 s8, s46, s20
	s_addc_u32 s9, s47, 0
	global_load_dwordx4 v[144:147], v76, s[8:9]
	s_add_u32 s8, s8, 0x16280
	s_addc_u32 s9, s9, 0
	global_load_dwordx4 v[148:151], v76, s[8:9]
	s_add_u32 s8, s8, 0x16280
	s_addc_u32 s9, s9, 0
	global_load_dwordx4 v[152:155], v76, s[8:9]
	s_add_u32 s8, s8, 0x16280
	s_addc_u32 s9, s9, 0
	global_load_dwordx4 v[156:159], v76, s[8:9]
	s_add_u32 s8, s8, 0x16280
	s_addc_u32 s9, s9, 0
	global_load_dwordx4 v[160:163], v76, s[8:9]
	s_add_u32 s8, s8, 0x16280
	s_addc_u32 s9, s9, 0
	global_load_dwordx4 v[164:167], v76, s[8:9]
	s_add_u32 s8, s8, 0x16280
	s_addc_u32 s9, s9, 0
	global_load_dwordx4 v[168:171], v76, s[8:9]
	s_add_u32 s8, s8, 0x16280
	s_addc_u32 s9, s9, 0
	global_load_dwordx4 v[172:175], v76, s[8:9]
	s_add_i32 s24, s23, 0
	s_mul_i32 s20, s24, 0x100000
	s_add_u32 s6, s48, s20
	s_addc_u32 s7, s49, 0
	s_cmp_lt_u32 s24, 16
	s_cselect_b32 s20, 1, 0
	s_sub_i32 s21, s24, 16
	s_bitcmp0_b32 s21, 2
	s_cselect_b32 s21, 1, 0
	s_cmp_lt_u32 s24, 40
	s_cselect_b32 s21, s21, 0
	s_or_b32 s20, s20, s21
	s_cmp_lg_u32 s20, 0
	s_cselect_b64 s[20:21], -1, 0
	v_cndmask_b32_e64 v91, v83, v87, s[20:21]
	v_cndmask_b32_e64 v92, v84, v88, s[20:21]
	v_cndmask_b32_e64 v93, v85, v89, s[20:21]
	v_cndmask_b32_e64 v94, v86, v90, s[20:21]
	ds_read_b32 v226, v112
	ds_read_b32 v227, v112 offset:512
	ds_read_b32 v228, v112 offset:1024
	ds_read_b32 v229, v112 offset:1536
	ds_read_b32 v230, v112 offset:2048
	ds_read_b32 v231, v112 offset:2560
	ds_read_b32 v232, v112 offset:3072
	ds_read_b32 v233, v112 offset:3584
	s_waitcnt lgkmcnt(0)
	v_bfe_u32 v120, v226, 16, 1
	v_bfe_u32 v121, v227, 16, 1
	v_bfe_u32 v122, v228, 16, 1
	v_bfe_u32 v123, v229, 16, 1
	v_bfe_u32 v124, v230, 16, 1
	v_bfe_u32 v125, v231, 16, 1
	v_bfe_u32 v126, v232, 16, 1
	v_bfe_u32 v127, v233, 16, 1
	v_add3_u32 v226, v226, v120, s63
	v_add3_u32 v227, v227, v121, s63
	v_add3_u32 v228, v228, v122, s63
	v_add3_u32 v229, v229, v123, s63
	v_add3_u32 v230, v230, v124, s63
	v_add3_u32 v231, v231, v125, s63
	v_add3_u32 v232, v232, v126, s63
	v_add3_u32 v233, v233, v127, s63
	v_perm_b32 v242, v227, v226, s64
	v_perm_b32 v243, v229, v228, s64
	v_perm_b32 v244, v231, v230, s64
	v_perm_b32 v245, v233, v232, s64
	s_nop 0
	global_store_dwordx4 v91, v[242:245], s[6:7]
	ds_read_b32 v226, v114
	ds_read_b32 v227, v114 offset:512
	ds_read_b32 v228, v114 offset:1024
	ds_read_b32 v229, v114 offset:1536
	ds_read_b32 v230, v114 offset:2048
	ds_read_b32 v231, v114 offset:2560
	ds_read_b32 v232, v114 offset:3072
	ds_read_b32 v233, v114 offset:3584
	s_waitcnt lgkmcnt(0)
	v_bfe_u32 v120, v226, 16, 1
	v_bfe_u32 v121, v227, 16, 1
	v_bfe_u32 v122, v228, 16, 1
	v_bfe_u32 v123, v229, 16, 1
	v_bfe_u32 v124, v230, 16, 1
	v_bfe_u32 v125, v231, 16, 1
	v_bfe_u32 v126, v232, 16, 1
	v_bfe_u32 v127, v233, 16, 1
	v_add3_u32 v226, v226, v120, s63
	v_add3_u32 v227, v227, v121, s63
	v_add3_u32 v228, v228, v122, s63
	v_add3_u32 v229, v229, v123, s63
	v_add3_u32 v230, v230, v124, s63
	v_add3_u32 v231, v231, v125, s63
	v_add3_u32 v232, v232, v126, s63
	v_add3_u32 v233, v233, v127, s63
	v_perm_b32 v242, v227, v226, s64
	v_perm_b32 v243, v229, v228, s64
	v_perm_b32 v244, v231, v230, s64
	v_perm_b32 v245, v233, v232, s64
	s_nop 0
	global_store_dwordx4 v92, v[242:245], s[6:7]
	ds_read_b32 v226, v116
	ds_read_b32 v227, v116 offset:512
	ds_read_b32 v228, v116 offset:1024
	ds_read_b32 v229, v116 offset:1536
	ds_read_b32 v230, v116 offset:2048
	ds_read_b32 v231, v116 offset:2560
	ds_read_b32 v232, v116 offset:3072
	ds_read_b32 v233, v116 offset:3584
	s_waitcnt lgkmcnt(0)
	v_bfe_u32 v120, v226, 16, 1
	v_bfe_u32 v121, v227, 16, 1
	v_bfe_u32 v122, v228, 16, 1
	v_bfe_u32 v123, v229, 16, 1
	v_bfe_u32 v124, v230, 16, 1
	v_bfe_u32 v125, v231, 16, 1
	v_bfe_u32 v126, v232, 16, 1
	v_bfe_u32 v127, v233, 16, 1
	v_add3_u32 v226, v226, v120, s63
	v_add3_u32 v227, v227, v121, s63
	v_add3_u32 v228, v228, v122, s63
	v_add3_u32 v229, v229, v123, s63
	v_add3_u32 v230, v230, v124, s63
	v_add3_u32 v231, v231, v125, s63
	v_add3_u32 v232, v232, v126, s63
	v_add3_u32 v233, v233, v127, s63
	v_perm_b32 v242, v227, v226, s64
	v_perm_b32 v243, v229, v228, s64
	v_perm_b32 v244, v231, v230, s64
	v_perm_b32 v245, v233, v232, s64
	s_nop 0
	global_store_dwordx4 v93, v[242:245], s[6:7]
	ds_read_b32 v226, v118
	ds_read_b32 v227, v118 offset:512
	ds_read_b32 v228, v118 offset:1024
	ds_read_b32 v229, v118 offset:1536
	ds_read_b32 v230, v118 offset:2048
	ds_read_b32 v231, v118 offset:2560
	ds_read_b32 v232, v118 offset:3072
	ds_read_b32 v233, v118 offset:3584
	s_waitcnt lgkmcnt(0)
	v_bfe_u32 v120, v226, 16, 1
	v_bfe_u32 v121, v227, 16, 1
	v_bfe_u32 v122, v228, 16, 1
	v_bfe_u32 v123, v229, 16, 1
	v_bfe_u32 v124, v230, 16, 1
	v_bfe_u32 v125, v231, 16, 1
	v_bfe_u32 v126, v232, 16, 1
	v_bfe_u32 v127, v233, 16, 1
	v_add3_u32 v226, v226, v120, s63
	v_add3_u32 v227, v227, v121, s63
	v_add3_u32 v228, v228, v122, s63
	v_add3_u32 v229, v229, v123, s63
	v_add3_u32 v230, v230, v124, s63
	v_add3_u32 v231, v231, v125, s63
	v_add3_u32 v232, v232, v126, s63
	v_add3_u32 v233, v233, v127, s63
	v_perm_b32 v242, v227, v226, s64
	v_perm_b32 v243, v229, v228, s64
	v_perm_b32 v244, v231, v230, s64
	v_perm_b32 v245, v233, v232, s64
	s_nop 0
	global_store_dwordx4 v94, v[242:245], s[6:7]
	s_waitcnt vmcnt(14)
	v_mul_f32_e32 v176, v42, v176
	v_mul_f32_e32 v177, v42, v177
	v_mul_f32_e32 v178, v42, v178
	v_mul_f32_e32 v179, v42, v179
	ds_write_b128 v210, v[176:179]
	v_mul_f32_e32 v180, v43, v180
	v_mul_f32_e32 v181, v43, v181
	v_mul_f32_e32 v182, v43, v182
	v_mul_f32_e32 v183, v43, v183
	ds_write_b128 v210, v[180:183] offset:1024
	v_mul_f32_e32 v184, v44, v184
	v_mul_f32_e32 v185, v44, v185
	v_mul_f32_e32 v186, v44, v186
	v_mul_f32_e32 v187, v44, v187
	ds_write_b128 v210, v[184:187] offset:2048
	v_mul_f32_e32 v188, v45, v188
	v_mul_f32_e32 v189, v45, v189
	v_mul_f32_e32 v190, v45, v190
	v_mul_f32_e32 v191, v45, v191
	ds_write_b128 v210, v[188:191] offset:3072
	v_mul_f32_e32 v192, v46, v192
	v_mul_f32_e32 v193, v46, v193
	v_mul_f32_e32 v194, v46, v194
	v_mul_f32_e32 v195, v46, v195
	ds_write_b128 v210, v[192:195] offset:4096
	v_mul_f32_e32 v196, v47, v196
	v_mul_f32_e32 v197, v47, v197
	v_mul_f32_e32 v198, v47, v198
	v_mul_f32_e32 v199, v47, v199
	ds_write_b128 v210, v[196:199] offset:5120
	v_mul_f32_e32 v200, v48, v200
	v_mul_f32_e32 v201, v48, v201
	v_mul_f32_e32 v202, v48, v202
	v_mul_f32_e32 v203, v48, v203
	ds_write_b128 v210, v[200:203] offset:6144
	v_mul_f32_e32 v204, v49, v204
	v_mul_f32_e32 v205, v49, v205
	v_mul_f32_e32 v206, v49, v206
	v_mul_f32_e32 v207, v49, v207
	ds_write_b128 v210, v[204:207] offset:7168
	s_waitcnt lgkmcnt(0)
	s_barrier
; #define GAS __attribute__((address_space(1)))
; #define LAS __attribute__((address_space(3)))
; #define LDS_WAIT() asm volatile("s_waitcnt lgkmcnt(0)" ::: "memory")
; __device__ __forceinline__ unsigned pk2(float lo, float hi) { return f2bf(lo) | (f2bf(hi) << 16); }
; __device__ __forceinline__ int nat_dim(int p) { return (p >> 1) + 64 * (p & 1); }
; __device__ __forceinline__ int src_col_in(int c) {
;     if (c < 5120) { const int blk = c >> 7, p = c & 127; const bool rope = blk < 16 || ((((blk - 16) >> 2) & 1) == 0); const int d = rope ? (p >> 1) + 64 * (p & 1) : p; return blk * 128 + d; }
;     if (c < OFF_Z) return c + 2096;
; template <int MAP, bool KS, bool KPERM = false>
; __device__ __forceinline__ void p0_transpose_item(const float* W, int K, int Nsrc, int nblk, bf16* WT, const float* ksA, const float* ksB, int ksplit, LAS float* scr, int item, int lane) {
;     const int kb = item / nblk, nb = item % nblk, k0 = 64 * kb, n0 = 32 * nb;
;     const int nr = n0 + (lane & 31); const int sc = MAP == 1 ? src_col_in(nr) : (MAP == 2 ? nat_dim(nr) : nr);
;     float v[32];
; #pragma unroll
;     for (int i = 0; i < 32; ++i) { const int k = k0 + 2 * i + (lane >> 5); const int ksrc = KPERM ? ((k & ~127) + nat_dim(k & 127)) : k;
;         v[i] = sc >= 0 ? W[(size_t)ksrc * Nsrc + sc] : 0.f; }
; #pragma unroll
;     for (int i = 0; i < 32; ++i) { const int kk = 2 * i + (lane >> 5); const int k = k0 + kk;
;         if (KS) v[i] *= (k < ksplit ? ksA[k] : ksB[k - ksplit]);
;         scr[kk * 33 + (lane & 31)] = v[i]; }
;     LDS_WAIT(); asm volatile("" ::: "memory");
;     const int c = lane & 7;
; #pragma unroll
;     for (int j = 0; j < 4; ++j) { const int n = (lane >> 3) + 8 * j; const LAS float* s = scr + (8 * c) * 33 + n;
;         v4u o; o.x = pk2(s[0 * 33], s[1 * 33]); o.y = pk2(s[2 * 33], s[3 * 33]); o.z = pk2(s[4 * 33], s[5 * 33]); o.w = pk2(s[6 * 33], s[7 * 33]);
;         *(GAS v4u*)(WT + (size_t)(n0 + n) * K + k0 + 8 * c) = o; }
;     LDS_WAIT(); asm volatile("" ::: "memory");
	s_add_i32 s24, s23, 24
	s_lshl_b32 s20, s24, 7
	s_cmp_lt_u32 s24, 40
	s_cselect_b32 s21, 0, 0x830
	s_cmp_lt_u32 s24, 72
	s_cselect_b32 s21, s21, 0xfffff030
	s_add_i32 s20, s20, s21
	s_lshl_b32 s20, s20, 2
	s_add_u32 s8, s46, s20
	s_addc_u32 s9, s47, 0
	global_load_dwordx4 v[176:179], v76, s[8:9]
	s_add_u32 s8, s8, 0x16280
	s_addc_u32 s9, s9, 0
	global_load_dwordx4 v[180:183], v76, s[8:9]
	s_add_u32 s8, s8, 0x16280
	s_addc_u32 s9, s9, 0
	global_load_dwordx4 v[184:187], v76, s[8:9]
	s_add_u32 s8, s8, 0x16280
	s_addc_u32 s9, s9, 0
	global_load_dwordx4 v[188:191], v76, s[8:9]
	s_add_u32 s8, s8, 0x16280
	s_addc_u32 s9, s9, 0
	global_load_dwordx4 v[192:195], v76, s[8:9]
	s_add_u32 s8, s8, 0x16280
	s_addc_u32 s9, s9, 0
	global_load_dwordx4 v[196:199], v76, s[8:9]
	s_add_u32 s8, s8, 0x16280
	s_addc_u32 s9, s9, 0
	global_load_dwordx4 v[200:203], v76, s[8:9]
	s_add_u32 s8, s8, 0x16280
	s_addc_u32 s9, s9, 0
	global_load_dwordx4 v[204:207], v76, s[8:9]
	s_add_i32 s24, s23, 8
	s_mul_i32 s20, s24, 0x100000
	s_add_u32 s6, s48, s20
	s_addc_u32 s7, s49, 0
	s_cmp_lt_u32 s24, 16
	s_cselect_b32 s20, 1, 0
	s_sub_i32 s21, s24, 16
	s_bitcmp0_b32 s21, 2
	s_cselect_b32 s21, 1, 0
	s_cmp_lt_u32 s24, 40
	s_cselect_b32 s21, s21, 0
	s_or_b32 s20, s20, s21
	s_cmp_lg_u32 s20, 0
	s_cselect_b64 s[20:21], -1, 0
	v_cndmask_b32_e64 v91, v83, v87, s[20:21]
	v_cndmask_b32_e64 v92, v84, v88, s[20:21]
	v_cndmask_b32_e64 v93, v85, v89, s[20:21]
	v_cndmask_b32_e64 v94, v86, v90, s[20:21]
	ds_read_b32 v226, v113
	ds_read_b32 v227, v113 offset:512
	ds_read_b32 v228, v113 offset:1024
	ds_read_b32 v229, v113 offset:1536
	ds_read_b32 v230, v113 offset:2048
	ds_read_b32 v231, v113 offset:2560
	ds_read_b32 v232, v113 offset:3072
	ds_read_b32 v233, v113 offset:3584
	s_waitcnt lgkmcnt(0)
	v_bfe_u32 v120, v226, 16, 1
	v_bfe_u32 v121, v227, 16, 1
	v_bfe_u32 v122, v228, 16, 1
	v_bfe_u32 v123, v229, 16, 1
	v_bfe_u32 v124, v230, 16, 1
	v_bfe_u32 v125, v231, 16, 1
	v_bfe_u32 v126, v232, 16, 1
	v_bfe_u32 v127, v233, 16, 1
	v_add3_u32 v226, v226, v120, s63
	v_add3_u32 v227, v227, v121, s63
	v_add3_u32 v228, v228, v122, s63
	v_add3_u32 v229, v229, v123, s63
	v_add3_u32 v230, v230, v124, s63
	v_add3_u32 v231, v231, v125, s63
	v_add3_u32 v232, v232, v126, s63
	v_add3_u32 v233, v233, v127, s63
	v_perm_b32 v242, v227, v226, s64
	v_perm_b32 v243, v229, v228, s64
	v_perm_b32 v244, v231, v230, s64
	v_perm_b32 v245, v233, v232, s64
	s_nop 0
	global_store_dwordx4 v91, v[242:245], s[6:7]
	ds_read_b32 v226, v115
	ds_read_b32 v227, v115 offset:512
	ds_read_b32 v228, v115 offset:1024
	ds_read_b32 v229, v115 offset:1536
	ds_read_b32 v230, v115 offset:2048
	ds_read_b32 v231, v115 offset:2560
	ds_read_b32 v232, v115 offset:3072
	ds_read_b32 v233, v115 offset:3584
	s_waitcnt lgkmcnt(0)
	v_bfe_u32 v120, v226, 16, 1
	v_bfe_u32 v121, v227, 16, 1
	v_bfe_u32 v122, v228, 16, 1
	v_bfe_u32 v123, v229, 16, 1
	v_bfe_u32 v124, v230, 16, 1
	v_bfe_u32 v125, v231, 16, 1
	v_bfe_u32 v126, v232, 16, 1
	v_bfe_u32 v127, v233, 16, 1
	v_add3_u32 v226, v226, v120, s63
	v_add3_u32 v227, v227, v121, s63
	v_add3_u32 v228, v228, v122, s63
	v_add3_u32 v229, v229, v123, s63
	v_add3_u32 v230, v230, v124, s63
	v_add3_u32 v231, v231, v125, s63
	v_add3_u32 v232, v232, v126, s63
	v_add3_u32 v233, v233, v127, s63
	v_perm_b32 v242, v227, v226, s64
	v_perm_b32 v243, v229, v228, s64
	v_perm_b32 v244, v231, v230, s64
	v_perm_b32 v245, v233, v232, s64
	s_nop 0
	global_store_dwordx4 v92, v[242:245], s[6:7]
	ds_read_b32 v226, v117
	ds_read_b32 v227, v117 offset:512
	ds_read_b32 v228, v117 offset:1024
	ds_read_b32 v229, v117 offset:1536
	ds_read_b32 v230, v117 offset:2048
	ds_read_b32 v231, v117 offset:2560
	ds_read_b32 v232, v117 offset:3072
	ds_read_b32 v233, v117 offset:3584
	s_waitcnt lgkmcnt(0)
	v_bfe_u32 v120, v226, 16, 1
	v_bfe_u32 v121, v227, 16, 1
	v_bfe_u32 v122, v228, 16, 1
	v_bfe_u32 v123, v229, 16, 1
	v_bfe_u32 v124, v230, 16, 1
	v_bfe_u32 v125, v231, 16, 1
	v_bfe_u32 v126, v232, 16, 1
	v_bfe_u32 v127, v233, 16, 1
	v_add3_u32 v226, v226, v120, s63
	v_add3_u32 v227, v227, v121, s63
	v_add3_u32 v228, v228, v122, s63
	v_add3_u32 v229, v229, v123, s63
	v_add3_u32 v230, v230, v124, s63
	v_add3_u32 v231, v231, v125, s63
	v_add3_u32 v232, v232, v126, s63
	v_add3_u32 v233, v233, v127, s63
	v_perm_b32 v242, v227, v226, s64
	v_perm_b32 v243, v229, v228, s64
	v_perm_b32 v244, v231, v230, s64
	v_perm_b32 v245, v233, v232, s64
	s_nop 0
	global_store_dwordx4 v93, v[242:245], s[6:7]
	ds_read_b32 v226, v119
	ds_read_b32 v227, v119 offset:512
	ds_read_b32 v228, v119 offset:1024
	ds_read_b32 v229, v119 offset:1536
	ds_read_b32 v230, v119 offset:2048
	ds_read_b32 v231, v119 offset:2560
	ds_read_b32 v232, v119 offset:3072
	ds_read_b32 v233, v119 offset:3584
	s_waitcnt lgkmcnt(0)
	v_bfe_u32 v120, v226, 16, 1
	v_bfe_u32 v121, v227, 16, 1
	v_bfe_u32 v122, v228, 16, 1
	v_bfe_u32 v123, v229, 16, 1
	v_bfe_u32 v124, v230, 16, 1
	v_bfe_u32 v125, v231, 16, 1
	v_bfe_u32 v126, v232, 16, 1
	v_bfe_u32 v127, v233, 16, 1
	v_add3_u32 v226, v226, v120, s63
	v_add3_u32 v227, v227, v121, s63
	v_add3_u32 v228, v228, v122, s63
	v_add3_u32 v229, v229, v123, s63
	v_add3_u32 v230, v230, v124, s63
	v_add3_u32 v231, v231, v125, s63
	v_add3_u32 v232, v232, v126, s63
	v_add3_u32 v233, v233, v127, s63
	v_perm_b32 v242, v227, v226, s64
	v_perm_b32 v243, v229, v228, s64
	v_perm_b32 v244, v231, v230, s64
	v_perm_b32 v245, v233, v232, s64
	s_nop 0
	global_store_dwordx4 v94, v[242:245], s[6:7]
	s_waitcnt vmcnt(16)
	v_mul_f32_e32 v144, v42, v144
	v_mul_f32_e32 v145, v42, v145
	v_mul_f32_e32 v146, v42, v146
	v_mul_f32_e32 v147, v42, v147
	ds_write_b128 v209, v[144:147]
	v_mul_f32_e32 v148, v43, v148
	v_mul_f32_e32 v149, v43, v149
	v_mul_f32_e32 v150, v43, v150
	v_mul_f32_e32 v151, v43, v151
	ds_write_b128 v209, v[148:151] offset:1024
	v_mul_f32_e32 v152, v44, v152
	v_mul_f32_e32 v153, v44, v153
	v_mul_f32_e32 v154, v44, v154
	v_mul_f32_e32 v155, v44, v155
	ds_write_b128 v209, v[152:155] offset:2048
	v_mul_f32_e32 v156, v45, v156
	v_mul_f32_e32 v157, v45, v157
	v_mul_f32_e32 v158, v45, v158
	v_mul_f32_e32 v159, v45, v159
	ds_write_b128 v209, v[156:159] offset:3072
	v_mul_f32_e32 v160, v46, v160
	v_mul_f32_e32 v161, v46, v161
	v_mul_f32_e32 v162, v46, v162
	v_mul_f32_e32 v163, v46, v163
	ds_write_b128 v209, v[160:163] offset:4096
	v_mul_f32_e32 v164, v47, v164
	v_mul_f32_e32 v165, v47, v165
	v_mul_f32_e32 v166, v47, v166
	v_mul_f32_e32 v167, v47, v167
	ds_write_b128 v209, v[164:167] offset:5120
	v_mul_f32_e32 v168, v48, v168
	v_mul_f32_e32 v169, v48, v169
	v_mul_f32_e32 v170, v48, v170
	v_mul_f32_e32 v171, v48, v171
	ds_write_b128 v209, v[168:171] offset:6144
	v_mul_f32_e32 v172, v49, v172
	v_mul_f32_e32 v173, v49, v173
	v_mul_f32_e32 v174, v49, v174
	v_mul_f32_e32 v175, v49, v175
	ds_write_b128 v209, v[172:175] offset:7168
	s_waitcnt lgkmcnt(0)
	s_barrier
; #define GAS __attribute__((address_space(1)))
; #define LAS __attribute__((address_space(3)))
; #define LDS_WAIT() asm volatile("s_waitcnt lgkmcnt(0)" ::: "memory")
; __device__ __forceinline__ unsigned pk2(float lo, float hi) { return f2bf(lo) | (f2bf(hi) << 16); }
; __device__ __forceinline__ int nat_dim(int p) { return (p >> 1) + 64 * (p & 1); }
; __device__ __forceinline__ int src_col_in(int c) {
;     if (c < 5120) { const int blk = c >> 7, p = c & 127; const bool rope = blk < 16 || ((((blk - 16) >> 2) & 1) == 0); const int d = rope ? (p >> 1) + 64 * (p & 1) : p; return blk * 128 + d; }
;     if (c < OFF_Z) return c + 2096;
; template <int MAP, bool KS, bool KPERM = false>
; __device__ __forceinline__ void p0_transpose_item(const float* W, int K, int Nsrc, int nblk, bf16* WT, const float* ksA, const float* ksB, int ksplit, LAS float* scr, int item, int lane) {
;     const int kb = item / nblk, nb = item % nblk, k0 = 64 * kb, n0 = 32 * nb;
;     const int nr = n0 + (lane & 31); const int sc = MAP == 1 ? src_col_in(nr) : (MAP == 2 ? nat_dim(nr) : nr);
;     float v[32];
; #pragma unroll
;     for (int i = 0; i < 32; ++i) { const int k = k0 + 2 * i + (lane >> 5); const int ksrc = KPERM ? ((k & ~127) + nat_dim(k & 127)) : k;
;         v[i] = sc >= 0 ? W[(size_t)ksrc * Nsrc + sc] : 0.f; }
; #pragma unroll
;     for (int i = 0; i < 32; ++i) { const int kk = 2 * i + (lane >> 5); const int k = k0 + kk;
;         if (KS) v[i] *= (k < ksplit ? ksA[k] : ksB[k - ksplit]);
;         scr[kk * 33 + (lane & 31)] = v[i]; }
;     LDS_WAIT(); asm volatile("" ::: "memory");
;     const int c = lane & 7;
; #pragma unroll
;     for (int j = 0; j < 4; ++j) { const int n = (lane >> 3) + 8 * j; const LAS float* s = scr + (8 * c) * 33 + n;
;         v4u o; o.x = pk2(s[0 * 33], s[1 * 33]); o.y = pk2(s[2 * 33], s[3 * 33]); o.z = pk2(s[4 * 33], s[5 * 33]); o.w = pk2(s[6 * 33], s[7 * 33]);
;         *(GAS v4u*)(WT + (size_t)(n0 + n) * K + k0 + 8 * c) = o; }
;     LDS_WAIT(); asm volatile("" ::: "memory");
	s_add_i32 s24, s23, 32
	s_lshl_b32 s20, s24, 7
	s_cmp_lt_u32 s24, 40
	s_cselect_b32 s21, 0, 0x830
	s_cmp_lt_u32 s24, 72
	s_cselect_b32 s21, s21, 0xfffff030
	s_add_i32 s20, s20, s21
	s_lshl_b32 s20, s20, 2
	s_add_u32 s8, s46, s20
	s_addc_u32 s9, s47, 0
	global_load_dwordx4 v[144:147], v76, s[8:9]
	s_add_u32 s8, s8, 0x16280
	s_addc_u32 s9, s9, 0
	global_load_dwordx4 v[148:151], v76, s[8:9]
	s_add_u32 s8, s8, 0x16280
	s_addc_u32 s9, s9, 0
	global_load_dwordx4 v[152:155], v76, s[8:9]
	s_add_u32 s8, s8, 0x16280
	s_addc_u32 s9, s9, 0
	global_load_dwordx4 v[156:159], v76, s[8:9]
	s_add_u32 s8, s8, 0x16280
	s_addc_u32 s9, s9, 0
	global_load_dwordx4 v[160:163], v76, s[8:9]
	s_add_u32 s8, s8, 0x16280
	s_addc_u32 s9, s9, 0
	global_load_dwordx4 v[164:167], v76, s[8:9]
	s_add_u32 s8, s8, 0x16280
	s_addc_u32 s9, s9, 0
	global_load_dwordx4 v[168:171], v76, s[8:9]
	s_add_u32 s8, s8, 0x16280
	s_addc_u32 s9, s9, 0
	global_load_dwordx4 v[172:175], v76, s[8:9]
	s_add_i32 s24, s23, 16
	s_mul_i32 s20, s24, 0x100000
	s_add_u32 s6, s48, s20
	s_addc_u32 s7, s49, 0
	s_cmp_lt_u32 s24, 16
	s_cselect_b32 s20, 1, 0
	s_sub_i32 s21, s24, 16
	s_bitcmp0_b32 s21, 2
	s_cselect_b32 s21, 1, 0
	s_cmp_lt_u32 s24, 40
	s_cselect_b32 s21, s21, 0
	s_or_b32 s20, s20, s21
	s_cmp_lg_u32 s20, 0
	s_cselect_b64 s[20:21], -1, 0
	v_cndmask_b32_e64 v91, v83, v87, s[20:21]
	v_cndmask_b32_e64 v92, v84, v88, s[20:21]
	v_cndmask_b32_e64 v93, v85, v89, s[20:21]
	v_cndmask_b32_e64 v94, v86, v90, s[20:21]
	ds_read_b32 v226, v112
	ds_read_b32 v227, v112 offset:512
	ds_read_b32 v228, v112 offset:1024
	ds_read_b32 v229, v112 offset:1536
	ds_read_b32 v230, v112 offset:2048
	ds_read_b32 v231, v112 offset:2560
	ds_read_b32 v232, v112 offset:3072
	ds_read_b32 v233, v112 offset:3584
	s_waitcnt lgkmcnt(0)
	v_bfe_u32 v120, v226, 16, 1
	v_bfe_u32 v121, v227, 16, 1
	v_bfe_u32 v122, v228, 16, 1
	v_bfe_u32 v123, v229, 16, 1
	v_bfe_u32 v124, v230, 16, 1
	v_bfe_u32 v125, v231, 16, 1
	v_bfe_u32 v126, v232, 16, 1
	v_bfe_u32 v127, v233, 16, 1
	v_add3_u32 v226, v226, v120, s63
	v_add3_u32 v227, v227, v121, s63
	v_add3_u32 v228, v228, v122, s63
	v_add3_u32 v229, v229, v123, s63
	v_add3_u32 v230, v230, v124, s63
	v_add3_u32 v231, v231, v125, s63
	v_add3_u32 v232, v232, v126, s63
	v_add3_u32 v233, v233, v127, s63
	v_perm_b32 v242, v227, v226, s64
	v_perm_b32 v243, v229, v228, s64
	v_perm_b32 v244, v231, v230, s64
	v_perm_b32 v245, v233, v232, s64
	s_nop 0
	global_store_dwordx4 v91, v[242:245], s[6:7]
	ds_read_b32 v226, v114
	ds_read_b32 v227, v114 offset:512
	ds_read_b32 v228, v114 offset:1024
	ds_read_b32 v229, v114 offset:1536
	ds_read_b32 v230, v114 offset:2048
	ds_read_b32 v231, v114 offset:2560
	ds_read_b32 v232, v114 offset:3072
	ds_read_b32 v233, v114 offset:3584
	s_waitcnt lgkmcnt(0)
	v_bfe_u32 v120, v226, 16, 1
	v_bfe_u32 v121, v227, 16, 1
	v_bfe_u32 v122, v228, 16, 1
	v_bfe_u32 v123, v229, 16, 1
	v_bfe_u32 v124, v230, 16, 1
	v_bfe_u32 v125, v231, 16, 1
	v_bfe_u32 v126, v232, 16, 1
	v_bfe_u32 v127, v233, 16, 1
	v_add3_u32 v226, v226, v120, s63
	v_add3_u32 v227, v227, v121, s63
	v_add3_u32 v228, v228, v122, s63
	v_add3_u32 v229, v229, v123, s63
	v_add3_u32 v230, v230, v124, s63
	v_add3_u32 v231, v231, v125, s63
	v_add3_u32 v232, v232, v126, s63
	v_add3_u32 v233, v233, v127, s63
	v_perm_b32 v242, v227, v226, s64
	v_perm_b32 v243, v229, v228, s64
	v_perm_b32 v244, v231, v230, s64
	v_perm_b32 v245, v233, v232, s64
	s_nop 0
	global_store_dwordx4 v92, v[242:245], s[6:7]
	ds_read_b32 v226, v116
	ds_read_b32 v227, v116 offset:512
	ds_read_b32 v228, v116 offset:1024
	ds_read_b32 v229, v116 offset:1536
	ds_read_b32 v230, v116 offset:2048
	ds_read_b32 v231, v116 offset:2560
	ds_read_b32 v232, v116 offset:3072
	ds_read_b32 v233, v116 offset:3584
	s_waitcnt lgkmcnt(0)
	v_bfe_u32 v120, v226, 16, 1
	v_bfe_u32 v121, v227, 16, 1
	v_bfe_u32 v122, v228, 16, 1
	v_bfe_u32 v123, v229, 16, 1
	v_bfe_u32 v124, v230, 16, 1
	v_bfe_u32 v125, v231, 16, 1
	v_bfe_u32 v126, v232, 16, 1
	v_bfe_u32 v127, v233, 16, 1
	v_add3_u32 v226, v226, v120, s63
	v_add3_u32 v227, v227, v121, s63
	v_add3_u32 v228, v228, v122, s63
	v_add3_u32 v229, v229, v123, s63
	v_add3_u32 v230, v230, v124, s63
	v_add3_u32 v231, v231, v125, s63
	v_add3_u32 v232, v232, v126, s63
	v_add3_u32 v233, v233, v127, s63
	v_perm_b32 v242, v227, v226, s64
	v_perm_b32 v243, v229, v228, s64
	v_perm_b32 v244, v231, v230, s64
	v_perm_b32 v245, v233, v232, s64
	s_nop 0
	global_store_dwordx4 v93, v[242:245], s[6:7]
	ds_read_b32 v226, v118
	ds_read_b32 v227, v118 offset:512
	ds_read_b32 v228, v118 offset:1024
	ds_read_b32 v229, v118 offset:1536
	ds_read_b32 v230, v118 offset:2048
	ds_read_b32 v231, v118 offset:2560
	ds_read_b32 v232, v118 offset:3072
	ds_read_b32 v233, v118 offset:3584
	s_waitcnt lgkmcnt(0)
	v_bfe_u32 v120, v226, 16, 1
	v_bfe_u32 v121, v227, 16, 1
	v_bfe_u32 v122, v228, 16, 1
	v_bfe_u32 v123, v229, 16, 1
	v_bfe_u32 v124, v230, 16, 1
	v_bfe_u32 v125, v231, 16, 1
	v_bfe_u32 v126, v232, 16, 1
	v_bfe_u32 v127, v233, 16, 1
	v_add3_u32 v226, v226, v120, s63
	v_add3_u32 v227, v227, v121, s63
	v_add3_u32 v228, v228, v122, s63
	v_add3_u32 v229, v229, v123, s63
	v_add3_u32 v230, v230, v124, s63
	v_add3_u32 v231, v231, v125, s63
	v_add3_u32 v232, v232, v126, s63
	v_add3_u32 v233, v233, v127, s63
	v_perm_b32 v242, v227, v226, s64
	v_perm_b32 v243, v229, v228, s64
	v_perm_b32 v244, v231, v230, s64
	v_perm_b32 v245, v233, v232, s64
	s_nop 0
	global_store_dwordx4 v94, v[242:245], s[6:7]
	s_waitcnt vmcnt(16)
	v_mul_f32_e32 v176, v42, v176
	v_mul_f32_e32 v177, v42, v177
	v_mul_f32_e32 v178, v42, v178
	v_mul_f32_e32 v179, v42, v179
	ds_write_b128 v210, v[176:179]
	v_mul_f32_e32 v180, v43, v180
	v_mul_f32_e32 v181, v43, v181
	v_mul_f32_e32 v182, v43, v182
	v_mul_f32_e32 v183, v43, v183
	ds_write_b128 v210, v[180:183] offset:1024
	v_mul_f32_e32 v184, v44, v184
	v_mul_f32_e32 v185, v44, v185
	v_mul_f32_e32 v186, v44, v186
	v_mul_f32_e32 v187, v44, v187
	ds_write_b128 v210, v[184:187] offset:2048
	v_mul_f32_e32 v188, v45, v188
	v_mul_f32_e32 v189, v45, v189
	v_mul_f32_e32 v190, v45, v190
	v_mul_f32_e32 v191, v45, v191
	ds_write_b128 v210, v[188:191] offset:3072
	v_mul_f32_e32 v192, v46, v192
	v_mul_f32_e32 v193, v46, v193
	v_mul_f32_e32 v194, v46, v194
	v_mul_f32_e32 v195, v46, v195
	ds_write_b128 v210, v[192:195] offset:4096
	v_mul_f32_e32 v196, v47, v196
	v_mul_f32_e32 v197, v47, v197
	v_mul_f32_e32 v198, v47, v198
	v_mul_f32_e32 v199, v47, v199
	ds_write_b128 v210, v[196:199] offset:5120
	v_mul_f32_e32 v200, v48, v200
	v_mul_f32_e32 v201, v48, v201
	v_mul_f32_e32 v202, v48, v202
	v_mul_f32_e32 v203, v48, v203
	ds_write_b128 v210, v[200:203] offset:6144
	v_mul_f32_e32 v204, v49, v204
	v_mul_f32_e32 v205, v49, v205
	v_mul_f32_e32 v206, v49, v206
	v_mul_f32_e32 v207, v49, v207
	ds_write_b128 v210, v[204:207] offset:7168
	s_waitcnt lgkmcnt(0)
	s_barrier
; #define GAS __attribute__((address_space(1)))
; #define LAS __attribute__((address_space(3)))
; #define LDS_WAIT() asm volatile("s_waitcnt lgkmcnt(0)" ::: "memory")
; __device__ __forceinline__ unsigned pk2(float lo, float hi) { return f2bf(lo) | (f2bf(hi) << 16); }
; __device__ __forceinline__ int nat_dim(int p) { return (p >> 1) + 64 * (p & 1); }
; __device__ __forceinline__ int src_col_in(int c) {
;     if (c < 5120) { const int blk = c >> 7, p = c & 127; const bool rope = blk < 16 || ((((blk - 16) >> 2) & 1) == 0); const int d = rope ? (p >> 1) + 64 * (p & 1) : p; return blk * 128 + d; }
;     if (c < OFF_Z) return c + 2096;
; template <int MAP, bool KS, bool KPERM = false>
; __device__ __forceinline__ void p0_transpose_item(const float* W, int K, int Nsrc, int nblk, bf16* WT, const float* ksA, const float* ksB, int ksplit, LAS float* scr, int item, int lane) {
;     const int kb = item / nblk, nb = item % nblk, k0 = 64 * kb, n0 = 32 * nb;
;     const int nr = n0 + (lane & 31); const int sc = MAP == 1 ? src_col_in(nr) : (MAP == 2 ? nat_dim(nr) : nr);
;     float v[32];
; #pragma unroll
;     for (int i = 0; i < 32; ++i) { const int k = k0 + 2 * i + (lane >> 5); const int ksrc = KPERM ? ((k & ~127) + nat_dim(k & 127)) : k;
;         v[i] = sc >= 0 ? W[(size_t)ksrc * Nsrc + sc] : 0.f; }
; #pragma unroll
;     for (int i = 0; i < 32; ++i) { const int kk = 2 * i + (lane >> 5); const int k = k0 + kk;
;         if (KS) v[i] *= (k < ksplit ? ksA[k] : ksB[k - ksplit]);
;         scr[kk * 33 + (lane & 31)] = v[i]; }
;     LDS_WAIT(); asm volatile("" ::: "memory");
;     const int c = lane & 7;
; #pragma unroll
;     for (int j = 0; j < 4; ++j) { const int n = (lane >> 3) + 8 * j; const LAS float* s = scr + (8 * c) * 33 + n;
;         v4u o; o.x = pk2(s[0 * 33], s[1 * 33]); o.y = pk2(s[2 * 33], s[3 * 33]); o.z = pk2(s[4 * 33], s[5 * 33]); o.w = pk2(s[6 * 33], s[7 * 33]);
;         *(GAS v4u*)(WT + (size_t)(n0 + n) * K + k0 + 8 * c) = o; }
;     LDS_WAIT(); asm volatile("" ::: "memory");
	s_add_i32 s24, s23, 40
	s_lshl_b32 s20, s24, 7
	s_cmp_lt_u32 s24, 40
	s_cselect_b32 s21, 0, 0x830
	s_cmp_lt_u32 s24, 72
	s_cselect_b32 s21, s21, 0xfffff030
	s_add_i32 s20, s20, s21
	s_lshl_b32 s20, s20, 2
	s_add_u32 s8, s46, s20
	s_addc_u32 s9, s47, 0
	global_load_dwordx4 v[176:179], v76, s[8:9]
	s_add_u32 s8, s8, 0x16280
	s_addc_u32 s9, s9, 0
	global_load_dwordx4 v[180:183], v76, s[8:9]
	s_add_u32 s8, s8, 0x16280
	s_addc_u32 s9, s9, 0
	global_load_dwordx4 v[184:187], v76, s[8:9]
	s_add_u32 s8, s8, 0x16280
	s_addc_u32 s9, s9, 0
	global_load_dwordx4 v[188:191], v76, s[8:9]
	s_add_u32 s8, s8, 0x16280
	s_addc_u32 s9, s9, 0
	global_load_dwordx4 v[192:195], v76, s[8:9]
	s_add_u32 s8, s8, 0x16280
	s_addc_u32 s9, s9, 0
	global_load_dwordx4 v[196:199], v76, s[8:9]
	s_add_u32 s8, s8, 0x16280
	s_addc_u32 s9, s9, 0
	global_load_dwordx4 v[200:203], v76, s[8:9]
	s_add_u32 s8, s8, 0x16280
	s_addc_u32 s9, s9, 0
	global_load_dwordx4 v[204:207], v76, s[8:9]
	s_add_i32 s24, s23, 24
	s_mul_i32 s20, s24, 0x100000
	s_add_u32 s6, s48, s20
	s_addc_u32 s7, s49, 0
	s_cmp_lt_u32 s24, 16
	s_cselect_b32 s20, 1, 0
	s_sub_i32 s21, s24, 16
	s_bitcmp0_b32 s21, 2
	s_cselect_b32 s21, 1, 0
	s_cmp_lt_u32 s24, 40
	s_cselect_b32 s21, s21, 0
	s_or_b32 s20, s20, s21
	s_cmp_lg_u32 s20, 0
	s_cselect_b64 s[20:21], -1, 0
	v_cndmask_b32_e64 v91, v83, v87, s[20:21]
	v_cndmask_b32_e64 v92, v84, v88, s[20:21]
	v_cndmask_b32_e64 v93, v85, v89, s[20:21]
	v_cndmask_b32_e64 v94, v86, v90, s[20:21]
	ds_read_b32 v226, v113
	ds_read_b32 v227, v113 offset:512
	ds_read_b32 v228, v113 offset:1024
	ds_read_b32 v229, v113 offset:1536
	ds_read_b32 v230, v113 offset:2048
	ds_read_b32 v231, v113 offset:2560
	ds_read_b32 v232, v113 offset:3072
	ds_read_b32 v233, v113 offset:3584
	s_waitcnt lgkmcnt(0)
	v_bfe_u32 v120, v226, 16, 1
	v_bfe_u32 v121, v227, 16, 1
	v_bfe_u32 v122, v228, 16, 1
	v_bfe_u32 v123, v229, 16, 1
	v_bfe_u32 v124, v230, 16, 1
	v_bfe_u32 v125, v231, 16, 1
	v_bfe_u32 v126, v232, 16, 1
	v_bfe_u32 v127, v233, 16, 1
	v_add3_u32 v226, v226, v120, s63
	v_add3_u32 v227, v227, v121, s63
	v_add3_u32 v228, v228, v122, s63
	v_add3_u32 v229, v229, v123, s63
	v_add3_u32 v230, v230, v124, s63
	v_add3_u32 v231, v231, v125, s63
	v_add3_u32 v232, v232, v126, s63
	v_add3_u32 v233, v233, v127, s63
	v_perm_b32 v242, v227, v226, s64
	v_perm_b32 v243, v229, v228, s64
	v_perm_b32 v244, v231, v230, s64
	v_perm_b32 v245, v233, v232, s64
	s_nop 0
	global_store_dwordx4 v91, v[242:245], s[6:7]
	ds_read_b32 v226, v115
	ds_read_b32 v227, v115 offset:512
	ds_read_b32 v228, v115 offset:1024
	ds_read_b32 v229, v115 offset:1536
	ds_read_b32 v230, v115 offset:2048
	ds_read_b32 v231, v115 offset:2560
	ds_read_b32 v232, v115 offset:3072
	ds_read_b32 v233, v115 offset:3584
	s_waitcnt lgkmcnt(0)
	v_bfe_u32 v120, v226, 16, 1
	v_bfe_u32 v121, v227, 16, 1
	v_bfe_u32 v122, v228, 16, 1
	v_bfe_u32 v123, v229, 16, 1
	v_bfe_u32 v124, v230, 16, 1
	v_bfe_u32 v125, v231, 16, 1
	v_bfe_u32 v126, v232, 16, 1
	v_bfe_u32 v127, v233, 16, 1
	v_add3_u32 v226, v226, v120, s63
	v_add3_u32 v227, v227, v121, s63
	v_add3_u32 v228, v228, v122, s63
	v_add3_u32 v229, v229, v123, s63
	v_add3_u32 v230, v230, v124, s63
	v_add3_u32 v231, v231, v125, s63
	v_add3_u32 v232, v232, v126, s63
	v_add3_u32 v233, v233, v127, s63
	v_perm_b32 v242, v227, v226, s64
	v_perm_b32 v243, v229, v228, s64
	v_perm_b32 v244, v231, v230, s64
	v_perm_b32 v245, v233, v232, s64
	s_nop 0
	global_store_dwordx4 v92, v[242:245], s[6:7]
	ds_read_b32 v226, v117
	ds_read_b32 v227, v117 offset:512
	ds_read_b32 v228, v117 offset:1024
	ds_read_b32 v229, v117 offset:1536
	ds_read_b32 v230, v117 offset:2048
	ds_read_b32 v231, v117 offset:2560
	ds_read_b32 v232, v117 offset:3072
	ds_read_b32 v233, v117 offset:3584
	s_waitcnt lgkmcnt(0)
	v_bfe_u32 v120, v226, 16, 1
	v_bfe_u32 v121, v227, 16, 1
	v_bfe_u32 v122, v228, 16, 1
	v_bfe_u32 v123, v229, 16, 1
	v_bfe_u32 v124, v230, 16, 1
	v_bfe_u32 v125, v231, 16, 1
	v_bfe_u32 v126, v232, 16, 1
	v_bfe_u32 v127, v233, 16, 1
	v_add3_u32 v226, v226, v120, s63
	v_add3_u32 v227, v227, v121, s63
	v_add3_u32 v228, v228, v122, s63
	v_add3_u32 v229, v229, v123, s63
	v_add3_u32 v230, v230, v124, s63
	v_add3_u32 v231, v231, v125, s63
	v_add3_u32 v232, v232, v126, s63
	v_add3_u32 v233, v233, v127, s63
	v_perm_b32 v242, v227, v226, s64
	v_perm_b32 v243, v229, v228, s64
	v_perm_b32 v244, v231, v230, s64
	v_perm_b32 v245, v233, v232, s64
	s_nop 0
	global_store_dwordx4 v93, v[242:245], s[6:7]
	ds_read_b32 v226, v119
	ds_read_b32 v227, v119 offset:512
	ds_read_b32 v228, v119 offset:1024
	ds_read_b32 v229, v119 offset:1536
	ds_read_b32 v230, v119 offset:2048
	ds_read_b32 v231, v119 offset:2560
	ds_read_b32 v232, v119 offset:3072
	ds_read_b32 v233, v119 offset:3584
	s_waitcnt lgkmcnt(0)
	v_bfe_u32 v120, v226, 16, 1
	v_bfe_u32 v121, v227, 16, 1
	v_bfe_u32 v122, v228, 16, 1
	v_bfe_u32 v123, v229, 16, 1
	v_bfe_u32 v124, v230, 16, 1
	v_bfe_u32 v125, v231, 16, 1
	v_bfe_u32 v126, v232, 16, 1
	v_bfe_u32 v127, v233, 16, 1
	v_add3_u32 v226, v226, v120, s63
	v_add3_u32 v227, v227, v121, s63
	v_add3_u32 v228, v228, v122, s63
	v_add3_u32 v229, v229, v123, s63
	v_add3_u32 v230, v230, v124, s63
	v_add3_u32 v231, v231, v125, s63
	v_add3_u32 v232, v232, v126, s63
	v_add3_u32 v233, v233, v127, s63
	v_perm_b32 v242, v227, v226, s64
	v_perm_b32 v243, v229, v228, s64
	v_perm_b32 v244, v231, v230, s64
	v_perm_b32 v245, v233, v232, s64
	s_nop 0
	global_store_dwordx4 v94, v[242:245], s[6:7]
	s_waitcnt vmcnt(16)
	v_mul_f32_e32 v144, v42, v144
	v_mul_f32_e32 v145, v42, v145
	v_mul_f32_e32 v146, v42, v146
	v_mul_f32_e32 v147, v42, v147
	ds_write_b128 v209, v[144:147]
	v_mul_f32_e32 v148, v43, v148
	v_mul_f32_e32 v149, v43, v149
	v_mul_f32_e32 v150, v43, v150
	v_mul_f32_e32 v151, v43, v151
	ds_write_b128 v209, v[148:151] offset:1024
	v_mul_f32_e32 v152, v44, v152
	v_mul_f32_e32 v153, v44, v153
	v_mul_f32_e32 v154, v44, v154
	v_mul_f32_e32 v155, v44, v155
	ds_write_b128 v209, v[152:155] offset:2048
	v_mul_f32_e32 v156, v45, v156
	v_mul_f32_e32 v157, v45, v157
	v_mul_f32_e32 v158, v45, v158
	v_mul_f32_e32 v159, v45, v159
	ds_write_b128 v209, v[156:159] offset:3072
	v_mul_f32_e32 v160, v46, v160
	v_mul_f32_e32 v161, v46, v161
	v_mul_f32_e32 v162, v46, v162
	v_mul_f32_e32 v163, v46, v163
	ds_write_b128 v209, v[160:163] offset:4096
	v_mul_f32_e32 v164, v47, v164
	v_mul_f32_e32 v165, v47, v165
	v_mul_f32_e32 v166, v47, v166
	v_mul_f32_e32 v167, v47, v167
	ds_write_b128 v209, v[164:167] offset:5120
	v_mul_f32_e32 v168, v48, v168
	v_mul_f32_e32 v169, v48, v169
	v_mul_f32_e32 v170, v48, v170
	v_mul_f32_e32 v171, v48, v171
	ds_write_b128 v209, v[168:171] offset:6144
	v_mul_f32_e32 v172, v49, v172
	v_mul_f32_e32 v173, v49, v173
	v_mul_f32_e32 v174, v49, v174
	v_mul_f32_e32 v175, v49, v175
	ds_write_b128 v209, v[172:175] offset:7168
	s_waitcnt lgkmcnt(0)
	s_barrier
; #define GAS __attribute__((address_space(1)))
; #define LAS __attribute__((address_space(3)))
; #define LDS_WAIT() asm volatile("s_waitcnt lgkmcnt(0)" ::: "memory")
; __device__ __forceinline__ unsigned pk2(float lo, float hi) { return f2bf(lo) | (f2bf(hi) << 16); }
; __device__ __forceinline__ int nat_dim(int p) { return (p >> 1) + 64 * (p & 1); }
; __device__ __forceinline__ int src_col_in(int c) {
;     if (c < 5120) { const int blk = c >> 7, p = c & 127; const bool rope = blk < 16 || ((((blk - 16) >> 2) & 1) == 0); const int d = rope ? (p >> 1) + 64 * (p & 1) : p; return blk * 128 + d; }
;     if (c < OFF_Z) return c + 2096;
; template <int MAP, bool KS, bool KPERM = false>
; __device__ __forceinline__ void p0_transpose_item(const float* W, int K, int Nsrc, int nblk, bf16* WT, const float* ksA, const float* ksB, int ksplit, LAS float* scr, int item, int lane) {
;     const int kb = item / nblk, nb = item % nblk, k0 = 64 * kb, n0 = 32 * nb;
;     const int nr = n0 + (lane & 31); const int sc = MAP == 1 ? src_col_in(nr) : (MAP == 2 ? nat_dim(nr) : nr);
;     float v[32];
; #pragma unroll
;     for (int i = 0; i < 32; ++i) { const int k = k0 + 2 * i + (lane >> 5); const int ksrc = KPERM ? ((k & ~127) + nat_dim(k & 127)) : k;
;         v[i] = sc >= 0 ? W[(size_t)ksrc * Nsrc + sc] : 0.f; }
; #pragma unroll
;     for (int i = 0; i < 32; ++i) { const int kk = 2 * i + (lane >> 5); const int k = k0 + kk;
;         if (KS) v[i] *= (k < ksplit ? ksA[k] : ksB[k - ksplit]);
;         scr[kk * 33 + (lane & 31)] = v[i]; }
;     LDS_WAIT(); asm volatile("" ::: "memory");
;     const int c = lane & 7;
; #pragma unroll
;     for (int j = 0; j < 4; ++j) { const int n = (lane >> 3) + 8 * j; const LAS float* s = scr + (8 * c) * 33 + n;
;         v4u o; o.x = pk2(s[0 * 33], s[1 * 33]); o.y = pk2(s[2 * 33], s[3 * 33]); o.z = pk2(s[4 * 33], s[5 * 33]); o.w = pk2(s[6 * 33], s[7 * 33]);
;         *(GAS v4u*)(WT + (size_t)(n0 + n) * K + k0 + 8 * c) = o; }
;     LDS_WAIT(); asm volatile("" ::: "memory");
	s_add_i32 s24, s23, 48
	s_lshl_b32 s20, s24, 7
	s_cmp_lt_u32 s24, 40
	s_cselect_b32 s21, 0, 0x830
	s_cmp_lt_u32 s24, 72
	s_cselect_b32 s21, s21, 0xfffff030
	s_add_i32 s20, s20, s21
	s_lshl_b32 s20, s20, 2
	s_add_u32 s8, s46, s20
	s_addc_u32 s9, s47, 0
	global_load_dwordx4 v[144:147], v76, s[8:9]
	s_add_u32 s8, s8, 0x16280
	s_addc_u32 s9, s9, 0
	global_load_dwordx4 v[148:151], v76, s[8:9]
	s_add_u32 s8, s8, 0x16280
	s_addc_u32 s9, s9, 0
	global_load_dwordx4 v[152:155], v76, s[8:9]
	s_add_u32 s8, s8, 0x16280
	s_addc_u32 s9, s9, 0
	global_load_dwordx4 v[156:159], v76, s[8:9]
	s_add_u32 s8, s8, 0x16280
	s_addc_u32 s9, s9, 0
	global_load_dwordx4 v[160:163], v76, s[8:9]
	s_add_u32 s8, s8, 0x16280
	s_addc_u32 s9, s9, 0
	global_load_dwordx4 v[164:167], v76, s[8:9]
	s_add_u32 s8, s8, 0x16280
	s_addc_u32 s9, s9, 0
	global_load_dwordx4 v[168:171], v76, s[8:9]
	s_add_u32 s8, s8, 0x16280
	s_addc_u32 s9, s9, 0
	global_load_dwordx4 v[172:175], v76, s[8:9]
	s_add_i32 s24, s23, 32
	s_mul_i32 s20, s24, 0x100000
	s_add_u32 s6, s48, s20
	s_addc_u32 s7, s49, 0
	s_cmp_lt_u32 s24, 16
	s_cselect_b32 s20, 1, 0
	s_sub_i32 s21, s24, 16
	s_bitcmp0_b32 s21, 2
	s_cselect_b32 s21, 1, 0
	s_cmp_lt_u32 s24, 40
	s_cselect_b32 s21, s21, 0
	s_or_b32 s20, s20, s21
	s_cmp_lg_u32 s20, 0
	s_cselect_b64 s[20:21], -1, 0
	v_cndmask_b32_e64 v91, v83, v87, s[20:21]
	v_cndmask_b32_e64 v92, v84, v88, s[20:21]
	v_cndmask_b32_e64 v93, v85, v89, s[20:21]
	v_cndmask_b32_e64 v94, v86, v90, s[20:21]
	ds_read_b32 v226, v112
	ds_read_b32 v227, v112 offset:512
	ds_read_b32 v228, v112 offset:1024
	ds_read_b32 v229, v112 offset:1536
	ds_read_b32 v230, v112 offset:2048
	ds_read_b32 v231, v112 offset:2560
	ds_read_b32 v232, v112 offset:3072
	ds_read_b32 v233, v112 offset:3584
	s_waitcnt lgkmcnt(0)
	v_bfe_u32 v120, v226, 16, 1
	v_bfe_u32 v121, v227, 16, 1
	v_bfe_u32 v122, v228, 16, 1
	v_bfe_u32 v123, v229, 16, 1
	v_bfe_u32 v124, v230, 16, 1
	v_bfe_u32 v125, v231, 16, 1
	v_bfe_u32 v126, v232, 16, 1
	v_bfe_u32 v127, v233, 16, 1
	v_add3_u32 v226, v226, v120, s63
	v_add3_u32 v227, v227, v121, s63
	v_add3_u32 v228, v228, v122, s63
	v_add3_u32 v229, v229, v123, s63
	v_add3_u32 v230, v230, v124, s63
	v_add3_u32 v231, v231, v125, s63
	v_add3_u32 v232, v232, v126, s63
	v_add3_u32 v233, v233, v127, s63
	v_perm_b32 v242, v227, v226, s64
	v_perm_b32 v243, v229, v228, s64
	v_perm_b32 v244, v231, v230, s64
	v_perm_b32 v245, v233, v232, s64
	s_nop 0
	global_store_dwordx4 v91, v[242:245], s[6:7]
	ds_read_b32 v226, v114
	ds_read_b32 v227, v114 offset:512
	ds_read_b32 v228, v114 offset:1024
	ds_read_b32 v229, v114 offset:1536
	ds_read_b32 v230, v114 offset:2048
	ds_read_b32 v231, v114 offset:2560
	ds_read_b32 v232, v114 offset:3072
	ds_read_b32 v233, v114 offset:3584
	s_waitcnt lgkmcnt(0)
	v_bfe_u32 v120, v226, 16, 1
	v_bfe_u32 v121, v227, 16, 1
	v_bfe_u32 v122, v228, 16, 1
	v_bfe_u32 v123, v229, 16, 1
	v_bfe_u32 v124, v230, 16, 1
	v_bfe_u32 v125, v231, 16, 1
	v_bfe_u32 v126, v232, 16, 1
	v_bfe_u32 v127, v233, 16, 1
	v_add3_u32 v226, v226, v120, s63
	v_add3_u32 v227, v227, v121, s63
	v_add3_u32 v228, v228, v122, s63
	v_add3_u32 v229, v229, v123, s63
	v_add3_u32 v230, v230, v124, s63
	v_add3_u32 v231, v231, v125, s63
	v_add3_u32 v232, v232, v126, s63
	v_add3_u32 v233, v233, v127, s63
	v_perm_b32 v242, v227, v226, s64
	v_perm_b32 v243, v229, v228, s64
	v_perm_b32 v244, v231, v230, s64
	v_perm_b32 v245, v233, v232, s64
	s_nop 0
	global_store_dwordx4 v92, v[242:245], s[6:7]
	ds_read_b32 v226, v116
	ds_read_b32 v227, v116 offset:512
	ds_read_b32 v228, v116 offset:1024
	ds_read_b32 v229, v116 offset:1536
	ds_read_b32 v230, v116 offset:2048
	ds_read_b32 v231, v116 offset:2560
	ds_read_b32 v232, v116 offset:3072
	ds_read_b32 v233, v116 offset:3584
	s_waitcnt lgkmcnt(0)
	v_bfe_u32 v120, v226, 16, 1
	v_bfe_u32 v121, v227, 16, 1
	v_bfe_u32 v122, v228, 16, 1
	v_bfe_u32 v123, v229, 16, 1
	v_bfe_u32 v124, v230, 16, 1
	v_bfe_u32 v125, v231, 16, 1
	v_bfe_u32 v126, v232, 16, 1
	v_bfe_u32 v127, v233, 16, 1
	v_add3_u32 v226, v226, v120, s63
	v_add3_u32 v227, v227, v121, s63
	v_add3_u32 v228, v228, v122, s63
	v_add3_u32 v229, v229, v123, s63
	v_add3_u32 v230, v230, v124, s63
	v_add3_u32 v231, v231, v125, s63
	v_add3_u32 v232, v232, v126, s63
	v_add3_u32 v233, v233, v127, s63
	v_perm_b32 v242, v227, v226, s64
	v_perm_b32 v243, v229, v228, s64
	v_perm_b32 v244, v231, v230, s64
	v_perm_b32 v245, v233, v232, s64
	s_nop 0
	global_store_dwordx4 v93, v[242:245], s[6:7]
	ds_read_b32 v226, v118
	ds_read_b32 v227, v118 offset:512
	ds_read_b32 v228, v118 offset:1024
	ds_read_b32 v229, v118 offset:1536
	ds_read_b32 v230, v118 offset:2048
	ds_read_b32 v231, v118 offset:2560
	ds_read_b32 v232, v118 offset:3072
	ds_read_b32 v233, v118 offset:3584
	s_waitcnt lgkmcnt(0)
	v_bfe_u32 v120, v226, 16, 1
	v_bfe_u32 v121, v227, 16, 1
	v_bfe_u32 v122, v228, 16, 1
	v_bfe_u32 v123, v229, 16, 1
	v_bfe_u32 v124, v230, 16, 1
	v_bfe_u32 v125, v231, 16, 1
	v_bfe_u32 v126, v232, 16, 1
	v_bfe_u32 v127, v233, 16, 1
	v_add3_u32 v226, v226, v120, s63
	v_add3_u32 v227, v227, v121, s63
	v_add3_u32 v228, v228, v122, s63
	v_add3_u32 v229, v229, v123, s63
	v_add3_u32 v230, v230, v124, s63
	v_add3_u32 v231, v231, v125, s63
	v_add3_u32 v232, v232, v126, s63
	v_add3_u32 v233, v233, v127, s63
	v_perm_b32 v242, v227, v226, s64
	v_perm_b32 v243, v229, v228, s64
	v_perm_b32 v244, v231, v230, s64
	v_perm_b32 v245, v233, v232, s64
	s_nop 0
	global_store_dwordx4 v94, v[242:245], s[6:7]
	s_waitcnt vmcnt(16)
	v_mul_f32_e32 v176, v42, v176
	v_mul_f32_e32 v177, v42, v177
	v_mul_f32_e32 v178, v42, v178
	v_mul_f32_e32 v179, v42, v179
	ds_write_b128 v210, v[176:179]
	v_mul_f32_e32 v180, v43, v180
	v_mul_f32_e32 v181, v43, v181
	v_mul_f32_e32 v182, v43, v182
	v_mul_f32_e32 v183, v43, v183
	ds_write_b128 v210, v[180:183] offset:1024
	v_mul_f32_e32 v184, v44, v184
	v_mul_f32_e32 v185, v44, v185
	v_mul_f32_e32 v186, v44, v186
	v_mul_f32_e32 v187, v44, v187
	ds_write_b128 v210, v[184:187] offset:2048
	v_mul_f32_e32 v188, v45, v188
	v_mul_f32_e32 v189, v45, v189
	v_mul_f32_e32 v190, v45, v190
	v_mul_f32_e32 v191, v45, v191
	ds_write_b128 v210, v[188:191] offset:3072
	v_mul_f32_e32 v192, v46, v192
	v_mul_f32_e32 v193, v46, v193
	v_mul_f32_e32 v194, v46, v194
	v_mul_f32_e32 v195, v46, v195
	ds_write_b128 v210, v[192:195] offset:4096
	v_mul_f32_e32 v196, v47, v196
	v_mul_f32_e32 v197, v47, v197
	v_mul_f32_e32 v198, v47, v198
	v_mul_f32_e32 v199, v47, v199
	ds_write_b128 v210, v[196:199] offset:5120
	v_mul_f32_e32 v200, v48, v200
	v_mul_f32_e32 v201, v48, v201
	v_mul_f32_e32 v202, v48, v202
	v_mul_f32_e32 v203, v48, v203
	ds_write_b128 v210, v[200:203] offset:6144
	v_mul_f32_e32 v204, v49, v204
	v_mul_f32_e32 v205, v49, v205
	v_mul_f32_e32 v206, v49, v206
	v_mul_f32_e32 v207, v49, v207
	ds_write_b128 v210, v[204:207] offset:7168
	s_waitcnt lgkmcnt(0)
	s_barrier
; #define GAS __attribute__((address_space(1)))
; #define LAS __attribute__((address_space(3)))
; #define LDS_WAIT() asm volatile("s_waitcnt lgkmcnt(0)" ::: "memory")
; __device__ __forceinline__ unsigned pk2(float lo, float hi) { return f2bf(lo) | (f2bf(hi) << 16); }
; __device__ __forceinline__ int nat_dim(int p) { return (p >> 1) + 64 * (p & 1); }
; __device__ __forceinline__ int src_col_in(int c) {
;     if (c < 5120) { const int blk = c >> 7, p = c & 127; const bool rope = blk < 16 || ((((blk - 16) >> 2) & 1) == 0); const int d = rope ? (p >> 1) + 64 * (p & 1) : p; return blk * 128 + d; }
;     if (c < OFF_Z) return c + 2096;
; template <int MAP, bool KS, bool KPERM = false>
; __device__ __forceinline__ void p0_transpose_item(const float* W, int K, int Nsrc, int nblk, bf16* WT, const float* ksA, const float* ksB, int ksplit, LAS float* scr, int item, int lane) {
;     const int kb = item / nblk, nb = item % nblk, k0 = 64 * kb, n0 = 32 * nb;
;     const int nr = n0 + (lane & 31); const int sc = MAP == 1 ? src_col_in(nr) : (MAP == 2 ? nat_dim(nr) : nr);
;     float v[32];
; #pragma unroll
;     for (int i = 0; i < 32; ++i) { const int k = k0 + 2 * i + (lane >> 5); const int ksrc = KPERM ? ((k & ~127) + nat_dim(k & 127)) : k;
;         v[i] = sc >= 0 ? W[(size_t)ksrc * Nsrc + sc] : 0.f; }
; #pragma unroll
;     for (int i = 0; i < 32; ++i) { const int kk = 2 * i + (lane >> 5); const int k = k0 + kk;
;         if (KS) v[i] *= (k < ksplit ? ksA[k] : ksB[k - ksplit]);
;         scr[kk * 33 + (lane & 31)] = v[i]; }
;     LDS_WAIT(); asm volatile("" ::: "memory");
;     const int c = lane & 7;
; #pragma unroll
;     for (int j = 0; j < 4; ++j) { const int n = (lane >> 3) + 8 * j; const LAS float* s = scr + (8 * c) * 33 + n;
;         v4u o; o.x = pk2(s[0 * 33], s[1 * 33]); o.y = pk2(s[2 * 33], s[3 * 33]); o.z = pk2(s[4 * 33], s[5 * 33]); o.w = pk2(s[6 * 33], s[7 * 33]);
;         *(GAS v4u*)(WT + (size_t)(n0 + n) * K + k0 + 8 * c) = o; }
;     LDS_WAIT(); asm volatile("" ::: "memory");
	s_add_i32 s24, s23, 56
	s_lshl_b32 s20, s24, 7
	s_cmp_lt_u32 s24, 40
	s_cselect_b32 s21, 0, 0x830
	s_cmp_lt_u32 s24, 72
	s_cselect_b32 s21, s21, 0xfffff030
	s_add_i32 s20, s20, s21
	s_lshl_b32 s20, s20, 2
	s_add_u32 s8, s46, s20
	s_addc_u32 s9, s47, 0
	global_load_dwordx4 v[176:179], v76, s[8:9]
	s_add_u32 s8, s8, 0x16280
	s_addc_u32 s9, s9, 0
	global_load_dwordx4 v[180:183], v76, s[8:9]
	s_add_u32 s8, s8, 0x16280
	s_addc_u32 s9, s9, 0
	global_load_dwordx4 v[184:187], v76, s[8:9]
	s_add_u32 s8, s8, 0x16280
	s_addc_u32 s9, s9, 0
	global_load_dwordx4 v[188:191], v76, s[8:9]
	s_add_u32 s8, s8, 0x16280
	s_addc_u32 s9, s9, 0
	global_load_dwordx4 v[192:195], v76, s[8:9]
	s_add_u32 s8, s8, 0x16280
	s_addc_u32 s9, s9, 0
	global_load_dwordx4 v[196:199], v76, s[8:9]
	s_add_u32 s8, s8, 0x16280
	s_addc_u32 s9, s9, 0
	global_load_dwordx4 v[200:203], v76, s[8:9]
	s_add_u32 s8, s8, 0x16280
	s_addc_u32 s9, s9, 0
	global_load_dwordx4 v[204:207], v76, s[8:9]
	s_add_i32 s24, s23, 40
	s_mul_i32 s20, s24, 0x100000
	s_add_u32 s6, s48, s20
	s_addc_u32 s7, s49, 0
	s_cmp_lt_u32 s24, 16
	s_cselect_b32 s20, 1, 0
	s_sub_i32 s21, s24, 16
	s_bitcmp0_b32 s21, 2
	s_cselect_b32 s21, 1, 0
	s_cmp_lt_u32 s24, 40
	s_cselect_b32 s21, s21, 0
	s_or_b32 s20, s20, s21
	s_cmp_lg_u32 s20, 0
	s_cselect_b64 s[20:21], -1, 0
	v_cndmask_b32_e64 v91, v83, v87, s[20:21]
	v_cndmask_b32_e64 v92, v84, v88, s[20:21]
	v_cndmask_b32_e64 v93, v85, v89, s[20:21]
	v_cndmask_b32_e64 v94, v86, v90, s[20:21]
	ds_read_b32 v226, v113
	ds_read_b32 v227, v113 offset:512
	ds_read_b32 v228, v113 offset:1024
	ds_read_b32 v229, v113 offset:1536
	ds_read_b32 v230, v113 offset:2048
	ds_read_b32 v231, v113 offset:2560
	ds_read_b32 v232, v113 offset:3072
	ds_read_b32 v233, v113 offset:3584
	s_waitcnt lgkmcnt(0)
	v_bfe_u32 v120, v226, 16, 1
	v_bfe_u32 v121, v227, 16, 1
	v_bfe_u32 v122, v228, 16, 1
	v_bfe_u32 v123, v229, 16, 1
	v_bfe_u32 v124, v230, 16, 1
	v_bfe_u32 v125, v231, 16, 1
	v_bfe_u32 v126, v232, 16, 1
	v_bfe_u32 v127, v233, 16, 1
	v_add3_u32 v226, v226, v120, s63
	v_add3_u32 v227, v227, v121, s63
	v_add3_u32 v228, v228, v122, s63
	v_add3_u32 v229, v229, v123, s63
	v_add3_u32 v230, v230, v124, s63
	v_add3_u32 v231, v231, v125, s63
	v_add3_u32 v232, v232, v126, s63
	v_add3_u32 v233, v233, v127, s63
	v_perm_b32 v242, v227, v226, s64
	v_perm_b32 v243, v229, v228, s64
	v_perm_b32 v244, v231, v230, s64
	v_perm_b32 v245, v233, v232, s64
	s_nop 0
	global_store_dwordx4 v91, v[242:245], s[6:7]
	ds_read_b32 v226, v115
	ds_read_b32 v227, v115 offset:512
	ds_read_b32 v228, v115 offset:1024
	ds_read_b32 v229, v115 offset:1536
	ds_read_b32 v230, v115 offset:2048
	ds_read_b32 v231, v115 offset:2560
	ds_read_b32 v232, v115 offset:3072
	ds_read_b32 v233, v115 offset:3584
	s_waitcnt lgkmcnt(0)
	v_bfe_u32 v120, v226, 16, 1
	v_bfe_u32 v121, v227, 16, 1
	v_bfe_u32 v122, v228, 16, 1
	v_bfe_u32 v123, v229, 16, 1
	v_bfe_u32 v124, v230, 16, 1
	v_bfe_u32 v125, v231, 16, 1
	v_bfe_u32 v126, v232, 16, 1
	v_bfe_u32 v127, v233, 16, 1
	v_add3_u32 v226, v226, v120, s63
	v_add3_u32 v227, v227, v121, s63
	v_add3_u32 v228, v228, v122, s63
	v_add3_u32 v229, v229, v123, s63
	v_add3_u32 v230, v230, v124, s63
	v_add3_u32 v231, v231, v125, s63
	v_add3_u32 v232, v232, v126, s63
	v_add3_u32 v233, v233, v127, s63
	v_perm_b32 v242, v227, v226, s64
	v_perm_b32 v243, v229, v228, s64
	v_perm_b32 v244, v231, v230, s64
	v_perm_b32 v245, v233, v232, s64
	s_nop 0
	global_store_dwordx4 v92, v[242:245], s[6:7]
	ds_read_b32 v226, v117
	ds_read_b32 v227, v117 offset:512
	ds_read_b32 v228, v117 offset:1024
	ds_read_b32 v229, v117 offset:1536
	ds_read_b32 v230, v117 offset:2048
	ds_read_b32 v231, v117 offset:2560
	ds_read_b32 v232, v117 offset:3072
	ds_read_b32 v233, v117 offset:3584
	s_waitcnt lgkmcnt(0)
	v_bfe_u32 v120, v226, 16, 1
	v_bfe_u32 v121, v227, 16, 1
	v_bfe_u32 v122, v228, 16, 1
	v_bfe_u32 v123, v229, 16, 1
	v_bfe_u32 v124, v230, 16, 1
	v_bfe_u32 v125, v231, 16, 1
	v_bfe_u32 v126, v232, 16, 1
	v_bfe_u32 v127, v233, 16, 1
	v_add3_u32 v226, v226, v120, s63
	v_add3_u32 v227, v227, v121, s63
	v_add3_u32 v228, v228, v122, s63
	v_add3_u32 v229, v229, v123, s63
	v_add3_u32 v230, v230, v124, s63
	v_add3_u32 v231, v231, v125, s63
	v_add3_u32 v232, v232, v126, s63
	v_add3_u32 v233, v233, v127, s63
	v_perm_b32 v242, v227, v226, s64
	v_perm_b32 v243, v229, v228, s64
	v_perm_b32 v244, v231, v230, s64
	v_perm_b32 v245, v233, v232, s64
	s_nop 0
	global_store_dwordx4 v93, v[242:245], s[6:7]
	ds_read_b32 v226, v119
	ds_read_b32 v227, v119 offset:512
	ds_read_b32 v228, v119 offset:1024
	ds_read_b32 v229, v119 offset:1536
	ds_read_b32 v230, v119 offset:2048
	ds_read_b32 v231, v119 offset:2560
	ds_read_b32 v232, v119 offset:3072
	ds_read_b32 v233, v119 offset:3584
	s_waitcnt lgkmcnt(0)
	v_bfe_u32 v120, v226, 16, 1
	v_bfe_u32 v121, v227, 16, 1
	v_bfe_u32 v122, v228, 16, 1
	v_bfe_u32 v123, v229, 16, 1
	v_bfe_u32 v124, v230, 16, 1
	v_bfe_u32 v125, v231, 16, 1
	v_bfe_u32 v126, v232, 16, 1
	v_bfe_u32 v127, v233, 16, 1
	v_add3_u32 v226, v226, v120, s63
	v_add3_u32 v227, v227, v121, s63
	v_add3_u32 v228, v228, v122, s63
	v_add3_u32 v229, v229, v123, s63
	v_add3_u32 v230, v230, v124, s63
	v_add3_u32 v231, v231, v125, s63
	v_add3_u32 v232, v232, v126, s63
	v_add3_u32 v233, v233, v127, s63
	v_perm_b32 v242, v227, v226, s64
	v_perm_b32 v243, v229, v228, s64
	v_perm_b32 v244, v231, v230, s64
	v_perm_b32 v245, v233, v232, s64
	s_nop 0
	global_store_dwordx4 v94, v[242:245], s[6:7]
	s_waitcnt vmcnt(16)
	v_mul_f32_e32 v144, v42, v144
	v_mul_f32_e32 v145, v42, v145
	v_mul_f32_e32 v146, v42, v146
	v_mul_f32_e32 v147, v42, v147
	ds_write_b128 v209, v[144:147]
	v_mul_f32_e32 v148, v43, v148
	v_mul_f32_e32 v149, v43, v149
	v_mul_f32_e32 v150, v43, v150
	v_mul_f32_e32 v151, v43, v151
	ds_write_b128 v209, v[148:151] offset:1024
	v_mul_f32_e32 v152, v44, v152
	v_mul_f32_e32 v153, v44, v153
	v_mul_f32_e32 v154, v44, v154
	v_mul_f32_e32 v155, v44, v155
	ds_write_b128 v209, v[152:155] offset:2048
	v_mul_f32_e32 v156, v45, v156
	v_mul_f32_e32 v157, v45, v157
	v_mul_f32_e32 v158, v45, v158
	v_mul_f32_e32 v159, v45, v159
	ds_write_b128 v209, v[156:159] offset:3072
	v_mul_f32_e32 v160, v46, v160
	v_mul_f32_e32 v161, v46, v161
	v_mul_f32_e32 v162, v46, v162
	v_mul_f32_e32 v163, v46, v163
	ds_write_b128 v209, v[160:163] offset:4096
	v_mul_f32_e32 v164, v47, v164
	v_mul_f32_e32 v165, v47, v165
	v_mul_f32_e32 v166, v47, v166
	v_mul_f32_e32 v167, v47, v167
	ds_write_b128 v209, v[164:167] offset:5120
	v_mul_f32_e32 v168, v48, v168
	v_mul_f32_e32 v169, v48, v169
	v_mul_f32_e32 v170, v48, v170
	v_mul_f32_e32 v171, v48, v171
	ds_write_b128 v209, v[168:171] offset:6144
	v_mul_f32_e32 v172, v49, v172
	v_mul_f32_e32 v173, v49, v173
	v_mul_f32_e32 v174, v49, v174
	v_mul_f32_e32 v175, v49, v175
	ds_write_b128 v209, v[172:175] offset:7168
	s_waitcnt lgkmcnt(0)
	s_barrier
; #define GAS __attribute__((address_space(1)))
; #define LAS __attribute__((address_space(3)))
; #define LDS_WAIT() asm volatile("s_waitcnt lgkmcnt(0)" ::: "memory")
; __device__ __forceinline__ unsigned pk2(float lo, float hi) { return f2bf(lo) | (f2bf(hi) << 16); }
; __device__ __forceinline__ int nat_dim(int p) { return (p >> 1) + 64 * (p & 1); }
; __device__ __forceinline__ int src_col_in(int c) {
;     if (c < 5120) { const int blk = c >> 7, p = c & 127; const bool rope = blk < 16 || ((((blk - 16) >> 2) & 1) == 0); const int d = rope ? (p >> 1) + 64 * (p & 1) : p; return blk * 128 + d; }
;     if (c < OFF_Z) return c + 2096;
; template <int MAP, bool KS, bool KPERM = false>
; __device__ __forceinline__ void p0_transpose_item(const float* W, int K, int Nsrc, int nblk, bf16* WT, const float* ksA, const float* ksB, int ksplit, LAS float* scr, int item, int lane) {
;     const int kb = item / nblk, nb = item % nblk, k0 = 64 * kb, n0 = 32 * nb;
;     const int nr = n0 + (lane & 31); const int sc = MAP == 1 ? src_col_in(nr) : (MAP == 2 ? nat_dim(nr) : nr);
;     float v[32];
; #pragma unroll
;     for (int i = 0; i < 32; ++i) { const int k = k0 + 2 * i + (lane >> 5); const int ksrc = KPERM ? ((k & ~127) + nat_dim(k & 127)) : k;
;         v[i] = sc >= 0 ? W[(size_t)ksrc * Nsrc + sc] : 0.f; }
; #pragma unroll
;     for (int i = 0; i < 32; ++i) { const int kk = 2 * i + (lane >> 5); const int k = k0 + kk;
;         if (KS) v[i] *= (k < ksplit ? ksA[k] : ksB[k - ksplit]);
;         scr[kk * 33 + (lane & 31)] = v[i]; }
;     LDS_WAIT(); asm volatile("" ::: "memory");
;     const int c = lane & 7;
; #pragma unroll
;     for (int j = 0; j < 4; ++j) { const int n = (lane >> 3) + 8 * j; const LAS float* s = scr + (8 * c) * 33 + n;
;         v4u o; o.x = pk2(s[0 * 33], s[1 * 33]); o.y = pk2(s[2 * 33], s[3 * 33]); o.z = pk2(s[4 * 33], s[5 * 33]); o.w = pk2(s[6 * 33], s[7 * 33]);
;         *(GAS v4u*)(WT + (size_t)(n0 + n) * K + k0 + 8 * c) = o; }
;     LDS_WAIT(); asm volatile("" ::: "memory");
	s_add_i32 s24, s23, 64
	s_lshl_b32 s20, s24, 7
	s_cmp_lt_u32 s24, 40
	s_cselect_b32 s21, 0, 0x830
	s_cmp_lt_u32 s24, 72
	s_cselect_b32 s21, s21, 0xfffff030
	s_add_i32 s20, s20, s21
	s_lshl_b32 s20, s20, 2
	s_add_u32 s8, s46, s20
	s_addc_u32 s9, s47, 0
	global_load_dwordx4 v[144:147], v76, s[8:9]
	s_add_u32 s8, s8, 0x16280
	s_addc_u32 s9, s9, 0
	global_load_dwordx4 v[148:151], v76, s[8:9]
	s_add_u32 s8, s8, 0x16280
	s_addc_u32 s9, s9, 0
	global_load_dwordx4 v[152:155], v76, s[8:9]
	s_add_u32 s8, s8, 0x16280
	s_addc_u32 s9, s9, 0
	global_load_dwordx4 v[156:159], v76, s[8:9]
	s_add_u32 s8, s8, 0x16280
	s_addc_u32 s9, s9, 0
	global_load_dwordx4 v[160:163], v76, s[8:9]
	s_add_u32 s8, s8, 0x16280
	s_addc_u32 s9, s9, 0
	global_load_dwordx4 v[164:167], v76, s[8:9]
	s_add_u32 s8, s8, 0x16280
	s_addc_u32 s9, s9, 0
	global_load_dwordx4 v[168:171], v76, s[8:9]
	s_add_u32 s8, s8, 0x16280
	s_addc_u32 s9, s9, 0
	global_load_dwordx4 v[172:175], v76, s[8:9]
	s_add_i32 s24, s23, 48
	s_mul_i32 s20, s24, 0x100000
	s_add_u32 s6, s48, s20
	s_addc_u32 s7, s49, 0
	s_cmp_lt_u32 s24, 16
	s_cselect_b32 s20, 1, 0
	s_sub_i32 s21, s24, 16
	s_bitcmp0_b32 s21, 2
	s_cselect_b32 s21, 1, 0
	s_cmp_lt_u32 s24, 40
	s_cselect_b32 s21, s21, 0
	s_or_b32 s20, s20, s21
	s_cmp_lg_u32 s20, 0
	s_cselect_b64 s[20:21], -1, 0
	v_cndmask_b32_e64 v91, v83, v87, s[20:21]
	v_cndmask_b32_e64 v92, v84, v88, s[20:21]
	v_cndmask_b32_e64 v93, v85, v89, s[20:21]
	v_cndmask_b32_e64 v94, v86, v90, s[20:21]
	ds_read_b32 v226, v112
	ds_read_b32 v227, v112 offset:512
	ds_read_b32 v228, v112 offset:1024
	ds_read_b32 v229, v112 offset:1536
	ds_read_b32 v230, v112 offset:2048
	ds_read_b32 v231, v112 offset:2560
	ds_read_b32 v232, v112 offset:3072
	ds_read_b32 v233, v112 offset:3584
	s_waitcnt lgkmcnt(0)
	v_bfe_u32 v120, v226, 16, 1
	v_bfe_u32 v121, v227, 16, 1
	v_bfe_u32 v122, v228, 16, 1
	v_bfe_u32 v123, v229, 16, 1
	v_bfe_u32 v124, v230, 16, 1
	v_bfe_u32 v125, v231, 16, 1
	v_bfe_u32 v126, v232, 16, 1
	v_bfe_u32 v127, v233, 16, 1
	v_add3_u32 v226, v226, v120, s63
	v_add3_u32 v227, v227, v121, s63
	v_add3_u32 v228, v228, v122, s63
	v_add3_u32 v229, v229, v123, s63
	v_add3_u32 v230, v230, v124, s63
	v_add3_u32 v231, v231, v125, s63
	v_add3_u32 v232, v232, v126, s63
	v_add3_u32 v233, v233, v127, s63
	v_perm_b32 v242, v227, v226, s64
	v_perm_b32 v243, v229, v228, s64
	v_perm_b32 v244, v231, v230, s64
	v_perm_b32 v245, v233, v232, s64
	s_nop 0
	global_store_dwordx4 v91, v[242:245], s[6:7]
	ds_read_b32 v226, v114
	ds_read_b32 v227, v114 offset:512
	ds_read_b32 v228, v114 offset:1024
	ds_read_b32 v229, v114 offset:1536
	ds_read_b32 v230, v114 offset:2048
	ds_read_b32 v231, v114 offset:2560
	ds_read_b32 v232, v114 offset:3072
	ds_read_b32 v233, v114 offset:3584
	s_waitcnt lgkmcnt(0)
	v_bfe_u32 v120, v226, 16, 1
	v_bfe_u32 v121, v227, 16, 1
	v_bfe_u32 v122, v228, 16, 1
	v_bfe_u32 v123, v229, 16, 1
	v_bfe_u32 v124, v230, 16, 1
	v_bfe_u32 v125, v231, 16, 1
	v_bfe_u32 v126, v232, 16, 1
	v_bfe_u32 v127, v233, 16, 1
	v_add3_u32 v226, v226, v120, s63
	v_add3_u32 v227, v227, v121, s63
	v_add3_u32 v228, v228, v122, s63
	v_add3_u32 v229, v229, v123, s63
	v_add3_u32 v230, v230, v124, s63
	v_add3_u32 v231, v231, v125, s63
	v_add3_u32 v232, v232, v126, s63
	v_add3_u32 v233, v233, v127, s63
	v_perm_b32 v242, v227, v226, s64
	v_perm_b32 v243, v229, v228, s64
	v_perm_b32 v244, v231, v230, s64
	v_perm_b32 v245, v233, v232, s64
	s_nop 0
	global_store_dwordx4 v92, v[242:245], s[6:7]
	ds_read_b32 v226, v116
	ds_read_b32 v227, v116 offset:512
	ds_read_b32 v228, v116 offset:1024
	ds_read_b32 v229, v116 offset:1536
	ds_read_b32 v230, v116 offset:2048
	ds_read_b32 v231, v116 offset:2560
	ds_read_b32 v232, v116 offset:3072
	ds_read_b32 v233, v116 offset:3584
	s_waitcnt lgkmcnt(0)
	v_bfe_u32 v120, v226, 16, 1
	v_bfe_u32 v121, v227, 16, 1
	v_bfe_u32 v122, v228, 16, 1
	v_bfe_u32 v123, v229, 16, 1
	v_bfe_u32 v124, v230, 16, 1
	v_bfe_u32 v125, v231, 16, 1
	v_bfe_u32 v126, v232, 16, 1
	v_bfe_u32 v127, v233, 16, 1
	v_add3_u32 v226, v226, v120, s63
	v_add3_u32 v227, v227, v121, s63
	v_add3_u32 v228, v228, v122, s63
	v_add3_u32 v229, v229, v123, s63
	v_add3_u32 v230, v230, v124, s63
	v_add3_u32 v231, v231, v125, s63
	v_add3_u32 v232, v232, v126, s63
	v_add3_u32 v233, v233, v127, s63
	v_perm_b32 v242, v227, v226, s64
	v_perm_b32 v243, v229, v228, s64
	v_perm_b32 v244, v231, v230, s64
	v_perm_b32 v245, v233, v232, s64
	s_nop 0
	global_store_dwordx4 v93, v[242:245], s[6:7]
	ds_read_b32 v226, v118
	ds_read_b32 v227, v118 offset:512
	ds_read_b32 v228, v118 offset:1024
	ds_read_b32 v229, v118 offset:1536
	ds_read_b32 v230, v118 offset:2048
	ds_read_b32 v231, v118 offset:2560
	ds_read_b32 v232, v118 offset:3072
	ds_read_b32 v233, v118 offset:3584
	s_waitcnt lgkmcnt(0)
	v_bfe_u32 v120, v226, 16, 1
	v_bfe_u32 v121, v227, 16, 1
	v_bfe_u32 v122, v228, 16, 1
	v_bfe_u32 v123, v229, 16, 1
	v_bfe_u32 v124, v230, 16, 1
	v_bfe_u32 v125, v231, 16, 1
	v_bfe_u32 v126, v232, 16, 1
	v_bfe_u32 v127, v233, 16, 1
	v_add3_u32 v226, v226, v120, s63
	v_add3_u32 v227, v227, v121, s63
	v_add3_u32 v228, v228, v122, s63
	v_add3_u32 v229, v229, v123, s63
	v_add3_u32 v230, v230, v124, s63
	v_add3_u32 v231, v231, v125, s63
	v_add3_u32 v232, v232, v126, s63
	v_add3_u32 v233, v233, v127, s63
	v_perm_b32 v242, v227, v226, s64
	v_perm_b32 v243, v229, v228, s64
	v_perm_b32 v244, v231, v230, s64
	v_perm_b32 v245, v233, v232, s64
	s_nop 0
	global_store_dwordx4 v94, v[242:245], s[6:7]
	s_waitcnt vmcnt(16)
	v_mul_f32_e32 v176, v42, v176
	v_mul_f32_e32 v177, v42, v177
	v_mul_f32_e32 v178, v42, v178
	v_mul_f32_e32 v179, v42, v179
	ds_write_b128 v210, v[176:179]
	v_mul_f32_e32 v180, v43, v180
	v_mul_f32_e32 v181, v43, v181
	v_mul_f32_e32 v182, v43, v182
	v_mul_f32_e32 v183, v43, v183
	ds_write_b128 v210, v[180:183] offset:1024
	v_mul_f32_e32 v184, v44, v184
	v_mul_f32_e32 v185, v44, v185
	v_mul_f32_e32 v186, v44, v186
	v_mul_f32_e32 v187, v44, v187
	ds_write_b128 v210, v[184:187] offset:2048
	v_mul_f32_e32 v188, v45, v188
	v_mul_f32_e32 v189, v45, v189
	v_mul_f32_e32 v190, v45, v190
	v_mul_f32_e32 v191, v45, v191
	ds_write_b128 v210, v[188:191] offset:3072
	v_mul_f32_e32 v192, v46, v192
	v_mul_f32_e32 v193, v46, v193
	v_mul_f32_e32 v194, v46, v194
	v_mul_f32_e32 v195, v46, v195
	ds_write_b128 v210, v[192:195] offset:4096
	v_mul_f32_e32 v196, v47, v196
	v_mul_f32_e32 v197, v47, v197
	v_mul_f32_e32 v198, v47, v198
	v_mul_f32_e32 v199, v47, v199
	ds_write_b128 v210, v[196:199] offset:5120
	v_mul_f32_e32 v200, v48, v200
	v_mul_f32_e32 v201, v48, v201
	v_mul_f32_e32 v202, v48, v202
	v_mul_f32_e32 v203, v48, v203
	ds_write_b128 v210, v[200:203] offset:6144
	v_mul_f32_e32 v204, v49, v204
	v_mul_f32_e32 v205, v49, v205
	v_mul_f32_e32 v206, v49, v206
	v_mul_f32_e32 v207, v49, v207
	ds_write_b128 v210, v[204:207] offset:7168
	s_waitcnt lgkmcnt(0)
	s_barrier
; #define GAS __attribute__((address_space(1)))
; #define LAS __attribute__((address_space(3)))
; #define LDS_WAIT() asm volatile("s_waitcnt lgkmcnt(0)" ::: "memory")
; __device__ __forceinline__ unsigned pk2(float lo, float hi) { return f2bf(lo) | (f2bf(hi) << 16); }
; __device__ __forceinline__ int nat_dim(int p) { return (p >> 1) + 64 * (p & 1); }
; __device__ __forceinline__ int src_col_in(int c) {
;     if (c < 5120) { const int blk = c >> 7, p = c & 127; const bool rope = blk < 16 || ((((blk - 16) >> 2) & 1) == 0); const int d = rope ? (p >> 1) + 64 * (p & 1) : p; return blk * 128 + d; }
;     if (c < OFF_Z) return c + 2096;
; template <int MAP, bool KS, bool KPERM = false>
; __device__ __forceinline__ void p0_transpose_item(const float* W, int K, int Nsrc, int nblk, bf16* WT, const float* ksA, const float* ksB, int ksplit, LAS float* scr, int item, int lane) {
;     const int kb = item / nblk, nb = item % nblk, k0 = 64 * kb, n0 = 32 * nb;
;     const int nr = n0 + (lane & 31); const int sc = MAP == 1 ? src_col_in(nr) : (MAP == 2 ? nat_dim(nr) : nr);
;     float v[32];
; #pragma unroll
;     for (int i = 0; i < 32; ++i) { const int k = k0 + 2 * i + (lane >> 5); const int ksrc = KPERM ? ((k & ~127) + nat_dim(k & 127)) : k;
;         v[i] = sc >= 0 ? W[(size_t)ksrc * Nsrc + sc] : 0.f; }
; #pragma unroll
;     for (int i = 0; i < 32; ++i) { const int kk = 2 * i + (lane >> 5); const int k = k0 + kk;
;         if (KS) v[i] *= (k < ksplit ? ksA[k] : ksB[k - ksplit]);
;         scr[kk * 33 + (lane & 31)] = v[i]; }
;     LDS_WAIT(); asm volatile("" ::: "memory");
;     const int c = lane & 7;
; #pragma unroll
;     for (int j = 0; j < 4; ++j) { const int n = (lane >> 3) + 8 * j; const LAS float* s = scr + (8 * c) * 33 + n;
;         v4u o; o.x = pk2(s[0 * 33], s[1 * 33]); o.y = pk2(s[2 * 33], s[3 * 33]); o.z = pk2(s[4 * 33], s[5 * 33]); o.w = pk2(s[6 * 33], s[7 * 33]);
;         *(GAS v4u*)(WT + (size_t)(n0 + n) * K + k0 + 8 * c) = o; }
;     LDS_WAIT(); asm volatile("" ::: "memory");
	s_add_i32 s24, s23, 72
	s_lshl_b32 s20, s24, 7
	s_cmp_lt_u32 s24, 40
	s_cselect_b32 s21, 0, 0x830
	s_cmp_lt_u32 s24, 72
	s_cselect_b32 s21, s21, 0xfffff030
	s_add_i32 s20, s20, s21
	s_lshl_b32 s20, s20, 2
	s_add_u32 s8, s46, s20
	s_addc_u32 s9, s47, 0
	global_load_dwordx4 v[176:179], v76, s[8:9]
	s_add_u32 s8, s8, 0x16280
	s_addc_u32 s9, s9, 0
	global_load_dwordx4 v[180:183], v76, s[8:9]
	s_add_u32 s8, s8, 0x16280
	s_addc_u32 s9, s9, 0
	global_load_dwordx4 v[184:187], v76, s[8:9]
	s_add_u32 s8, s8, 0x16280
	s_addc_u32 s9, s9, 0
	global_load_dwordx4 v[188:191], v76, s[8:9]
	s_add_u32 s8, s8, 0x16280
	s_addc_u32 s9, s9, 0
	global_load_dwordx4 v[192:195], v76, s[8:9]
	s_add_u32 s8, s8, 0x16280
	s_addc_u32 s9, s9, 0
	global_load_dwordx4 v[196:199], v76, s[8:9]
	s_add_u32 s8, s8, 0x16280
	s_addc_u32 s9, s9, 0
	global_load_dwordx4 v[200:203], v76, s[8:9]
	s_add_u32 s8, s8, 0x16280
	s_addc_u32 s9, s9, 0
	global_load_dwordx4 v[204:207], v76, s[8:9]
	s_add_i32 s24, s23, 56
	s_mul_i32 s20, s24, 0x100000
	s_add_u32 s6, s48, s20
	s_addc_u32 s7, s49, 0
	s_cmp_lt_u32 s24, 16
	s_cselect_b32 s20, 1, 0
	s_sub_i32 s21, s24, 16
	s_bitcmp0_b32 s21, 2
	s_cselect_b32 s21, 1, 0
	s_cmp_lt_u32 s24, 40
	s_cselect_b32 s21, s21, 0
	s_or_b32 s20, s20, s21
	s_cmp_lg_u32 s20, 0
	s_cselect_b64 s[20:21], -1, 0
	v_cndmask_b32_e64 v91, v83, v87, s[20:21]
	v_cndmask_b32_e64 v92, v84, v88, s[20:21]
	v_cndmask_b32_e64 v93, v85, v89, s[20:21]
	v_cndmask_b32_e64 v94, v86, v90, s[20:21]
	ds_read_b32 v226, v113
	ds_read_b32 v227, v113 offset:512
	ds_read_b32 v228, v113 offset:1024
	ds_read_b32 v229, v113 offset:1536
	ds_read_b32 v230, v113 offset:2048
	ds_read_b32 v231, v113 offset:2560
	ds_read_b32 v232, v113 offset:3072
	ds_read_b32 v233, v113 offset:3584
	s_waitcnt lgkmcnt(0)
	v_bfe_u32 v120, v226, 16, 1
	v_bfe_u32 v121, v227, 16, 1
	v_bfe_u32 v122, v228, 16, 1
	v_bfe_u32 v123, v229, 16, 1
	v_bfe_u32 v124, v230, 16, 1
	v_bfe_u32 v125, v231, 16, 1
	v_bfe_u32 v126, v232, 16, 1
	v_bfe_u32 v127, v233, 16, 1
	v_add3_u32 v226, v226, v120, s63
	v_add3_u32 v227, v227, v121, s63
	v_add3_u32 v228, v228, v122, s63
	v_add3_u32 v229, v229, v123, s63
	v_add3_u32 v230, v230, v124, s63
	v_add3_u32 v231, v231, v125, s63
	v_add3_u32 v232, v232, v126, s63
	v_add3_u32 v233, v233, v127, s63
	v_perm_b32 v242, v227, v226, s64
	v_perm_b32 v243, v229, v228, s64
	v_perm_b32 v244, v231, v230, s64
	v_perm_b32 v245, v233, v232, s64
	s_nop 0
	global_store_dwordx4 v91, v[242:245], s[6:7]
	ds_read_b32 v226, v115
	ds_read_b32 v227, v115 offset:512
	ds_read_b32 v228, v115 offset:1024
	ds_read_b32 v229, v115 offset:1536
	ds_read_b32 v230, v115 offset:2048
	ds_read_b32 v231, v115 offset:2560
	ds_read_b32 v232, v115 offset:3072
	ds_read_b32 v233, v115 offset:3584
	s_waitcnt lgkmcnt(0)
	v_bfe_u32 v120, v226, 16, 1
	v_bfe_u32 v121, v227, 16, 1
	v_bfe_u32 v122, v228, 16, 1
	v_bfe_u32 v123, v229, 16, 1
	v_bfe_u32 v124, v230, 16, 1
	v_bfe_u32 v125, v231, 16, 1
	v_bfe_u32 v126, v232, 16, 1
	v_bfe_u32 v127, v233, 16, 1
	v_add3_u32 v226, v226, v120, s63
	v_add3_u32 v227, v227, v121, s63
	v_add3_u32 v228, v228, v122, s63
	v_add3_u32 v229, v229, v123, s63
	v_add3_u32 v230, v230, v124, s63
	v_add3_u32 v231, v231, v125, s63
	v_add3_u32 v232, v232, v126, s63
	v_add3_u32 v233, v233, v127, s63
	v_perm_b32 v242, v227, v226, s64
	v_perm_b32 v243, v229, v228, s64
	v_perm_b32 v244, v231, v230, s64
	v_perm_b32 v245, v233, v232, s64
	s_nop 0
	global_store_dwordx4 v92, v[242:245], s[6:7]
	ds_read_b32 v226, v117
	ds_read_b32 v227, v117 offset:512
	ds_read_b32 v228, v117 offset:1024
	ds_read_b32 v229, v117 offset:1536
	ds_read_b32 v230, v117 offset:2048
	ds_read_b32 v231, v117 offset:2560
	ds_read_b32 v232, v117 offset:3072
	ds_read_b32 v233, v117 offset:3584
	s_waitcnt lgkmcnt(0)
	v_bfe_u32 v120, v226, 16, 1
	v_bfe_u32 v121, v227, 16, 1
	v_bfe_u32 v122, v228, 16, 1
	v_bfe_u32 v123, v229, 16, 1
	v_bfe_u32 v124, v230, 16, 1
	v_bfe_u32 v125, v231, 16, 1
	v_bfe_u32 v126, v232, 16, 1
	v_bfe_u32 v127, v233, 16, 1
	v_add3_u32 v226, v226, v120, s63
	v_add3_u32 v227, v227, v121, s63
	v_add3_u32 v228, v228, v122, s63
	v_add3_u32 v229, v229, v123, s63
	v_add3_u32 v230, v230, v124, s63
	v_add3_u32 v231, v231, v125, s63
	v_add3_u32 v232, v232, v126, s63
	v_add3_u32 v233, v233, v127, s63
	v_perm_b32 v242, v227, v226, s64
	v_perm_b32 v243, v229, v228, s64
	v_perm_b32 v244, v231, v230, s64
	v_perm_b32 v245, v233, v232, s64
	s_nop 0
	global_store_dwordx4 v93, v[242:245], s[6:7]
	ds_read_b32 v226, v119
	ds_read_b32 v227, v119 offset:512
	ds_read_b32 v228, v119 offset:1024
	ds_read_b32 v229, v119 offset:1536
	ds_read_b32 v230, v119 offset:2048
	ds_read_b32 v231, v119 offset:2560
	ds_read_b32 v232, v119 offset:3072
	ds_read_b32 v233, v119 offset:3584
	s_waitcnt lgkmcnt(0)
	v_bfe_u32 v120, v226, 16, 1
	v_bfe_u32 v121, v227, 16, 1
	v_bfe_u32 v122, v228, 16, 1
	v_bfe_u32 v123, v229, 16, 1
	v_bfe_u32 v124, v230, 16, 1
	v_bfe_u32 v125, v231, 16, 1
	v_bfe_u32 v126, v232, 16, 1
	v_bfe_u32 v127, v233, 16, 1
	v_add3_u32 v226, v226, v120, s63
	v_add3_u32 v227, v227, v121, s63
	v_add3_u32 v228, v228, v122, s63
	v_add3_u32 v229, v229, v123, s63
	v_add3_u32 v230, v230, v124, s63
	v_add3_u32 v231, v231, v125, s63
	v_add3_u32 v232, v232, v126, s63
	v_add3_u32 v233, v233, v127, s63
	v_perm_b32 v242, v227, v226, s64
	v_perm_b32 v243, v229, v228, s64
	v_perm_b32 v244, v231, v230, s64
	v_perm_b32 v245, v233, v232, s64
	s_nop 0
	global_store_dwordx4 v94, v[242:245], s[6:7]
	s_waitcnt vmcnt(16)
	v_mul_f32_e32 v144, v42, v144
	v_mul_f32_e32 v145, v42, v145
	v_mul_f32_e32 v146, v42, v146
	v_mul_f32_e32 v147, v42, v147
	ds_write_b128 v209, v[144:147]
	v_mul_f32_e32 v148, v43, v148
	v_mul_f32_e32 v149, v43, v149
	v_mul_f32_e32 v150, v43, v150
	v_mul_f32_e32 v151, v43, v151
	ds_write_b128 v209, v[148:151] offset:1024
	v_mul_f32_e32 v152, v44, v152
	v_mul_f32_e32 v153, v44, v153
	v_mul_f32_e32 v154, v44, v154
	v_mul_f32_e32 v155, v44, v155
	ds_write_b128 v209, v[152:155] offset:2048
	v_mul_f32_e32 v156, v45, v156
	v_mul_f32_e32 v157, v45, v157
	v_mul_f32_e32 v158, v45, v158
	v_mul_f32_e32 v159, v45, v159
	ds_write_b128 v209, v[156:159] offset:3072
	v_mul_f32_e32 v160, v46, v160
	v_mul_f32_e32 v161, v46, v161
	v_mul_f32_e32 v162, v46, v162
	v_mul_f32_e32 v163, v46, v163
	ds_write_b128 v209, v[160:163] offset:4096
	v_mul_f32_e32 v164, v47, v164
	v_mul_f32_e32 v165, v47, v165
	v_mul_f32_e32 v166, v47, v166
	v_mul_f32_e32 v167, v47, v167
	ds_write_b128 v209, v[164:167] offset:5120
	v_mul_f32_e32 v168, v48, v168
	v_mul_f32_e32 v169, v48, v169
	v_mul_f32_e32 v170, v48, v170
	v_mul_f32_e32 v171, v48, v171
	ds_write_b128 v209, v[168:171] offset:6144
	v_mul_f32_e32 v172, v49, v172
	v_mul_f32_e32 v173, v49, v173
	v_mul_f32_e32 v174, v49, v174
	v_mul_f32_e32 v175, v49, v175
	ds_write_b128 v209, v[172:175] offset:7168
	s_waitcnt lgkmcnt(0)
	s_barrier
; #define GAS __attribute__((address_space(1)))
; #define LAS __attribute__((address_space(3)))
; #define LDS_WAIT() asm volatile("s_waitcnt lgkmcnt(0)" ::: "memory")
; __device__ __forceinline__ unsigned pk2(float lo, float hi) { return f2bf(lo) | (f2bf(hi) << 16); }
; __device__ __forceinline__ int nat_dim(int p) { return (p >> 1) + 64 * (p & 1); }
; __device__ __forceinline__ int src_col_in(int c) {
;     if (c < 5120) { const int blk = c >> 7, p = c & 127; const bool rope = blk < 16 || ((((blk - 16) >> 2) & 1) == 0); const int d = rope ? (p >> 1) + 64 * (p & 1) : p; return blk * 128 + d; }
;     if (c < OFF_Z) return c + 2096;
; template <int MAP, bool KS, bool KPERM = false>
; __device__ __forceinline__ void p0_transpose_item(const float* W, int K, int Nsrc, int nblk, bf16* WT, const float* ksA, const float* ksB, int ksplit, LAS float* scr, int item, int lane) {
;     const int kb = item / nblk, nb = item % nblk, k0 = 64 * kb, n0 = 32 * nb;
;     const int nr = n0 + (lane & 31); const int sc = MAP == 1 ? src_col_in(nr) : (MAP == 2 ? nat_dim(nr) : nr);
;     float v[32];
; #pragma unroll
;     for (int i = 0; i < 32; ++i) { const int k = k0 + 2 * i + (lane >> 5); const int ksrc = KPERM ? ((k & ~127) + nat_dim(k & 127)) : k;
;         v[i] = sc >= 0 ? W[(size_t)ksrc * Nsrc + sc] : 0.f; }
; #pragma unroll
;     for (int i = 0; i < 32; ++i) { const int kk = 2 * i + (lane >> 5); const int k = k0 + kk;
;         if (KS) v[i] *= (k < ksplit ? ksA[k] : ksB[k - ksplit]);
;         scr[kk * 33 + (lane & 31)] = v[i]; }
;     LDS_WAIT(); asm volatile("" ::: "memory");
;     const int c = lane & 7;
; #pragma unroll
;     for (int j = 0; j < 4; ++j) { const int n = (lane >> 3) + 8 * j; const LAS float* s = scr + (8 * c) * 33 + n;
;         v4u o; o.x = pk2(s[0 * 33], s[1 * 33]); o.y = pk2(s[2 * 33], s[3 * 33]); o.z = pk2(s[4 * 33], s[5 * 33]); o.w = pk2(s[6 * 33], s[7 * 33]);
;         *(GAS v4u*)(WT + (size_t)(n0 + n) * K + k0 + 8 * c) = o; }
;     LDS_WAIT(); asm volatile("" ::: "memory");
	s_add_i32 s24, s23, 80
	s_lshl_b32 s20, s24, 7
	s_cmp_lt_u32 s24, 40
	s_cselect_b32 s21, 0, 0x830
	s_cmp_lt_u32 s24, 72
	s_cselect_b32 s21, s21, 0xfffff030
	s_add_i32 s20, s20, s21
	s_lshl_b32 s20, s20, 2
	s_add_u32 s8, s46, s20
	s_addc_u32 s9, s47, 0
	global_load_dwordx4 v[144:147], v76, s[8:9]
	s_add_u32 s8, s8, 0x16280
	s_addc_u32 s9, s9, 0
	global_load_dwordx4 v[148:151], v76, s[8:9]
	s_add_u32 s8, s8, 0x16280
	s_addc_u32 s9, s9, 0
	global_load_dwordx4 v[152:155], v76, s[8:9]
	s_add_u32 s8, s8, 0x16280
	s_addc_u32 s9, s9, 0
	global_load_dwordx4 v[156:159], v76, s[8:9]
	s_add_u32 s8, s8, 0x16280
	s_addc_u32 s9, s9, 0
	global_load_dwordx4 v[160:163], v76, s[8:9]
	s_add_u32 s8, s8, 0x16280
	s_addc_u32 s9, s9, 0
	global_load_dwordx4 v[164:167], v76, s[8:9]
	s_add_u32 s8, s8, 0x16280
	s_addc_u32 s9, s9, 0
	global_load_dwordx4 v[168:171], v76, s[8:9]
	s_add_u32 s8, s8, 0x16280
	s_addc_u32 s9, s9, 0
	global_load_dwordx4 v[172:175], v76, s[8:9]
	s_add_i32 s24, s23, 64
	s_mul_i32 s20, s24, 0x100000
	s_add_u32 s6, s48, s20
	s_addc_u32 s7, s49, 0
	s_cmp_lt_u32 s24, 16
	s_cselect_b32 s20, 1, 0
	s_sub_i32 s21, s24, 16
	s_bitcmp0_b32 s21, 2
	s_cselect_b32 s21, 1, 0
	s_cmp_lt_u32 s24, 40
	s_cselect_b32 s21, s21, 0
	s_or_b32 s20, s20, s21
	s_cmp_lg_u32 s20, 0
	s_cselect_b64 s[20:21], -1, 0
	v_cndmask_b32_e64 v91, v83, v87, s[20:21]
	v_cndmask_b32_e64 v92, v84, v88, s[20:21]
	v_cndmask_b32_e64 v93, v85, v89, s[20:21]
	v_cndmask_b32_e64 v94, v86, v90, s[20:21]
	ds_read_b32 v226, v112
	ds_read_b32 v227, v112 offset:512
	ds_read_b32 v228, v112 offset:1024
	ds_read_b32 v229, v112 offset:1536
	ds_read_b32 v230, v112 offset:2048
	ds_read_b32 v231, v112 offset:2560
	ds_read_b32 v232, v112 offset:3072
	ds_read_b32 v233, v112 offset:3584
	s_waitcnt lgkmcnt(0)
	v_bfe_u32 v120, v226, 16, 1
	v_bfe_u32 v121, v227, 16, 1
	v_bfe_u32 v122, v228, 16, 1
	v_bfe_u32 v123, v229, 16, 1
	v_bfe_u32 v124, v230, 16, 1
	v_bfe_u32 v125, v231, 16, 1
	v_bfe_u32 v126, v232, 16, 1
	v_bfe_u32 v127, v233, 16, 1
	v_add3_u32 v226, v226, v120, s63
	v_add3_u32 v227, v227, v121, s63
	v_add3_u32 v228, v228, v122, s63
	v_add3_u32 v229, v229, v123, s63
	v_add3_u32 v230, v230, v124, s63
	v_add3_u32 v231, v231, v125, s63
	v_add3_u32 v232, v232, v126, s63
	v_add3_u32 v233, v233, v127, s63
	v_perm_b32 v242, v227, v226, s64
	v_perm_b32 v243, v229, v228, s64
	v_perm_b32 v244, v231, v230, s64
	v_perm_b32 v245, v233, v232, s64
	s_nop 0
	global_store_dwordx4 v91, v[242:245], s[6:7]
	ds_read_b32 v226, v114
	ds_read_b32 v227, v114 offset:512
	ds_read_b32 v228, v114 offset:1024
	ds_read_b32 v229, v114 offset:1536
	ds_read_b32 v230, v114 offset:2048
	ds_read_b32 v231, v114 offset:2560
	ds_read_b32 v232, v114 offset:3072
	ds_read_b32 v233, v114 offset:3584
	s_waitcnt lgkmcnt(0)
	v_bfe_u32 v120, v226, 16, 1
	v_bfe_u32 v121, v227, 16, 1
	v_bfe_u32 v122, v228, 16, 1
	v_bfe_u32 v123, v229, 16, 1
	v_bfe_u32 v124, v230, 16, 1
	v_bfe_u32 v125, v231, 16, 1
	v_bfe_u32 v126, v232, 16, 1
	v_bfe_u32 v127, v233, 16, 1
	v_add3_u32 v226, v226, v120, s63
	v_add3_u32 v227, v227, v121, s63
	v_add3_u32 v228, v228, v122, s63
	v_add3_u32 v229, v229, v123, s63
	v_add3_u32 v230, v230, v124, s63
	v_add3_u32 v231, v231, v125, s63
	v_add3_u32 v232, v232, v126, s63
	v_add3_u32 v233, v233, v127, s63
	v_perm_b32 v242, v227, v226, s64
	v_perm_b32 v243, v229, v228, s64
	v_perm_b32 v244, v231, v230, s64
	v_perm_b32 v245, v233, v232, s64
	s_nop 0
	global_store_dwordx4 v92, v[242:245], s[6:7]
	ds_read_b32 v226, v116
	ds_read_b32 v227, v116 offset:512
	ds_read_b32 v228, v116 offset:1024
	ds_read_b32 v229, v116 offset:1536
	ds_read_b32 v230, v116 offset:2048
	ds_read_b32 v231, v116 offset:2560
	ds_read_b32 v232, v116 offset:3072
	ds_read_b32 v233, v116 offset:3584
	s_waitcnt lgkmcnt(0)
	v_bfe_u32 v120, v226, 16, 1
	v_bfe_u32 v121, v227, 16, 1
	v_bfe_u32 v122, v228, 16, 1
	v_bfe_u32 v123, v229, 16, 1
	v_bfe_u32 v124, v230, 16, 1
	v_bfe_u32 v125, v231, 16, 1
	v_bfe_u32 v126, v232, 16, 1
	v_bfe_u32 v127, v233, 16, 1
	v_add3_u32 v226, v226, v120, s63
	v_add3_u32 v227, v227, v121, s63
	v_add3_u32 v228, v228, v122, s63
	v_add3_u32 v229, v229, v123, s63
	v_add3_u32 v230, v230, v124, s63
	v_add3_u32 v231, v231, v125, s63
	v_add3_u32 v232, v232, v126, s63
	v_add3_u32 v233, v233, v127, s63
	v_perm_b32 v242, v227, v226, s64
	v_perm_b32 v243, v229, v228, s64
	v_perm_b32 v244, v231, v230, s64
	v_perm_b32 v245, v233, v232, s64
	s_nop 0
	global_store_dwordx4 v93, v[242:245], s[6:7]
	ds_read_b32 v226, v118
	ds_read_b32 v227, v118 offset:512
	ds_read_b32 v228, v118 offset:1024
	ds_read_b32 v229, v118 offset:1536
	ds_read_b32 v230, v118 offset:2048
	ds_read_b32 v231, v118 offset:2560
	ds_read_b32 v232, v118 offset:3072
	ds_read_b32 v233, v118 offset:3584
	s_waitcnt lgkmcnt(0)
	v_bfe_u32 v120, v226, 16, 1
	v_bfe_u32 v121, v227, 16, 1
	v_bfe_u32 v122, v228, 16, 1
	v_bfe_u32 v123, v229, 16, 1
	v_bfe_u32 v124, v230, 16, 1
	v_bfe_u32 v125, v231, 16, 1
	v_bfe_u32 v126, v232, 16, 1
	v_bfe_u32 v127, v233, 16, 1
	v_add3_u32 v226, v226, v120, s63
	v_add3_u32 v227, v227, v121, s63
	v_add3_u32 v228, v228, v122, s63
	v_add3_u32 v229, v229, v123, s63
	v_add3_u32 v230, v230, v124, s63
	v_add3_u32 v231, v231, v125, s63
	v_add3_u32 v232, v232, v126, s63
	v_add3_u32 v233, v233, v127, s63
	v_perm_b32 v242, v227, v226, s64
	v_perm_b32 v243, v229, v228, s64
	v_perm_b32 v244, v231, v230, s64
	v_perm_b32 v245, v233, v232, s64
	s_nop 0
	global_store_dwordx4 v94, v[242:245], s[6:7]
	s_waitcnt vmcnt(16)
	v_mul_f32_e32 v176, v42, v176
	v_mul_f32_e32 v177, v42, v177
	v_mul_f32_e32 v178, v42, v178
	v_mul_f32_e32 v179, v42, v179
	ds_write_b128 v210, v[176:179]
	v_mul_f32_e32 v180, v43, v180
	v_mul_f32_e32 v181, v43, v181
	v_mul_f32_e32 v182, v43, v182
	v_mul_f32_e32 v183, v43, v183
	ds_write_b128 v210, v[180:183] offset:1024
	v_mul_f32_e32 v184, v44, v184
	v_mul_f32_e32 v185, v44, v185
	v_mul_f32_e32 v186, v44, v186
	v_mul_f32_e32 v187, v44, v187
	ds_write_b128 v210, v[184:187] offset:2048
	v_mul_f32_e32 v188, v45, v188
	v_mul_f32_e32 v189, v45, v189
	v_mul_f32_e32 v190, v45, v190
	v_mul_f32_e32 v191, v45, v191
	ds_write_b128 v210, v[188:191] offset:3072
	v_mul_f32_e32 v192, v46, v192
	v_mul_f32_e32 v193, v46, v193
	v_mul_f32_e32 v194, v46, v194
	v_mul_f32_e32 v195, v46, v195
	ds_write_b128 v210, v[192:195] offset:4096
	v_mul_f32_e32 v196, v47, v196
	v_mul_f32_e32 v197, v47, v197
	v_mul_f32_e32 v198, v47, v198
	v_mul_f32_e32 v199, v47, v199
	ds_write_b128 v210, v[196:199] offset:5120
	v_mul_f32_e32 v200, v48, v200
	v_mul_f32_e32 v201, v48, v201
	v_mul_f32_e32 v202, v48, v202
	v_mul_f32_e32 v203, v48, v203
	ds_write_b128 v210, v[200:203] offset:6144
	v_mul_f32_e32 v204, v49, v204
	v_mul_f32_e32 v205, v49, v205
	v_mul_f32_e32 v206, v49, v206
	v_mul_f32_e32 v207, v49, v207
	ds_write_b128 v210, v[204:207] offset:7168
	s_waitcnt lgkmcnt(0)
	s_barrier
; #define GAS __attribute__((address_space(1)))
; #define LAS __attribute__((address_space(3)))
; #define LDS_WAIT() asm volatile("s_waitcnt lgkmcnt(0)" ::: "memory")
; __device__ __forceinline__ unsigned pk2(float lo, float hi) { return f2bf(lo) | (f2bf(hi) << 16); }
; __device__ __forceinline__ int nat_dim(int p) { return (p >> 1) + 64 * (p & 1); }
; __device__ __forceinline__ int src_col_in(int c) {
;     if (c < 5120) { const int blk = c >> 7, p = c & 127; const bool rope = blk < 16 || ((((blk - 16) >> 2) & 1) == 0); const int d = rope ? (p >> 1) + 64 * (p & 1) : p; return blk * 128 + d; }
;     if (c < OFF_Z) return c + 2096;
; template <int MAP, bool KS, bool KPERM = false>
; __device__ __forceinline__ void p0_transpose_item(const float* W, int K, int Nsrc, int nblk, bf16* WT, const float* ksA, const float* ksB, int ksplit, LAS float* scr, int item, int lane) {
;     const int kb = item / nblk, nb = item % nblk, k0 = 64 * kb, n0 = 32 * nb;
;     const int nr = n0 + (lane & 31); const int sc = MAP == 1 ? src_col_in(nr) : (MAP == 2 ? nat_dim(nr) : nr);
;     float v[32];
; #pragma unroll
;     for (int i = 0; i < 32; ++i) { const int k = k0 + 2 * i + (lane >> 5); const int ksrc = KPERM ? ((k & ~127) + nat_dim(k & 127)) : k;
;         v[i] = sc >= 0 ? W[(size_t)ksrc * Nsrc + sc] : 0.f; }
; #pragma unroll
;     for (int i = 0; i < 32; ++i) { const int kk = 2 * i + (lane >> 5); const int k = k0 + kk;
;         if (KS) v[i] *= (k < ksplit ? ksA[k] : ksB[k - ksplit]);
;         scr[kk * 33 + (lane & 31)] = v[i]; }
;     LDS_WAIT(); asm volatile("" ::: "memory");
;     const int c = lane & 7;
; #pragma unroll
;     for (int j = 0; j < 4; ++j) { const int n = (lane >> 3) + 8 * j; const LAS float* s = scr + (8 * c) * 33 + n;
;         v4u o; o.x = pk2(s[0 * 33], s[1 * 33]); o.y = pk2(s[2 * 33], s[3 * 33]); o.z = pk2(s[4 * 33], s[5 * 33]); o.w = pk2(s[6 * 33], s[7 * 33]);
;         *(GAS v4u*)(WT + (size_t)(n0 + n) * K + k0 + 8 * c) = o; }
;     LDS_WAIT(); asm volatile("" ::: "memory");
	s_add_i32 s24, s23, 0
	s_lshl_b32 s20, s24, 7
	s_cmp_lt_u32 s24, 40
	s_cselect_b32 s21, 0, 0x830
	s_cmp_lt_u32 s24, 72
	s_cselect_b32 s21, s21, 0xfffff030
	s_add_i32 s20, s20, s21
	s_lshl_b32 s20, s20, 2
	s_add_u32 s8, s50, s20
	s_addc_u32 s9, s51, 0
	global_load_dwordx4 v[176:179], v76, s[8:9]
	s_add_u32 s8, s8, 0x16280
	s_addc_u32 s9, s9, 0
	global_load_dwordx4 v[180:183], v76, s[8:9]
	s_add_u32 s8, s8, 0x16280
	s_addc_u32 s9, s9, 0
	global_load_dwordx4 v[184:187], v76, s[8:9]
	s_add_u32 s8, s8, 0x16280
	s_addc_u32 s9, s9, 0
	global_load_dwordx4 v[188:191], v76, s[8:9]
	s_add_u32 s8, s8, 0x16280
	s_addc_u32 s9, s9, 0
	global_load_dwordx4 v[192:195], v76, s[8:9]
	s_add_u32 s8, s8, 0x16280
	s_addc_u32 s9, s9, 0
	global_load_dwordx4 v[196:199], v76, s[8:9]
	s_add_u32 s8, s8, 0x16280
	s_addc_u32 s9, s9, 0
	global_load_dwordx4 v[200:203], v76, s[8:9]
	s_add_u32 s8, s8, 0x16280
	s_addc_u32 s9, s9, 0
	global_load_dwordx4 v[204:207], v76, s[8:9]
	s_add_i32 s24, s23, 72
	s_mul_i32 s20, s24, 0x100000
	s_add_u32 s6, s48, s20
	s_addc_u32 s7, s49, 0
	s_cmp_lt_u32 s24, 16
	s_cselect_b32 s20, 1, 0
	s_sub_i32 s21, s24, 16
	s_bitcmp0_b32 s21, 2
	s_cselect_b32 s21, 1, 0
	s_cmp_lt_u32 s24, 40
	s_cselect_b32 s21, s21, 0
	s_or_b32 s20, s20, s21
	s_cmp_lg_u32 s20, 0
	s_cselect_b64 s[20:21], -1, 0
	v_cndmask_b32_e64 v91, v83, v87, s[20:21]
	v_cndmask_b32_e64 v92, v84, v88, s[20:21]
	v_cndmask_b32_e64 v93, v85, v89, s[20:21]
	v_cndmask_b32_e64 v94, v86, v90, s[20:21]
	ds_read_b32 v226, v113
	ds_read_b32 v227, v113 offset:512
	ds_read_b32 v228, v113 offset:1024
	ds_read_b32 v229, v113 offset:1536
	ds_read_b32 v230, v113 offset:2048
	ds_read_b32 v231, v113 offset:2560
	ds_read_b32 v232, v113 offset:3072
	ds_read_b32 v233, v113 offset:3584
	s_waitcnt lgkmcnt(0)
	v_bfe_u32 v120, v226, 16, 1
	v_bfe_u32 v121, v227, 16, 1
	v_bfe_u32 v122, v228, 16, 1
	v_bfe_u32 v123, v229, 16, 1
	v_bfe_u32 v124, v230, 16, 1
	v_bfe_u32 v125, v231, 16, 1
	v_bfe_u32 v126, v232, 16, 1
	v_bfe_u32 v127, v233, 16, 1
	v_add3_u32 v226, v226, v120, s63
	v_add3_u32 v227, v227, v121, s63
	v_add3_u32 v228, v228, v122, s63
	v_add3_u32 v229, v229, v123, s63
	v_add3_u32 v230, v230, v124, s63
	v_add3_u32 v231, v231, v125, s63
	v_add3_u32 v232, v232, v126, s63
	v_add3_u32 v233, v233, v127, s63
	v_perm_b32 v242, v227, v226, s64
	v_perm_b32 v243, v229, v228, s64
	v_perm_b32 v244, v231, v230, s64
	v_perm_b32 v245, v233, v232, s64
	s_nop 0
	global_store_dwordx4 v91, v[242:245], s[6:7]
	ds_read_b32 v226, v115
	ds_read_b32 v227, v115 offset:512
	ds_read_b32 v228, v115 offset:1024
	ds_read_b32 v229, v115 offset:1536
	ds_read_b32 v230, v115 offset:2048
	ds_read_b32 v231, v115 offset:2560
	ds_read_b32 v232, v115 offset:3072
	ds_read_b32 v233, v115 offset:3584
	s_waitcnt lgkmcnt(0)
	v_bfe_u32 v120, v226, 16, 1
	v_bfe_u32 v121, v227, 16, 1
	v_bfe_u32 v122, v228, 16, 1
	v_bfe_u32 v123, v229, 16, 1
	v_bfe_u32 v124, v230, 16, 1
	v_bfe_u32 v125, v231, 16, 1
	v_bfe_u32 v126, v232, 16, 1
	v_bfe_u32 v127, v233, 16, 1
	v_add3_u32 v226, v226, v120, s63
	v_add3_u32 v227, v227, v121, s63
	v_add3_u32 v228, v228, v122, s63
	v_add3_u32 v229, v229, v123, s63
	v_add3_u32 v230, v230, v124, s63
	v_add3_u32 v231, v231, v125, s63
	v_add3_u32 v232, v232, v126, s63
	v_add3_u32 v233, v233, v127, s63
	v_perm_b32 v242, v227, v226, s64
	v_perm_b32 v243, v229, v228, s64
	v_perm_b32 v244, v231, v230, s64
	v_perm_b32 v245, v233, v232, s64
	s_nop 0
	global_store_dwordx4 v92, v[242:245], s[6:7]
	ds_read_b32 v226, v117
	ds_read_b32 v227, v117 offset:512
	ds_read_b32 v228, v117 offset:1024
	ds_read_b32 v229, v117 offset:1536
	ds_read_b32 v230, v117 offset:2048
	ds_read_b32 v231, v117 offset:2560
	ds_read_b32 v232, v117 offset:3072
	ds_read_b32 v233, v117 offset:3584
	s_waitcnt lgkmcnt(0)
	v_bfe_u32 v120, v226, 16, 1
	v_bfe_u32 v121, v227, 16, 1
	v_bfe_u32 v122, v228, 16, 1
	v_bfe_u32 v123, v229, 16, 1
	v_bfe_u32 v124, v230, 16, 1
	v_bfe_u32 v125, v231, 16, 1
	v_bfe_u32 v126, v232, 16, 1
	v_bfe_u32 v127, v233, 16, 1
	v_add3_u32 v226, v226, v120, s63
	v_add3_u32 v227, v227, v121, s63
	v_add3_u32 v228, v228, v122, s63
	v_add3_u32 v229, v229, v123, s63
	v_add3_u32 v230, v230, v124, s63
	v_add3_u32 v231, v231, v125, s63
	v_add3_u32 v232, v232, v126, s63
	v_add3_u32 v233, v233, v127, s63
	v_perm_b32 v242, v227, v226, s64
	v_perm_b32 v243, v229, v228, s64
	v_perm_b32 v244, v231, v230, s64
	v_perm_b32 v245, v233, v232, s64
	s_nop 0
	global_store_dwordx4 v93, v[242:245], s[6:7]
	ds_read_b32 v226, v119
	ds_read_b32 v227, v119 offset:512
	ds_read_b32 v228, v119 offset:1024
	ds_read_b32 v229, v119 offset:1536
	ds_read_b32 v230, v119 offset:2048
	ds_read_b32 v231, v119 offset:2560
	ds_read_b32 v232, v119 offset:3072
	ds_read_b32 v233, v119 offset:3584
	s_waitcnt lgkmcnt(0)
	v_bfe_u32 v120, v226, 16, 1
	v_bfe_u32 v121, v227, 16, 1
	v_bfe_u32 v122, v228, 16, 1
	v_bfe_u32 v123, v229, 16, 1
	v_bfe_u32 v124, v230, 16, 1
	v_bfe_u32 v125, v231, 16, 1
	v_bfe_u32 v126, v232, 16, 1
	v_bfe_u32 v127, v233, 16, 1
	v_add3_u32 v226, v226, v120, s63
	v_add3_u32 v227, v227, v121, s63
	v_add3_u32 v228, v228, v122, s63
	v_add3_u32 v229, v229, v123, s63
	v_add3_u32 v230, v230, v124, s63
	v_add3_u32 v231, v231, v125, s63
	v_add3_u32 v232, v232, v126, s63
	v_add3_u32 v233, v233, v127, s63
	v_perm_b32 v242, v227, v226, s64
	v_perm_b32 v243, v229, v228, s64
	v_perm_b32 v244, v231, v230, s64
	v_perm_b32 v245, v233, v232, s64
	s_nop 0
	global_store_dwordx4 v94, v[242:245], s[6:7]
	s_waitcnt vmcnt(16)
	v_mul_f32_e32 v144, v42, v144
	v_mul_f32_e32 v145, v42, v145
	v_mul_f32_e32 v146, v42, v146
	v_mul_f32_e32 v147, v42, v147
	ds_write_b128 v209, v[144:147]
	v_mul_f32_e32 v148, v43, v148
	v_mul_f32_e32 v149, v43, v149
	v_mul_f32_e32 v150, v43, v150
	v_mul_f32_e32 v151, v43, v151
	ds_write_b128 v209, v[148:151] offset:1024
	v_mul_f32_e32 v152, v44, v152
	v_mul_f32_e32 v153, v44, v153
	v_mul_f32_e32 v154, v44, v154
	v_mul_f32_e32 v155, v44, v155
	ds_write_b128 v209, v[152:155] offset:2048
	v_mul_f32_e32 v156, v45, v156
	v_mul_f32_e32 v157, v45, v157
	v_mul_f32_e32 v158, v45, v158
	v_mul_f32_e32 v159, v45, v159
	ds_write_b128 v209, v[156:159] offset:3072
	v_mul_f32_e32 v160, v46, v160
	v_mul_f32_e32 v161, v46, v161
	v_mul_f32_e32 v162, v46, v162
	v_mul_f32_e32 v163, v46, v163
	ds_write_b128 v209, v[160:163] offset:4096
	v_mul_f32_e32 v164, v47, v164
	v_mul_f32_e32 v165, v47, v165
	v_mul_f32_e32 v166, v47, v166
	v_mul_f32_e32 v167, v47, v167
	ds_write_b128 v209, v[164:167] offset:5120
	v_mul_f32_e32 v168, v48, v168
	v_mul_f32_e32 v169, v48, v169
	v_mul_f32_e32 v170, v48, v170
	v_mul_f32_e32 v171, v48, v171
	ds_write_b128 v209, v[168:171] offset:6144
	v_mul_f32_e32 v172, v49, v172
	v_mul_f32_e32 v173, v49, v173
	v_mul_f32_e32 v174, v49, v174
	v_mul_f32_e32 v175, v49, v175
	ds_write_b128 v209, v[172:175] offset:7168
	s_waitcnt lgkmcnt(0)
	s_barrier
; #define GAS __attribute__((address_space(1)))
; #define LAS __attribute__((address_space(3)))
; #define LDS_WAIT() asm volatile("s_waitcnt lgkmcnt(0)" ::: "memory")
; __device__ __forceinline__ unsigned pk2(float lo, float hi) { return f2bf(lo) | (f2bf(hi) << 16); }
; __device__ __forceinline__ int nat_dim(int p) { return (p >> 1) + 64 * (p & 1); }
; __device__ __forceinline__ int src_col_in(int c) {
;     if (c < 5120) { const int blk = c >> 7, p = c & 127; const bool rope = blk < 16 || ((((blk - 16) >> 2) & 1) == 0); const int d = rope ? (p >> 1) + 64 * (p & 1) : p; return blk * 128 + d; }
;     if (c < OFF_Z) return c + 2096;
; template <int MAP, bool KS, bool KPERM = false>
; __device__ __forceinline__ void p0_transpose_item(const float* W, int K, int Nsrc, int nblk, bf16* WT, const float* ksA, const float* ksB, int ksplit, LAS float* scr, int item, int lane) {
;     const int kb = item / nblk, nb = item % nblk, k0 = 64 * kb, n0 = 32 * nb;
;     const int nr = n0 + (lane & 31); const int sc = MAP == 1 ? src_col_in(nr) : (MAP == 2 ? nat_dim(nr) : nr);
;     float v[32];
; #pragma unroll
;     for (int i = 0; i < 32; ++i) { const int k = k0 + 2 * i + (lane >> 5); const int ksrc = KPERM ? ((k & ~127) + nat_dim(k & 127)) : k;
;         v[i] = sc >= 0 ? W[(size_t)ksrc * Nsrc + sc] : 0.f; }
; #pragma unroll
;     for (int i = 0; i < 32; ++i) { const int kk = 2 * i + (lane >> 5); const int k = k0 + kk;
;         if (KS) v[i] *= (k < ksplit ? ksA[k] : ksB[k - ksplit]);
;         scr[kk * 33 + (lane & 31)] = v[i]; }
;     LDS_WAIT(); asm volatile("" ::: "memory");
;     const int c = lane & 7;
; #pragma unroll
;     for (int j = 0; j < 4; ++j) { const int n = (lane >> 3) + 8 * j; const LAS float* s = scr + (8 * c) * 33 + n;
;         v4u o; o.x = pk2(s[0 * 33], s[1 * 33]); o.y = pk2(s[2 * 33], s[3 * 33]); o.z = pk2(s[4 * 33], s[5 * 33]); o.w = pk2(s[6 * 33], s[7 * 33]);
;         *(GAS v4u*)(WT + (size_t)(n0 + n) * K + k0 + 8 * c) = o; }
;     LDS_WAIT(); asm volatile("" ::: "memory");
	s_add_i32 s24, s23, 8
	s_lshl_b32 s20, s24, 7
	s_cmp_lt_u32 s24, 40
	s_cselect_b32 s21, 0, 0x830
	s_cmp_lt_u32 s24, 72
	s_cselect_b32 s21, s21, 0xfffff030
	s_add_i32 s20, s20, s21
	s_lshl_b32 s20, s20, 2
	s_add_u32 s8, s50, s20
	s_addc_u32 s9, s51, 0
	global_load_dwordx4 v[144:147], v76, s[8:9]
	s_add_u32 s8, s8, 0x16280
	s_addc_u32 s9, s9, 0
	global_load_dwordx4 v[148:151], v76, s[8:9]
	s_add_u32 s8, s8, 0x16280
	s_addc_u32 s9, s9, 0
	global_load_dwordx4 v[152:155], v76, s[8:9]
	s_add_u32 s8, s8, 0x16280
	s_addc_u32 s9, s9, 0
	global_load_dwordx4 v[156:159], v76, s[8:9]
	s_add_u32 s8, s8, 0x16280
	s_addc_u32 s9, s9, 0
	global_load_dwordx4 v[160:163], v76, s[8:9]
	s_add_u32 s8, s8, 0x16280
	s_addc_u32 s9, s9, 0
	global_load_dwordx4 v[164:167], v76, s[8:9]
	s_add_u32 s8, s8, 0x16280
	s_addc_u32 s9, s9, 0
	global_load_dwordx4 v[168:171], v76, s[8:9]
	s_add_u32 s8, s8, 0x16280
	s_addc_u32 s9, s9, 0
	global_load_dwordx4 v[172:175], v76, s[8:9]
	s_add_i32 s24, s23, 80
	s_mul_i32 s20, s24, 0x100000
	s_add_u32 s6, s48, s20
	s_addc_u32 s7, s49, 0
	s_cmp_lt_u32 s24, 16
	s_cselect_b32 s20, 1, 0
	s_sub_i32 s21, s24, 16
	s_bitcmp0_b32 s21, 2
	s_cselect_b32 s21, 1, 0
	s_cmp_lt_u32 s24, 40
	s_cselect_b32 s21, s21, 0
	s_or_b32 s20, s20, s21
	s_cmp_lg_u32 s20, 0
	s_cselect_b64 s[20:21], -1, 0
	v_cndmask_b32_e64 v91, v83, v87, s[20:21]
	v_cndmask_b32_e64 v92, v84, v88, s[20:21]
	v_cndmask_b32_e64 v93, v85, v89, s[20:21]
	v_cndmask_b32_e64 v94, v86, v90, s[20:21]
	ds_read_b32 v226, v112
	ds_read_b32 v227, v112 offset:512
	ds_read_b32 v228, v112 offset:1024
	ds_read_b32 v229, v112 offset:1536
	ds_read_b32 v230, v112 offset:2048
	ds_read_b32 v231, v112 offset:2560
	ds_read_b32 v232, v112 offset:3072
	ds_read_b32 v233, v112 offset:3584
	s_waitcnt lgkmcnt(0)
	v_bfe_u32 v120, v226, 16, 1
	v_bfe_u32 v121, v227, 16, 1
	v_bfe_u32 v122, v228, 16, 1
	v_bfe_u32 v123, v229, 16, 1
	v_bfe_u32 v124, v230, 16, 1
	v_bfe_u32 v125, v231, 16, 1
	v_bfe_u32 v126, v232, 16, 1
	v_bfe_u32 v127, v233, 16, 1
	v_add3_u32 v226, v226, v120, s63
	v_add3_u32 v227, v227, v121, s63
	v_add3_u32 v228, v228, v122, s63
	v_add3_u32 v229, v229, v123, s63
	v_add3_u32 v230, v230, v124, s63
	v_add3_u32 v231, v231, v125, s63
	v_add3_u32 v232, v232, v126, s63
	v_add3_u32 v233, v233, v127, s63
	v_perm_b32 v242, v227, v226, s64
	v_perm_b32 v243, v229, v228, s64
	v_perm_b32 v244, v231, v230, s64
	v_perm_b32 v245, v233, v232, s64
	s_nop 0
	global_store_dwordx4 v91, v[242:245], s[6:7]
	ds_read_b32 v226, v114
	ds_read_b32 v227, v114 offset:512
	ds_read_b32 v228, v114 offset:1024
	ds_read_b32 v229, v114 offset:1536
	ds_read_b32 v230, v114 offset:2048
	ds_read_b32 v231, v114 offset:2560
	ds_read_b32 v232, v114 offset:3072
	ds_read_b32 v233, v114 offset:3584
	s_waitcnt lgkmcnt(0)
	v_bfe_u32 v120, v226, 16, 1
	v_bfe_u32 v121, v227, 16, 1
	v_bfe_u32 v122, v228, 16, 1
	v_bfe_u32 v123, v229, 16, 1
	v_bfe_u32 v124, v230, 16, 1
	v_bfe_u32 v125, v231, 16, 1
	v_bfe_u32 v126, v232, 16, 1
	v_bfe_u32 v127, v233, 16, 1
	v_add3_u32 v226, v226, v120, s63
	v_add3_u32 v227, v227, v121, s63
	v_add3_u32 v228, v228, v122, s63
	v_add3_u32 v229, v229, v123, s63
	v_add3_u32 v230, v230, v124, s63
	v_add3_u32 v231, v231, v125, s63
	v_add3_u32 v232, v232, v126, s63
	v_add3_u32 v233, v233, v127, s63
	v_perm_b32 v242, v227, v226, s64
	v_perm_b32 v243, v229, v228, s64
	v_perm_b32 v244, v231, v230, s64
	v_perm_b32 v245, v233, v232, s64
	s_nop 0
	global_store_dwordx4 v92, v[242:245], s[6:7]
	ds_read_b32 v226, v116
	ds_read_b32 v227, v116 offset:512
	ds_read_b32 v228, v116 offset:1024
	ds_read_b32 v229, v116 offset:1536
	ds_read_b32 v230, v116 offset:2048
	ds_read_b32 v231, v116 offset:2560
	ds_read_b32 v232, v116 offset:3072
	ds_read_b32 v233, v116 offset:3584
	s_waitcnt lgkmcnt(0)
	v_bfe_u32 v120, v226, 16, 1
	v_bfe_u32 v121, v227, 16, 1
	v_bfe_u32 v122, v228, 16, 1
	v_bfe_u32 v123, v229, 16, 1
	v_bfe_u32 v124, v230, 16, 1
	v_bfe_u32 v125, v231, 16, 1
	v_bfe_u32 v126, v232, 16, 1
	v_bfe_u32 v127, v233, 16, 1
	v_add3_u32 v226, v226, v120, s63
	v_add3_u32 v227, v227, v121, s63
	v_add3_u32 v228, v228, v122, s63
	v_add3_u32 v229, v229, v123, s63
	v_add3_u32 v230, v230, v124, s63
	v_add3_u32 v231, v231, v125, s63
	v_add3_u32 v232, v232, v126, s63
	v_add3_u32 v233, v233, v127, s63
	v_perm_b32 v242, v227, v226, s64
	v_perm_b32 v243, v229, v228, s64
	v_perm_b32 v244, v231, v230, s64
	v_perm_b32 v245, v233, v232, s64
	s_nop 0
	global_store_dwordx4 v93, v[242:245], s[6:7]
	ds_read_b32 v226, v118
	ds_read_b32 v227, v118 offset:512
	ds_read_b32 v228, v118 offset:1024
	ds_read_b32 v229, v118 offset:1536
	ds_read_b32 v230, v118 offset:2048
	ds_read_b32 v231, v118 offset:2560
	ds_read_b32 v232, v118 offset:3072
	ds_read_b32 v233, v118 offset:3584
	s_waitcnt lgkmcnt(0)
	v_bfe_u32 v120, v226, 16, 1
	v_bfe_u32 v121, v227, 16, 1
	v_bfe_u32 v122, v228, 16, 1
	v_bfe_u32 v123, v229, 16, 1
	v_bfe_u32 v124, v230, 16, 1
	v_bfe_u32 v125, v231, 16, 1
	v_bfe_u32 v126, v232, 16, 1
	v_bfe_u32 v127, v233, 16, 1
	v_add3_u32 v226, v226, v120, s63
	v_add3_u32 v227, v227, v121, s63
	v_add3_u32 v228, v228, v122, s63
	v_add3_u32 v229, v229, v123, s63
	v_add3_u32 v230, v230, v124, s63
	v_add3_u32 v231, v231, v125, s63
	v_add3_u32 v232, v232, v126, s63
	v_add3_u32 v233, v233, v127, s63
	v_perm_b32 v242, v227, v226, s64
	v_perm_b32 v243, v229, v228, s64
	v_perm_b32 v244, v231, v230, s64
	v_perm_b32 v245, v233, v232, s64
	s_nop 0
	global_store_dwordx4 v94, v[242:245], s[6:7]
	s_waitcnt vmcnt(16)
	v_mul_f32_e32 v176, v50, v176
	v_mul_f32_e32 v177, v50, v177
	v_mul_f32_e32 v178, v50, v178
	v_mul_f32_e32 v179, v50, v179
	ds_write_b128 v210, v[176:179]
	v_mul_f32_e32 v180, v51, v180
	v_mul_f32_e32 v181, v51, v181
	v_mul_f32_e32 v182, v51, v182
	v_mul_f32_e32 v183, v51, v183
	ds_write_b128 v210, v[180:183] offset:1024
	v_mul_f32_e32 v184, v52, v184
	v_mul_f32_e32 v185, v52, v185
	v_mul_f32_e32 v186, v52, v186
	v_mul_f32_e32 v187, v52, v187
	ds_write_b128 v210, v[184:187] offset:2048
	v_mul_f32_e32 v188, v53, v188
	v_mul_f32_e32 v189, v53, v189
	v_mul_f32_e32 v190, v53, v190
	v_mul_f32_e32 v191, v53, v191
	ds_write_b128 v210, v[188:191] offset:3072
	v_mul_f32_e32 v192, v54, v192
	v_mul_f32_e32 v193, v54, v193
	v_mul_f32_e32 v194, v54, v194
	v_mul_f32_e32 v195, v54, v195
	ds_write_b128 v210, v[192:195] offset:4096
	v_mul_f32_e32 v196, v55, v196
	v_mul_f32_e32 v197, v55, v197
	v_mul_f32_e32 v198, v55, v198
	v_mul_f32_e32 v199, v55, v199
	ds_write_b128 v210, v[196:199] offset:5120
	v_mul_f32_e32 v200, v56, v200
	v_mul_f32_e32 v201, v56, v201
	v_mul_f32_e32 v202, v56, v202
	v_mul_f32_e32 v203, v56, v203
	ds_write_b128 v210, v[200:203] offset:6144
	v_mul_f32_e32 v204, v57, v204
	v_mul_f32_e32 v205, v57, v205
	v_mul_f32_e32 v206, v57, v206
	v_mul_f32_e32 v207, v57, v207
	ds_write_b128 v210, v[204:207] offset:7168
	s_waitcnt lgkmcnt(0)
	s_barrier
; #define GAS __attribute__((address_space(1)))
; #define LAS __attribute__((address_space(3)))
; #define LDS_WAIT() asm volatile("s_waitcnt lgkmcnt(0)" ::: "memory")
; __device__ __forceinline__ int src_col_in(int c) {
;     if (c < 5120) { const int blk = c >> 7, p = c & 127; const bool rope = blk < 16 || ((((blk - 16) >> 2) & 1) == 0); const int d = rope ? (p >> 1) + 64 * (p & 1) : p; return blk * 128 + d; }
;     if (c < OFF_Z) return c + 2096;
;     if (c < OFF_G) return c - 4048;
;     if (c < OFF_DT) return 5120 + (c - OFF_G);
;     const int pr = item >> 1, kb = 2 * (pr / nblk) + (item & 1), nb = pr % nblk, k0 = 64 * kb, n0 = 32 * nb;
;     const int nr = n0 + (lane & 31); const int sc = MAP == 1 ? src_col_in(nr) : nr;
;     float v[32];
; #pragma unroll
;     for (int i = 0; i < 32; ++i) v[i] = sc >= 0 ? W[(size_t)(k0 + 2 * i + (lane >> 5)) * Nsrc + sc] : 0.f;
; #pragma unroll
;     for (int i = 0; i < 32; ++i) { const int k = k0 + 2 * i + (lane >> 5); float x = v[i] * wscale; if (KS) x *= (k < ksplit ? ksA[k] : ksB[k - ksplit]); scr[(2 * i + (lane >> 5)) * 33 + (lane & 31)] = x; }
;     LDS_WAIT(); asm volatile("" ::: "memory");
;     const int c = lane & 7;
; #pragma unroll
;     for (int j = 0; j < 4; ++j) { const int n = (lane >> 3) + 8 * j; const LAS float* s = scr + (8 * c) * 33 + n;
;         const unsigned long long o = (unsigned long long)pg8::pk4_fp8(s[0 * 33], s[1 * 33], s[2 * 33], s[3 * 33]) | ((unsigned long long)pg8::pk4_fp8(s[4 * 33], s[5 * 33], s[6 * 33], s[7 * 33]) << 32);
;         *(GAS unsigned long long*)(WT + (size_t)(n0 + n) * K + k0 + 8 * c) = o; }
;     LDS_WAIT(); asm volatile("" ::: "memory");
	s_add_i32 s24, s23, 16
	s_lshl_b32 s20, s24, 7
	s_cmp_lt_u32 s24, 40
	s_cselect_b32 s21, 0, 0x830
	s_cmp_lt_u32 s24, 72
	s_cselect_b32 s21, s21, 0xfffff030
	s_add_i32 s20, s20, s21
	s_lshl_b32 s20, s20, 2
	s_add_u32 s8, s50, s20
	s_addc_u32 s9, s51, 0
	global_load_dwordx4 v[176:179], v76, s[8:9]
	s_add_u32 s8, s8, 0x16280
	s_addc_u32 s9, s9, 0
	global_load_dwordx4 v[180:183], v76, s[8:9]
	s_add_u32 s8, s8, 0x16280
	s_addc_u32 s9, s9, 0
	global_load_dwordx4 v[184:187], v76, s[8:9]
	s_add_u32 s8, s8, 0x16280
	s_addc_u32 s9, s9, 0
	global_load_dwordx4 v[188:191], v76, s[8:9]
	s_add_u32 s8, s8, 0x16280
	s_addc_u32 s9, s9, 0
	global_load_dwordx4 v[192:195], v76, s[8:9]
	s_add_u32 s8, s8, 0x16280
	s_addc_u32 s9, s9, 0
	global_load_dwordx4 v[196:199], v76, s[8:9]
	s_add_u32 s8, s8, 0x16280
	s_addc_u32 s9, s9, 0
	global_load_dwordx4 v[200:203], v76, s[8:9]
	s_add_u32 s8, s8, 0x16280
	s_addc_u32 s9, s9, 0
	global_load_dwordx4 v[204:207], v76, s[8:9]
	s_add_i32 s24, s23, 0
	s_mul_i32 s20, s24, 0x80000
	s_add_u32 s6, s52, s20
	s_addc_u32 s7, s53, 0
	s_cmp_lt_u32 s24, 16
	s_cselect_b32 s20, 1, 0
	s_sub_i32 s21, s24, 16
	s_bitcmp0_b32 s21, 2
	s_cselect_b32 s21, 1, 0
	s_cmp_lt_u32 s24, 40
	s_cselect_b32 s21, s21, 0
	s_or_b32 s20, s20, s21
	s_cmp_lg_u32 s20, 0
	s_cselect_b64 s[20:21], -1, 0
	v_cndmask_b32_e64 v91, v77, v81, s[20:21]
	v_cndmask_b32_e64 v92, v78, v82, s[20:21]
	ds_read_b32 v226, v212
	ds_read_b32 v227, v212 offset:512
	ds_read_b32 v228, v212 offset:1024
	ds_read_b32 v229, v212 offset:1536
	ds_read_b32 v230, v212 offset:2048
	ds_read_b32 v231, v212 offset:2560
	ds_read_b32 v232, v212 offset:3072
	ds_read_b32 v233, v212 offset:3584
	ds_read_b32 v234, v212 offset:4096
	ds_read_b32 v235, v212 offset:4608
	ds_read_b32 v236, v212 offset:5120
	ds_read_b32 v237, v212 offset:5632
	ds_read_b32 v238, v212 offset:6144
	ds_read_b32 v239, v212 offset:6656
	ds_read_b32 v240, v212 offset:7168
	ds_read_b32 v241, v212 offset:7680
	s_waitcnt lgkmcnt(0)
	v_max_f32_e32 v226, v226, v226
	v_max_f32_e32 v227, v227, v227
	v_max_f32_e32 v228, v228, v228
	v_max_f32_e32 v229, v229, v229
	v_max_f32_e32 v230, v230, v230
	v_max_f32_e32 v231, v231, v231
	v_max_f32_e32 v232, v232, v232
	v_max_f32_e32 v233, v233, v233
	v_max_f32_e32 v234, v234, v234
	v_max_f32_e32 v235, v235, v235
	v_max_f32_e32 v236, v236, v236
	v_max_f32_e32 v237, v237, v237
	v_max_f32_e32 v238, v238, v238
	v_max_f32_e32 v239, v239, v239
	v_max_f32_e32 v240, v240, v240
	v_max_f32_e32 v241, v241, v241
	v_med3_f32 v226, v226, s62, v95
	v_med3_f32 v227, v227, s62, v95
	v_med3_f32 v228, v228, s62, v95
	v_med3_f32 v229, v229, s62, v95
	v_med3_f32 v230, v230, s62, v95
	v_med3_f32 v231, v231, s62, v95
	v_med3_f32 v232, v232, s62, v95
	v_med3_f32 v233, v233, s62, v95
	v_med3_f32 v234, v234, s62, v95
	v_med3_f32 v235, v235, s62, v95
	v_med3_f32 v236, v236, s62, v95
	v_med3_f32 v237, v237, s62, v95
	v_med3_f32 v238, v238, s62, v95
	v_med3_f32 v239, v239, s62, v95
	v_med3_f32 v240, v240, s62, v95
	v_med3_f32 v241, v241, s62, v95
	v_mov_b32_e32 v242, 0
	v_mov_b32_e32 v243, 0
	v_mov_b32_e32 v244, 0
	v_mov_b32_e32 v245, 0
	v_cvt_pk_fp8_f32 v242, v226, v227
	v_cvt_pk_fp8_f32 v243, v230, v231
	v_cvt_pk_fp8_f32 v244, v234, v235
	v_cvt_pk_fp8_f32 v245, v238, v239
	v_cvt_pk_fp8_f32 v242, v228, v229 op_sel:[0,0,1]
	v_cvt_pk_fp8_f32 v243, v232, v233 op_sel:[0,0,1]
	v_cvt_pk_fp8_f32 v244, v236, v237 op_sel:[0,0,1]
	v_cvt_pk_fp8_f32 v245, v240, v241 op_sel:[0,0,1]
	s_nop 0
	global_store_dwordx4 v91, v[242:245], s[6:7]
	ds_read_b32 v226, v214
	ds_read_b32 v227, v214 offset:512
	ds_read_b32 v228, v214 offset:1024
	ds_read_b32 v229, v214 offset:1536
	ds_read_b32 v230, v214 offset:2048
	ds_read_b32 v231, v214 offset:2560
	ds_read_b32 v232, v214 offset:3072
	ds_read_b32 v233, v214 offset:3584
	ds_read_b32 v234, v214 offset:4096
	ds_read_b32 v235, v214 offset:4608
	ds_read_b32 v236, v214 offset:5120
	ds_read_b32 v237, v214 offset:5632
	ds_read_b32 v238, v214 offset:6144
	ds_read_b32 v239, v214 offset:6656
	ds_read_b32 v240, v214 offset:7168
	ds_read_b32 v241, v214 offset:7680
	s_waitcnt lgkmcnt(0)
	v_max_f32_e32 v226, v226, v226
	v_max_f32_e32 v227, v227, v227
	v_max_f32_e32 v228, v228, v228
	v_max_f32_e32 v229, v229, v229
	v_max_f32_e32 v230, v230, v230
	v_max_f32_e32 v231, v231, v231
	v_max_f32_e32 v232, v232, v232
	v_max_f32_e32 v233, v233, v233
	v_max_f32_e32 v234, v234, v234
	v_max_f32_e32 v235, v235, v235
	v_max_f32_e32 v236, v236, v236
	v_max_f32_e32 v237, v237, v237
	v_max_f32_e32 v238, v238, v238
	v_max_f32_e32 v239, v239, v239
	v_max_f32_e32 v240, v240, v240
	v_max_f32_e32 v241, v241, v241
	v_med3_f32 v226, v226, s62, v95
	v_med3_f32 v227, v227, s62, v95
	v_med3_f32 v228, v228, s62, v95
	v_med3_f32 v229, v229, s62, v95
	v_med3_f32 v230, v230, s62, v95
	v_med3_f32 v231, v231, s62, v95
	v_med3_f32 v232, v232, s62, v95
	v_med3_f32 v233, v233, s62, v95
	v_med3_f32 v234, v234, s62, v95
	v_med3_f32 v235, v235, s62, v95
	v_med3_f32 v236, v236, s62, v95
	v_med3_f32 v237, v237, s62, v95
	v_med3_f32 v238, v238, s62, v95
	v_med3_f32 v239, v239, s62, v95
	v_med3_f32 v240, v240, s62, v95
	v_med3_f32 v241, v241, s62, v95
	v_mov_b32_e32 v242, 0
	v_mov_b32_e32 v243, 0
	v_mov_b32_e32 v244, 0
	v_mov_b32_e32 v245, 0
	v_cvt_pk_fp8_f32 v242, v226, v227
	v_cvt_pk_fp8_f32 v243, v230, v231
	v_cvt_pk_fp8_f32 v244, v234, v235
	v_cvt_pk_fp8_f32 v245, v238, v239
	v_cvt_pk_fp8_f32 v242, v228, v229 op_sel:[0,0,1]
	v_cvt_pk_fp8_f32 v243, v232, v233 op_sel:[0,0,1]
	v_cvt_pk_fp8_f32 v244, v236, v237 op_sel:[0,0,1]
	v_cvt_pk_fp8_f32 v245, v240, v241 op_sel:[0,0,1]
	s_nop 0
	global_store_dwordx4 v92, v[242:245], s[6:7]
	s_waitcnt vmcnt(14)
	v_mul_f32_e32 v144, v50, v144
	v_mul_f32_e32 v145, v50, v145
	v_mul_f32_e32 v146, v50, v146
	v_mul_f32_e32 v147, v50, v147
	ds_write_b128 v209, v[144:147]
	v_mul_f32_e32 v148, v51, v148
	v_mul_f32_e32 v149, v51, v149
	v_mul_f32_e32 v150, v51, v150
	v_mul_f32_e32 v151, v51, v151
	ds_write_b128 v209, v[148:151] offset:1024
	v_mul_f32_e32 v152, v52, v152
	v_mul_f32_e32 v153, v52, v153
	v_mul_f32_e32 v154, v52, v154
	v_mul_f32_e32 v155, v52, v155
	ds_write_b128 v209, v[152:155] offset:2048
	v_mul_f32_e32 v156, v53, v156
	v_mul_f32_e32 v157, v53, v157
	v_mul_f32_e32 v158, v53, v158
	v_mul_f32_e32 v159, v53, v159
	ds_write_b128 v209, v[156:159] offset:3072
	v_mul_f32_e32 v160, v54, v160
	v_mul_f32_e32 v161, v54, v161
	v_mul_f32_e32 v162, v54, v162
	v_mul_f32_e32 v163, v54, v163
	ds_write_b128 v209, v[160:163] offset:4096
	v_mul_f32_e32 v164, v55, v164
	v_mul_f32_e32 v165, v55, v165
	v_mul_f32_e32 v166, v55, v166
	v_mul_f32_e32 v167, v55, v167
	ds_write_b128 v209, v[164:167] offset:5120
	v_mul_f32_e32 v168, v56, v168
	v_mul_f32_e32 v169, v56, v169
	v_mul_f32_e32 v170, v56, v170
	v_mul_f32_e32 v171, v56, v171
	ds_write_b128 v209, v[168:171] offset:6144
	v_mul_f32_e32 v172, v57, v172
	v_mul_f32_e32 v173, v57, v173
	v_mul_f32_e32 v174, v57, v174
	v_mul_f32_e32 v175, v57, v175
	ds_write_b128 v209, v[172:175] offset:7168
	s_waitcnt lgkmcnt(0)
	s_barrier
; #define GAS __attribute__((address_space(1)))
; #define LAS __attribute__((address_space(3)))
; #define LDS_WAIT() asm volatile("s_waitcnt lgkmcnt(0)" ::: "memory")
; __device__ __forceinline__ int src_col_in(int c) {
;     if (c < 5120) { const int blk = c >> 7, p = c & 127; const bool rope = blk < 16 || ((((blk - 16) >> 2) & 1) == 0); const int d = rope ? (p >> 1) + 64 * (p & 1) : p; return blk * 128 + d; }
;     if (c < OFF_Z) return c + 2096;
;     if (c < OFF_G) return c - 4048;
;     if (c < OFF_DT) return 5120 + (c - OFF_G);
;     const int pr = item >> 1, kb = 2 * (pr / nblk) + (item & 1), nb = pr % nblk, k0 = 64 * kb, n0 = 32 * nb;
;     const int nr = n0 + (lane & 31); const int sc = MAP == 1 ? src_col_in(nr) : nr;
;     float v[32];
; #pragma unroll
;     for (int i = 0; i < 32; ++i) v[i] = sc >= 0 ? W[(size_t)(k0 + 2 * i + (lane >> 5)) * Nsrc + sc] : 0.f;
; #pragma unroll
;     for (int i = 0; i < 32; ++i) { const int k = k0 + 2 * i + (lane >> 5); float x = v[i] * wscale; if (KS) x *= (k < ksplit ? ksA[k] : ksB[k - ksplit]); scr[(2 * i + (lane >> 5)) * 33 + (lane & 31)] = x; }
;     LDS_WAIT(); asm volatile("" ::: "memory");
;     const int c = lane & 7;
; #pragma unroll
;     for (int j = 0; j < 4; ++j) { const int n = (lane >> 3) + 8 * j; const LAS float* s = scr + (8 * c) * 33 + n;
;         const unsigned long long o = (unsigned long long)pg8::pk4_fp8(s[0 * 33], s[1 * 33], s[2 * 33], s[3 * 33]) | ((unsigned long long)pg8::pk4_fp8(s[4 * 33], s[5 * 33], s[6 * 33], s[7 * 33]) << 32);
;         *(GAS unsigned long long*)(WT + (size_t)(n0 + n) * K + k0 + 8 * c) = o; }
;     LDS_WAIT(); asm volatile("" ::: "memory");
	s_add_i32 s24, s23, 24
	s_lshl_b32 s20, s24, 7
	s_cmp_lt_u32 s24, 40
	s_cselect_b32 s21, 0, 0x830
	s_cmp_lt_u32 s24, 72
	s_cselect_b32 s21, s21, 0xfffff030
	s_add_i32 s20, s20, s21
	s_lshl_b32 s20, s20, 2
	s_add_u32 s8, s50, s20
	s_addc_u32 s9, s51, 0
	global_load_dwordx4 v[144:147], v76, s[8:9]
	s_add_u32 s8, s8, 0x16280
	s_addc_u32 s9, s9, 0
	global_load_dwordx4 v[148:151], v76, s[8:9]
	s_add_u32 s8, s8, 0x16280
	s_addc_u32 s9, s9, 0
	global_load_dwordx4 v[152:155], v76, s[8:9]
	s_add_u32 s8, s8, 0x16280
	s_addc_u32 s9, s9, 0
	global_load_dwordx4 v[156:159], v76, s[8:9]
	s_add_u32 s8, s8, 0x16280
	s_addc_u32 s9, s9, 0
	global_load_dwordx4 v[160:163], v76, s[8:9]
	s_add_u32 s8, s8, 0x16280
	s_addc_u32 s9, s9, 0
	global_load_dwordx4 v[164:167], v76, s[8:9]
	s_add_u32 s8, s8, 0x16280
	s_addc_u32 s9, s9, 0
	global_load_dwordx4 v[168:171], v76, s[8:9]
	s_add_u32 s8, s8, 0x16280
	s_addc_u32 s9, s9, 0
	global_load_dwordx4 v[172:175], v76, s[8:9]
	s_add_i32 s24, s23, 8
	s_mul_i32 s20, s24, 0x80000
	s_add_u32 s6, s52, s20
	s_addc_u32 s7, s53, 0
	s_cmp_lt_u32 s24, 16
	s_cselect_b32 s20, 1, 0
	s_sub_i32 s21, s24, 16
	s_bitcmp0_b32 s21, 2
	s_cselect_b32 s21, 1, 0
	s_cmp_lt_u32 s24, 40
	s_cselect_b32 s21, s21, 0
	s_or_b32 s20, s20, s21
	s_cmp_lg_u32 s20, 0
	s_cselect_b64 s[20:21], -1, 0
	v_cndmask_b32_e64 v91, v77, v81, s[20:21]
	v_cndmask_b32_e64 v92, v78, v82, s[20:21]
	ds_read_b32 v226, v211
	ds_read_b32 v227, v211 offset:512
	ds_read_b32 v228, v211 offset:1024
	ds_read_b32 v229, v211 offset:1536
	ds_read_b32 v230, v211 offset:2048
	ds_read_b32 v231, v211 offset:2560
	ds_read_b32 v232, v211 offset:3072
	ds_read_b32 v233, v211 offset:3584
	ds_read_b32 v234, v211 offset:4096
	ds_read_b32 v235, v211 offset:4608
	ds_read_b32 v236, v211 offset:5120
	ds_read_b32 v237, v211 offset:5632
	ds_read_b32 v238, v211 offset:6144
	ds_read_b32 v239, v211 offset:6656
	ds_read_b32 v240, v211 offset:7168
	ds_read_b32 v241, v211 offset:7680
	s_waitcnt lgkmcnt(0)
	v_max_f32_e32 v226, v226, v226
	v_max_f32_e32 v227, v227, v227
	v_max_f32_e32 v228, v228, v228
	v_max_f32_e32 v229, v229, v229
	v_max_f32_e32 v230, v230, v230
	v_max_f32_e32 v231, v231, v231
	v_max_f32_e32 v232, v232, v232
	v_max_f32_e32 v233, v233, v233
	v_max_f32_e32 v234, v234, v234
	v_max_f32_e32 v235, v235, v235
	v_max_f32_e32 v236, v236, v236
	v_max_f32_e32 v237, v237, v237
	v_max_f32_e32 v238, v238, v238
	v_max_f32_e32 v239, v239, v239
	v_max_f32_e32 v240, v240, v240
	v_max_f32_e32 v241, v241, v241
	v_med3_f32 v226, v226, s62, v95
	v_med3_f32 v227, v227, s62, v95
	v_med3_f32 v228, v228, s62, v95
	v_med3_f32 v229, v229, s62, v95
	v_med3_f32 v230, v230, s62, v95
	v_med3_f32 v231, v231, s62, v95
	v_med3_f32 v232, v232, s62, v95
	v_med3_f32 v233, v233, s62, v95
	v_med3_f32 v234, v234, s62, v95
	v_med3_f32 v235, v235, s62, v95
	v_med3_f32 v236, v236, s62, v95
	v_med3_f32 v237, v237, s62, v95
	v_med3_f32 v238, v238, s62, v95
	v_med3_f32 v239, v239, s62, v95
	v_med3_f32 v240, v240, s62, v95
	v_med3_f32 v241, v241, s62, v95
	v_mov_b32_e32 v242, 0
	v_mov_b32_e32 v243, 0
	v_mov_b32_e32 v244, 0
	v_mov_b32_e32 v245, 0
	v_cvt_pk_fp8_f32 v242, v226, v227
	v_cvt_pk_fp8_f32 v243, v230, v231
	v_cvt_pk_fp8_f32 v244, v234, v235
	v_cvt_pk_fp8_f32 v245, v238, v239
	v_cvt_pk_fp8_f32 v242, v228, v229 op_sel:[0,0,1]
	v_cvt_pk_fp8_f32 v243, v232, v233 op_sel:[0,0,1]
	v_cvt_pk_fp8_f32 v244, v236, v237 op_sel:[0,0,1]
	v_cvt_pk_fp8_f32 v245, v240, v241 op_sel:[0,0,1]
	s_nop 0
	global_store_dwordx4 v91, v[242:245], s[6:7]
	ds_read_b32 v226, v213
	ds_read_b32 v227, v213 offset:512
	ds_read_b32 v228, v213 offset:1024
	ds_read_b32 v229, v213 offset:1536
	ds_read_b32 v230, v213 offset:2048
	ds_read_b32 v231, v213 offset:2560
	ds_read_b32 v232, v213 offset:3072
	ds_read_b32 v233, v213 offset:3584
	ds_read_b32 v234, v213 offset:4096
	ds_read_b32 v235, v213 offset:4608
	ds_read_b32 v236, v213 offset:5120
	ds_read_b32 v237, v213 offset:5632
	ds_read_b32 v238, v213 offset:6144
	ds_read_b32 v239, v213 offset:6656
	ds_read_b32 v240, v213 offset:7168
	ds_read_b32 v241, v213 offset:7680
	s_waitcnt lgkmcnt(0)
	v_max_f32_e32 v226, v226, v226
	v_max_f32_e32 v227, v227, v227
	v_max_f32_e32 v228, v228, v228
	v_max_f32_e32 v229, v229, v229
	v_max_f32_e32 v230, v230, v230
	v_max_f32_e32 v231, v231, v231
	v_max_f32_e32 v232, v232, v232
	v_max_f32_e32 v233, v233, v233
	v_max_f32_e32 v234, v234, v234
	v_max_f32_e32 v235, v235, v235
	v_max_f32_e32 v236, v236, v236
	v_max_f32_e32 v237, v237, v237
	v_max_f32_e32 v238, v238, v238
	v_max_f32_e32 v239, v239, v239
	v_max_f32_e32 v240, v240, v240
	v_max_f32_e32 v241, v241, v241
	v_med3_f32 v226, v226, s62, v95
	v_med3_f32 v227, v227, s62, v95
	v_med3_f32 v228, v228, s62, v95
	v_med3_f32 v229, v229, s62, v95
	v_med3_f32 v230, v230, s62, v95
	v_med3_f32 v231, v231, s62, v95
	v_med3_f32 v232, v232, s62, v95
	v_med3_f32 v233, v233, s62, v95
	v_med3_f32 v234, v234, s62, v95
	v_med3_f32 v235, v235, s62, v95
	v_med3_f32 v236, v236, s62, v95
	v_med3_f32 v237, v237, s62, v95
	v_med3_f32 v238, v238, s62, v95
	v_med3_f32 v239, v239, s62, v95
	v_med3_f32 v240, v240, s62, v95
	v_med3_f32 v241, v241, s62, v95
	v_mov_b32_e32 v242, 0
	v_mov_b32_e32 v243, 0
	v_mov_b32_e32 v244, 0
	v_mov_b32_e32 v245, 0
	v_cvt_pk_fp8_f32 v242, v226, v227
	v_cvt_pk_fp8_f32 v243, v230, v231
	v_cvt_pk_fp8_f32 v244, v234, v235
	v_cvt_pk_fp8_f32 v245, v238, v239
	v_cvt_pk_fp8_f32 v242, v228, v229 op_sel:[0,0,1]
	v_cvt_pk_fp8_f32 v243, v232, v233 op_sel:[0,0,1]
	v_cvt_pk_fp8_f32 v244, v236, v237 op_sel:[0,0,1]
	v_cvt_pk_fp8_f32 v245, v240, v241 op_sel:[0,0,1]
	s_nop 0
	global_store_dwordx4 v92, v[242:245], s[6:7]
	s_waitcnt vmcnt(12)
	v_mul_f32_e32 v176, v50, v176
	v_mul_f32_e32 v177, v50, v177
	v_mul_f32_e32 v178, v50, v178
	v_mul_f32_e32 v179, v50, v179
	ds_write_b128 v210, v[176:179]
	v_mul_f32_e32 v180, v51, v180
	v_mul_f32_e32 v181, v51, v181
	v_mul_f32_e32 v182, v51, v182
	v_mul_f32_e32 v183, v51, v183
	ds_write_b128 v210, v[180:183] offset:1024
	v_mul_f32_e32 v184, v52, v184
	v_mul_f32_e32 v185, v52, v185
	v_mul_f32_e32 v186, v52, v186
	v_mul_f32_e32 v187, v52, v187
	ds_write_b128 v210, v[184:187] offset:2048
	v_mul_f32_e32 v188, v53, v188
	v_mul_f32_e32 v189, v53, v189
	v_mul_f32_e32 v190, v53, v190
	v_mul_f32_e32 v191, v53, v191
	ds_write_b128 v210, v[188:191] offset:3072
	v_mul_f32_e32 v192, v54, v192
	v_mul_f32_e32 v193, v54, v193
	v_mul_f32_e32 v194, v54, v194
	v_mul_f32_e32 v195, v54, v195
	ds_write_b128 v210, v[192:195] offset:4096
	v_mul_f32_e32 v196, v55, v196
	v_mul_f32_e32 v197, v55, v197
	v_mul_f32_e32 v198, v55, v198
	v_mul_f32_e32 v199, v55, v199
	ds_write_b128 v210, v[196:199] offset:5120
	v_mul_f32_e32 v200, v56, v200
	v_mul_f32_e32 v201, v56, v201
	v_mul_f32_e32 v202, v56, v202
	v_mul_f32_e32 v203, v56, v203
	ds_write_b128 v210, v[200:203] offset:6144
	v_mul_f32_e32 v204, v57, v204
	v_mul_f32_e32 v205, v57, v205
	v_mul_f32_e32 v206, v57, v206
	v_mul_f32_e32 v207, v57, v207
	ds_write_b128 v210, v[204:207] offset:7168
	s_waitcnt lgkmcnt(0)
	s_barrier
; #define GAS __attribute__((address_space(1)))
; #define LAS __attribute__((address_space(3)))
; #define LDS_WAIT() asm volatile("s_waitcnt lgkmcnt(0)" ::: "memory")
; __device__ __forceinline__ int src_col_in(int c) {
;     if (c < 5120) { const int blk = c >> 7, p = c & 127; const bool rope = blk < 16 || ((((blk - 16) >> 2) & 1) == 0); const int d = rope ? (p >> 1) + 64 * (p & 1) : p; return blk * 128 + d; }
;     if (c < OFF_Z) return c + 2096;
;     if (c < OFF_G) return c - 4048;
;     if (c < OFF_DT) return 5120 + (c - OFF_G);
;     const int pr = item >> 1, kb = 2 * (pr / nblk) + (item & 1), nb = pr % nblk, k0 = 64 * kb, n0 = 32 * nb;
;     const int nr = n0 + (lane & 31); const int sc = MAP == 1 ? src_col_in(nr) : nr;
;     float v[32];
; #pragma unroll
;     for (int i = 0; i < 32; ++i) v[i] = sc >= 0 ? W[(size_t)(k0 + 2 * i + (lane >> 5)) * Nsrc + sc] : 0.f;
; #pragma unroll
;     for (int i = 0; i < 32; ++i) { const int k = k0 + 2 * i + (lane >> 5); float x = v[i] * wscale; if (KS) x *= (k < ksplit ? ksA[k] : ksB[k - ksplit]); scr[(2 * i + (lane >> 5)) * 33 + (lane & 31)] = x; }
;     LDS_WAIT(); asm volatile("" ::: "memory");
;     const int c = lane & 7;
; #pragma unroll
;     for (int j = 0; j < 4; ++j) { const int n = (lane >> 3) + 8 * j; const LAS float* s = scr + (8 * c) * 33 + n;
;         const unsigned long long o = (unsigned long long)pg8::pk4_fp8(s[0 * 33], s[1 * 33], s[2 * 33], s[3 * 33]) | ((unsigned long long)pg8::pk4_fp8(s[4 * 33], s[5 * 33], s[6 * 33], s[7 * 33]) << 32);
;         *(GAS unsigned long long*)(WT + (size_t)(n0 + n) * K + k0 + 8 * c) = o; }
;     LDS_WAIT(); asm volatile("" ::: "memory");
	s_add_i32 s24, s23, 32
	s_lshl_b32 s20, s24, 7
	s_cmp_lt_u32 s24, 40
	s_cselect_b32 s21, 0, 0x830
	s_cmp_lt_u32 s24, 72
	s_cselect_b32 s21, s21, 0xfffff030
	s_add_i32 s20, s20, s21
	s_lshl_b32 s20, s20, 2
	s_add_u32 s8, s50, s20
	s_addc_u32 s9, s51, 0
	global_load_dwordx4 v[176:179], v76, s[8:9]
	s_add_u32 s8, s8, 0x16280
	s_addc_u32 s9, s9, 0
	global_load_dwordx4 v[180:183], v76, s[8:9]
	s_add_u32 s8, s8, 0x16280
	s_addc_u32 s9, s9, 0
	global_load_dwordx4 v[184:187], v76, s[8:9]
	s_add_u32 s8, s8, 0x16280
	s_addc_u32 s9, s9, 0
	global_load_dwordx4 v[188:191], v76, s[8:9]
	s_add_u32 s8, s8, 0x16280
	s_addc_u32 s9, s9, 0
	global_load_dwordx4 v[192:195], v76, s[8:9]
	s_add_u32 s8, s8, 0x16280
	s_addc_u32 s9, s9, 0
	global_load_dwordx4 v[196:199], v76, s[8:9]
	s_add_u32 s8, s8, 0x16280
	s_addc_u32 s9, s9, 0
	global_load_dwordx4 v[200:203], v76, s[8:9]
	s_add_u32 s8, s8, 0x16280
	s_addc_u32 s9, s9, 0
	global_load_dwordx4 v[204:207], v76, s[8:9]
	s_add_i32 s24, s23, 16
	s_mul_i32 s20, s24, 0x80000
	s_add_u32 s6, s52, s20
	s_addc_u32 s7, s53, 0
	s_cmp_lt_u32 s24, 16
	s_cselect_b32 s20, 1, 0
	s_sub_i32 s21, s24, 16
	s_bitcmp0_b32 s21, 2
	s_cselect_b32 s21, 1, 0
	s_cmp_lt_u32 s24, 40
	s_cselect_b32 s21, s21, 0
	s_or_b32 s20, s20, s21
	s_cmp_lg_u32 s20, 0
	s_cselect_b64 s[20:21], -1, 0
	v_cndmask_b32_e64 v91, v77, v81, s[20:21]
	v_cndmask_b32_e64 v92, v78, v82, s[20:21]
	ds_read_b32 v226, v212
	ds_read_b32 v227, v212 offset:512
	ds_read_b32 v228, v212 offset:1024
	ds_read_b32 v229, v212 offset:1536
	ds_read_b32 v230, v212 offset:2048
	ds_read_b32 v231, v212 offset:2560
	ds_read_b32 v232, v212 offset:3072
	ds_read_b32 v233, v212 offset:3584
	ds_read_b32 v234, v212 offset:4096
	ds_read_b32 v235, v212 offset:4608
	ds_read_b32 v236, v212 offset:5120
	ds_read_b32 v237, v212 offset:5632
	ds_read_b32 v238, v212 offset:6144
	ds_read_b32 v239, v212 offset:6656
	ds_read_b32 v240, v212 offset:7168
	ds_read_b32 v241, v212 offset:7680
	s_waitcnt lgkmcnt(0)
	v_max_f32_e32 v226, v226, v226
	v_max_f32_e32 v227, v227, v227
	v_max_f32_e32 v228, v228, v228
	v_max_f32_e32 v229, v229, v229
	v_max_f32_e32 v230, v230, v230
	v_max_f32_e32 v231, v231, v231
	v_max_f32_e32 v232, v232, v232
	v_max_f32_e32 v233, v233, v233
	v_max_f32_e32 v234, v234, v234
	v_max_f32_e32 v235, v235, v235
	v_max_f32_e32 v236, v236, v236
	v_max_f32_e32 v237, v237, v237
	v_max_f32_e32 v238, v238, v238
	v_max_f32_e32 v239, v239, v239
	v_max_f32_e32 v240, v240, v240
	v_max_f32_e32 v241, v241, v241
	v_med3_f32 v226, v226, s62, v95
	v_med3_f32 v227, v227, s62, v95
	v_med3_f32 v228, v228, s62, v95
	v_med3_f32 v229, v229, s62, v95
	v_med3_f32 v230, v230, s62, v95
	v_med3_f32 v231, v231, s62, v95
	v_med3_f32 v232, v232, s62, v95
	v_med3_f32 v233, v233, s62, v95
	v_med3_f32 v234, v234, s62, v95
	v_med3_f32 v235, v235, s62, v95
	v_med3_f32 v236, v236, s62, v95
	v_med3_f32 v237, v237, s62, v95
	v_med3_f32 v238, v238, s62, v95
	v_med3_f32 v239, v239, s62, v95
	v_med3_f32 v240, v240, s62, v95
	v_med3_f32 v241, v241, s62, v95
	v_mov_b32_e32 v242, 0
	v_mov_b32_e32 v243, 0
	v_mov_b32_e32 v244, 0
	v_mov_b32_e32 v245, 0
	v_cvt_pk_fp8_f32 v242, v226, v227
	v_cvt_pk_fp8_f32 v243, v230, v231
	v_cvt_pk_fp8_f32 v244, v234, v235
	v_cvt_pk_fp8_f32 v245, v238, v239
	v_cvt_pk_fp8_f32 v242, v228, v229 op_sel:[0,0,1]
	v_cvt_pk_fp8_f32 v243, v232, v233 op_sel:[0,0,1]
	v_cvt_pk_fp8_f32 v244, v236, v237 op_sel:[0,0,1]
	v_cvt_pk_fp8_f32 v245, v240, v241 op_sel:[0,0,1]
	s_nop 0
	global_store_dwordx4 v91, v[242:245], s[6:7]
	ds_read_b32 v226, v214
	ds_read_b32 v227, v214 offset:512
	ds_read_b32 v228, v214 offset:1024
	ds_read_b32 v229, v214 offset:1536
	ds_read_b32 v230, v214 offset:2048
	ds_read_b32 v231, v214 offset:2560
	ds_read_b32 v232, v214 offset:3072
	ds_read_b32 v233, v214 offset:3584
	ds_read_b32 v234, v214 offset:4096
	ds_read_b32 v235, v214 offset:4608
	ds_read_b32 v236, v214 offset:5120
	ds_read_b32 v237, v214 offset:5632
	ds_read_b32 v238, v214 offset:6144
	ds_read_b32 v239, v214 offset:6656
	ds_read_b32 v240, v214 offset:7168
	ds_read_b32 v241, v214 offset:7680
	s_waitcnt lgkmcnt(0)
	v_max_f32_e32 v226, v226, v226
	v_max_f32_e32 v227, v227, v227
	v_max_f32_e32 v228, v228, v228
	v_max_f32_e32 v229, v229, v229
	v_max_f32_e32 v230, v230, v230
	v_max_f32_e32 v231, v231, v231
	v_max_f32_e32 v232, v232, v232
	v_max_f32_e32 v233, v233, v233
	v_max_f32_e32 v234, v234, v234
	v_max_f32_e32 v235, v235, v235
	v_max_f32_e32 v236, v236, v236
	v_max_f32_e32 v237, v237, v237
	v_max_f32_e32 v238, v238, v238
	v_max_f32_e32 v239, v239, v239
	v_max_f32_e32 v240, v240, v240
	v_max_f32_e32 v241, v241, v241
	v_med3_f32 v226, v226, s62, v95
	v_med3_f32 v227, v227, s62, v95
	v_med3_f32 v228, v228, s62, v95
	v_med3_f32 v229, v229, s62, v95
	v_med3_f32 v230, v230, s62, v95
	v_med3_f32 v231, v231, s62, v95
	v_med3_f32 v232, v232, s62, v95
	v_med3_f32 v233, v233, s62, v95
	v_med3_f32 v234, v234, s62, v95
	v_med3_f32 v235, v235, s62, v95
	v_med3_f32 v236, v236, s62, v95
	v_med3_f32 v237, v237, s62, v95
	v_med3_f32 v238, v238, s62, v95
	v_med3_f32 v239, v239, s62, v95
	v_med3_f32 v240, v240, s62, v95
	v_med3_f32 v241, v241, s62, v95
	v_mov_b32_e32 v242, 0
	v_mov_b32_e32 v243, 0
	v_mov_b32_e32 v244, 0
	v_mov_b32_e32 v245, 0
	v_cvt_pk_fp8_f32 v242, v226, v227
	v_cvt_pk_fp8_f32 v243, v230, v231
	v_cvt_pk_fp8_f32 v244, v234, v235
	v_cvt_pk_fp8_f32 v245, v238, v239
	v_cvt_pk_fp8_f32 v242, v228, v229 op_sel:[0,0,1]
	v_cvt_pk_fp8_f32 v243, v232, v233 op_sel:[0,0,1]
	v_cvt_pk_fp8_f32 v244, v236, v237 op_sel:[0,0,1]
	v_cvt_pk_fp8_f32 v245, v240, v241 op_sel:[0,0,1]
	s_nop 0
	global_store_dwordx4 v92, v[242:245], s[6:7]
	s_waitcnt vmcnt(12)
	v_mul_f32_e32 v144, v50, v144
	v_mul_f32_e32 v145, v50, v145
	v_mul_f32_e32 v146, v50, v146
	v_mul_f32_e32 v147, v50, v147
	ds_write_b128 v209, v[144:147]
	v_mul_f32_e32 v148, v51, v148
	v_mul_f32_e32 v149, v51, v149
	v_mul_f32_e32 v150, v51, v150
	v_mul_f32_e32 v151, v51, v151
	ds_write_b128 v209, v[148:151] offset:1024
	v_mul_f32_e32 v152, v52, v152
	v_mul_f32_e32 v153, v52, v153
	v_mul_f32_e32 v154, v52, v154
	v_mul_f32_e32 v155, v52, v155
	ds_write_b128 v209, v[152:155] offset:2048
	v_mul_f32_e32 v156, v53, v156
	v_mul_f32_e32 v157, v53, v157
	v_mul_f32_e32 v158, v53, v158
	v_mul_f32_e32 v159, v53, v159
	ds_write_b128 v209, v[156:159] offset:3072
	v_mul_f32_e32 v160, v54, v160
	v_mul_f32_e32 v161, v54, v161
	v_mul_f32_e32 v162, v54, v162
	v_mul_f32_e32 v163, v54, v163
	ds_write_b128 v209, v[160:163] offset:4096
	v_mul_f32_e32 v164, v55, v164
	v_mul_f32_e32 v165, v55, v165
	v_mul_f32_e32 v166, v55, v166
	v_mul_f32_e32 v167, v55, v167
	ds_write_b128 v209, v[164:167] offset:5120
	v_mul_f32_e32 v168, v56, v168
	v_mul_f32_e32 v169, v56, v169
	v_mul_f32_e32 v170, v56, v170
	v_mul_f32_e32 v171, v56, v171
	ds_write_b128 v209, v[168:171] offset:6144
	v_mul_f32_e32 v172, v57, v172
	v_mul_f32_e32 v173, v57, v173
	v_mul_f32_e32 v174, v57, v174
	v_mul_f32_e32 v175, v57, v175
	ds_write_b128 v209, v[172:175] offset:7168
	s_waitcnt lgkmcnt(0)
	s_barrier
; #define GAS __attribute__((address_space(1)))
; #define LAS __attribute__((address_space(3)))
; #define LDS_WAIT() asm volatile("s_waitcnt lgkmcnt(0)" ::: "memory")
; __device__ __forceinline__ int src_col_in(int c) {
;     if (c < 5120) { const int blk = c >> 7, p = c & 127; const bool rope = blk < 16 || ((((blk - 16) >> 2) & 1) == 0); const int d = rope ? (p >> 1) + 64 * (p & 1) : p; return blk * 128 + d; }
;     if (c < OFF_Z) return c + 2096;
;     if (c < OFF_G) return c - 4048;
;     if (c < OFF_DT) return 5120 + (c - OFF_G);
;     const int pr = item >> 1, kb = 2 * (pr / nblk) + (item & 1), nb = pr % nblk, k0 = 64 * kb, n0 = 32 * nb;
;     const int nr = n0 + (lane & 31); const int sc = MAP == 1 ? src_col_in(nr) : nr;
;     float v[32];
; #pragma unroll
;     for (int i = 0; i < 32; ++i) v[i] = sc >= 0 ? W[(size_t)(k0 + 2 * i + (lane >> 5)) * Nsrc + sc] : 0.f;
; #pragma unroll
;     for (int i = 0; i < 32; ++i) { const int k = k0 + 2 * i + (lane >> 5); float x = v[i] * wscale; if (KS) x *= (k < ksplit ? ksA[k] : ksB[k - ksplit]); scr[(2 * i + (lane >> 5)) * 33 + (lane & 31)] = x; }
;     LDS_WAIT(); asm volatile("" ::: "memory");
;     const int c = lane & 7;
; #pragma unroll
;     for (int j = 0; j < 4; ++j) { const int n = (lane >> 3) + 8 * j; const LAS float* s = scr + (8 * c) * 33 + n;
;         const unsigned long long o = (unsigned long long)pg8::pk4_fp8(s[0 * 33], s[1 * 33], s[2 * 33], s[3 * 33]) | ((unsigned long long)pg8::pk4_fp8(s[4 * 33], s[5 * 33], s[6 * 33], s[7 * 33]) << 32);
;         *(GAS unsigned long long*)(WT + (size_t)(n0 + n) * K + k0 + 8 * c) = o; }
;     LDS_WAIT(); asm volatile("" ::: "memory");
	s_add_i32 s24, s23, 40
	s_lshl_b32 s20, s24, 7
	s_cmp_lt_u32 s24, 40
	s_cselect_b32 s21, 0, 0x830
	s_cmp_lt_u32 s24, 72
	s_cselect_b32 s21, s21, 0xfffff030
	s_add_i32 s20, s20, s21
	s_lshl_b32 s20, s20, 2
	s_add_u32 s8, s50, s20
	s_addc_u32 s9, s51, 0
	global_load_dwordx4 v[144:147], v76, s[8:9]
	s_add_u32 s8, s8, 0x16280
	s_addc_u32 s9, s9, 0
	global_load_dwordx4 v[148:151], v76, s[8:9]
	s_add_u32 s8, s8, 0x16280
	s_addc_u32 s9, s9, 0
	global_load_dwordx4 v[152:155], v76, s[8:9]
	s_add_u32 s8, s8, 0x16280
	s_addc_u32 s9, s9, 0
	global_load_dwordx4 v[156:159], v76, s[8:9]
	s_add_u32 s8, s8, 0x16280
	s_addc_u32 s9, s9, 0
	global_load_dwordx4 v[160:163], v76, s[8:9]
	s_add_u32 s8, s8, 0x16280
	s_addc_u32 s9, s9, 0
	global_load_dwordx4 v[164:167], v76, s[8:9]
	s_add_u32 s8, s8, 0x16280
	s_addc_u32 s9, s9, 0
	global_load_dwordx4 v[168:171], v76, s[8:9]
	s_add_u32 s8, s8, 0x16280
	s_addc_u32 s9, s9, 0
	global_load_dwordx4 v[172:175], v76, s[8:9]
	s_add_i32 s24, s23, 24
	s_mul_i32 s20, s24, 0x80000
	s_add_u32 s6, s52, s20
	s_addc_u32 s7, s53, 0
	s_cmp_lt_u32 s24, 16
	s_cselect_b32 s20, 1, 0
	s_sub_i32 s21, s24, 16
	s_bitcmp0_b32 s21, 2
	s_cselect_b32 s21, 1, 0
	s_cmp_lt_u32 s24, 40
	s_cselect_b32 s21, s21, 0
	s_or_b32 s20, s20, s21
	s_cmp_lg_u32 s20, 0
	s_cselect_b64 s[20:21], -1, 0
	v_cndmask_b32_e64 v91, v77, v81, s[20:21]
	v_cndmask_b32_e64 v92, v78, v82, s[20:21]
	ds_read_b32 v226, v211
	ds_read_b32 v227, v211 offset:512
	ds_read_b32 v228, v211 offset:1024
	ds_read_b32 v229, v211 offset:1536
	ds_read_b32 v230, v211 offset:2048
	ds_read_b32 v231, v211 offset:2560
	ds_read_b32 v232, v211 offset:3072
	ds_read_b32 v233, v211 offset:3584
	ds_read_b32 v234, v211 offset:4096
	ds_read_b32 v235, v211 offset:4608
	ds_read_b32 v236, v211 offset:5120
	ds_read_b32 v237, v211 offset:5632
	ds_read_b32 v238, v211 offset:6144
	ds_read_b32 v239, v211 offset:6656
	ds_read_b32 v240, v211 offset:7168
	ds_read_b32 v241, v211 offset:7680
	s_waitcnt lgkmcnt(0)
	v_max_f32_e32 v226, v226, v226
	v_max_f32_e32 v227, v227, v227
	v_max_f32_e32 v228, v228, v228
	v_max_f32_e32 v229, v229, v229
	v_max_f32_e32 v230, v230, v230
	v_max_f32_e32 v231, v231, v231
	v_max_f32_e32 v232, v232, v232
	v_max_f32_e32 v233, v233, v233
	v_max_f32_e32 v234, v234, v234
	v_max_f32_e32 v235, v235, v235
	v_max_f32_e32 v236, v236, v236
	v_max_f32_e32 v237, v237, v237
	v_max_f32_e32 v238, v238, v238
	v_max_f32_e32 v239, v239, v239
	v_max_f32_e32 v240, v240, v240
	v_max_f32_e32 v241, v241, v241
	v_med3_f32 v226, v226, s62, v95
	v_med3_f32 v227, v227, s62, v95
	v_med3_f32 v228, v228, s62, v95
	v_med3_f32 v229, v229, s62, v95
	v_med3_f32 v230, v230, s62, v95
	v_med3_f32 v231, v231, s62, v95
	v_med3_f32 v232, v232, s62, v95
	v_med3_f32 v233, v233, s62, v95
	v_med3_f32 v234, v234, s62, v95
	v_med3_f32 v235, v235, s62, v95
	v_med3_f32 v236, v236, s62, v95
	v_med3_f32 v237, v237, s62, v95
	v_med3_f32 v238, v238, s62, v95
	v_med3_f32 v239, v239, s62, v95
	v_med3_f32 v240, v240, s62, v95
	v_med3_f32 v241, v241, s62, v95
	v_mov_b32_e32 v242, 0
	v_mov_b32_e32 v243, 0
	v_mov_b32_e32 v244, 0
	v_mov_b32_e32 v245, 0
	v_cvt_pk_fp8_f32 v242, v226, v227
	v_cvt_pk_fp8_f32 v243, v230, v231
	v_cvt_pk_fp8_f32 v244, v234, v235
	v_cvt_pk_fp8_f32 v245, v238, v239
	v_cvt_pk_fp8_f32 v242, v228, v229 op_sel:[0,0,1]
	v_cvt_pk_fp8_f32 v243, v232, v233 op_sel:[0,0,1]
	v_cvt_pk_fp8_f32 v244, v236, v237 op_sel:[0,0,1]
	v_cvt_pk_fp8_f32 v245, v240, v241 op_sel:[0,0,1]
	s_nop 0
	global_store_dwordx4 v91, v[242:245], s[6:7]
	ds_read_b32 v226, v213
	ds_read_b32 v227, v213 offset:512
	ds_read_b32 v228, v213 offset:1024
	ds_read_b32 v229, v213 offset:1536
	ds_read_b32 v230, v213 offset:2048
	ds_read_b32 v231, v213 offset:2560
	ds_read_b32 v232, v213 offset:3072
	ds_read_b32 v233, v213 offset:3584
	ds_read_b32 v234, v213 offset:4096
	ds_read_b32 v235, v213 offset:4608
	ds_read_b32 v236, v213 offset:5120
	ds_read_b32 v237, v213 offset:5632
	ds_read_b32 v238, v213 offset:6144
	ds_read_b32 v239, v213 offset:6656
	ds_read_b32 v240, v213 offset:7168
	ds_read_b32 v241, v213 offset:7680
	s_waitcnt lgkmcnt(0)
	v_max_f32_e32 v226, v226, v226
	v_max_f32_e32 v227, v227, v227
	v_max_f32_e32 v228, v228, v228
	v_max_f32_e32 v229, v229, v229
	v_max_f32_e32 v230, v230, v230
	v_max_f32_e32 v231, v231, v231
	v_max_f32_e32 v232, v232, v232
	v_max_f32_e32 v233, v233, v233
	v_max_f32_e32 v234, v234, v234
	v_max_f32_e32 v235, v235, v235
	v_max_f32_e32 v236, v236, v236
	v_max_f32_e32 v237, v237, v237
	v_max_f32_e32 v238, v238, v238
	v_max_f32_e32 v239, v239, v239
	v_max_f32_e32 v240, v240, v240
	v_max_f32_e32 v241, v241, v241
	v_med3_f32 v226, v226, s62, v95
	v_med3_f32 v227, v227, s62, v95
	v_med3_f32 v228, v228, s62, v95
	v_med3_f32 v229, v229, s62, v95
	v_med3_f32 v230, v230, s62, v95
	v_med3_f32 v231, v231, s62, v95
	v_med3_f32 v232, v232, s62, v95
	v_med3_f32 v233, v233, s62, v95
	v_med3_f32 v234, v234, s62, v95
	v_med3_f32 v235, v235, s62, v95
	v_med3_f32 v236, v236, s62, v95
	v_med3_f32 v237, v237, s62, v95
	v_med3_f32 v238, v238, s62, v95
	v_med3_f32 v239, v239, s62, v95
	v_med3_f32 v240, v240, s62, v95
	v_med3_f32 v241, v241, s62, v95
	v_mov_b32_e32 v242, 0
	v_mov_b32_e32 v243, 0
	v_mov_b32_e32 v244, 0
	v_mov_b32_e32 v245, 0
	v_cvt_pk_fp8_f32 v242, v226, v227
	v_cvt_pk_fp8_f32 v243, v230, v231
	v_cvt_pk_fp8_f32 v244, v234, v235
	v_cvt_pk_fp8_f32 v245, v238, v239
	v_cvt_pk_fp8_f32 v242, v228, v229 op_sel:[0,0,1]
	v_cvt_pk_fp8_f32 v243, v232, v233 op_sel:[0,0,1]
	v_cvt_pk_fp8_f32 v244, v236, v237 op_sel:[0,0,1]
	v_cvt_pk_fp8_f32 v245, v240, v241 op_sel:[0,0,1]
	s_nop 0
	global_store_dwordx4 v92, v[242:245], s[6:7]
	s_waitcnt vmcnt(12)
	v_mul_f32_e32 v176, v50, v176
	v_mul_f32_e32 v177, v50, v177
	v_mul_f32_e32 v178, v50, v178
	v_mul_f32_e32 v179, v50, v179
	ds_write_b128 v210, v[176:179]
	v_mul_f32_e32 v180, v51, v180
	v_mul_f32_e32 v181, v51, v181
	v_mul_f32_e32 v182, v51, v182
	v_mul_f32_e32 v183, v51, v183
	ds_write_b128 v210, v[180:183] offset:1024
	v_mul_f32_e32 v184, v52, v184
	v_mul_f32_e32 v185, v52, v185
	v_mul_f32_e32 v186, v52, v186
	v_mul_f32_e32 v187, v52, v187
	ds_write_b128 v210, v[184:187] offset:2048
	v_mul_f32_e32 v188, v53, v188
	v_mul_f32_e32 v189, v53, v189
	v_mul_f32_e32 v190, v53, v190
	v_mul_f32_e32 v191, v53, v191
	ds_write_b128 v210, v[188:191] offset:3072
	v_mul_f32_e32 v192, v54, v192
	v_mul_f32_e32 v193, v54, v193
	v_mul_f32_e32 v194, v54, v194
	v_mul_f32_e32 v195, v54, v195
	ds_write_b128 v210, v[192:195] offset:4096
	v_mul_f32_e32 v196, v55, v196
	v_mul_f32_e32 v197, v55, v197
	v_mul_f32_e32 v198, v55, v198
	v_mul_f32_e32 v199, v55, v199
	ds_write_b128 v210, v[196:199] offset:5120
	v_mul_f32_e32 v200, v56, v200
	v_mul_f32_e32 v201, v56, v201
	v_mul_f32_e32 v202, v56, v202
	v_mul_f32_e32 v203, v56, v203
	ds_write_b128 v210, v[200:203] offset:6144
	v_mul_f32_e32 v204, v57, v204
	v_mul_f32_e32 v205, v57, v205
	v_mul_f32_e32 v206, v57, v206
	v_mul_f32_e32 v207, v57, v207
	ds_write_b128 v210, v[204:207] offset:7168
	s_waitcnt lgkmcnt(0)
	s_barrier
; #define GAS __attribute__((address_space(1)))
; #define LAS __attribute__((address_space(3)))
; #define LDS_WAIT() asm volatile("s_waitcnt lgkmcnt(0)" ::: "memory")
; __device__ __forceinline__ int src_col_in(int c) {
;     if (c < 5120) { const int blk = c >> 7, p = c & 127; const bool rope = blk < 16 || ((((blk - 16) >> 2) & 1) == 0); const int d = rope ? (p >> 1) + 64 * (p & 1) : p; return blk * 128 + d; }
;     if (c < OFF_Z) return c + 2096;
;     if (c < OFF_G) return c - 4048;
;     if (c < OFF_DT) return 5120 + (c - OFF_G);
;     if (c < NSRC) return c;
;     return -1;
; }
;     const int pr = item >> 1, kb = 2 * (pr / nblk) + (item & 1), nb = pr % nblk, k0 = 64 * kb, n0 = 32 * nb;
;     const int nr = n0 + (lane & 31); const int sc = MAP == 1 ? src_col_in(nr) : nr;
;     float v[32];
; #pragma unroll
;     for (int i = 0; i < 32; ++i) v[i] = sc >= 0 ? W[(size_t)(k0 + 2 * i + (lane >> 5)) * Nsrc + sc] : 0.f;
; #pragma unroll
;     for (int i = 0; i < 32; ++i) { const int k = k0 + 2 * i + (lane >> 5); float x = v[i] * wscale; if (KS) x *= (k < ksplit ? ksA[k] : ksB[k - ksplit]); scr[(2 * i + (lane >> 5)) * 33 + (lane & 31)] = x; }
;     LDS_WAIT(); asm volatile("" ::: "memory");
;     const int c = lane & 7;
; #pragma unroll
;     for (int j = 0; j < 4; ++j) { const int n = (lane >> 3) + 8 * j; const LAS float* s = scr + (8 * c) * 33 + n;
;         const unsigned long long o = (unsigned long long)pg8::pk4_fp8(s[0 * 33], s[1 * 33], s[2 * 33], s[3 * 33]) | ((unsigned long long)pg8::pk4_fp8(s[4 * 33], s[5 * 33], s[6 * 33], s[7 * 33]) << 32);
;         *(GAS unsigned long long*)(WT + (size_t)(n0 + n) * K + k0 + 8 * c) = o; }
;     LDS_WAIT(); asm volatile("" ::: "memory");
; }
	s_add_i32 s24, s23, 48
	s_lshl_b32 s20, s24, 7
	s_cmp_lt_u32 s24, 40
	s_cselect_b32 s21, 0, 0x830
	s_cmp_lt_u32 s24, 72
	s_cselect_b32 s21, s21, 0xfffff030
	s_add_i32 s20, s20, s21
	s_lshl_b32 s20, s20, 2
	s_add_u32 s8, s50, s20
	s_addc_u32 s9, s51, 0
	global_load_dwordx4 v[176:179], v76, s[8:9]
	s_add_u32 s8, s8, 0x16280
	s_addc_u32 s9, s9, 0
	global_load_dwordx4 v[180:183], v76, s[8:9]
	s_add_u32 s8, s8, 0x16280
	s_addc_u32 s9, s9, 0
	global_load_dwordx4 v[184:187], v76, s[8:9]
	s_add_u32 s8, s8, 0x16280
	s_addc_u32 s9, s9, 0
	global_load_dwordx4 v[188:191], v76, s[8:9]
	s_add_u32 s8, s8, 0x16280
	s_addc_u32 s9, s9, 0
	global_load_dwordx4 v[192:195], v76, s[8:9]
	s_add_u32 s8, s8, 0x16280
	s_addc_u32 s9, s9, 0
	global_load_dwordx4 v[196:199], v76, s[8:9]
	s_add_u32 s8, s8, 0x16280
	s_addc_u32 s9, s9, 0
	global_load_dwordx4 v[200:203], v76, s[8:9]
	s_add_u32 s8, s8, 0x16280
	s_addc_u32 s9, s9, 0
	global_load_dwordx4 v[204:207], v76, s[8:9]
	s_add_i32 s24, s23, 32
	s_mul_i32 s20, s24, 0x80000
	s_add_u32 s6, s52, s20
	s_addc_u32 s7, s53, 0
	s_cmp_lt_u32 s24, 16
	s_cselect_b32 s20, 1, 0
	s_sub_i32 s21, s24, 16
	s_bitcmp0_b32 s21, 2
	s_cselect_b32 s21, 1, 0
	s_cmp_lt_u32 s24, 40
	s_cselect_b32 s21, s21, 0
	s_or_b32 s20, s20, s21
	s_cmp_lg_u32 s20, 0
	s_cselect_b64 s[20:21], -1, 0
	v_cndmask_b32_e64 v91, v77, v81, s[20:21]
	v_cndmask_b32_e64 v92, v78, v82, s[20:21]
	ds_read_b32 v226, v212
	ds_read_b32 v227, v212 offset:512
	ds_read_b32 v228, v212 offset:1024
	ds_read_b32 v229, v212 offset:1536
	ds_read_b32 v230, v212 offset:2048
	ds_read_b32 v231, v212 offset:2560
	ds_read_b32 v232, v212 offset:3072
	ds_read_b32 v233, v212 offset:3584
	ds_read_b32 v234, v212 offset:4096
	ds_read_b32 v235, v212 offset:4608
	ds_read_b32 v236, v212 offset:5120
	ds_read_b32 v237, v212 offset:5632
	ds_read_b32 v238, v212 offset:6144
	ds_read_b32 v239, v212 offset:6656
	ds_read_b32 v240, v212 offset:7168
	ds_read_b32 v241, v212 offset:7680
	s_waitcnt lgkmcnt(0)
	v_max_f32_e32 v226, v226, v226
	v_max_f32_e32 v227, v227, v227
	v_max_f32_e32 v228, v228, v228
	v_max_f32_e32 v229, v229, v229
	v_max_f32_e32 v230, v230, v230
	v_max_f32_e32 v231, v231, v231
	v_max_f32_e32 v232, v232, v232
	v_max_f32_e32 v233, v233, v233
	v_max_f32_e32 v234, v234, v234
	v_max_f32_e32 v235, v235, v235
	v_max_f32_e32 v236, v236, v236
	v_max_f32_e32 v237, v237, v237
	v_max_f32_e32 v238, v238, v238
	v_max_f32_e32 v239, v239, v239
	v_max_f32_e32 v240, v240, v240
	v_max_f32_e32 v241, v241, v241
	v_med3_f32 v226, v226, s62, v95
	v_med3_f32 v227, v227, s62, v95
	v_med3_f32 v228, v228, s62, v95
	v_med3_f32 v229, v229, s62, v95
	v_med3_f32 v230, v230, s62, v95
	v_med3_f32 v231, v231, s62, v95
	v_med3_f32 v232, v232, s62, v95
	v_med3_f32 v233, v233, s62, v95
	v_med3_f32 v234, v234, s62, v95
	v_med3_f32 v235, v235, s62, v95
	v_med3_f32 v236, v236, s62, v95
	v_med3_f32 v237, v237, s62, v95
	v_med3_f32 v238, v238, s62, v95
	v_med3_f32 v239, v239, s62, v95
	v_med3_f32 v240, v240, s62, v95
	v_med3_f32 v241, v241, s62, v95
	v_mov_b32_e32 v242, 0
	v_mov_b32_e32 v243, 0
	v_mov_b32_e32 v244, 0
	v_mov_b32_e32 v245, 0
	v_cvt_pk_fp8_f32 v242, v226, v227
	v_cvt_pk_fp8_f32 v243, v230, v231
	v_cvt_pk_fp8_f32 v244, v234, v235
	v_cvt_pk_fp8_f32 v245, v238, v239
	v_cvt_pk_fp8_f32 v242, v228, v229 op_sel:[0,0,1]
	v_cvt_pk_fp8_f32 v243, v232, v233 op_sel:[0,0,1]
	v_cvt_pk_fp8_f32 v244, v236, v237 op_sel:[0,0,1]
	v_cvt_pk_fp8_f32 v245, v240, v241 op_sel:[0,0,1]
	s_nop 0
	global_store_dwordx4 v91, v[242:245], s[6:7]
	ds_read_b32 v226, v214
	ds_read_b32 v227, v214 offset:512
	ds_read_b32 v228, v214 offset:1024
	ds_read_b32 v229, v214 offset:1536
	ds_read_b32 v230, v214 offset:2048
	ds_read_b32 v231, v214 offset:2560
	ds_read_b32 v232, v214 offset:3072
	ds_read_b32 v233, v214 offset:3584
	ds_read_b32 v234, v214 offset:4096
	ds_read_b32 v235, v214 offset:4608
	ds_read_b32 v236, v214 offset:5120
	ds_read_b32 v237, v214 offset:5632
	ds_read_b32 v238, v214 offset:6144
	ds_read_b32 v239, v214 offset:6656
	ds_read_b32 v240, v214 offset:7168
	ds_read_b32 v241, v214 offset:7680
	s_waitcnt lgkmcnt(0)
	v_max_f32_e32 v226, v226, v226
	v_max_f32_e32 v227, v227, v227
	v_max_f32_e32 v228, v228, v228
	v_max_f32_e32 v229, v229, v229
	v_max_f32_e32 v230, v230, v230
	v_max_f32_e32 v231, v231, v231
	v_max_f32_e32 v232, v232, v232
	v_max_f32_e32 v233, v233, v233
	v_max_f32_e32 v234, v234, v234
	v_max_f32_e32 v235, v235, v235
	v_max_f32_e32 v236, v236, v236
	v_max_f32_e32 v237, v237, v237
	v_max_f32_e32 v238, v238, v238
	v_max_f32_e32 v239, v239, v239
	v_max_f32_e32 v240, v240, v240
	v_max_f32_e32 v241, v241, v241
	v_med3_f32 v226, v226, s62, v95
	v_med3_f32 v227, v227, s62, v95
	v_med3_f32 v228, v228, s62, v95
	v_med3_f32 v229, v229, s62, v95
	v_med3_f32 v230, v230, s62, v95
	v_med3_f32 v231, v231, s62, v95
	v_med3_f32 v232, v232, s62, v95
	v_med3_f32 v233, v233, s62, v95
	v_med3_f32 v234, v234, s62, v95
	v_med3_f32 v235, v235, s62, v95
	v_med3_f32 v236, v236, s62, v95
	v_med3_f32 v237, v237, s62, v95
	v_med3_f32 v238, v238, s62, v95
	v_med3_f32 v239, v239, s62, v95
	v_med3_f32 v240, v240, s62, v95
	v_med3_f32 v241, v241, s62, v95
	v_mov_b32_e32 v242, 0
	v_mov_b32_e32 v243, 0
	v_mov_b32_e32 v244, 0
	v_mov_b32_e32 v245, 0
	v_cvt_pk_fp8_f32 v242, v226, v227
	v_cvt_pk_fp8_f32 v243, v230, v231
	v_cvt_pk_fp8_f32 v244, v234, v235
	v_cvt_pk_fp8_f32 v245, v238, v239
	v_cvt_pk_fp8_f32 v242, v228, v229 op_sel:[0,0,1]
	v_cvt_pk_fp8_f32 v243, v232, v233 op_sel:[0,0,1]
	v_cvt_pk_fp8_f32 v244, v236, v237 op_sel:[0,0,1]
	v_cvt_pk_fp8_f32 v245, v240, v241 op_sel:[0,0,1]
	s_nop 0
	global_store_dwordx4 v92, v[242:245], s[6:7]
	s_waitcnt vmcnt(12)
	v_mul_f32_e32 v144, v50, v144
	v_mul_f32_e32 v145, v50, v145
	v_mul_f32_e32 v146, v50, v146
	v_mul_f32_e32 v147, v50, v147
	ds_write_b128 v209, v[144:147]
	v_mul_f32_e32 v148, v51, v148
	v_mul_f32_e32 v149, v51, v149
	v_mul_f32_e32 v150, v51, v150
	v_mul_f32_e32 v151, v51, v151
	ds_write_b128 v209, v[148:151] offset:1024
	v_mul_f32_e32 v152, v52, v152
	v_mul_f32_e32 v153, v52, v153
	v_mul_f32_e32 v154, v52, v154
	v_mul_f32_e32 v155, v52, v155
	ds_write_b128 v209, v[152:155] offset:2048
	v_mul_f32_e32 v156, v53, v156
	v_mul_f32_e32 v157, v53, v157
	v_mul_f32_e32 v158, v53, v158
	v_mul_f32_e32 v159, v53, v159
	ds_write_b128 v209, v[156:159] offset:3072
	v_mul_f32_e32 v160, v54, v160
	v_mul_f32_e32 v161, v54, v161
	v_mul_f32_e32 v162, v54, v162
	v_mul_f32_e32 v163, v54, v163
	ds_write_b128 v209, v[160:163] offset:4096
	v_mul_f32_e32 v164, v55, v164
	v_mul_f32_e32 v165, v55, v165
	v_mul_f32_e32 v166, v55, v166
	v_mul_f32_e32 v167, v55, v167
	ds_write_b128 v209, v[164:167] offset:5120
	v_mul_f32_e32 v168, v56, v168
	v_mul_f32_e32 v169, v56, v169
	v_mul_f32_e32 v170, v56, v170
	v_mul_f32_e32 v171, v56, v171
	ds_write_b128 v209, v[168:171] offset:6144
	v_mul_f32_e32 v172, v57, v172
	v_mul_f32_e32 v173, v57, v173
	v_mul_f32_e32 v174, v57, v174
	v_mul_f32_e32 v175, v57, v175
	ds_write_b128 v209, v[172:175] offset:7168
	s_waitcnt lgkmcnt(0)
	s_barrier
; #define GAS __attribute__((address_space(1)))
; #define LAS __attribute__((address_space(3)))
; #define LDS_WAIT() asm volatile("s_waitcnt lgkmcnt(0)" ::: "memory")
; __device__ __forceinline__ int src_col_in(int c) {
;     if (c < 5120) { const int blk = c >> 7, p = c & 127; const bool rope = blk < 16 || ((((blk - 16) >> 2) & 1) == 0); const int d = rope ? (p >> 1) + 64 * (p & 1) : p; return blk * 128 + d; }
;     if (c < OFF_Z) return c + 2096;
;     if (c < OFF_G) return c - 4048;
;     if (c < OFF_DT) return 5120 + (c - OFF_G);
;     if (c < NSRC) return c;
;     return -1;
; }
;     const int pr = item >> 1, kb = 2 * (pr / nblk) + (item & 1), nb = pr % nblk, k0 = 64 * kb, n0 = 32 * nb;
;     const int nr = n0 + (lane & 31); const int sc = MAP == 1 ? src_col_in(nr) : nr;
;     float v[32];
; #pragma unroll
;     for (int i = 0; i < 32; ++i) v[i] = sc >= 0 ? W[(size_t)(k0 + 2 * i + (lane >> 5)) * Nsrc + sc] : 0.f;
; #pragma unroll
;     for (int i = 0; i < 32; ++i) { const int k = k0 + 2 * i + (lane >> 5); float x = v[i] * wscale; if (KS) x *= (k < ksplit ? ksA[k] : ksB[k - ksplit]); scr[(2 * i + (lane >> 5)) * 33 + (lane & 31)] = x; }
;     LDS_WAIT(); asm volatile("" ::: "memory");
;     const int c = lane & 7;
; #pragma unroll
;     for (int j = 0; j < 4; ++j) { const int n = (lane >> 3) + 8 * j; const LAS float* s = scr + (8 * c) * 33 + n;
;         const unsigned long long o = (unsigned long long)pg8::pk4_fp8(s[0 * 33], s[1 * 33], s[2 * 33], s[3 * 33]) | ((unsigned long long)pg8::pk4_fp8(s[4 * 33], s[5 * 33], s[6 * 33], s[7 * 33]) << 32);
;         *(GAS unsigned long long*)(WT + (size_t)(n0 + n) * K + k0 + 8 * c) = o; }
;     LDS_WAIT(); asm volatile("" ::: "memory");
; }
	s_add_i32 s24, s23, 56
	s_lshl_b32 s20, s24, 7
	s_cmp_lt_u32 s24, 40
	s_cselect_b32 s21, 0, 0x830
	s_cmp_lt_u32 s24, 72
	s_cselect_b32 s21, s21, 0xfffff030
	s_add_i32 s20, s20, s21
	s_lshl_b32 s20, s20, 2
	s_add_u32 s8, s50, s20
	s_addc_u32 s9, s51, 0
	global_load_dwordx4 v[144:147], v76, s[8:9]
	s_add_u32 s8, s8, 0x16280
	s_addc_u32 s9, s9, 0
	global_load_dwordx4 v[148:151], v76, s[8:9]
	s_add_u32 s8, s8, 0x16280
	s_addc_u32 s9, s9, 0
	global_load_dwordx4 v[152:155], v76, s[8:9]
	s_add_u32 s8, s8, 0x16280
	s_addc_u32 s9, s9, 0
	global_load_dwordx4 v[156:159], v76, s[8:9]
	s_add_u32 s8, s8, 0x16280
	s_addc_u32 s9, s9, 0
	global_load_dwordx4 v[160:163], v76, s[8:9]
	s_add_u32 s8, s8, 0x16280
	s_addc_u32 s9, s9, 0
	global_load_dwordx4 v[164:167], v76, s[8:9]
	s_add_u32 s8, s8, 0x16280
	s_addc_u32 s9, s9, 0
	global_load_dwordx4 v[168:171], v76, s[8:9]
	s_add_u32 s8, s8, 0x16280
	s_addc_u32 s9, s9, 0
	global_load_dwordx4 v[172:175], v76, s[8:9]
	s_add_i32 s24, s23, 40
	s_mul_i32 s20, s24, 0x80000
	s_add_u32 s6, s52, s20
	s_addc_u32 s7, s53, 0
	s_cmp_lt_u32 s24, 16
	s_cselect_b32 s20, 1, 0
	s_sub_i32 s21, s24, 16
	s_bitcmp0_b32 s21, 2
	s_cselect_b32 s21, 1, 0
	s_cmp_lt_u32 s24, 40
	s_cselect_b32 s21, s21, 0
	s_or_b32 s20, s20, s21
	s_cmp_lg_u32 s20, 0
	s_cselect_b64 s[20:21], -1, 0
	v_cndmask_b32_e64 v91, v77, v81, s[20:21]
	v_cndmask_b32_e64 v92, v78, v82, s[20:21]
	ds_read_b32 v226, v211
	ds_read_b32 v227, v211 offset:512
	ds_read_b32 v228, v211 offset:1024
	ds_read_b32 v229, v211 offset:1536
	ds_read_b32 v230, v211 offset:2048
	ds_read_b32 v231, v211 offset:2560
	ds_read_b32 v232, v211 offset:3072
	ds_read_b32 v233, v211 offset:3584
	ds_read_b32 v234, v211 offset:4096
	ds_read_b32 v235, v211 offset:4608
	ds_read_b32 v236, v211 offset:5120
	ds_read_b32 v237, v211 offset:5632
	ds_read_b32 v238, v211 offset:6144
	ds_read_b32 v239, v211 offset:6656
	ds_read_b32 v240, v211 offset:7168
	ds_read_b32 v241, v211 offset:7680
	s_waitcnt lgkmcnt(0)
	v_max_f32_e32 v226, v226, v226
	v_max_f32_e32 v227, v227, v227
	v_max_f32_e32 v228, v228, v228
	v_max_f32_e32 v229, v229, v229
	v_max_f32_e32 v230, v230, v230
	v_max_f32_e32 v231, v231, v231
	v_max_f32_e32 v232, v232, v232
	v_max_f32_e32 v233, v233, v233
	v_max_f32_e32 v234, v234, v234
	v_max_f32_e32 v235, v235, v235
	v_max_f32_e32 v236, v236, v236
	v_max_f32_e32 v237, v237, v237
	v_max_f32_e32 v238, v238, v238
	v_max_f32_e32 v239, v239, v239
	v_max_f32_e32 v240, v240, v240
	v_max_f32_e32 v241, v241, v241
	v_med3_f32 v226, v226, s62, v95
	v_med3_f32 v227, v227, s62, v95
	v_med3_f32 v228, v228, s62, v95
	v_med3_f32 v229, v229, s62, v95
	v_med3_f32 v230, v230, s62, v95
	v_med3_f32 v231, v231, s62, v95
	v_med3_f32 v232, v232, s62, v95
	v_med3_f32 v233, v233, s62, v95
	v_med3_f32 v234, v234, s62, v95
	v_med3_f32 v235, v235, s62, v95
	v_med3_f32 v236, v236, s62, v95
	v_med3_f32 v237, v237, s62, v95
	v_med3_f32 v238, v238, s62, v95
	v_med3_f32 v239, v239, s62, v95
	v_med3_f32 v240, v240, s62, v95
	v_med3_f32 v241, v241, s62, v95
	v_mov_b32_e32 v242, 0
	v_mov_b32_e32 v243, 0
	v_mov_b32_e32 v244, 0
	v_mov_b32_e32 v245, 0
	v_cvt_pk_fp8_f32 v242, v226, v227
	v_cvt_pk_fp8_f32 v243, v230, v231
	v_cvt_pk_fp8_f32 v244, v234, v235
	v_cvt_pk_fp8_f32 v245, v238, v239
	v_cvt_pk_fp8_f32 v242, v228, v229 op_sel:[0,0,1]
	v_cvt_pk_fp8_f32 v243, v232, v233 op_sel:[0,0,1]
	v_cvt_pk_fp8_f32 v244, v236, v237 op_sel:[0,0,1]
	v_cvt_pk_fp8_f32 v245, v240, v241 op_sel:[0,0,1]
	s_nop 0
	global_store_dwordx4 v91, v[242:245], s[6:7]
	ds_read_b32 v226, v213
	ds_read_b32 v227, v213 offset:512
	ds_read_b32 v228, v213 offset:1024
	ds_read_b32 v229, v213 offset:1536
	ds_read_b32 v230, v213 offset:2048
	ds_read_b32 v231, v213 offset:2560
	ds_read_b32 v232, v213 offset:3072
	ds_read_b32 v233, v213 offset:3584
	ds_read_b32 v234, v213 offset:4096
	ds_read_b32 v235, v213 offset:4608
	ds_read_b32 v236, v213 offset:5120
	ds_read_b32 v237, v213 offset:5632
	ds_read_b32 v238, v213 offset:6144
	ds_read_b32 v239, v213 offset:6656
	ds_read_b32 v240, v213 offset:7168
	ds_read_b32 v241, v213 offset:7680
	s_waitcnt lgkmcnt(0)
	v_max_f32_e32 v226, v226, v226
	v_max_f32_e32 v227, v227, v227
	v_max_f32_e32 v228, v228, v228
	v_max_f32_e32 v229, v229, v229
	v_max_f32_e32 v230, v230, v230
	v_max_f32_e32 v231, v231, v231
	v_max_f32_e32 v232, v232, v232
	v_max_f32_e32 v233, v233, v233
	v_max_f32_e32 v234, v234, v234
	v_max_f32_e32 v235, v235, v235
	v_max_f32_e32 v236, v236, v236
	v_max_f32_e32 v237, v237, v237
	v_max_f32_e32 v238, v238, v238
	v_max_f32_e32 v239, v239, v239
	v_max_f32_e32 v240, v240, v240
	v_max_f32_e32 v241, v241, v241
	v_med3_f32 v226, v226, s62, v95
	v_med3_f32 v227, v227, s62, v95
	v_med3_f32 v228, v228, s62, v95
	v_med3_f32 v229, v229, s62, v95
	v_med3_f32 v230, v230, s62, v95
	v_med3_f32 v231, v231, s62, v95
	v_med3_f32 v232, v232, s62, v95
	v_med3_f32 v233, v233, s62, v95
	v_med3_f32 v234, v234, s62, v95
	v_med3_f32 v235, v235, s62, v95
	v_med3_f32 v236, v236, s62, v95
	v_med3_f32 v237, v237, s62, v95
	v_med3_f32 v238, v238, s62, v95
	v_med3_f32 v239, v239, s62, v95
	v_med3_f32 v240, v240, s62, v95
	v_med3_f32 v241, v241, s62, v95
	v_mov_b32_e32 v242, 0
	v_mov_b32_e32 v243, 0
	v_mov_b32_e32 v244, 0
	v_mov_b32_e32 v245, 0
	v_cvt_pk_fp8_f32 v242, v226, v227
	v_cvt_pk_fp8_f32 v243, v230, v231
	v_cvt_pk_fp8_f32 v244, v234, v235
	v_cvt_pk_fp8_f32 v245, v238, v239
	v_cvt_pk_fp8_f32 v242, v228, v229 op_sel:[0,0,1]
	v_cvt_pk_fp8_f32 v243, v232, v233 op_sel:[0,0,1]
	v_cvt_pk_fp8_f32 v244, v236, v237 op_sel:[0,0,1]
	v_cvt_pk_fp8_f32 v245, v240, v241 op_sel:[0,0,1]
	s_nop 0
	global_store_dwordx4 v92, v[242:245], s[6:7]
	s_waitcnt vmcnt(12)
	v_mul_f32_e32 v176, v50, v176
	v_mul_f32_e32 v177, v50, v177
	v_mul_f32_e32 v178, v50, v178
	v_mul_f32_e32 v179, v50, v179
	ds_write_b128 v210, v[176:179]
	v_mul_f32_e32 v180, v51, v180
	v_mul_f32_e32 v181, v51, v181
	v_mul_f32_e32 v182, v51, v182
	v_mul_f32_e32 v183, v51, v183
	ds_write_b128 v210, v[180:183] offset:1024
	v_mul_f32_e32 v184, v52, v184
	v_mul_f32_e32 v185, v52, v185
	v_mul_f32_e32 v186, v52, v186
	v_mul_f32_e32 v187, v52, v187
	ds_write_b128 v210, v[184:187] offset:2048
	v_mul_f32_e32 v188, v53, v188
	v_mul_f32_e32 v189, v53, v189
	v_mul_f32_e32 v190, v53, v190
	v_mul_f32_e32 v191, v53, v191
	ds_write_b128 v210, v[188:191] offset:3072
	v_mul_f32_e32 v192, v54, v192
	v_mul_f32_e32 v193, v54, v193
	v_mul_f32_e32 v194, v54, v194
	v_mul_f32_e32 v195, v54, v195
	ds_write_b128 v210, v[192:195] offset:4096
	v_mul_f32_e32 v196, v55, v196
	v_mul_f32_e32 v197, v55, v197
	v_mul_f32_e32 v198, v55, v198
	v_mul_f32_e32 v199, v55, v199
	ds_write_b128 v210, v[196:199] offset:5120
	v_mul_f32_e32 v200, v56, v200
	v_mul_f32_e32 v201, v56, v201
	v_mul_f32_e32 v202, v56, v202
	v_mul_f32_e32 v203, v56, v203
	ds_write_b128 v210, v[200:203] offset:6144
	v_mul_f32_e32 v204, v57, v204
	v_mul_f32_e32 v205, v57, v205
	v_mul_f32_e32 v206, v57, v206
	v_mul_f32_e32 v207, v57, v207
	ds_write_b128 v210, v[204:207] offset:7168
	s_waitcnt lgkmcnt(0)
	s_barrier
; #define GAS __attribute__((address_space(1)))
; #define LAS __attribute__((address_space(3)))
; #define LDS_WAIT() asm volatile("s_waitcnt lgkmcnt(0)" ::: "memory")
; __device__ __forceinline__ int src_col_in(int c) {
;     if (c < 5120) { const int blk = c >> 7, p = c & 127; const bool rope = blk < 16 || ((((blk - 16) >> 2) & 1) == 0); const int d = rope ? (p >> 1) + 64 * (p & 1) : p; return blk * 128 + d; }
;     if (c < OFF_Z) return c + 2096;
;     if (c < OFF_G) return c - 4048;
;     if (c < OFF_DT) return 5120 + (c - OFF_G);
;     if (c < NSRC) return c;
;     return -1;
; }
;     const int pr = item >> 1, kb = 2 * (pr / nblk) + (item & 1), nb = pr % nblk, k0 = 64 * kb, n0 = 32 * nb;
;     const int nr = n0 + (lane & 31); const int sc = MAP == 1 ? src_col_in(nr) : nr;
;     float v[32];
; #pragma unroll
;     for (int i = 0; i < 32; ++i) v[i] = sc >= 0 ? W[(size_t)(k0 + 2 * i + (lane >> 5)) * Nsrc + sc] : 0.f;
; #pragma unroll
;     for (int i = 0; i < 32; ++i) { const int k = k0 + 2 * i + (lane >> 5); float x = v[i] * wscale; if (KS) x *= (k < ksplit ? ksA[k] : ksB[k - ksplit]); scr[(2 * i + (lane >> 5)) * 33 + (lane & 31)] = x; }
;     LDS_WAIT(); asm volatile("" ::: "memory");
;     const int c = lane & 7;
; #pragma unroll
;     for (int j = 0; j < 4; ++j) { const int n = (lane >> 3) + 8 * j; const LAS float* s = scr + (8 * c) * 33 + n;
;         const unsigned long long o = (unsigned long long)pg8::pk4_fp8(s[0 * 33], s[1 * 33], s[2 * 33], s[3 * 33]) | ((unsigned long long)pg8::pk4_fp8(s[4 * 33], s[5 * 33], s[6 * 33], s[7 * 33]) << 32);
;         *(GAS unsigned long long*)(WT + (size_t)(n0 + n) * K + k0 + 8 * c) = o; }
;     LDS_WAIT(); asm volatile("" ::: "memory");
; }
	s_add_i32 s24, s23, 64
	s_lshl_b32 s20, s24, 7
	s_cmp_lt_u32 s24, 40
	s_cselect_b32 s21, 0, 0x830
	s_cmp_lt_u32 s24, 72
	s_cselect_b32 s21, s21, 0xfffff030
	s_add_i32 s20, s20, s21
	s_lshl_b32 s20, s20, 2
	s_add_u32 s8, s50, s20
	s_addc_u32 s9, s51, 0
	global_load_dwordx4 v[176:179], v76, s[8:9]
	s_add_u32 s8, s8, 0x16280
	s_addc_u32 s9, s9, 0
	global_load_dwordx4 v[180:183], v76, s[8:9]
	s_add_u32 s8, s8, 0x16280
	s_addc_u32 s9, s9, 0
	global_load_dwordx4 v[184:187], v76, s[8:9]
	s_add_u32 s8, s8, 0x16280
	s_addc_u32 s9, s9, 0
	global_load_dwordx4 v[188:191], v76, s[8:9]
	s_add_u32 s8, s8, 0x16280
	s_addc_u32 s9, s9, 0
	global_load_dwordx4 v[192:195], v76, s[8:9]
	s_add_u32 s8, s8, 0x16280
	s_addc_u32 s9, s9, 0
	global_load_dwordx4 v[196:199], v76, s[8:9]
	s_add_u32 s8, s8, 0x16280
	s_addc_u32 s9, s9, 0
	global_load_dwordx4 v[200:203], v76, s[8:9]
	s_add_u32 s8, s8, 0x16280
	s_addc_u32 s9, s9, 0
	global_load_dwordx4 v[204:207], v76, s[8:9]
	s_add_i32 s24, s23, 48
	s_mul_i32 s20, s24, 0x80000
	s_add_u32 s6, s52, s20
	s_addc_u32 s7, s53, 0
	s_cmp_lt_u32 s24, 16
	s_cselect_b32 s20, 1, 0
	s_sub_i32 s21, s24, 16
	s_bitcmp0_b32 s21, 2
	s_cselect_b32 s21, 1, 0
	s_cmp_lt_u32 s24, 40
	s_cselect_b32 s21, s21, 0
	s_or_b32 s20, s20, s21
	s_cmp_lg_u32 s20, 0
	s_cselect_b64 s[20:21], -1, 0
	v_cndmask_b32_e64 v91, v77, v81, s[20:21]
	v_cndmask_b32_e64 v92, v78, v82, s[20:21]
	ds_read_b32 v226, v212
	ds_read_b32 v227, v212 offset:512
	ds_read_b32 v228, v212 offset:1024
	ds_read_b32 v229, v212 offset:1536
	ds_read_b32 v230, v212 offset:2048
	ds_read_b32 v231, v212 offset:2560
	ds_read_b32 v232, v212 offset:3072
	ds_read_b32 v233, v212 offset:3584
	ds_read_b32 v234, v212 offset:4096
	ds_read_b32 v235, v212 offset:4608
	ds_read_b32 v236, v212 offset:5120
	ds_read_b32 v237, v212 offset:5632
	ds_read_b32 v238, v212 offset:6144
	ds_read_b32 v239, v212 offset:6656
	ds_read_b32 v240, v212 offset:7168
	ds_read_b32 v241, v212 offset:7680
	s_waitcnt lgkmcnt(0)
	v_max_f32_e32 v226, v226, v226
	v_max_f32_e32 v227, v227, v227
	v_max_f32_e32 v228, v228, v228
	v_max_f32_e32 v229, v229, v229
	v_max_f32_e32 v230, v230, v230
	v_max_f32_e32 v231, v231, v231
	v_max_f32_e32 v232, v232, v232
	v_max_f32_e32 v233, v233, v233
	v_max_f32_e32 v234, v234, v234
	v_max_f32_e32 v235, v235, v235
	v_max_f32_e32 v236, v236, v236
	v_max_f32_e32 v237, v237, v237
	v_max_f32_e32 v238, v238, v238
	v_max_f32_e32 v239, v239, v239
	v_max_f32_e32 v240, v240, v240
	v_max_f32_e32 v241, v241, v241
	v_med3_f32 v226, v226, s62, v95
	v_med3_f32 v227, v227, s62, v95
	v_med3_f32 v228, v228, s62, v95
	v_med3_f32 v229, v229, s62, v95
	v_med3_f32 v230, v230, s62, v95
	v_med3_f32 v231, v231, s62, v95
	v_med3_f32 v232, v232, s62, v95
	v_med3_f32 v233, v233, s62, v95
	v_med3_f32 v234, v234, s62, v95
	v_med3_f32 v235, v235, s62, v95
	v_med3_f32 v236, v236, s62, v95
	v_med3_f32 v237, v237, s62, v95
	v_med3_f32 v238, v238, s62, v95
	v_med3_f32 v239, v239, s62, v95
	v_med3_f32 v240, v240, s62, v95
	v_med3_f32 v241, v241, s62, v95
	v_mov_b32_e32 v242, 0
	v_mov_b32_e32 v243, 0
	v_mov_b32_e32 v244, 0
	v_mov_b32_e32 v245, 0
	v_cvt_pk_fp8_f32 v242, v226, v227
	v_cvt_pk_fp8_f32 v243, v230, v231
	v_cvt_pk_fp8_f32 v244, v234, v235
	v_cvt_pk_fp8_f32 v245, v238, v239
	v_cvt_pk_fp8_f32 v242, v228, v229 op_sel:[0,0,1]
	v_cvt_pk_fp8_f32 v243, v232, v233 op_sel:[0,0,1]
	v_cvt_pk_fp8_f32 v244, v236, v237 op_sel:[0,0,1]
	v_cvt_pk_fp8_f32 v245, v240, v241 op_sel:[0,0,1]
	s_nop 0
	global_store_dwordx4 v91, v[242:245], s[6:7]
	ds_read_b32 v226, v214
	ds_read_b32 v227, v214 offset:512
	ds_read_b32 v228, v214 offset:1024
	ds_read_b32 v229, v214 offset:1536
	ds_read_b32 v230, v214 offset:2048
	ds_read_b32 v231, v214 offset:2560
	ds_read_b32 v232, v214 offset:3072
	ds_read_b32 v233, v214 offset:3584
	ds_read_b32 v234, v214 offset:4096
	ds_read_b32 v235, v214 offset:4608
	ds_read_b32 v236, v214 offset:5120
	ds_read_b32 v237, v214 offset:5632
	ds_read_b32 v238, v214 offset:6144
	ds_read_b32 v239, v214 offset:6656
	ds_read_b32 v240, v214 offset:7168
	ds_read_b32 v241, v214 offset:7680
	s_waitcnt lgkmcnt(0)
	v_max_f32_e32 v226, v226, v226
	v_max_f32_e32 v227, v227, v227
	v_max_f32_e32 v228, v228, v228
	v_max_f32_e32 v229, v229, v229
	v_max_f32_e32 v230, v230, v230
	v_max_f32_e32 v231, v231, v231
	v_max_f32_e32 v232, v232, v232
	v_max_f32_e32 v233, v233, v233
	v_max_f32_e32 v234, v234, v234
	v_max_f32_e32 v235, v235, v235
	v_max_f32_e32 v236, v236, v236
	v_max_f32_e32 v237, v237, v237
	v_max_f32_e32 v238, v238, v238
	v_max_f32_e32 v239, v239, v239
	v_max_f32_e32 v240, v240, v240
	v_max_f32_e32 v241, v241, v241
	v_med3_f32 v226, v226, s62, v95
	v_med3_f32 v227, v227, s62, v95
	v_med3_f32 v228, v228, s62, v95
	v_med3_f32 v229, v229, s62, v95
	v_med3_f32 v230, v230, s62, v95
	v_med3_f32 v231, v231, s62, v95
	v_med3_f32 v232, v232, s62, v95
	v_med3_f32 v233, v233, s62, v95
	v_med3_f32 v234, v234, s62, v95
	v_med3_f32 v235, v235, s62, v95
	v_med3_f32 v236, v236, s62, v95
	v_med3_f32 v237, v237, s62, v95
	v_med3_f32 v238, v238, s62, v95
	v_med3_f32 v239, v239, s62, v95
	v_med3_f32 v240, v240, s62, v95
	v_med3_f32 v241, v241, s62, v95
	v_mov_b32_e32 v242, 0
	v_mov_b32_e32 v243, 0
	v_mov_b32_e32 v244, 0
	v_mov_b32_e32 v245, 0
	v_cvt_pk_fp8_f32 v242, v226, v227
	v_cvt_pk_fp8_f32 v243, v230, v231
	v_cvt_pk_fp8_f32 v244, v234, v235
	v_cvt_pk_fp8_f32 v245, v238, v239
	v_cvt_pk_fp8_f32 v242, v228, v229 op_sel:[0,0,1]
	v_cvt_pk_fp8_f32 v243, v232, v233 op_sel:[0,0,1]
	v_cvt_pk_fp8_f32 v244, v236, v237 op_sel:[0,0,1]
	v_cvt_pk_fp8_f32 v245, v240, v241 op_sel:[0,0,1]
	s_nop 0
	global_store_dwordx4 v92, v[242:245], s[6:7]
	s_waitcnt vmcnt(12)
	v_mul_f32_e32 v144, v50, v144
	v_mul_f32_e32 v145, v50, v145
	v_mul_f32_e32 v146, v50, v146
	v_mul_f32_e32 v147, v50, v147
	ds_write_b128 v209, v[144:147]
	v_mul_f32_e32 v148, v51, v148
	v_mul_f32_e32 v149, v51, v149
	v_mul_f32_e32 v150, v51, v150
	v_mul_f32_e32 v151, v51, v151
	ds_write_b128 v209, v[148:151] offset:1024
	v_mul_f32_e32 v152, v52, v152
	v_mul_f32_e32 v153, v52, v153
	v_mul_f32_e32 v154, v52, v154
	v_mul_f32_e32 v155, v52, v155
	ds_write_b128 v209, v[152:155] offset:2048
	v_mul_f32_e32 v156, v53, v156
	v_mul_f32_e32 v157, v53, v157
	v_mul_f32_e32 v158, v53, v158
	v_mul_f32_e32 v159, v53, v159
	ds_write_b128 v209, v[156:159] offset:3072
	v_mul_f32_e32 v160, v54, v160
	v_mul_f32_e32 v161, v54, v161
	v_mul_f32_e32 v162, v54, v162
	v_mul_f32_e32 v163, v54, v163
	ds_write_b128 v209, v[160:163] offset:4096
	v_mul_f32_e32 v164, v55, v164
	v_mul_f32_e32 v165, v55, v165
	v_mul_f32_e32 v166, v55, v166
	v_mul_f32_e32 v167, v55, v167
	ds_write_b128 v209, v[164:167] offset:5120
	v_mul_f32_e32 v168, v56, v168
	v_mul_f32_e32 v169, v56, v169
	v_mul_f32_e32 v170, v56, v170
	v_mul_f32_e32 v171, v56, v171
	ds_write_b128 v209, v[168:171] offset:6144
	v_mul_f32_e32 v172, v57, v172
	v_mul_f32_e32 v173, v57, v173
	v_mul_f32_e32 v174, v57, v174
	v_mul_f32_e32 v175, v57, v175
	ds_write_b128 v209, v[172:175] offset:7168
	s_waitcnt lgkmcnt(0)
	s_barrier
; #define GAS __attribute__((address_space(1)))
; #define LAS __attribute__((address_space(3)))
; #define LDS_WAIT() asm volatile("s_waitcnt lgkmcnt(0)" ::: "memory")
; __device__ __forceinline__ int src_col_in(int c) {
;     if (c < 5120) { const int blk = c >> 7, p = c & 127; const bool rope = blk < 16 || ((((blk - 16) >> 2) & 1) == 0); const int d = rope ? (p >> 1) + 64 * (p & 1) : p; return blk * 128 + d; }
;     if (c < OFF_Z) return c + 2096;
;     if (c < OFF_G) return c - 4048;
;     if (c < OFF_DT) return 5120 + (c - OFF_G);
;     if (c < NSRC) return c;
;     return -1;
; }
;     const int pr = item >> 1, kb = 2 * (pr / nblk) + (item & 1), nb = pr % nblk, k0 = 64 * kb, n0 = 32 * nb;
;     const int nr = n0 + (lane & 31); const int sc = MAP == 1 ? src_col_in(nr) : nr;
;     float v[32];
; #pragma unroll
;     for (int i = 0; i < 32; ++i) v[i] = sc >= 0 ? W[(size_t)(k0 + 2 * i + (lane >> 5)) * Nsrc + sc] : 0.f;
; #pragma unroll
;     for (int i = 0; i < 32; ++i) { const int k = k0 + 2 * i + (lane >> 5); float x = v[i] * wscale; if (KS) x *= (k < ksplit ? ksA[k] : ksB[k - ksplit]); scr[(2 * i + (lane >> 5)) * 33 + (lane & 31)] = x; }
;     LDS_WAIT(); asm volatile("" ::: "memory");
;     const int c = lane & 7;
; #pragma unroll
;     for (int j = 0; j < 4; ++j) { const int n = (lane >> 3) + 8 * j; const LAS float* s = scr + (8 * c) * 33 + n;
;         const unsigned long long o = (unsigned long long)pg8::pk4_fp8(s[0 * 33], s[1 * 33], s[2 * 33], s[3 * 33]) | ((unsigned long long)pg8::pk4_fp8(s[4 * 33], s[5 * 33], s[6 * 33], s[7 * 33]) << 32);
;         *(GAS unsigned long long*)(WT + (size_t)(n0 + n) * K + k0 + 8 * c) = o; }
;     LDS_WAIT(); asm volatile("" ::: "memory");
; }
	s_add_i32 s24, s23, 72
	s_lshl_b32 s20, s24, 7
	s_cmp_lt_u32 s24, 40
	s_cselect_b32 s21, 0, 0x830
	s_cmp_lt_u32 s24, 72
	s_cselect_b32 s21, s21, 0xfffff030
	s_add_i32 s20, s20, s21
	s_lshl_b32 s20, s20, 2
	s_add_u32 s8, s50, s20
	s_addc_u32 s9, s51, 0
	global_load_dwordx4 v[144:147], v76, s[8:9]
	s_add_u32 s8, s8, 0x16280
	s_addc_u32 s9, s9, 0
	global_load_dwordx4 v[148:151], v76, s[8:9]
	s_add_u32 s8, s8, 0x16280
	s_addc_u32 s9, s9, 0
	global_load_dwordx4 v[152:155], v76, s[8:9]
	s_add_u32 s8, s8, 0x16280
	s_addc_u32 s9, s9, 0
	global_load_dwordx4 v[156:159], v76, s[8:9]
	s_add_u32 s8, s8, 0x16280
	s_addc_u32 s9, s9, 0
	global_load_dwordx4 v[160:163], v76, s[8:9]
	s_add_u32 s8, s8, 0x16280
	s_addc_u32 s9, s9, 0
	global_load_dwordx4 v[164:167], v76, s[8:9]
	s_add_u32 s8, s8, 0x16280
	s_addc_u32 s9, s9, 0
	global_load_dwordx4 v[168:171], v76, s[8:9]
	s_add_u32 s8, s8, 0x16280
	s_addc_u32 s9, s9, 0
	global_load_dwordx4 v[172:175], v76, s[8:9]
	s_add_i32 s24, s23, 56
	s_mul_i32 s20, s24, 0x80000
	s_add_u32 s6, s52, s20
	s_addc_u32 s7, s53, 0
	s_cmp_lt_u32 s24, 16
	s_cselect_b32 s20, 1, 0
	s_sub_i32 s21, s24, 16
	s_bitcmp0_b32 s21, 2
	s_cselect_b32 s21, 1, 0
	s_cmp_lt_u32 s24, 40
	s_cselect_b32 s21, s21, 0
	s_or_b32 s20, s20, s21
	s_cmp_lg_u32 s20, 0
	s_cselect_b64 s[20:21], -1, 0
	v_cndmask_b32_e64 v91, v77, v81, s[20:21]
	v_cndmask_b32_e64 v92, v78, v82, s[20:21]
	ds_read_b32 v226, v211
	ds_read_b32 v227, v211 offset:512
	ds_read_b32 v228, v211 offset:1024
	ds_read_b32 v229, v211 offset:1536
	ds_read_b32 v230, v211 offset:2048
	ds_read_b32 v231, v211 offset:2560
	ds_read_b32 v232, v211 offset:3072
	ds_read_b32 v233, v211 offset:3584
	ds_read_b32 v234, v211 offset:4096
	ds_read_b32 v235, v211 offset:4608
	ds_read_b32 v236, v211 offset:5120
	ds_read_b32 v237, v211 offset:5632
	ds_read_b32 v238, v211 offset:6144
	ds_read_b32 v239, v211 offset:6656
	ds_read_b32 v240, v211 offset:7168
	ds_read_b32 v241, v211 offset:7680
	s_waitcnt lgkmcnt(0)
	v_max_f32_e32 v226, v226, v226
	v_max_f32_e32 v227, v227, v227
	v_max_f32_e32 v228, v228, v228
	v_max_f32_e32 v229, v229, v229
	v_max_f32_e32 v230, v230, v230
	v_max_f32_e32 v231, v231, v231
	v_max_f32_e32 v232, v232, v232
	v_max_f32_e32 v233, v233, v233
	v_max_f32_e32 v234, v234, v234
	v_max_f32_e32 v235, v235, v235
	v_max_f32_e32 v236, v236, v236
	v_max_f32_e32 v237, v237, v237
	v_max_f32_e32 v238, v238, v238
	v_max_f32_e32 v239, v239, v239
	v_max_f32_e32 v240, v240, v240
	v_max_f32_e32 v241, v241, v241
	v_med3_f32 v226, v226, s62, v95
	v_med3_f32 v227, v227, s62, v95
	v_med3_f32 v228, v228, s62, v95
	v_med3_f32 v229, v229, s62, v95
	v_med3_f32 v230, v230, s62, v95
	v_med3_f32 v231, v231, s62, v95
	v_med3_f32 v232, v232, s62, v95
	v_med3_f32 v233, v233, s62, v95
	v_med3_f32 v234, v234, s62, v95
	v_med3_f32 v235, v235, s62, v95
	v_med3_f32 v236, v236, s62, v95
	v_med3_f32 v237, v237, s62, v95
	v_med3_f32 v238, v238, s62, v95
	v_med3_f32 v239, v239, s62, v95
	v_med3_f32 v240, v240, s62, v95
	v_med3_f32 v241, v241, s62, v95
	v_mov_b32_e32 v242, 0
	v_mov_b32_e32 v243, 0
	v_mov_b32_e32 v244, 0
	v_mov_b32_e32 v245, 0
	v_cvt_pk_fp8_f32 v242, v226, v227
	v_cvt_pk_fp8_f32 v243, v230, v231
	v_cvt_pk_fp8_f32 v244, v234, v235
	v_cvt_pk_fp8_f32 v245, v238, v239
	v_cvt_pk_fp8_f32 v242, v228, v229 op_sel:[0,0,1]
	v_cvt_pk_fp8_f32 v243, v232, v233 op_sel:[0,0,1]
	v_cvt_pk_fp8_f32 v244, v236, v237 op_sel:[0,0,1]
	v_cvt_pk_fp8_f32 v245, v240, v241 op_sel:[0,0,1]
	s_nop 0
	global_store_dwordx4 v91, v[242:245], s[6:7]
	ds_read_b32 v226, v213
	ds_read_b32 v227, v213 offset:512
	ds_read_b32 v228, v213 offset:1024
	ds_read_b32 v229, v213 offset:1536
	ds_read_b32 v230, v213 offset:2048
	ds_read_b32 v231, v213 offset:2560
	ds_read_b32 v232, v213 offset:3072
	ds_read_b32 v233, v213 offset:3584
	ds_read_b32 v234, v213 offset:4096
	ds_read_b32 v235, v213 offset:4608
	ds_read_b32 v236, v213 offset:5120
	ds_read_b32 v237, v213 offset:5632
	ds_read_b32 v238, v213 offset:6144
	ds_read_b32 v239, v213 offset:6656
	ds_read_b32 v240, v213 offset:7168
	ds_read_b32 v241, v213 offset:7680
	s_waitcnt lgkmcnt(0)
	v_max_f32_e32 v226, v226, v226
	v_max_f32_e32 v227, v227, v227
	v_max_f32_e32 v228, v228, v228
	v_max_f32_e32 v229, v229, v229
	v_max_f32_e32 v230, v230, v230
	v_max_f32_e32 v231, v231, v231
	v_max_f32_e32 v232, v232, v232
	v_max_f32_e32 v233, v233, v233
	v_max_f32_e32 v234, v234, v234
	v_max_f32_e32 v235, v235, v235
	v_max_f32_e32 v236, v236, v236
	v_max_f32_e32 v237, v237, v237
	v_max_f32_e32 v238, v238, v238
	v_max_f32_e32 v239, v239, v239
	v_max_f32_e32 v240, v240, v240
	v_max_f32_e32 v241, v241, v241
	v_med3_f32 v226, v226, s62, v95
	v_med3_f32 v227, v227, s62, v95
	v_med3_f32 v228, v228, s62, v95
	v_med3_f32 v229, v229, s62, v95
	v_med3_f32 v230, v230, s62, v95
	v_med3_f32 v231, v231, s62, v95
	v_med3_f32 v232, v232, s62, v95
	v_med3_f32 v233, v233, s62, v95
	v_med3_f32 v234, v234, s62, v95
	v_med3_f32 v235, v235, s62, v95
	v_med3_f32 v236, v236, s62, v95
	v_med3_f32 v237, v237, s62, v95
	v_med3_f32 v238, v238, s62, v95
	v_med3_f32 v239, v239, s62, v95
	v_med3_f32 v240, v240, s62, v95
	v_med3_f32 v241, v241, s62, v95
	v_mov_b32_e32 v242, 0
	v_mov_b32_e32 v243, 0
	v_mov_b32_e32 v244, 0
	v_mov_b32_e32 v245, 0
	v_cvt_pk_fp8_f32 v242, v226, v227
	v_cvt_pk_fp8_f32 v243, v230, v231
	v_cvt_pk_fp8_f32 v244, v234, v235
	v_cvt_pk_fp8_f32 v245, v238, v239
	v_cvt_pk_fp8_f32 v242, v228, v229 op_sel:[0,0,1]
	v_cvt_pk_fp8_f32 v243, v232, v233 op_sel:[0,0,1]
	v_cvt_pk_fp8_f32 v244, v236, v237 op_sel:[0,0,1]
	v_cvt_pk_fp8_f32 v245, v240, v241 op_sel:[0,0,1]
	s_nop 0
	global_store_dwordx4 v92, v[242:245], s[6:7]
	s_waitcnt vmcnt(12)
	v_mul_f32_e32 v176, v50, v176
	v_mul_f32_e32 v177, v50, v177
	v_mul_f32_e32 v178, v50, v178
	v_mul_f32_e32 v179, v50, v179
	ds_write_b128 v210, v[176:179]
	v_mul_f32_e32 v180, v51, v180
	v_mul_f32_e32 v181, v51, v181
	v_mul_f32_e32 v182, v51, v182
	v_mul_f32_e32 v183, v51, v183
	ds_write_b128 v210, v[180:183] offset:1024
	v_mul_f32_e32 v184, v52, v184
	v_mul_f32_e32 v185, v52, v185
	v_mul_f32_e32 v186, v52, v186
	v_mul_f32_e32 v187, v52, v187
	ds_write_b128 v210, v[184:187] offset:2048
	v_mul_f32_e32 v188, v53, v188
	v_mul_f32_e32 v189, v53, v189
	v_mul_f32_e32 v190, v53, v190
	v_mul_f32_e32 v191, v53, v191
	ds_write_b128 v210, v[188:191] offset:3072
	v_mul_f32_e32 v192, v54, v192
	v_mul_f32_e32 v193, v54, v193
	v_mul_f32_e32 v194, v54, v194
	v_mul_f32_e32 v195, v54, v195
	ds_write_b128 v210, v[192:195] offset:4096
	v_mul_f32_e32 v196, v55, v196
	v_mul_f32_e32 v197, v55, v197
	v_mul_f32_e32 v198, v55, v198
	v_mul_f32_e32 v199, v55, v199
	ds_write_b128 v210, v[196:199] offset:5120
	v_mul_f32_e32 v200, v56, v200
	v_mul_f32_e32 v201, v56, v201
	v_mul_f32_e32 v202, v56, v202
	v_mul_f32_e32 v203, v56, v203
	ds_write_b128 v210, v[200:203] offset:6144
	v_mul_f32_e32 v204, v57, v204
	v_mul_f32_e32 v205, v57, v205
	v_mul_f32_e32 v206, v57, v206
	v_mul_f32_e32 v207, v57, v207
	ds_write_b128 v210, v[204:207] offset:7168
	s_waitcnt lgkmcnt(0)
	s_barrier
; #define GAS __attribute__((address_space(1)))
; #define LAS __attribute__((address_space(3)))
; #define LDS_WAIT() asm volatile("s_waitcnt lgkmcnt(0)" ::: "memory")
; __device__ __forceinline__ int src_col_in(int c) {
;     if (c < 5120) { const int blk = c >> 7, p = c & 127; const bool rope = blk < 16 || ((((blk - 16) >> 2) & 1) == 0); const int d = rope ? (p >> 1) + 64 * (p & 1) : p; return blk * 128 + d; }
;     if (c < OFF_Z) return c + 2096;
;     if (c < OFF_G) return c - 4048;
;     if (c < OFF_DT) return 5120 + (c - OFF_G);
;     if (c < NSRC) return c;
;     return -1;
; }
;     const int pr = item >> 1, kb = 2 * (pr / nblk) + (item & 1), nb = pr % nblk, k0 = 64 * kb, n0 = 32 * nb;
;     const int nr = n0 + (lane & 31); const int sc = MAP == 1 ? src_col_in(nr) : nr;
;     float v[32];
; #pragma unroll
;     for (int i = 0; i < 32; ++i) v[i] = sc >= 0 ? W[(size_t)(k0 + 2 * i + (lane >> 5)) * Nsrc + sc] : 0.f;
; #pragma unroll
;     for (int i = 0; i < 32; ++i) { const int k = k0 + 2 * i + (lane >> 5); float x = v[i] * wscale; if (KS) x *= (k < ksplit ? ksA[k] : ksB[k - ksplit]); scr[(2 * i + (lane >> 5)) * 33 + (lane & 31)] = x; }
;     LDS_WAIT(); asm volatile("" ::: "memory");
;     const int c = lane & 7;
; #pragma unroll
;     for (int j = 0; j < 4; ++j) { const int n = (lane >> 3) + 8 * j; const LAS float* s = scr + (8 * c) * 33 + n;
;         const unsigned long long o = (unsigned long long)pg8::pk4_fp8(s[0 * 33], s[1 * 33], s[2 * 33], s[3 * 33]) | ((unsigned long long)pg8::pk4_fp8(s[4 * 33], s[5 * 33], s[6 * 33], s[7 * 33]) << 32);
;         *(GAS unsigned long long*)(WT + (size_t)(n0 + n) * K + k0 + 8 * c) = o; }
;     LDS_WAIT(); asm volatile("" ::: "memory");
; }
	s_add_i32 s24, s23, 80
	s_lshl_b32 s20, s24, 7
	s_cmp_lt_u32 s24, 40
	s_cselect_b32 s21, 0, 0x830
	s_cmp_lt_u32 s24, 72
	s_cselect_b32 s21, s21, 0xfffff030
	s_add_i32 s20, s20, s21
	s_lshl_b32 s20, s20, 2
	s_add_u32 s8, s50, s20
	s_addc_u32 s9, s51, 0
	global_load_dwordx4 v[176:179], v76, s[8:9]
	s_add_u32 s8, s8, 0x16280
	s_addc_u32 s9, s9, 0
	global_load_dwordx4 v[180:183], v76, s[8:9]
	s_add_u32 s8, s8, 0x16280
	s_addc_u32 s9, s9, 0
	global_load_dwordx4 v[184:187], v76, s[8:9]
	s_add_u32 s8, s8, 0x16280
	s_addc_u32 s9, s9, 0
	global_load_dwordx4 v[188:191], v76, s[8:9]
	s_add_u32 s8, s8, 0x16280
	s_addc_u32 s9, s9, 0
	global_load_dwordx4 v[192:195], v76, s[8:9]
	s_add_u32 s8, s8, 0x16280
	s_addc_u32 s9, s9, 0
	global_load_dwordx4 v[196:199], v76, s[8:9]
	s_add_u32 s8, s8, 0x16280
	s_addc_u32 s9, s9, 0
	global_load_dwordx4 v[200:203], v76, s[8:9]
	s_add_u32 s8, s8, 0x16280
	s_addc_u32 s9, s9, 0
	global_load_dwordx4 v[204:207], v76, s[8:9]
	s_add_i32 s24, s23, 64
	s_mul_i32 s20, s24, 0x80000
	s_add_u32 s6, s52, s20
	s_addc_u32 s7, s53, 0
	s_cmp_lt_u32 s24, 16
	s_cselect_b32 s20, 1, 0
	s_sub_i32 s21, s24, 16
	s_bitcmp0_b32 s21, 2
	s_cselect_b32 s21, 1, 0
	s_cmp_lt_u32 s24, 40
	s_cselect_b32 s21, s21, 0
	s_or_b32 s20, s20, s21
	s_cmp_lg_u32 s20, 0
	s_cselect_b64 s[20:21], -1, 0
	v_cndmask_b32_e64 v91, v77, v81, s[20:21]
	v_cndmask_b32_e64 v92, v78, v82, s[20:21]
	ds_read_b32 v226, v212
	ds_read_b32 v227, v212 offset:512
	ds_read_b32 v228, v212 offset:1024
	ds_read_b32 v229, v212 offset:1536
	ds_read_b32 v230, v212 offset:2048
	ds_read_b32 v231, v212 offset:2560
	ds_read_b32 v232, v212 offset:3072
	ds_read_b32 v233, v212 offset:3584
	ds_read_b32 v234, v212 offset:4096
	ds_read_b32 v235, v212 offset:4608
	ds_read_b32 v236, v212 offset:5120
	ds_read_b32 v237, v212 offset:5632
	ds_read_b32 v238, v212 offset:6144
	ds_read_b32 v239, v212 offset:6656
	ds_read_b32 v240, v212 offset:7168
	ds_read_b32 v241, v212 offset:7680
	s_waitcnt lgkmcnt(0)
	v_max_f32_e32 v226, v226, v226
	v_max_f32_e32 v227, v227, v227
	v_max_f32_e32 v228, v228, v228
	v_max_f32_e32 v229, v229, v229
	v_max_f32_e32 v230, v230, v230
	v_max_f32_e32 v231, v231, v231
	v_max_f32_e32 v232, v232, v232
	v_max_f32_e32 v233, v233, v233
	v_max_f32_e32 v234, v234, v234
	v_max_f32_e32 v235, v235, v235
	v_max_f32_e32 v236, v236, v236
	v_max_f32_e32 v237, v237, v237
	v_max_f32_e32 v238, v238, v238
	v_max_f32_e32 v239, v239, v239
	v_max_f32_e32 v240, v240, v240
	v_max_f32_e32 v241, v241, v241
	v_med3_f32 v226, v226, s62, v95
	v_med3_f32 v227, v227, s62, v95
	v_med3_f32 v228, v228, s62, v95
	v_med3_f32 v229, v229, s62, v95
	v_med3_f32 v230, v230, s62, v95
	v_med3_f32 v231, v231, s62, v95
	v_med3_f32 v232, v232, s62, v95
	v_med3_f32 v233, v233, s62, v95
	v_med3_f32 v234, v234, s62, v95
	v_med3_f32 v235, v235, s62, v95
	v_med3_f32 v236, v236, s62, v95
	v_med3_f32 v237, v237, s62, v95
	v_med3_f32 v238, v238, s62, v95
	v_med3_f32 v239, v239, s62, v95
	v_med3_f32 v240, v240, s62, v95
	v_med3_f32 v241, v241, s62, v95
	v_mov_b32_e32 v242, 0
	v_mov_b32_e32 v243, 0
	v_mov_b32_e32 v244, 0
	v_mov_b32_e32 v245, 0
	v_cvt_pk_fp8_f32 v242, v226, v227
	v_cvt_pk_fp8_f32 v243, v230, v231
	v_cvt_pk_fp8_f32 v244, v234, v235
	v_cvt_pk_fp8_f32 v245, v238, v239
	v_cvt_pk_fp8_f32 v242, v228, v229 op_sel:[0,0,1]
	v_cvt_pk_fp8_f32 v243, v232, v233 op_sel:[0,0,1]
	v_cvt_pk_fp8_f32 v244, v236, v237 op_sel:[0,0,1]
	v_cvt_pk_fp8_f32 v245, v240, v241 op_sel:[0,0,1]
	s_nop 0
	global_store_dwordx4 v91, v[242:245], s[6:7]
	ds_read_b32 v226, v214
	ds_read_b32 v227, v214 offset:512
	ds_read_b32 v228, v214 offset:1024
	ds_read_b32 v229, v214 offset:1536
	ds_read_b32 v230, v214 offset:2048
	ds_read_b32 v231, v214 offset:2560
	ds_read_b32 v232, v214 offset:3072
	ds_read_b32 v233, v214 offset:3584
	ds_read_b32 v234, v214 offset:4096
	ds_read_b32 v235, v214 offset:4608
	ds_read_b32 v236, v214 offset:5120
	ds_read_b32 v237, v214 offset:5632
	ds_read_b32 v238, v214 offset:6144
	ds_read_b32 v239, v214 offset:6656
	ds_read_b32 v240, v214 offset:7168
	ds_read_b32 v241, v214 offset:7680
	s_waitcnt lgkmcnt(0)
	v_max_f32_e32 v226, v226, v226
	v_max_f32_e32 v227, v227, v227
	v_max_f32_e32 v228, v228, v228
	v_max_f32_e32 v229, v229, v229
	v_max_f32_e32 v230, v230, v230
	v_max_f32_e32 v231, v231, v231
	v_max_f32_e32 v232, v232, v232
	v_max_f32_e32 v233, v233, v233
	v_max_f32_e32 v234, v234, v234
	v_max_f32_e32 v235, v235, v235
	v_max_f32_e32 v236, v236, v236
	v_max_f32_e32 v237, v237, v237
	v_max_f32_e32 v238, v238, v238
	v_max_f32_e32 v239, v239, v239
	v_max_f32_e32 v240, v240, v240
	v_max_f32_e32 v241, v241, v241
	v_med3_f32 v226, v226, s62, v95
	v_med3_f32 v227, v227, s62, v95
	v_med3_f32 v228, v228, s62, v95
	v_med3_f32 v229, v229, s62, v95
	v_med3_f32 v230, v230, s62, v95
	v_med3_f32 v231, v231, s62, v95
	v_med3_f32 v232, v232, s62, v95
	v_med3_f32 v233, v233, s62, v95
	v_med3_f32 v234, v234, s62, v95
	v_med3_f32 v235, v235, s62, v95
	v_med3_f32 v236, v236, s62, v95
	v_med3_f32 v237, v237, s62, v95
	v_med3_f32 v238, v238, s62, v95
	v_med3_f32 v239, v239, s62, v95
	v_med3_f32 v240, v240, s62, v95
	v_med3_f32 v241, v241, s62, v95
	v_mov_b32_e32 v242, 0
	v_mov_b32_e32 v243, 0
	v_mov_b32_e32 v244, 0
	v_mov_b32_e32 v245, 0
	v_cvt_pk_fp8_f32 v242, v226, v227
	v_cvt_pk_fp8_f32 v243, v230, v231
	v_cvt_pk_fp8_f32 v244, v234, v235
	v_cvt_pk_fp8_f32 v245, v238, v239
	v_cvt_pk_fp8_f32 v242, v228, v229 op_sel:[0,0,1]
	v_cvt_pk_fp8_f32 v243, v232, v233 op_sel:[0,0,1]
	v_cvt_pk_fp8_f32 v244, v236, v237 op_sel:[0,0,1]
	v_cvt_pk_fp8_f32 v245, v240, v241 op_sel:[0,0,1]
	s_nop 0
	global_store_dwordx4 v92, v[242:245], s[6:7]
	s_waitcnt vmcnt(12)
	v_mul_f32_e32 v144, v50, v144
	v_mul_f32_e32 v145, v50, v145
	v_mul_f32_e32 v146, v50, v146
	v_mul_f32_e32 v147, v50, v147
	ds_write_b128 v209, v[144:147]
	v_mul_f32_e32 v148, v51, v148
	v_mul_f32_e32 v149, v51, v149
	v_mul_f32_e32 v150, v51, v150
	v_mul_f32_e32 v151, v51, v151
	ds_write_b128 v209, v[148:151] offset:1024
	v_mul_f32_e32 v152, v52, v152
	v_mul_f32_e32 v153, v52, v153
	v_mul_f32_e32 v154, v52, v154
	v_mul_f32_e32 v155, v52, v155
	ds_write_b128 v209, v[152:155] offset:2048
	v_mul_f32_e32 v156, v53, v156
	v_mul_f32_e32 v157, v53, v157
	v_mul_f32_e32 v158, v53, v158
	v_mul_f32_e32 v159, v53, v159
	ds_write_b128 v209, v[156:159] offset:3072
	v_mul_f32_e32 v160, v54, v160
	v_mul_f32_e32 v161, v54, v161
	v_mul_f32_e32 v162, v54, v162
	v_mul_f32_e32 v163, v54, v163
	ds_write_b128 v209, v[160:163] offset:4096
	v_mul_f32_e32 v164, v55, v164
	v_mul_f32_e32 v165, v55, v165
	v_mul_f32_e32 v166, v55, v166
	v_mul_f32_e32 v167, v55, v167
	ds_write_b128 v209, v[164:167] offset:5120
	v_mul_f32_e32 v168, v56, v168
	v_mul_f32_e32 v169, v56, v169
	v_mul_f32_e32 v170, v56, v170
	v_mul_f32_e32 v171, v56, v171
	ds_write_b128 v209, v[168:171] offset:6144
	v_mul_f32_e32 v172, v57, v172
	v_mul_f32_e32 v173, v57, v173
	v_mul_f32_e32 v174, v57, v174
	v_mul_f32_e32 v175, v57, v175
	ds_write_b128 v209, v[172:175] offset:7168
	s_waitcnt lgkmcnt(0)
	s_barrier
; template <int MAP, bool KS, bool KPERM = false>
; __device__ __forceinline__ void p0_transpose_item(const float* W, int K, int Nsrc, int nblk, bf16* WT, const float* ksA, const float* ksB, int ksplit, LAS float* scr, int item, int lane) {
;     const int kb = item / nblk, nb = item % nblk, k0 = 64 * kb, n0 = 32 * nb;
;     const int nr = n0 + (lane & 31); const int sc = MAP == 1 ? src_col_in(nr) : (MAP == 2 ? nat_dim(nr) : nr);
;     float v[32];
; #pragma unroll
;     for (int i = 0; i < 32; ++i) { const int k = k0 + 2 * i + (lane >> 5); const int ksrc = KPERM ? ((k & ~127) + nat_dim(k & 127)) : k;
;         v[i] = sc >= 0 ? W[(size_t)ksrc * Nsrc + sc] : 0.f; }
; #pragma unroll
;     for (int i = 0; i < 32; ++i) { const int kk = 2 * i + (lane >> 5); const int k = k0 + kk;
;         if (KS) v[i] *= (k < ksplit ? ksA[k] : ksB[k - ksplit]);
;         scr[kk * 33 + (lane & 31)] = v[i]; }
;     LDS_WAIT(); asm volatile("" ::: "memory");
;     const int c = lane & 7;
; #pragma unroll
;     for (int j = 0; j < 4; ++j) { const int n = (lane >> 3) + 8 * j; const LAS float* s = scr + (8 * c) * 33 + n;
;         v4u o; o.x = pk2(s[0 * 33], s[1 * 33]); o.y = pk2(s[2 * 33], s[3 * 33]); o.z = pk2(s[4 * 33], s[5 * 33]); o.w = pk2(s[6 * 33], s[7 * 33]);
;     const int pr = item >> 1, kb = 2 * (pr / nblk) + (item & 1), nb = pr % nblk, k0 = 64 * kb, n0 = 32 * nb;
;     const int nr = n0 + (lane & 31); const int sc = MAP == 1 ? src_col_in(nr) : nr;
;     float v[32];
; #pragma unroll
;     for (int i = 0; i < 32; ++i) v[i] = sc >= 0 ? W[(size_t)(k0 + 2 * i + (lane >> 5)) * Nsrc + sc] : 0.f;
; #pragma unroll
;     for (int i = 0; i < 32; ++i) { const int k = k0 + 2 * i + (lane >> 5); float x = v[i] * wscale; if (KS) x *= (k < ksplit ? ksA[k] : ksB[k - ksplit]); scr[(2 * i + (lane >> 5)) * 33 + (lane & 31)] = x; }
;     LDS_WAIT(); asm volatile("" ::: "memory");
;     const int c = lane & 7;
; #pragma unroll
;     for (int j = 0; j < 4; ++j) { const int n = (lane >> 3) + 8 * j; const LAS float* s = scr + (8 * c) * 33 + n;
;         const unsigned long long o = (unsigned long long)pg8::pk4_fp8(s[0 * 33], s[1 * 33], s[2 * 33], s[3 * 33]) | ((unsigned long long)pg8::pk4_fp8(s[4 * 33], s[5 * 33], s[6 * 33], s[7 * 33]) << 32);
;         *(GAS unsigned long long*)(WT + (size_t)(n0 + n) * K + k0 + 8 * c) = o; }
;     LDS_WAIT(); asm volatile("" ::: "memory");
; }
	s_mov_b64 s[8:9], s[54:55]
	global_load_dwordx4 v[144:147], v75, s[8:9]
	s_add_u32 s8, s8, 0x8000
	s_addc_u32 s9, s9, 0
	global_load_dwordx4 v[148:151], v75, s[8:9]
	s_add_u32 s8, s8, 0x8000
	s_addc_u32 s9, s9, 0
	global_load_dwordx4 v[152:155], v75, s[8:9]
	s_add_u32 s8, s8, 0x8000
	s_addc_u32 s9, s9, 0
	global_load_dwordx4 v[156:159], v75, s[8:9]
	s_add_u32 s8, s8, 0x8000
	s_addc_u32 s9, s9, 0
	global_load_dwordx4 v[160:163], v75, s[8:9]
	s_add_u32 s8, s8, 0x8000
	s_addc_u32 s9, s9, 0
	global_load_dwordx4 v[164:167], v75, s[8:9]
	s_add_u32 s8, s8, 0x8000
	s_addc_u32 s9, s9, 0
	global_load_dwordx4 v[168:171], v75, s[8:9]
	s_add_u32 s8, s8, 0x8000
	s_addc_u32 s9, s9, 0
	global_load_dwordx4 v[172:175], v75, s[8:9]
	s_add_i32 s24, s23, 72
	s_mul_i32 s20, s24, 0x80000
	s_add_u32 s6, s52, s20
	s_addc_u32 s7, s53, 0
	s_cmp_lt_u32 s24, 16
	s_cselect_b32 s20, 1, 0
	s_sub_i32 s21, s24, 16
	s_bitcmp0_b32 s21, 2
	s_cselect_b32 s21, 1, 0
	s_cmp_lt_u32 s24, 40
	s_cselect_b32 s21, s21, 0
	s_or_b32 s20, s20, s21
	s_cmp_lg_u32 s20, 0
	s_cselect_b64 s[20:21], -1, 0
	v_cndmask_b32_e64 v91, v77, v81, s[20:21]
	v_cndmask_b32_e64 v92, v78, v82, s[20:21]
	ds_read_b32 v226, v211
	ds_read_b32 v227, v211 offset:512
	ds_read_b32 v228, v211 offset:1024
	ds_read_b32 v229, v211 offset:1536
	ds_read_b32 v230, v211 offset:2048
	ds_read_b32 v231, v211 offset:2560
	ds_read_b32 v232, v211 offset:3072
	ds_read_b32 v233, v211 offset:3584
	ds_read_b32 v234, v211 offset:4096
	ds_read_b32 v235, v211 offset:4608
	ds_read_b32 v236, v211 offset:5120
	ds_read_b32 v237, v211 offset:5632
	ds_read_b32 v238, v211 offset:6144
	ds_read_b32 v239, v211 offset:6656
	ds_read_b32 v240, v211 offset:7168
	ds_read_b32 v241, v211 offset:7680
	s_waitcnt lgkmcnt(0)
	v_max_f32_e32 v226, v226, v226
	v_max_f32_e32 v227, v227, v227
	v_max_f32_e32 v228, v228, v228
	v_max_f32_e32 v229, v229, v229
	v_max_f32_e32 v230, v230, v230
	v_max_f32_e32 v231, v231, v231
	v_max_f32_e32 v232, v232, v232
	v_max_f32_e32 v233, v233, v233
	v_max_f32_e32 v234, v234, v234
	v_max_f32_e32 v235, v235, v235
	v_max_f32_e32 v236, v236, v236
	v_max_f32_e32 v237, v237, v237
	v_max_f32_e32 v238, v238, v238
	v_max_f32_e32 v239, v239, v239
	v_max_f32_e32 v240, v240, v240
	v_max_f32_e32 v241, v241, v241
	v_med3_f32 v226, v226, s62, v95
	v_med3_f32 v227, v227, s62, v95
	v_med3_f32 v228, v228, s62, v95
	v_med3_f32 v229, v229, s62, v95
	v_med3_f32 v230, v230, s62, v95
	v_med3_f32 v231, v231, s62, v95
	v_med3_f32 v232, v232, s62, v95
	v_med3_f32 v233, v233, s62, v95
	v_med3_f32 v234, v234, s62, v95
	v_med3_f32 v235, v235, s62, v95
	v_med3_f32 v236, v236, s62, v95
	v_med3_f32 v237, v237, s62, v95
	v_med3_f32 v238, v238, s62, v95
	v_med3_f32 v239, v239, s62, v95
	v_med3_f32 v240, v240, s62, v95
	v_med3_f32 v241, v241, s62, v95
	v_mov_b32_e32 v242, 0
	v_mov_b32_e32 v243, 0
	v_mov_b32_e32 v244, 0
	v_mov_b32_e32 v245, 0
	v_cvt_pk_fp8_f32 v242, v226, v227
	v_cvt_pk_fp8_f32 v243, v230, v231
	v_cvt_pk_fp8_f32 v244, v234, v235
	v_cvt_pk_fp8_f32 v245, v238, v239
	v_cvt_pk_fp8_f32 v242, v228, v229 op_sel:[0,0,1]
	v_cvt_pk_fp8_f32 v243, v232, v233 op_sel:[0,0,1]
	v_cvt_pk_fp8_f32 v244, v236, v237 op_sel:[0,0,1]
	v_cvt_pk_fp8_f32 v245, v240, v241 op_sel:[0,0,1]
	s_nop 0
	global_store_dwordx4 v91, v[242:245], s[6:7]
	ds_read_b32 v226, v213
	ds_read_b32 v227, v213 offset:512
	ds_read_b32 v228, v213 offset:1024
	ds_read_b32 v229, v213 offset:1536
	ds_read_b32 v230, v213 offset:2048
	ds_read_b32 v231, v213 offset:2560
	ds_read_b32 v232, v213 offset:3072
	ds_read_b32 v233, v213 offset:3584
	ds_read_b32 v234, v213 offset:4096
	ds_read_b32 v235, v213 offset:4608
	ds_read_b32 v236, v213 offset:5120
	ds_read_b32 v237, v213 offset:5632
	ds_read_b32 v238, v213 offset:6144
	ds_read_b32 v239, v213 offset:6656
	ds_read_b32 v240, v213 offset:7168
	ds_read_b32 v241, v213 offset:7680
	s_waitcnt lgkmcnt(0)
	v_max_f32_e32 v226, v226, v226
	v_max_f32_e32 v227, v227, v227
	v_max_f32_e32 v228, v228, v228
	v_max_f32_e32 v229, v229, v229
	v_max_f32_e32 v230, v230, v230
	v_max_f32_e32 v231, v231, v231
	v_max_f32_e32 v232, v232, v232
	v_max_f32_e32 v233, v233, v233
	v_max_f32_e32 v234, v234, v234
	v_max_f32_e32 v235, v235, v235
	v_max_f32_e32 v236, v236, v236
	v_max_f32_e32 v237, v237, v237
	v_max_f32_e32 v238, v238, v238
	v_max_f32_e32 v239, v239, v239
	v_max_f32_e32 v240, v240, v240
	v_max_f32_e32 v241, v241, v241
	v_med3_f32 v226, v226, s62, v95
	v_med3_f32 v227, v227, s62, v95
	v_med3_f32 v228, v228, s62, v95
	v_med3_f32 v229, v229, s62, v95
	v_med3_f32 v230, v230, s62, v95
	v_med3_f32 v231, v231, s62, v95
	v_med3_f32 v232, v232, s62, v95
	v_med3_f32 v233, v233, s62, v95
	v_med3_f32 v234, v234, s62, v95
	v_med3_f32 v235, v235, s62, v95
	v_med3_f32 v236, v236, s62, v95
	v_med3_f32 v237, v237, s62, v95
	v_med3_f32 v238, v238, s62, v95
	v_med3_f32 v239, v239, s62, v95
	v_med3_f32 v240, v240, s62, v95
	v_med3_f32 v241, v241, s62, v95
	v_mov_b32_e32 v242, 0
	v_mov_b32_e32 v243, 0
	v_mov_b32_e32 v244, 0
	v_mov_b32_e32 v245, 0
	v_cvt_pk_fp8_f32 v242, v226, v227
	v_cvt_pk_fp8_f32 v243, v230, v231
	v_cvt_pk_fp8_f32 v244, v234, v235
	v_cvt_pk_fp8_f32 v245, v238, v239
	v_cvt_pk_fp8_f32 v242, v228, v229 op_sel:[0,0,1]
	v_cvt_pk_fp8_f32 v243, v232, v233 op_sel:[0,0,1]
	v_cvt_pk_fp8_f32 v244, v236, v237 op_sel:[0,0,1]
	v_cvt_pk_fp8_f32 v245, v240, v241 op_sel:[0,0,1]
	s_nop 0
	global_store_dwordx4 v92, v[242:245], s[6:7]
	s_waitcnt vmcnt(12)
	v_mul_f32_e32 v176, v50, v176
	v_mul_f32_e32 v177, v50, v177
	v_mul_f32_e32 v178, v50, v178
	v_mul_f32_e32 v179, v50, v179
	ds_write_b128 v210, v[176:179]
	v_mul_f32_e32 v180, v51, v180
	v_mul_f32_e32 v181, v51, v181
	v_mul_f32_e32 v182, v51, v182
	v_mul_f32_e32 v183, v51, v183
	ds_write_b128 v210, v[180:183] offset:1024
	v_mul_f32_e32 v184, v52, v184
	v_mul_f32_e32 v185, v52, v185
	v_mul_f32_e32 v186, v52, v186
	v_mul_f32_e32 v187, v52, v187
	ds_write_b128 v210, v[184:187] offset:2048
	v_mul_f32_e32 v188, v53, v188
	v_mul_f32_e32 v189, v53, v189
	v_mul_f32_e32 v190, v53, v190
	v_mul_f32_e32 v191, v53, v191
	ds_write_b128 v210, v[188:191] offset:3072
	v_mul_f32_e32 v192, v54, v192
	v_mul_f32_e32 v193, v54, v193
	v_mul_f32_e32 v194, v54, v194
	v_mul_f32_e32 v195, v54, v195
	ds_write_b128 v210, v[192:195] offset:4096
	v_mul_f32_e32 v196, v55, v196
	v_mul_f32_e32 v197, v55, v197
	v_mul_f32_e32 v198, v55, v198
	v_mul_f32_e32 v199, v55, v199
	ds_write_b128 v210, v[196:199] offset:5120
	v_mul_f32_e32 v200, v56, v200
	v_mul_f32_e32 v201, v56, v201
	v_mul_f32_e32 v202, v56, v202
	v_mul_f32_e32 v203, v56, v203
	ds_write_b128 v210, v[200:203] offset:6144
	v_mul_f32_e32 v204, v57, v204
	v_mul_f32_e32 v205, v57, v205
	v_mul_f32_e32 v206, v57, v206
	v_mul_f32_e32 v207, v57, v207
	ds_write_b128 v210, v[204:207] offset:7168
	s_waitcnt lgkmcnt(0)
	s_barrier
; template <int MAP, bool KS, bool KPERM = false>
; __device__ __forceinline__ void p0_transpose_item(const float* W, int K, int Nsrc, int nblk, bf16* WT, const float* ksA, const float* ksB, int ksplit, LAS float* scr, int item, int lane) {
;     const int kb = item / nblk, nb = item % nblk, k0 = 64 * kb, n0 = 32 * nb;
;     const int nr = n0 + (lane & 31); const int sc = MAP == 1 ? src_col_in(nr) : (MAP == 2 ? nat_dim(nr) : nr);
;     float v[32];
; #pragma unroll
;     for (int i = 0; i < 32; ++i) { const int k = k0 + 2 * i + (lane >> 5); const int ksrc = KPERM ? ((k & ~127) + nat_dim(k & 127)) : k;
;         v[i] = sc >= 0 ? W[(size_t)ksrc * Nsrc + sc] : 0.f; }
; #pragma unroll
;     for (int i = 0; i < 32; ++i) { const int kk = 2 * i + (lane >> 5); const int k = k0 + kk;
;         if (KS) v[i] *= (k < ksplit ? ksA[k] : ksB[k - ksplit]);
;         scr[kk * 33 + (lane & 31)] = v[i]; }
;     LDS_WAIT(); asm volatile("" ::: "memory");
;     const int c = lane & 7;
; #pragma unroll
;     for (int j = 0; j < 4; ++j) { const int n = (lane >> 3) + 8 * j; const LAS float* s = scr + (8 * c) * 33 + n;
;         v4u o; o.x = pk2(s[0 * 33], s[1 * 33]); o.y = pk2(s[2 * 33], s[3 * 33]); o.z = pk2(s[4 * 33], s[5 * 33]); o.w = pk2(s[6 * 33], s[7 * 33]);
;     const int pr = item >> 1, kb = 2 * (pr / nblk) + (item & 1), nb = pr % nblk, k0 = 64 * kb, n0 = 32 * nb;
;     const int nr = n0 + (lane & 31); const int sc = MAP == 1 ? src_col_in(nr) : nr;
;     float v[32];
; #pragma unroll
;     for (int i = 0; i < 32; ++i) v[i] = sc >= 0 ? W[(size_t)(k0 + 2 * i + (lane >> 5)) * Nsrc + sc] : 0.f;
; #pragma unroll
;     for (int i = 0; i < 32; ++i) { const int k = k0 + 2 * i + (lane >> 5); float x = v[i] * wscale; if (KS) x *= (k < ksplit ? ksA[k] : ksB[k - ksplit]); scr[(2 * i + (lane >> 5)) * 33 + (lane & 31)] = x; }
;     LDS_WAIT(); asm volatile("" ::: "memory");
;     const int c = lane & 7;
; #pragma unroll
;     for (int j = 0; j < 4; ++j) { const int n = (lane >> 3) + 8 * j; const LAS float* s = scr + (8 * c) * 33 + n;
;         const unsigned long long o = (unsigned long long)pg8::pk4_fp8(s[0 * 33], s[1 * 33], s[2 * 33], s[3 * 33]) | ((unsigned long long)pg8::pk4_fp8(s[4 * 33], s[5 * 33], s[6 * 33], s[7 * 33]) << 32);
;         *(GAS unsigned long long*)(WT + (size_t)(n0 + n) * K + k0 + 8 * c) = o; }
;     LDS_WAIT(); asm volatile("" ::: "memory");
; }
	s_add_u32 s8, s54, 0x1000
	s_addc_u32 s9, s55, 0
	global_load_dwordx4 v[176:179], v75, s[8:9]
	s_add_u32 s8, s8, 0x8000
	s_addc_u32 s9, s9, 0
	global_load_dwordx4 v[180:183], v75, s[8:9]
	s_add_u32 s8, s8, 0x8000
	s_addc_u32 s9, s9, 0
	global_load_dwordx4 v[184:187], v75, s[8:9]
	s_add_u32 s8, s8, 0x8000
	s_addc_u32 s9, s9, 0
	global_load_dwordx4 v[188:191], v75, s[8:9]
	s_add_u32 s8, s8, 0x8000
	s_addc_u32 s9, s9, 0
	global_load_dwordx4 v[192:195], v75, s[8:9]
	s_add_u32 s8, s8, 0x8000
	s_addc_u32 s9, s9, 0
	global_load_dwordx4 v[196:199], v75, s[8:9]
	s_add_u32 s8, s8, 0x8000
	s_addc_u32 s9, s9, 0
	global_load_dwordx4 v[200:203], v75, s[8:9]
	s_add_u32 s8, s8, 0x8000
	s_addc_u32 s9, s9, 0
	global_load_dwordx4 v[204:207], v75, s[8:9]
	s_add_i32 s24, s23, 80
	s_mul_i32 s20, s24, 0x80000
	s_add_u32 s6, s52, s20
	s_addc_u32 s7, s53, 0
	s_cmp_lt_u32 s24, 16
	s_cselect_b32 s20, 1, 0
	s_sub_i32 s21, s24, 16
	s_bitcmp0_b32 s21, 2
	s_cselect_b32 s21, 1, 0
	s_cmp_lt_u32 s24, 40
	s_cselect_b32 s21, s21, 0
	s_or_b32 s20, s20, s21
	s_cmp_lg_u32 s20, 0
	s_cselect_b64 s[20:21], -1, 0
	v_cndmask_b32_e64 v91, v77, v81, s[20:21]
	v_cndmask_b32_e64 v92, v78, v82, s[20:21]
	ds_read_b32 v226, v212
	ds_read_b32 v227, v212 offset:512
	ds_read_b32 v228, v212 offset:1024
	ds_read_b32 v229, v212 offset:1536
	ds_read_b32 v230, v212 offset:2048
	ds_read_b32 v231, v212 offset:2560
	ds_read_b32 v232, v212 offset:3072
	ds_read_b32 v233, v212 offset:3584
	ds_read_b32 v234, v212 offset:4096
	ds_read_b32 v235, v212 offset:4608
	ds_read_b32 v236, v212 offset:5120
	ds_read_b32 v237, v212 offset:5632
	ds_read_b32 v238, v212 offset:6144
	ds_read_b32 v239, v212 offset:6656
	ds_read_b32 v240, v212 offset:7168
	ds_read_b32 v241, v212 offset:7680
	s_waitcnt lgkmcnt(0)
	v_max_f32_e32 v226, v226, v226
	v_max_f32_e32 v227, v227, v227
	v_max_f32_e32 v228, v228, v228
	v_max_f32_e32 v229, v229, v229
	v_max_f32_e32 v230, v230, v230
	v_max_f32_e32 v231, v231, v231
	v_max_f32_e32 v232, v232, v232
	v_max_f32_e32 v233, v233, v233
	v_max_f32_e32 v234, v234, v234
	v_max_f32_e32 v235, v235, v235
	v_max_f32_e32 v236, v236, v236
	v_max_f32_e32 v237, v237, v237
	v_max_f32_e32 v238, v238, v238
	v_max_f32_e32 v239, v239, v239
	v_max_f32_e32 v240, v240, v240
	v_max_f32_e32 v241, v241, v241
	v_med3_f32 v226, v226, s62, v95
	v_med3_f32 v227, v227, s62, v95
	v_med3_f32 v228, v228, s62, v95
	v_med3_f32 v229, v229, s62, v95
	v_med3_f32 v230, v230, s62, v95
	v_med3_f32 v231, v231, s62, v95
	v_med3_f32 v232, v232, s62, v95
	v_med3_f32 v233, v233, s62, v95
	v_med3_f32 v234, v234, s62, v95
	v_med3_f32 v235, v235, s62, v95
	v_med3_f32 v236, v236, s62, v95
	v_med3_f32 v237, v237, s62, v95
	v_med3_f32 v238, v238, s62, v95
	v_med3_f32 v239, v239, s62, v95
	v_med3_f32 v240, v240, s62, v95
	v_med3_f32 v241, v241, s62, v95
	v_mov_b32_e32 v242, 0
	v_mov_b32_e32 v243, 0
	v_mov_b32_e32 v244, 0
	v_mov_b32_e32 v245, 0
	v_cvt_pk_fp8_f32 v242, v226, v227
	v_cvt_pk_fp8_f32 v243, v230, v231
	v_cvt_pk_fp8_f32 v244, v234, v235
	v_cvt_pk_fp8_f32 v245, v238, v239
	v_cvt_pk_fp8_f32 v242, v228, v229 op_sel:[0,0,1]
	v_cvt_pk_fp8_f32 v243, v232, v233 op_sel:[0,0,1]
	v_cvt_pk_fp8_f32 v244, v236, v237 op_sel:[0,0,1]
	v_cvt_pk_fp8_f32 v245, v240, v241 op_sel:[0,0,1]
	s_nop 0
	global_store_dwordx4 v91, v[242:245], s[6:7]
	ds_read_b32 v226, v214
	ds_read_b32 v227, v214 offset:512
	ds_read_b32 v228, v214 offset:1024
	ds_read_b32 v229, v214 offset:1536
	ds_read_b32 v230, v214 offset:2048
	ds_read_b32 v231, v214 offset:2560
	ds_read_b32 v232, v214 offset:3072
	ds_read_b32 v233, v214 offset:3584
	ds_read_b32 v234, v214 offset:4096
	ds_read_b32 v235, v214 offset:4608
	ds_read_b32 v236, v214 offset:5120
	ds_read_b32 v237, v214 offset:5632
	ds_read_b32 v238, v214 offset:6144
	ds_read_b32 v239, v214 offset:6656
	ds_read_b32 v240, v214 offset:7168
	ds_read_b32 v241, v214 offset:7680
	s_waitcnt lgkmcnt(0)
	v_max_f32_e32 v226, v226, v226
	v_max_f32_e32 v227, v227, v227
	v_max_f32_e32 v228, v228, v228
	v_max_f32_e32 v229, v229, v229
	v_max_f32_e32 v230, v230, v230
	v_max_f32_e32 v231, v231, v231
	v_max_f32_e32 v232, v232, v232
	v_max_f32_e32 v233, v233, v233
	v_max_f32_e32 v234, v234, v234
	v_max_f32_e32 v235, v235, v235
	v_max_f32_e32 v236, v236, v236
	v_max_f32_e32 v237, v237, v237
	v_max_f32_e32 v238, v238, v238
	v_max_f32_e32 v239, v239, v239
	v_max_f32_e32 v240, v240, v240
	v_max_f32_e32 v241, v241, v241
	v_med3_f32 v226, v226, s62, v95
	v_med3_f32 v227, v227, s62, v95
	v_med3_f32 v228, v228, s62, v95
	v_med3_f32 v229, v229, s62, v95
	v_med3_f32 v230, v230, s62, v95
	v_med3_f32 v231, v231, s62, v95
	v_med3_f32 v232, v232, s62, v95
	v_med3_f32 v233, v233, s62, v95
	v_med3_f32 v234, v234, s62, v95
	v_med3_f32 v235, v235, s62, v95
	v_med3_f32 v236, v236, s62, v95
	v_med3_f32 v237, v237, s62, v95
	v_med3_f32 v238, v238, s62, v95
	v_med3_f32 v239, v239, s62, v95
	v_med3_f32 v240, v240, s62, v95
	v_med3_f32 v241, v241, s62, v95
	v_mov_b32_e32 v242, 0
	v_mov_b32_e32 v243, 0
	v_mov_b32_e32 v244, 0
	v_mov_b32_e32 v245, 0
	v_cvt_pk_fp8_f32 v242, v226, v227
	v_cvt_pk_fp8_f32 v243, v230, v231
	v_cvt_pk_fp8_f32 v244, v234, v235
	v_cvt_pk_fp8_f32 v245, v238, v239
	v_cvt_pk_fp8_f32 v242, v228, v229 op_sel:[0,0,1]
	v_cvt_pk_fp8_f32 v243, v232, v233 op_sel:[0,0,1]
	v_cvt_pk_fp8_f32 v244, v236, v237 op_sel:[0,0,1]
	v_cvt_pk_fp8_f32 v245, v240, v241 op_sel:[0,0,1]
	s_nop 0
	global_store_dwordx4 v92, v[242:245], s[6:7]
	s_waitcnt vmcnt(12)
	v_mul_f32_e32 v144, v58, v144
	v_mul_f32_e32 v145, v58, v145
	v_mul_f32_e32 v146, v58, v146
	v_mul_f32_e32 v147, v58, v147
	ds_write_b128 v209, v[144:147]
	v_mul_f32_e32 v148, v59, v148
	v_mul_f32_e32 v149, v59, v149
	v_mul_f32_e32 v150, v59, v150
	v_mul_f32_e32 v151, v59, v151
	ds_write_b128 v209, v[148:151] offset:1024
	v_mul_f32_e32 v152, v60, v152
	v_mul_f32_e32 v153, v60, v153
	v_mul_f32_e32 v154, v60, v154
	v_mul_f32_e32 v155, v60, v155
	ds_write_b128 v209, v[152:155] offset:2048
	v_mul_f32_e32 v156, v61, v156
	v_mul_f32_e32 v157, v61, v157
	v_mul_f32_e32 v158, v61, v158
	v_mul_f32_e32 v159, v61, v159
	ds_write_b128 v209, v[156:159] offset:3072
	v_mul_f32_e32 v160, v62, v160
	v_mul_f32_e32 v161, v62, v161
	v_mul_f32_e32 v162, v62, v162
	v_mul_f32_e32 v163, v62, v163
	ds_write_b128 v209, v[160:163] offset:4096
	v_mul_f32_e32 v164, v63, v164
	v_mul_f32_e32 v165, v63, v165
	v_mul_f32_e32 v166, v63, v166
	v_mul_f32_e32 v167, v63, v167
	ds_write_b128 v209, v[164:167] offset:5120
	v_mul_f32_e32 v168, v64, v168
	v_mul_f32_e32 v169, v64, v169
	v_mul_f32_e32 v170, v64, v170
	v_mul_f32_e32 v171, v64, v171
	ds_write_b128 v209, v[168:171] offset:6144
	v_mul_f32_e32 v172, v65, v172
	v_mul_f32_e32 v173, v65, v173
	v_mul_f32_e32 v174, v65, v174
	v_mul_f32_e32 v175, v65, v175
	ds_write_b128 v209, v[172:175] offset:7168
	s_waitcnt lgkmcnt(0)
	s_barrier
; #define GAS __attribute__((address_space(1)))
; #define LAS __attribute__((address_space(3)))
; #define LDS_WAIT() asm volatile("s_waitcnt lgkmcnt(0)" ::: "memory")
; __device__ __forceinline__ unsigned pk2(float lo, float hi) { return f2bf(lo) | (f2bf(hi) << 16); }
; __device__ __forceinline__ int nat_dim(int p) { return (p >> 1) + 64 * (p & 1); }
; template <int MAP, bool KS, bool KPERM = false>
; __device__ __forceinline__ void p0_transpose_item(const float* W, int K, int Nsrc, int nblk, bf16* WT, const float* ksA, const float* ksB, int ksplit, LAS float* scr, int item, int lane) {
;     const int kb = item / nblk, nb = item % nblk, k0 = 64 * kb, n0 = 32 * nb;
;     const int nr = n0 + (lane & 31); const int sc = MAP == 1 ? src_col_in(nr) : (MAP == 2 ? nat_dim(nr) : nr);
;     float v[32];
; #pragma unroll
;     for (int i = 0; i < 32; ++i) { const int k = k0 + 2 * i + (lane >> 5); const int ksrc = KPERM ? ((k & ~127) + nat_dim(k & 127)) : k;
;         v[i] = sc >= 0 ? W[(size_t)ksrc * Nsrc + sc] : 0.f; }
; #pragma unroll
;     for (int i = 0; i < 32; ++i) { const int kk = 2 * i + (lane >> 5); const int k = k0 + kk;
;         if (KS) v[i] *= (k < ksplit ? ksA[k] : ksB[k - ksplit]);
;         scr[kk * 33 + (lane & 31)] = v[i]; }
;     LDS_WAIT(); asm volatile("" ::: "memory");
;     const int c = lane & 7;
; #pragma unroll
;     for (int j = 0; j < 4; ++j) { const int n = (lane >> 3) + 8 * j; const LAS float* s = scr + (8 * c) * 33 + n;
;         v4u o; o.x = pk2(s[0 * 33], s[1 * 33]); o.y = pk2(s[2 * 33], s[3 * 33]); o.z = pk2(s[4 * 33], s[5 * 33]); o.w = pk2(s[6 * 33], s[7 * 33]);
;         *(GAS v4u*)(WT + (size_t)(n0 + n) * K + k0 + 8 * c) = o; }
;     LDS_WAIT(); asm volatile("" ::: "memory");
	s_add_u32 s8, s54, 0x2000
	s_addc_u32 s9, s55, 0
	global_load_dwordx4 v[144:147], v75, s[8:9]
	s_add_u32 s8, s8, 0x8000
	s_addc_u32 s9, s9, 0
	global_load_dwordx4 v[148:151], v75, s[8:9]
	s_add_u32 s8, s8, 0x8000
	s_addc_u32 s9, s9, 0
	global_load_dwordx4 v[152:155], v75, s[8:9]
	s_add_u32 s8, s8, 0x8000
	s_addc_u32 s9, s9, 0
	global_load_dwordx4 v[156:159], v75, s[8:9]
	s_add_u32 s8, s8, 0x8000
	s_addc_u32 s9, s9, 0
	global_load_dwordx4 v[160:163], v75, s[8:9]
	s_add_u32 s8, s8, 0x8000
	s_addc_u32 s9, s9, 0
	global_load_dwordx4 v[164:167], v75, s[8:9]
	s_add_u32 s8, s8, 0x8000
	s_addc_u32 s9, s9, 0
	global_load_dwordx4 v[168:171], v75, s[8:9]
	s_add_u32 s8, s8, 0x8000
	s_addc_u32 s9, s9, 0
	global_load_dwordx4 v[172:175], v75, s[8:9]
	s_mov_b64 s[6:7], s[56:57]
	ds_read_b32 v226, v112
	ds_read_b32 v227, v112 offset:512
	ds_read_b32 v228, v112 offset:1024
	ds_read_b32 v229, v112 offset:1536
	ds_read_b32 v230, v112 offset:2048
	ds_read_b32 v231, v112 offset:2560
	ds_read_b32 v232, v112 offset:3072
	ds_read_b32 v233, v112 offset:3584
	s_waitcnt lgkmcnt(0)
	v_bfe_u32 v120, v226, 16, 1
	v_bfe_u32 v121, v227, 16, 1
	v_bfe_u32 v122, v228, 16, 1
	v_bfe_u32 v123, v229, 16, 1
	v_bfe_u32 v124, v230, 16, 1
	v_bfe_u32 v125, v231, 16, 1
	v_bfe_u32 v126, v232, 16, 1
	v_bfe_u32 v127, v233, 16, 1
	v_add3_u32 v226, v226, v120, s63
	v_add3_u32 v227, v227, v121, s63
	v_add3_u32 v228, v228, v122, s63
	v_add3_u32 v229, v229, v123, s63
	v_add3_u32 v230, v230, v124, s63
	v_add3_u32 v231, v231, v125, s63
	v_add3_u32 v232, v232, v126, s63
	v_add3_u32 v233, v233, v127, s63
	v_perm_b32 v242, v227, v226, s64
	v_perm_b32 v243, v229, v228, s64
	v_perm_b32 v244, v231, v230, s64
	v_perm_b32 v245, v233, v232, s64
	s_nop 0
	global_store_dwordx4 v83, v[242:245], s[6:7]
	ds_read_b32 v226, v114
	ds_read_b32 v227, v114 offset:512
	ds_read_b32 v228, v114 offset:1024
	ds_read_b32 v229, v114 offset:1536
	ds_read_b32 v230, v114 offset:2048
	ds_read_b32 v231, v114 offset:2560
	ds_read_b32 v232, v114 offset:3072
	ds_read_b32 v233, v114 offset:3584
	s_waitcnt lgkmcnt(0)
	v_bfe_u32 v120, v226, 16, 1
	v_bfe_u32 v121, v227, 16, 1
	v_bfe_u32 v122, v228, 16, 1
	v_bfe_u32 v123, v229, 16, 1
	v_bfe_u32 v124, v230, 16, 1
	v_bfe_u32 v125, v231, 16, 1
	v_bfe_u32 v126, v232, 16, 1
	v_bfe_u32 v127, v233, 16, 1
	v_add3_u32 v226, v226, v120, s63
	v_add3_u32 v227, v227, v121, s63
	v_add3_u32 v228, v228, v122, s63
	v_add3_u32 v229, v229, v123, s63
	v_add3_u32 v230, v230, v124, s63
	v_add3_u32 v231, v231, v125, s63
	v_add3_u32 v232, v232, v126, s63
	v_add3_u32 v233, v233, v127, s63
	v_perm_b32 v242, v227, v226, s64
	v_perm_b32 v243, v229, v228, s64
	v_perm_b32 v244, v231, v230, s64
	v_perm_b32 v245, v233, v232, s64
	s_nop 0
	global_store_dwordx4 v84, v[242:245], s[6:7]
	ds_read_b32 v226, v116
	ds_read_b32 v227, v116 offset:512
	ds_read_b32 v228, v116 offset:1024
	ds_read_b32 v229, v116 offset:1536
	ds_read_b32 v230, v116 offset:2048
	ds_read_b32 v231, v116 offset:2560
	ds_read_b32 v232, v116 offset:3072
	ds_read_b32 v233, v116 offset:3584
	s_waitcnt lgkmcnt(0)
	v_bfe_u32 v120, v226, 16, 1
	v_bfe_u32 v121, v227, 16, 1
	v_bfe_u32 v122, v228, 16, 1
	v_bfe_u32 v123, v229, 16, 1
	v_bfe_u32 v124, v230, 16, 1
	v_bfe_u32 v125, v231, 16, 1
	v_bfe_u32 v126, v232, 16, 1
	v_bfe_u32 v127, v233, 16, 1
	v_add3_u32 v226, v226, v120, s63
	v_add3_u32 v227, v227, v121, s63
	v_add3_u32 v228, v228, v122, s63
	v_add3_u32 v229, v229, v123, s63
	v_add3_u32 v230, v230, v124, s63
	v_add3_u32 v231, v231, v125, s63
	v_add3_u32 v232, v232, v126, s63
	v_add3_u32 v233, v233, v127, s63
	v_perm_b32 v242, v227, v226, s64
	v_perm_b32 v243, v229, v228, s64
	v_perm_b32 v244, v231, v230, s64
	v_perm_b32 v245, v233, v232, s64
	s_nop 0
	global_store_dwordx4 v85, v[242:245], s[6:7]
	ds_read_b32 v226, v118
	ds_read_b32 v227, v118 offset:512
	ds_read_b32 v228, v118 offset:1024
	ds_read_b32 v229, v118 offset:1536
	ds_read_b32 v230, v118 offset:2048
	ds_read_b32 v231, v118 offset:2560
	ds_read_b32 v232, v118 offset:3072
	ds_read_b32 v233, v118 offset:3584
	s_waitcnt lgkmcnt(0)
	v_bfe_u32 v120, v226, 16, 1
	v_bfe_u32 v121, v227, 16, 1
	v_bfe_u32 v122, v228, 16, 1
	v_bfe_u32 v123, v229, 16, 1
	v_bfe_u32 v124, v230, 16, 1
	v_bfe_u32 v125, v231, 16, 1
	v_bfe_u32 v126, v232, 16, 1
	v_bfe_u32 v127, v233, 16, 1
	v_add3_u32 v226, v226, v120, s63
	v_add3_u32 v227, v227, v121, s63
	v_add3_u32 v228, v228, v122, s63
	v_add3_u32 v229, v229, v123, s63
	v_add3_u32 v230, v230, v124, s63
	v_add3_u32 v231, v231, v125, s63
	v_add3_u32 v232, v232, v126, s63
	v_add3_u32 v233, v233, v127, s63
	v_perm_b32 v242, v227, v226, s64
	v_perm_b32 v243, v229, v228, s64
	v_perm_b32 v244, v231, v230, s64
	v_perm_b32 v245, v233, v232, s64
	s_nop 0
	global_store_dwordx4 v86, v[242:245], s[6:7]
	s_waitcnt vmcnt(14)
	v_mul_f32_e32 v176, v58, v176
	v_mul_f32_e32 v177, v58, v177
	v_mul_f32_e32 v178, v58, v178
	v_mul_f32_e32 v179, v58, v179
	ds_write_b128 v210, v[176:179]
	v_mul_f32_e32 v180, v59, v180
	v_mul_f32_e32 v181, v59, v181
	v_mul_f32_e32 v182, v59, v182
	v_mul_f32_e32 v183, v59, v183
	ds_write_b128 v210, v[180:183] offset:1024
	v_mul_f32_e32 v184, v60, v184
	v_mul_f32_e32 v185, v60, v185
	v_mul_f32_e32 v186, v60, v186
	v_mul_f32_e32 v187, v60, v187
	ds_write_b128 v210, v[184:187] offset:2048
	v_mul_f32_e32 v188, v61, v188
	v_mul_f32_e32 v189, v61, v189
	v_mul_f32_e32 v190, v61, v190
	v_mul_f32_e32 v191, v61, v191
	ds_write_b128 v210, v[188:191] offset:3072
	v_mul_f32_e32 v192, v62, v192
	v_mul_f32_e32 v193, v62, v193
	v_mul_f32_e32 v194, v62, v194
	v_mul_f32_e32 v195, v62, v195
	ds_write_b128 v210, v[192:195] offset:4096
	v_mul_f32_e32 v196, v63, v196
	v_mul_f32_e32 v197, v63, v197
	v_mul_f32_e32 v198, v63, v198
	v_mul_f32_e32 v199, v63, v199
	ds_write_b128 v210, v[196:199] offset:5120
	v_mul_f32_e32 v200, v64, v200
	v_mul_f32_e32 v201, v64, v201
	v_mul_f32_e32 v202, v64, v202
	v_mul_f32_e32 v203, v64, v203
	ds_write_b128 v210, v[200:203] offset:6144
	v_mul_f32_e32 v204, v65, v204
	v_mul_f32_e32 v205, v65, v205
	v_mul_f32_e32 v206, v65, v206
	v_mul_f32_e32 v207, v65, v207
	ds_write_b128 v210, v[204:207] offset:7168
	s_waitcnt lgkmcnt(0)
	s_barrier
; #define GAS __attribute__((address_space(1)))
; #define LAS __attribute__((address_space(3)))
; #define LDS_WAIT() asm volatile("s_waitcnt lgkmcnt(0)" ::: "memory")
; __device__ __forceinline__ unsigned pk2(float lo, float hi) { return f2bf(lo) | (f2bf(hi) << 16); }
; __device__ __forceinline__ int nat_dim(int p) { return (p >> 1) + 64 * (p & 1); }
; template <int MAP, bool KS, bool KPERM = false>
; __device__ __forceinline__ void p0_transpose_item(const float* W, int K, int Nsrc, int nblk, bf16* WT, const float* ksA, const float* ksB, int ksplit, LAS float* scr, int item, int lane) {
;     const int kb = item / nblk, nb = item % nblk, k0 = 64 * kb, n0 = 32 * nb;
;     const int nr = n0 + (lane & 31); const int sc = MAP == 1 ? src_col_in(nr) : (MAP == 2 ? nat_dim(nr) : nr);
;     float v[32];
; #pragma unroll
;     for (int i = 0; i < 32; ++i) { const int k = k0 + 2 * i + (lane >> 5); const int ksrc = KPERM ? ((k & ~127) + nat_dim(k & 127)) : k;
;         v[i] = sc >= 0 ? W[(size_t)ksrc * Nsrc + sc] : 0.f; }
; #pragma unroll
;     for (int i = 0; i < 32; ++i) { const int kk = 2 * i + (lane >> 5); const int k = k0 + kk;
;         if (KS) v[i] *= (k < ksplit ? ksA[k] : ksB[k - ksplit]);
;         scr[kk * 33 + (lane & 31)] = v[i]; }
;     LDS_WAIT(); asm volatile("" ::: "memory");
;     const int c = lane & 7;
; #pragma unroll
;     for (int j = 0; j < 4; ++j) { const int n = (lane >> 3) + 8 * j; const LAS float* s = scr + (8 * c) * 33 + n;
;         v4u o; o.x = pk2(s[0 * 33], s[1 * 33]); o.y = pk2(s[2 * 33], s[3 * 33]); o.z = pk2(s[4 * 33], s[5 * 33]); o.w = pk2(s[6 * 33], s[7 * 33]);
;         *(GAS v4u*)(WT + (size_t)(n0 + n) * K + k0 + 8 * c) = o; }
;     LDS_WAIT(); asm volatile("" ::: "memory");
	s_add_u32 s8, s54, 0x3000
	s_addc_u32 s9, s55, 0
	global_load_dwordx4 v[176:179], v75, s[8:9]
	s_add_u32 s8, s8, 0x8000
	s_addc_u32 s9, s9, 0
	global_load_dwordx4 v[180:183], v75, s[8:9]
	s_add_u32 s8, s8, 0x8000
	s_addc_u32 s9, s9, 0
	global_load_dwordx4 v[184:187], v75, s[8:9]
	s_add_u32 s8, s8, 0x8000
	s_addc_u32 s9, s9, 0
	global_load_dwordx4 v[188:191], v75, s[8:9]
	s_add_u32 s8, s8, 0x8000
	s_addc_u32 s9, s9, 0
	global_load_dwordx4 v[192:195], v75, s[8:9]
	s_add_u32 s8, s8, 0x8000
	s_addc_u32 s9, s9, 0
	global_load_dwordx4 v[196:199], v75, s[8:9]
	s_add_u32 s8, s8, 0x8000
	s_addc_u32 s9, s9, 0
	global_load_dwordx4 v[200:203], v75, s[8:9]
	s_add_u32 s8, s8, 0x8000
	s_addc_u32 s9, s9, 0
	global_load_dwordx4 v[204:207], v75, s[8:9]
	s_add_u32 s6, s56, 0x800000
	s_addc_u32 s7, s57, 0
	ds_read_b32 v226, v113
	ds_read_b32 v227, v113 offset:512
	ds_read_b32 v228, v113 offset:1024
	ds_read_b32 v229, v113 offset:1536
	ds_read_b32 v230, v113 offset:2048
	ds_read_b32 v231, v113 offset:2560
	ds_read_b32 v232, v113 offset:3072
	ds_read_b32 v233, v113 offset:3584
	s_waitcnt lgkmcnt(0)
	v_bfe_u32 v120, v226, 16, 1
	v_bfe_u32 v121, v227, 16, 1
	v_bfe_u32 v122, v228, 16, 1
	v_bfe_u32 v123, v229, 16, 1
	v_bfe_u32 v124, v230, 16, 1
	v_bfe_u32 v125, v231, 16, 1
	v_bfe_u32 v126, v232, 16, 1
	v_bfe_u32 v127, v233, 16, 1
	v_add3_u32 v226, v226, v120, s63
	v_add3_u32 v227, v227, v121, s63
	v_add3_u32 v228, v228, v122, s63
	v_add3_u32 v229, v229, v123, s63
	v_add3_u32 v230, v230, v124, s63
	v_add3_u32 v231, v231, v125, s63
	v_add3_u32 v232, v232, v126, s63
	v_add3_u32 v233, v233, v127, s63
	v_perm_b32 v242, v227, v226, s64
	v_perm_b32 v243, v229, v228, s64
	v_perm_b32 v244, v231, v230, s64
	v_perm_b32 v245, v233, v232, s64
	s_nop 0
	global_store_dwordx4 v83, v[242:245], s[6:7]
	ds_read_b32 v226, v115
	ds_read_b32 v227, v115 offset:512
	ds_read_b32 v228, v115 offset:1024
	ds_read_b32 v229, v115 offset:1536
	ds_read_b32 v230, v115 offset:2048
	ds_read_b32 v231, v115 offset:2560
	ds_read_b32 v232, v115 offset:3072
	ds_read_b32 v233, v115 offset:3584
	s_waitcnt lgkmcnt(0)
	v_bfe_u32 v120, v226, 16, 1
	v_bfe_u32 v121, v227, 16, 1
	v_bfe_u32 v122, v228, 16, 1
	v_bfe_u32 v123, v229, 16, 1
	v_bfe_u32 v124, v230, 16, 1
	v_bfe_u32 v125, v231, 16, 1
	v_bfe_u32 v126, v232, 16, 1
	v_bfe_u32 v127, v233, 16, 1
	v_add3_u32 v226, v226, v120, s63
	v_add3_u32 v227, v227, v121, s63
	v_add3_u32 v228, v228, v122, s63
	v_add3_u32 v229, v229, v123, s63
	v_add3_u32 v230, v230, v124, s63
	v_add3_u32 v231, v231, v125, s63
	v_add3_u32 v232, v232, v126, s63
	v_add3_u32 v233, v233, v127, s63
	v_perm_b32 v242, v227, v226, s64
	v_perm_b32 v243, v229, v228, s64
	v_perm_b32 v244, v231, v230, s64
	v_perm_b32 v245, v233, v232, s64
	s_nop 0
	global_store_dwordx4 v84, v[242:245], s[6:7]
	ds_read_b32 v226, v117
	ds_read_b32 v227, v117 offset:512
	ds_read_b32 v228, v117 offset:1024
	ds_read_b32 v229, v117 offset:1536
	ds_read_b32 v230, v117 offset:2048
	ds_read_b32 v231, v117 offset:2560
	ds_read_b32 v232, v117 offset:3072
	ds_read_b32 v233, v117 offset:3584
	s_waitcnt lgkmcnt(0)
	v_bfe_u32 v120, v226, 16, 1
	v_bfe_u32 v121, v227, 16, 1
	v_bfe_u32 v122, v228, 16, 1
	v_bfe_u32 v123, v229, 16, 1
	v_bfe_u32 v124, v230, 16, 1
	v_bfe_u32 v125, v231, 16, 1
	v_bfe_u32 v126, v232, 16, 1
	v_bfe_u32 v127, v233, 16, 1
	v_add3_u32 v226, v226, v120, s63
	v_add3_u32 v227, v227, v121, s63
	v_add3_u32 v228, v228, v122, s63
	v_add3_u32 v229, v229, v123, s63
	v_add3_u32 v230, v230, v124, s63
	v_add3_u32 v231, v231, v125, s63
	v_add3_u32 v232, v232, v126, s63
	v_add3_u32 v233, v233, v127, s63
	v_perm_b32 v242, v227, v226, s64
	v_perm_b32 v243, v229, v228, s64
	v_perm_b32 v244, v231, v230, s64
	v_perm_b32 v245, v233, v232, s64
	s_nop 0
	global_store_dwordx4 v85, v[242:245], s[6:7]
	ds_read_b32 v226, v119
	ds_read_b32 v227, v119 offset:512
	ds_read_b32 v228, v119 offset:1024
	ds_read_b32 v229, v119 offset:1536
	ds_read_b32 v230, v119 offset:2048
	ds_read_b32 v231, v119 offset:2560
	ds_read_b32 v232, v119 offset:3072
	ds_read_b32 v233, v119 offset:3584
	s_waitcnt lgkmcnt(0)
	v_bfe_u32 v120, v226, 16, 1
	v_bfe_u32 v121, v227, 16, 1
	v_bfe_u32 v122, v228, 16, 1
	v_bfe_u32 v123, v229, 16, 1
	v_bfe_u32 v124, v230, 16, 1
	v_bfe_u32 v125, v231, 16, 1
	v_bfe_u32 v126, v232, 16, 1
	v_bfe_u32 v127, v233, 16, 1
	v_add3_u32 v226, v226, v120, s63
	v_add3_u32 v227, v227, v121, s63
	v_add3_u32 v228, v228, v122, s63
	v_add3_u32 v229, v229, v123, s63
	v_add3_u32 v230, v230, v124, s63
	v_add3_u32 v231, v231, v125, s63
	v_add3_u32 v232, v232, v126, s63
	v_add3_u32 v233, v233, v127, s63
	v_perm_b32 v242, v227, v226, s64
	v_perm_b32 v243, v229, v228, s64
	v_perm_b32 v244, v231, v230, s64
	v_perm_b32 v245, v233, v232, s64
	s_nop 0
	global_store_dwordx4 v86, v[242:245], s[6:7]
	s_waitcnt vmcnt(16)
	v_mul_f32_e32 v144, v58, v144
	v_mul_f32_e32 v145, v58, v145
	v_mul_f32_e32 v146, v58, v146
	v_mul_f32_e32 v147, v58, v147
	ds_write_b128 v209, v[144:147]
	v_mul_f32_e32 v148, v59, v148
	v_mul_f32_e32 v149, v59, v149
	v_mul_f32_e32 v150, v59, v150
	v_mul_f32_e32 v151, v59, v151
	ds_write_b128 v209, v[148:151] offset:1024
	v_mul_f32_e32 v152, v60, v152
	v_mul_f32_e32 v153, v60, v153
	v_mul_f32_e32 v154, v60, v154
	v_mul_f32_e32 v155, v60, v155
	ds_write_b128 v209, v[152:155] offset:2048
	v_mul_f32_e32 v156, v61, v156
	v_mul_f32_e32 v157, v61, v157
	v_mul_f32_e32 v158, v61, v158
	v_mul_f32_e32 v159, v61, v159
	ds_write_b128 v209, v[156:159] offset:3072
	v_mul_f32_e32 v160, v62, v160
	v_mul_f32_e32 v161, v62, v161
	v_mul_f32_e32 v162, v62, v162
	v_mul_f32_e32 v163, v62, v163
	ds_write_b128 v209, v[160:163] offset:4096
	v_mul_f32_e32 v164, v63, v164
	v_mul_f32_e32 v165, v63, v165
	v_mul_f32_e32 v166, v63, v166
	v_mul_f32_e32 v167, v63, v167
	ds_write_b128 v209, v[164:167] offset:5120
	v_mul_f32_e32 v168, v64, v168
	v_mul_f32_e32 v169, v64, v169
	v_mul_f32_e32 v170, v64, v170
	v_mul_f32_e32 v171, v64, v171
	ds_write_b128 v209, v[168:171] offset:6144
	v_mul_f32_e32 v172, v65, v172
	v_mul_f32_e32 v173, v65, v173
	v_mul_f32_e32 v174, v65, v174
	v_mul_f32_e32 v175, v65, v175
	ds_write_b128 v209, v[172:175] offset:7168
	s_waitcnt lgkmcnt(0)
	s_barrier
; template <int MAP, bool KS, bool KPERM = false>
; __device__ __forceinline__ void p0_transpose_item(const float* W, int K, int Nsrc, int nblk, bf16* WT, const float* ksA, const float* ksB, int ksplit, LAS float* scr, int item, int lane) {
;     const int kb = item / nblk, nb = item % nblk, k0 = 64 * kb, n0 = 32 * nb;
;     const int nr = n0 + (lane & 31); const int sc = MAP == 1 ? src_col_in(nr) : (MAP == 2 ? nat_dim(nr) : nr);
;     float v[32];
; #pragma unroll
;     for (int i = 0; i < 32; ++i) { const int k = k0 + 2 * i + (lane >> 5); const int ksrc = KPERM ? ((k & ~127) + nat_dim(k & 127)) : k;
;         v[i] = sc >= 0 ? W[(size_t)ksrc * Nsrc + sc] : 0.f; }
; #pragma unroll
;     for (int i = 0; i < 32; ++i) { const int kk = 2 * i + (lane >> 5); const int k = k0 + kk;
;         if (KS) v[i] *= (k < ksplit ? ksA[k] : ksB[k - ksplit]);
;         scr[kk * 33 + (lane & 31)] = v[i]; }
;     LDS_WAIT(); asm volatile("" ::: "memory");
;     const int c = lane & 7;
; #pragma unroll
;     for (int j = 0; j < 4; ++j) { const int n = (lane >> 3) + 8 * j; const LAS float* s = scr + (8 * c) * 33 + n;
;         v4u o; o.x = pk2(s[0 * 33], s[1 * 33]); o.y = pk2(s[2 * 33], s[3 * 33]); o.z = pk2(s[4 * 33], s[5 * 33]); o.w = pk2(s[6 * 33], s[7 * 33]);
;         *(GAS v4u*)(WT + (size_t)(n0 + n) * K + k0 + 8 * c) = o; }
;     LDS_WAIT(); asm volatile("" ::: "memory");
;     const int pr = item >> 1, kb = 2 * (pr / nblk) + (item & 1), nb = pr % nblk, k0 = 64 * kb, n0 = 32 * nb;
;     const int nr = n0 + (lane & 31); const int sc = MAP == 1 ? src_col_in(nr) : nr;
;     float v[32];
; #pragma unroll
;     for (int i = 0; i < 32; ++i) v[i] = sc >= 0 ? W[(size_t)(k0 + 2 * i + (lane >> 5)) * Nsrc + sc] : 0.f;
; #pragma unroll
;     for (int i = 0; i < 32; ++i) { const int k = k0 + 2 * i + (lane >> 5); float x = v[i] * wscale; if (KS) x *= (k < ksplit ? ksA[k] : ksB[k - ksplit]); scr[(2 * i + (lane >> 5)) * 33 + (lane & 31)] = x; }
;     LDS_WAIT(); asm volatile("" ::: "memory");
;     const int c = lane & 7;
; #pragma unroll
;     for (int j = 0; j < 4; ++j) { const int n = (lane >> 3) + 8 * j; const LAS float* s = scr + (8 * c) * 33 + n;
;         const unsigned long long o = (unsigned long long)pg8::pk4_fp8(s[0 * 33], s[1 * 33], s[2 * 33], s[3 * 33]) | ((unsigned long long)pg8::pk4_fp8(s[4 * 33], s[5 * 33], s[6 * 33], s[7 * 33]) << 32);
	s_mov_b64 s[8:9], s[58:59]
	global_load_dwordx4 v[144:147], v75, s[8:9]
	s_add_u32 s8, s8, 0x8000
	s_addc_u32 s9, s9, 0
	global_load_dwordx4 v[148:151], v75, s[8:9]
	s_add_u32 s8, s8, 0x8000
	s_addc_u32 s9, s9, 0
	global_load_dwordx4 v[152:155], v75, s[8:9]
	s_add_u32 s8, s8, 0x8000
	s_addc_u32 s9, s9, 0
	global_load_dwordx4 v[156:159], v75, s[8:9]
	s_add_u32 s8, s8, 0x8000
	s_addc_u32 s9, s9, 0
	global_load_dwordx4 v[160:163], v75, s[8:9]
	s_add_u32 s8, s8, 0x8000
	s_addc_u32 s9, s9, 0
	global_load_dwordx4 v[164:167], v75, s[8:9]
	s_add_u32 s8, s8, 0x8000
	s_addc_u32 s9, s9, 0
	global_load_dwordx4 v[168:171], v75, s[8:9]
	s_add_u32 s8, s8, 0x8000
	s_addc_u32 s9, s9, 0
	global_load_dwordx4 v[172:175], v75, s[8:9]
	s_add_u32 s6, s56, 0x1000000
	s_addc_u32 s7, s57, 0
	ds_read_b32 v226, v112
	ds_read_b32 v227, v112 offset:512
	ds_read_b32 v228, v112 offset:1024
	ds_read_b32 v229, v112 offset:1536
	ds_read_b32 v230, v112 offset:2048
	ds_read_b32 v231, v112 offset:2560
	ds_read_b32 v232, v112 offset:3072
	ds_read_b32 v233, v112 offset:3584
	s_waitcnt lgkmcnt(0)
	v_bfe_u32 v120, v226, 16, 1
	v_bfe_u32 v121, v227, 16, 1
	v_bfe_u32 v122, v228, 16, 1
	v_bfe_u32 v123, v229, 16, 1
	v_bfe_u32 v124, v230, 16, 1
	v_bfe_u32 v125, v231, 16, 1
	v_bfe_u32 v126, v232, 16, 1
	v_bfe_u32 v127, v233, 16, 1
	v_add3_u32 v226, v226, v120, s63
	v_add3_u32 v227, v227, v121, s63
	v_add3_u32 v228, v228, v122, s63
	v_add3_u32 v229, v229, v123, s63
	v_add3_u32 v230, v230, v124, s63
	v_add3_u32 v231, v231, v125, s63
	v_add3_u32 v232, v232, v126, s63
	v_add3_u32 v233, v233, v127, s63
	v_perm_b32 v242, v227, v226, s64
	v_perm_b32 v243, v229, v228, s64
	v_perm_b32 v244, v231, v230, s64
	v_perm_b32 v245, v233, v232, s64
	s_nop 0
	global_store_dwordx4 v83, v[242:245], s[6:7]
	ds_read_b32 v226, v114
	ds_read_b32 v227, v114 offset:512
	ds_read_b32 v228, v114 offset:1024
	ds_read_b32 v229, v114 offset:1536
	ds_read_b32 v230, v114 offset:2048
	ds_read_b32 v231, v114 offset:2560
	ds_read_b32 v232, v114 offset:3072
	ds_read_b32 v233, v114 offset:3584
	s_waitcnt lgkmcnt(0)
	v_bfe_u32 v120, v226, 16, 1
	v_bfe_u32 v121, v227, 16, 1
	v_bfe_u32 v122, v228, 16, 1
	v_bfe_u32 v123, v229, 16, 1
	v_bfe_u32 v124, v230, 16, 1
	v_bfe_u32 v125, v231, 16, 1
	v_bfe_u32 v126, v232, 16, 1
	v_bfe_u32 v127, v233, 16, 1
	v_add3_u32 v226, v226, v120, s63
	v_add3_u32 v227, v227, v121, s63
	v_add3_u32 v228, v228, v122, s63
	v_add3_u32 v229, v229, v123, s63
	v_add3_u32 v230, v230, v124, s63
	v_add3_u32 v231, v231, v125, s63
	v_add3_u32 v232, v232, v126, s63
	v_add3_u32 v233, v233, v127, s63
	v_perm_b32 v242, v227, v226, s64
	v_perm_b32 v243, v229, v228, s64
	v_perm_b32 v244, v231, v230, s64
	v_perm_b32 v245, v233, v232, s64
	s_nop 0
	global_store_dwordx4 v84, v[242:245], s[6:7]
	ds_read_b32 v226, v116
	ds_read_b32 v227, v116 offset:512
	ds_read_b32 v228, v116 offset:1024
	ds_read_b32 v229, v116 offset:1536
	ds_read_b32 v230, v116 offset:2048
	ds_read_b32 v231, v116 offset:2560
	ds_read_b32 v232, v116 offset:3072
	ds_read_b32 v233, v116 offset:3584
	s_waitcnt lgkmcnt(0)
	v_bfe_u32 v120, v226, 16, 1
	v_bfe_u32 v121, v227, 16, 1
	v_bfe_u32 v122, v228, 16, 1
	v_bfe_u32 v123, v229, 16, 1
	v_bfe_u32 v124, v230, 16, 1
	v_bfe_u32 v125, v231, 16, 1
	v_bfe_u32 v126, v232, 16, 1
	v_bfe_u32 v127, v233, 16, 1
	v_add3_u32 v226, v226, v120, s63
	v_add3_u32 v227, v227, v121, s63
	v_add3_u32 v228, v228, v122, s63
	v_add3_u32 v229, v229, v123, s63
	v_add3_u32 v230, v230, v124, s63
	v_add3_u32 v231, v231, v125, s63
	v_add3_u32 v232, v232, v126, s63
	v_add3_u32 v233, v233, v127, s63
	v_perm_b32 v242, v227, v226, s64
	v_perm_b32 v243, v229, v228, s64
	v_perm_b32 v244, v231, v230, s64
	v_perm_b32 v245, v233, v232, s64
	s_nop 0
	global_store_dwordx4 v85, v[242:245], s[6:7]
	ds_read_b32 v226, v118
	ds_read_b32 v227, v118 offset:512
	ds_read_b32 v228, v118 offset:1024
	ds_read_b32 v229, v118 offset:1536
	ds_read_b32 v230, v118 offset:2048
	ds_read_b32 v231, v118 offset:2560
	ds_read_b32 v232, v118 offset:3072
	ds_read_b32 v233, v118 offset:3584
	s_waitcnt lgkmcnt(0)
	v_bfe_u32 v120, v226, 16, 1
	v_bfe_u32 v121, v227, 16, 1
	v_bfe_u32 v122, v228, 16, 1
	v_bfe_u32 v123, v229, 16, 1
	v_bfe_u32 v124, v230, 16, 1
	v_bfe_u32 v125, v231, 16, 1
	v_bfe_u32 v126, v232, 16, 1
	v_bfe_u32 v127, v233, 16, 1
	v_add3_u32 v226, v226, v120, s63
	v_add3_u32 v227, v227, v121, s63
	v_add3_u32 v228, v228, v122, s63
	v_add3_u32 v229, v229, v123, s63
	v_add3_u32 v230, v230, v124, s63
	v_add3_u32 v231, v231, v125, s63
	v_add3_u32 v232, v232, v126, s63
	v_add3_u32 v233, v233, v127, s63
	v_perm_b32 v242, v227, v226, s64
	v_perm_b32 v243, v229, v228, s64
	v_perm_b32 v244, v231, v230, s64
	v_perm_b32 v245, v233, v232, s64
	s_nop 0
	global_store_dwordx4 v86, v[242:245], s[6:7]
	s_waitcnt vmcnt(16)
	v_mul_f32_e32 v176, v58, v176
	v_mul_f32_e32 v177, v58, v177
	v_mul_f32_e32 v178, v58, v178
	v_mul_f32_e32 v179, v58, v179
	ds_write_b128 v210, v[176:179]
	v_mul_f32_e32 v180, v59, v180
	v_mul_f32_e32 v181, v59, v181
	v_mul_f32_e32 v182, v59, v182
	v_mul_f32_e32 v183, v59, v183
	ds_write_b128 v210, v[180:183] offset:1024
	v_mul_f32_e32 v184, v60, v184
	v_mul_f32_e32 v185, v60, v185
	v_mul_f32_e32 v186, v60, v186
	v_mul_f32_e32 v187, v60, v187
	ds_write_b128 v210, v[184:187] offset:2048
	v_mul_f32_e32 v188, v61, v188
	v_mul_f32_e32 v189, v61, v189
	v_mul_f32_e32 v190, v61, v190
	v_mul_f32_e32 v191, v61, v191
	ds_write_b128 v210, v[188:191] offset:3072
	v_mul_f32_e32 v192, v62, v192
	v_mul_f32_e32 v193, v62, v193
	v_mul_f32_e32 v194, v62, v194
	v_mul_f32_e32 v195, v62, v195
	ds_write_b128 v210, v[192:195] offset:4096
	v_mul_f32_e32 v196, v63, v196
	v_mul_f32_e32 v197, v63, v197
	v_mul_f32_e32 v198, v63, v198
	v_mul_f32_e32 v199, v63, v199
	ds_write_b128 v210, v[196:199] offset:5120
	v_mul_f32_e32 v200, v64, v200
	v_mul_f32_e32 v201, v64, v201
	v_mul_f32_e32 v202, v64, v202
	v_mul_f32_e32 v203, v64, v203
	ds_write_b128 v210, v[200:203] offset:6144
	v_mul_f32_e32 v204, v65, v204
	v_mul_f32_e32 v205, v65, v205
	v_mul_f32_e32 v206, v65, v206
	v_mul_f32_e32 v207, v65, v207
	ds_write_b128 v210, v[204:207] offset:7168
	s_waitcnt lgkmcnt(0)
	s_barrier
; template <int MAP, bool KS, bool KPERM = false>
; __device__ __forceinline__ void p0_transpose_item(const float* W, int K, int Nsrc, int nblk, bf16* WT, const float* ksA, const float* ksB, int ksplit, LAS float* scr, int item, int lane) {
;     const int kb = item / nblk, nb = item % nblk, k0 = 64 * kb, n0 = 32 * nb;
;     const int nr = n0 + (lane & 31); const int sc = MAP == 1 ? src_col_in(nr) : (MAP == 2 ? nat_dim(nr) : nr);
;     float v[32];
; #pragma unroll
;     for (int i = 0; i < 32; ++i) { const int k = k0 + 2 * i + (lane >> 5); const int ksrc = KPERM ? ((k & ~127) + nat_dim(k & 127)) : k;
;         v[i] = sc >= 0 ? W[(size_t)ksrc * Nsrc + sc] : 0.f; }
; #pragma unroll
;     for (int i = 0; i < 32; ++i) { const int kk = 2 * i + (lane >> 5); const int k = k0 + kk;
;         if (KS) v[i] *= (k < ksplit ? ksA[k] : ksB[k - ksplit]);
;         scr[kk * 33 + (lane & 31)] = v[i]; }
;     LDS_WAIT(); asm volatile("" ::: "memory");
;     const int c = lane & 7;
; #pragma unroll
;     for (int j = 0; j < 4; ++j) { const int n = (lane >> 3) + 8 * j; const LAS float* s = scr + (8 * c) * 33 + n;
;         v4u o; o.x = pk2(s[0 * 33], s[1 * 33]); o.y = pk2(s[2 * 33], s[3 * 33]); o.z = pk2(s[4 * 33], s[5 * 33]); o.w = pk2(s[6 * 33], s[7 * 33]);
;         *(GAS v4u*)(WT + (size_t)(n0 + n) * K + k0 + 8 * c) = o; }
;     LDS_WAIT(); asm volatile("" ::: "memory");
;     const int pr = item >> 1, kb = 2 * (pr / nblk) + (item & 1), nb = pr % nblk, k0 = 64 * kb, n0 = 32 * nb;
;     const int nr = n0 + (lane & 31); const int sc = MAP == 1 ? src_col_in(nr) : nr;
;     float v[32];
; #pragma unroll
;     for (int i = 0; i < 32; ++i) v[i] = sc >= 0 ? W[(size_t)(k0 + 2 * i + (lane >> 5)) * Nsrc + sc] : 0.f;
; #pragma unroll
;     for (int i = 0; i < 32; ++i) { const int k = k0 + 2 * i + (lane >> 5); float x = v[i] * wscale; if (KS) x *= (k < ksplit ? ksA[k] : ksB[k - ksplit]); scr[(2 * i + (lane >> 5)) * 33 + (lane & 31)] = x; }
;     LDS_WAIT(); asm volatile("" ::: "memory");
;     const int c = lane & 7;
; #pragma unroll
;     for (int j = 0; j < 4; ++j) { const int n = (lane >> 3) + 8 * j; const LAS float* s = scr + (8 * c) * 33 + n;
;         const unsigned long long o = (unsigned long long)pg8::pk4_fp8(s[0 * 33], s[1 * 33], s[2 * 33], s[3 * 33]) | ((unsigned long long)pg8::pk4_fp8(s[4 * 33], s[5 * 33], s[6 * 33], s[7 * 33]) << 32);
	s_add_u32 s8, s58, 0x1000
	s_addc_u32 s9, s59, 0
	global_load_dwordx4 v[176:179], v75, s[8:9]
	s_add_u32 s8, s8, 0x8000
	s_addc_u32 s9, s9, 0
	global_load_dwordx4 v[180:183], v75, s[8:9]
	s_add_u32 s8, s8, 0x8000
	s_addc_u32 s9, s9, 0
	global_load_dwordx4 v[184:187], v75, s[8:9]
	s_add_u32 s8, s8, 0x8000
	s_addc_u32 s9, s9, 0
	global_load_dwordx4 v[188:191], v75, s[8:9]
	s_add_u32 s8, s8, 0x8000
	s_addc_u32 s9, s9, 0
	global_load_dwordx4 v[192:195], v75, s[8:9]
	s_add_u32 s8, s8, 0x8000
	s_addc_u32 s9, s9, 0
	global_load_dwordx4 v[196:199], v75, s[8:9]
	s_add_u32 s8, s8, 0x8000
	s_addc_u32 s9, s9, 0
	global_load_dwordx4 v[200:203], v75, s[8:9]
	s_add_u32 s8, s8, 0x8000
	s_addc_u32 s9, s9, 0
	global_load_dwordx4 v[204:207], v75, s[8:9]
	s_add_u32 s6, s56, 0x1800000
	s_addc_u32 s7, s57, 0
	ds_read_b32 v226, v113
	ds_read_b32 v227, v113 offset:512
	ds_read_b32 v228, v113 offset:1024
	ds_read_b32 v229, v113 offset:1536
	ds_read_b32 v230, v113 offset:2048
	ds_read_b32 v231, v113 offset:2560
	ds_read_b32 v232, v113 offset:3072
	ds_read_b32 v233, v113 offset:3584
	s_waitcnt lgkmcnt(0)
	v_bfe_u32 v120, v226, 16, 1
	v_bfe_u32 v121, v227, 16, 1
	v_bfe_u32 v122, v228, 16, 1
	v_bfe_u32 v123, v229, 16, 1
	v_bfe_u32 v124, v230, 16, 1
	v_bfe_u32 v125, v231, 16, 1
	v_bfe_u32 v126, v232, 16, 1
	v_bfe_u32 v127, v233, 16, 1
	v_add3_u32 v226, v226, v120, s63
	v_add3_u32 v227, v227, v121, s63
	v_add3_u32 v228, v228, v122, s63
	v_add3_u32 v229, v229, v123, s63
	v_add3_u32 v230, v230, v124, s63
	v_add3_u32 v231, v231, v125, s63
	v_add3_u32 v232, v232, v126, s63
	v_add3_u32 v233, v233, v127, s63
	v_perm_b32 v242, v227, v226, s64
	v_perm_b32 v243, v229, v228, s64
	v_perm_b32 v244, v231, v230, s64
	v_perm_b32 v245, v233, v232, s64
	s_nop 0
	global_store_dwordx4 v83, v[242:245], s[6:7]
	ds_read_b32 v226, v115
	ds_read_b32 v227, v115 offset:512
	ds_read_b32 v228, v115 offset:1024
	ds_read_b32 v229, v115 offset:1536
	ds_read_b32 v230, v115 offset:2048
	ds_read_b32 v231, v115 offset:2560
	ds_read_b32 v232, v115 offset:3072
	ds_read_b32 v233, v115 offset:3584
	s_waitcnt lgkmcnt(0)
	v_bfe_u32 v120, v226, 16, 1
	v_bfe_u32 v121, v227, 16, 1
	v_bfe_u32 v122, v228, 16, 1
	v_bfe_u32 v123, v229, 16, 1
	v_bfe_u32 v124, v230, 16, 1
	v_bfe_u32 v125, v231, 16, 1
	v_bfe_u32 v126, v232, 16, 1
	v_bfe_u32 v127, v233, 16, 1
	v_add3_u32 v226, v226, v120, s63
	v_add3_u32 v227, v227, v121, s63
	v_add3_u32 v228, v228, v122, s63
	v_add3_u32 v229, v229, v123, s63
	v_add3_u32 v230, v230, v124, s63
	v_add3_u32 v231, v231, v125, s63
	v_add3_u32 v232, v232, v126, s63
	v_add3_u32 v233, v233, v127, s63
	v_perm_b32 v242, v227, v226, s64
	v_perm_b32 v243, v229, v228, s64
	v_perm_b32 v244, v231, v230, s64
	v_perm_b32 v245, v233, v232, s64
	s_nop 0
	global_store_dwordx4 v84, v[242:245], s[6:7]
	ds_read_b32 v226, v117
	ds_read_b32 v227, v117 offset:512
	ds_read_b32 v228, v117 offset:1024
	ds_read_b32 v229, v117 offset:1536
	ds_read_b32 v230, v117 offset:2048
	ds_read_b32 v231, v117 offset:2560
	ds_read_b32 v232, v117 offset:3072
	ds_read_b32 v233, v117 offset:3584
	s_waitcnt lgkmcnt(0)
	v_bfe_u32 v120, v226, 16, 1
	v_bfe_u32 v121, v227, 16, 1
	v_bfe_u32 v122, v228, 16, 1
	v_bfe_u32 v123, v229, 16, 1
	v_bfe_u32 v124, v230, 16, 1
	v_bfe_u32 v125, v231, 16, 1
	v_bfe_u32 v126, v232, 16, 1
	v_bfe_u32 v127, v233, 16, 1
	v_add3_u32 v226, v226, v120, s63
	v_add3_u32 v227, v227, v121, s63
	v_add3_u32 v228, v228, v122, s63
	v_add3_u32 v229, v229, v123, s63
	v_add3_u32 v230, v230, v124, s63
	v_add3_u32 v231, v231, v125, s63
	v_add3_u32 v232, v232, v126, s63
	v_add3_u32 v233, v233, v127, s63
	v_perm_b32 v242, v227, v226, s64
	v_perm_b32 v243, v229, v228, s64
	v_perm_b32 v244, v231, v230, s64
	v_perm_b32 v245, v233, v232, s64
	s_nop 0
	global_store_dwordx4 v85, v[242:245], s[6:7]
	ds_read_b32 v226, v119
	ds_read_b32 v227, v119 offset:512
	ds_read_b32 v228, v119 offset:1024
	ds_read_b32 v229, v119 offset:1536
	ds_read_b32 v230, v119 offset:2048
	ds_read_b32 v231, v119 offset:2560
	ds_read_b32 v232, v119 offset:3072
	ds_read_b32 v233, v119 offset:3584
	s_waitcnt lgkmcnt(0)
	v_bfe_u32 v120, v226, 16, 1
	v_bfe_u32 v121, v227, 16, 1
	v_bfe_u32 v122, v228, 16, 1
	v_bfe_u32 v123, v229, 16, 1
	v_bfe_u32 v124, v230, 16, 1
	v_bfe_u32 v125, v231, 16, 1
	v_bfe_u32 v126, v232, 16, 1
	v_bfe_u32 v127, v233, 16, 1
	v_add3_u32 v226, v226, v120, s63
	v_add3_u32 v227, v227, v121, s63
	v_add3_u32 v228, v228, v122, s63
	v_add3_u32 v229, v229, v123, s63
	v_add3_u32 v230, v230, v124, s63
	v_add3_u32 v231, v231, v125, s63
	v_add3_u32 v232, v232, v126, s63
	v_add3_u32 v233, v233, v127, s63
	v_perm_b32 v242, v227, v226, s64
	v_perm_b32 v243, v229, v228, s64
	v_perm_b32 v244, v231, v230, s64
	v_perm_b32 v245, v233, v232, s64
	s_nop 0
	global_store_dwordx4 v86, v[242:245], s[6:7]
	s_waitcnt vmcnt(16)
	v_mul_f32_e32 v144, v66, v144
	v_mul_f32_e32 v145, v66, v145
	v_mul_f32_e32 v146, v66, v146
	v_mul_f32_e32 v147, v66, v147
	ds_write_b128 v209, v[144:147]
	v_mul_f32_e32 v148, v67, v148
	v_mul_f32_e32 v149, v67, v149
	v_mul_f32_e32 v150, v67, v150
	v_mul_f32_e32 v151, v67, v151
	ds_write_b128 v209, v[148:151] offset:1024
	v_mul_f32_e32 v152, v68, v152
	v_mul_f32_e32 v153, v68, v153
	v_mul_f32_e32 v154, v68, v154
	v_mul_f32_e32 v155, v68, v155
	ds_write_b128 v209, v[152:155] offset:2048
	v_mul_f32_e32 v156, v69, v156
	v_mul_f32_e32 v157, v69, v157
	v_mul_f32_e32 v158, v69, v158
	v_mul_f32_e32 v159, v69, v159
	ds_write_b128 v209, v[156:159] offset:3072
	v_mul_f32_e32 v160, v70, v160
	v_mul_f32_e32 v161, v70, v161
	v_mul_f32_e32 v162, v70, v162
	v_mul_f32_e32 v163, v70, v163
	ds_write_b128 v209, v[160:163] offset:4096
	v_mul_f32_e32 v164, v71, v164
	v_mul_f32_e32 v165, v71, v165
	v_mul_f32_e32 v166, v71, v166
	v_mul_f32_e32 v167, v71, v167
	ds_write_b128 v209, v[164:167] offset:5120
	v_mul_f32_e32 v168, v72, v168
	v_mul_f32_e32 v169, v72, v169
	v_mul_f32_e32 v170, v72, v170
	v_mul_f32_e32 v171, v72, v171
	ds_write_b128 v209, v[168:171] offset:6144
	v_mul_f32_e32 v172, v73, v172
	v_mul_f32_e32 v173, v73, v173
	v_mul_f32_e32 v174, v73, v174
	v_mul_f32_e32 v175, v73, v175
	ds_write_b128 v209, v[172:175] offset:7168
	s_waitcnt lgkmcnt(0)
	s_barrier
; #define GAS __attribute__((address_space(1)))
; #define LAS __attribute__((address_space(3)))
; #define LDS_WAIT() asm volatile("s_waitcnt lgkmcnt(0)" ::: "memory")
;     const int pr = item >> 1, kb = 2 * (pr / nblk) + (item & 1), nb = pr % nblk, k0 = 64 * kb, n0 = 32 * nb;
;     const int nr = n0 + (lane & 31); const int sc = MAP == 1 ? src_col_in(nr) : nr;
;     float v[32];
; #pragma unroll
;     for (int i = 0; i < 32; ++i) v[i] = sc >= 0 ? W[(size_t)(k0 + 2 * i + (lane >> 5)) * Nsrc + sc] : 0.f;
; #pragma unroll
;     for (int i = 0; i < 32; ++i) { const int k = k0 + 2 * i + (lane >> 5); float x = v[i] * wscale; if (KS) x *= (k < ksplit ? ksA[k] : ksB[k - ksplit]); scr[(2 * i + (lane >> 5)) * 33 + (lane & 31)] = x; }
;     LDS_WAIT(); asm volatile("" ::: "memory");
;     const int c = lane & 7;
; #pragma unroll
;     for (int j = 0; j < 4; ++j) { const int n = (lane >> 3) + 8 * j; const LAS float* s = scr + (8 * c) * 33 + n;
;         const unsigned long long o = (unsigned long long)pg8::pk4_fp8(s[0 * 33], s[1 * 33], s[2 * 33], s[3 * 33]) | ((unsigned long long)pg8::pk4_fp8(s[4 * 33], s[5 * 33], s[6 * 33], s[7 * 33]) << 32);
;         *(GAS unsigned long long*)(WT + (size_t)(n0 + n) * K + k0 + 8 * c) = o; }
;     LDS_WAIT(); asm volatile("" ::: "memory");
; }
	s_add_u32 s8, s58, 0x2000
	s_addc_u32 s9, s59, 0
	global_load_dwordx4 v[144:147], v75, s[8:9]
	s_add_u32 s8, s8, 0x8000
	s_addc_u32 s9, s9, 0
	global_load_dwordx4 v[148:151], v75, s[8:9]
	s_add_u32 s8, s8, 0x8000
	s_addc_u32 s9, s9, 0
	global_load_dwordx4 v[152:155], v75, s[8:9]
	s_add_u32 s8, s8, 0x8000
	s_addc_u32 s9, s9, 0
	global_load_dwordx4 v[156:159], v75, s[8:9]
	s_add_u32 s8, s8, 0x8000
	s_addc_u32 s9, s9, 0
	global_load_dwordx4 v[160:163], v75, s[8:9]
	s_add_u32 s8, s8, 0x8000
	s_addc_u32 s9, s9, 0
	global_load_dwordx4 v[164:167], v75, s[8:9]
	s_add_u32 s8, s8, 0x8000
	s_addc_u32 s9, s9, 0
	global_load_dwordx4 v[168:171], v75, s[8:9]
	s_add_u32 s8, s8, 0x8000
	s_addc_u32 s9, s9, 0
	global_load_dwordx4 v[172:175], v75, s[8:9]
	s_mov_b64 s[6:7], s[60:61]
	ds_read_b32 v226, v211
	ds_read_b32 v227, v211 offset:512
	ds_read_b32 v228, v211 offset:1024
	ds_read_b32 v229, v211 offset:1536
	ds_read_b32 v230, v211 offset:2048
	ds_read_b32 v231, v211 offset:2560
	ds_read_b32 v232, v211 offset:3072
	ds_read_b32 v233, v211 offset:3584
	ds_read_b32 v234, v211 offset:4096
	ds_read_b32 v235, v211 offset:4608
	ds_read_b32 v236, v211 offset:5120
	ds_read_b32 v237, v211 offset:5632
	ds_read_b32 v238, v211 offset:6144
	ds_read_b32 v239, v211 offset:6656
	ds_read_b32 v240, v211 offset:7168
	ds_read_b32 v241, v211 offset:7680
	s_waitcnt lgkmcnt(0)
	v_max_f32_e32 v226, v226, v226
	v_max_f32_e32 v227, v227, v227
	v_max_f32_e32 v228, v228, v228
	v_max_f32_e32 v229, v229, v229
	v_max_f32_e32 v230, v230, v230
	v_max_f32_e32 v231, v231, v231
	v_max_f32_e32 v232, v232, v232
	v_max_f32_e32 v233, v233, v233
	v_max_f32_e32 v234, v234, v234
	v_max_f32_e32 v235, v235, v235
	v_max_f32_e32 v236, v236, v236
	v_max_f32_e32 v237, v237, v237
	v_max_f32_e32 v238, v238, v238
	v_max_f32_e32 v239, v239, v239
	v_max_f32_e32 v240, v240, v240
	v_max_f32_e32 v241, v241, v241
	v_med3_f32 v226, v226, s62, v95
	v_med3_f32 v227, v227, s62, v95
	v_med3_f32 v228, v228, s62, v95
	v_med3_f32 v229, v229, s62, v95
	v_med3_f32 v230, v230, s62, v95
	v_med3_f32 v231, v231, s62, v95
	v_med3_f32 v232, v232, s62, v95
	v_med3_f32 v233, v233, s62, v95
	v_med3_f32 v234, v234, s62, v95
	v_med3_f32 v235, v235, s62, v95
	v_med3_f32 v236, v236, s62, v95
	v_med3_f32 v237, v237, s62, v95
	v_med3_f32 v238, v238, s62, v95
	v_med3_f32 v239, v239, s62, v95
	v_med3_f32 v240, v240, s62, v95
	v_med3_f32 v241, v241, s62, v95
	v_mov_b32_e32 v242, 0
	v_mov_b32_e32 v243, 0
	v_mov_b32_e32 v244, 0
	v_mov_b32_e32 v245, 0
	v_cvt_pk_fp8_f32 v242, v226, v227
	v_cvt_pk_fp8_f32 v243, v230, v231
	v_cvt_pk_fp8_f32 v244, v234, v235
	v_cvt_pk_fp8_f32 v245, v238, v239
	v_cvt_pk_fp8_f32 v242, v228, v229 op_sel:[0,0,1]
	v_cvt_pk_fp8_f32 v243, v232, v233 op_sel:[0,0,1]
	v_cvt_pk_fp8_f32 v244, v236, v237 op_sel:[0,0,1]
	v_cvt_pk_fp8_f32 v245, v240, v241 op_sel:[0,0,1]
	s_nop 0
	global_store_dwordx4 v77, v[242:245], s[6:7]
	ds_read_b32 v226, v213
	ds_read_b32 v227, v213 offset:512
	ds_read_b32 v228, v213 offset:1024
	ds_read_b32 v229, v213 offset:1536
	ds_read_b32 v230, v213 offset:2048
	ds_read_b32 v231, v213 offset:2560
	ds_read_b32 v232, v213 offset:3072
	ds_read_b32 v233, v213 offset:3584
	ds_read_b32 v234, v213 offset:4096
	ds_read_b32 v235, v213 offset:4608
	ds_read_b32 v236, v213 offset:5120
	ds_read_b32 v237, v213 offset:5632
	ds_read_b32 v238, v213 offset:6144
	ds_read_b32 v239, v213 offset:6656
	ds_read_b32 v240, v213 offset:7168
	ds_read_b32 v241, v213 offset:7680
	s_waitcnt lgkmcnt(0)
	v_max_f32_e32 v226, v226, v226
	v_max_f32_e32 v227, v227, v227
	v_max_f32_e32 v228, v228, v228
	v_max_f32_e32 v229, v229, v229
	v_max_f32_e32 v230, v230, v230
	v_max_f32_e32 v231, v231, v231
	v_max_f32_e32 v232, v232, v232
	v_max_f32_e32 v233, v233, v233
	v_max_f32_e32 v234, v234, v234
	v_max_f32_e32 v235, v235, v235
	v_max_f32_e32 v236, v236, v236
	v_max_f32_e32 v237, v237, v237
	v_max_f32_e32 v238, v238, v238
	v_max_f32_e32 v239, v239, v239
	v_max_f32_e32 v240, v240, v240
	v_max_f32_e32 v241, v241, v241
	v_med3_f32 v226, v226, s62, v95
	v_med3_f32 v227, v227, s62, v95
	v_med3_f32 v228, v228, s62, v95
	v_med3_f32 v229, v229, s62, v95
	v_med3_f32 v230, v230, s62, v95
	v_med3_f32 v231, v231, s62, v95
	v_med3_f32 v232, v232, s62, v95
	v_med3_f32 v233, v233, s62, v95
	v_med3_f32 v234, v234, s62, v95
	v_med3_f32 v235, v235, s62, v95
	v_med3_f32 v236, v236, s62, v95
	v_med3_f32 v237, v237, s62, v95
	v_med3_f32 v238, v238, s62, v95
	v_med3_f32 v239, v239, s62, v95
	v_med3_f32 v240, v240, s62, v95
	v_med3_f32 v241, v241, s62, v95
	v_mov_b32_e32 v242, 0
	v_mov_b32_e32 v243, 0
	v_mov_b32_e32 v244, 0
	v_mov_b32_e32 v245, 0
	v_cvt_pk_fp8_f32 v242, v226, v227
	v_cvt_pk_fp8_f32 v243, v230, v231
	v_cvt_pk_fp8_f32 v244, v234, v235
	v_cvt_pk_fp8_f32 v245, v238, v239
	v_cvt_pk_fp8_f32 v242, v228, v229 op_sel:[0,0,1]
	v_cvt_pk_fp8_f32 v243, v232, v233 op_sel:[0,0,1]
	v_cvt_pk_fp8_f32 v244, v236, v237 op_sel:[0,0,1]
	v_cvt_pk_fp8_f32 v245, v240, v241 op_sel:[0,0,1]
	s_nop 0
	global_store_dwordx4 v78, v[242:245], s[6:7]
	s_waitcnt vmcnt(14)
	v_mul_f32_e32 v176, v66, v176
	v_mul_f32_e32 v177, v66, v177
	v_mul_f32_e32 v178, v66, v178
	v_mul_f32_e32 v179, v66, v179
	ds_write_b128 v210, v[176:179]
	v_mul_f32_e32 v180, v67, v180
	v_mul_f32_e32 v181, v67, v181
	v_mul_f32_e32 v182, v67, v182
	v_mul_f32_e32 v183, v67, v183
	ds_write_b128 v210, v[180:183] offset:1024
	v_mul_f32_e32 v184, v68, v184
	v_mul_f32_e32 v185, v68, v185
	v_mul_f32_e32 v186, v68, v186
	v_mul_f32_e32 v187, v68, v187
	ds_write_b128 v210, v[184:187] offset:2048
	v_mul_f32_e32 v188, v69, v188
	v_mul_f32_e32 v189, v69, v189
	v_mul_f32_e32 v190, v69, v190
	v_mul_f32_e32 v191, v69, v191
	ds_write_b128 v210, v[188:191] offset:3072
	v_mul_f32_e32 v192, v70, v192
	v_mul_f32_e32 v193, v70, v193
	v_mul_f32_e32 v194, v70, v194
	v_mul_f32_e32 v195, v70, v195
	ds_write_b128 v210, v[192:195] offset:4096
	v_mul_f32_e32 v196, v71, v196
	v_mul_f32_e32 v197, v71, v197
	v_mul_f32_e32 v198, v71, v198
	v_mul_f32_e32 v199, v71, v199
	ds_write_b128 v210, v[196:199] offset:5120
	v_mul_f32_e32 v200, v72, v200
	v_mul_f32_e32 v201, v72, v201
	v_mul_f32_e32 v202, v72, v202
	v_mul_f32_e32 v203, v72, v203
	ds_write_b128 v210, v[200:203] offset:6144
	v_mul_f32_e32 v204, v73, v204
	v_mul_f32_e32 v205, v73, v205
	v_mul_f32_e32 v206, v73, v206
	v_mul_f32_e32 v207, v73, v207
	ds_write_b128 v210, v[204:207] offset:7168
	s_waitcnt lgkmcnt(0)
	s_barrier
; #define GAS __attribute__((address_space(1)))
; #define LAS __attribute__((address_space(3)))
; #define LDS_WAIT() asm volatile("s_waitcnt lgkmcnt(0)" ::: "memory")
;     const int pr = item >> 1, kb = 2 * (pr / nblk) + (item & 1), nb = pr % nblk, k0 = 64 * kb, n0 = 32 * nb;
;     const int nr = n0 + (lane & 31); const int sc = MAP == 1 ? src_col_in(nr) : nr;
;     float v[32];
; #pragma unroll
;     for (int i = 0; i < 32; ++i) v[i] = sc >= 0 ? W[(size_t)(k0 + 2 * i + (lane >> 5)) * Nsrc + sc] : 0.f;
; #pragma unroll
;     for (int i = 0; i < 32; ++i) { const int k = k0 + 2 * i + (lane >> 5); float x = v[i] * wscale; if (KS) x *= (k < ksplit ? ksA[k] : ksB[k - ksplit]); scr[(2 * i + (lane >> 5)) * 33 + (lane & 31)] = x; }
;     LDS_WAIT(); asm volatile("" ::: "memory");
;     const int c = lane & 7;
; #pragma unroll
;     for (int j = 0; j < 4; ++j) { const int n = (lane >> 3) + 8 * j; const LAS float* s = scr + (8 * c) * 33 + n;
;         const unsigned long long o = (unsigned long long)pg8::pk4_fp8(s[0 * 33], s[1 * 33], s[2 * 33], s[3 * 33]) | ((unsigned long long)pg8::pk4_fp8(s[4 * 33], s[5 * 33], s[6 * 33], s[7 * 33]) << 32);
;         *(GAS unsigned long long*)(WT + (size_t)(n0 + n) * K + k0 + 8 * c) = o; }
;     LDS_WAIT(); asm volatile("" ::: "memory");
; }
	s_add_u32 s8, s58, 0x3000
	s_addc_u32 s9, s59, 0
	global_load_dwordx4 v[176:179], v75, s[8:9]
	s_add_u32 s8, s8, 0x8000
	s_addc_u32 s9, s9, 0
	global_load_dwordx4 v[180:183], v75, s[8:9]
	s_add_u32 s8, s8, 0x8000
	s_addc_u32 s9, s9, 0
	global_load_dwordx4 v[184:187], v75, s[8:9]
	s_add_u32 s8, s8, 0x8000
	s_addc_u32 s9, s9, 0
	global_load_dwordx4 v[188:191], v75, s[8:9]
	s_add_u32 s8, s8, 0x8000
	s_addc_u32 s9, s9, 0
	global_load_dwordx4 v[192:195], v75, s[8:9]
	s_add_u32 s8, s8, 0x8000
	s_addc_u32 s9, s9, 0
	global_load_dwordx4 v[196:199], v75, s[8:9]
	s_add_u32 s8, s8, 0x8000
	s_addc_u32 s9, s9, 0
	global_load_dwordx4 v[200:203], v75, s[8:9]
	s_add_u32 s8, s8, 0x8000
	s_addc_u32 s9, s9, 0
	global_load_dwordx4 v[204:207], v75, s[8:9]
	s_add_u32 s6, s60, 0x400000
	s_addc_u32 s7, s61, 0
	ds_read_b32 v226, v212
	ds_read_b32 v227, v212 offset:512
	ds_read_b32 v228, v212 offset:1024
	ds_read_b32 v229, v212 offset:1536
	ds_read_b32 v230, v212 offset:2048
	ds_read_b32 v231, v212 offset:2560
	ds_read_b32 v232, v212 offset:3072
	ds_read_b32 v233, v212 offset:3584
	ds_read_b32 v234, v212 offset:4096
	ds_read_b32 v235, v212 offset:4608
	ds_read_b32 v236, v212 offset:5120
	ds_read_b32 v237, v212 offset:5632
	ds_read_b32 v238, v212 offset:6144
	ds_read_b32 v239, v212 offset:6656
	ds_read_b32 v240, v212 offset:7168
	ds_read_b32 v241, v212 offset:7680
	s_waitcnt lgkmcnt(0)
	v_max_f32_e32 v226, v226, v226
	v_max_f32_e32 v227, v227, v227
	v_max_f32_e32 v228, v228, v228
	v_max_f32_e32 v229, v229, v229
	v_max_f32_e32 v230, v230, v230
	v_max_f32_e32 v231, v231, v231
	v_max_f32_e32 v232, v232, v232
	v_max_f32_e32 v233, v233, v233
	v_max_f32_e32 v234, v234, v234
	v_max_f32_e32 v235, v235, v235
	v_max_f32_e32 v236, v236, v236
	v_max_f32_e32 v237, v237, v237
	v_max_f32_e32 v238, v238, v238
	v_max_f32_e32 v239, v239, v239
	v_max_f32_e32 v240, v240, v240
	v_max_f32_e32 v241, v241, v241
	v_med3_f32 v226, v226, s62, v95
	v_med3_f32 v227, v227, s62, v95
	v_med3_f32 v228, v228, s62, v95
	v_med3_f32 v229, v229, s62, v95
	v_med3_f32 v230, v230, s62, v95
	v_med3_f32 v231, v231, s62, v95
	v_med3_f32 v232, v232, s62, v95
	v_med3_f32 v233, v233, s62, v95
	v_med3_f32 v234, v234, s62, v95
	v_med3_f32 v235, v235, s62, v95
	v_med3_f32 v236, v236, s62, v95
	v_med3_f32 v237, v237, s62, v95
	v_med3_f32 v238, v238, s62, v95
	v_med3_f32 v239, v239, s62, v95
	v_med3_f32 v240, v240, s62, v95
	v_med3_f32 v241, v241, s62, v95
	v_mov_b32_e32 v242, 0
	v_mov_b32_e32 v243, 0
	v_mov_b32_e32 v244, 0
	v_mov_b32_e32 v245, 0
	v_cvt_pk_fp8_f32 v242, v226, v227
	v_cvt_pk_fp8_f32 v243, v230, v231
	v_cvt_pk_fp8_f32 v244, v234, v235
	v_cvt_pk_fp8_f32 v245, v238, v239
	v_cvt_pk_fp8_f32 v242, v228, v229 op_sel:[0,0,1]
	v_cvt_pk_fp8_f32 v243, v232, v233 op_sel:[0,0,1]
	v_cvt_pk_fp8_f32 v244, v236, v237 op_sel:[0,0,1]
	v_cvt_pk_fp8_f32 v245, v240, v241 op_sel:[0,0,1]
	s_nop 0
	global_store_dwordx4 v77, v[242:245], s[6:7]
	ds_read_b32 v226, v214
	ds_read_b32 v227, v214 offset:512
	ds_read_b32 v228, v214 offset:1024
	ds_read_b32 v229, v214 offset:1536
	ds_read_b32 v230, v214 offset:2048
	ds_read_b32 v231, v214 offset:2560
	ds_read_b32 v232, v214 offset:3072
	ds_read_b32 v233, v214 offset:3584
	ds_read_b32 v234, v214 offset:4096
	ds_read_b32 v235, v214 offset:4608
	ds_read_b32 v236, v214 offset:5120
	ds_read_b32 v237, v214 offset:5632
	ds_read_b32 v238, v214 offset:6144
	ds_read_b32 v239, v214 offset:6656
	ds_read_b32 v240, v214 offset:7168
	ds_read_b32 v241, v214 offset:7680
	s_waitcnt lgkmcnt(0)
	v_max_f32_e32 v226, v226, v226
	v_max_f32_e32 v227, v227, v227
	v_max_f32_e32 v228, v228, v228
	v_max_f32_e32 v229, v229, v229
	v_max_f32_e32 v230, v230, v230
	v_max_f32_e32 v231, v231, v231
	v_max_f32_e32 v232, v232, v232
	v_max_f32_e32 v233, v233, v233
	v_max_f32_e32 v234, v234, v234
	v_max_f32_e32 v235, v235, v235
	v_max_f32_e32 v236, v236, v236
	v_max_f32_e32 v237, v237, v237
	v_max_f32_e32 v238, v238, v238
	v_max_f32_e32 v239, v239, v239
	v_max_f32_e32 v240, v240, v240
	v_max_f32_e32 v241, v241, v241
	v_med3_f32 v226, v226, s62, v95
	v_med3_f32 v227, v227, s62, v95
	v_med3_f32 v228, v228, s62, v95
	v_med3_f32 v229, v229, s62, v95
	v_med3_f32 v230, v230, s62, v95
	v_med3_f32 v231, v231, s62, v95
	v_med3_f32 v232, v232, s62, v95
	v_med3_f32 v233, v233, s62, v95
	v_med3_f32 v234, v234, s62, v95
	v_med3_f32 v235, v235, s62, v95
	v_med3_f32 v236, v236, s62, v95
	v_med3_f32 v237, v237, s62, v95
	v_med3_f32 v238, v238, s62, v95
	v_med3_f32 v239, v239, s62, v95
	v_med3_f32 v240, v240, s62, v95
	v_med3_f32 v241, v241, s62, v95
	v_mov_b32_e32 v242, 0
	v_mov_b32_e32 v243, 0
	v_mov_b32_e32 v244, 0
	v_mov_b32_e32 v245, 0
	v_cvt_pk_fp8_f32 v242, v226, v227
	v_cvt_pk_fp8_f32 v243, v230, v231
	v_cvt_pk_fp8_f32 v244, v234, v235
	v_cvt_pk_fp8_f32 v245, v238, v239
	v_cvt_pk_fp8_f32 v242, v228, v229 op_sel:[0,0,1]
	v_cvt_pk_fp8_f32 v243, v232, v233 op_sel:[0,0,1]
	v_cvt_pk_fp8_f32 v244, v236, v237 op_sel:[0,0,1]
	v_cvt_pk_fp8_f32 v245, v240, v241 op_sel:[0,0,1]
	s_nop 0
	global_store_dwordx4 v78, v[242:245], s[6:7]
	s_waitcnt vmcnt(12)
	v_mul_f32_e32 v144, v66, v144
	v_mul_f32_e32 v145, v66, v145
	v_mul_f32_e32 v146, v66, v146
	v_mul_f32_e32 v147, v66, v147
	ds_write_b128 v209, v[144:147]
	v_mul_f32_e32 v148, v67, v148
	v_mul_f32_e32 v149, v67, v149
	v_mul_f32_e32 v150, v67, v150
	v_mul_f32_e32 v151, v67, v151
	ds_write_b128 v209, v[148:151] offset:1024
	v_mul_f32_e32 v152, v68, v152
	v_mul_f32_e32 v153, v68, v153
	v_mul_f32_e32 v154, v68, v154
	v_mul_f32_e32 v155, v68, v155
	ds_write_b128 v209, v[152:155] offset:2048
	v_mul_f32_e32 v156, v69, v156
	v_mul_f32_e32 v157, v69, v157
	v_mul_f32_e32 v158, v69, v158
	v_mul_f32_e32 v159, v69, v159
	ds_write_b128 v209, v[156:159] offset:3072
	v_mul_f32_e32 v160, v70, v160
	v_mul_f32_e32 v161, v70, v161
	v_mul_f32_e32 v162, v70, v162
	v_mul_f32_e32 v163, v70, v163
	ds_write_b128 v209, v[160:163] offset:4096
	v_mul_f32_e32 v164, v71, v164
	v_mul_f32_e32 v165, v71, v165
	v_mul_f32_e32 v166, v71, v166
	v_mul_f32_e32 v167, v71, v167
	ds_write_b128 v209, v[164:167] offset:5120
	v_mul_f32_e32 v168, v72, v168
	v_mul_f32_e32 v169, v72, v169
	v_mul_f32_e32 v170, v72, v170
	v_mul_f32_e32 v171, v72, v171
	ds_write_b128 v209, v[168:171] offset:6144
	v_mul_f32_e32 v172, v73, v172
	v_mul_f32_e32 v173, v73, v173
	v_mul_f32_e32 v174, v73, v174
	v_mul_f32_e32 v175, v73, v175
	ds_write_b128 v209, v[172:175] offset:7168
	s_waitcnt lgkmcnt(0)
	s_barrier
; #define GAS __attribute__((address_space(1)))
; #define LAS __attribute__((address_space(3)))
; #define LDS_WAIT() asm volatile("s_waitcnt lgkmcnt(0)" ::: "memory")
;     const int pr = item >> 1, kb = 2 * (pr / nblk) + (item & 1), nb = pr % nblk, k0 = 64 * kb, n0 = 32 * nb;
;     const int nr = n0 + (lane & 31); const int sc = MAP == 1 ? src_col_in(nr) : nr;
;     float v[32];
; #pragma unroll
;     for (int i = 0; i < 32; ++i) v[i] = sc >= 0 ? W[(size_t)(k0 + 2 * i + (lane >> 5)) * Nsrc + sc] : 0.f;
; #pragma unroll
;     for (int i = 0; i < 32; ++i) { const int k = k0 + 2 * i + (lane >> 5); float x = v[i] * wscale; if (KS) x *= (k < ksplit ? ksA[k] : ksB[k - ksplit]); scr[(2 * i + (lane >> 5)) * 33 + (lane & 31)] = x; }
;     LDS_WAIT(); asm volatile("" ::: "memory");
;     const int c = lane & 7;
; #pragma unroll
;     for (int j = 0; j < 4; ++j) { const int n = (lane >> 3) + 8 * j; const LAS float* s = scr + (8 * c) * 33 + n;
;         const unsigned long long o = (unsigned long long)pg8::pk4_fp8(s[0 * 33], s[1 * 33], s[2 * 33], s[3 * 33]) | ((unsigned long long)pg8::pk4_fp8(s[4 * 33], s[5 * 33], s[6 * 33], s[7 * 33]) << 32);
;         *(GAS unsigned long long*)(WT + (size_t)(n0 + n) * K + k0 + 8 * c) = o; }
;     LDS_WAIT(); asm volatile("" ::: "memory");
; }
	s_add_u32 s6, s60, 0x800000
	s_addc_u32 s7, s61, 0
	ds_read_b32 v226, v211
	ds_read_b32 v227, v211 offset:512
	ds_read_b32 v228, v211 offset:1024
	ds_read_b32 v229, v211 offset:1536
	ds_read_b32 v230, v211 offset:2048
	ds_read_b32 v231, v211 offset:2560
	ds_read_b32 v232, v211 offset:3072
	ds_read_b32 v233, v211 offset:3584
	ds_read_b32 v234, v211 offset:4096
	ds_read_b32 v235, v211 offset:4608
	ds_read_b32 v236, v211 offset:5120
	ds_read_b32 v237, v211 offset:5632
	ds_read_b32 v238, v211 offset:6144
	ds_read_b32 v239, v211 offset:6656
	ds_read_b32 v240, v211 offset:7168
	ds_read_b32 v241, v211 offset:7680
	s_waitcnt lgkmcnt(0)
	v_max_f32_e32 v226, v226, v226
	v_max_f32_e32 v227, v227, v227
	v_max_f32_e32 v228, v228, v228
	v_max_f32_e32 v229, v229, v229
	v_max_f32_e32 v230, v230, v230
	v_max_f32_e32 v231, v231, v231
	v_max_f32_e32 v232, v232, v232
	v_max_f32_e32 v233, v233, v233
	v_max_f32_e32 v234, v234, v234
	v_max_f32_e32 v235, v235, v235
	v_max_f32_e32 v236, v236, v236
	v_max_f32_e32 v237, v237, v237
	v_max_f32_e32 v238, v238, v238
	v_max_f32_e32 v239, v239, v239
	v_max_f32_e32 v240, v240, v240
	v_max_f32_e32 v241, v241, v241
	v_med3_f32 v226, v226, s62, v95
	v_med3_f32 v227, v227, s62, v95
	v_med3_f32 v228, v228, s62, v95
	v_med3_f32 v229, v229, s62, v95
	v_med3_f32 v230, v230, s62, v95
	v_med3_f32 v231, v231, s62, v95
	v_med3_f32 v232, v232, s62, v95
	v_med3_f32 v233, v233, s62, v95
	v_med3_f32 v234, v234, s62, v95
	v_med3_f32 v235, v235, s62, v95
	v_med3_f32 v236, v236, s62, v95
	v_med3_f32 v237, v237, s62, v95
	v_med3_f32 v238, v238, s62, v95
	v_med3_f32 v239, v239, s62, v95
	v_med3_f32 v240, v240, s62, v95
	v_med3_f32 v241, v241, s62, v95
	v_mov_b32_e32 v242, 0
	v_mov_b32_e32 v243, 0
	v_mov_b32_e32 v244, 0
	v_mov_b32_e32 v245, 0
	v_cvt_pk_fp8_f32 v242, v226, v227
	v_cvt_pk_fp8_f32 v243, v230, v231
	v_cvt_pk_fp8_f32 v244, v234, v235
	v_cvt_pk_fp8_f32 v245, v238, v239
	v_cvt_pk_fp8_f32 v242, v228, v229 op_sel:[0,0,1]
	v_cvt_pk_fp8_f32 v243, v232, v233 op_sel:[0,0,1]
	v_cvt_pk_fp8_f32 v244, v236, v237 op_sel:[0,0,1]
	v_cvt_pk_fp8_f32 v245, v240, v241 op_sel:[0,0,1]
	s_nop 0
	global_store_dwordx4 v77, v[242:245], s[6:7]
	ds_read_b32 v226, v213
	ds_read_b32 v227, v213 offset:512
	ds_read_b32 v228, v213 offset:1024
	ds_read_b32 v229, v213 offset:1536
	ds_read_b32 v230, v213 offset:2048
	ds_read_b32 v231, v213 offset:2560
	ds_read_b32 v232, v213 offset:3072
	ds_read_b32 v233, v213 offset:3584
	ds_read_b32 v234, v213 offset:4096
	ds_read_b32 v235, v213 offset:4608
	ds_read_b32 v236, v213 offset:5120
	ds_read_b32 v237, v213 offset:5632
	ds_read_b32 v238, v213 offset:6144
	ds_read_b32 v239, v213 offset:6656
	ds_read_b32 v240, v213 offset:7168
	ds_read_b32 v241, v213 offset:7680
	s_waitcnt lgkmcnt(0)
	v_max_f32_e32 v226, v226, v226
	v_max_f32_e32 v227, v227, v227
	v_max_f32_e32 v228, v228, v228
	v_max_f32_e32 v229, v229, v229
	v_max_f32_e32 v230, v230, v230
	v_max_f32_e32 v231, v231, v231
	v_max_f32_e32 v232, v232, v232
	v_max_f32_e32 v233, v233, v233
	v_max_f32_e32 v234, v234, v234
	v_max_f32_e32 v235, v235, v235
	v_max_f32_e32 v236, v236, v236
	v_max_f32_e32 v237, v237, v237
	v_max_f32_e32 v238, v238, v238
	v_max_f32_e32 v239, v239, v239
	v_max_f32_e32 v240, v240, v240
	v_max_f32_e32 v241, v241, v241
	v_med3_f32 v226, v226, s62, v95
	v_med3_f32 v227, v227, s62, v95
	v_med3_f32 v228, v228, s62, v95
	v_med3_f32 v229, v229, s62, v95
	v_med3_f32 v230, v230, s62, v95
	v_med3_f32 v231, v231, s62, v95
	v_med3_f32 v232, v232, s62, v95
	v_med3_f32 v233, v233, s62, v95
	v_med3_f32 v234, v234, s62, v95
	v_med3_f32 v235, v235, s62, v95
	v_med3_f32 v236, v236, s62, v95
	v_med3_f32 v237, v237, s62, v95
	v_med3_f32 v238, v238, s62, v95
	v_med3_f32 v239, v239, s62, v95
	v_med3_f32 v240, v240, s62, v95
	v_med3_f32 v241, v241, s62, v95
	v_mov_b32_e32 v242, 0
	v_mov_b32_e32 v243, 0
	v_mov_b32_e32 v244, 0
	v_mov_b32_e32 v245, 0
	v_cvt_pk_fp8_f32 v242, v226, v227
	v_cvt_pk_fp8_f32 v243, v230, v231
	v_cvt_pk_fp8_f32 v244, v234, v235
	v_cvt_pk_fp8_f32 v245, v238, v239
	v_cvt_pk_fp8_f32 v242, v228, v229 op_sel:[0,0,1]
	v_cvt_pk_fp8_f32 v243, v232, v233 op_sel:[0,0,1]
	v_cvt_pk_fp8_f32 v244, v236, v237 op_sel:[0,0,1]
	v_cvt_pk_fp8_f32 v245, v240, v241 op_sel:[0,0,1]
	s_nop 0
	global_store_dwordx4 v78, v[242:245], s[6:7]
	s_waitcnt vmcnt(4)
	v_mul_f32_e32 v176, v66, v176
	v_mul_f32_e32 v177, v66, v177
	v_mul_f32_e32 v178, v66, v178
	v_mul_f32_e32 v179, v66, v179
	ds_write_b128 v210, v[176:179]
	v_mul_f32_e32 v180, v67, v180
	v_mul_f32_e32 v181, v67, v181
	v_mul_f32_e32 v182, v67, v182
	v_mul_f32_e32 v183, v67, v183
	ds_write_b128 v210, v[180:183] offset:1024
	v_mul_f32_e32 v184, v68, v184
	v_mul_f32_e32 v185, v68, v185
	v_mul_f32_e32 v186, v68, v186
	v_mul_f32_e32 v187, v68, v187
	ds_write_b128 v210, v[184:187] offset:2048
	v_mul_f32_e32 v188, v69, v188
	v_mul_f32_e32 v189, v69, v189
	v_mul_f32_e32 v190, v69, v190
	v_mul_f32_e32 v191, v69, v191
	ds_write_b128 v210, v[188:191] offset:3072
	v_mul_f32_e32 v192, v70, v192
	v_mul_f32_e32 v193, v70, v193
	v_mul_f32_e32 v194, v70, v194
	v_mul_f32_e32 v195, v70, v195
	ds_write_b128 v210, v[192:195] offset:4096
	v_mul_f32_e32 v196, v71, v196
	v_mul_f32_e32 v197, v71, v197
	v_mul_f32_e32 v198, v71, v198
	v_mul_f32_e32 v199, v71, v199
	ds_write_b128 v210, v[196:199] offset:5120
	v_mul_f32_e32 v200, v72, v200
	v_mul_f32_e32 v201, v72, v201
	v_mul_f32_e32 v202, v72, v202
	v_mul_f32_e32 v203, v72, v203
	ds_write_b128 v210, v[200:203] offset:6144
	v_mul_f32_e32 v204, v73, v204
	v_mul_f32_e32 v205, v73, v205
	v_mul_f32_e32 v206, v73, v206
	v_mul_f32_e32 v207, v73, v207
	ds_write_b128 v210, v[204:207] offset:7168
	s_waitcnt lgkmcnt(0)
	s_barrier
; #define GAS __attribute__((address_space(1)))
; #define LAS __attribute__((address_space(3)))
; #define LDS_WAIT() asm volatile("s_waitcnt lgkmcnt(0)" ::: "memory")
;     const int pr = item >> 1, kb = 2 * (pr / nblk) + (item & 1), nb = pr % nblk, k0 = 64 * kb, n0 = 32 * nb;
;     const int nr = n0 + (lane & 31); const int sc = MAP == 1 ? src_col_in(nr) : nr;
;     float v[32];
; #pragma unroll
;     for (int i = 0; i < 32; ++i) v[i] = sc >= 0 ? W[(size_t)(k0 + 2 * i + (lane >> 5)) * Nsrc + sc] : 0.f;
; #pragma unroll
;     for (int i = 0; i < 32; ++i) { const int k = k0 + 2 * i + (lane >> 5); float x = v[i] * wscale; if (KS) x *= (k < ksplit ? ksA[k] : ksB[k - ksplit]); scr[(2 * i + (lane >> 5)) * 33 + (lane & 31)] = x; }
;     LDS_WAIT(); asm volatile("" ::: "memory");
;     const int c = lane & 7;
; #pragma unroll
;     for (int j = 0; j < 4; ++j) { const int n = (lane >> 3) + 8 * j; const LAS float* s = scr + (8 * c) * 33 + n;
;         const unsigned long long o = (unsigned long long)pg8::pk4_fp8(s[0 * 33], s[1 * 33], s[2 * 33], s[3 * 33]) | ((unsigned long long)pg8::pk4_fp8(s[4 * 33], s[5 * 33], s[6 * 33], s[7 * 33]) << 32);
;         *(GAS unsigned long long*)(WT + (size_t)(n0 + n) * K + k0 + 8 * c) = o; }
;     LDS_WAIT(); asm volatile("" ::: "memory");
; }
	s_add_u32 s6, s60, 0xc00000
	s_addc_u32 s7, s61, 0
	ds_read_b32 v226, v212
	ds_read_b32 v227, v212 offset:512
	ds_read_b32 v228, v212 offset:1024
	ds_read_b32 v229, v212 offset:1536
	ds_read_b32 v230, v212 offset:2048
	ds_read_b32 v231, v212 offset:2560
	ds_read_b32 v232, v212 offset:3072
	ds_read_b32 v233, v212 offset:3584
	ds_read_b32 v234, v212 offset:4096
	ds_read_b32 v235, v212 offset:4608
	ds_read_b32 v236, v212 offset:5120
	ds_read_b32 v237, v212 offset:5632
	ds_read_b32 v238, v212 offset:6144
	ds_read_b32 v239, v212 offset:6656
	ds_read_b32 v240, v212 offset:7168
	ds_read_b32 v241, v212 offset:7680
	s_waitcnt lgkmcnt(0)
	v_max_f32_e32 v226, v226, v226
	v_max_f32_e32 v227, v227, v227
	v_max_f32_e32 v228, v228, v228
	v_max_f32_e32 v229, v229, v229
	v_max_f32_e32 v230, v230, v230
	v_max_f32_e32 v231, v231, v231
	v_max_f32_e32 v232, v232, v232
	v_max_f32_e32 v233, v233, v233
	v_max_f32_e32 v234, v234, v234
	v_max_f32_e32 v235, v235, v235
	v_max_f32_e32 v236, v236, v236
	v_max_f32_e32 v237, v237, v237
	v_max_f32_e32 v238, v238, v238
	v_max_f32_e32 v239, v239, v239
	v_max_f32_e32 v240, v240, v240
	v_max_f32_e32 v241, v241, v241
	v_med3_f32 v226, v226, s62, v95
	v_med3_f32 v227, v227, s62, v95
	v_med3_f32 v228, v228, s62, v95
	v_med3_f32 v229, v229, s62, v95
	v_med3_f32 v230, v230, s62, v95
	v_med3_f32 v231, v231, s62, v95
	v_med3_f32 v232, v232, s62, v95
	v_med3_f32 v233, v233, s62, v95
	v_med3_f32 v234, v234, s62, v95
	v_med3_f32 v235, v235, s62, v95
	v_med3_f32 v236, v236, s62, v95
	v_med3_f32 v237, v237, s62, v95
	v_med3_f32 v238, v238, s62, v95
	v_med3_f32 v239, v239, s62, v95
	v_med3_f32 v240, v240, s62, v95
	v_med3_f32 v241, v241, s62, v95
	v_mov_b32_e32 v242, 0
	v_mov_b32_e32 v243, 0
	v_mov_b32_e32 v244, 0
	v_mov_b32_e32 v245, 0
	v_cvt_pk_fp8_f32 v242, v226, v227
	v_cvt_pk_fp8_f32 v243, v230, v231
	v_cvt_pk_fp8_f32 v244, v234, v235
	v_cvt_pk_fp8_f32 v245, v238, v239
	v_cvt_pk_fp8_f32 v242, v228, v229 op_sel:[0,0,1]
	v_cvt_pk_fp8_f32 v243, v232, v233 op_sel:[0,0,1]
	v_cvt_pk_fp8_f32 v244, v236, v237 op_sel:[0,0,1]
	v_cvt_pk_fp8_f32 v245, v240, v241 op_sel:[0,0,1]
	s_nop 0
	global_store_dwordx4 v77, v[242:245], s[6:7]
	ds_read_b32 v226, v214
	ds_read_b32 v227, v214 offset:512
	ds_read_b32 v228, v214 offset:1024
	ds_read_b32 v229, v214 offset:1536
	ds_read_b32 v230, v214 offset:2048
	ds_read_b32 v231, v214 offset:2560
	ds_read_b32 v232, v214 offset:3072
	ds_read_b32 v233, v214 offset:3584
	ds_read_b32 v234, v214 offset:4096
	ds_read_b32 v235, v214 offset:4608
	ds_read_b32 v236, v214 offset:5120
	ds_read_b32 v237, v214 offset:5632
	ds_read_b32 v238, v214 offset:6144
	ds_read_b32 v239, v214 offset:6656
	ds_read_b32 v240, v214 offset:7168
	ds_read_b32 v241, v214 offset:7680
	s_waitcnt lgkmcnt(0)
	v_max_f32_e32 v226, v226, v226
	v_max_f32_e32 v227, v227, v227
	v_max_f32_e32 v228, v228, v228
	v_max_f32_e32 v229, v229, v229
	v_max_f32_e32 v230, v230, v230
	v_max_f32_e32 v231, v231, v231
	v_max_f32_e32 v232, v232, v232
	v_max_f32_e32 v233, v233, v233
	v_max_f32_e32 v234, v234, v234
	v_max_f32_e32 v235, v235, v235
	v_max_f32_e32 v236, v236, v236
	v_max_f32_e32 v237, v237, v237
	v_max_f32_e32 v238, v238, v238
	v_max_f32_e32 v239, v239, v239
	v_max_f32_e32 v240, v240, v240
	v_max_f32_e32 v241, v241, v241
	v_med3_f32 v226, v226, s62, v95
	v_med3_f32 v227, v227, s62, v95
	v_med3_f32 v228, v228, s62, v95
	v_med3_f32 v229, v229, s62, v95
	v_med3_f32 v230, v230, s62, v95
	v_med3_f32 v231, v231, s62, v95
	v_med3_f32 v232, v232, s62, v95
	v_med3_f32 v233, v233, s62, v95
	v_med3_f32 v234, v234, s62, v95
	v_med3_f32 v235, v235, s62, v95
	v_med3_f32 v236, v236, s62, v95
	v_med3_f32 v237, v237, s62, v95
	v_med3_f32 v238, v238, s62, v95
	v_med3_f32 v239, v239, s62, v95
	v_med3_f32 v240, v240, s62, v95
	v_med3_f32 v241, v241, s62, v95
	v_mov_b32_e32 v242, 0
	v_mov_b32_e32 v243, 0
	v_mov_b32_e32 v244, 0
	v_mov_b32_e32 v245, 0
	v_cvt_pk_fp8_f32 v242, v226, v227
	v_cvt_pk_fp8_f32 v243, v230, v231
	v_cvt_pk_fp8_f32 v244, v234, v235
	v_cvt_pk_fp8_f32 v245, v238, v239
	v_cvt_pk_fp8_f32 v242, v228, v229 op_sel:[0,0,1]
	v_cvt_pk_fp8_f32 v243, v232, v233 op_sel:[0,0,1]
	v_cvt_pk_fp8_f32 v244, v236, v237 op_sel:[0,0,1]
	v_cvt_pk_fp8_f32 v245, v240, v241 op_sel:[0,0,1]
	s_nop 0
	global_store_dwordx4 v78, v[242:245], s[6:7]
	s_waitcnt lgkmcnt(0)
	s_barrier
; __global__ void __launch_bounds__(NWAVES * 64, 2) hybrid_fwd(Args args) {
;     ...
;     for (int L = 0; L < DEPTH; ++L) {
;         { unsigned long long wz = 0; asm volatile("" : "+s"(wz)); ws = args.ws + wz; }
;         bf16* Hres = (bf16*)(ws + WS_H);     static_assert(DEPTH == 2 && WO_F8_FROM == 1 && PROJ_F8_FROM == 1, "the phase instantiations below are written for this precision plan");
;         bf16* XN = (bf16*)(ws + WS_XN); bf16* PROJ = (bf16*)(ws + WS_PROJ); bf16* ACT = (bf16*)(ws + WS_ACT); unsigned char* CAT = (unsigned char*)(ws + WS_CAT);     const bool wo_f8 = L >= WO_F8_FROM;
;         float* ATT = (float*)(ws + WS_ATT); bf16* XBC = (bf16*)(ws + WS_XBC); bf16* Y = (bf16*)(ws + WS_Y);
;         bf16* KC = (bf16*)(ws + WS_KC); bf16* VC = (bf16*)(ws + WS_VC); float* DT = (float*)(ws + WS_DT); float* ADT = (float*)(ws + WS_ADT);
;         float* COS = (float*)(ws + WS_COS); float* SIN = (float*)(ws + WS_SIN); unsigned* BMP = (unsigned*)(ws + WS_BMP);
;         bf16* AO = (bf16*)(ws + WS_ACT);     float* STT = (float*)(ws + WS_ST); bf16* PREVB = (bf16*)(ws + WS_PREV);     float* ACSG = (float*)(ws + WS_ACSG); float* DEC = (float*)(ws + WS_DEC);
;         {
;             const bool split = (L < PROJ_F8_FROM) && (F.G == 256);
;             if (L >= PROJ_F8_FROM) { pg8::StaticOrder So; So.init(S, NPROJ, F.G, (int)blockIdx.x); pg8::Gemm g{XN, (const bf16*)(ws + WS_WIN + L * SZ_WIN), S, NPROJ, DM / 2};
;                 pg8::EpiProj E{PROJ, NPROJ, COS, SIN, QSCALE, 1.f / (XN8_SCALE * WUP8_SCALE), 0};
;                 pg8::gemm_phase<pg8::EpiProj, pg8::StaticOrder, true, true, true>(F.lds + RING_OFF, g, So, E); }
	v_readlane_b32 s12, v253, 35
	v_readlane_b32 s18, v253, 41
	v_readlane_b32 s19, v253, 42
	s_add_u32 s81, s18, 0x1f600000
	s_addc_u32 s94, s19, 0
	s_add_u32 s24, s18, 0xf600000
	v_or_b32_e32 v2, 2, v6
	v_mov_b32_e32 v3, 0x630
	v_readlane_b32 s13, v253, 36
	v_readlane_b32 s14, v253, 37
	v_readlane_b32 s15, v253, 38
	s_addc_u32 s25, s19, 0
	v_mad_u32_u24 v58, v2, s0, v3
	v_mov_b32_e32 v3, 0xc60
	s_add_u32 s26, s18, 0xb600000
	v_mad_u32_u24 v59, v2, s0, v3
	v_readlane_b32 s0, v253, 19
	s_addc_u32 s27, s19, 0
	v_readlane_b32 s2, v253, 21
	v_readlane_b32 s10, v253, 29
	v_readlane_b32 s3, v253, 22
	v_readlane_b32 s11, v253, 30
	s_add_u32 s2, s10, 0x4000000
	v_readlane_b32 s40, v253, 3
	s_addc_u32 s3, s11, 0
	v_readlane_b32 s52, v253, 15
	v_readlane_b32 s53, v253, 16
	s_add_u32 s22, s52, 0x2000
	v_readlane_b32 s8, v253, 27
	s_addc_u32 s23, s53, 0
	v_readlane_b32 s9, v253, 28
	s_add_u32 s84, s8, 0x2000
	s_addc_u32 s85, s9, 0
	s_add_u32 s33, s18, 0x200000
	v_readlane_b32 s44, v253, 7
	s_addc_u32 s38, s19, 0
	v_mov_b32_e32 v9, v11
	v_readlane_b32 s1, v253, 20
	v_readlane_b32 s45, v253, 8
	s_add_u32 s86, s44, 0xb140000
	v_mul_u32_u24_e32 v57, 0x84, v2
	v_readlane_b32 s42, v253, 5
	v_lshl_add_u64 v[2:3], s[18:19], 0, v[8:9]
	s_mov_b64 s[0:1], 0xd600000
	s_addc_u32 s87, s45, 0
	v_readlane_b32 s12, v253, 31
	v_readlane_b32 s13, v253, 32
	v_readlane_b32 s14, v253, 33
	v_readlane_b32 s15, v253, 34
	v_readlane_b32 s43, v253, 6
	v_readlane_b32 s54, v253, 17
	v_readlane_b32 s55, v253, 18
	v_lshl_add_u64 v[12:13], v[2:3], 0, s[0:1]
	s_add_u32 s88, s42, 0x4000
	s_mov_b64 s[0:1], 0x5c00000
	v_readlane_b32 s41, v253, 4
	v_readlane_b32 s46, v253, 9
	v_readlane_b32 s47, v253, 10
	v_readlane_b32 s48, v253, 11
	v_readlane_b32 s49, v253, 12
	v_readlane_b32 s50, v253, 13
	s_addc_u32 s89, s43, 0
	v_lshlrev_b32_e32 v4, 6, v18
	v_lshl_add_u64 v[14:15], v[2:3], 0, s[0:1]
	s_lshl_b32 s0, s80, 5
	s_movk_i32 s12, 0xe000
	s_movk_i32 s14, 0xe008
	s_movk_i32 s18, 0xe010
	s_movk_i32 s78, 0xe018
	s_movk_i32 s92, 0xe0d0
	s_movk_i32 s28, 0xe0d8
	s_movk_i32 s34, 0xe0e0
	s_movk_i32 s52, 0xe0e8
	s_movk_i32 s54, 0xe0f0
	s_movk_i32 s56, 0xe0f8
	v_or_b32_e32 v26, 0x2000, v18
	v_or_b32_e32 v27, 0x4000, v18
	v_or_b32_e32 v28, 0x6000, v18
	v_or_b32_e32 v29, 0x8000, v18
	v_or_b32_e32 v30, 0xa000, v18
	v_or_b32_e32 v31, 0xc000, v18
	v_or_b32_e32 v32, 0xe000, v18
	v_or_b32_e32 v33, 0x10000, v18
	v_or_b32_e32 v34, 0x12000, v18
	v_or_b32_e32 v35, 0x14000, v18
	v_or_b32_e32 v36, 0x16000, v18
	v_or_b32_e32 v37, 0x18000, v18
	v_or_b32_e32 v38, 0x1a000, v18
	v_or_b32_e32 v39, 0x1c000, v18
	v_or_b32_e32 v40, 0x1e000, v18
	v_or_b32_e32 v41, 0x20000, v18
	v_or_b32_e32 v42, 0x22000, v18
	v_or_b32_e32 v43, 0x24000, v18
	v_or_b32_e32 v44, 0x26000, v18
	v_or_b32_e32 v45, 0x28000, v18
	v_or_b32_e32 v46, 0x2a000, v18
	v_or_b32_e32 v47, 0x2c000, v18
	v_or_b32_e32 v48, 0x2e000, v18
	v_or_b32_e32 v49, 0x30000, v18
	v_or_b32_e32 v50, 0x32000, v18
	v_or_b32_e32 v51, 0x34000, v18
	v_or_b32_e32 v52, 0x36000, v18
	v_or_b32_e32 v53, 0x38000, v18
	v_or_b32_e32 v54, 0x3a000, v18
	v_or_b32_e32 v55, 0x3c000, v18
	v_or_b32_e32 v56, 0x3e000, v18
	v_and_b32_e32 v60, 64, v4
	v_mov_b32_e32 v7, v11
	s_lshl_b32 s39, s80, 6
	s_add_i32 s40, s0, 0xfff4c000
	s_lshl_b32 s41, s83, 8
	s_lshl_b32 s42, s80, 4
	s_lshl_b32 s43, s83, 7
	s_mov_b32 s91, 0
	s_mov_b32 s44, 0xc3e00000
	s_movk_i32 s45, 0x7fff
	s_mov_b32 s46, 0xffff0000
	s_movk_i32 s47, 0x2c2f
	s_movk_i32 s48, 0x2c50
	s_mov_b32 s49, 0xb140
	v_add_u32_e32 v61, 0x400, v19
	v_add_u32_e32 v62, 0x800, v19
	v_add_u32_e32 v63, 0xc00, v19
	v_mov_b32_e32 v64, 0x43e00000
	s_mov_b32 s50, s80
	s_mov_b32 s13, -1
	s_mov_b32 s15, -1
	s_mov_b32 s19, -1
	s_mov_b32 s79, -1
	s_mov_b32 s93, -1
	s_mov_b32 s29, -1
	s_mov_b32 s35, -1
	s_mov_b32 s53, -1
	s_mov_b32 s55, -1
	s_mov_b32 s57, -1
	v_readlane_b32 s16, v253, 39
	v_readlane_b32 s17, v253, 40
	v_readlane_b32 s4, v253, 23
	v_readlane_b32 s5, v253, 24
	v_readlane_b32 s6, v253, 25
	v_readlane_b32 s7, v253, 26
	v_readlane_b32 s51, v253, 14
	s_branch .LBB0_15
